# GEMM1 forget-gate epilogue: wave-uniform dispatch on the layer's lower bounds (all <= 0 / all > 0 / mixed) into copies of the block with the unused log_forget branch removed by dead-code elimination;
# baseline (speedup 1.0000x reference)
; __device__ __forceinline__ float log_forget(float z, float lb) {
;   const float r0 = fminf(z, 0.f) - __logf(1.f + __expf(-fabsf(z)));
;   const float r1 = __logf(lb + (1.f - lb) / (1.f + __expf(-z)));
;   return lb <= 0.f ? r0 : r1;
; }
;   __device__ __forceinline__ void operator()(const f32x4 (&acc)[2][2][4][2], const pg8::Unit& u, int wr, int wc, int fr, int fq) const {
;     ...
;       for (int bj = 0; bj < 2; ++bj) { const int c = col0 + bj * 128 - C_HF; const f32x4 l0 = *(const f32x4*)(lb + (c & 511)), l1 = *(const f32x4*)(lb + (c & 511) + 4);
; #pragma unroll
;         for (int ai = 0; ai < 2; ++ai)
; #pragma unroll
;           for (int qh = 0; qh < 2; ++qh) { float g[4][4], cs[4][4], carry[4];
;             const f32x4 lq = qh == 0 ? l0 : l1;
; #pragma unroll
;             for (int q = 0; q < 4; ++q) carry[q] = 0.f;
; #pragma unroll
;             for (int m = 0; m < 4; ++m)
; #pragma unroll
;               for (int q = 0; q < 4; ++q) { const float gv = log_forget(acc[ai][bj][m][qh][q], lq[q]); g[m][q] = gv;
.Lep1_B:
	s_nop 0
	v_and_b32_e32 v72, 0x178, v154
	v_lshlrev_b32_e32 v155, 2, v72
	global_load_dwordx4 v[72:75], v155, s[66:67] offset:16
	global_load_dwordx4 v[92:95], v155, s[66:67]
	v_mul_f32_e32 v134, 0xbfb8aa3b, v134
	v_exp_f32_e32 v134, v134
	s_cmp_gt_u32 s2, 5
	v_add_f32_e32 v134, 1.0, v134
	v_add_u32_e32 v96, 0xfffffc00, v154
	s_cselect_b64 s[42:43], -1, 0
	s_waitcnt vmcnt(0)
	v_sub_f32_e32 v157, 1.0, v92
	v_div_scale_f32 v159, s[2:3], v134, v134, v157
	v_rcp_f32_e32 v161, v159
	s_nop 0
	v_fma_f32 v163, -v159, v161, 1.0
	v_fmac_f32_e32 v161, v163, v161
	v_div_scale_f32 v163, vcc, v157, v134, v157
	v_mul_f32_e32 v165, v163, v161
	v_fma_f32 v167, -v159, v165, v163
	v_fmac_f32_e32 v165, v167, v161
	v_fma_f32 v159, -v159, v165, v163
	v_div_fmas_f32 v159, v159, v161, v165
	v_div_fixup_f32 v134, v159, v134, v157
	v_add_f32_e32 v134, v92, v134
	v_cmp_gt_f32_e32 vcc, s37, v134
	s_nop 1
	v_cndmask_b32_e64 v159, 0, 32, vcc
	v_ldexp_f32 v134, v134, v159
	v_log_f32_e32 v134, v134
	s_nop 0
	v_mul_f32_e32 v159, 0x3f317217, v134
	v_fma_f32 v159, v134, s33, -v159
	v_fmac_f32_e32 v159, 0x3377d1cf, v134
	v_fmac_f32_e32 v159, 0x3f317217, v134
	v_cmp_lt_f32_e64 s[44:45], |v134|, s36
	s_nop 1
	v_cndmask_b32_e64 v134, v134, v159, s[44:45]
	v_cndmask_b32_e32 v159, 0, v216, vcc
	v_sub_f32_e32 v165, v134, v159
	s_nop 0
	s_nop 1
	s_nop 0
	s_nop 1
	v_mul_f32_e32 v134, 0xbfb8aa3b, v135
	v_exp_f32_e32 v134, v134
	v_sub_f32_e32 v159, 1.0, v93
	v_add_f32_e32 v134, 1.0, v134
	v_div_scale_f32 v135, s[2:3], v134, v134, v159
	v_rcp_f32_e32 v161, v135
	s_nop 0
	v_fma_f32 v163, -v135, v161, 1.0
	v_fmac_f32_e32 v161, v163, v161
	v_div_scale_f32 v163, vcc, v159, v134, v159
	v_mul_f32_e32 v169, v163, v161
	v_fma_f32 v171, -v135, v169, v163
	v_fmac_f32_e32 v169, v171, v161
	v_fma_f32 v135, -v135, v169, v163
	v_div_fmas_f32 v135, v135, v161, v169
	v_div_fixup_f32 v134, v135, v134, v159
	v_add_f32_e32 v134, v93, v134
	v_cmp_gt_f32_e32 vcc, s37, v134
	s_nop 1
	v_cndmask_b32_e64 v135, 0, 32, vcc
	v_ldexp_f32 v134, v134, v135
	v_log_f32_e32 v134, v134
	s_nop 0
	v_mul_f32_e32 v135, 0x3f317217, v134
	v_fma_f32 v135, v134, s33, -v135
	v_fmac_f32_e32 v135, 0x3377d1cf, v134
	v_fmac_f32_e32 v135, 0x3f317217, v134
	v_cmp_lt_f32_e64 s[44:45], |v134|, s36
	s_nop 1
	v_cndmask_b32_e64 v134, v134, v135, s[44:45]
	v_cndmask_b32_e32 v135, 0, v216, vcc
	v_sub_f32_e32 v169, v134, v135
	s_nop 1
	s_nop 0
	s_nop 1
	v_mul_f32_e32 v135, 0xbfb8aa3b, v136
	v_exp_f32_e32 v135, v135
	v_sub_f32_e32 v161, 1.0, v94
	v_add_f32_e32 v135, 1.0, v135
	v_div_scale_f32 v136, s[2:3], v135, v135, v161
	v_rcp_f32_e32 v163, v136
	s_nop 0
	v_fma_f32 v171, -v136, v163, 1.0
	v_fmac_f32_e32 v163, v171, v163
	v_div_scale_f32 v171, vcc, v161, v135, v161
	v_mul_f32_e32 v173, v171, v163
	v_fma_f32 v177, -v136, v173, v171
	v_fmac_f32_e32 v173, v177, v163
	v_fma_f32 v136, -v136, v173, v171
	v_div_fmas_f32 v136, v136, v163, v173
	v_div_fixup_f32 v135, v136, v135, v161
	v_add_f32_e32 v135, v94, v135
	v_cmp_gt_f32_e32 vcc, s37, v135
	s_nop 1
	v_cndmask_b32_e64 v136, 0, 32, vcc
	v_ldexp_f32 v135, v135, v136
	v_log_f32_e32 v135, v135
	s_nop 0
	v_mul_f32_e32 v136, 0x3f317217, v135
	v_fma_f32 v136, v135, s33, -v136
	v_fmac_f32_e32 v136, 0x3377d1cf, v135
	v_fmac_f32_e32 v136, 0x3f317217, v135
	v_cmp_lt_f32_e64 s[44:45], |v135|, s36
	s_nop 1
	v_cndmask_b32_e64 v135, v135, v136, s[44:45]
	v_cndmask_b32_e32 v136, 0, v216, vcc
	v_sub_f32_e32 v171, v135, v136
	s_nop 1
	s_nop 0
	s_nop 1
	v_mul_f32_e32 v136, 0xbfb8aa3b, v137
	v_exp_f32_e32 v136, v136
	v_sub_f32_e32 v163, 1.0, v95
	v_add_f32_e32 v136, 1.0, v136
	v_div_scale_f32 v137, s[2:3], v136, v136, v163
	v_rcp_f32_e32 v173, v137
	s_nop 0
	v_fma_f32 v180, -v137, v173, 1.0
	v_fmac_f32_e32 v173, v180, v173
	v_div_scale_f32 v180, vcc, v163, v136, v163
	v_mul_f32_e32 v181, v180, v173
	v_fma_f32 v182, -v137, v181, v180
	v_fmac_f32_e32 v181, v182, v173
	v_fma_f32 v137, -v137, v181, v180
	v_div_fmas_f32 v137, v137, v173, v181
	v_div_fixup_f32 v136, v137, v136, v163
	v_add_f32_e32 v136, v95, v136
	v_cmp_gt_f32_e32 vcc, s37, v136
	s_nop 1
	v_cndmask_b32_e64 v137, 0, 32, vcc
	v_ldexp_f32 v136, v136, v137
	v_log_f32_e32 v136, v136
	s_nop 0
	v_mul_f32_e32 v137, 0x3f317217, v136
	v_fma_f32 v137, v136, s33, -v137
	v_fmac_f32_e32 v137, 0x3377d1cf, v136
	v_fmac_f32_e32 v137, 0x3f317217, v136
	v_cmp_lt_f32_e64 s[44:45], |v136|, s36
	s_nop 1
	v_cndmask_b32_e64 v136, v136, v137, s[44:45]
	v_cndmask_b32_e32 v137, 0, v216, vcc
	v_sub_f32_e32 v173, v136, v137
	v_mul_f32_e32 v130, 0xbfb8aa3b, v130
	v_exp_f32_e32 v130, v130
	s_nop 0
	v_add_f32_e32 v130, 1.0, v130
	s_nop 0
	s_nop 1
	v_div_scale_f32 v137, s[2:3], v130, v130, v157
	v_rcp_f32_e32 v181, v137
	s_nop 0
	v_fma_f32 v182, -v137, v181, 1.0
	v_fmac_f32_e32 v181, v182, v181
	v_div_scale_f32 v182, vcc, v157, v130, v157
	v_mul_f32_e32 v183, v182, v181
	v_fma_f32 v184, -v137, v183, v182
	v_fmac_f32_e32 v183, v184, v181
	v_fma_f32 v137, -v137, v183, v182
	v_div_fmas_f32 v137, v137, v181, v183
	v_div_fixup_f32 v130, v137, v130, v157
	v_add_f32_e32 v130, v92, v130
	v_cmp_gt_f32_e32 vcc, s37, v130
	s_nop 1
	v_cndmask_b32_e64 v137, 0, 32, vcc
	v_ldexp_f32 v130, v130, v137
	v_log_f32_e32 v130, v130
	s_nop 0
	v_mul_f32_e32 v137, 0x3f317217, v130
	v_fma_f32 v137, v130, s33, -v137
	v_fmac_f32_e32 v137, 0x3377d1cf, v130
	v_fmac_f32_e32 v137, 0x3f317217, v130
	v_cmp_lt_f32_e64 s[44:45], |v130|, s36
	s_nop 1
	v_cndmask_b32_e64 v130, v130, v137, s[44:45]
	v_cndmask_b32_e32 v137, 0, v216, vcc
	v_sub_f32_e32 v204, v130, v137
	s_nop 0
	s_nop 1
	s_nop 0
	s_nop 1
	v_mul_f32_e32 v130, 0xbfb8aa3b, v131
	v_exp_f32_e32 v130, v130
	s_nop 0
	v_add_f32_e32 v130, 1.0, v130
; __device__ __forceinline__ float log_forget(float z, float lb) {
;   const float r0 = fminf(z, 0.f) - __logf(1.f + __expf(-fabsf(z)));
;   const float r1 = __logf(lb + (1.f - lb) / (1.f + __expf(-z)));
;   return lb <= 0.f ? r0 : r1;
; }
;   __device__ __forceinline__ void operator()(const f32x4 (&acc)[2][2][4][2], const pg8::Unit& u, int wr, int wc, int fr, int fq) const {
;     ...
;             for (int m = 0; m < 4; ++m)
; #pragma unroll
;               for (int q = 0; q < 4; ++q) { const float gv = log_forget(acc[ai][bj][m][qh][q], lq[q]); g[m][q] = gv;
	v_div_scale_f32 v131, s[2:3], v130, v130, v159
	v_rcp_f32_e32 v182, v131
	s_nop 0
	v_fma_f32 v183, -v131, v182, 1.0
	v_fmac_f32_e32 v182, v183, v182
	v_div_scale_f32 v183, vcc, v159, v130, v159
	v_mul_f32_e32 v184, v183, v182
	v_fma_f32 v185, -v131, v184, v183
	v_fmac_f32_e32 v184, v185, v182
	v_fma_f32 v131, -v131, v184, v183
	v_div_fmas_f32 v131, v131, v182, v184
	v_div_fixup_f32 v130, v131, v130, v159
	v_add_f32_e32 v130, v93, v130
	v_cmp_gt_f32_e32 vcc, s37, v130
	s_nop 1
	v_cndmask_b32_e64 v131, 0, 32, vcc
	v_ldexp_f32 v130, v130, v131
	v_log_f32_e32 v130, v130
	s_nop 0
	v_mul_f32_e32 v131, 0x3f317217, v130
	v_fma_f32 v131, v130, s33, -v131
	v_fmac_f32_e32 v131, 0x3377d1cf, v130
	v_fmac_f32_e32 v131, 0x3f317217, v130
	v_cmp_lt_f32_e64 s[44:45], |v130|, s36
	s_nop 1
	v_cndmask_b32_e64 v130, v130, v131, s[44:45]
	v_cndmask_b32_e32 v131, 0, v216, vcc
	v_sub_f32_e32 v205, v130, v131
	v_mov_b32_e32 v137, v205
	s_nop 1
	v_mov_b32_dpp v181, v137 row_shr:1 row_mask:0xf bank_mask:0xf bound_ctrl:1
	s_nop 0
	s_nop 0
	s_nop 1
	v_mul_f32_e32 v131, 0xbfb8aa3b, v132
	v_exp_f32_e32 v131, v131
	s_nop 0
	v_add_f32_e32 v131, 1.0, v131
	v_div_scale_f32 v132, s[2:3], v131, v131, v161
	v_rcp_f32_e32 v183, v132
	s_nop 0
	v_fma_f32 v184, -v132, v183, 1.0
	v_fmac_f32_e32 v183, v184, v183
	v_div_scale_f32 v184, vcc, v161, v131, v161
	v_mul_f32_e32 v185, v184, v183
	v_fma_f32 v186, -v132, v185, v184
	v_fmac_f32_e32 v185, v186, v183
	v_fma_f32 v132, -v132, v185, v184
	v_div_fmas_f32 v132, v132, v183, v185
	v_div_fixup_f32 v131, v132, v131, v161
	v_add_f32_e32 v131, v94, v131
	v_cmp_gt_f32_e32 vcc, s37, v131
	s_nop 1
	v_cndmask_b32_e64 v132, 0, 32, vcc
	v_ldexp_f32 v131, v131, v132
	v_log_f32_e32 v131, v131
	s_nop 0
	v_mul_f32_e32 v132, 0x3f317217, v131
	v_fma_f32 v132, v131, s33, -v132
	v_fmac_f32_e32 v132, 0x3377d1cf, v131
	v_fmac_f32_e32 v132, 0x3f317217, v131
	v_cmp_lt_f32_e64 s[44:45], |v131|, s36
	s_nop 1
	v_cndmask_b32_e64 v131, v131, v132, s[44:45]
	v_cndmask_b32_e32 v132, 0, v216, vcc
	v_sub_f32_e32 v206, v131, v132
	s_nop 1
	s_nop 0
	s_nop 1
	v_mul_f32_e32 v132, 0xbfb8aa3b, v133
	v_exp_f32_e32 v132, v132
	s_nop 0
	v_add_f32_e32 v132, 1.0, v132
	v_div_scale_f32 v133, s[2:3], v132, v132, v163
	v_rcp_f32_e32 v184, v133
	s_nop 0
	v_fma_f32 v185, -v133, v184, 1.0
	v_fmac_f32_e32 v184, v185, v184
	v_div_scale_f32 v185, vcc, v163, v132, v163
	v_mul_f32_e32 v186, v185, v184
	v_fma_f32 v187, -v133, v186, v185
	v_fmac_f32_e32 v186, v187, v184
	v_fma_f32 v133, -v133, v186, v185
	v_div_fmas_f32 v133, v133, v184, v186
	v_div_fixup_f32 v132, v133, v132, v163
	v_add_f32_e32 v132, v95, v132
	v_cmp_gt_f32_e32 vcc, s37, v132
	s_nop 1
	v_cndmask_b32_e64 v133, 0, 32, vcc
	v_ldexp_f32 v132, v132, v133
	v_log_f32_e32 v132, v132
	s_nop 0
	v_mul_f32_e32 v133, 0x3f317217, v132
	v_fma_f32 v133, v132, s33, -v133
	v_fmac_f32_e32 v133, 0x3377d1cf, v132
	v_fmac_f32_e32 v133, 0x3f317217, v132
	v_cmp_lt_f32_e64 s[44:45], |v132|, s36
	s_nop 1
	v_cndmask_b32_e64 v132, v132, v133, s[44:45]
	v_cndmask_b32_e32 v133, 0, v216, vcc
	v_sub_f32_e32 v207, v132, v133
	v_mul_f32_e32 v126, 0xbfb8aa3b, v126
	v_exp_f32_e32 v126, v126
	s_nop 0
	v_add_f32_e32 v126, 1.0, v126
	s_nop 0
	s_nop 1
	v_div_scale_f32 v133, s[2:3], v126, v126, v157
	v_rcp_f32_e32 v185, v133
	s_nop 0
	v_fma_f32 v186, -v133, v185, 1.0
	v_fmac_f32_e32 v185, v186, v185
	v_div_scale_f32 v186, vcc, v157, v126, v157
	v_mul_f32_e32 v187, v186, v185
	v_fma_f32 v188, -v133, v187, v186
	v_fmac_f32_e32 v187, v188, v185
	v_fma_f32 v133, -v133, v187, v186
	v_div_fmas_f32 v133, v133, v185, v187
	v_div_fixup_f32 v126, v133, v126, v157
	v_add_f32_e32 v126, v92, v126
	v_cmp_gt_f32_e32 vcc, s37, v126
	s_nop 1
	v_cndmask_b32_e64 v133, 0, 32, vcc
	v_ldexp_f32 v126, v126, v133
	v_log_f32_e32 v126, v126
	s_nop 0
	v_mul_f32_e32 v133, 0x3f317217, v126
	v_fma_f32 v133, v126, s33, -v133
	v_fmac_f32_e32 v133, 0x3377d1cf, v126
	v_fmac_f32_e32 v133, 0x3f317217, v126
	v_cmp_lt_f32_e64 s[44:45], |v126|, s36
	s_nop 1
	v_cndmask_b32_e64 v126, v126, v133, s[44:45]
	v_cndmask_b32_e32 v133, 0, v216, vcc
	v_sub_f32_e32 v210, v126, v133
	s_nop 0
	s_nop 1
	s_nop 0
	s_nop 1
	v_mul_f32_e32 v126, 0xbfb8aa3b, v127
	v_exp_f32_e32 v126, v126
	s_nop 0
	v_add_f32_e32 v126, 1.0, v126
	v_div_scale_f32 v127, s[2:3], v126, v126, v159
	v_rcp_f32_e32 v186, v127
	s_nop 0
	v_fma_f32 v187, -v127, v186, 1.0
	v_fmac_f32_e32 v186, v187, v186
	v_div_scale_f32 v187, vcc, v159, v126, v159
	v_mul_f32_e32 v188, v187, v186
	v_fma_f32 v189, -v127, v188, v187
	v_fmac_f32_e32 v188, v189, v186
	v_fma_f32 v127, -v127, v188, v187
	v_div_fmas_f32 v127, v127, v186, v188
	v_div_fixup_f32 v126, v127, v126, v159
	v_add_f32_e32 v126, v93, v126
	v_cmp_gt_f32_e32 vcc, s37, v126
	s_nop 1
	v_cndmask_b32_e64 v127, 0, 32, vcc
	v_ldexp_f32 v126, v126, v127
	v_log_f32_e32 v126, v126
	s_nop 0
	v_mul_f32_e32 v127, 0x3f317217, v126
	v_fma_f32 v127, v126, s33, -v127
	v_fmac_f32_e32 v127, 0x3377d1cf, v126
	v_fmac_f32_e32 v127, 0x3f317217, v126
	v_cmp_lt_f32_e64 s[44:45], |v126|, s36
	s_nop 1
	v_cndmask_b32_e64 v126, v126, v127, s[44:45]
	v_cndmask_b32_e32 v127, 0, v216, vcc
	v_sub_f32_e32 v211, v126, v127
	v_mov_b32_e32 v185, v211
	s_nop 1
	v_mov_b32_dpp v133, v185 row_shr:1 row_mask:0xf bank_mask:0xf bound_ctrl:1
	s_nop 0
	s_nop 0
	s_nop 1
	v_mul_f32_e32 v126, 0xbfb8aa3b, v128
	v_exp_f32_e32 v126, v126
	s_nop 0
	v_add_f32_e32 v126, 1.0, v126
	v_div_scale_f32 v127, s[2:3], v126, v126, v161
	v_rcp_f32_e32 v128, v127
	s_nop 0
	v_fma_f32 v187, -v127, v128, 1.0
	v_fmac_f32_e32 v128, v187, v128
	v_div_scale_f32 v187, vcc, v161, v126, v161
	v_mul_f32_e32 v189, v187, v128
	v_fma_f32 v190, -v127, v189, v187
; __device__ __forceinline__ float log_forget(float z, float lb) {
;   const float r0 = fminf(z, 0.f) - __logf(1.f + __expf(-fabsf(z)));
;   const float r1 = __logf(lb + (1.f - lb) / (1.f + __expf(-z)));
;   return lb <= 0.f ? r0 : r1;
; }
;   __device__ __forceinline__ void operator()(const f32x4 (&acc)[2][2][4][2], const pg8::Unit& u, int wr, int wc, int fr, int fq) const {
;     ...
;             for (int m = 0; m < 4; ++m)
; #pragma unroll
;               for (int q = 0; q < 4; ++q) { const float gv = log_forget(acc[ai][bj][m][qh][q], lq[q]); g[m][q] = gv;
	v_fmac_f32_e32 v189, v190, v128
	v_fma_f32 v127, -v127, v189, v187
	v_div_fmas_f32 v127, v127, v128, v189
	v_div_fixup_f32 v126, v127, v126, v161
	v_add_f32_e32 v126, v94, v126
	v_cmp_gt_f32_e32 vcc, s37, v126
	s_nop 1
	v_cndmask_b32_e64 v127, 0, 32, vcc
	v_ldexp_f32 v126, v126, v127
	v_log_f32_e32 v126, v126
	s_nop 0
	v_mul_f32_e32 v127, 0x3f317217, v126
	v_fma_f32 v127, v126, s33, -v127
	v_fmac_f32_e32 v127, 0x3377d1cf, v126
	v_fmac_f32_e32 v127, 0x3f317217, v126
	v_cmp_lt_f32_e64 s[44:45], |v126|, s36
	s_nop 1
	v_cndmask_b32_e64 v126, v126, v127, s[44:45]
	v_cndmask_b32_e32 v127, 0, v216, vcc
	v_sub_f32_e32 v226, v126, v127
	s_nop 0
	s_nop 1
	s_nop 0
	s_nop 1
	v_mul_f32_e32 v126, 0xbfb8aa3b, v129
	v_exp_f32_e32 v126, v126
	s_nop 0
	v_add_f32_e32 v126, 1.0, v126
	v_div_scale_f32 v127, s[2:3], v126, v126, v163
	v_rcp_f32_e32 v128, v127
	s_nop 0
	v_fma_f32 v129, -v127, v128, 1.0
	v_fmac_f32_e32 v128, v129, v128
	v_div_scale_f32 v129, vcc, v163, v126, v163
	v_mul_f32_e32 v190, v129, v128
	v_fma_f32 v191, -v127, v190, v129
	v_fmac_f32_e32 v190, v191, v128
	v_fma_f32 v127, -v127, v190, v129
	v_div_fmas_f32 v127, v127, v128, v190
	v_div_fixup_f32 v126, v127, v126, v163
	v_add_f32_e32 v126, v95, v126
	v_cmp_gt_f32_e32 vcc, s37, v126
	s_nop 1
	v_cndmask_b32_e64 v127, 0, 32, vcc
	v_ldexp_f32 v126, v126, v127
	v_log_f32_e32 v126, v126
	s_nop 0
	v_mul_f32_e32 v127, 0x3f317217, v126
	v_fma_f32 v127, v126, s33, -v127
	v_fmac_f32_e32 v127, 0x3377d1cf, v126
	v_fmac_f32_e32 v127, 0x3f317217, v126
	v_cmp_lt_f32_e64 s[44:45], |v126|, s36
	s_nop 1
	v_cndmask_b32_e64 v126, v126, v127, s[44:45]
	v_cndmask_b32_e32 v127, 0, v216, vcc
	v_sub_f32_e32 v227, v126, v127
	v_mul_f32_e32 v122, 0xbfb8aa3b, v122
	v_exp_f32_e32 v122, v122
	s_nop 0
	v_add_f32_e32 v122, 1.0, v122
	s_nop 0
	s_nop 0
	s_nop 1
	v_div_scale_f32 v126, s[2:3], v122, v122, v157
	v_rcp_f32_e32 v127, v126
	s_nop 0
	v_fma_f32 v128, -v126, v127, 1.0
	v_fmac_f32_e32 v127, v128, v127
	v_div_scale_f32 v128, vcc, v157, v122, v157
	v_mul_f32_e32 v129, v128, v127
	v_fma_f32 v191, -v126, v129, v128
	v_fmac_f32_e32 v129, v191, v127
	v_fma_f32 v126, -v126, v129, v128
	v_div_fmas_f32 v126, v126, v127, v129
	v_div_fixup_f32 v122, v126, v122, v157
	v_add_f32_e32 v122, v92, v122
	v_cmp_gt_f32_e32 vcc, s37, v122
	s_nop 1
	v_cndmask_b32_e64 v126, 0, 32, vcc
	v_ldexp_f32 v122, v122, v126
	v_log_f32_e32 v122, v122
	s_nop 0
	v_mul_f32_e32 v126, 0x3f317217, v122
	v_fma_f32 v126, v122, s33, -v126
	v_fmac_f32_e32 v126, 0x3377d1cf, v122
	v_fmac_f32_e32 v126, 0x3f317217, v122
	v_cmp_lt_f32_e64 s[44:45], |v122|, s36
	s_nop 1
	v_cndmask_b32_e64 v122, v122, v126, s[44:45]
	v_cndmask_b32_e32 v126, 0, v216, vcc
	v_sub_f32_e32 v228, v122, v126
	s_nop 0
	s_nop 1
	s_nop 0
	s_nop 1
	v_mul_f32_e32 v122, 0xbfb8aa3b, v123
	v_exp_f32_e32 v122, v122
	s_nop 0
	v_add_f32_e32 v122, 1.0, v122
	v_div_scale_f32 v123, s[2:3], v122, v122, v159
	v_rcp_f32_e32 v126, v123
	s_nop 0
	v_fma_f32 v127, -v123, v126, 1.0
	v_fmac_f32_e32 v126, v127, v126
	v_div_scale_f32 v127, vcc, v159, v122, v159
	v_mul_f32_e32 v128, v127, v126
	v_fma_f32 v129, -v123, v128, v127
	v_fmac_f32_e32 v128, v129, v126
	v_fma_f32 v123, -v123, v128, v127
	v_div_fmas_f32 v123, v123, v126, v128
	v_div_fixup_f32 v122, v123, v122, v159
	v_add_f32_e32 v122, v93, v122
	v_cmp_gt_f32_e32 vcc, s37, v122
	s_nop 1
	v_cndmask_b32_e64 v123, 0, 32, vcc
	v_ldexp_f32 v122, v122, v123
	v_log_f32_e32 v122, v122
	s_nop 0
	v_mul_f32_e32 v123, 0x3f317217, v122
	v_fma_f32 v123, v122, s33, -v123
	v_fmac_f32_e32 v123, 0x3377d1cf, v122
	v_fmac_f32_e32 v123, 0x3f317217, v122
	v_cmp_lt_f32_e64 s[44:45], |v122|, s36
	s_nop 1
	v_cndmask_b32_e64 v122, v122, v123, s[44:45]
	v_cndmask_b32_e32 v123, 0, v216, vcc
	v_sub_f32_e32 v229, v122, v123
	s_nop 0
	s_nop 1
	s_nop 0
	s_nop 1
	v_mul_f32_e32 v122, 0xbfb8aa3b, v124
	v_exp_f32_e32 v122, v122
	s_nop 0
	v_add_f32_e32 v122, 1.0, v122
	v_div_scale_f32 v123, s[2:3], v122, v122, v161
	v_rcp_f32_e32 v124, v123
	s_nop 0
	v_fma_f32 v126, -v123, v124, 1.0
	v_fmac_f32_e32 v124, v126, v124
	v_div_scale_f32 v126, vcc, v161, v122, v161
	v_mul_f32_e32 v127, v126, v124
	v_fma_f32 v128, -v123, v127, v126
	v_fmac_f32_e32 v127, v128, v124
	v_fma_f32 v123, -v123, v127, v126
	v_div_fmas_f32 v123, v123, v124, v127
	v_div_fixup_f32 v122, v123, v122, v161
	v_add_f32_e32 v122, v94, v122
	v_cmp_gt_f32_e32 vcc, s37, v122
	s_nop 1
	v_cndmask_b32_e64 v123, 0, 32, vcc
	v_ldexp_f32 v122, v122, v123
	v_log_f32_e32 v122, v122
	s_nop 0
	v_mul_f32_e32 v123, 0x3f317217, v122
	v_fma_f32 v123, v122, s33, -v123
	v_fmac_f32_e32 v123, 0x3377d1cf, v122
	v_fmac_f32_e32 v123, 0x3f317217, v122
	v_cmp_lt_f32_e64 s[44:45], |v122|, s36
	s_nop 1
	v_cndmask_b32_e64 v122, v122, v123, s[44:45]
	v_cndmask_b32_e32 v123, 0, v216, vcc
	v_sub_f32_e32 v230, v122, v123
	s_nop 0
	s_nop 1
	s_nop 0
	s_nop 1
	v_mul_f32_e32 v122, 0xbfb8aa3b, v125
	v_exp_f32_e32 v122, v122
	s_nop 0
	v_add_f32_e32 v122, 1.0, v122
	v_div_scale_f32 v123, s[2:3], v122, v122, v163
	v_rcp_f32_e32 v124, v123
	s_nop 0
	v_fma_f32 v125, -v123, v124, 1.0
	v_fmac_f32_e32 v124, v125, v124
	v_div_scale_f32 v125, vcc, v163, v122, v163
	v_mul_f32_e32 v126, v125, v124
	v_fma_f32 v127, -v123, v126, v125
	v_fmac_f32_e32 v126, v127, v124
	v_fma_f32 v123, -v123, v126, v125
	v_div_fmas_f32 v123, v123, v124, v126
	v_div_fixup_f32 v122, v123, v122, v163
	v_add_f32_e32 v122, v95, v122
	v_cmp_gt_f32_e32 vcc, s37, v122
	s_nop 1
	v_cndmask_b32_e64 v123, 0, 32, vcc
	v_ldexp_f32 v122, v122, v123
	v_log_f32_e32 v122, v122
	s_nop 0
	v_mul_f32_e32 v123, 0x3f317217, v122
	v_fma_f32 v123, v122, s33, -v123
	v_fmac_f32_e32 v123, 0x3377d1cf, v122
	v_fmac_f32_e32 v123, 0x3f317217, v122
; template <int CTRL> __device__ __forceinline__ float dppx(float v) { return __int_as_float(__builtin_amdgcn_update_dpp(0, __float_as_int(v), CTRL, 0xf, 0xf, true)); }
; __device__ __forceinline__ unsigned cvt_pk_bf16(float lo, float hi) { unsigned r; asm volatile("v_cvt_pk_bf16_f32 %0, %1, %2" : "=v"(r) : "v"(lo), "v"(hi)); return r; }
;   __device__ __forceinline__ void operator()(const f32x4 (&acc)[2][2][4][2], const pg8::Unit& u, int wr, int wc, int fr, int fq) const {
;     ...
;             for (int m = 0; m < 4; ++m)
; #pragma unroll
;               for (int q = 0; q < 4; ++q) { const float gv = log_forget(acc[ai][bj][m][qh][q], lq[q]); g[m][q] = gv;
;                 float sc = gv; sc += dppx<0x111>(sc); sc += dppx<0x112>(sc); sc += dppx<0x114>(sc); sc += dppx<0x118>(sc);
;                 const float tot16 = __int_as_float(__builtin_amdgcn_ds_swizzle(__float_as_int(sc), 0x1F0));
;                 cs[m][q] = sc + carry[q]; carry[q] += tot16; }
; #pragma unroll
;             for (int m = 0; m < 4; ++m) { const int r = row0 + ai * 128 + m * 16; float bq[4], kq[4];
; #pragma unroll
;               for (int q = 0; q < 4; ++q) { bq[q] = bwd ? (carry[q] - cs[m][q]) + g[m][q] : cs[m][q]; kq[q] = 1.f - __expf(g[m][q]); }
;               *(f32x4*)(logfp + (size_t)r * 1024 + c + 4 * qh) = (f32x4){bq[0], bq[1], bq[2], bq[3]};
;               u32x2 w; w.x = pg8::cvt_pk_bf16(kq[0], kq[1]); w.y = pg8::cvt_pk_bf16(kq[2], kq[3]);
;               *(u32x2*)(km + (size_t)r * 1024 + c + 4 * qh) = w; } } }
	v_cmp_lt_f32_e64 s[44:45], |v122|, s36
	s_nop 1
	v_cndmask_b32_e64 v122, v122, v123, s[44:45]
	v_cndmask_b32_e32 v123, 0, v216, vcc
	v_sub_f32_e32 v231, v122, v123
	v_mov_b32_e32 v199, v169
	v_lshlrev_b64 v[166:167], 2, v[96:97]
	v_mov_b32_e32 v198, v165
	v_mov_b32_dpp v123, v199 row_shr:1 row_mask:0xf bank_mask:0xf bound_ctrl:1
	v_mov_b32_e32 v136, v204
	v_mov_b32_dpp v122, v198 row_shr:1 row_mask:0xf bank_mask:0xf bound_ctrl:1
	v_pk_add_f32 v[122:123], v[198:199], v[122:123]
	v_mov_b32_dpp v180, v136 row_shr:1 row_mask:0xf bank_mask:0xf bound_ctrl:1
	v_pk_add_f32 v[180:181], v[136:137], v[180:181]
	v_mov_b32_dpp v124, v122 row_shr:2 row_mask:0xf bank_mask:0xf bound_ctrl:1
	v_mov_b32_dpp v125, v123 row_shr:2 row_mask:0xf bank_mask:0xf bound_ctrl:1
	v_pk_add_f32 v[122:123], v[122:123], v[124:125]
	v_mov_b32_dpp v204, v180 row_shr:2 row_mask:0xf bank_mask:0xf bound_ctrl:1
	v_mov_b32_dpp v205, v181 row_shr:2 row_mask:0xf bank_mask:0xf bound_ctrl:1
	v_mov_b32_dpp v124, v122 row_shr:4 row_mask:0xf bank_mask:0xf bound_ctrl:1
	v_mov_b32_dpp v125, v123 row_shr:4 row_mask:0xf bank_mask:0xf bound_ctrl:1
	v_pk_add_f32 v[180:181], v[180:181], v[204:205]
	v_pk_add_f32 v[122:123], v[122:123], v[124:125]
	v_mov_b32_e32 v184, v210
	v_mov_b32_dpp v204, v180 row_shr:4 row_mask:0xf bank_mask:0xf bound_ctrl:1
	v_mov_b32_dpp v205, v181 row_shr:4 row_mask:0xf bank_mask:0xf bound_ctrl:1
	v_mov_b32_dpp v124, v122 row_shr:8 row_mask:0xf bank_mask:0xf bound_ctrl:1
	v_mov_b32_dpp v125, v123 row_shr:8 row_mask:0xf bank_mask:0xf bound_ctrl:1
	v_pk_add_f32 v[180:181], v[180:181], v[204:205]
	v_pk_add_f32 v[122:123], v[122:123], v[124:125]
	ds_swizzle_b32 v124, v122 offset:swizzle(BROADCAST,16,15)
	v_mov_b32_dpp v204, v180 row_shr:8 row_mask:0xf bank_mask:0xf bound_ctrl:1
	v_mov_b32_dpp v205, v181 row_shr:8 row_mask:0xf bank_mask:0xf bound_ctrl:1
	ds_swizzle_b32 v125, v123 offset:swizzle(BROADCAST,16,15)
	v_pk_add_f32 v[180:181], v[180:181], v[204:205]
	ds_swizzle_b32 v208, v180 offset:swizzle(BROADCAST,16,15)
	ds_swizzle_b32 v209, v181 offset:swizzle(BROADCAST,16,15)
	v_mov_b32_dpp v132, v184 row_shr:1 row_mask:0xf bank_mask:0xf bound_ctrl:1
	s_waitcnt lgkmcnt(2)
	v_pk_add_f32 v[126:127], v[124:125], 0 op_sel_hi:[1,0]
	v_pk_add_f32 v[132:133], v[184:185], v[132:133]
	v_pk_add_f32 v[204:205], v[126:127], v[180:181]
	s_waitcnt lgkmcnt(0)
	v_pk_add_f32 v[212:213], v[126:127], v[208:209]
	v_mul_f32_e32 v126, 0x3fb8aa3b, v137
	v_exp_f32_e32 v126, v126
	v_pk_add_f32 v[200:201], v[122:123], 0 op_sel_hi:[1,0]
	v_mul_f32_e32 v122, 0x3fb8aa3b, v198
	v_exp_f32_e32 v122, v122
	v_sub_f32_e32 v235, 1.0, v126
	v_mov_b32_dpp v182, v132 row_shr:2 row_mask:0xf bank_mask:0xf bound_ctrl:1
	v_mov_b32_dpp v183, v133 row_shr:2 row_mask:0xf bank_mask:0xf bound_ctrl:1
	v_pk_add_f32 v[132:133], v[132:133], v[182:183]
	v_sub_f32_e32 v169, 1.0, v122
	v_mul_f32_e32 v122, 0x3fb8aa3b, v199
	v_mov_b32_dpp v182, v132 row_shr:4 row_mask:0xf bank_mask:0xf bound_ctrl:1
	v_mov_b32_dpp v183, v133 row_shr:4 row_mask:0xf bank_mask:0xf bound_ctrl:1
	v_pk_add_f32 v[132:133], v[132:133], v[182:183]
	v_exp_f32_e32 v122, v122
	v_mov_b32_e32 v207, v207
	v_mov_b32_dpp v182, v132 row_shr:8 row_mask:0xf bank_mask:0xf bound_ctrl:1
	v_mov_b32_dpp v183, v133 row_shr:8 row_mask:0xf bank_mask:0xf bound_ctrl:1
	v_pk_add_f32 v[132:133], v[132:133], v[182:183]
	ds_swizzle_b32 v182, v132 offset:swizzle(BROADCAST,16,15)
	v_pk_add_f32 v[210:211], v[212:213], v[132:133]
	v_mul_f32_e32 v132, 0x3fb8aa3b, v184
	v_exp_f32_e32 v132, v132
	ds_swizzle_b32 v183, v133 offset:swizzle(BROADCAST,16,15)
	v_sub_f32_e32 v232, 1.0, v122
	v_sub_f32_e32 v238, 1.0, v132
	v_mul_f32_e32 v132, 0x3fb8aa3b, v185
	v_exp_f32_e32 v132, v132
	s_waitcnt lgkmcnt(0)
	v_pk_add_f32 v[212:213], v[212:213], v[182:183]
	v_mov_b32_e32 v135, v173
	v_mov_b32_e32 v134, v171
	v_sub_f32_e32 v239, 1.0, v132
	s_nop 0
	v_mov_b32_dpp v122, v134 row_shr:1 row_mask:0xf bank_mask:0xf bound_ctrl:1
	v_mov_b32_e32 v191, v229
	v_mov_b32_e32 v190, v228
	v_mov_b32_dpp v123, v135 row_shr:1 row_mask:0xf bank_mask:0xf bound_ctrl:1
	v_mov_b32_dpp v189, v191 row_shr:1 row_mask:0xf bank_mask:0xf bound_ctrl:1
	v_mov_b32_dpp v188, v190 row_shr:1 row_mask:0xf bank_mask:0xf bound_ctrl:1
	v_pk_add_f32 v[188:189], v[190:191], v[188:189]
	v_pk_add_f32 v[122:123], v[134:135], v[122:123]
	v_mov_b32_e32 v206, v206
	v_mov_b32_dpp v192, v188 row_shr:2 row_mask:0xf bank_mask:0xf bound_ctrl:1
	v_mov_b32_dpp v193, v189 row_shr:2 row_mask:0xf bank_mask:0xf bound_ctrl:1
	v_pk_add_f32 v[188:189], v[188:189], v[192:193]
	v_mov_b32_dpp v124, v122 row_shr:2 row_mask:0xf bank_mask:0xf bound_ctrl:1
	v_mov_b32_dpp v125, v123 row_shr:2 row_mask:0xf bank_mask:0xf bound_ctrl:1
	v_mov_b32_dpp v192, v188 row_shr:4 row_mask:0xf bank_mask:0xf bound_ctrl:1
	v_mov_b32_dpp v193, v189 row_shr:4 row_mask:0xf bank_mask:0xf bound_ctrl:1
	v_pk_add_f32 v[188:189], v[188:189], v[192:193]
	v_pk_add_f32 v[122:123], v[122:123], v[124:125]
	v_mov_b32_dpp v126, v206 row_shr:1 row_mask:0xf bank_mask:0xf bound_ctrl:1
	v_mov_b32_dpp v192, v188 row_shr:8 row_mask:0xf bank_mask:0xf bound_ctrl:1
	v_mov_b32_dpp v193, v189 row_shr:8 row_mask:0xf bank_mask:0xf bound_ctrl:1
	v_pk_add_f32 v[188:189], v[188:189], v[192:193]
	ds_swizzle_b32 v192, v188 offset:swizzle(BROADCAST,16,15)
	v_pk_add_f32 v[228:229], v[212:213], v[188:189]
	v_mul_f32_e32 v188, 0x3fb8aa3b, v190
	v_exp_f32_e32 v188, v188
	v_mov_b32_dpp v124, v122 row_shr:4 row_mask:0xf bank_mask:0xf bound_ctrl:1
	v_mov_b32_dpp v125, v123 row_shr:4 row_mask:0xf bank_mask:0xf bound_ctrl:1
	v_mov_b32_dpp v127, v207 row_shr:1 row_mask:0xf bank_mask:0xf bound_ctrl:1
	v_sub_f32_e32 v242, 1.0, v188
; template <int CTRL> __device__ __forceinline__ float dppx(float v) { return __int_as_float(__builtin_amdgcn_update_dpp(0, __float_as_int(v), CTRL, 0xf, 0xf, true)); }
; __device__ __forceinline__ unsigned cvt_pk_bf16(float lo, float hi) { unsigned r; asm volatile("v_cvt_pk_bf16_f32 %0, %1, %2" : "=v"(r) : "v"(lo), "v"(hi)); return r; }
;   __device__ __forceinline__ void operator()(const f32x4 (&acc)[2][2][4][2], const pg8::Unit& u, int wr, int wc, int fr, int fq) const {
;     ...
;             for (int m = 0; m < 4; ++m)
; #pragma unroll
;               for (int q = 0; q < 4; ++q) { const float gv = log_forget(acc[ai][bj][m][qh][q], lq[q]); g[m][q] = gv;
;                 float sc = gv; sc += dppx<0x111>(sc); sc += dppx<0x112>(sc); sc += dppx<0x114>(sc); sc += dppx<0x118>(sc);
;                 const float tot16 = __int_as_float(__builtin_amdgcn_ds_swizzle(__float_as_int(sc), 0x1F0));
;                 cs[m][q] = sc + carry[q]; carry[q] += tot16; }
; #pragma unroll
;             for (int m = 0; m < 4; ++m) { const int r = row0 + ai * 128 + m * 16; float bq[4], kq[4];
; #pragma unroll
;               for (int q = 0; q < 4; ++q) { bq[q] = bwd ? (carry[q] - cs[m][q]) + g[m][q] : cs[m][q]; kq[q] = 1.f - __expf(g[m][q]); }
;               *(f32x4*)(logfp + (size_t)r * 1024 + c + 4 * qh) = (f32x4){bq[0], bq[1], bq[2], bq[3]};
;               u32x2 w; w.x = pg8::cvt_pk_bf16(kq[0], kq[1]); w.y = pg8::cvt_pk_bf16(kq[2], kq[3]);
;               *(u32x2*)(km + (size_t)r * 1024 + c + 4 * qh) = w; } } }
	v_mul_f32_e32 v188, 0x3fb8aa3b, v191
	v_exp_f32_e32 v188, v188
	v_mov_b32_e32 v215, v227
	v_mov_b32_e32 v214, v226
	ds_swizzle_b32 v193, v189 offset:swizzle(BROADCAST,16,15)
	v_sub_f32_e32 v243, 1.0, v188
	v_pk_add_f32 v[122:123], v[122:123], v[124:125]
	v_pk_add_f32 v[126:127], v[206:207], v[126:127]
	v_mov_b32_dpp v132, v214 row_shr:1 row_mask:0xf bank_mask:0xf bound_ctrl:1
	v_mov_b32_dpp v133, v215 row_shr:1 row_mask:0xf bank_mask:0xf bound_ctrl:1
	v_mov_b32_e32 v195, v231
	v_mov_b32_e32 v194, v230
	v_mov_b32_dpp v124, v122 row_shr:8 row_mask:0xf bank_mask:0xf bound_ctrl:1
	v_mov_b32_dpp v125, v123 row_shr:8 row_mask:0xf bank_mask:0xf bound_ctrl:1
	v_mov_b32_dpp v130, v126 row_shr:2 row_mask:0xf bank_mask:0xf bound_ctrl:1
	v_mov_b32_dpp v131, v127 row_shr:2 row_mask:0xf bank_mask:0xf bound_ctrl:1
	v_pk_add_f32 v[132:133], v[214:215], v[132:133]
	v_mov_b32_dpp v188, v194 row_shr:1 row_mask:0xf bank_mask:0xf bound_ctrl:1
	v_mov_b32_dpp v189, v195 row_shr:1 row_mask:0xf bank_mask:0xf bound_ctrl:1
	v_pk_add_f32 v[122:123], v[122:123], v[124:125]
	v_pk_add_f32 v[126:127], v[126:127], v[130:131]
	v_mov_b32_dpp v182, v132 row_shr:2 row_mask:0xf bank_mask:0xf bound_ctrl:1
	v_mov_b32_dpp v183, v133 row_shr:2 row_mask:0xf bank_mask:0xf bound_ctrl:1
	v_pk_add_f32 v[188:189], v[194:195], v[188:189]
	ds_swizzle_b32 v124, v122 offset:swizzle(BROADCAST,16,15)
	ds_swizzle_b32 v125, v123 offset:swizzle(BROADCAST,16,15)
	v_mov_b32_dpp v130, v126 row_shr:4 row_mask:0xf bank_mask:0xf bound_ctrl:1
	v_mov_b32_dpp v131, v127 row_shr:4 row_mask:0xf bank_mask:0xf bound_ctrl:1
	v_pk_add_f32 v[132:133], v[132:133], v[182:183]
	v_mov_b32_dpp v196, v188 row_shr:2 row_mask:0xf bank_mask:0xf bound_ctrl:1
	v_mov_b32_dpp v197, v189 row_shr:2 row_mask:0xf bank_mask:0xf bound_ctrl:1
	v_pk_add_f32 v[126:127], v[126:127], v[130:131]
	v_mov_b32_dpp v182, v132 row_shr:4 row_mask:0xf bank_mask:0xf bound_ctrl:1
	v_mov_b32_dpp v183, v133 row_shr:4 row_mask:0xf bank_mask:0xf bound_ctrl:1
	v_pk_add_f32 v[188:189], v[188:189], v[196:197]
	v_pk_add_f32 v[202:203], v[122:123], 0 op_sel_hi:[1,0]
	v_mul_f32_e32 v122, 0x3fb8aa3b, v134
	v_mov_b32_dpp v130, v126 row_shr:8 row_mask:0xf bank_mask:0xf bound_ctrl:1
	v_mov_b32_dpp v131, v127 row_shr:8 row_mask:0xf bank_mask:0xf bound_ctrl:1
	v_pk_add_f32 v[132:133], v[132:133], v[182:183]
	v_mov_b32_dpp v196, v188 row_shr:4 row_mask:0xf bank_mask:0xf bound_ctrl:1
	v_mov_b32_dpp v197, v189 row_shr:4 row_mask:0xf bank_mask:0xf bound_ctrl:1
	v_exp_f32_e32 v122, v122
	v_pk_add_f32 v[126:127], v[126:127], v[130:131]
	v_mov_b32_dpp v182, v132 row_shr:8 row_mask:0xf bank_mask:0xf bound_ctrl:1
	v_mov_b32_dpp v183, v133 row_shr:8 row_mask:0xf bank_mask:0xf bound_ctrl:1
	v_pk_add_f32 v[188:189], v[188:189], v[196:197]
	ds_swizzle_b32 v130, v126 offset:swizzle(BROADCAST,16,15)
	ds_swizzle_b32 v131, v127 offset:swizzle(BROADCAST,16,15)
	v_pk_add_f32 v[132:133], v[132:133], v[182:183]
	v_mov_b32_dpp v196, v188 row_shr:8 row_mask:0xf bank_mask:0xf bound_ctrl:1
	v_mov_b32_dpp v197, v189 row_shr:8 row_mask:0xf bank_mask:0xf bound_ctrl:1
	s_waitcnt lgkmcnt(2)
	v_pk_add_f32 v[128:129], v[124:125], 0 op_sel_hi:[1,0]
	ds_swizzle_b32 v182, v132 offset:swizzle(BROADCAST,16,15)
	ds_swizzle_b32 v183, v133 offset:swizzle(BROADCAST,16,15)
	v_pk_add_f32 v[188:189], v[188:189], v[196:197]
	v_pk_add_f32 v[208:209], v[128:129], v[126:127]
	v_mul_f32_e32 v126, 0x3fb8aa3b, v206
	ds_swizzle_b32 v196, v188 offset:swizzle(BROADCAST,16,15)
	ds_swizzle_b32 v197, v189 offset:swizzle(BROADCAST,16,15)
	v_sub_f32_e32 v233, 1.0, v122
	v_mul_f32_e32 v122, 0x3fb8aa3b, v135
	v_exp_f32_e32 v126, v126
	v_exp_f32_e32 v122, v122
	s_waitcnt lgkmcnt(4)
	v_pk_add_f32 v[130:131], v[128:129], v[130:131]
	v_ashrrev_i32_e32 v165, 31, v164
	v_pk_add_f32 v[226:227], v[130:131], v[132:133]
	s_waitcnt lgkmcnt(2)
	v_pk_add_f32 v[186:187], v[130:131], v[182:183]
	v_mul_f32_e32 v130, 0x3fb8aa3b, v214
	v_sub_f32_e32 v236, 1.0, v126
	v_mul_f32_e32 v126, 0x3fb8aa3b, v207
	v_exp_f32_e32 v130, v130
	v_pk_add_f32 v[192:193], v[212:213], v[192:193]
	s_waitcnt lgkmcnt(0)
	v_pk_add_f32 v[196:197], v[186:187], v[196:197]
	v_sub_f32_e32 v234, 1.0, v122
	v_lshlrev_b64 v[122:123], 12, v[164:165]
	v_exp_f32_e32 v126, v126
	v_pk_add_f32 v[212:213], v[186:187], v[188:189]
	v_pk_add_f32 v[186:187], v[192:193], v[200:201] neg_lo:[0,1] neg_hi:[0,1]
	v_pk_add_f32 v[188:189], v[196:197], v[202:203] neg_lo:[0,1] neg_hi:[0,1]
	v_lshl_add_u64 v[122:123], s[22:23], 0, v[122:123]
	v_lshlrev_b64 v[124:125], 11, v[164:165]
	v_pk_add_f32 v[186:187], v[198:199], v[186:187]
	v_pk_add_f32 v[134:135], v[134:135], v[188:189]
	v_lshl_add_u64 v[176:177], v[122:123], 0, v[166:167]
	v_lshl_add_u64 v[124:125], s[0:1], 0, v[124:125]
	v_lshlrev_b64 v[164:165], 1, v[96:97]
	v_mul_f32_e32 v96, 0x3fb8aa3b, v136
	v_cndmask_b32_e64 v189, v203, v135, s[42:43]
	v_cndmask_b32_e64 v188, v202, v134, s[42:43]
	v_cndmask_b32_e64 v187, v201, v187, s[42:43]
	v_cndmask_b32_e64 v186, v200, v186, s[42:43]
	v_lshl_add_u64 v[174:175], v[124:125], 0, v[164:165]
	v_exp_f32_e32 v96, v96
	v_ashrrev_i32_e32 v173, 31, v172
	v_sub_f32_e32 v240, 1.0, v130
	v_mul_f32_e32 v130, 0x3fb8aa3b, v215
	global_store_dwordx4 v[176:177], v[186:189], off
	v_cvt_pk_bf16_f32 v134, v169, v232
	v_cvt_pk_bf16_f32 v135, v233, v234
	v_sub_f32_e32 v237, 1.0, v126
	v_lshlrev_b64 v[126:127], 12, v[172:173]
	v_exp_f32_e32 v130, v130
	global_store_dwordx2 v[174:175], v[134:135], off
	v_pk_add_f32 v[134:135], v[192:193], v[204:205] neg_lo:[0,1] neg_hi:[0,1]
	v_pk_add_f32 v[186:187], v[196:197], v[208:209] neg_lo:[0,1] neg_hi:[0,1]
	v_lshl_add_u64 v[126:127], s[22:23], 0, v[126:127]
; __device__ __forceinline__ unsigned cvt_pk_bf16(float lo, float hi) { unsigned r; asm volatile("v_cvt_pk_bf16_f32 %0, %1, %2" : "=v"(r) : "v"(lo), "v"(hi)); return r; }
; __device__ __forceinline__ float log_forget(float z, float lb) {
;   const float r0 = fminf(z, 0.f) - __logf(1.f + __expf(-fabsf(z)));
;   const float r1 = __logf(lb + (1.f - lb) / (1.f + __expf(-z)));
;   return lb <= 0.f ? r0 : r1;
; }
;   __device__ __forceinline__ void operator()(const f32x4 (&acc)[2][2][4][2], const pg8::Unit& u, int wr, int wc, int fr, int fq) const {
;     ...
;             for (int m = 0; m < 4; ++m) { const int r = row0 + ai * 128 + m * 16; float bq[4], kq[4];
; #pragma unroll
;               for (int q = 0; q < 4; ++q) { bq[q] = bwd ? (carry[q] - cs[m][q]) + g[m][q] : cs[m][q]; kq[q] = 1.f - __expf(g[m][q]); }
;               *(f32x4*)(logfp + (size_t)r * 1024 + c + 4 * qh) = (f32x4){bq[0], bq[1], bq[2], bq[3]};
;               u32x2 w; w.x = pg8::cvt_pk_bf16(kq[0], kq[1]); w.y = pg8::cvt_pk_bf16(kq[2], kq[3]);
;               *(u32x2*)(km + (size_t)r * 1024 + c + 4 * qh) = w; } } }
	v_lshlrev_b64 v[128:129], 11, v[172:173]
	v_pk_add_f32 v[134:135], v[136:137], v[134:135]
	v_pk_add_f32 v[136:137], v[206:207], v[186:187]
	v_lshl_add_u64 v[180:181], v[126:127], 0, v[166:167]
	v_lshl_add_u64 v[128:129], s[0:1], 0, v[128:129]
	v_cndmask_b32_e64 v137, v209, v137, s[42:43]
	v_cndmask_b32_e64 v136, v208, v136, s[42:43]
	v_cndmask_b32_e64 v135, v205, v135, s[42:43]
	v_cndmask_b32_e64 v134, v204, v134, s[42:43]
	v_sub_f32_e32 v96, 1.0, v96
	v_lshl_add_u64 v[172:173], v[128:129], 0, v[164:165]
	v_ashrrev_i32_e32 v171, 31, v170
	global_store_dwordx4 v[180:181], v[134:137], off
	v_sub_f32_e32 v241, 1.0, v130
	v_lshlrev_b64 v[130:131], 12, v[170:171]
	v_cvt_pk_bf16_f32 v134, v96, v235
	v_cvt_pk_bf16_f32 v135, v236, v237
	global_store_dwordx2 v[172:173], v[134:135], off
	v_pk_add_f32 v[134:135], v[192:193], v[210:211] neg_lo:[0,1] neg_hi:[0,1]
	v_pk_add_f32 v[136:137], v[196:197], v[226:227] neg_lo:[0,1] neg_hi:[0,1]
	v_lshl_add_u64 v[130:131], s[22:23], 0, v[130:131]
	v_lshlrev_b64 v[132:133], 11, v[170:171]
	v_pk_add_f32 v[134:135], v[184:185], v[134:135]
	v_pk_add_f32 v[136:137], v[214:215], v[136:137]
	v_lshl_add_u64 v[182:183], v[130:131], 0, v[166:167]
	v_lshl_add_u64 v[132:133], s[0:1], 0, v[132:133]
	v_cndmask_b32_e64 v137, v227, v137, s[42:43]
	v_cndmask_b32_e64 v136, v226, v136, s[42:43]
	v_cndmask_b32_e64 v135, v211, v135, s[42:43]
	v_cndmask_b32_e64 v134, v210, v134, s[42:43]
	v_lshl_add_u64 v[170:171], v[132:133], 0, v[164:165]
	global_store_dwordx4 v[182:183], v[134:137], off
	v_mul_f32_e32 v96, 0x3fb8aa3b, v194
	v_exp_f32_e32 v96, v96
	v_cvt_pk_bf16_f32 v134, v238, v239
	v_cvt_pk_bf16_f32 v135, v240, v241
	global_store_dwordx2 v[170:171], v[134:135], off
	v_pk_add_f32 v[134:135], v[192:193], v[228:229] neg_lo:[0,1] neg_hi:[0,1]
	v_pk_add_f32 v[136:137], v[196:197], v[212:213] neg_lo:[0,1] neg_hi:[0,1]
	v_pk_add_f32 v[134:135], v[190:191], v[134:135]
	v_pk_add_f32 v[136:137], v[194:195], v[136:137]
	v_cndmask_b32_e64 v186, v228, v134, s[42:43]
	v_mul_f32_e32 v134, 0x3fb8aa3b, v195
	v_exp_f32_e32 v134, v134
	v_ashrrev_i32_e32 v169, 31, v168
	v_cndmask_b32_e64 v188, v212, v136, s[42:43]
	v_cndmask_b32_e64 v187, v229, v135, s[42:43]
	v_sub_f32_e32 v136, 1.0, v134
	v_lshlrev_b64 v[134:135], 12, v[168:169]
	v_lshl_add_u64 v[134:135], s[22:23], 0, v[134:135]
	v_cndmask_b32_e64 v189, v213, v137, s[42:43]
	v_lshl_add_u64 v[184:185], v[134:135], 0, v[166:167]
	v_sub_f32_e32 v96, 1.0, v96
	global_store_dwordx4 v[184:185], v[186:189], off
	v_sub_f32_e32 v206, 1.0, v72
	v_sub_f32_e32 v205, 1.0, v73
	v_cvt_pk_bf16_f32 v186, v242, v243
	v_cvt_pk_bf16_f32 v187, v96, v136
	v_lshlrev_b64 v[136:137], 11, v[168:169]
	v_lshl_add_u64 v[136:137], s[0:1], 0, v[136:137]
	v_lshl_add_u64 v[168:169], v[136:137], 0, v[164:165]
	global_store_dwordx2 v[168:169], v[186:187], off
	v_sub_f32_e32 v204, 1.0, v74
	s_nop 1
	s_nop 0
	s_nop 1
	v_mul_f32_e32 v96, 0xbfb8aa3b, v118
	v_exp_f32_e32 v96, v96
	s_nop 0
	v_add_f32_e32 v96, 1.0, v96
	v_div_scale_f32 v118, s[2:3], v96, v96, v206
	v_rcp_f32_e32 v187, v118
	s_nop 0
	v_fma_f32 v189, -v118, v187, 1.0
	v_fmac_f32_e32 v187, v189, v187
	v_div_scale_f32 v189, vcc, v206, v96, v206
	v_mul_f32_e32 v190, v189, v187
	v_fma_f32 v191, -v118, v190, v189
	v_fmac_f32_e32 v190, v191, v187
	v_fma_f32 v118, -v118, v190, v189
	v_div_fmas_f32 v118, v118, v187, v190
	v_div_fixup_f32 v96, v118, v96, v206
	v_add_f32_e32 v96, v72, v96
	v_cmp_gt_f32_e32 vcc, s37, v96
	s_nop 1
	v_cndmask_b32_e64 v118, 0, 32, vcc
	v_ldexp_f32 v96, v96, v118
	v_log_f32_e32 v96, v96
	s_nop 0
	v_mul_f32_e32 v118, 0x3f317217, v96
	v_fma_f32 v118, v96, s33, -v118
	v_fmac_f32_e32 v118, 0x3377d1cf, v96
	v_fmac_f32_e32 v118, 0x3f317217, v96
	v_cmp_lt_f32_e64 s[52:53], |v96|, s36
	s_nop 1
	v_cndmask_b32_e64 v96, v96, v118, s[52:53]
	v_cndmask_b32_e32 v118, 0, v216, vcc
	v_sub_f32_e32 v207, v96, v118
	s_nop 0
	s_nop 1
	s_nop 0
	s_nop 1
	v_mul_f32_e32 v96, 0xbfb8aa3b, v119
	v_exp_f32_e32 v96, v96
	s_nop 0
	v_add_f32_e32 v96, 1.0, v96
	v_div_scale_f32 v118, s[2:3], v96, v96, v205
	v_rcp_f32_e32 v119, v118
	s_nop 0
	v_fma_f32 v190, -v118, v119, 1.0
	v_fmac_f32_e32 v119, v190, v119
	v_div_scale_f32 v190, vcc, v205, v96, v205
	v_mul_f32_e32 v191, v190, v119
	v_fma_f32 v192, -v118, v191, v190
	v_fmac_f32_e32 v191, v192, v119
	v_fma_f32 v118, -v118, v191, v190
	v_div_fmas_f32 v118, v118, v119, v191
	v_div_fixup_f32 v96, v118, v96, v205
	v_add_f32_e32 v96, v73, v96
	v_cmp_gt_f32_e32 vcc, s37, v96
	s_nop 1
	v_cndmask_b32_e64 v118, 0, 32, vcc
	v_ldexp_f32 v96, v96, v118
	v_log_f32_e32 v96, v96
	s_nop 0
	v_mul_f32_e32 v118, 0x3f317217, v96
	v_fma_f32 v118, v96, s33, -v118
	v_fmac_f32_e32 v118, 0x3377d1cf, v96
	v_fmac_f32_e32 v118, 0x3f317217, v96
	v_cmp_lt_f32_e64 s[52:53], |v96|, s36
	s_nop 1
	v_cndmask_b32_e64 v96, v96, v118, s[52:53]
	v_cndmask_b32_e32 v118, 0, v216, vcc
	v_sub_f32_e32 v208, v96, v118
	s_nop 0
	s_nop 1
	s_nop 0
	s_nop 1
	v_mul_f32_e32 v96, 0xbfb8aa3b, v120
	v_exp_f32_e32 v96, v96
	s_nop 0
	v_add_f32_e32 v96, 1.0, v96
	v_div_scale_f32 v119, s[2:3], v96, v96, v204
	v_rcp_f32_e32 v120, v119
	s_nop 0
	v_fma_f32 v191, -v119, v120, 1.0
	v_fmac_f32_e32 v120, v191, v120
	v_div_scale_f32 v191, vcc, v204, v96, v204
	v_mul_f32_e32 v192, v191, v120
	v_fma_f32 v193, -v119, v192, v191
	v_fmac_f32_e32 v192, v193, v120
	v_fma_f32 v119, -v119, v192, v191
	v_div_fmas_f32 v119, v119, v120, v192
	v_div_fixup_f32 v96, v119, v96, v204
	v_add_f32_e32 v96, v74, v96
	v_cmp_gt_f32_e32 vcc, s37, v96
	s_nop 1
	v_cndmask_b32_e64 v119, 0, 32, vcc
	v_ldexp_f32 v96, v96, v119
	v_log_f32_e32 v96, v96
	s_nop 0
	v_mul_f32_e32 v119, 0x3f317217, v96
	v_fma_f32 v119, v96, s33, -v119
; __device__ __forceinline__ float log_forget(float z, float lb) {
;   const float r0 = fminf(z, 0.f) - __logf(1.f + __expf(-fabsf(z)));
;   const float r1 = __logf(lb + (1.f - lb) / (1.f + __expf(-z)));
;   return lb <= 0.f ? r0 : r1;
; }
;   __device__ __forceinline__ void operator()(const f32x4 (&acc)[2][2][4][2], const pg8::Unit& u, int wr, int wc, int fr, int fq) const {
;     ...
;             for (int m = 0; m < 4; ++m)
; #pragma unroll
;               for (int q = 0; q < 4; ++q) { const float gv = log_forget(acc[ai][bj][m][qh][q], lq[q]); g[m][q] = gv;
	v_fmac_f32_e32 v119, 0x3377d1cf, v96
	v_fmac_f32_e32 v119, 0x3f317217, v96
	v_cmp_lt_f32_e64 s[52:53], |v96|, s36
	s_nop 1
	v_cndmask_b32_e64 v96, v96, v119, s[52:53]
	v_cndmask_b32_e32 v119, 0, v216, vcc
	v_sub_f32_e32 v209, v96, v119
	s_nop 0
	s_nop 1
	s_nop 0
	s_nop 1
	v_mul_f32_e32 v120, 0xbfb8aa3b, v121
	v_exp_f32_e32 v120, v120
	v_sub_f32_e32 v96, 1.0, v75
	v_add_f32_e32 v120, 1.0, v120
	v_div_scale_f32 v121, s[2:3], v120, v120, v96
	v_rcp_f32_e32 v192, v121
	v_mov_b32_e32 v118, v209
	v_fma_f32 v193, -v121, v192, 1.0
	v_fmac_f32_e32 v192, v193, v192
	v_div_scale_f32 v193, vcc, v96, v120, v96
	v_mul_f32_e32 v194, v193, v192
	v_fma_f32 v195, -v121, v194, v193
	v_fmac_f32_e32 v194, v195, v192
	v_fma_f32 v121, -v121, v194, v193
	v_div_fmas_f32 v121, v121, v192, v194
	v_div_fixup_f32 v120, v121, v120, v96
	v_add_f32_e32 v120, v75, v120
	v_cmp_gt_f32_e32 vcc, s37, v120
	s_nop 1
	v_cndmask_b32_e64 v121, 0, 32, vcc
	v_ldexp_f32 v120, v120, v121
	v_log_f32_e32 v120, v120
	s_nop 0
	v_mul_f32_e32 v121, 0x3f317217, v120
	v_fma_f32 v121, v120, s33, -v121
	v_fmac_f32_e32 v121, 0x3377d1cf, v120
	v_fmac_f32_e32 v121, 0x3f317217, v120
	v_cmp_lt_f32_e64 s[52:53], |v120|, s36
	s_nop 1
	v_cndmask_b32_e64 v120, v120, v121, s[52:53]
	v_cndmask_b32_e32 v121, 0, v216, vcc
	v_sub_f32_e32 v210, v120, v121
	v_mul_f32_e32 v114, 0xbfb8aa3b, v114
	v_exp_f32_e32 v114, v114
	v_mov_b32_e32 v119, v210
	v_add_f32_e32 v114, 1.0, v114
	s_nop 1
	v_div_scale_f32 v121, s[2:3], v114, v114, v206
	v_rcp_f32_e32 v193, v121
	s_nop 0
	v_fma_f32 v194, -v121, v193, 1.0
	v_fmac_f32_e32 v193, v194, v193
	v_div_scale_f32 v194, vcc, v206, v114, v206
	v_mul_f32_e32 v195, v194, v193
	v_fma_f32 v196, -v121, v195, v194
	v_fmac_f32_e32 v195, v196, v193
	v_fma_f32 v121, -v121, v195, v194
	v_div_fmas_f32 v121, v121, v193, v195
	v_div_fixup_f32 v114, v121, v114, v206
	v_add_f32_e32 v114, v72, v114
	v_cmp_gt_f32_e32 vcc, s37, v114
	s_nop 1
	v_cndmask_b32_e64 v121, 0, 32, vcc
	v_ldexp_f32 v114, v114, v121
	v_log_f32_e32 v114, v114
	s_nop 0
	v_mul_f32_e32 v121, 0x3f317217, v114
	v_fma_f32 v121, v114, s33, -v121
	v_fmac_f32_e32 v121, 0x3377d1cf, v114
	v_fmac_f32_e32 v121, 0x3f317217, v114
	v_cmp_lt_f32_e64 s[52:53], |v114|, s36
	s_nop 1
	v_cndmask_b32_e64 v114, v114, v121, s[52:53]
	v_cndmask_b32_e32 v121, 0, v216, vcc
	v_sub_f32_e32 v211, v114, v121
	s_nop 0
	s_nop 1
	s_nop 0
	s_nop 1
	v_mul_f32_e32 v114, 0xbfb8aa3b, v115
	v_exp_f32_e32 v114, v114
	s_nop 0
	v_add_f32_e32 v114, 1.0, v114
	v_div_scale_f32 v115, s[2:3], v114, v114, v205
	v_rcp_f32_e32 v194, v115
	s_nop 0
	v_fma_f32 v195, -v115, v194, 1.0
	v_fmac_f32_e32 v194, v195, v194
	v_div_scale_f32 v195, vcc, v205, v114, v205
	v_mul_f32_e32 v196, v195, v194
	v_fma_f32 v197, -v115, v196, v195
	v_fmac_f32_e32 v196, v197, v194
	v_fma_f32 v115, -v115, v196, v195
	v_div_fmas_f32 v115, v115, v194, v196
	v_div_fixup_f32 v114, v115, v114, v205
	v_add_f32_e32 v114, v73, v114
	v_cmp_gt_f32_e32 vcc, s37, v114
	s_nop 1
	v_cndmask_b32_e64 v115, 0, 32, vcc
	v_ldexp_f32 v114, v114, v115
	v_log_f32_e32 v114, v114
	s_nop 0
	v_mul_f32_e32 v115, 0x3f317217, v114
	v_fma_f32 v115, v114, s33, -v115
	v_fmac_f32_e32 v115, 0x3377d1cf, v114
	v_fmac_f32_e32 v115, 0x3f317217, v114
	v_cmp_lt_f32_e64 s[52:53], |v114|, s36
	s_nop 1
	v_cndmask_b32_e64 v114, v114, v115, s[52:53]
	v_cndmask_b32_e32 v115, 0, v216, vcc
	v_sub_f32_e32 v226, v114, v115
	v_mov_b32_e32 v121, v226
	s_nop 1
	s_nop 0
	s_nop 1
	v_mul_f32_e32 v115, 0xbfb8aa3b, v116
	v_exp_f32_e32 v115, v115
	s_nop 0
	v_add_f32_e32 v115, 1.0, v115
	v_div_scale_f32 v116, s[2:3], v115, v115, v204
	v_rcp_f32_e32 v195, v116
	s_nop 0
	v_fma_f32 v196, -v116, v195, 1.0
	v_fmac_f32_e32 v195, v196, v195
	v_div_scale_f32 v196, vcc, v204, v115, v204
	v_mul_f32_e32 v197, v196, v195
	v_fma_f32 v198, -v116, v197, v196
	v_fmac_f32_e32 v197, v198, v195
	v_fma_f32 v116, -v116, v197, v196
	v_div_fmas_f32 v116, v116, v195, v197
	v_div_fixup_f32 v115, v116, v115, v204
	v_add_f32_e32 v115, v74, v115
	v_cmp_gt_f32_e32 vcc, s37, v115
	s_nop 1
	v_cndmask_b32_e64 v116, 0, 32, vcc
	v_ldexp_f32 v115, v115, v116
	v_log_f32_e32 v115, v115
	s_nop 0
	v_mul_f32_e32 v116, 0x3f317217, v115
	v_fma_f32 v116, v115, s33, -v116
	v_fmac_f32_e32 v116, 0x3377d1cf, v115
	v_fmac_f32_e32 v116, 0x3f317217, v115
	v_cmp_lt_f32_e64 s[52:53], |v115|, s36
	s_nop 1
	v_cndmask_b32_e64 v115, v115, v116, s[52:53]
	v_cndmask_b32_e32 v116, 0, v216, vcc
	v_sub_f32_e32 v227, v115, v116
	s_nop 1
	s_nop 0
	s_nop 1
	v_mul_f32_e32 v116, 0xbfb8aa3b, v117
	v_exp_f32_e32 v116, v116
	s_nop 0
	v_add_f32_e32 v116, 1.0, v116
	v_div_scale_f32 v117, s[2:3], v116, v116, v96
	v_rcp_f32_e32 v196, v117
	v_mov_b32_e32 v114, v227
	v_fma_f32 v197, -v117, v196, 1.0
	v_fmac_f32_e32 v196, v197, v196
	v_div_scale_f32 v197, vcc, v96, v116, v96
	v_mul_f32_e32 v198, v197, v196
	v_fma_f32 v199, -v117, v198, v197
	v_fmac_f32_e32 v198, v199, v196
	v_fma_f32 v117, -v117, v198, v197
	v_div_fmas_f32 v117, v117, v196, v198
	v_div_fixup_f32 v116, v117, v116, v96
	v_add_f32_e32 v116, v75, v116
	v_cmp_gt_f32_e32 vcc, s37, v116
	s_nop 1
	v_cndmask_b32_e64 v117, 0, 32, vcc
	v_ldexp_f32 v116, v116, v117
	v_log_f32_e32 v116, v116
	s_nop 0
	v_mul_f32_e32 v117, 0x3f317217, v116
	v_fma_f32 v117, v116, s33, -v117
	v_fmac_f32_e32 v117, 0x3377d1cf, v116
	v_fmac_f32_e32 v117, 0x3f317217, v116
	v_cmp_lt_f32_e64 s[52:53], |v116|, s36
	s_nop 1
	v_cndmask_b32_e64 v116, v116, v117, s[52:53]
	v_cndmask_b32_e32 v117, 0, v216, vcc
	v_sub_f32_e32 v228, v116, v117
	v_mul_f32_e32 v110, 0xbfb8aa3b, v110
	v_exp_f32_e32 v110, v110
	v_mov_b32_e32 v115, v228
	v_add_f32_e32 v110, 1.0, v110
	s_nop 1
	v_div_scale_f32 v117, s[2:3], v110, v110, v206
; __device__ __forceinline__ float log_forget(float z, float lb) {
;   const float r0 = fminf(z, 0.f) - __logf(1.f + __expf(-fabsf(z)));
;   const float r1 = __logf(lb + (1.f - lb) / (1.f + __expf(-z)));
;   return lb <= 0.f ? r0 : r1;
; }
;   __device__ __forceinline__ void operator()(const f32x4 (&acc)[2][2][4][2], const pg8::Unit& u, int wr, int wc, int fr, int fq) const {
;     ...
;             for (int m = 0; m < 4; ++m)
; #pragma unroll
;               for (int q = 0; q < 4; ++q) { const float gv = log_forget(acc[ai][bj][m][qh][q], lq[q]); g[m][q] = gv;
	v_rcp_f32_e32 v197, v117
	s_nop 0
	v_fma_f32 v198, -v117, v197, 1.0
	v_fmac_f32_e32 v197, v198, v197
	v_div_scale_f32 v198, vcc, v206, v110, v206
	v_mul_f32_e32 v199, v198, v197
	v_fma_f32 v200, -v117, v199, v198
	v_fmac_f32_e32 v199, v200, v197
	v_fma_f32 v117, -v117, v199, v198
	v_div_fmas_f32 v117, v117, v197, v199
	v_div_fixup_f32 v110, v117, v110, v206
	v_add_f32_e32 v110, v72, v110
	v_cmp_gt_f32_e32 vcc, s37, v110
	s_nop 1
	v_cndmask_b32_e64 v117, 0, 32, vcc
	v_ldexp_f32 v110, v110, v117
	v_log_f32_e32 v110, v110
	s_nop 0
	v_mul_f32_e32 v117, 0x3f317217, v110
	v_fma_f32 v117, v110, s33, -v117
	v_fmac_f32_e32 v117, 0x3377d1cf, v110
	v_fmac_f32_e32 v117, 0x3f317217, v110
	v_cmp_lt_f32_e64 s[52:53], |v110|, s36
	s_nop 1
	v_cndmask_b32_e64 v110, v110, v117, s[52:53]
	v_cndmask_b32_e32 v117, 0, v216, vcc
	v_sub_f32_e32 v229, v110, v117
	s_nop 0
	s_nop 1
	s_nop 0
	s_nop 1
	v_mul_f32_e32 v110, 0xbfb8aa3b, v111
	v_exp_f32_e32 v110, v110
	s_nop 0
	v_add_f32_e32 v110, 1.0, v110
	v_div_scale_f32 v111, s[2:3], v110, v110, v205
	v_rcp_f32_e32 v198, v111
	s_nop 0
	v_fma_f32 v199, -v111, v198, 1.0
	v_fmac_f32_e32 v198, v199, v198
	v_div_scale_f32 v199, vcc, v205, v110, v205
	v_mul_f32_e32 v200, v199, v198
	v_fma_f32 v201, -v111, v200, v199
	v_fmac_f32_e32 v200, v201, v198
	v_fma_f32 v111, -v111, v200, v199
	v_div_fmas_f32 v111, v111, v198, v200
	v_div_fixup_f32 v110, v111, v110, v205
	v_add_f32_e32 v110, v73, v110
	v_cmp_gt_f32_e32 vcc, s37, v110
	s_nop 1
	v_cndmask_b32_e64 v111, 0, 32, vcc
	v_ldexp_f32 v110, v110, v111
	v_log_f32_e32 v110, v110
	s_nop 0
	v_mul_f32_e32 v111, 0x3f317217, v110
	v_fma_f32 v111, v110, s33, -v111
	v_fmac_f32_e32 v111, 0x3377d1cf, v110
	v_fmac_f32_e32 v111, 0x3f317217, v110
	v_cmp_lt_f32_e64 s[52:53], |v110|, s36
	s_nop 1
	v_cndmask_b32_e64 v110, v110, v111, s[52:53]
	v_cndmask_b32_e32 v111, 0, v216, vcc
	v_sub_f32_e32 v230, v110, v111
	v_mov_b32_e32 v117, v230
	s_nop 1
	v_mov_b32_dpp v197, v117 row_shr:1 row_mask:0xf bank_mask:0xf bound_ctrl:1
	s_nop 0
	s_nop 0
	s_nop 1
	v_mul_f32_e32 v111, 0xbfb8aa3b, v112
	v_exp_f32_e32 v111, v111
	s_nop 0
	v_add_f32_e32 v111, 1.0, v111
	v_div_scale_f32 v112, s[2:3], v111, v111, v204
	v_rcp_f32_e32 v199, v112
	s_nop 0
	v_fma_f32 v200, -v112, v199, 1.0
	v_fmac_f32_e32 v199, v200, v199
	v_div_scale_f32 v200, vcc, v204, v111, v204
	v_mul_f32_e32 v201, v200, v199
	v_fma_f32 v202, -v112, v201, v200
	v_fmac_f32_e32 v201, v202, v199
	v_fma_f32 v112, -v112, v201, v200
	v_div_fmas_f32 v112, v112, v199, v201
	v_div_fixup_f32 v111, v112, v111, v204
	v_add_f32_e32 v111, v74, v111
	v_cmp_gt_f32_e32 vcc, s37, v111
	s_nop 1
	v_cndmask_b32_e64 v112, 0, 32, vcc
	v_ldexp_f32 v111, v111, v112
	v_log_f32_e32 v111, v111
	s_nop 0
	v_mul_f32_e32 v112, 0x3f317217, v111
	v_fma_f32 v112, v111, s33, -v112
	v_fmac_f32_e32 v112, 0x3377d1cf, v111
	v_fmac_f32_e32 v112, 0x3f317217, v111
	v_cmp_lt_f32_e64 s[52:53], |v111|, s36
	s_nop 1
	v_cndmask_b32_e64 v111, v111, v112, s[52:53]
	v_cndmask_b32_e32 v112, 0, v216, vcc
	v_sub_f32_e32 v231, v111, v112
	s_nop 1
	s_nop 0
	s_nop 1
	v_mul_f32_e32 v112, 0xbfb8aa3b, v113
	v_exp_f32_e32 v112, v112
	s_nop 0
	v_add_f32_e32 v112, 1.0, v112
	v_div_scale_f32 v113, s[2:3], v112, v112, v96
	v_rcp_f32_e32 v200, v113
	v_mov_b32_e32 v110, v231
	v_fma_f32 v201, -v113, v200, 1.0
	v_fmac_f32_e32 v200, v201, v200
	v_div_scale_f32 v201, vcc, v96, v112, v96
	v_mul_f32_e32 v202, v201, v200
	v_fma_f32 v203, -v113, v202, v201
	v_fmac_f32_e32 v202, v203, v200
	v_fma_f32 v113, -v113, v202, v201
	v_div_fmas_f32 v113, v113, v200, v202
	v_div_fixup_f32 v112, v113, v112, v96
	v_add_f32_e32 v112, v75, v112
	v_cmp_gt_f32_e32 vcc, s37, v112
	v_mov_b32_dpp v198, v110 row_shr:1 row_mask:0xf bank_mask:0xf bound_ctrl:1
	s_nop 0
	v_cndmask_b32_e64 v113, 0, 32, vcc
	v_ldexp_f32 v112, v112, v113
	v_log_f32_e32 v112, v112
	s_nop 0
	v_mul_f32_e32 v113, 0x3f317217, v112
	v_fma_f32 v113, v112, s33, -v113
	v_fmac_f32_e32 v113, 0x3377d1cf, v112
	v_fmac_f32_e32 v113, 0x3f317217, v112
	v_cmp_lt_f32_e64 s[52:53], |v112|, s36
	s_nop 1
	v_cndmask_b32_e64 v112, v112, v113, s[52:53]
	v_cndmask_b32_e32 v113, 0, v216, vcc
	v_sub_f32_e32 v232, v112, v113
	v_mul_f32_e32 v106, 0xbfb8aa3b, v106
	v_exp_f32_e32 v106, v106
	v_mov_b32_e32 v111, v232
	v_add_f32_e32 v106, 1.0, v106
	s_nop 0
	v_mov_b32_dpp v199, v111 row_shr:1 row_mask:0xf bank_mask:0xf bound_ctrl:1
	v_pk_add_f32 v[198:199], v[110:111], v[198:199]
	s_nop 1
	v_div_scale_f32 v113, s[2:3], v106, v106, v206
	v_rcp_f32_e32 v201, v113
	s_nop 0
	v_fma_f32 v202, -v113, v201, 1.0
	v_fmac_f32_e32 v201, v202, v201
	v_div_scale_f32 v202, vcc, v206, v106, v206
	v_mul_f32_e32 v203, v202, v201
	v_fma_f32 v212, -v113, v203, v202
	v_fmac_f32_e32 v203, v212, v201
	v_fma_f32 v113, -v113, v203, v202
	v_div_fmas_f32 v113, v113, v201, v203
	v_div_fixup_f32 v106, v113, v106, v206
	v_add_f32_e32 v106, v72, v106
	v_cmp_gt_f32_e32 vcc, s37, v106
	s_nop 1
	v_cndmask_b32_e64 v113, 0, 32, vcc
	v_ldexp_f32 v106, v106, v113
	v_log_f32_e32 v106, v106
	s_nop 0
	v_mul_f32_e32 v113, 0x3f317217, v106
	v_fma_f32 v113, v106, s33, -v113
	v_fmac_f32_e32 v113, 0x3377d1cf, v106
	v_fmac_f32_e32 v113, 0x3f317217, v106
	v_cmp_lt_f32_e64 s[52:53], |v106|, s36
	s_nop 1
	v_cndmask_b32_e64 v106, v106, v113, s[52:53]
	v_cndmask_b32_e32 v113, 0, v216, vcc
	v_sub_f32_e32 v233, v106, v113
	s_nop 0
	s_nop 1
	s_nop 0
	s_nop 1
	v_mul_f32_e32 v106, 0xbfb8aa3b, v107
	v_exp_f32_e32 v106, v106
	s_nop 0
	v_add_f32_e32 v106, 1.0, v106
	v_div_scale_f32 v107, s[2:3], v106, v106, v205
	v_rcp_f32_e32 v202, v107
	s_nop 0
	v_fma_f32 v203, -v107, v202, 1.0
	v_fmac_f32_e32 v202, v203, v202
	v_div_scale_f32 v203, vcc, v205, v106, v205
; template <int CTRL> __device__ __forceinline__ float dppx(float v) { return __int_as_float(__builtin_amdgcn_update_dpp(0, __float_as_int(v), CTRL, 0xf, 0xf, true)); }
; __device__ __forceinline__ unsigned cvt_pk_bf16(float lo, float hi) { unsigned r; asm volatile("v_cvt_pk_bf16_f32 %0, %1, %2" : "=v"(r) : "v"(lo), "v"(hi)); return r; }
; __device__ __forceinline__ float log_forget(float z, float lb) {
;   const float r0 = fminf(z, 0.f) - __logf(1.f + __expf(-fabsf(z)));
;   const float r1 = __logf(lb + (1.f - lb) / (1.f + __expf(-z)));
;   return lb <= 0.f ? r0 : r1;
; }
;   __device__ __forceinline__ void operator()(const f32x4 (&acc)[2][2][4][2], const pg8::Unit& u, int wr, int wc, int fr, int fq) const {
;     ...
;             for (int m = 0; m < 4; ++m)
; #pragma unroll
;               for (int q = 0; q < 4; ++q) { const float gv = log_forget(acc[ai][bj][m][qh][q], lq[q]); g[m][q] = gv;
;                 float sc = gv; sc += dppx<0x111>(sc); sc += dppx<0x112>(sc); sc += dppx<0x114>(sc); sc += dppx<0x118>(sc);
;                 const float tot16 = __int_as_float(__builtin_amdgcn_ds_swizzle(__float_as_int(sc), 0x1F0));
;                 cs[m][q] = sc + carry[q]; carry[q] += tot16; }
; #pragma unroll
;             for (int m = 0; m < 4; ++m) { const int r = row0 + ai * 128 + m * 16; float bq[4], kq[4];
; #pragma unroll
;               for (int q = 0; q < 4; ++q) { bq[q] = bwd ? (carry[q] - cs[m][q]) + g[m][q] : cs[m][q]; kq[q] = 1.f - __expf(g[m][q]); }
;               *(f32x4*)(logfp + (size_t)r * 1024 + c + 4 * qh) = (f32x4){bq[0], bq[1], bq[2], bq[3]};
;               u32x2 w; w.x = pg8::cvt_pk_bf16(kq[0], kq[1]); w.y = pg8::cvt_pk_bf16(kq[2], kq[3]);
;               *(u32x2*)(km + (size_t)r * 1024 + c + 4 * qh) = w; } } }
	v_mul_f32_e32 v212, v203, v202
	v_fma_f32 v213, -v107, v212, v203
	v_fmac_f32_e32 v212, v213, v202
	v_fma_f32 v107, -v107, v212, v203
	v_div_fmas_f32 v107, v107, v202, v212
	v_div_fixup_f32 v106, v107, v106, v205
	v_add_f32_e32 v106, v73, v106
	v_cmp_gt_f32_e32 vcc, s37, v106
	s_nop 1
	v_cndmask_b32_e64 v107, 0, 32, vcc
	v_ldexp_f32 v106, v106, v107
	v_log_f32_e32 v106, v106
	s_nop 0
	v_mul_f32_e32 v107, 0x3f317217, v106
	v_fma_f32 v107, v106, s33, -v107
	v_fmac_f32_e32 v107, 0x3377d1cf, v106
	v_fmac_f32_e32 v107, 0x3f317217, v106
	v_cmp_lt_f32_e64 s[52:53], |v106|, s36
	s_nop 1
	v_cndmask_b32_e64 v106, v106, v107, s[52:53]
	v_cndmask_b32_e32 v107, 0, v216, vcc
	v_sub_f32_e32 v234, v106, v107
	v_mov_b32_e32 v113, v234
	s_nop 1
	v_mov_b32_dpp v201, v113 row_shr:1 row_mask:0xf bank_mask:0xf bound_ctrl:1
	s_nop 0
	s_nop 0
	s_nop 1
	v_mul_f32_e32 v107, 0xbfb8aa3b, v108
	v_exp_f32_e32 v107, v107
	s_nop 0
	v_add_f32_e32 v107, 1.0, v107
	v_div_scale_f32 v108, s[2:3], v107, v107, v204
	v_rcp_f32_e32 v203, v108
	s_nop 0
	v_fma_f32 v212, -v108, v203, 1.0
	v_fmac_f32_e32 v203, v212, v203
	v_div_scale_f32 v212, vcc, v204, v107, v204
	v_mul_f32_e32 v213, v212, v203
	v_fma_f32 v214, -v108, v213, v212
	v_fmac_f32_e32 v213, v214, v203
	v_fma_f32 v108, -v108, v213, v212
	v_div_fmas_f32 v108, v108, v203, v213
	v_div_fixup_f32 v107, v108, v107, v204
	v_add_f32_e32 v107, v74, v107
	v_cmp_gt_f32_e32 vcc, s37, v107
	s_nop 1
	v_cndmask_b32_e64 v108, 0, 32, vcc
	v_ldexp_f32 v107, v107, v108
	v_log_f32_e32 v107, v107
	s_nop 0
	v_mul_f32_e32 v108, 0x3f317217, v107
	v_fma_f32 v108, v107, s33, -v108
	v_fmac_f32_e32 v108, 0x3377d1cf, v107
	v_fmac_f32_e32 v108, 0x3f317217, v107
	v_cmp_lt_f32_e64 s[52:53], |v107|, s36
	s_nop 1
	v_cndmask_b32_e64 v107, v107, v108, s[52:53]
	v_cndmask_b32_e32 v108, 0, v216, vcc
	v_sub_f32_e32 v235, v107, v108
	s_nop 1
	s_nop 0
	s_nop 1
	v_mul_f32_e32 v108, 0xbfb8aa3b, v109
	v_exp_f32_e32 v108, v108
	s_nop 0
	v_add_f32_e32 v108, 1.0, v108
	v_div_scale_f32 v109, s[2:3], v108, v108, v96
	v_rcp_f32_e32 v212, v109
	v_mov_b32_e32 v202, v235
	v_fma_f32 v213, -v109, v212, 1.0
	v_fmac_f32_e32 v212, v213, v212
	v_div_scale_f32 v213, vcc, v96, v108, v96
	v_mul_f32_e32 v214, v213, v212
	v_fma_f32 v215, -v109, v214, v213
	v_fmac_f32_e32 v214, v215, v212
	v_fma_f32 v109, -v109, v214, v213
	v_div_fmas_f32 v109, v109, v212, v214
	v_div_fixup_f32 v108, v109, v108, v96
	v_add_f32_e32 v108, v75, v108
	v_cmp_gt_f32_e32 vcc, s37, v108
	v_mov_b32_dpp v106, v202 row_shr:1 row_mask:0xf bank_mask:0xf bound_ctrl:1
	s_nop 0
	v_cndmask_b32_e64 v109, 0, 32, vcc
	v_ldexp_f32 v108, v108, v109
	v_log_f32_e32 v108, v108
	s_nop 0
	v_mul_f32_e32 v109, 0x3f317217, v108
	v_fma_f32 v109, v108, s33, -v109
	v_fmac_f32_e32 v109, 0x3377d1cf, v108
	v_fmac_f32_e32 v109, 0x3f317217, v108
	v_cmp_lt_f32_e64 s[52:53], |v108|, s36
	s_nop 1
	v_cndmask_b32_e64 v108, v108, v109, s[52:53]
	v_cndmask_b32_e32 v109, 0, v216, vcc
	v_sub_f32_e32 v214, v108, v109
	v_mov_b32_e32 v109, v208
	v_mov_b32_e32 v203, v214
	v_mov_b32_e32 v108, v207
	v_mov_b32_dpp v187, v109 row_shr:1 row_mask:0xf bank_mask:0xf bound_ctrl:1
	v_mov_b32_e32 v120, v211
	v_mov_b32_dpp v186, v108 row_shr:1 row_mask:0xf bank_mask:0xf bound_ctrl:1
	v_pk_add_f32 v[186:187], v[108:109], v[186:187]
	v_mov_b32_e32 v116, v229
	v_mov_b32_e32 v112, v233
	v_mov_b32_dpp v188, v186 row_shr:2 row_mask:0xf bank_mask:0xf bound_ctrl:1
	v_mov_b32_dpp v189, v187 row_shr:2 row_mask:0xf bank_mask:0xf bound_ctrl:1
	v_pk_add_f32 v[186:187], v[186:187], v[188:189]
	v_mov_b32_dpp v196, v116 row_shr:1 row_mask:0xf bank_mask:0xf bound_ctrl:1
	v_pk_add_f32 v[196:197], v[116:117], v[196:197]
	v_mov_b32_dpp v188, v186 row_shr:4 row_mask:0xf bank_mask:0xf bound_ctrl:1
	v_mov_b32_dpp v189, v187 row_shr:4 row_mask:0xf bank_mask:0xf bound_ctrl:1
	v_pk_add_f32 v[186:187], v[186:187], v[188:189]
	v_mov_b32_dpp v200, v112 row_shr:1 row_mask:0xf bank_mask:0xf bound_ctrl:1
	v_pk_add_f32 v[200:201], v[112:113], v[200:201]
	v_mov_b32_dpp v188, v186 row_shr:8 row_mask:0xf bank_mask:0xf bound_ctrl:1
	v_mov_b32_dpp v189, v187 row_shr:8 row_mask:0xf bank_mask:0xf bound_ctrl:1
	v_pk_add_f32 v[186:187], v[186:187], v[188:189]
	ds_swizzle_b32 v188, v186 offset:swizzle(BROADCAST,16,15)
	ds_swizzle_b32 v189, v187 offset:swizzle(BROADCAST,16,15)
	v_mov_b32_dpp v107, v203 row_shr:1 row_mask:0xf bank_mask:0xf bound_ctrl:1
	v_pk_add_f32 v[106:107], v[202:203], v[106:107]
	v_pk_add_f32 v[186:187], v[186:187], 0 op_sel_hi:[1,0]
	s_waitcnt lgkmcnt(0)
	v_pk_add_f32 v[212:213], v[188:189], 0 op_sel_hi:[1,0]
	v_mul_f32_e32 v188, 0x3fb8aa3b, v108
	v_exp_f32_e32 v188, v188
	v_mov_b32_dpp v189, v119 row_shr:1 row_mask:0xf bank_mask:0xf bound_ctrl:1
	v_sub_f32_e32 v207, 1.0, v188
	v_mul_f32_e32 v188, 0x3fb8aa3b, v109
	v_exp_f32_e32 v188, v188
	s_nop 0
	v_sub_f32_e32 v215, 1.0, v188
	v_mov_b32_dpp v188, v118 row_shr:1 row_mask:0xf bank_mask:0xf bound_ctrl:1
	v_pk_add_f32 v[188:189], v[118:119], v[188:189]
	s_nop 1
	v_mov_b32_dpp v190, v188 row_shr:2 row_mask:0xf bank_mask:0xf bound_ctrl:1
	v_mov_b32_dpp v191, v189 row_shr:2 row_mask:0xf bank_mask:0xf bound_ctrl:1
	v_pk_add_f32 v[188:189], v[188:189], v[190:191]
	s_nop 1
	v_mov_b32_dpp v190, v188 row_shr:4 row_mask:0xf bank_mask:0xf bound_ctrl:1
	v_mov_b32_dpp v191, v189 row_shr:4 row_mask:0xf bank_mask:0xf bound_ctrl:1
	v_pk_add_f32 v[188:189], v[188:189], v[190:191]
	s_nop 1
	v_mov_b32_dpp v190, v188 row_shr:8 row_mask:0xf bank_mask:0xf bound_ctrl:1
	v_mov_b32_dpp v191, v189 row_shr:8 row_mask:0xf bank_mask:0xf bound_ctrl:1
	v_pk_add_f32 v[188:189], v[188:189], v[190:191]
	ds_swizzle_b32 v190, v188 offset:swizzle(BROADCAST,16,15)
	ds_swizzle_b32 v191, v189 offset:swizzle(BROADCAST,16,15)
	v_pk_add_f32 v[188:189], v[188:189], 0 op_sel_hi:[1,0]
	s_waitcnt lgkmcnt(0)
; template <int CTRL> __device__ __forceinline__ float dppx(float v) { return __int_as_float(__builtin_amdgcn_update_dpp(0, __float_as_int(v), CTRL, 0xf, 0xf, true)); }
;   __device__ __forceinline__ void operator()(const f32x4 (&acc)[2][2][4][2], const pg8::Unit& u, int wr, int wc, int fr, int fq) const {
;     ...
;             for (int m = 0; m < 4; ++m)
; #pragma unroll
;               for (int q = 0; q < 4; ++q) { const float gv = log_forget(acc[ai][bj][m][qh][q], lq[q]); g[m][q] = gv;
;                 float sc = gv; sc += dppx<0x111>(sc); sc += dppx<0x112>(sc); sc += dppx<0x114>(sc); sc += dppx<0x118>(sc);
;                 const float tot16 = __int_as_float(__builtin_amdgcn_ds_swizzle(__float_as_int(sc), 0x1F0));
;                 cs[m][q] = sc + carry[q]; carry[q] += tot16; }
;     ...
;               for (int q = 0; q < 4; ++q) { bq[q] = bwd ? (carry[q] - cs[m][q]) + g[m][q] : cs[m][q]; kq[q] = 1.f - __expf(g[m][q]); }
	v_pk_add_f32 v[208:209], v[190:191], 0 op_sel_hi:[1,0]
	v_mul_f32_e32 v190, 0x3fb8aa3b, v118
	v_exp_f32_e32 v190, v190
	v_mov_b32_dpp v191, v121 row_shr:1 row_mask:0xf bank_mask:0xf bound_ctrl:1
	v_sub_f32_e32 v236, 1.0, v190
	v_mul_f32_e32 v190, 0x3fb8aa3b, v119
	v_exp_f32_e32 v190, v190
	s_nop 0
	v_sub_f32_e32 v237, 1.0, v190
	v_mov_b32_dpp v190, v120 row_shr:1 row_mask:0xf bank_mask:0xf bound_ctrl:1
	v_pk_add_f32 v[190:191], v[120:121], v[190:191]
	s_nop 1
	v_mov_b32_dpp v192, v190 row_shr:2 row_mask:0xf bank_mask:0xf bound_ctrl:1
	v_mov_b32_dpp v193, v191 row_shr:2 row_mask:0xf bank_mask:0xf bound_ctrl:1
	v_pk_add_f32 v[190:191], v[190:191], v[192:193]
	s_nop 1
	v_mov_b32_dpp v192, v190 row_shr:4 row_mask:0xf bank_mask:0xf bound_ctrl:1
	v_mov_b32_dpp v193, v191 row_shr:4 row_mask:0xf bank_mask:0xf bound_ctrl:1
	v_pk_add_f32 v[190:191], v[190:191], v[192:193]
	s_nop 1
	v_mov_b32_dpp v192, v190 row_shr:8 row_mask:0xf bank_mask:0xf bound_ctrl:1
	v_mov_b32_dpp v193, v191 row_shr:8 row_mask:0xf bank_mask:0xf bound_ctrl:1
	v_pk_add_f32 v[190:191], v[190:191], v[192:193]
	ds_swizzle_b32 v192, v190 offset:swizzle(BROADCAST,16,15)
	ds_swizzle_b32 v193, v191 offset:swizzle(BROADCAST,16,15)
	v_pk_add_f32 v[190:191], v[212:213], v[190:191]
	s_waitcnt lgkmcnt(0)
	v_pk_add_f32 v[210:211], v[212:213], v[192:193]
	v_mul_f32_e32 v192, 0x3fb8aa3b, v120
	v_exp_f32_e32 v192, v192
	v_mov_b32_dpp v193, v115 row_shr:1 row_mask:0xf bank_mask:0xf bound_ctrl:1
	v_sub_f32_e32 v226, 1.0, v192
	v_mul_f32_e32 v192, 0x3fb8aa3b, v121
	v_exp_f32_e32 v192, v192
	s_nop 0
	v_sub_f32_e32 v238, 1.0, v192
	v_mov_b32_dpp v192, v114 row_shr:1 row_mask:0xf bank_mask:0xf bound_ctrl:1
	v_pk_add_f32 v[192:193], v[114:115], v[192:193]
	s_nop 1
	v_mov_b32_dpp v194, v192 row_shr:2 row_mask:0xf bank_mask:0xf bound_ctrl:1
	v_mov_b32_dpp v195, v193 row_shr:2 row_mask:0xf bank_mask:0xf bound_ctrl:1
	v_pk_add_f32 v[192:193], v[192:193], v[194:195]
	s_nop 1
	v_mov_b32_dpp v194, v192 row_shr:4 row_mask:0xf bank_mask:0xf bound_ctrl:1
	v_mov_b32_dpp v195, v193 row_shr:4 row_mask:0xf bank_mask:0xf bound_ctrl:1
	v_pk_add_f32 v[192:193], v[192:193], v[194:195]
	s_nop 1
	v_mov_b32_dpp v194, v192 row_shr:8 row_mask:0xf bank_mask:0xf bound_ctrl:1
	v_mov_b32_dpp v195, v193 row_shr:8 row_mask:0xf bank_mask:0xf bound_ctrl:1
	v_pk_add_f32 v[192:193], v[192:193], v[194:195]
	ds_swizzle_b32 v194, v192 offset:swizzle(BROADCAST,16,15)
	ds_swizzle_b32 v195, v193 offset:swizzle(BROADCAST,16,15)
	v_pk_add_f32 v[192:193], v[208:209], v[192:193]
	s_waitcnt lgkmcnt(0)
	v_pk_add_f32 v[194:195], v[208:209], v[194:195]
	v_mul_f32_e32 v208, 0x3fb8aa3b, v114
	v_exp_f32_e32 v208, v208
	v_mov_b32_dpp v209, v197 row_shr:2 row_mask:0xf bank_mask:0xf bound_ctrl:1
	v_sub_f32_e32 v227, 1.0, v208
	v_mul_f32_e32 v208, 0x3fb8aa3b, v115
	v_exp_f32_e32 v208, v208
	s_nop 0
	v_sub_f32_e32 v228, 1.0, v208
	v_mov_b32_dpp v208, v196 row_shr:2 row_mask:0xf bank_mask:0xf bound_ctrl:1
	v_pk_add_f32 v[196:197], v[196:197], v[208:209]
	s_nop 1
	v_mov_b32_dpp v208, v196 row_shr:4 row_mask:0xf bank_mask:0xf bound_ctrl:1
	v_mov_b32_dpp v209, v197 row_shr:4 row_mask:0xf bank_mask:0xf bound_ctrl:1
	v_pk_add_f32 v[196:197], v[196:197], v[208:209]
	s_nop 1
	v_mov_b32_dpp v208, v196 row_shr:8 row_mask:0xf bank_mask:0xf bound_ctrl:1
	v_mov_b32_dpp v209, v197 row_shr:8 row_mask:0xf bank_mask:0xf bound_ctrl:1
	v_pk_add_f32 v[196:197], v[196:197], v[208:209]
	ds_swizzle_b32 v208, v196 offset:swizzle(BROADCAST,16,15)
	ds_swizzle_b32 v209, v197 offset:swizzle(BROADCAST,16,15)
	v_pk_add_f32 v[196:197], v[210:211], v[196:197]
	s_waitcnt lgkmcnt(0)
	v_pk_add_f32 v[208:209], v[210:211], v[208:209]
	v_mul_f32_e32 v210, 0x3fb8aa3b, v116
	v_exp_f32_e32 v210, v210
	v_mov_b32_dpp v211, v199 row_shr:2 row_mask:0xf bank_mask:0xf bound_ctrl:1
	v_sub_f32_e32 v229, 1.0, v210
	v_mul_f32_e32 v210, 0x3fb8aa3b, v117
	v_exp_f32_e32 v210, v210
	s_nop 0
	v_sub_f32_e32 v230, 1.0, v210
	v_mov_b32_dpp v210, v198 row_shr:2 row_mask:0xf bank_mask:0xf bound_ctrl:1
	v_pk_add_f32 v[198:199], v[198:199], v[210:211]
	s_nop 1
	v_mov_b32_dpp v210, v198 row_shr:4 row_mask:0xf bank_mask:0xf bound_ctrl:1
	v_mov_b32_dpp v211, v199 row_shr:4 row_mask:0xf bank_mask:0xf bound_ctrl:1
	v_pk_add_f32 v[198:199], v[198:199], v[210:211]
	s_nop 1
	v_mov_b32_dpp v210, v198 row_shr:8 row_mask:0xf bank_mask:0xf bound_ctrl:1
	v_mov_b32_dpp v211, v199 row_shr:8 row_mask:0xf bank_mask:0xf bound_ctrl:1
	v_pk_add_f32 v[198:199], v[198:199], v[210:211]
	ds_swizzle_b32 v210, v198 offset:swizzle(BROADCAST,16,15)
	ds_swizzle_b32 v211, v199 offset:swizzle(BROADCAST,16,15)
	v_pk_add_f32 v[198:199], v[194:195], v[198:199]
	s_waitcnt lgkmcnt(0)
	v_pk_add_f32 v[194:195], v[194:195], v[210:211]
	v_mul_f32_e32 v210, 0x3fb8aa3b, v110
	v_exp_f32_e32 v210, v210
	v_mov_b32_dpp v211, v201 row_shr:2 row_mask:0xf bank_mask:0xf bound_ctrl:1
	v_sub_f32_e32 v231, 1.0, v210
	v_mul_f32_e32 v210, 0x3fb8aa3b, v111
	v_exp_f32_e32 v210, v210
	s_nop 0
	v_sub_f32_e32 v232, 1.0, v210
	v_mov_b32_dpp v210, v200 row_shr:2 row_mask:0xf bank_mask:0xf bound_ctrl:1
	v_pk_add_f32 v[200:201], v[200:201], v[210:211]
	s_nop 1
	v_mov_b32_dpp v210, v200 row_shr:4 row_mask:0xf bank_mask:0xf bound_ctrl:1
	v_mov_b32_dpp v211, v201 row_shr:4 row_mask:0xf bank_mask:0xf bound_ctrl:1
	v_pk_add_f32 v[200:201], v[200:201], v[210:211]
	s_nop 1
	v_mov_b32_dpp v210, v200 row_shr:8 row_mask:0xf bank_mask:0xf bound_ctrl:1
	v_mov_b32_dpp v211, v201 row_shr:8 row_mask:0xf bank_mask:0xf bound_ctrl:1
	v_pk_add_f32 v[200:201], v[200:201], v[210:211]
	ds_swizzle_b32 v210, v200 offset:swizzle(BROADCAST,16,15)
	ds_swizzle_b32 v211, v201 offset:swizzle(BROADCAST,16,15)
	v_pk_add_f32 v[200:201], v[208:209], v[200:201]
	s_waitcnt lgkmcnt(0)
; __device__ __forceinline__ unsigned cvt_pk_bf16(float lo, float hi) { unsigned r; asm volatile("v_cvt_pk_bf16_f32 %0, %1, %2" : "=v"(r) : "v"(lo), "v"(hi)); return r; }
; __device__ __forceinline__ float log_forget(float z, float lb) {
;   const float r0 = fminf(z, 0.f) - __logf(1.f + __expf(-fabsf(z)));
;   const float r1 = __logf(lb + (1.f - lb) / (1.f + __expf(-z)));
;   return lb <= 0.f ? r0 : r1;
; }
;   __device__ __forceinline__ void operator()(const f32x4 (&acc)[2][2][4][2], const pg8::Unit& u, int wr, int wc, int fr, int fq) const {
;     ...
;             for (int m = 0; m < 4; ++m) { const int r = row0 + ai * 128 + m * 16; float bq[4], kq[4];
; #pragma unroll
;               for (int q = 0; q < 4; ++q) { bq[q] = bwd ? (carry[q] - cs[m][q]) + g[m][q] : cs[m][q]; kq[q] = 1.f - __expf(g[m][q]); }
;               *(f32x4*)(logfp + (size_t)r * 1024 + c + 4 * qh) = (f32x4){bq[0], bq[1], bq[2], bq[3]};
;               u32x2 w; w.x = pg8::cvt_pk_bf16(kq[0], kq[1]); w.y = pg8::cvt_pk_bf16(kq[2], kq[3]);
;               *(u32x2*)(km + (size_t)r * 1024 + c + 4 * qh) = w; } } }
	v_pk_add_f32 v[208:209], v[208:209], v[210:211]
	v_mul_f32_e32 v210, 0x3fb8aa3b, v112
	v_exp_f32_e32 v210, v210
	v_mov_b32_dpp v211, v107 row_shr:2 row_mask:0xf bank_mask:0xf bound_ctrl:1
	v_sub_f32_e32 v233, 1.0, v210
	v_mul_f32_e32 v210, 0x3fb8aa3b, v113
	v_exp_f32_e32 v210, v210
	s_nop 0
	v_sub_f32_e32 v234, 1.0, v210
	v_mov_b32_dpp v210, v106 row_shr:2 row_mask:0xf bank_mask:0xf bound_ctrl:1
	v_pk_add_f32 v[106:107], v[106:107], v[210:211]
	s_nop 1
	v_mov_b32_dpp v210, v106 row_shr:4 row_mask:0xf bank_mask:0xf bound_ctrl:1
	v_mov_b32_dpp v211, v107 row_shr:4 row_mask:0xf bank_mask:0xf bound_ctrl:1
	v_pk_add_f32 v[106:107], v[106:107], v[210:211]
	s_nop 1
	v_mov_b32_dpp v210, v106 row_shr:8 row_mask:0xf bank_mask:0xf bound_ctrl:1
	v_mov_b32_dpp v211, v107 row_shr:8 row_mask:0xf bank_mask:0xf bound_ctrl:1
	v_pk_add_f32 v[106:107], v[106:107], v[210:211]
	ds_swizzle_b32 v210, v106 offset:swizzle(BROADCAST,16,15)
	ds_swizzle_b32 v211, v107 offset:swizzle(BROADCAST,16,15)
	v_pk_add_f32 v[212:213], v[194:195], v[106:107]
	v_pk_add_f32 v[106:107], v[208:209], v[186:187] neg_lo:[0,1] neg_hi:[0,1]
	s_waitcnt lgkmcnt(0)
	v_pk_add_f32 v[194:195], v[194:195], v[210:211]
	s_nop 0
	v_pk_add_f32 v[210:211], v[194:195], v[188:189] neg_lo:[0,1] neg_hi:[0,1]
	v_pk_add_f32 v[106:107], v[108:109], v[106:107]
	v_pk_add_f32 v[108:109], v[118:119], v[210:211]
	v_cndmask_b32_e64 v107, v187, v107, s[42:43]
	v_cndmask_b32_e64 v109, v189, v109, s[42:43]
	v_cndmask_b32_e64 v108, v188, v108, s[42:43]
	v_cndmask_b32_e64 v106, v186, v106, s[42:43]
	global_store_dwordx4 v[176:177], v[106:109], off offset:16
	s_nop 1
	v_cvt_pk_bf16_f32 v106, v207, v215
	v_cvt_pk_bf16_f32 v107, v236, v237
	global_store_dwordx2 v[174:175], v[106:107], off offset:8
	v_pk_add_f32 v[106:107], v[208:209], v[190:191] neg_lo:[0,1] neg_hi:[0,1]
	v_pk_add_f32 v[108:109], v[194:195], v[192:193] neg_lo:[0,1] neg_hi:[0,1]
	v_pk_add_f32 v[106:107], v[120:121], v[106:107]
	v_pk_add_f32 v[108:109], v[114:115], v[108:109]
	v_cndmask_b32_e64 v107, v191, v107, s[42:43]
	v_cndmask_b32_e64 v109, v193, v109, s[42:43]
	v_cndmask_b32_e64 v108, v192, v108, s[42:43]
	v_cndmask_b32_e64 v106, v190, v106, s[42:43]
	global_store_dwordx4 v[180:181], v[106:109], off offset:16
	s_nop 1
	v_cvt_pk_bf16_f32 v106, v226, v238
	v_cvt_pk_bf16_f32 v107, v227, v228
	global_store_dwordx2 v[172:173], v[106:107], off offset:8
	v_pk_add_f32 v[106:107], v[208:209], v[196:197] neg_lo:[0,1] neg_hi:[0,1]
	v_pk_add_f32 v[108:109], v[194:195], v[198:199] neg_lo:[0,1] neg_hi:[0,1]
	v_pk_add_f32 v[106:107], v[116:117], v[106:107]
	v_pk_add_f32 v[108:109], v[110:111], v[108:109]
	v_cndmask_b32_e64 v107, v197, v107, s[42:43]
	v_cndmask_b32_e64 v109, v199, v109, s[42:43]
	v_cndmask_b32_e64 v108, v198, v108, s[42:43]
	v_cndmask_b32_e64 v106, v196, v106, s[42:43]
	global_store_dwordx4 v[182:183], v[106:109], off offset:16
	v_mul_f32_e32 v111, 0x3fb8aa3b, v203
	v_exp_f32_e32 v111, v111
	v_cvt_pk_bf16_f32 v106, v229, v230
	v_cvt_pk_bf16_f32 v107, v231, v232
	global_store_dwordx2 v[170:171], v[106:107], off offset:8
	v_mul_f32_e32 v106, 0x3fb8aa3b, v202
	v_exp_f32_e32 v106, v106
	v_pk_add_f32 v[108:109], v[194:195], v[212:213] neg_lo:[0,1] neg_hi:[0,1]
	v_sub_f32_e32 v111, 1.0, v111
	v_pk_add_f32 v[108:109], v[202:203], v[108:109]
	v_sub_f32_e32 v110, 1.0, v106
	v_pk_add_f32 v[106:107], v[208:209], v[200:201] neg_lo:[0,1] neg_hi:[0,1]
	v_cndmask_b32_e64 v109, v213, v109, s[42:43]
	v_pk_add_f32 v[106:107], v[112:113], v[106:107]
	v_cndmask_b32_e64 v108, v212, v108, s[42:43]
	v_cndmask_b32_e64 v107, v201, v107, s[42:43]
	v_cndmask_b32_e64 v106, v200, v106, s[42:43]
	global_store_dwordx4 v[184:185], v[106:109], off offset:16
	s_nop 1
	v_cvt_pk_bf16_f32 v106, v233, v234
	v_cvt_pk_bf16_f32 v107, v110, v111
	global_store_dwordx2 v[168:169], v[106:107], off offset:8
	v_mul_f32_e32 v102, 0xbfb8aa3b, v102
	v_exp_f32_e32 v102, v102
	s_nop 0
	v_add_f32_e32 v102, 1.0, v102
	s_nop 0
	s_nop 1
	v_div_scale_f32 v107, s[2:3], v102, v102, v157
	v_rcp_f32_e32 v109, v107
	s_nop 0
	v_fma_f32 v110, -v107, v109, 1.0
	v_fmac_f32_e32 v109, v110, v109
	v_div_scale_f32 v110, vcc, v157, v102, v157
	v_mul_f32_e32 v111, v110, v109
	v_fma_f32 v112, -v107, v111, v110
	v_fmac_f32_e32 v111, v112, v109
	v_fma_f32 v107, -v107, v111, v110
	v_div_fmas_f32 v107, v107, v109, v111
	v_div_fixup_f32 v102, v107, v102, v157
	v_add_f32_e32 v102, v92, v102
	v_cmp_gt_f32_e32 vcc, s37, v102
	s_nop 1
	v_cndmask_b32_e64 v107, 0, 32, vcc
	v_ldexp_f32 v102, v102, v107
	v_log_f32_e32 v102, v102
	s_nop 0
	v_mul_f32_e32 v107, 0x3f317217, v102
	v_fma_f32 v107, v102, s33, -v107
	v_fmac_f32_e32 v107, 0x3377d1cf, v102
	v_fmac_f32_e32 v107, 0x3f317217, v102
	v_cmp_lt_f32_e64 s[60:61], |v102|, s36
	s_nop 1
	v_cndmask_b32_e64 v102, v102, v107, s[60:61]
	v_cndmask_b32_e32 v107, 0, v216, vcc
	v_sub_f32_e32 v180, v102, v107
	s_nop 0
	s_nop 1
	s_nop 0
	s_nop 1
	v_mul_f32_e32 v102, 0xbfb8aa3b, v103
	v_exp_f32_e32 v102, v102
	s_nop 0
	v_add_f32_e32 v102, 1.0, v102
	v_div_scale_f32 v103, s[2:3], v102, v102, v159
	v_rcp_f32_e32 v110, v103
	s_nop 0
	v_fma_f32 v111, -v103, v110, 1.0
	v_fmac_f32_e32 v110, v111, v110
	v_div_scale_f32 v111, vcc, v159, v102, v159
	v_mul_f32_e32 v112, v111, v110
	v_fma_f32 v113, -v103, v112, v111
	v_fmac_f32_e32 v112, v113, v110
	v_fma_f32 v103, -v103, v112, v111
	v_div_fmas_f32 v103, v103, v110, v112
	v_div_fixup_f32 v102, v103, v102, v159
	v_add_f32_e32 v102, v93, v102
	v_cmp_gt_f32_e32 vcc, s37, v102
	s_nop 1
	v_cndmask_b32_e64 v103, 0, 32, vcc
	v_ldexp_f32 v102, v102, v103
	v_log_f32_e32 v102, v102
	s_nop 0
	v_mul_f32_e32 v103, 0x3f317217, v102
	v_fma_f32 v103, v102, s33, -v103
; __device__ __forceinline__ float log_forget(float z, float lb) {
;   const float r0 = fminf(z, 0.f) - __logf(1.f + __expf(-fabsf(z)));
;   const float r1 = __logf(lb + (1.f - lb) / (1.f + __expf(-z)));
;   return lb <= 0.f ? r0 : r1;
; }
;   __device__ __forceinline__ void operator()(const f32x4 (&acc)[2][2][4][2], const pg8::Unit& u, int wr, int wc, int fr, int fq) const {
;     ...
;             for (int m = 0; m < 4; ++m)
; #pragma unroll
;               for (int q = 0; q < 4; ++q) { const float gv = log_forget(acc[ai][bj][m][qh][q], lq[q]); g[m][q] = gv;
	v_fmac_f32_e32 v103, 0x3377d1cf, v102
	v_fmac_f32_e32 v103, 0x3f317217, v102
	v_cmp_lt_f32_e64 s[60:61], |v102|, s36
	s_nop 1
	v_cndmask_b32_e64 v102, v102, v103, s[60:61]
	v_cndmask_b32_e32 v103, 0, v216, vcc
	v_sub_f32_e32 v181, v102, v103
	s_nop 1
	s_nop 0
	s_nop 1
	v_mul_f32_e32 v103, 0xbfb8aa3b, v104
	v_exp_f32_e32 v103, v103
	s_nop 0
	v_add_f32_e32 v103, 1.0, v103
	v_div_scale_f32 v104, s[2:3], v103, v103, v161
	v_rcp_f32_e32 v111, v104
	s_nop 0
	v_fma_f32 v112, -v104, v111, 1.0
	v_fmac_f32_e32 v111, v112, v111
	v_div_scale_f32 v112, vcc, v161, v103, v161
	v_mul_f32_e32 v113, v112, v111
	v_fma_f32 v114, -v104, v113, v112
	v_fmac_f32_e32 v113, v114, v111
	v_fma_f32 v104, -v104, v113, v112
	v_div_fmas_f32 v104, v104, v111, v113
	v_div_fixup_f32 v103, v104, v103, v161
	v_add_f32_e32 v103, v94, v103
	v_cmp_gt_f32_e32 vcc, s37, v103
	s_nop 1
	v_cndmask_b32_e64 v104, 0, 32, vcc
	v_ldexp_f32 v103, v103, v104
	v_log_f32_e32 v103, v103
	s_nop 0
	v_mul_f32_e32 v104, 0x3f317217, v103
	v_fma_f32 v104, v103, s33, -v104
	v_fmac_f32_e32 v104, 0x3377d1cf, v103
	v_fmac_f32_e32 v104, 0x3f317217, v103
	v_cmp_lt_f32_e64 s[60:61], |v103|, s36
	s_nop 1
	v_cndmask_b32_e64 v103, v103, v104, s[60:61]
	v_cndmask_b32_e32 v104, 0, v216, vcc
	v_sub_f32_e32 v104, v103, v104
	v_mul_f32_e32 v105, 0xbfb8aa3b, v105
	v_exp_f32_e32 v105, v105
	s_nop 0
	v_add_f32_e32 v105, 1.0, v105
	s_nop 0
	v_div_scale_f32 v112, s[2:3], v105, v105, v163
	v_rcp_f32_e32 v113, v112
	s_nop 0
	v_fma_f32 v114, -v112, v113, 1.0
	v_fmac_f32_e32 v113, v114, v113
	v_div_scale_f32 v114, vcc, v163, v105, v163
	v_mul_f32_e32 v115, v114, v113
	v_fma_f32 v116, -v112, v115, v114
	v_fmac_f32_e32 v115, v116, v113
	v_fma_f32 v112, -v112, v115, v114
	v_div_fmas_f32 v112, v112, v113, v115
	v_div_fixup_f32 v105, v112, v105, v163
	v_add_f32_e32 v105, v95, v105
	v_cmp_gt_f32_e32 vcc, s37, v105
	s_nop 1
	v_cndmask_b32_e64 v112, 0, 32, vcc
	v_ldexp_f32 v105, v105, v112
	v_log_f32_e32 v105, v105
	s_nop 0
	v_mul_f32_e32 v112, 0x3f317217, v105
	v_fma_f32 v112, v105, s33, -v112
	v_fmac_f32_e32 v112, 0x3377d1cf, v105
	v_fmac_f32_e32 v112, 0x3f317217, v105
	v_cmp_lt_f32_e64 s[60:61], |v105|, s36
	s_nop 1
	v_cndmask_b32_e64 v105, v105, v112, s[60:61]
	v_cndmask_b32_e32 v112, 0, v216, vcc
	v_sub_f32_e32 v105, v105, v112
	v_mul_f32_e32 v98, 0xbfb8aa3b, v98
	v_exp_f32_e32 v98, v98
	s_nop 0
	v_add_f32_e32 v98, 1.0, v98
	s_nop 0
	v_div_scale_f32 v113, s[2:3], v98, v98, v157
	v_rcp_f32_e32 v115, v113
	s_nop 0
	v_fma_f32 v116, -v113, v115, 1.0
	v_fmac_f32_e32 v115, v116, v115
	v_div_scale_f32 v116, vcc, v157, v98, v157
	v_mul_f32_e32 v117, v116, v115
	v_fma_f32 v118, -v113, v117, v116
	v_fmac_f32_e32 v117, v118, v115
	v_fma_f32 v113, -v113, v117, v116
	v_div_fmas_f32 v113, v113, v115, v117
	v_div_fixup_f32 v98, v113, v98, v157
	v_add_f32_e32 v98, v92, v98
	v_cmp_gt_f32_e32 vcc, s37, v98
	s_nop 1
	v_cndmask_b32_e64 v113, 0, 32, vcc
	v_ldexp_f32 v98, v98, v113
	v_log_f32_e32 v98, v98
	s_nop 0
	v_mul_f32_e32 v113, 0x3f317217, v98
	v_fma_f32 v113, v98, s33, -v113
	v_fmac_f32_e32 v113, 0x3377d1cf, v98
	v_fmac_f32_e32 v113, 0x3f317217, v98
	v_cmp_lt_f32_e64 s[60:61], |v98|, s36
	s_nop 1
	v_cndmask_b32_e64 v98, v98, v113, s[60:61]
	v_cndmask_b32_e32 v113, 0, v216, vcc
	v_sub_f32_e32 v188, v98, v113
	s_nop 0
	s_nop 1
	s_nop 0
	s_nop 1
	v_mul_f32_e32 v98, 0xbfb8aa3b, v99
	v_exp_f32_e32 v98, v98
	s_nop 0
	v_add_f32_e32 v98, 1.0, v98
	v_div_scale_f32 v99, s[2:3], v98, v98, v159
	v_rcp_f32_e32 v116, v99
	s_nop 0
	v_fma_f32 v117, -v99, v116, 1.0
	v_fmac_f32_e32 v116, v117, v116
	v_div_scale_f32 v117, vcc, v159, v98, v159
	v_mul_f32_e32 v118, v117, v116
	v_fma_f32 v119, -v99, v118, v117
	v_fmac_f32_e32 v118, v119, v116
	v_fma_f32 v99, -v99, v118, v117
	v_div_fmas_f32 v99, v99, v116, v118
	v_div_fixup_f32 v98, v99, v98, v159
	v_add_f32_e32 v98, v93, v98
	v_cmp_gt_f32_e32 vcc, s37, v98
	s_nop 1
	v_cndmask_b32_e64 v99, 0, 32, vcc
	v_ldexp_f32 v98, v98, v99
	v_log_f32_e32 v98, v98
	s_nop 0
	v_mul_f32_e32 v99, 0x3f317217, v98
	v_fma_f32 v99, v98, s33, -v99
	v_fmac_f32_e32 v99, 0x3377d1cf, v98
	v_fmac_f32_e32 v99, 0x3f317217, v98
	v_cmp_lt_f32_e64 s[60:61], |v98|, s36
	s_nop 1
	v_cndmask_b32_e64 v98, v98, v99, s[60:61]
	v_cndmask_b32_e32 v99, 0, v216, vcc
	v_sub_f32_e32 v189, v98, v99
	s_nop 1
	s_nop 0
	s_nop 1
	v_mul_f32_e32 v99, 0xbfb8aa3b, v100
	v_exp_f32_e32 v99, v99
	s_nop 0
	v_add_f32_e32 v99, 1.0, v99
	v_div_scale_f32 v100, s[2:3], v99, v99, v161
	v_rcp_f32_e32 v117, v100
	s_nop 0
	v_fma_f32 v118, -v100, v117, 1.0
	v_fmac_f32_e32 v117, v118, v117
	v_div_scale_f32 v118, vcc, v161, v99, v161
	v_mul_f32_e32 v119, v118, v117
	v_fma_f32 v120, -v100, v119, v118
	v_fmac_f32_e32 v119, v120, v117
	v_fma_f32 v100, -v100, v119, v118
	v_div_fmas_f32 v100, v100, v117, v119
	v_div_fixup_f32 v99, v100, v99, v161
	v_add_f32_e32 v99, v94, v99
	v_cmp_gt_f32_e32 vcc, s37, v99
	s_nop 1
	v_cndmask_b32_e64 v100, 0, 32, vcc
	v_ldexp_f32 v99, v99, v100
	v_log_f32_e32 v99, v99
	s_nop 0
	v_mul_f32_e32 v100, 0x3f317217, v99
	v_fma_f32 v100, v99, s33, -v100
	v_fmac_f32_e32 v100, 0x3377d1cf, v99
	v_fmac_f32_e32 v100, 0x3f317217, v99
	v_cmp_lt_f32_e64 s[60:61], |v99|, s36
	s_nop 1
	v_cndmask_b32_e64 v99, v99, v100, s[60:61]
	v_cndmask_b32_e32 v100, 0, v216, vcc
	v_sub_f32_e32 v190, v99, v100
	s_nop 1
	s_nop 0
	s_nop 1
	v_mul_f32_e32 v100, 0xbfb8aa3b, v101
	v_exp_f32_e32 v100, v100
	s_nop 0
	v_add_f32_e32 v100, 1.0, v100
	v_div_scale_f32 v101, s[2:3], v100, v100, v163
	v_rcp_f32_e32 v118, v101
	s_nop 0
	v_fma_f32 v119, -v101, v118, 1.0
	v_fmac_f32_e32 v118, v119, v118
	v_div_scale_f32 v119, vcc, v163, v100, v163
	v_mul_f32_e32 v120, v119, v118
; __device__ __forceinline__ float log_forget(float z, float lb) {
;   const float r0 = fminf(z, 0.f) - __logf(1.f + __expf(-fabsf(z)));
;   const float r1 = __logf(lb + (1.f - lb) / (1.f + __expf(-z)));
;   return lb <= 0.f ? r0 : r1;
; }
;   __device__ __forceinline__ void operator()(const f32x4 (&acc)[2][2][4][2], const pg8::Unit& u, int wr, int wc, int fr, int fq) const {
;     ...
;             for (int m = 0; m < 4; ++m)
; #pragma unroll
;               for (int q = 0; q < 4; ++q) { const float gv = log_forget(acc[ai][bj][m][qh][q], lq[q]); g[m][q] = gv;
	v_fma_f32 v121, -v101, v120, v119
	v_fmac_f32_e32 v120, v121, v118
	v_fma_f32 v101, -v101, v120, v119
	v_div_fmas_f32 v101, v101, v118, v120
	v_div_fixup_f32 v100, v101, v100, v163
	v_add_f32_e32 v100, v95, v100
	v_cmp_gt_f32_e32 vcc, s37, v100
	s_nop 1
	v_cndmask_b32_e64 v101, 0, 32, vcc
	v_ldexp_f32 v100, v100, v101
	v_log_f32_e32 v100, v100
	s_nop 0
	v_mul_f32_e32 v101, 0x3f317217, v100
	v_fma_f32 v101, v100, s33, -v101
	v_fmac_f32_e32 v101, 0x3377d1cf, v100
	v_fmac_f32_e32 v101, 0x3f317217, v100
	v_cmp_lt_f32_e64 s[60:61], |v100|, s36
	s_nop 1
	v_cndmask_b32_e64 v100, v100, v101, s[60:61]
	v_cndmask_b32_e32 v101, 0, v216, vcc
	v_sub_f32_e32 v191, v100, v101
	v_mul_f32_e32 v88, 0xbfb8aa3b, v88
	v_exp_f32_e32 v88, v88
	s_nop 0
	v_add_f32_e32 v88, 1.0, v88
	s_nop 0
	s_nop 1
	v_div_scale_f32 v101, s[2:3], v88, v88, v157
	v_rcp_f32_e32 v119, v101
	s_nop 0
	v_fma_f32 v120, -v101, v119, 1.0
	v_fmac_f32_e32 v119, v120, v119
	v_div_scale_f32 v120, vcc, v157, v88, v157
	v_mul_f32_e32 v121, v120, v119
	v_fma_f32 v168, -v101, v121, v120
	v_fmac_f32_e32 v121, v168, v119
	v_fma_f32 v101, -v101, v121, v120
	v_div_fmas_f32 v101, v101, v119, v121
	v_div_fixup_f32 v88, v101, v88, v157
	v_add_f32_e32 v88, v92, v88
	v_cmp_gt_f32_e32 vcc, s37, v88
	s_nop 1
	v_cndmask_b32_e64 v101, 0, 32, vcc
	v_ldexp_f32 v88, v88, v101
	v_log_f32_e32 v88, v88
	s_nop 0
	v_mul_f32_e32 v101, 0x3f317217, v88
	v_fma_f32 v101, v88, s33, -v101
	v_fmac_f32_e32 v101, 0x3377d1cf, v88
	v_fmac_f32_e32 v101, 0x3f317217, v88
	v_cmp_lt_f32_e64 s[60:61], |v88|, s36
	s_nop 1
	v_cndmask_b32_e64 v88, v88, v101, s[60:61]
	v_cndmask_b32_e32 v101, 0, v216, vcc
	v_sub_f32_e32 v192, v88, v101
	s_nop 0
	s_nop 1
	s_nop 0
	s_nop 1
	v_mul_f32_e32 v88, 0xbfb8aa3b, v89
	v_exp_f32_e32 v88, v88
	s_nop 0
	v_add_f32_e32 v88, 1.0, v88
	v_div_scale_f32 v89, s[2:3], v88, v88, v159
	v_rcp_f32_e32 v120, v89
	v_mov_b32_e32 v100, v192
	v_fma_f32 v121, -v89, v120, 1.0
	v_fmac_f32_e32 v120, v121, v120
	v_div_scale_f32 v121, vcc, v159, v88, v159
	v_mul_f32_e32 v168, v121, v120
	v_fma_f32 v169, -v89, v168, v121
	v_fmac_f32_e32 v168, v169, v120
	v_fma_f32 v89, -v89, v168, v121
	v_div_fmas_f32 v89, v89, v120, v168
	v_div_fixup_f32 v88, v89, v88, v159
	v_add_f32_e32 v88, v93, v88
	v_cmp_gt_f32_e32 vcc, s37, v88
	s_nop 1
	v_cndmask_b32_e64 v89, 0, 32, vcc
	v_ldexp_f32 v88, v88, v89
	v_log_f32_e32 v88, v88
	s_nop 0
	v_mul_f32_e32 v89, 0x3f317217, v88
	v_fma_f32 v89, v88, s33, -v89
	v_fmac_f32_e32 v89, 0x3377d1cf, v88
	v_fmac_f32_e32 v89, 0x3f317217, v88
	v_cmp_lt_f32_e64 s[60:61], |v88|, s36
	s_nop 1
	v_cndmask_b32_e64 v88, v88, v89, s[60:61]
	v_cndmask_b32_e32 v89, 0, v216, vcc
	v_sub_f32_e32 v193, v88, v89
	v_mov_b32_e32 v101, v193
	s_nop 1
	s_nop 0
	s_nop 1
	v_mul_f32_e32 v88, 0xbfb8aa3b, v90
	v_exp_f32_e32 v88, v88
	s_nop 0
	v_add_f32_e32 v88, 1.0, v88
	v_div_scale_f32 v89, s[2:3], v88, v88, v161
	v_rcp_f32_e32 v90, v89
	s_nop 0
	v_fma_f32 v121, -v89, v90, 1.0
	v_fmac_f32_e32 v90, v121, v90
	v_div_scale_f32 v121, vcc, v161, v88, v161
	v_mul_f32_e32 v169, v121, v90
	v_fma_f32 v170, -v89, v169, v121
	v_fmac_f32_e32 v169, v170, v90
	v_fma_f32 v89, -v89, v169, v121
	v_div_fmas_f32 v89, v89, v90, v169
	v_div_fixup_f32 v88, v89, v88, v161
	v_add_f32_e32 v88, v94, v88
	v_cmp_gt_f32_e32 vcc, s37, v88
	s_nop 1
	v_cndmask_b32_e64 v89, 0, 32, vcc
	v_ldexp_f32 v88, v88, v89
	v_log_f32_e32 v88, v88
	s_nop 0
	v_mul_f32_e32 v89, 0x3f317217, v88
	v_fma_f32 v89, v88, s33, -v89
	v_fmac_f32_e32 v89, 0x3377d1cf, v88
	v_fmac_f32_e32 v89, 0x3f317217, v88
	v_cmp_lt_f32_e64 s[60:61], |v88|, s36
	s_nop 1
	v_cndmask_b32_e64 v88, v88, v89, s[60:61]
	v_cndmask_b32_e32 v89, 0, v216, vcc
	v_sub_f32_e32 v194, v88, v89
	s_nop 0
	s_nop 1
	s_nop 0
	s_nop 1
	v_mul_f32_e32 v88, 0xbfb8aa3b, v91
	v_exp_f32_e32 v88, v88
	s_nop 0
	v_add_f32_e32 v88, 1.0, v88
	v_div_scale_f32 v89, s[2:3], v88, v88, v163
	v_rcp_f32_e32 v90, v89
	s_nop 0
	v_fma_f32 v91, -v89, v90, 1.0
	v_fmac_f32_e32 v90, v91, v90
	v_div_scale_f32 v91, vcc, v163, v88, v163
	v_mul_f32_e32 v170, v91, v90
	v_fma_f32 v171, -v89, v170, v91
	v_fmac_f32_e32 v170, v171, v90
	v_fma_f32 v89, -v89, v170, v91
	v_div_fmas_f32 v89, v89, v90, v170
	v_div_fixup_f32 v88, v89, v88, v163
	v_add_f32_e32 v88, v95, v88
	v_cmp_gt_f32_e32 vcc, s37, v88
	s_nop 1
	v_cndmask_b32_e64 v89, 0, 32, vcc
	v_ldexp_f32 v88, v88, v89
	v_log_f32_e32 v88, v88
	s_nop 0
	v_mul_f32_e32 v89, 0x3f317217, v88
	v_fma_f32 v89, v88, s33, -v89
	v_fmac_f32_e32 v89, 0x3377d1cf, v88
	v_fmac_f32_e32 v89, 0x3f317217, v88
	v_cmp_lt_f32_e64 s[60:61], |v88|, s36
	s_nop 1
	v_cndmask_b32_e64 v88, v88, v89, s[60:61]
	v_cndmask_b32_e32 v89, 0, v216, vcc
	v_sub_f32_e32 v195, v88, v89
	v_mul_f32_e32 v84, 0xbfb8aa3b, v84
	v_exp_f32_e32 v84, v84
	s_nop 0
	v_add_f32_e32 v84, 1.0, v84
	s_nop 0
	s_nop 0
	s_nop 1
	v_div_scale_f32 v88, s[2:3], v84, v84, v157
	v_rcp_f32_e32 v89, v88
	s_nop 0
	v_fma_f32 v90, -v88, v89, 1.0
	v_fmac_f32_e32 v89, v90, v89
	v_div_scale_f32 v90, vcc, v157, v84, v157
	v_mul_f32_e32 v91, v90, v89
	v_fma_f32 v171, -v88, v91, v90
	v_fmac_f32_e32 v91, v171, v89
	v_fma_f32 v88, -v88, v91, v90
	v_div_fmas_f32 v88, v88, v89, v91
	v_div_fixup_f32 v84, v88, v84, v157
	v_add_f32_e32 v84, v92, v84
	v_cmp_gt_f32_e32 vcc, s37, v84
	s_nop 1
	v_cndmask_b32_e64 v88, 0, 32, vcc
	v_ldexp_f32 v84, v84, v88
	v_log_f32_e32 v84, v84
	s_nop 0
	v_mul_f32_e32 v88, 0x3f317217, v84
	v_fma_f32 v88, v84, s33, -v88
	v_fmac_f32_e32 v88, 0x3377d1cf, v84
	v_fmac_f32_e32 v88, 0x3f317217, v84
	v_cmp_lt_f32_e64 s[60:61], |v84|, s36
	s_nop 1
	v_cndmask_b32_e64 v84, v84, v88, s[60:61]
	v_cndmask_b32_e32 v88, 0, v216, vcc
	v_sub_f32_e32 v157, v84, v88
	s_nop 0
	s_nop 1
; template <int CTRL> __device__ __forceinline__ float dppx(float v) { return __int_as_float(__builtin_amdgcn_update_dpp(0, __float_as_int(v), CTRL, 0xf, 0xf, true)); }
; __device__ __forceinline__ float log_forget(float z, float lb) {
;   const float r0 = fminf(z, 0.f) - __logf(1.f + __expf(-fabsf(z)));
;   const float r1 = __logf(lb + (1.f - lb) / (1.f + __expf(-z)));
;   return lb <= 0.f ? r0 : r1;
; }
;   __device__ __forceinline__ void operator()(const f32x4 (&acc)[2][2][4][2], const pg8::Unit& u, int wr, int wc, int fr, int fq) const {
;     ...
;             for (int m = 0; m < 4; ++m)
; #pragma unroll
;               for (int q = 0; q < 4; ++q) { const float gv = log_forget(acc[ai][bj][m][qh][q], lq[q]); g[m][q] = gv;
;                 float sc = gv; sc += dppx<0x111>(sc); sc += dppx<0x112>(sc); sc += dppx<0x114>(sc); sc += dppx<0x118>(sc);
;                 const float tot16 = __int_as_float(__builtin_amdgcn_ds_swizzle(__float_as_int(sc), 0x1F0));
;                 cs[m][q] = sc + carry[q]; carry[q] += tot16; }
	s_nop 0
	s_nop 1
	v_mul_f32_e32 v84, 0xbfb8aa3b, v85
	v_exp_f32_e32 v84, v84
	s_nop 0
	v_add_f32_e32 v84, 1.0, v84
	v_div_scale_f32 v85, s[2:3], v84, v84, v159
	v_rcp_f32_e32 v88, v85
	s_nop 0
	v_fma_f32 v89, -v85, v88, 1.0
	v_fmac_f32_e32 v88, v89, v88
	v_div_scale_f32 v89, vcc, v159, v84, v159
	v_mul_f32_e32 v90, v89, v88
	v_fma_f32 v91, -v85, v90, v89
	v_fmac_f32_e32 v90, v91, v88
	v_fma_f32 v85, -v85, v90, v89
	v_div_fmas_f32 v85, v85, v88, v90
	v_div_fixup_f32 v84, v85, v84, v159
	v_add_f32_e32 v84, v93, v84
	v_cmp_gt_f32_e32 vcc, s37, v84
	v_ashrrev_i32_e32 v159, 31, v158
	s_nop 0
	v_cndmask_b32_e64 v85, 0, 32, vcc
	v_ldexp_f32 v84, v84, v85
	v_log_f32_e32 v84, v84
	v_mov_b32_e32 v115, v189
	v_mov_b32_e32 v114, v188
	v_mul_f32_e32 v85, 0x3f317217, v84
	v_fma_f32 v85, v84, s33, -v85
	v_fmac_f32_e32 v85, 0x3377d1cf, v84
	v_fmac_f32_e32 v85, 0x3f317217, v84
	v_cmp_lt_f32_e64 s[60:61], |v84|, s36
	v_mov_b32_dpp v92, v114 row_shr:1 row_mask:0xf bank_mask:0xf bound_ctrl:1
	v_mov_b32_dpp v93, v115 row_shr:1 row_mask:0xf bank_mask:0xf bound_ctrl:1
	v_cndmask_b32_e64 v84, v84, v85, s[60:61]
	v_cndmask_b32_e32 v85, 0, v216, vcc
	v_sub_f32_e32 v196, v84, v85
	v_pk_add_f32 v[92:93], v[114:115], v[92:93]
	s_nop 1
	s_nop 0
	s_nop 1
	v_mul_f32_e32 v84, 0xbfb8aa3b, v86
	v_exp_f32_e32 v84, v84
	s_nop 0
	v_add_f32_e32 v84, 1.0, v84
	v_div_scale_f32 v85, s[2:3], v84, v84, v161
	v_rcp_f32_e32 v86, v85
	s_nop 0
	v_fma_f32 v88, -v85, v86, 1.0
	v_fmac_f32_e32 v86, v88, v86
	v_div_scale_f32 v88, vcc, v161, v84, v161
	v_mul_f32_e32 v89, v88, v86
	v_fma_f32 v90, -v85, v89, v88
	v_fmac_f32_e32 v89, v90, v86
	v_fma_f32 v85, -v85, v89, v88
	v_div_fmas_f32 v85, v85, v86, v89
	v_div_fixup_f32 v84, v85, v84, v161
	v_add_f32_e32 v84, v94, v84
	v_cmp_gt_f32_e32 vcc, s37, v84
	v_mov_b32_dpp v94, v92 row_shr:2 row_mask:0xf bank_mask:0xf bound_ctrl:1
	v_ashrrev_i32_e32 v161, 31, v160
	v_cndmask_b32_e64 v85, 0, 32, vcc
	v_ldexp_f32 v84, v84, v85
	v_log_f32_e32 v84, v84
	s_nop 0
	v_mul_f32_e32 v85, 0x3f317217, v84
	v_fma_f32 v85, v84, s33, -v85
	v_fmac_f32_e32 v85, 0x3377d1cf, v84
	v_fmac_f32_e32 v85, 0x3f317217, v84
	v_cmp_lt_f32_e64 s[60:61], |v84|, s36
	s_nop 1
	v_cndmask_b32_e64 v84, v84, v85, s[60:61]
	v_cndmask_b32_e32 v85, 0, v216, vcc
	v_sub_f32_e32 v197, v84, v85
	s_nop 0
	s_nop 1
	s_nop 0
	s_nop 1
	v_mul_f32_e32 v84, 0xbfb8aa3b, v87
	v_exp_f32_e32 v84, v84
	s_nop 0
	v_add_f32_e32 v84, 1.0, v84
	v_div_scale_f32 v85, s[2:3], v84, v84, v163
	v_rcp_f32_e32 v86, v85
	s_nop 0
	v_fma_f32 v87, -v85, v86, 1.0
	v_fmac_f32_e32 v86, v87, v86
	v_div_scale_f32 v87, vcc, v163, v84, v163
	v_mul_f32_e32 v88, v87, v86
	v_fma_f32 v89, -v85, v88, v87
	v_fmac_f32_e32 v88, v89, v86
	v_fma_f32 v85, -v85, v88, v87
	v_div_fmas_f32 v85, v85, v86, v88
	v_div_fixup_f32 v84, v85, v84, v163
	v_add_f32_e32 v84, v95, v84
	v_cmp_gt_f32_e32 vcc, s37, v84
	v_mov_b32_dpp v95, v93 row_shr:2 row_mask:0xf bank_mask:0xf bound_ctrl:1
	v_pk_add_f32 v[92:93], v[92:93], v[94:95]
	v_cndmask_b32_e64 v85, 0, 32, vcc
	v_ldexp_f32 v84, v84, v85
	v_log_f32_e32 v84, v84
	v_mov_b32_dpp v94, v92 row_shr:4 row_mask:0xf bank_mask:0xf bound_ctrl:1
	v_mov_b32_dpp v95, v93 row_shr:4 row_mask:0xf bank_mask:0xf bound_ctrl:1
	v_pk_add_f32 v[92:93], v[92:93], v[94:95]
	v_mul_f32_e32 v85, 0x3f317217, v84
	v_fma_f32 v85, v84, s33, -v85
	v_fmac_f32_e32 v85, 0x3377d1cf, v84
	v_fmac_f32_e32 v85, 0x3f317217, v84
	v_cmp_lt_f32_e64 s[60:61], |v84|, s36
	v_mov_b32_dpp v94, v92 row_shr:8 row_mask:0xf bank_mask:0xf bound_ctrl:1
	v_mov_b32_dpp v95, v93 row_shr:8 row_mask:0xf bank_mask:0xf bound_ctrl:1
	v_cndmask_b32_e64 v84, v84, v85, s[60:61]
	v_cndmask_b32_e32 v85, 0, v216, vcc
	v_sub_f32_e32 v198, v84, v85
	v_pk_add_f32 v[92:93], v[92:93], v[94:95]
	v_mov_b32_e32 v181, v181
	v_mov_b32_e32 v180, v180
	ds_swizzle_b32 v94, v92 offset:swizzle(BROADCAST,16,15)
	v_mov_b32_dpp v85, v181 row_shr:1 row_mask:0xf bank_mask:0xf bound_ctrl:1
	v_mov_b32_dpp v84, v180 row_shr:1 row_mask:0xf bank_mask:0xf bound_ctrl:1
	v_pk_add_f32 v[84:85], v[180:181], v[84:85]
	ds_swizzle_b32 v95, v93 offset:swizzle(BROADCAST,16,15)
	v_ashrrev_i32_e32 v163, 31, v162
	v_mov_b32_dpp v86, v84 row_shr:2 row_mask:0xf bank_mask:0xf bound_ctrl:1
	v_mov_b32_dpp v87, v85 row_shr:2 row_mask:0xf bank_mask:0xf bound_ctrl:1
	v_pk_add_f32 v[84:85], v[84:85], v[86:87]
	s_nop 1
	v_mov_b32_dpp v86, v84 row_shr:4 row_mask:0xf bank_mask:0xf bound_ctrl:1
	v_mov_b32_dpp v87, v85 row_shr:4 row_mask:0xf bank_mask:0xf bound_ctrl:1
	v_pk_add_f32 v[84:85], v[84:85], v[86:87]
	s_nop 1
	v_mov_b32_dpp v86, v84 row_shr:8 row_mask:0xf bank_mask:0xf bound_ctrl:1
	v_mov_b32_dpp v87, v85 row_shr:8 row_mask:0xf bank_mask:0xf bound_ctrl:1
	v_pk_add_f32 v[84:85], v[84:85], v[86:87]
	ds_swizzle_b32 v86, v84 offset:swizzle(BROADCAST,16,15)
	v_pk_add_f32 v[182:183], v[84:85], 0 op_sel_hi:[1,0]
	v_mul_f32_e32 v84, 0x3fb8aa3b, v180
	v_exp_f32_e32 v84, v84
	ds_swizzle_b32 v87, v85 offset:swizzle(BROADCAST,16,15)
	v_sub_f32_e32 v199, 1.0, v84
	v_mul_f32_e32 v84, 0x3fb8aa3b, v181
	v_exp_f32_e32 v84, v84
	s_waitcnt lgkmcnt(0)
; template <int CTRL> __device__ __forceinline__ float dppx(float v) { return __int_as_float(__builtin_amdgcn_update_dpp(0, __float_as_int(v), CTRL, 0xf, 0xf, true)); }
; __device__ __forceinline__ unsigned cvt_pk_bf16(float lo, float hi) { unsigned r; asm volatile("v_cvt_pk_bf16_f32 %0, %1, %2" : "=v"(r) : "v"(lo), "v"(hi)); return r; }
;   __device__ __forceinline__ void operator()(const f32x4 (&acc)[2][2][4][2], const pg8::Unit& u, int wr, int wc, int fr, int fq) const {
;     ...
;             for (int m = 0; m < 4; ++m)
; #pragma unroll
;               for (int q = 0; q < 4; ++q) { const float gv = log_forget(acc[ai][bj][m][qh][q], lq[q]); g[m][q] = gv;
;                 float sc = gv; sc += dppx<0x111>(sc); sc += dppx<0x112>(sc); sc += dppx<0x114>(sc); sc += dppx<0x118>(sc);
;                 const float tot16 = __int_as_float(__builtin_amdgcn_ds_swizzle(__float_as_int(sc), 0x1F0));
;                 cs[m][q] = sc + carry[q]; carry[q] += tot16; }
; #pragma unroll
;             for (int m = 0; m < 4; ++m) { const int r = row0 + ai * 128 + m * 16; float bq[4], kq[4];
; #pragma unroll
;               for (int q = 0; q < 4; ++q) { bq[q] = bwd ? (carry[q] - cs[m][q]) + g[m][q] : cs[m][q]; kq[q] = 1.f - __expf(g[m][q]); }
;               *(f32x4*)(logfp + (size_t)r * 1024 + c + 4 * qh) = (f32x4){bq[0], bq[1], bq[2], bq[3]};
;               u32x2 w; w.x = pg8::cvt_pk_bf16(kq[0], kq[1]); w.y = pg8::cvt_pk_bf16(kq[2], kq[3]);
;               *(u32x2*)(km + (size_t)r * 1024 + c + 4 * qh) = w; } } }
	v_pk_add_f32 v[88:89], v[86:87], 0 op_sel_hi:[1,0]
	v_sub_f32_e32 v200, 1.0, v84
	v_mov_b32_dpp v110, v100 row_shr:1 row_mask:0xf bank_mask:0xf bound_ctrl:1
	v_mov_b32_e32 v185, v105
	v_mov_b32_e32 v184, v104
	v_mov_b32_dpp v111, v101 row_shr:1 row_mask:0xf bank_mask:0xf bound_ctrl:1
	v_mov_b32_dpp v85, v185 row_shr:1 row_mask:0xf bank_mask:0xf bound_ctrl:1
	v_mov_b32_dpp v84, v184 row_shr:1 row_mask:0xf bank_mask:0xf bound_ctrl:1
	v_pk_add_f32 v[84:85], v[184:185], v[84:85]
	v_pk_add_f32 v[110:111], v[100:101], v[110:111]
	s_nop 0
	v_mov_b32_dpp v86, v84 row_shr:2 row_mask:0xf bank_mask:0xf bound_ctrl:1
	v_mov_b32_dpp v87, v85 row_shr:2 row_mask:0xf bank_mask:0xf bound_ctrl:1
	v_pk_add_f32 v[84:85], v[84:85], v[86:87]
	v_mov_b32_dpp v112, v110 row_shr:2 row_mask:0xf bank_mask:0xf bound_ctrl:1
	v_mov_b32_dpp v113, v111 row_shr:2 row_mask:0xf bank_mask:0xf bound_ctrl:1
	v_mov_b32_dpp v86, v84 row_shr:4 row_mask:0xf bank_mask:0xf bound_ctrl:1
	v_mov_b32_dpp v87, v85 row_shr:4 row_mask:0xf bank_mask:0xf bound_ctrl:1
	v_pk_add_f32 v[84:85], v[84:85], v[86:87]
	v_pk_add_f32 v[110:111], v[110:111], v[112:113]
	s_nop 0
	v_mov_b32_dpp v86, v84 row_shr:8 row_mask:0xf bank_mask:0xf bound_ctrl:1
	v_mov_b32_dpp v87, v85 row_shr:8 row_mask:0xf bank_mask:0xf bound_ctrl:1
	v_pk_add_f32 v[84:85], v[84:85], v[86:87]
	ds_swizzle_b32 v86, v84 offset:swizzle(BROADCAST,16,15)
	v_pk_add_f32 v[186:187], v[84:85], 0 op_sel_hi:[1,0]
	v_mul_f32_e32 v84, 0x3fb8aa3b, v184
	v_exp_f32_e32 v84, v84
	ds_swizzle_b32 v87, v85 offset:swizzle(BROADCAST,16,15)
	v_mov_b32_dpp v112, v110 row_shr:4 row_mask:0xf bank_mask:0xf bound_ctrl:1
	v_mov_b32_dpp v113, v111 row_shr:4 row_mask:0xf bank_mask:0xf bound_ctrl:1
	v_sub_f32_e32 v201, 1.0, v84
	v_mul_f32_e32 v84, 0x3fb8aa3b, v185
	v_exp_f32_e32 v84, v84
	s_waitcnt lgkmcnt(0)
	v_pk_add_f32 v[90:91], v[86:87], 0 op_sel_hi:[1,0]
	v_lshlrev_b64 v[86:87], 11, v[162:163]
	v_pk_add_f32 v[110:111], v[110:111], v[112:113]
	v_sub_f32_e32 v202, 1.0, v84
	v_lshlrev_b64 v[84:85], 12, v[162:163]
	v_pk_add_f32 v[162:163], v[88:89], v[92:93]
	v_pk_add_f32 v[92:93], v[88:89], v[94:95]
	v_mul_f32_e32 v88, 0x3fb8aa3b, v114
	v_exp_f32_e32 v88, v88
	v_mov_b32_dpp v112, v110 row_shr:8 row_mask:0xf bank_mask:0xf bound_ctrl:1
	v_mov_b32_dpp v113, v111 row_shr:8 row_mask:0xf bank_mask:0xf bound_ctrl:1
	v_pk_add_f32 v[110:111], v[110:111], v[112:113]
	v_sub_f32_e32 v203, 1.0, v88
	v_mul_f32_e32 v88, 0x3fb8aa3b, v115
	v_exp_f32_e32 v88, v88
	ds_swizzle_b32 v112, v110 offset:swizzle(BROADCAST,16,15)
	ds_swizzle_b32 v113, v111 offset:swizzle(BROADCAST,16,15)
	v_lshl_add_u64 v[84:85], s[22:23], 0, v[84:85]
	v_sub_f32_e32 v207, 1.0, v88
	v_lshl_add_u64 v[104:105], v[84:85], 0, v[166:167]
	v_mov_b32_e32 v99, v191
	v_mov_b32_e32 v98, v190
	s_waitcnt lgkmcnt(0)
	v_pk_add_f32 v[118:119], v[92:93], v[112:113]
	v_mov_b32_dpp v89, v99 row_shr:1 row_mask:0xf bank_mask:0xf bound_ctrl:1
	v_mov_b32_dpp v88, v98 row_shr:1 row_mask:0xf bank_mask:0xf bound_ctrl:1
	v_pk_add_f32 v[88:89], v[98:99], v[88:89]
	v_lshl_add_u64 v[86:87], s[0:1], 0, v[86:87]
	v_lshl_add_u64 v[102:103], v[86:87], 0, v[164:165]
	v_mov_b32_dpp v94, v88 row_shr:2 row_mask:0xf bank_mask:0xf bound_ctrl:1
	v_mov_b32_dpp v95, v89 row_shr:2 row_mask:0xf bank_mask:0xf bound_ctrl:1
	v_pk_add_f32 v[88:89], v[88:89], v[94:95]
	s_nop 1
	v_mov_b32_dpp v94, v88 row_shr:4 row_mask:0xf bank_mask:0xf bound_ctrl:1
	v_mov_b32_dpp v95, v89 row_shr:4 row_mask:0xf bank_mask:0xf bound_ctrl:1
	v_pk_add_f32 v[88:89], v[88:89], v[94:95]
	s_nop 1
	v_mov_b32_dpp v94, v88 row_shr:8 row_mask:0xf bank_mask:0xf bound_ctrl:1
	v_mov_b32_dpp v95, v89 row_shr:8 row_mask:0xf bank_mask:0xf bound_ctrl:1
	v_pk_add_f32 v[88:89], v[88:89], v[94:95]
	ds_swizzle_b32 v94, v88 offset:swizzle(BROADCAST,16,15)
	v_pk_add_f32 v[116:117], v[90:91], v[88:89]
	v_mul_f32_e32 v88, 0x3fb8aa3b, v98
	v_exp_f32_e32 v88, v88
	ds_swizzle_b32 v95, v89 offset:swizzle(BROADCAST,16,15)
	v_sub_f32_e32 v208, 1.0, v88
	v_mul_f32_e32 v88, 0x3fb8aa3b, v99
	v_exp_f32_e32 v88, v88
	s_waitcnt lgkmcnt(0)
	v_pk_add_f32 v[94:95], v[90:91], v[94:95]
	v_lshlrev_b64 v[90:91], 11, v[160:161]
	v_lshl_add_u64 v[90:91], s[0:1], 0, v[90:91]
	v_sub_f32_e32 v209, 1.0, v88
	v_lshlrev_b64 v[88:89], 12, v[160:161]
	v_pk_add_f32 v[160:161], v[92:93], v[110:111]
	v_mul_f32_e32 v92, 0x3fb8aa3b, v100
	v_exp_f32_e32 v92, v92
	v_lshl_add_u64 v[88:89], s[22:23], 0, v[88:89]
	v_lshl_add_u64 v[108:109], v[88:89], 0, v[166:167]
	v_lshl_add_u64 v[106:107], v[90:91], 0, v[164:165]
	v_sub_f32_e32 v192, 1.0, v92
	v_mul_f32_e32 v92, 0x3fb8aa3b, v101
	v_exp_f32_e32 v92, v92
	s_nop 0
	v_sub_f32_e32 v193, 1.0, v92
	s_nop 0
	v_mov_b32_e32 v169, v195
	v_mov_b32_e32 v168, v194
	s_nop 0
	v_mov_b32_dpp v93, v169 row_shr:1 row_mask:0xf bank_mask:0xf bound_ctrl:1
	v_mov_b32_dpp v92, v168 row_shr:1 row_mask:0xf bank_mask:0xf bound_ctrl:1
	v_pk_add_f32 v[92:93], v[168:169], v[92:93]
	s_nop 1
	v_mov_b32_dpp v110, v92 row_shr:2 row_mask:0xf bank_mask:0xf bound_ctrl:1
	v_mov_b32_dpp v111, v93 row_shr:2 row_mask:0xf bank_mask:0xf bound_ctrl:1
	v_pk_add_f32 v[92:93], v[92:93], v[110:111]
	s_nop 1
	v_mov_b32_dpp v110, v92 row_shr:4 row_mask:0xf bank_mask:0xf bound_ctrl:1
	v_mov_b32_dpp v111, v93 row_shr:4 row_mask:0xf bank_mask:0xf bound_ctrl:1
	v_pk_add_f32 v[92:93], v[92:93], v[110:111]
	s_nop 1
	v_mov_b32_dpp v110, v92 row_shr:8 row_mask:0xf bank_mask:0xf bound_ctrl:1
	v_mov_b32_dpp v111, v93 row_shr:8 row_mask:0xf bank_mask:0xf bound_ctrl:1
	v_pk_add_f32 v[92:93], v[92:93], v[110:111]
	ds_swizzle_b32 v110, v92 offset:swizzle(BROADCAST,16,15)
	v_pk_add_f32 v[188:189], v[94:95], v[92:93]
	v_mul_f32_e32 v92, 0x3fb8aa3b, v168
	v_exp_f32_e32 v92, v92
	ds_swizzle_b32 v111, v93 offset:swizzle(BROADCAST,16,15)
	v_sub_f32_e32 v194, 1.0, v92
	v_mul_f32_e32 v92, 0x3fb8aa3b, v169
	v_exp_f32_e32 v92, v92
	s_waitcnt lgkmcnt(0)
; template <int CTRL> __device__ __forceinline__ float dppx(float v) { return __int_as_float(__builtin_amdgcn_update_dpp(0, __float_as_int(v), CTRL, 0xf, 0xf, true)); }
; __device__ __forceinline__ unsigned cvt_pk_bf16(float lo, float hi) { unsigned r; asm volatile("v_cvt_pk_bf16_f32 %0, %1, %2" : "=v"(r) : "v"(lo), "v"(hi)); return r; }
;   __device__ __forceinline__ void operator()(const f32x4 (&acc)[2][2][4][2], const pg8::Unit& u, int wr, int wc, int fr, int fq) const {
;     ...
;               for (int q = 0; q < 4; ++q) { const float gv = log_forget(acc[ai][bj][m][qh][q], lq[q]); g[m][q] = gv;
;                 float sc = gv; sc += dppx<0x111>(sc); sc += dppx<0x112>(sc); sc += dppx<0x114>(sc); sc += dppx<0x118>(sc);
;                 const float tot16 = __int_as_float(__builtin_amdgcn_ds_swizzle(__float_as_int(sc), 0x1F0));
;                 cs[m][q] = sc + carry[q]; carry[q] += tot16; }
; #pragma unroll
;             for (int m = 0; m < 4; ++m) { const int r = row0 + ai * 128 + m * 16; float bq[4], kq[4];
; #pragma unroll
;               for (int q = 0; q < 4; ++q) { bq[q] = bwd ? (carry[q] - cs[m][q]) + g[m][q] : cs[m][q]; kq[q] = 1.f - __expf(g[m][q]); }
;               *(f32x4*)(logfp + (size_t)r * 1024 + c + 4 * qh) = (f32x4){bq[0], bq[1], bq[2], bq[3]};
;               u32x2 w; w.x = pg8::cvt_pk_bf16(kq[0], kq[1]); w.y = pg8::cvt_pk_bf16(kq[2], kq[3]);
;               *(u32x2*)(km + (size_t)r * 1024 + c + 4 * qh) = w; } } }
	v_pk_add_f32 v[120:121], v[94:95], v[110:111]
	v_lshlrev_b64 v[94:95], 11, v[158:159]
	v_lshl_add_u64 v[94:95], s[0:1], 0, v[94:95]
	v_sub_f32_e32 v195, 1.0, v92
	v_lshlrev_b64 v[92:93], 12, v[158:159]
	v_lshl_add_u64 v[92:93], s[22:23], 0, v[92:93]
	v_mov_b32_e32 v159, v196
	v_mov_b32_e32 v158, v157
	v_lshl_add_u64 v[110:111], v[92:93], 0, v[166:167]
	v_mov_b32_dpp v171, v159 row_shr:1 row_mask:0xf bank_mask:0xf bound_ctrl:1
	v_mov_b32_dpp v170, v158 row_shr:1 row_mask:0xf bank_mask:0xf bound_ctrl:1
	v_pk_add_f32 v[170:171], v[158:159], v[170:171]
	v_lshl_add_u64 v[112:113], v[94:95], 0, v[164:165]
	v_ashrrev_i32_e32 v157, 31, v156
	v_mov_b32_dpp v172, v170 row_shr:2 row_mask:0xf bank_mask:0xf bound_ctrl:1
	v_mov_b32_dpp v173, v171 row_shr:2 row_mask:0xf bank_mask:0xf bound_ctrl:1
	v_pk_add_f32 v[170:171], v[170:171], v[172:173]
	s_nop 1
	v_mov_b32_dpp v172, v170 row_shr:4 row_mask:0xf bank_mask:0xf bound_ctrl:1
	v_mov_b32_dpp v173, v171 row_shr:4 row_mask:0xf bank_mask:0xf bound_ctrl:1
	v_pk_add_f32 v[170:171], v[170:171], v[172:173]
	s_nop 1
	v_mov_b32_dpp v172, v170 row_shr:8 row_mask:0xf bank_mask:0xf bound_ctrl:1
	v_mov_b32_dpp v173, v171 row_shr:8 row_mask:0xf bank_mask:0xf bound_ctrl:1
	v_pk_add_f32 v[170:171], v[170:171], v[172:173]
	ds_swizzle_b32 v172, v170 offset:swizzle(BROADCAST,16,15)
	ds_swizzle_b32 v173, v171 offset:swizzle(BROADCAST,16,15)
	v_pk_add_f32 v[170:171], v[118:119], v[170:171]
	s_waitcnt lgkmcnt(0)
	v_pk_add_f32 v[172:173], v[118:119], v[172:173]
	v_mul_f32_e32 v118, 0x3fb8aa3b, v158
	v_exp_f32_e32 v118, v118
	s_nop 0
	v_sub_f32_e32 v196, 1.0, v118
	v_mul_f32_e32 v118, 0x3fb8aa3b, v159
	v_exp_f32_e32 v118, v118
	s_nop 0
	v_sub_f32_e32 v210, 1.0, v118
	s_nop 0
	v_mov_b32_e32 v175, v198
	v_mov_b32_e32 v174, v197
	s_nop 0
	v_mov_b32_dpp v119, v175 row_shr:1 row_mask:0xf bank_mask:0xf bound_ctrl:1
	v_mov_b32_dpp v118, v174 row_shr:1 row_mask:0xf bank_mask:0xf bound_ctrl:1
	v_pk_add_f32 v[118:119], v[174:175], v[118:119]
	s_nop 1
	v_mov_b32_dpp v176, v118 row_shr:2 row_mask:0xf bank_mask:0xf bound_ctrl:1
	v_mov_b32_dpp v177, v119 row_shr:2 row_mask:0xf bank_mask:0xf bound_ctrl:1
	v_pk_add_f32 v[118:119], v[118:119], v[176:177]
	s_nop 1
	v_mov_b32_dpp v176, v118 row_shr:4 row_mask:0xf bank_mask:0xf bound_ctrl:1
	v_mov_b32_dpp v177, v119 row_shr:4 row_mask:0xf bank_mask:0xf bound_ctrl:1
	v_pk_add_f32 v[118:119], v[118:119], v[176:177]
	s_nop 1
	v_mov_b32_dpp v176, v118 row_shr:8 row_mask:0xf bank_mask:0xf bound_ctrl:1
	v_mov_b32_dpp v177, v119 row_shr:8 row_mask:0xf bank_mask:0xf bound_ctrl:1
	v_pk_add_f32 v[118:119], v[118:119], v[176:177]
	ds_swizzle_b32 v176, v118 offset:swizzle(BROADCAST,16,15)
	ds_swizzle_b32 v177, v119 offset:swizzle(BROADCAST,16,15)
	v_pk_add_f32 v[190:191], v[120:121], v[118:119]
	v_pk_add_f32 v[118:119], v[172:173], v[182:183] neg_lo:[0,1] neg_hi:[0,1]
	s_waitcnt lgkmcnt(0)
	v_pk_add_f32 v[176:177], v[120:121], v[176:177]
	s_nop 0
	v_pk_add_f32 v[120:121], v[176:177], v[186:187] neg_lo:[0,1] neg_hi:[0,1]
	v_pk_add_f32 v[118:119], v[180:181], v[118:119]
	v_pk_add_f32 v[120:121], v[184:185], v[120:121]
	v_cndmask_b32_e64 v119, v183, v119, s[42:43]
	v_cndmask_b32_e64 v121, v187, v121, s[42:43]
	v_cndmask_b32_e64 v120, v186, v120, s[42:43]
	v_cndmask_b32_e64 v118, v182, v118, s[42:43]
	global_store_dwordx4 v[104:105], v[118:121], off
	s_nop 1
	v_cvt_pk_bf16_f32 v118, v199, v200
	v_cvt_pk_bf16_f32 v119, v201, v202
	global_store_dwordx2 v[102:103], v[118:119], off
	v_pk_add_f32 v[118:119], v[172:173], v[162:163] neg_lo:[0,1] neg_hi:[0,1]
	v_pk_add_f32 v[120:121], v[176:177], v[116:117] neg_lo:[0,1] neg_hi:[0,1]
	v_pk_add_f32 v[114:115], v[114:115], v[118:119]
	v_pk_add_f32 v[98:99], v[98:99], v[120:121]
	v_cndmask_b32_e64 v115, v163, v115, s[42:43]
	v_cndmask_b32_e64 v117, v117, v99, s[42:43]
	v_cndmask_b32_e64 v116, v116, v98, s[42:43]
	v_cndmask_b32_e64 v114, v162, v114, s[42:43]
	global_store_dwordx4 v[108:109], v[114:117], off
	v_cvt_pk_bf16_f32 v98, v203, v207
	v_cvt_pk_bf16_f32 v99, v208, v209
	global_store_dwordx2 v[106:107], v[98:99], off
	v_pk_add_f32 v[98:99], v[172:173], v[160:161] neg_lo:[0,1] neg_hi:[0,1]
	v_pk_add_f32 v[114:115], v[176:177], v[188:189] neg_lo:[0,1] neg_hi:[0,1]
	v_pk_add_f32 v[98:99], v[100:101], v[98:99]
	v_pk_add_f32 v[100:101], v[168:169], v[114:115]
	v_cndmask_b32_e64 v99, v161, v99, s[42:43]
	v_cndmask_b32_e64 v101, v189, v101, s[42:43]
	v_cndmask_b32_e64 v100, v188, v100, s[42:43]
	v_cndmask_b32_e64 v98, v160, v98, s[42:43]
	global_store_dwordx4 v[110:111], v[98:101], off
	s_nop 1
	v_cvt_pk_bf16_f32 v98, v192, v193
	v_cvt_pk_bf16_f32 v99, v194, v195
	global_store_dwordx2 v[112:113], v[98:99], off
	v_mul_f32_e32 v98, 0x3fb8aa3b, v174
	v_exp_f32_e32 v98, v98
	v_pk_add_f32 v[100:101], v[176:177], v[190:191] neg_lo:[0,1] neg_hi:[0,1]
	v_sub_f32_e32 v120, 1.0, v98
	v_pk_add_f32 v[98:99], v[172:173], v[170:171] neg_lo:[0,1] neg_hi:[0,1]
	v_pk_add_f32 v[100:101], v[174:175], v[100:101]
	v_pk_add_f32 v[98:99], v[158:159], v[98:99]
	v_cndmask_b32_e64 v118, v190, v100, s[42:43]
	v_cndmask_b32_e64 v116, v170, v98, s[42:43]
	v_mul_f32_e32 v98, 0x3fb8aa3b, v175
	v_exp_f32_e32 v98, v98
	v_cndmask_b32_e64 v117, v171, v99, s[42:43]
	v_cndmask_b32_e64 v119, v191, v101, s[42:43]
	v_sub_f32_e32 v100, 1.0, v98
	v_lshlrev_b64 v[98:99], 12, v[156:157]
	v_lshl_add_u64 v[98:99], s[22:23], 0, v[98:99]
	v_lshl_add_u64 v[114:115], v[98:99], 0, v[166:167]
	global_store_dwordx4 v[114:115], v[116:119], off
	s_nop 1
	v_cvt_pk_bf16_f32 v118, v196, v210
	v_cvt_pk_bf16_f32 v119, v120, v100
	v_lshlrev_b64 v[100:101], 11, v[156:157]
	v_lshl_add_u64 v[100:101], s[0:1], 0, v[100:101]
; __device__ __forceinline__ float log_forget(float z, float lb) {
;   const float r0 = fminf(z, 0.f) - __logf(1.f + __expf(-fabsf(z)));
;   const float r1 = __logf(lb + (1.f - lb) / (1.f + __expf(-z)));
;   return lb <= 0.f ? r0 : r1;
; }
;   __device__ __forceinline__ void operator()(const f32x4 (&acc)[2][2][4][2], const pg8::Unit& u, int wr, int wc, int fr, int fq) const {
;     ...
;           for (int qh = 0; qh < 2; ++qh) { float g[4][4], cs[4][4], carry[4];
;             const f32x4 lq = qh == 0 ? l0 : l1;
; #pragma unroll
;             for (int q = 0; q < 4; ++q) carry[q] = 0.f;
; #pragma unroll
;             for (int m = 0; m < 4; ++m)
; #pragma unroll
;               for (int q = 0; q < 4; ++q) { const float gv = log_forget(acc[ai][bj][m][qh][q], lq[q]); g[m][q] = gv;
	v_lshl_add_u64 v[116:117], v[100:101], 0, v[164:165]
	global_store_dwordx2 v[116:117], v[118:119], off
	v_mul_f32_e32 v80, 0xbfb8aa3b, v80
	v_exp_f32_e32 v80, v80
	s_nop 0
	v_add_f32_e32 v80, 1.0, v80
	s_nop 0
	s_nop 1
	v_div_scale_f32 v119, s[2:3], v80, v80, v206
	v_rcp_f32_e32 v121, v119
	s_nop 0
	v_fma_f32 v156, -v119, v121, 1.0
	v_fmac_f32_e32 v121, v156, v121
	v_div_scale_f32 v156, vcc, v206, v80, v206
	v_mul_f32_e32 v157, v156, v121
	v_fma_f32 v158, -v119, v157, v156
	v_fmac_f32_e32 v157, v158, v121
	v_fma_f32 v119, -v119, v157, v156
	v_div_fmas_f32 v119, v119, v121, v157
	v_div_fixup_f32 v80, v119, v80, v206
	v_add_f32_e32 v80, v72, v80
	v_cmp_gt_f32_e32 vcc, s37, v80
	s_nop 1
	v_cndmask_b32_e64 v119, 0, 32, vcc
	v_ldexp_f32 v80, v80, v119
	v_log_f32_e32 v80, v80
	s_nop 0
	v_mul_f32_e32 v119, 0x3f317217, v80
	v_fma_f32 v119, v80, s33, -v119
	v_fmac_f32_e32 v119, 0x3377d1cf, v80
	v_fmac_f32_e32 v119, 0x3f317217, v80
	v_cmp_lt_f32_e64 s[44:45], |v80|, s36
	s_nop 1
	v_cndmask_b32_e64 v80, v80, v119, s[44:45]
	v_cndmask_b32_e32 v119, 0, v216, vcc
	v_sub_f32_e32 v168, v80, v119
	s_nop 0
	s_nop 1
	s_nop 0
	s_nop 1
	v_mul_f32_e32 v80, 0xbfb8aa3b, v81
	v_exp_f32_e32 v80, v80
	s_nop 0
	v_add_f32_e32 v80, 1.0, v80
	v_div_scale_f32 v81, s[2:3], v80, v80, v205
	v_rcp_f32_e32 v156, v81
	s_nop 0
	v_fma_f32 v157, -v81, v156, 1.0
	v_fmac_f32_e32 v156, v157, v156
	v_div_scale_f32 v157, vcc, v205, v80, v205
	v_mul_f32_e32 v158, v157, v156
	v_fma_f32 v159, -v81, v158, v157
	v_fmac_f32_e32 v158, v159, v156
	v_fma_f32 v81, -v81, v158, v157
	v_div_fmas_f32 v81, v81, v156, v158
	v_div_fixup_f32 v80, v81, v80, v205
	v_add_f32_e32 v80, v73, v80
	v_cmp_gt_f32_e32 vcc, s37, v80
	s_nop 1
	v_cndmask_b32_e64 v81, 0, 32, vcc
	v_ldexp_f32 v80, v80, v81
	v_log_f32_e32 v80, v80
	s_nop 0
	v_mul_f32_e32 v81, 0x3f317217, v80
	v_fma_f32 v81, v80, s33, -v81
	v_fmac_f32_e32 v81, 0x3377d1cf, v80
	v_fmac_f32_e32 v81, 0x3f317217, v80
	v_cmp_lt_f32_e64 s[44:45], |v80|, s36
	s_nop 1
	v_cndmask_b32_e64 v80, v80, v81, s[44:45]
	v_cndmask_b32_e32 v81, 0, v216, vcc
	v_sub_f32_e32 v169, v80, v81
	s_nop 1
	s_nop 0
	s_nop 1
	v_mul_f32_e32 v81, 0xbfb8aa3b, v82
	v_exp_f32_e32 v81, v81
	s_nop 0
	v_add_f32_e32 v81, 1.0, v81
	v_div_scale_f32 v82, s[2:3], v81, v81, v204
	v_rcp_f32_e32 v157, v82
	s_nop 0
	v_fma_f32 v158, -v82, v157, 1.0
	v_fmac_f32_e32 v157, v158, v157
	v_div_scale_f32 v158, vcc, v204, v81, v204
	v_mul_f32_e32 v159, v158, v157
	v_fma_f32 v160, -v82, v159, v158
	v_fmac_f32_e32 v159, v160, v157
	v_fma_f32 v82, -v82, v159, v158
	v_div_fmas_f32 v82, v82, v157, v159
	v_div_fixup_f32 v81, v82, v81, v204
	v_add_f32_e32 v81, v74, v81
	v_cmp_gt_f32_e32 vcc, s37, v81
	s_nop 1
	v_cndmask_b32_e64 v82, 0, 32, vcc
	v_ldexp_f32 v81, v81, v82
	v_log_f32_e32 v81, v81
	s_nop 0
	v_mul_f32_e32 v82, 0x3f317217, v81
	v_fma_f32 v82, v81, s33, -v82
	v_fmac_f32_e32 v82, 0x3377d1cf, v81
	v_fmac_f32_e32 v82, 0x3f317217, v81
	v_cmp_lt_f32_e64 s[44:45], |v81|, s36
	s_nop 1
	v_cndmask_b32_e64 v81, v81, v82, s[44:45]
	v_cndmask_b32_e32 v82, 0, v216, vcc
	v_sub_f32_e32 v170, v81, v82
	s_nop 1
	s_nop 0
	s_nop 1
	v_mul_f32_e32 v82, 0xbfb8aa3b, v83
	v_exp_f32_e32 v82, v82
	s_nop 0
	v_add_f32_e32 v82, 1.0, v82
	v_div_scale_f32 v83, s[2:3], v82, v82, v96
	v_rcp_f32_e32 v158, v83
	v_mov_b32_e32 v80, v170
	v_fma_f32 v159, -v83, v158, 1.0
	v_fmac_f32_e32 v158, v159, v158
	v_div_scale_f32 v159, vcc, v96, v82, v96
	v_mul_f32_e32 v160, v159, v158
	v_fma_f32 v161, -v83, v160, v159
	v_fmac_f32_e32 v160, v161, v158
	v_fma_f32 v83, -v83, v160, v159
	v_div_fmas_f32 v83, v83, v158, v160
	v_div_fixup_f32 v82, v83, v82, v96
	v_add_f32_e32 v82, v75, v82
	v_cmp_gt_f32_e32 vcc, s37, v82
	s_nop 1
	v_cndmask_b32_e64 v83, 0, 32, vcc
	v_ldexp_f32 v82, v82, v83
	v_log_f32_e32 v82, v82
	s_nop 0
	v_mul_f32_e32 v83, 0x3f317217, v82
	v_fma_f32 v83, v82, s33, -v83
	v_fmac_f32_e32 v83, 0x3377d1cf, v82
	v_fmac_f32_e32 v83, 0x3f317217, v82
	v_cmp_lt_f32_e64 s[44:45], |v82|, s36
	s_nop 1
	v_cndmask_b32_e64 v82, v82, v83, s[44:45]
	v_cndmask_b32_e32 v83, 0, v216, vcc
	v_sub_f32_e32 v171, v82, v83
	v_mul_f32_e32 v76, 0xbfb8aa3b, v76
	v_exp_f32_e32 v76, v76
	v_mov_b32_e32 v81, v171
	v_add_f32_e32 v76, 1.0, v76
	s_nop 1
	v_div_scale_f32 v83, s[2:3], v76, v76, v206
	v_rcp_f32_e32 v159, v83
	s_nop 0
	v_fma_f32 v160, -v83, v159, 1.0
	v_fmac_f32_e32 v159, v160, v159
	v_div_scale_f32 v160, vcc, v206, v76, v206
	v_mul_f32_e32 v161, v160, v159
	v_fma_f32 v162, -v83, v161, v160
	v_fmac_f32_e32 v161, v162, v159
	v_fma_f32 v83, -v83, v161, v160
	v_div_fmas_f32 v83, v83, v159, v161
	v_div_fixup_f32 v76, v83, v76, v206
	v_add_f32_e32 v76, v72, v76
	v_cmp_gt_f32_e32 vcc, s37, v76
	s_nop 1
	v_cndmask_b32_e64 v83, 0, 32, vcc
	v_ldexp_f32 v76, v76, v83
	v_log_f32_e32 v76, v76
	s_nop 0
	v_mul_f32_e32 v83, 0x3f317217, v76
	v_fma_f32 v83, v76, s33, -v83
	v_fmac_f32_e32 v83, 0x3377d1cf, v76
	v_fmac_f32_e32 v83, 0x3f317217, v76
	v_cmp_lt_f32_e64 s[44:45], |v76|, s36
	s_nop 1
	v_cndmask_b32_e64 v76, v76, v83, s[44:45]
	v_cndmask_b32_e32 v83, 0, v216, vcc
	v_sub_f32_e32 v172, v76, v83
	s_nop 0
	s_nop 1
	s_nop 0
	s_nop 1
	v_mul_f32_e32 v76, 0xbfb8aa3b, v77
	v_exp_f32_e32 v76, v76
	s_nop 0
	v_add_f32_e32 v76, 1.0, v76
	v_div_scale_f32 v77, s[2:3], v76, v76, v205
	v_rcp_f32_e32 v160, v77
	v_mov_b32_e32 v82, v172
	v_fma_f32 v161, -v77, v160, 1.0
	v_fmac_f32_e32 v160, v161, v160
	v_div_scale_f32 v161, vcc, v205, v76, v205
	v_mul_f32_e32 v162, v161, v160
	v_fma_f32 v163, -v77, v162, v161
	v_fmac_f32_e32 v162, v163, v160
	v_fma_f32 v77, -v77, v162, v161
	v_div_fmas_f32 v77, v77, v160, v162
	v_div_fixup_f32 v76, v77, v76, v205
	v_add_f32_e32 v76, v73, v76
; template <int CTRL> __device__ __forceinline__ float dppx(float v) { return __int_as_float(__builtin_amdgcn_update_dpp(0, __float_as_int(v), CTRL, 0xf, 0xf, true)); }
; __device__ __forceinline__ float log_forget(float z, float lb) {
;   const float r0 = fminf(z, 0.f) - __logf(1.f + __expf(-fabsf(z)));
;   const float r1 = __logf(lb + (1.f - lb) / (1.f + __expf(-z)));
;   return lb <= 0.f ? r0 : r1;
; }
;   __device__ __forceinline__ void operator()(const f32x4 (&acc)[2][2][4][2], const pg8::Unit& u, int wr, int wc, int fr, int fq) const {
;     ...
;           for (int qh = 0; qh < 2; ++qh) { float g[4][4], cs[4][4], carry[4];
;             const f32x4 lq = qh == 0 ? l0 : l1;
; #pragma unroll
;             for (int q = 0; q < 4; ++q) carry[q] = 0.f;
; #pragma unroll
;             for (int m = 0; m < 4; ++m)
; #pragma unroll
;               for (int q = 0; q < 4; ++q) { const float gv = log_forget(acc[ai][bj][m][qh][q], lq[q]); g[m][q] = gv;
;                 float sc = gv; sc += dppx<0x111>(sc); sc += dppx<0x112>(sc); sc += dppx<0x114>(sc); sc += dppx<0x118>(sc);
	v_cmp_gt_f32_e32 vcc, s37, v76
	s_nop 1
	v_cndmask_b32_e64 v77, 0, 32, vcc
	v_ldexp_f32 v76, v76, v77
	v_log_f32_e32 v76, v76
	s_nop 0
	v_mul_f32_e32 v77, 0x3f317217, v76
	v_fma_f32 v77, v76, s33, -v77
	v_fmac_f32_e32 v77, 0x3377d1cf, v76
	v_fmac_f32_e32 v77, 0x3f317217, v76
	v_cmp_lt_f32_e64 s[44:45], |v76|, s36
	s_nop 1
	v_cndmask_b32_e64 v76, v76, v77, s[44:45]
	v_cndmask_b32_e32 v77, 0, v216, vcc
	v_sub_f32_e32 v173, v76, v77
	v_mov_b32_e32 v83, v173
	s_nop 1
	s_nop 0
	s_nop 1
	v_mul_f32_e32 v77, 0xbfb8aa3b, v78
	v_exp_f32_e32 v77, v77
	s_nop 0
	v_add_f32_e32 v77, 1.0, v77
	v_div_scale_f32 v78, s[2:3], v77, v77, v204
	v_rcp_f32_e32 v161, v78
	s_nop 0
	v_fma_f32 v162, -v78, v161, 1.0
	v_fmac_f32_e32 v161, v162, v161
	v_div_scale_f32 v162, vcc, v204, v77, v204
	v_mul_f32_e32 v163, v162, v161
	v_fma_f32 v164, -v78, v163, v162
	v_fmac_f32_e32 v163, v164, v161
	v_fma_f32 v78, -v78, v163, v162
	v_div_fmas_f32 v78, v78, v161, v163
	v_div_fixup_f32 v77, v78, v77, v204
	v_add_f32_e32 v77, v74, v77
	v_cmp_gt_f32_e32 vcc, s37, v77
	s_nop 1
	v_cndmask_b32_e64 v78, 0, 32, vcc
	v_ldexp_f32 v77, v77, v78
	v_log_f32_e32 v77, v77
	s_nop 0
	v_mul_f32_e32 v78, 0x3f317217, v77
	v_fma_f32 v78, v77, s33, -v78
	v_fmac_f32_e32 v78, 0x3377d1cf, v77
	v_fmac_f32_e32 v78, 0x3f317217, v77
	v_cmp_lt_f32_e64 s[44:45], |v77|, s36
	s_nop 1
	v_cndmask_b32_e64 v77, v77, v78, s[44:45]
	v_cndmask_b32_e32 v78, 0, v216, vcc
	v_sub_f32_e32 v174, v77, v78
	s_nop 1
	s_nop 0
	s_nop 1
	v_mul_f32_e32 v78, 0xbfb8aa3b, v79
	v_exp_f32_e32 v78, v78
	s_nop 0
	v_add_f32_e32 v78, 1.0, v78
	v_div_scale_f32 v79, s[2:3], v78, v78, v96
	v_rcp_f32_e32 v162, v79
	v_mov_b32_e32 v76, v174
	v_fma_f32 v163, -v79, v162, 1.0
	v_fmac_f32_e32 v162, v163, v162
	v_div_scale_f32 v163, vcc, v96, v78, v96
	v_mul_f32_e32 v164, v163, v162
	v_fma_f32 v165, -v79, v164, v163
	v_fmac_f32_e32 v164, v165, v162
	v_fma_f32 v79, -v79, v164, v163
	v_div_fmas_f32 v79, v79, v162, v164
	v_div_fixup_f32 v78, v79, v78, v96
	v_add_f32_e32 v78, v75, v78
	v_cmp_gt_f32_e32 vcc, s37, v78
	s_nop 1
	v_cndmask_b32_e64 v79, 0, 32, vcc
	v_ldexp_f32 v78, v78, v79
	v_log_f32_e32 v78, v78
	s_nop 0
	v_mul_f32_e32 v79, 0x3f317217, v78
	v_fma_f32 v79, v78, s33, -v79
	v_fmac_f32_e32 v79, 0x3377d1cf, v78
	v_fmac_f32_e32 v79, 0x3f317217, v78
	v_cmp_lt_f32_e64 s[44:45], |v78|, s36
	s_nop 1
	v_cndmask_b32_e64 v78, v78, v79, s[44:45]
	v_cndmask_b32_e32 v79, 0, v216, vcc
	v_sub_f32_e32 v175, v78, v79
	v_mul_f32_e32 v68, 0xbfb8aa3b, v68
	v_exp_f32_e32 v68, v68
	v_mov_b32_e32 v77, v175
	v_add_f32_e32 v68, 1.0, v68
	s_nop 1
	v_div_scale_f32 v79, s[2:3], v68, v68, v206
	v_rcp_f32_e32 v163, v79
	s_nop 0
	v_fma_f32 v164, -v79, v163, 1.0
	v_fmac_f32_e32 v163, v164, v163
	v_div_scale_f32 v164, vcc, v206, v68, v206
	v_mul_f32_e32 v165, v164, v163
	v_fma_f32 v166, -v79, v165, v164
	v_fmac_f32_e32 v165, v166, v163
	v_fma_f32 v79, -v79, v165, v164
	v_div_fmas_f32 v79, v79, v163, v165
	v_div_fixup_f32 v68, v79, v68, v206
	v_add_f32_e32 v68, v72, v68
	v_cmp_gt_f32_e32 vcc, s37, v68
	s_nop 1
	v_cndmask_b32_e64 v79, 0, 32, vcc
	v_ldexp_f32 v68, v68, v79
	v_log_f32_e32 v68, v68
	s_nop 0
	v_mul_f32_e32 v79, 0x3f317217, v68
	v_fma_f32 v79, v68, s33, -v79
	v_fmac_f32_e32 v79, 0x3377d1cf, v68
	v_fmac_f32_e32 v79, 0x3f317217, v68
	v_cmp_lt_f32_e64 s[44:45], |v68|, s36
	s_nop 1
	v_cndmask_b32_e64 v68, v68, v79, s[44:45]
	v_cndmask_b32_e32 v79, 0, v216, vcc
	v_sub_f32_e32 v176, v68, v79
	s_nop 0
	s_nop 1
	s_nop 0
	s_nop 1
	v_mul_f32_e32 v68, 0xbfb8aa3b, v69
	v_exp_f32_e32 v68, v68
	s_nop 0
	v_add_f32_e32 v68, 1.0, v68
	v_div_scale_f32 v69, s[2:3], v68, v68, v205
	v_rcp_f32_e32 v164, v69
	v_mov_b32_e32 v78, v176
	v_fma_f32 v165, -v69, v164, 1.0
	v_fmac_f32_e32 v164, v165, v164
	v_div_scale_f32 v165, vcc, v205, v68, v205
	v_mul_f32_e32 v166, v165, v164
	v_fma_f32 v167, -v69, v166, v165
	v_fmac_f32_e32 v166, v167, v164
	v_fma_f32 v69, -v69, v166, v165
	v_div_fmas_f32 v69, v69, v164, v166
	v_div_fixup_f32 v68, v69, v68, v205
	v_add_f32_e32 v68, v73, v68
	v_cmp_gt_f32_e32 vcc, s37, v68
	v_mov_b32_dpp v162, v78 row_shr:1 row_mask:0xf bank_mask:0xf bound_ctrl:1
	s_nop 0
	v_cndmask_b32_e64 v69, 0, 32, vcc
	v_ldexp_f32 v68, v68, v69
	v_log_f32_e32 v68, v68
	s_nop 0
	v_mul_f32_e32 v69, 0x3f317217, v68
	v_fma_f32 v69, v68, s33, -v69
	v_fmac_f32_e32 v69, 0x3377d1cf, v68
	v_fmac_f32_e32 v69, 0x3f317217, v68
	v_cmp_lt_f32_e64 s[44:45], |v68|, s36
	s_nop 1
	v_cndmask_b32_e64 v68, v68, v69, s[44:45]
	v_cndmask_b32_e32 v69, 0, v216, vcc
	v_sub_f32_e32 v177, v68, v69
	v_mov_b32_e32 v79, v177
	s_nop 1
	v_mov_b32_dpp v163, v79 row_shr:1 row_mask:0xf bank_mask:0xf bound_ctrl:1
	v_pk_add_f32 v[162:163], v[78:79], v[162:163]
	s_nop 0
	s_nop 1
	v_mul_f32_e32 v69, 0xbfb8aa3b, v70
	v_exp_f32_e32 v69, v69
	s_nop 0
	v_add_f32_e32 v69, 1.0, v69
	v_div_scale_f32 v70, s[2:3], v69, v69, v204
	v_rcp_f32_e32 v165, v70
	s_nop 0
	v_fma_f32 v166, -v70, v165, 1.0
	v_fmac_f32_e32 v165, v166, v165
	v_div_scale_f32 v166, vcc, v204, v69, v204
	v_mul_f32_e32 v167, v166, v165
	v_fma_f32 v180, -v70, v167, v166
	v_fmac_f32_e32 v167, v180, v165
	v_fma_f32 v70, -v70, v167, v166
	v_div_fmas_f32 v70, v70, v165, v167
	v_div_fixup_f32 v69, v70, v69, v204
	v_add_f32_e32 v69, v74, v69
	v_cmp_gt_f32_e32 vcc, s37, v69
	s_nop 1
	v_cndmask_b32_e64 v70, 0, 32, vcc
	v_ldexp_f32 v69, v69, v70
	v_log_f32_e32 v69, v69
	s_nop 0
	v_mul_f32_e32 v70, 0x3f317217, v69
	v_fma_f32 v70, v69, s33, -v70
	v_fmac_f32_e32 v70, 0x3377d1cf, v69
	v_fmac_f32_e32 v70, 0x3f317217, v69
	v_cmp_lt_f32_e64 s[44:45], |v69|, s36
	s_nop 1
	v_cndmask_b32_e64 v69, v69, v70, s[44:45]
	v_cndmask_b32_e32 v70, 0, v216, vcc
	v_sub_f32_e32 v180, v69, v70
; template <int CTRL> __device__ __forceinline__ float dppx(float v) { return __int_as_float(__builtin_amdgcn_update_dpp(0, __float_as_int(v), CTRL, 0xf, 0xf, true)); }
; __device__ __forceinline__ float log_forget(float z, float lb) {
;   const float r0 = fminf(z, 0.f) - __logf(1.f + __expf(-fabsf(z)));
;   const float r1 = __logf(lb + (1.f - lb) / (1.f + __expf(-z)));
;   return lb <= 0.f ? r0 : r1;
; }
;   __device__ __forceinline__ void operator()(const f32x4 (&acc)[2][2][4][2], const pg8::Unit& u, int wr, int wc, int fr, int fq) const {
;     ...
;           for (int qh = 0; qh < 2; ++qh) { float g[4][4], cs[4][4], carry[4];
;             const f32x4 lq = qh == 0 ? l0 : l1;
; #pragma unroll
;             for (int q = 0; q < 4; ++q) carry[q] = 0.f;
; #pragma unroll
;             for (int m = 0; m < 4; ++m)
; #pragma unroll
;               for (int q = 0; q < 4; ++q) { const float gv = log_forget(acc[ai][bj][m][qh][q], lq[q]); g[m][q] = gv;
;                 float sc = gv; sc += dppx<0x111>(sc); sc += dppx<0x112>(sc); sc += dppx<0x114>(sc); sc += dppx<0x118>(sc);
;                 const float tot16 = __int_as_float(__builtin_amdgcn_ds_swizzle(__float_as_int(sc), 0x1F0));
;                 cs[m][q] = sc + carry[q]; carry[q] += tot16; }
	s_nop 1
	s_nop 0
	s_nop 1
	v_mul_f32_e32 v70, 0xbfb8aa3b, v71
	v_exp_f32_e32 v70, v70
	s_nop 0
	v_add_f32_e32 v70, 1.0, v70
	v_div_scale_f32 v71, s[2:3], v70, v70, v96
	v_rcp_f32_e32 v166, v71
	v_mov_b32_e32 v68, v180
	v_fma_f32 v167, -v71, v166, 1.0
	v_fmac_f32_e32 v166, v167, v166
	v_div_scale_f32 v167, vcc, v96, v70, v96
	v_mul_f32_e32 v181, v167, v166
	v_fma_f32 v182, -v71, v181, v167
	v_fmac_f32_e32 v181, v182, v166
	v_fma_f32 v71, -v71, v181, v167
	v_div_fmas_f32 v71, v71, v166, v181
	v_div_fixup_f32 v70, v71, v70, v96
	v_add_f32_e32 v70, v75, v70
	v_cmp_gt_f32_e32 vcc, s37, v70
	v_mov_b32_dpp v164, v68 row_shr:1 row_mask:0xf bank_mask:0xf bound_ctrl:1
	s_nop 0
	v_cndmask_b32_e64 v71, 0, 32, vcc
	v_ldexp_f32 v70, v70, v71
	v_log_f32_e32 v70, v70
	s_nop 0
	v_mul_f32_e32 v71, 0x3f317217, v70
	v_fma_f32 v71, v70, s33, -v71
	v_fmac_f32_e32 v71, 0x3377d1cf, v70
	v_fmac_f32_e32 v71, 0x3f317217, v70
	v_cmp_lt_f32_e64 s[44:45], |v70|, s36
	s_nop 1
	v_cndmask_b32_e64 v70, v70, v71, s[44:45]
	v_cndmask_b32_e32 v71, 0, v216, vcc
	v_sub_f32_e32 v181, v70, v71
	v_mul_f32_e32 v64, 0xbfb8aa3b, v64
	v_exp_f32_e32 v64, v64
	v_mov_b32_e32 v69, v181
	v_add_f32_e32 v64, 1.0, v64
	s_nop 0
	v_mov_b32_dpp v165, v69 row_shr:1 row_mask:0xf bank_mask:0xf bound_ctrl:1
	v_pk_add_f32 v[164:165], v[68:69], v[164:165]
	s_nop 1
	v_div_scale_f32 v71, s[2:3], v64, v64, v206
	v_rcp_f32_e32 v167, v71
	s_nop 0
	v_fma_f32 v182, -v71, v167, 1.0
	v_fmac_f32_e32 v167, v182, v167
	v_div_scale_f32 v182, vcc, v206, v64, v206
	v_mul_f32_e32 v183, v182, v167
	v_fma_f32 v184, -v71, v183, v182
	v_fmac_f32_e32 v183, v184, v167
	v_fma_f32 v71, -v71, v183, v182
	v_div_fmas_f32 v71, v71, v167, v183
	v_div_fixup_f32 v64, v71, v64, v206
	v_add_f32_e32 v64, v72, v64
	v_cmp_gt_f32_e32 vcc, s37, v64
	s_nop 1
	v_cndmask_b32_e64 v71, 0, 32, vcc
	v_ldexp_f32 v64, v64, v71
	v_log_f32_e32 v64, v64
	s_nop 0
	v_mul_f32_e32 v71, 0x3f317217, v64
	v_fma_f32 v71, v64, s33, -v71
	v_fmac_f32_e32 v71, 0x3377d1cf, v64
	v_fmac_f32_e32 v71, 0x3f317217, v64
	v_cmp_lt_f32_e64 s[44:45], |v64|, s36
	s_nop 1
	v_cndmask_b32_e64 v64, v64, v71, s[44:45]
	v_cndmask_b32_e32 v71, 0, v216, vcc
	v_sub_f32_e32 v182, v64, v71
	s_nop 0
	s_nop 1
	s_nop 0
	s_nop 1
	v_mul_f32_e32 v64, 0xbfb8aa3b, v65
	v_exp_f32_e32 v64, v64
	s_nop 0
	v_add_f32_e32 v64, 1.0, v64
	v_div_scale_f32 v65, s[2:3], v64, v64, v205
	v_rcp_f32_e32 v72, v65
	v_mov_b32_e32 v70, v182
	v_fma_f32 v183, -v65, v72, 1.0
	v_fmac_f32_e32 v72, v183, v72
	v_div_scale_f32 v183, vcc, v205, v64, v205
	v_mul_f32_e32 v184, v183, v72
	v_fma_f32 v185, -v65, v184, v183
	v_fmac_f32_e32 v184, v185, v72
	v_fma_f32 v65, -v65, v184, v183
	v_div_fmas_f32 v65, v65, v72, v184
	v_div_fixup_f32 v64, v65, v64, v205
	v_add_f32_e32 v64, v73, v64
	v_cmp_gt_f32_e32 vcc, s37, v64
	v_mov_b32_dpp v166, v70 row_shr:1 row_mask:0xf bank_mask:0xf bound_ctrl:1
	s_nop 0
	v_cndmask_b32_e64 v65, 0, 32, vcc
	v_ldexp_f32 v64, v64, v65
	v_log_f32_e32 v64, v64
	s_nop 0
	v_mul_f32_e32 v65, 0x3f317217, v64
	v_fma_f32 v65, v64, s33, -v65
	v_fmac_f32_e32 v65, 0x3377d1cf, v64
	v_fmac_f32_e32 v65, 0x3f317217, v64
	v_cmp_lt_f32_e64 s[44:45], |v64|, s36
	s_nop 1
	v_cndmask_b32_e64 v64, v64, v65, s[44:45]
	v_cndmask_b32_e32 v65, 0, v216, vcc
	v_sub_f32_e32 v183, v64, v65
	v_mov_b32_e32 v71, v183
	s_nop 1
	v_mov_b32_dpp v167, v71 row_shr:1 row_mask:0xf bank_mask:0xf bound_ctrl:1
	v_pk_add_f32 v[166:167], v[70:71], v[166:167]
	s_nop 0
	s_nop 1
	v_mul_f32_e32 v65, 0xbfb8aa3b, v66
	v_exp_f32_e32 v65, v65
	s_nop 0
	v_add_f32_e32 v65, 1.0, v65
	v_div_scale_f32 v66, s[2:3], v65, v65, v204
	v_rcp_f32_e32 v73, v66
	s_nop 0
	v_fma_f32 v184, -v66, v73, 1.0
	v_fmac_f32_e32 v73, v184, v73
	v_div_scale_f32 v184, vcc, v204, v65, v204
	v_mul_f32_e32 v185, v184, v73
	v_fma_f32 v186, -v66, v185, v184
	v_fmac_f32_e32 v185, v186, v73
	v_fma_f32 v66, -v66, v185, v184
	v_div_fmas_f32 v66, v66, v73, v185
	v_div_fixup_f32 v65, v66, v65, v204
	v_add_f32_e32 v65, v74, v65
	v_cmp_gt_f32_e32 vcc, s37, v65
	s_nop 1
	v_cndmask_b32_e64 v66, 0, 32, vcc
	v_ldexp_f32 v65, v65, v66
	v_log_f32_e32 v65, v65
	s_nop 0
	v_mul_f32_e32 v66, 0x3f317217, v65
	v_fma_f32 v66, v65, s33, -v66
	v_fmac_f32_e32 v66, 0x3377d1cf, v65
	v_fmac_f32_e32 v66, 0x3f317217, v65
	v_cmp_lt_f32_e64 s[44:45], |v65|, s36
	s_nop 1
	v_cndmask_b32_e64 v65, v65, v66, s[44:45]
	v_cndmask_b32_e32 v66, 0, v216, vcc
	v_sub_f32_e32 v184, v65, v66
	s_nop 1
	s_nop 0
	s_nop 1
	v_mul_f32_e32 v66, 0xbfb8aa3b, v67
	v_exp_f32_e32 v66, v66
	s_nop 0
	v_add_f32_e32 v66, 1.0, v66
	v_div_scale_f32 v67, s[2:3], v66, v66, v96
	v_rcp_f32_e32 v74, v67
	v_mov_b32_e32 v72, v184
	v_fma_f32 v185, -v67, v74, 1.0
	v_fmac_f32_e32 v74, v185, v74
	v_div_scale_f32 v185, vcc, v96, v66, v96
	v_mul_f32_e32 v186, v185, v74
	v_fma_f32 v187, -v67, v186, v185
	v_fmac_f32_e32 v186, v187, v74
	v_fma_f32 v67, -v67, v186, v185
	v_div_fmas_f32 v67, v67, v74, v186
	v_div_fixup_f32 v66, v67, v66, v96
	v_add_f32_e32 v66, v75, v66
	v_cmp_gt_f32_e32 vcc, s37, v66
	v_mov_b32_dpp v64, v72 row_shr:1 row_mask:0xf bank_mask:0xf bound_ctrl:1
	s_nop 0
	v_cndmask_b32_e64 v67, 0, 32, vcc
	v_ldexp_f32 v66, v66, v67
	v_log_f32_e32 v66, v66
	s_nop 0
	v_mul_f32_e32 v67, 0x3f317217, v66
	v_fma_f32 v67, v66, s33, -v67
	v_fmac_f32_e32 v67, 0x3377d1cf, v66
	v_fmac_f32_e32 v67, 0x3f317217, v66
	v_cmp_lt_f32_e64 s[44:45], |v66|, s36
	s_nop 1
	v_cndmask_b32_e64 v66, v66, v67, s[44:45]
	v_cndmask_b32_e32 v67, 0, v216, vcc
	v_sub_f32_e32 v96, v66, v67
	v_mov_b32_e32 v73, v96
	v_mov_b32_e32 v67, v169
	v_mov_b32_e32 v66, v168
	v_mov_b32_dpp v65, v73 row_shr:1 row_mask:0xf bank_mask:0xf bound_ctrl:1
	v_mov_b32_dpp v75, v67 row_shr:1 row_mask:0xf bank_mask:0xf bound_ctrl:1
	v_mov_b32_dpp v74, v66 row_shr:1 row_mask:0xf bank_mask:0xf bound_ctrl:1
	v_pk_add_f32 v[74:75], v[66:67], v[74:75]
	v_pk_add_f32 v[64:65], v[72:73], v[64:65]
	v_add_u32_e32 v96, 0xfffffc80, v154
	v_mov_b32_dpp v118, v74 row_shr:2 row_mask:0xf bank_mask:0xf bound_ctrl:1
	v_mov_b32_dpp v119, v75 row_shr:2 row_mask:0xf bank_mask:0xf bound_ctrl:1
	v_pk_add_f32 v[74:75], v[74:75], v[118:119]
	s_nop 1
	v_mov_b32_dpp v118, v74 row_shr:4 row_mask:0xf bank_mask:0xf bound_ctrl:1
	v_mov_b32_dpp v119, v75 row_shr:4 row_mask:0xf bank_mask:0xf bound_ctrl:1
	v_pk_add_f32 v[74:75], v[74:75], v[118:119]
	s_nop 1
	v_mov_b32_dpp v118, v74 row_shr:8 row_mask:0xf bank_mask:0xf bound_ctrl:1
	v_mov_b32_dpp v119, v75 row_shr:8 row_mask:0xf bank_mask:0xf bound_ctrl:1
	v_pk_add_f32 v[74:75], v[74:75], v[118:119]
	ds_swizzle_b32 v118, v74 offset:swizzle(BROADCAST,16,15)
	ds_swizzle_b32 v119, v75 offset:swizzle(BROADCAST,16,15)
	v_pk_add_f32 v[74:75], v[74:75], 0 op_sel_hi:[1,0]
	s_waitcnt lgkmcnt(0)
; template <int CTRL> __device__ __forceinline__ float dppx(float v) { return __int_as_float(__builtin_amdgcn_update_dpp(0, __float_as_int(v), CTRL, 0xf, 0xf, true)); }
;   __device__ __forceinline__ void operator()(const f32x4 (&acc)[2][2][4][2], const pg8::Unit& u, int wr, int wc, int fr, int fq) const {
;     ...
;               for (int q = 0; q < 4; ++q) { const float gv = log_forget(acc[ai][bj][m][qh][q], lq[q]); g[m][q] = gv;
;                 float sc = gv; sc += dppx<0x111>(sc); sc += dppx<0x112>(sc); sc += dppx<0x114>(sc); sc += dppx<0x118>(sc);
;                 const float tot16 = __int_as_float(__builtin_amdgcn_ds_swizzle(__float_as_int(sc), 0x1F0));
;                 cs[m][q] = sc + carry[q]; carry[q] += tot16; }
; #pragma unroll
;             for (int m = 0; m < 4; ++m) { const int r = row0 + ai * 128 + m * 16; float bq[4], kq[4];
; #pragma unroll
;               for (int q = 0; q < 4; ++q) { bq[q] = bwd ? (carry[q] - cs[m][q]) + g[m][q] : cs[m][q]; kq[q] = 1.f - __expf(g[m][q]); }
	v_pk_add_f32 v[168:169], v[118:119], 0 op_sel_hi:[1,0]
	v_mul_f32_e32 v118, 0x3fb8aa3b, v66
	v_exp_f32_e32 v118, v118
	v_mov_b32_dpp v119, v81 row_shr:1 row_mask:0xf bank_mask:0xf bound_ctrl:1
	v_sub_f32_e32 v185, 1.0, v118
	v_mul_f32_e32 v118, 0x3fb8aa3b, v67
	v_exp_f32_e32 v118, v118
	s_nop 0
	v_sub_f32_e32 v186, 1.0, v118
	v_mov_b32_dpp v118, v80 row_shr:1 row_mask:0xf bank_mask:0xf bound_ctrl:1
	v_pk_add_f32 v[118:119], v[80:81], v[118:119]
	s_nop 1
	v_mov_b32_dpp v120, v118 row_shr:2 row_mask:0xf bank_mask:0xf bound_ctrl:1
	v_mov_b32_dpp v121, v119 row_shr:2 row_mask:0xf bank_mask:0xf bound_ctrl:1
	v_pk_add_f32 v[118:119], v[118:119], v[120:121]
	s_nop 1
	v_mov_b32_dpp v120, v118 row_shr:4 row_mask:0xf bank_mask:0xf bound_ctrl:1
	v_mov_b32_dpp v121, v119 row_shr:4 row_mask:0xf bank_mask:0xf bound_ctrl:1
	v_pk_add_f32 v[118:119], v[118:119], v[120:121]
	s_nop 1
	v_mov_b32_dpp v120, v118 row_shr:8 row_mask:0xf bank_mask:0xf bound_ctrl:1
	v_mov_b32_dpp v121, v119 row_shr:8 row_mask:0xf bank_mask:0xf bound_ctrl:1
	v_pk_add_f32 v[118:119], v[118:119], v[120:121]
	ds_swizzle_b32 v120, v118 offset:swizzle(BROADCAST,16,15)
	ds_swizzle_b32 v121, v119 offset:swizzle(BROADCAST,16,15)
	v_pk_add_f32 v[118:119], v[118:119], 0 op_sel_hi:[1,0]
	s_waitcnt lgkmcnt(0)
	v_pk_add_f32 v[170:171], v[120:121], 0 op_sel_hi:[1,0]
	v_mul_f32_e32 v120, 0x3fb8aa3b, v80
	v_exp_f32_e32 v120, v120
	v_mov_b32_dpp v121, v83 row_shr:1 row_mask:0xf bank_mask:0xf bound_ctrl:1
	v_sub_f32_e32 v187, 1.0, v120
	v_mul_f32_e32 v120, 0x3fb8aa3b, v81
	v_exp_f32_e32 v120, v120
	s_nop 0
	v_sub_f32_e32 v188, 1.0, v120
	v_mov_b32_dpp v120, v82 row_shr:1 row_mask:0xf bank_mask:0xf bound_ctrl:1
	v_pk_add_f32 v[120:121], v[82:83], v[120:121]
	s_nop 1
	v_mov_b32_dpp v156, v120 row_shr:2 row_mask:0xf bank_mask:0xf bound_ctrl:1
	v_mov_b32_dpp v157, v121 row_shr:2 row_mask:0xf bank_mask:0xf bound_ctrl:1
	v_pk_add_f32 v[120:121], v[120:121], v[156:157]
	s_nop 1
	v_mov_b32_dpp v156, v120 row_shr:4 row_mask:0xf bank_mask:0xf bound_ctrl:1
	v_mov_b32_dpp v157, v121 row_shr:4 row_mask:0xf bank_mask:0xf bound_ctrl:1
	v_pk_add_f32 v[120:121], v[120:121], v[156:157]
	s_nop 1
	v_mov_b32_dpp v156, v120 row_shr:8 row_mask:0xf bank_mask:0xf bound_ctrl:1
	v_mov_b32_dpp v157, v121 row_shr:8 row_mask:0xf bank_mask:0xf bound_ctrl:1
	v_pk_add_f32 v[120:121], v[120:121], v[156:157]
	ds_swizzle_b32 v156, v120 offset:swizzle(BROADCAST,16,15)
	ds_swizzle_b32 v157, v121 offset:swizzle(BROADCAST,16,15)
	v_pk_add_f32 v[120:121], v[168:169], v[120:121]
	s_waitcnt lgkmcnt(0)
	v_pk_add_f32 v[158:159], v[168:169], v[156:157]
	v_mul_f32_e32 v168, 0x3fb8aa3b, v76
	v_exp_f32_e32 v168, v168
	v_mov_b32_dpp v169, v163 row_shr:2 row_mask:0xf bank_mask:0xf bound_ctrl:1
	v_mul_f32_e32 v156, 0x3fb8aa3b, v82
	v_exp_f32_e32 v156, v156
	v_sub_f32_e32 v174, 1.0, v168
	v_mul_f32_e32 v168, 0x3fb8aa3b, v77
	v_exp_f32_e32 v168, v168
	v_sub_f32_e32 v172, 1.0, v156
	v_mul_f32_e32 v156, 0x3fb8aa3b, v83
	v_exp_f32_e32 v156, v156
	v_sub_f32_e32 v175, 1.0, v168
	v_mov_b32_dpp v168, v162 row_shr:2 row_mask:0xf bank_mask:0xf bound_ctrl:1
	v_pk_add_f32 v[162:163], v[162:163], v[168:169]
	v_sub_f32_e32 v173, 1.0, v156
	v_mov_b32_dpp v156, v76 row_shr:1 row_mask:0xf bank_mask:0xf bound_ctrl:1
	v_mov_b32_dpp v168, v162 row_shr:4 row_mask:0xf bank_mask:0xf bound_ctrl:1
	v_mov_b32_dpp v169, v163 row_shr:4 row_mask:0xf bank_mask:0xf bound_ctrl:1
	v_pk_add_f32 v[162:163], v[162:163], v[168:169]
	v_mov_b32_dpp v157, v77 row_shr:1 row_mask:0xf bank_mask:0xf bound_ctrl:1
	v_pk_add_f32 v[156:157], v[76:77], v[156:157]
	v_mov_b32_dpp v168, v162 row_shr:8 row_mask:0xf bank_mask:0xf bound_ctrl:1
	v_mov_b32_dpp v169, v163 row_shr:8 row_mask:0xf bank_mask:0xf bound_ctrl:1
	v_pk_add_f32 v[162:163], v[162:163], v[168:169]
	ds_swizzle_b32 v168, v162 offset:swizzle(BROADCAST,16,15)
	ds_swizzle_b32 v169, v163 offset:swizzle(BROADCAST,16,15)
	v_pk_add_f32 v[162:163], v[158:159], v[162:163]
	v_mov_b32_dpp v160, v156 row_shr:2 row_mask:0xf bank_mask:0xf bound_ctrl:1
	v_mov_b32_dpp v161, v157 row_shr:2 row_mask:0xf bank_mask:0xf bound_ctrl:1
	v_pk_add_f32 v[156:157], v[156:157], v[160:161]
	s_waitcnt lgkmcnt(0)
	v_pk_add_f32 v[158:159], v[158:159], v[168:169]
	v_mul_f32_e32 v168, 0x3fb8aa3b, v78
	v_exp_f32_e32 v168, v168
	v_mov_b32_dpp v169, v165 row_shr:2 row_mask:0xf bank_mask:0xf bound_ctrl:1
	v_mov_b32_dpp v160, v156 row_shr:4 row_mask:0xf bank_mask:0xf bound_ctrl:1
	v_mov_b32_dpp v161, v157 row_shr:4 row_mask:0xf bank_mask:0xf bound_ctrl:1
	v_sub_f32_e32 v176, 1.0, v168
	v_mul_f32_e32 v168, 0x3fb8aa3b, v79
	v_exp_f32_e32 v168, v168
	v_pk_add_f32 v[156:157], v[156:157], v[160:161]
	v_sub_f32_e32 v177, 1.0, v168
	v_mov_b32_dpp v168, v164 row_shr:2 row_mask:0xf bank_mask:0xf bound_ctrl:1
	v_pk_add_f32 v[164:165], v[164:165], v[168:169]
	v_mov_b32_dpp v160, v156 row_shr:8 row_mask:0xf bank_mask:0xf bound_ctrl:1
	v_mov_b32_dpp v161, v157 row_shr:8 row_mask:0xf bank_mask:0xf bound_ctrl:1
	v_mov_b32_dpp v168, v164 row_shr:4 row_mask:0xf bank_mask:0xf bound_ctrl:1
	v_mov_b32_dpp v169, v165 row_shr:4 row_mask:0xf bank_mask:0xf bound_ctrl:1
	v_pk_add_f32 v[164:165], v[164:165], v[168:169]
	v_pk_add_f32 v[156:157], v[156:157], v[160:161]
	ds_swizzle_b32 v160, v156 offset:swizzle(BROADCAST,16,15)
	v_mov_b32_dpp v168, v164 row_shr:8 row_mask:0xf bank_mask:0xf bound_ctrl:1
	v_mov_b32_dpp v169, v165 row_shr:8 row_mask:0xf bank_mask:0xf bound_ctrl:1
	ds_swizzle_b32 v161, v157 offset:swizzle(BROADCAST,16,15)
	v_pk_add_f32 v[164:165], v[164:165], v[168:169]
	ds_swizzle_b32 v168, v164 offset:swizzle(BROADCAST,16,15)
	ds_swizzle_b32 v169, v165 offset:swizzle(BROADCAST,16,15)
	v_pk_add_f32 v[156:157], v[170:171], v[156:157]
	s_waitcnt lgkmcnt(2)
; template <int CTRL> __device__ __forceinline__ float dppx(float v) { return __int_as_float(__builtin_amdgcn_update_dpp(0, __float_as_int(v), CTRL, 0xf, 0xf, true)); }
; __device__ __forceinline__ unsigned cvt_pk_bf16(float lo, float hi) { unsigned r; asm volatile("v_cvt_pk_bf16_f32 %0, %1, %2" : "=v"(r) : "v"(lo), "v"(hi)); return r; }
;   __device__ __forceinline__ void operator()(const f32x4 (&acc)[2][2][4][2], const pg8::Unit& u, int wr, int wc, int fr, int fq) const {
;     ...
;       for (int bj = 0; bj < 2; ++bj) { const int c = col0 + bj * 128 - C_HF; const f32x4 l0 = *(const f32x4*)(lb + (c & 511)), l1 = *(const f32x4*)(lb + (c & 511) + 4);
;     ...
;               for (int q = 0; q < 4; ++q) { const float gv = log_forget(acc[ai][bj][m][qh][q], lq[q]); g[m][q] = gv;
;                 float sc = gv; sc += dppx<0x111>(sc); sc += dppx<0x112>(sc); sc += dppx<0x114>(sc); sc += dppx<0x118>(sc);
;                 const float tot16 = __int_as_float(__builtin_amdgcn_ds_swizzle(__float_as_int(sc), 0x1F0));
;                 cs[m][q] = sc + carry[q]; carry[q] += tot16; }
; #pragma unroll
;             for (int m = 0; m < 4; ++m) { const int r = row0 + ai * 128 + m * 16; float bq[4], kq[4];
; #pragma unroll
;               for (int q = 0; q < 4; ++q) { bq[q] = bwd ? (carry[q] - cs[m][q]) + g[m][q] : cs[m][q]; kq[q] = 1.f - __expf(g[m][q]); }
;               *(f32x4*)(logfp + (size_t)r * 1024 + c + 4 * qh) = (f32x4){bq[0], bq[1], bq[2], bq[3]};
;               u32x2 w; w.x = pg8::cvt_pk_bf16(kq[0], kq[1]); w.y = pg8::cvt_pk_bf16(kq[2], kq[3]);
;               *(u32x2*)(km + (size_t)r * 1024 + c + 4 * qh) = w; } } }
	v_pk_add_f32 v[160:161], v[170:171], v[160:161]
	s_nop 0
	v_pk_add_f32 v[164:165], v[160:161], v[164:165]
	s_waitcnt lgkmcnt(0)
	v_pk_add_f32 v[160:161], v[160:161], v[168:169]
	v_mul_f32_e32 v168, 0x3fb8aa3b, v68
	v_exp_f32_e32 v168, v168
	v_mov_b32_dpp v169, v167 row_shr:2 row_mask:0xf bank_mask:0xf bound_ctrl:1
	v_sub_f32_e32 v180, 1.0, v168
	v_mul_f32_e32 v168, 0x3fb8aa3b, v69
	v_exp_f32_e32 v168, v168
	s_nop 0
	v_sub_f32_e32 v181, 1.0, v168
	v_mov_b32_dpp v168, v166 row_shr:2 row_mask:0xf bank_mask:0xf bound_ctrl:1
	v_pk_add_f32 v[166:167], v[166:167], v[168:169]
	s_nop 1
	v_mov_b32_dpp v168, v166 row_shr:4 row_mask:0xf bank_mask:0xf bound_ctrl:1
	v_mov_b32_dpp v169, v167 row_shr:4 row_mask:0xf bank_mask:0xf bound_ctrl:1
	v_pk_add_f32 v[166:167], v[166:167], v[168:169]
	s_nop 1
	v_mov_b32_dpp v168, v166 row_shr:8 row_mask:0xf bank_mask:0xf bound_ctrl:1
	v_mov_b32_dpp v169, v167 row_shr:8 row_mask:0xf bank_mask:0xf bound_ctrl:1
	v_pk_add_f32 v[166:167], v[166:167], v[168:169]
	ds_swizzle_b32 v168, v166 offset:swizzle(BROADCAST,16,15)
	ds_swizzle_b32 v169, v167 offset:swizzle(BROADCAST,16,15)
	v_pk_add_f32 v[166:167], v[158:159], v[166:167]
	s_waitcnt lgkmcnt(0)
	v_pk_add_f32 v[158:159], v[158:159], v[168:169]
	v_mul_f32_e32 v168, 0x3fb8aa3b, v70
	v_exp_f32_e32 v168, v168
	v_mov_b32_dpp v169, v65 row_shr:2 row_mask:0xf bank_mask:0xf bound_ctrl:1
	v_sub_f32_e32 v182, 1.0, v168
	v_mul_f32_e32 v168, 0x3fb8aa3b, v71
	v_exp_f32_e32 v168, v168
	s_nop 0
	v_sub_f32_e32 v183, 1.0, v168
	v_mov_b32_dpp v168, v64 row_shr:2 row_mask:0xf bank_mask:0xf bound_ctrl:1
	v_pk_add_f32 v[64:65], v[64:65], v[168:169]
	s_nop 1
	v_mov_b32_dpp v168, v64 row_shr:4 row_mask:0xf bank_mask:0xf bound_ctrl:1
	v_mov_b32_dpp v169, v65 row_shr:4 row_mask:0xf bank_mask:0xf bound_ctrl:1
	v_pk_add_f32 v[64:65], v[64:65], v[168:169]
	s_nop 1
	v_mov_b32_dpp v168, v64 row_shr:8 row_mask:0xf bank_mask:0xf bound_ctrl:1
	v_mov_b32_dpp v169, v65 row_shr:8 row_mask:0xf bank_mask:0xf bound_ctrl:1
	v_pk_add_f32 v[64:65], v[64:65], v[168:169]
	ds_swizzle_b32 v168, v64 offset:swizzle(BROADCAST,16,15)
	ds_swizzle_b32 v169, v65 offset:swizzle(BROADCAST,16,15)
	v_pk_add_f32 v[170:171], v[160:161], v[64:65]
	v_pk_add_f32 v[64:65], v[158:159], v[74:75] neg_lo:[0,1] neg_hi:[0,1]
	s_waitcnt lgkmcnt(0)
	v_pk_add_f32 v[160:161], v[160:161], v[168:169]
	s_nop 0
	v_pk_add_f32 v[168:169], v[160:161], v[118:119] neg_lo:[0,1] neg_hi:[0,1]
	v_pk_add_f32 v[64:65], v[66:67], v[64:65]
	v_pk_add_f32 v[66:67], v[80:81], v[168:169]
	v_cndmask_b32_e64 v65, v75, v65, s[42:43]
	v_cndmask_b32_e64 v67, v119, v67, s[42:43]
	v_cndmask_b32_e64 v66, v118, v66, s[42:43]
	v_cndmask_b32_e64 v64, v74, v64, s[42:43]
	global_store_dwordx4 v[104:105], v[64:67], off offset:16
	s_nop 1
	v_cvt_pk_bf16_f32 v64, v185, v186
	v_cvt_pk_bf16_f32 v65, v187, v188
	global_store_dwordx2 v[102:103], v[64:65], off offset:8
	v_pk_add_f32 v[64:65], v[158:159], v[120:121] neg_lo:[0,1] neg_hi:[0,1]
	v_pk_add_f32 v[66:67], v[160:161], v[156:157] neg_lo:[0,1] neg_hi:[0,1]
	v_pk_add_f32 v[64:65], v[82:83], v[64:65]
	v_pk_add_f32 v[66:67], v[76:77], v[66:67]
	v_cndmask_b32_e64 v65, v121, v65, s[42:43]
	v_cndmask_b32_e64 v67, v157, v67, s[42:43]
	v_cndmask_b32_e64 v66, v156, v66, s[42:43]
	v_cndmask_b32_e64 v64, v120, v64, s[42:43]
	global_store_dwordx4 v[108:109], v[64:67], off offset:16
	s_nop 1
	v_cvt_pk_bf16_f32 v64, v172, v173
	v_cvt_pk_bf16_f32 v65, v174, v175
	global_store_dwordx2 v[106:107], v[64:65], off offset:8
	v_pk_add_f32 v[64:65], v[158:159], v[162:163] neg_lo:[0,1] neg_hi:[0,1]
	v_pk_add_f32 v[66:67], v[160:161], v[164:165] neg_lo:[0,1] neg_hi:[0,1]
	v_pk_add_f32 v[64:65], v[78:79], v[64:65]
	v_pk_add_f32 v[66:67], v[68:69], v[66:67]
	v_cndmask_b32_e64 v65, v163, v65, s[42:43]
	v_cndmask_b32_e64 v67, v165, v67, s[42:43]
	v_cndmask_b32_e64 v66, v164, v66, s[42:43]
	v_cndmask_b32_e64 v64, v162, v64, s[42:43]
	global_store_dwordx4 v[110:111], v[64:67], off offset:16
	v_mul_f32_e32 v69, 0x3fb8aa3b, v73
	v_exp_f32_e32 v69, v69
	v_cvt_pk_bf16_f32 v64, v176, v177
	v_cvt_pk_bf16_f32 v65, v180, v181
	global_store_dwordx2 v[112:113], v[64:65], off offset:8
	v_mul_f32_e32 v64, 0x3fb8aa3b, v72
	v_exp_f32_e32 v64, v64
	v_pk_add_f32 v[66:67], v[160:161], v[170:171] neg_lo:[0,1] neg_hi:[0,1]
	v_sub_f32_e32 v69, 1.0, v69
	v_pk_add_f32 v[66:67], v[72:73], v[66:67]
	v_sub_f32_e32 v68, 1.0, v64
	v_pk_add_f32 v[64:65], v[158:159], v[166:167] neg_lo:[0,1] neg_hi:[0,1]
	v_cndmask_b32_e64 v67, v171, v67, s[42:43]
	v_pk_add_f32 v[64:65], v[70:71], v[64:65]
	v_cndmask_b32_e64 v66, v170, v66, s[42:43]
	v_cndmask_b32_e64 v65, v167, v65, s[42:43]
	v_cndmask_b32_e64 v64, v166, v64, s[42:43]
	global_store_dwordx4 v[114:115], v[64:67], off offset:16
	s_nop 1
	v_cvt_pk_bf16_f32 v64, v182, v183
	v_cvt_pk_bf16_f32 v65, v68, v69
	global_store_dwordx2 v[116:117], v[64:65], off offset:8
	global_load_dwordx4 v[64:67], v155, s[66:67] offset:528
	s_nop 0
	global_load_dwordx4 v[68:71], v155, s[66:67] offset:512
	v_mul_f32_e32 v60, 0xbfb8aa3b, v60
	v_exp_f32_e32 v60, v60
	s_nop 0
	v_add_f32_e32 v60, 1.0, v60
	s_waitcnt vmcnt(1)
	s_waitcnt vmcnt(0)
; __device__ __forceinline__ float log_forget(float z, float lb) {
;   const float r0 = fminf(z, 0.f) - __logf(1.f + __expf(-fabsf(z)));
;   const float r1 = __logf(lb + (1.f - lb) / (1.f + __expf(-z)));
;   return lb <= 0.f ? r0 : r1;
; }
;   __device__ __forceinline__ void operator()(const f32x4 (&acc)[2][2][4][2], const pg8::Unit& u, int wr, int wc, int fr, int fq) const {
;     ...
;       for (int bj = 0; bj < 2; ++bj) { const int c = col0 + bj * 128 - C_HF; const f32x4 l0 = *(const f32x4*)(lb + (c & 511)), l1 = *(const f32x4*)(lb + (c & 511) + 4);
; #pragma unroll
;         for (int ai = 0; ai < 2; ++ai)
; #pragma unroll
;           for (int qh = 0; qh < 2; ++qh) { float g[4][4], cs[4][4], carry[4];
;             const f32x4 lq = qh == 0 ? l0 : l1;
; #pragma unroll
;             for (int q = 0; q < 4; ++q) carry[q] = 0.f;
; #pragma unroll
;             for (int m = 0; m < 4; ++m)
; #pragma unroll
;               for (int q = 0; q < 4; ++q) { const float gv = log_forget(acc[ai][bj][m][qh][q], lq[q]); g[m][q] = gv;
	v_sub_f32_e32 v157, 1.0, v68
	v_div_scale_f32 v73, s[2:3], v60, v60, v157
	v_rcp_f32_e32 v75, v73
	v_sub_f32_e32 v156, 1.0, v69
	v_sub_f32_e32 v155, 1.0, v70
	v_sub_f32_e32 v154, 1.0, v71
	v_fma_f32 v76, -v73, v75, 1.0
	v_fmac_f32_e32 v75, v76, v75
	v_div_scale_f32 v76, vcc, v157, v60, v157
	v_mul_f32_e32 v77, v76, v75
	v_fma_f32 v78, -v73, v77, v76
	v_fmac_f32_e32 v77, v78, v75
	v_fma_f32 v73, -v73, v77, v76
	v_div_fmas_f32 v73, v73, v75, v77
	v_div_fixup_f32 v60, v73, v60, v157
	v_add_f32_e32 v60, v68, v60
	v_cmp_gt_f32_e32 vcc, s37, v60
	v_cmp_ge_f32_e64 s[46:47], 0, v69
	s_nop 0
	v_cndmask_b32_e64 v73, 0, 32, vcc
	v_ldexp_f32 v60, v60, v73
	v_log_f32_e32 v60, v60
	v_cmp_ge_f32_e64 s[56:57], 0, v66
	v_cmp_ge_f32_e64 s[58:59], 0, v67
	v_mul_f32_e32 v73, 0x3f317217, v60
	v_fma_f32 v73, v60, s33, -v73
	v_fmac_f32_e32 v73, 0x3377d1cf, v60
	v_fmac_f32_e32 v73, 0x3f317217, v60
	v_cmp_lt_f32_e64 s[44:45], |v60|, s36
	s_nop 1
	v_cndmask_b32_e64 v60, v60, v73, s[44:45]
	v_cndmask_b32_e32 v73, 0, v216, vcc
	v_sub_f32_e32 v116, v60, v73
	s_nop 0
	s_nop 1
	s_nop 0
	s_nop 1
	v_mul_f32_e32 v60, 0xbfb8aa3b, v61
	v_exp_f32_e32 v60, v60
	s_nop 0
	v_add_f32_e32 v60, 1.0, v60
	v_div_scale_f32 v61, s[2:3], v60, v60, v156
	v_rcp_f32_e32 v76, v61
	s_nop 0
	v_fma_f32 v77, -v61, v76, 1.0
	v_fmac_f32_e32 v76, v77, v76
	v_div_scale_f32 v77, vcc, v156, v60, v156
	v_mul_f32_e32 v78, v77, v76
	v_fma_f32 v79, -v61, v78, v77
	v_fmac_f32_e32 v78, v79, v76
	v_fma_f32 v61, -v61, v78, v77
	v_div_fmas_f32 v61, v61, v76, v78
	v_div_fixup_f32 v60, v61, v60, v156
	v_add_f32_e32 v60, v69, v60
	v_cmp_gt_f32_e32 vcc, s37, v60
	s_nop 1
	v_cndmask_b32_e64 v61, 0, 32, vcc
	v_ldexp_f32 v60, v60, v61
	v_log_f32_e32 v60, v60
	s_nop 0
	v_mul_f32_e32 v61, 0x3f317217, v60
	v_fma_f32 v61, v60, s33, -v61
	v_fmac_f32_e32 v61, 0x3377d1cf, v60
	v_fmac_f32_e32 v61, 0x3f317217, v60
	v_cmp_lt_f32_e64 s[44:45], |v60|, s36
	s_nop 1
	v_cndmask_b32_e64 v60, v60, v61, s[44:45]
	v_cndmask_b32_e32 v61, 0, v216, vcc
	v_sub_f32_e32 v117, v60, v61
	s_nop 1
	s_nop 0
	s_nop 1
	v_mul_f32_e32 v61, 0xbfb8aa3b, v62
	v_exp_f32_e32 v61, v61
	s_nop 0
	v_add_f32_e32 v61, 1.0, v61
	v_div_scale_f32 v62, s[2:3], v61, v61, v155
	v_rcp_f32_e32 v77, v62
	s_nop 0
	v_fma_f32 v78, -v62, v77, 1.0
	v_fmac_f32_e32 v77, v78, v77
	v_div_scale_f32 v78, vcc, v155, v61, v155
	v_mul_f32_e32 v79, v78, v77
	v_fma_f32 v80, -v62, v79, v78
	v_fmac_f32_e32 v79, v80, v77
	v_fma_f32 v62, -v62, v79, v78
	v_div_fmas_f32 v62, v62, v77, v79
	v_div_fixup_f32 v61, v62, v61, v155
	v_add_f32_e32 v61, v70, v61
	v_cmp_gt_f32_e32 vcc, s37, v61
	s_nop 1
	v_cndmask_b32_e64 v62, 0, 32, vcc
	v_ldexp_f32 v61, v61, v62
	v_log_f32_e32 v61, v61
	s_nop 0
	v_mul_f32_e32 v62, 0x3f317217, v61
	v_fma_f32 v62, v61, s33, -v62
	v_fmac_f32_e32 v62, 0x3377d1cf, v61
	v_fmac_f32_e32 v62, 0x3f317217, v61
	v_cmp_lt_f32_e64 s[44:45], |v61|, s36
	s_nop 1
	v_cndmask_b32_e64 v61, v61, v62, s[44:45]
	v_cndmask_b32_e32 v62, 0, v216, vcc
	v_sub_f32_e32 v118, v61, v62
	s_nop 1
	s_nop 0
	s_nop 1
	v_mul_f32_e32 v62, 0xbfb8aa3b, v63
	v_exp_f32_e32 v62, v62
	s_nop 0
	v_add_f32_e32 v62, 1.0, v62
	v_div_scale_f32 v63, s[2:3], v62, v62, v154
	v_rcp_f32_e32 v78, v63
	s_nop 0
	v_fma_f32 v79, -v63, v78, 1.0
	v_fmac_f32_e32 v78, v79, v78
	v_div_scale_f32 v79, vcc, v154, v62, v154
	v_mul_f32_e32 v80, v79, v78
	v_fma_f32 v81, -v63, v80, v79
	v_fmac_f32_e32 v80, v81, v78
	v_fma_f32 v63, -v63, v80, v79
	v_div_fmas_f32 v63, v63, v78, v80
	v_div_fixup_f32 v62, v63, v62, v154
	v_add_f32_e32 v62, v71, v62
	v_cmp_gt_f32_e32 vcc, s37, v62
	s_nop 1
	v_cndmask_b32_e64 v63, 0, 32, vcc
	v_ldexp_f32 v62, v62, v63
	v_log_f32_e32 v62, v62
	s_nop 0
	v_mul_f32_e32 v63, 0x3f317217, v62
	v_fma_f32 v63, v62, s33, -v63
	v_fmac_f32_e32 v63, 0x3377d1cf, v62
	v_fmac_f32_e32 v63, 0x3f317217, v62
	v_cmp_lt_f32_e64 s[44:45], |v62|, s36
	s_nop 1
	v_cndmask_b32_e64 v62, v62, v63, s[44:45]
	v_cndmask_b32_e32 v63, 0, v216, vcc
	v_sub_f32_e32 v119, v62, v63
	v_mul_f32_e32 v56, 0xbfb8aa3b, v56
	v_exp_f32_e32 v56, v56
	s_nop 0
	v_add_f32_e32 v56, 1.0, v56
	s_nop 0
	s_nop 1
	v_div_scale_f32 v63, s[2:3], v56, v56, v157
	v_rcp_f32_e32 v79, v63
	s_nop 0
	v_fma_f32 v80, -v63, v79, 1.0
	v_fmac_f32_e32 v79, v80, v79
	v_div_scale_f32 v80, vcc, v157, v56, v157
	v_mul_f32_e32 v81, v80, v79
	v_fma_f32 v82, -v63, v81, v80
	v_fmac_f32_e32 v81, v82, v79
	v_fma_f32 v63, -v63, v81, v80
	v_div_fmas_f32 v63, v63, v79, v81
	v_div_fixup_f32 v56, v63, v56, v157
	v_add_f32_e32 v56, v68, v56
	v_cmp_gt_f32_e32 vcc, s37, v56
	s_nop 1
	v_cndmask_b32_e64 v63, 0, 32, vcc
	v_ldexp_f32 v56, v56, v63
	v_log_f32_e32 v56, v56
	s_nop 0
	v_mul_f32_e32 v63, 0x3f317217, v56
	v_fma_f32 v63, v56, s33, -v63
	v_fmac_f32_e32 v63, 0x3377d1cf, v56
	v_fmac_f32_e32 v63, 0x3f317217, v56
	v_cmp_lt_f32_e64 s[44:45], |v56|, s36
	s_nop 1
	v_cndmask_b32_e64 v56, v56, v63, s[44:45]
	v_cndmask_b32_e32 v63, 0, v216, vcc
	v_sub_f32_e32 v120, v56, v63
	s_nop 0
	s_nop 1
	s_nop 0
	s_nop 1
	v_mul_f32_e32 v56, 0xbfb8aa3b, v57
	v_exp_f32_e32 v56, v56
	s_nop 0
	v_add_f32_e32 v56, 1.0, v56
	v_div_scale_f32 v57, s[2:3], v56, v56, v156
	v_rcp_f32_e32 v80, v57
	s_nop 0
	v_fma_f32 v81, -v57, v80, 1.0
	v_fmac_f32_e32 v80, v81, v80
	v_div_scale_f32 v81, vcc, v156, v56, v156
	v_mul_f32_e32 v82, v81, v80
	v_fma_f32 v83, -v57, v82, v81
	v_fmac_f32_e32 v82, v83, v80
	v_fma_f32 v57, -v57, v82, v81
	v_div_fmas_f32 v57, v57, v80, v82
	v_div_fixup_f32 v56, v57, v56, v156
	v_add_f32_e32 v56, v69, v56
	v_cmp_gt_f32_e32 vcc, s37, v56
	s_nop 1
	v_cndmask_b32_e64 v57, 0, 32, vcc
	v_ldexp_f32 v56, v56, v57
	v_log_f32_e32 v56, v56
	s_nop 0
	v_mul_f32_e32 v57, 0x3f317217, v56
	v_fma_f32 v57, v56, s33, -v57
; template <int CTRL> __device__ __forceinline__ float dppx(float v) { return __int_as_float(__builtin_amdgcn_update_dpp(0, __float_as_int(v), CTRL, 0xf, 0xf, true)); }
; __device__ __forceinline__ float log_forget(float z, float lb) {
;   const float r0 = fminf(z, 0.f) - __logf(1.f + __expf(-fabsf(z)));
;   const float r1 = __logf(lb + (1.f - lb) / (1.f + __expf(-z)));
;   return lb <= 0.f ? r0 : r1;
; }
;   __device__ __forceinline__ void operator()(const f32x4 (&acc)[2][2][4][2], const pg8::Unit& u, int wr, int wc, int fr, int fq) const {
;     ...
;           for (int qh = 0; qh < 2; ++qh) { float g[4][4], cs[4][4], carry[4];
;             const f32x4 lq = qh == 0 ? l0 : l1;
; #pragma unroll
;             for (int q = 0; q < 4; ++q) carry[q] = 0.f;
; #pragma unroll
;             for (int m = 0; m < 4; ++m)
; #pragma unroll
;               for (int q = 0; q < 4; ++q) { const float gv = log_forget(acc[ai][bj][m][qh][q], lq[q]); g[m][q] = gv;
;                 float sc = gv; sc += dppx<0x111>(sc); sc += dppx<0x112>(sc); sc += dppx<0x114>(sc); sc += dppx<0x118>(sc);
	v_fmac_f32_e32 v57, 0x3377d1cf, v56
	v_fmac_f32_e32 v57, 0x3f317217, v56
	v_cmp_lt_f32_e64 s[44:45], |v56|, s36
	s_nop 1
	v_cndmask_b32_e64 v56, v56, v57, s[44:45]
	v_cndmask_b32_e32 v57, 0, v216, vcc
	v_sub_f32_e32 v121, v56, v57
	v_mov_b32_e32 v79, v121
	s_nop 1
	v_mov_b32_dpp v63, v79 row_shr:1 row_mask:0xf bank_mask:0xf bound_ctrl:1
	s_nop 0
	s_nop 0
	s_nop 1
	v_mul_f32_e32 v57, 0xbfb8aa3b, v58
	v_exp_f32_e32 v57, v57
	s_nop 0
	v_add_f32_e32 v57, 1.0, v57
	v_div_scale_f32 v58, s[2:3], v57, v57, v155
	v_rcp_f32_e32 v81, v58
	s_nop 0
	v_fma_f32 v82, -v58, v81, 1.0
	v_fmac_f32_e32 v81, v82, v81
	v_div_scale_f32 v82, vcc, v155, v57, v155
	v_mul_f32_e32 v83, v82, v81
	v_fma_f32 v102, -v58, v83, v82
	v_fmac_f32_e32 v83, v102, v81
	v_fma_f32 v58, -v58, v83, v82
	v_div_fmas_f32 v58, v58, v81, v83
	v_div_fixup_f32 v57, v58, v57, v155
	v_add_f32_e32 v57, v70, v57
	v_cmp_gt_f32_e32 vcc, s37, v57
	s_nop 1
	v_cndmask_b32_e64 v58, 0, 32, vcc
	v_ldexp_f32 v57, v57, v58
	v_log_f32_e32 v57, v57
	s_nop 0
	v_mul_f32_e32 v58, 0x3f317217, v57
	v_fma_f32 v58, v57, s33, -v58
	v_fmac_f32_e32 v58, 0x3377d1cf, v57
	v_fmac_f32_e32 v58, 0x3f317217, v57
	v_cmp_lt_f32_e64 s[44:45], |v57|, s36
	s_nop 1
	v_cndmask_b32_e64 v57, v57, v58, s[44:45]
	v_cndmask_b32_e32 v58, 0, v216, vcc
	v_sub_f32_e32 v58, v57, v58
	v_mul_f32_e32 v59, 0xbfb8aa3b, v59
	v_exp_f32_e32 v59, v59
	s_nop 0
	v_add_f32_e32 v59, 1.0, v59
	s_nop 0
	v_div_scale_f32 v82, s[2:3], v59, v59, v154
	v_rcp_f32_e32 v83, v82
	s_nop 0
	v_fma_f32 v102, -v82, v83, 1.0
	v_fmac_f32_e32 v83, v102, v83
	v_div_scale_f32 v102, vcc, v154, v59, v154
	v_mul_f32_e32 v103, v102, v83
	v_fma_f32 v104, -v82, v103, v102
	v_fmac_f32_e32 v103, v104, v83
	v_fma_f32 v82, -v82, v103, v102
	v_div_fmas_f32 v82, v82, v83, v103
	v_div_fixup_f32 v59, v82, v59, v154
	v_add_f32_e32 v59, v71, v59
	v_cmp_gt_f32_e32 vcc, s37, v59
	s_nop 1
	v_cndmask_b32_e64 v82, 0, 32, vcc
	v_ldexp_f32 v59, v59, v82
	v_log_f32_e32 v59, v59
	v_mov_b32_e32 v80, v58
	v_mul_f32_e32 v82, 0x3f317217, v59
	v_fma_f32 v82, v59, s33, -v82
	v_fmac_f32_e32 v82, 0x3377d1cf, v59
	v_fmac_f32_e32 v82, 0x3f317217, v59
	v_cmp_lt_f32_e64 s[44:45], |v59|, s36
	v_mov_b32_dpp v56, v80 row_shr:1 row_mask:0xf bank_mask:0xf bound_ctrl:1
	s_nop 0
	v_cndmask_b32_e64 v59, v59, v82, s[44:45]
	v_cndmask_b32_e32 v82, 0, v216, vcc
	v_sub_f32_e32 v59, v59, v82
	v_mul_f32_e32 v52, 0xbfb8aa3b, v52
	v_exp_f32_e32 v52, v52
	s_nop 0
	v_add_f32_e32 v52, 1.0, v52
	v_mov_b32_e32 v81, v59
	v_div_scale_f32 v83, s[2:3], v52, v52, v157
	v_rcp_f32_e32 v103, v83
	v_mov_b32_dpp v57, v81 row_shr:1 row_mask:0xf bank_mask:0xf bound_ctrl:1
	v_pk_add_f32 v[56:57], v[80:81], v[56:57]
	v_fma_f32 v104, -v83, v103, 1.0
	v_fmac_f32_e32 v103, v104, v103
	v_div_scale_f32 v104, vcc, v157, v52, v157
	v_mul_f32_e32 v105, v104, v103
	v_fma_f32 v106, -v83, v105, v104
	v_fmac_f32_e32 v105, v106, v103
	v_fma_f32 v83, -v83, v105, v104
	v_div_fmas_f32 v83, v83, v103, v105
	v_div_fixup_f32 v52, v83, v52, v157
	v_add_f32_e32 v52, v68, v52
	v_cmp_gt_f32_e32 vcc, s37, v52
	v_mov_b32_dpp v58, v56 row_shr:2 row_mask:0xf bank_mask:0xf bound_ctrl:1
	v_mov_b32_dpp v59, v57 row_shr:2 row_mask:0xf bank_mask:0xf bound_ctrl:1
	v_cndmask_b32_e64 v83, 0, 32, vcc
	v_ldexp_f32 v52, v52, v83
	v_log_f32_e32 v52, v52
	v_pk_add_f32 v[56:57], v[56:57], v[58:59]
	v_mul_f32_e32 v83, 0x3f317217, v52
	v_fma_f32 v83, v52, s33, -v83
	v_fmac_f32_e32 v83, 0x3377d1cf, v52
	v_fmac_f32_e32 v83, 0x3f317217, v52
	v_cmp_lt_f32_e64 s[44:45], |v52|, s36
	v_mov_b32_dpp v58, v56 row_shr:4 row_mask:0xf bank_mask:0xf bound_ctrl:1
	v_mov_b32_dpp v59, v57 row_shr:4 row_mask:0xf bank_mask:0xf bound_ctrl:1
	v_cndmask_b32_e64 v52, v52, v83, s[44:45]
	v_cndmask_b32_e32 v83, 0, v216, vcc
	v_sub_f32_e32 v158, v52, v83
	v_pk_add_f32 v[56:57], v[56:57], v[58:59]
	s_nop 1
	v_mov_b32_dpp v58, v56 row_shr:8 row_mask:0xf bank_mask:0xf bound_ctrl:1
	v_mov_b32_dpp v59, v57 row_shr:8 row_mask:0xf bank_mask:0xf bound_ctrl:1
	v_pk_add_f32 v[56:57], v[56:57], v[58:59]
	ds_swizzle_b32 v58, v56 offset:swizzle(BROADCAST,16,15)
	ds_swizzle_b32 v59, v57 offset:swizzle(BROADCAST,16,15)
	s_nop 1
	v_mul_f32_e32 v52, 0xbfb8aa3b, v53
	v_exp_f32_e32 v52, v52
	s_nop 0
	v_add_f32_e32 v52, 1.0, v52
	v_div_scale_f32 v53, s[2:3], v52, v52, v156
	v_rcp_f32_e32 v104, v53
	s_nop 0
	v_fma_f32 v105, -v53, v104, 1.0
	v_fmac_f32_e32 v104, v105, v104
	v_div_scale_f32 v105, vcc, v156, v52, v156
	v_mul_f32_e32 v106, v105, v104
	v_fma_f32 v107, -v53, v106, v105
	v_fmac_f32_e32 v106, v107, v104
	v_fma_f32 v53, -v53, v106, v105
	v_div_fmas_f32 v53, v53, v104, v106
	v_div_fixup_f32 v52, v53, v52, v156
	v_add_f32_e32 v52, v69, v52
	v_cmp_gt_f32_e32 vcc, s37, v52
	s_nop 1
	v_cndmask_b32_e64 v53, 0, 32, vcc
	v_ldexp_f32 v52, v52, v53
	v_log_f32_e32 v52, v52
	s_nop 0
	v_mul_f32_e32 v53, 0x3f317217, v52
	v_fma_f32 v53, v52, s33, -v53
	v_fmac_f32_e32 v53, 0x3377d1cf, v52
	v_fmac_f32_e32 v53, 0x3f317217, v52
	v_cmp_lt_f32_e64 s[44:45], |v52|, s36
	s_nop 1
	v_cndmask_b32_e64 v52, v52, v53, s[44:45]
	v_cndmask_b32_e32 v53, 0, v216, vcc
	v_sub_f32_e32 v159, v52, v53
	v_mov_b32_e32 v83, v159
	s_nop 1
	v_mov_b32_dpp v103, v83 row_shr:1 row_mask:0xf bank_mask:0xf bound_ctrl:1
	s_nop 0
	s_nop 0
	s_nop 1
	v_mul_f32_e32 v52, 0xbfb8aa3b, v54
	v_exp_f32_e32 v52, v52
	s_nop 0
	v_add_f32_e32 v52, 1.0, v52
	v_div_scale_f32 v53, s[2:3], v52, v52, v155
	v_rcp_f32_e32 v54, v53
	s_nop 0
	v_fma_f32 v105, -v53, v54, 1.0
	v_fmac_f32_e32 v54, v105, v54
	v_div_scale_f32 v105, vcc, v155, v52, v155
	v_mul_f32_e32 v107, v105, v54
	v_fma_f32 v108, -v53, v107, v105
	v_fmac_f32_e32 v107, v108, v54
	v_fma_f32 v53, -v53, v107, v105
; __device__ __forceinline__ float log_forget(float z, float lb) {
;   const float r0 = fminf(z, 0.f) - __logf(1.f + __expf(-fabsf(z)));
;   const float r1 = __logf(lb + (1.f - lb) / (1.f + __expf(-z)));
;   return lb <= 0.f ? r0 : r1;
; }
;   __device__ __forceinline__ void operator()(const f32x4 (&acc)[2][2][4][2], const pg8::Unit& u, int wr, int wc, int fr, int fq) const {
;     ...
;           for (int qh = 0; qh < 2; ++qh) { float g[4][4], cs[4][4], carry[4];
;             const f32x4 lq = qh == 0 ? l0 : l1;
; #pragma unroll
;             for (int q = 0; q < 4; ++q) carry[q] = 0.f;
; #pragma unroll
;             for (int m = 0; m < 4; ++m)
; #pragma unroll
;               for (int q = 0; q < 4; ++q) { const float gv = log_forget(acc[ai][bj][m][qh][q], lq[q]); g[m][q] = gv;
	v_div_fmas_f32 v53, v53, v54, v107
	v_div_fixup_f32 v52, v53, v52, v155
	v_add_f32_e32 v52, v70, v52
	v_cmp_gt_f32_e32 vcc, s37, v52
	s_nop 1
	v_cndmask_b32_e64 v53, 0, 32, vcc
	v_ldexp_f32 v52, v52, v53
	v_log_f32_e32 v52, v52
	s_nop 0
	v_mul_f32_e32 v53, 0x3f317217, v52
	v_fma_f32 v53, v52, s33, -v53
	v_fmac_f32_e32 v53, 0x3377d1cf, v52
	v_fmac_f32_e32 v53, 0x3f317217, v52
	v_cmp_lt_f32_e64 s[44:45], |v52|, s36
	s_nop 1
	v_cndmask_b32_e64 v52, v52, v53, s[44:45]
	v_cndmask_b32_e32 v53, 0, v216, vcc
	v_sub_f32_e32 v160, v52, v53
	s_nop 0
	s_nop 1
	s_nop 0
	s_nop 1
	v_mul_f32_e32 v52, 0xbfb8aa3b, v55
	v_exp_f32_e32 v52, v52
	s_nop 0
	v_add_f32_e32 v52, 1.0, v52
	v_div_scale_f32 v53, s[2:3], v52, v52, v154
	v_rcp_f32_e32 v54, v53
	s_nop 0
	v_fma_f32 v55, -v53, v54, 1.0
	v_fmac_f32_e32 v54, v55, v54
	v_div_scale_f32 v55, vcc, v154, v52, v154
	v_mul_f32_e32 v108, v55, v54
	v_fma_f32 v109, -v53, v108, v55
	v_fmac_f32_e32 v108, v109, v54
	v_fma_f32 v53, -v53, v108, v55
	v_div_fmas_f32 v53, v53, v54, v108
	v_div_fixup_f32 v52, v53, v52, v154
	v_add_f32_e32 v52, v71, v52
	v_cmp_gt_f32_e32 vcc, s37, v52
	s_nop 1
	v_cndmask_b32_e64 v53, 0, 32, vcc
	v_ldexp_f32 v52, v52, v53
	v_log_f32_e32 v52, v52
	s_nop 0
	v_mul_f32_e32 v53, 0x3f317217, v52
	v_fma_f32 v53, v52, s33, -v53
	v_fmac_f32_e32 v53, 0x3377d1cf, v52
	v_fmac_f32_e32 v53, 0x3f317217, v52
	v_cmp_lt_f32_e64 s[44:45], |v52|, s36
	s_nop 1
	v_cndmask_b32_e64 v52, v52, v53, s[44:45]
	v_cndmask_b32_e32 v53, 0, v216, vcc
	v_sub_f32_e32 v161, v52, v53
	v_mul_f32_e32 v48, 0xbfb8aa3b, v48
	v_exp_f32_e32 v48, v48
	s_nop 0
	v_add_f32_e32 v48, 1.0, v48
	s_nop 0
	s_nop 0
	s_nop 1
	v_div_scale_f32 v52, s[2:3], v48, v48, v157
	v_rcp_f32_e32 v53, v52
	s_nop 0
	v_fma_f32 v54, -v52, v53, 1.0
	v_fmac_f32_e32 v53, v54, v53
	v_div_scale_f32 v54, vcc, v157, v48, v157
	v_mul_f32_e32 v55, v54, v53
	v_fma_f32 v109, -v52, v55, v54
	v_fmac_f32_e32 v55, v109, v53
	v_fma_f32 v52, -v52, v55, v54
	v_div_fmas_f32 v52, v52, v53, v55
	v_div_fixup_f32 v48, v52, v48, v157
	v_add_f32_e32 v48, v68, v48
	v_cmp_gt_f32_e32 vcc, s37, v48
	s_nop 1
	v_cndmask_b32_e64 v52, 0, 32, vcc
	v_ldexp_f32 v48, v48, v52
	v_log_f32_e32 v48, v48
	s_nop 0
	v_mul_f32_e32 v52, 0x3f317217, v48
	v_fma_f32 v52, v48, s33, -v52
	v_fmac_f32_e32 v52, 0x3377d1cf, v48
	v_fmac_f32_e32 v52, 0x3f317217, v48
	v_cmp_lt_f32_e64 s[44:45], |v48|, s36
	s_nop 1
	v_cndmask_b32_e64 v48, v48, v52, s[44:45]
	v_cndmask_b32_e32 v52, 0, v216, vcc
	v_sub_f32_e32 v162, v48, v52
	s_nop 0
	s_nop 1
	s_nop 0
	s_nop 1
	v_mul_f32_e32 v48, 0xbfb8aa3b, v49
	v_exp_f32_e32 v48, v48
	s_nop 0
	v_add_f32_e32 v48, 1.0, v48
	v_div_scale_f32 v49, s[2:3], v48, v48, v156
	v_rcp_f32_e32 v52, v49
	s_nop 0
	v_fma_f32 v53, -v49, v52, 1.0
	v_fmac_f32_e32 v52, v53, v52
	v_div_scale_f32 v53, vcc, v156, v48, v156
	v_mul_f32_e32 v54, v53, v52
	v_fma_f32 v55, -v49, v54, v53
	v_fmac_f32_e32 v54, v55, v52
	v_fma_f32 v49, -v49, v54, v53
	v_div_fmas_f32 v49, v49, v52, v54
	v_div_fixup_f32 v48, v49, v48, v156
	v_add_f32_e32 v48, v69, v48
	v_cmp_gt_f32_e32 vcc, s37, v48
	s_nop 1
	v_cndmask_b32_e64 v49, 0, 32, vcc
	v_ldexp_f32 v48, v48, v49
	v_log_f32_e32 v48, v48
	s_nop 0
	v_mul_f32_e32 v49, 0x3f317217, v48
	v_fma_f32 v49, v48, s33, -v49
	v_fmac_f32_e32 v49, 0x3377d1cf, v48
	v_fmac_f32_e32 v49, 0x3f317217, v48
	v_cmp_lt_f32_e64 s[44:45], |v48|, s36
	s_nop 1
	v_cndmask_b32_e64 v48, v48, v49, s[44:45]
	v_cndmask_b32_e32 v49, 0, v216, vcc
	v_sub_f32_e32 v163, v48, v49
	v_mov_b32_e32 v109, v163
	s_nop 1
	v_mov_b32_dpp v111, v109 row_shr:1 row_mask:0xf bank_mask:0xf bound_ctrl:1
	s_nop 0
	s_nop 0
	s_nop 1
	v_mul_f32_e32 v48, 0xbfb8aa3b, v50
	v_exp_f32_e32 v48, v48
	s_nop 0
	v_add_f32_e32 v48, 1.0, v48
	v_div_scale_f32 v49, s[2:3], v48, v48, v155
	v_rcp_f32_e32 v50, v49
	s_nop 0
	v_fma_f32 v52, -v49, v50, 1.0
	v_fmac_f32_e32 v50, v52, v50
	v_div_scale_f32 v52, vcc, v155, v48, v155
	v_mul_f32_e32 v53, v52, v50
	v_fma_f32 v54, -v49, v53, v52
	v_fmac_f32_e32 v53, v54, v50
	v_fma_f32 v49, -v49, v53, v52
	v_div_fmas_f32 v49, v49, v50, v53
	v_div_fixup_f32 v48, v49, v48, v155
	v_add_f32_e32 v48, v70, v48
	v_cmp_gt_f32_e32 vcc, s37, v48
	s_nop 1
	v_cndmask_b32_e64 v49, 0, 32, vcc
	v_ldexp_f32 v48, v48, v49
	v_log_f32_e32 v48, v48
	s_nop 0
	v_mul_f32_e32 v49, 0x3f317217, v48
	v_fma_f32 v49, v48, s33, -v49
	v_fmac_f32_e32 v49, 0x3377d1cf, v48
	v_fmac_f32_e32 v49, 0x3f317217, v48
	v_cmp_lt_f32_e64 s[44:45], |v48|, s36
	s_nop 1
	v_cndmask_b32_e64 v48, v48, v49, s[44:45]
	v_cndmask_b32_e32 v49, 0, v216, vcc
	v_sub_f32_e32 v164, v48, v49
	s_nop 0
	s_nop 1
	s_nop 0
	s_nop 1
	v_mul_f32_e32 v48, 0xbfb8aa3b, v51
	v_exp_f32_e32 v48, v48
	s_nop 0
	v_add_f32_e32 v48, 1.0, v48
	v_div_scale_f32 v49, s[2:3], v48, v48, v154
	v_rcp_f32_e32 v50, v49
	v_mov_b32_e32 v112, v164
	v_fma_f32 v51, -v49, v50, 1.0
	v_fmac_f32_e32 v50, v51, v50
	v_div_scale_f32 v51, vcc, v154, v48, v154
	v_mul_f32_e32 v52, v51, v50
	v_fma_f32 v53, -v49, v52, v51
	v_fmac_f32_e32 v52, v53, v50
	v_fma_f32 v49, -v49, v52, v51
	v_div_fmas_f32 v49, v49, v50, v52
	v_div_fixup_f32 v48, v49, v48, v154
	v_add_f32_e32 v48, v71, v48
	v_cmp_gt_f32_e32 vcc, s37, v48
	v_mov_b32_dpp v114, v112 row_shr:1 row_mask:0xf bank_mask:0xf bound_ctrl:1
	s_nop 0
	v_cndmask_b32_e64 v49, 0, 32, vcc
	v_ldexp_f32 v48, v48, v49
	v_log_f32_e32 v48, v48
	s_nop 0
	v_mul_f32_e32 v49, 0x3f317217, v48
	v_fma_f32 v49, v48, s33, -v49
	v_fmac_f32_e32 v49, 0x3377d1cf, v48
	v_fmac_f32_e32 v49, 0x3f317217, v48
	v_cmp_lt_f32_e64 s[44:45], |v48|, s36
	s_nop 1
	v_cndmask_b32_e64 v48, v48, v49, s[44:45]
	v_cndmask_b32_e32 v49, 0, v216, vcc
	v_sub_f32_e32 v165, v48, v49
	v_mov_b32_e32 v73, v117
	v_mov_b32_e32 v113, v165
; template <int CTRL> __device__ __forceinline__ float dppx(float v) { return __int_as_float(__builtin_amdgcn_update_dpp(0, __float_as_int(v), CTRL, 0xf, 0xf, true)); }
;   __device__ __forceinline__ void operator()(const f32x4 (&acc)[2][2][4][2], const pg8::Unit& u, int wr, int wc, int fr, int fq) const {
;     ...
;               for (int q = 0; q < 4; ++q) { const float gv = log_forget(acc[ai][bj][m][qh][q], lq[q]); g[m][q] = gv;
;                 float sc = gv; sc += dppx<0x111>(sc); sc += dppx<0x112>(sc); sc += dppx<0x114>(sc); sc += dppx<0x118>(sc);
;                 const float tot16 = __int_as_float(__builtin_amdgcn_ds_swizzle(__float_as_int(sc), 0x1F0));
;                 cs[m][q] = sc + carry[q]; carry[q] += tot16; }
; #pragma unroll
;             for (int m = 0; m < 4; ++m) { const int r = row0 + ai * 128 + m * 16; float bq[4], kq[4];
; #pragma unroll
;               for (int q = 0; q < 4; ++q) { bq[q] = bwd ? (carry[q] - cs[m][q]) + g[m][q] : cs[m][q]; kq[q] = 1.f - __expf(g[m][q]); }
;               *(f32x4*)(logfp + (size_t)r * 1024 + c + 4 * qh) = (f32x4){bq[0], bq[1], bq[2], bq[3]};
	v_mov_b32_e32 v72, v116
	v_mov_b32_dpp v49, v73 row_shr:1 row_mask:0xf bank_mask:0xf bound_ctrl:1
	v_mov_b32_e32 v78, v120
	v_mov_b32_dpp v48, v72 row_shr:1 row_mask:0xf bank_mask:0xf bound_ctrl:1
	v_pk_add_f32 v[48:49], v[72:73], v[48:49]
	v_mov_b32_dpp v62, v78 row_shr:1 row_mask:0xf bank_mask:0xf bound_ctrl:1
	v_mov_b32_e32 v82, v158
	v_mov_b32_dpp v50, v48 row_shr:2 row_mask:0xf bank_mask:0xf bound_ctrl:1
	v_mov_b32_dpp v51, v49 row_shr:2 row_mask:0xf bank_mask:0xf bound_ctrl:1
	v_pk_add_f32 v[48:49], v[48:49], v[50:51]
	v_pk_add_f32 v[62:63], v[78:79], v[62:63]
	v_mov_b32_dpp v102, v82 row_shr:1 row_mask:0xf bank_mask:0xf bound_ctrl:1
	v_mov_b32_dpp v50, v48 row_shr:4 row_mask:0xf bank_mask:0xf bound_ctrl:1
	v_mov_b32_dpp v51, v49 row_shr:4 row_mask:0xf bank_mask:0xf bound_ctrl:1
	v_pk_add_f32 v[48:49], v[48:49], v[50:51]
	v_pk_add_f32 v[102:103], v[82:83], v[102:103]
	v_mov_b32_e32 v108, v162
	v_mov_b32_dpp v50, v48 row_shr:8 row_mask:0xf bank_mask:0xf bound_ctrl:1
	v_mov_b32_dpp v51, v49 row_shr:8 row_mask:0xf bank_mask:0xf bound_ctrl:1
	v_pk_add_f32 v[48:49], v[48:49], v[50:51]
	ds_swizzle_b32 v50, v48 offset:swizzle(BROADCAST,16,15)
	v_pk_add_f32 v[74:75], v[48:49], 0 op_sel_hi:[1,0]
	v_mul_f32_e32 v48, 0x3fb8aa3b, v72
	v_exp_f32_e32 v48, v48
	ds_swizzle_b32 v51, v49 offset:swizzle(BROADCAST,16,15)
	v_mov_b32_dpp v110, v108 row_shr:1 row_mask:0xf bank_mask:0xf bound_ctrl:1
	v_pk_add_f32 v[110:111], v[108:109], v[110:111]
	v_sub_f32_e32 v168, 1.0, v48
	v_mul_f32_e32 v48, 0x3fb8aa3b, v73
	v_exp_f32_e32 v48, v48
	s_waitcnt lgkmcnt(0)
	v_pk_add_f32 v[166:167], v[50:51], 0 op_sel_hi:[1,0]
	v_mov_b32_dpp v115, v113 row_shr:1 row_mask:0xf bank_mask:0xf bound_ctrl:1
	v_pk_add_f32 v[114:115], v[112:113], v[114:115]
	v_sub_f32_e32 v169, 1.0, v48
	s_nop 0
	v_mov_b32_e32 v77, v119
	v_mov_b32_e32 v76, v118
	v_mov_b32_dpp v118, v62 row_shr:2 row_mask:0xf bank_mask:0xf bound_ctrl:1
	v_mov_b32_dpp v49, v77 row_shr:1 row_mask:0xf bank_mask:0xf bound_ctrl:1
	v_mov_b32_dpp v48, v76 row_shr:1 row_mask:0xf bank_mask:0xf bound_ctrl:1
	v_pk_add_f32 v[48:49], v[76:77], v[48:49]
	v_mov_b32_dpp v119, v63 row_shr:2 row_mask:0xf bank_mask:0xf bound_ctrl:1
	v_pk_add_f32 v[62:63], v[62:63], v[118:119]
	v_mov_b32_dpp v50, v48 row_shr:2 row_mask:0xf bank_mask:0xf bound_ctrl:1
	v_mov_b32_dpp v51, v49 row_shr:2 row_mask:0xf bank_mask:0xf bound_ctrl:1
	v_pk_add_f32 v[48:49], v[48:49], v[50:51]
	v_mov_b32_dpp v118, v62 row_shr:4 row_mask:0xf bank_mask:0xf bound_ctrl:1
	v_mov_b32_dpp v119, v63 row_shr:4 row_mask:0xf bank_mask:0xf bound_ctrl:1
	v_mov_b32_dpp v50, v48 row_shr:4 row_mask:0xf bank_mask:0xf bound_ctrl:1
	v_mov_b32_dpp v51, v49 row_shr:4 row_mask:0xf bank_mask:0xf bound_ctrl:1
	v_pk_add_f32 v[48:49], v[48:49], v[50:51]
	v_pk_add_f32 v[62:63], v[62:63], v[118:119]
	s_nop 0
	v_mov_b32_dpp v50, v48 row_shr:8 row_mask:0xf bank_mask:0xf bound_ctrl:1
	v_mov_b32_dpp v51, v49 row_shr:8 row_mask:0xf bank_mask:0xf bound_ctrl:1
	v_pk_add_f32 v[48:49], v[48:49], v[50:51]
	ds_swizzle_b32 v50, v48 offset:swizzle(BROADCAST,16,15)
	ds_swizzle_b32 v51, v49 offset:swizzle(BROADCAST,16,15)
	v_mov_b32_dpp v118, v62 row_shr:8 row_mask:0xf bank_mask:0xf bound_ctrl:1
	v_mov_b32_dpp v119, v63 row_shr:8 row_mask:0xf bank_mask:0xf bound_ctrl:1
	v_pk_add_f32 v[62:63], v[62:63], v[118:119]
	ds_swizzle_b32 v120, v62 offset:swizzle(BROADCAST,16,15)
	s_waitcnt lgkmcnt(1)
	v_pk_add_f32 v[60:61], v[50:51], 0 op_sel_hi:[1,0]
	v_lshlrev_b64 v[50:51], 2, v[96:97]
	v_lshl_add_u64 v[54:55], v[122:123], 0, v[50:51]
	v_mov_b32_dpp v122, v102 row_shr:2 row_mask:0xf bank_mask:0xf bound_ctrl:1
	v_mov_b32_dpp v123, v103 row_shr:2 row_mask:0xf bank_mask:0xf bound_ctrl:1
	v_pk_add_f32 v[102:103], v[102:103], v[122:123]
	ds_swizzle_b32 v121, v63 offset:swizzle(BROADCAST,16,15)
	v_pk_add_f32 v[118:119], v[166:167], v[62:63]
	v_mov_b32_dpp v122, v102 row_shr:4 row_mask:0xf bank_mask:0xf bound_ctrl:1
	v_mov_b32_dpp v123, v103 row_shr:4 row_mask:0xf bank_mask:0xf bound_ctrl:1
	v_pk_add_f32 v[102:103], v[102:103], v[122:123]
	s_waitcnt lgkmcnt(0)
	v_pk_add_f32 v[62:63], v[166:167], v[120:121]
	v_mul_f32_e32 v120, 0x3fb8aa3b, v79
	v_mov_b32_dpp v122, v102 row_shr:8 row_mask:0xf bank_mask:0xf bound_ctrl:1
	v_mov_b32_dpp v123, v103 row_shr:8 row_mask:0xf bank_mask:0xf bound_ctrl:1
	v_pk_add_f32 v[102:103], v[102:103], v[122:123]
	ds_swizzle_b32 v122, v102 offset:swizzle(BROADCAST,16,15)
	ds_swizzle_b32 v123, v103 offset:swizzle(BROADCAST,16,15)
	v_exp_f32_e32 v120, v120
	v_pk_add_f32 v[102:103], v[62:63], v[102:103]
	v_pk_add_f32 v[116:117], v[48:49], 0 op_sel_hi:[1,0]
	v_mul_f32_e32 v48, 0x3fb8aa3b, v76
	s_waitcnt lgkmcnt(0)
	v_pk_add_f32 v[122:123], v[62:63], v[122:123]
	v_mul_f32_e32 v62, 0x3fb8aa3b, v82
	v_exp_f32_e32 v62, v62
	v_sub_f32_e32 v166, 1.0, v120
	v_pk_add_f32 v[120:121], v[60:61], v[56:57]
	v_pk_add_f32 v[60:61], v[60:61], v[58:59]
	v_lshl_add_u64 v[58:59], v[126:127], 0, v[50:51]
	v_mov_b32_dpp v126, v110 row_shr:2 row_mask:0xf bank_mask:0xf bound_ctrl:1
	v_mov_b32_dpp v127, v111 row_shr:2 row_mask:0xf bank_mask:0xf bound_ctrl:1
	v_sub_f32_e32 v158, 1.0, v62
	v_mul_f32_e32 v62, 0x3fb8aa3b, v83
	v_pk_add_f32 v[110:111], v[110:111], v[126:127]
	v_exp_f32_e32 v62, v62
	v_exp_f32_e32 v48, v48
	v_mov_b32_dpp v126, v110 row_shr:4 row_mask:0xf bank_mask:0xf bound_ctrl:1
	v_mov_b32_dpp v127, v111 row_shr:4 row_mask:0xf bank_mask:0xf bound_ctrl:1
	v_pk_add_f32 v[110:111], v[110:111], v[126:127]
	v_sub_f32_e32 v159, 1.0, v62
	s_nop 0
	v_mov_b32_dpp v126, v110 row_shr:8 row_mask:0xf bank_mask:0xf bound_ctrl:1
	v_mov_b32_dpp v127, v111 row_shr:8 row_mask:0xf bank_mask:0xf bound_ctrl:1
	v_pk_add_f32 v[110:111], v[110:111], v[126:127]
	ds_swizzle_b32 v126, v110 offset:swizzle(BROADCAST,16,15)
	ds_swizzle_b32 v127, v111 offset:swizzle(BROADCAST,16,15)
	v_mov_b32_e32 v105, v161
	v_mov_b32_e32 v104, v160
	v_sub_f32_e32 v170, 1.0, v48
	v_mov_b32_dpp v63, v105 row_shr:1 row_mask:0xf bank_mask:0xf bound_ctrl:1
	v_mov_b32_dpp v62, v104 row_shr:1 row_mask:0xf bank_mask:0xf bound_ctrl:1
	v_pk_add_f32 v[62:63], v[104:105], v[62:63]
	v_mul_f32_e32 v48, 0x3fb8aa3b, v77
	v_exp_f32_e32 v48, v48
	v_mov_b32_dpp v106, v62 row_shr:2 row_mask:0xf bank_mask:0xf bound_ctrl:1
	v_mov_b32_dpp v107, v63 row_shr:2 row_mask:0xf bank_mask:0xf bound_ctrl:1
	v_pk_add_f32 v[62:63], v[62:63], v[106:107]
	v_pk_add_f32 v[110:111], v[122:123], v[110:111]
	s_waitcnt lgkmcnt(0)
; template <int CTRL> __device__ __forceinline__ float dppx(float v) { return __int_as_float(__builtin_amdgcn_update_dpp(0, __float_as_int(v), CTRL, 0xf, 0xf, true)); }
; __device__ __forceinline__ unsigned cvt_pk_bf16(float lo, float hi) { unsigned r; asm volatile("v_cvt_pk_bf16_f32 %0, %1, %2" : "=v"(r) : "v"(lo), "v"(hi)); return r; }
; __device__ __forceinline__ float log_forget(float z, float lb) {
;   const float r0 = fminf(z, 0.f) - __logf(1.f + __expf(-fabsf(z)));
;   const float r1 = __logf(lb + (1.f - lb) / (1.f + __expf(-z)));
;   return lb <= 0.f ? r0 : r1;
; }
;   __device__ __forceinline__ void operator()(const f32x4 (&acc)[2][2][4][2], const pg8::Unit& u, int wr, int wc, int fr, int fq) const {
;     ...
;               for (int q = 0; q < 4; ++q) { const float gv = log_forget(acc[ai][bj][m][qh][q], lq[q]); g[m][q] = gv;
;                 float sc = gv; sc += dppx<0x111>(sc); sc += dppx<0x112>(sc); sc += dppx<0x114>(sc); sc += dppx<0x118>(sc);
;                 const float tot16 = __int_as_float(__builtin_amdgcn_ds_swizzle(__float_as_int(sc), 0x1F0));
;                 cs[m][q] = sc + carry[q]; carry[q] += tot16; }
; #pragma unroll
;             for (int m = 0; m < 4; ++m) { const int r = row0 + ai * 128 + m * 16; float bq[4], kq[4];
; #pragma unroll
;               for (int q = 0; q < 4; ++q) { bq[q] = bwd ? (carry[q] - cs[m][q]) + g[m][q] : cs[m][q]; kq[q] = 1.f - __expf(g[m][q]); }
;               *(f32x4*)(logfp + (size_t)r * 1024 + c + 4 * qh) = (f32x4){bq[0], bq[1], bq[2], bq[3]};
;               u32x2 w; w.x = pg8::cvt_pk_bf16(kq[0], kq[1]); w.y = pg8::cvt_pk_bf16(kq[2], kq[3]);
;               *(u32x2*)(km + (size_t)r * 1024 + c + 4 * qh) = w; } } }
	v_pk_add_f32 v[122:123], v[122:123], v[126:127]
	v_mul_f32_e32 v126, 0x3fb8aa3b, v108
	v_mov_b32_dpp v106, v62 row_shr:4 row_mask:0xf bank_mask:0xf bound_ctrl:1
	v_mov_b32_dpp v107, v63 row_shr:4 row_mask:0xf bank_mask:0xf bound_ctrl:1
	v_exp_f32_e32 v126, v126
	v_pk_add_f32 v[62:63], v[62:63], v[106:107]
	v_sub_f32_e32 v171, 1.0, v48
	v_lshlrev_b64 v[48:49], 1, v[96:97]
	v_mov_b32_dpp v106, v62 row_shr:8 row_mask:0xf bank_mask:0xf bound_ctrl:1
	v_mov_b32_dpp v107, v63 row_shr:8 row_mask:0xf bank_mask:0xf bound_ctrl:1
	v_pk_add_f32 v[62:63], v[62:63], v[106:107]
	v_lshl_add_u64 v[52:53], v[124:125], 0, v[48:49]
	ds_swizzle_b32 v106, v62 offset:swizzle(BROADCAST,16,15)
	ds_swizzle_b32 v107, v63 offset:swizzle(BROADCAST,16,15)
	v_pk_add_f32 v[124:125], v[60:61], v[62:63]
	v_lshl_add_u64 v[62:63], v[130:131], 0, v[50:51]
	v_sub_f32_e32 v130, 1.0, v126
	v_mul_f32_e32 v126, 0x3fb8aa3b, v109
	v_exp_f32_e32 v126, v126
	v_mov_b32_dpp v127, v115 row_shr:2 row_mask:0xf bank_mask:0xf bound_ctrl:1
	v_mul_f32_e32 v56, 0x3fb8aa3b, v80
	v_exp_f32_e32 v56, v56
	v_sub_f32_e32 v131, 1.0, v126
	v_mov_b32_dpp v126, v114 row_shr:2 row_mask:0xf bank_mask:0xf bound_ctrl:1
	v_pk_add_f32 v[114:115], v[114:115], v[126:127]
	v_sub_f32_e32 v167, 1.0, v56
	v_mul_f32_e32 v56, 0x3fb8aa3b, v81
	v_mov_b32_dpp v126, v114 row_shr:4 row_mask:0xf bank_mask:0xf bound_ctrl:1
	v_mov_b32_dpp v127, v115 row_shr:4 row_mask:0xf bank_mask:0xf bound_ctrl:1
	v_pk_add_f32 v[114:115], v[114:115], v[126:127]
	v_exp_f32_e32 v56, v56
	s_waitcnt lgkmcnt(0)
	v_pk_add_f32 v[106:107], v[60:61], v[106:107]
	v_mov_b32_dpp v126, v114 row_shr:8 row_mask:0xf bank_mask:0xf bound_ctrl:1
	v_mov_b32_dpp v127, v115 row_shr:8 row_mask:0xf bank_mask:0xf bound_ctrl:1
	v_pk_add_f32 v[114:115], v[114:115], v[126:127]
	ds_swizzle_b32 v126, v114 offset:swizzle(BROADCAST,16,15)
	ds_swizzle_b32 v127, v115 offset:swizzle(BROADCAST,16,15)
	v_pk_add_f32 v[114:115], v[106:107], v[114:115]
	v_sub_f32_e32 v172, 1.0, v56
	v_lshl_add_u64 v[56:57], v[128:129], 0, v[48:49]
	v_mul_f32_e32 v60, 0x3fb8aa3b, v104
	s_waitcnt lgkmcnt(0)
	v_pk_add_f32 v[106:107], v[106:107], v[126:127]
	v_pk_add_f32 v[126:127], v[122:123], v[74:75] neg_lo:[0,1] neg_hi:[0,1]
	v_pk_add_f32 v[128:129], v[106:107], v[116:117] neg_lo:[0,1] neg_hi:[0,1]
	v_pk_add_f32 v[72:73], v[72:73], v[126:127]
	v_pk_add_f32 v[76:77], v[76:77], v[128:129]
	v_mul_f32_e32 v96, 0x3fb8aa3b, v78
	v_exp_f32_e32 v60, v60
	v_cndmask_b32_e64 v77, v117, v77, s[42:43]
	v_cndmask_b32_e64 v76, v116, v76, s[42:43]
	v_cndmask_b32_e64 v75, v75, v73, s[42:43]
	v_cndmask_b32_e64 v74, v74, v72, s[42:43]
	v_exp_f32_e32 v96, v96
	global_store_dwordx4 v[54:55], v[74:77], off
	v_cvt_pk_bf16_f32 v72, v168, v169
	v_cvt_pk_bf16_f32 v73, v170, v171
	global_store_dwordx2 v[52:53], v[72:73], off
	v_pk_add_f32 v[72:73], v[122:123], v[118:119] neg_lo:[0,1] neg_hi:[0,1]
	v_pk_add_f32 v[74:75], v[106:107], v[120:121] neg_lo:[0,1] neg_hi:[0,1]
	v_pk_add_f32 v[72:73], v[78:79], v[72:73]
	v_pk_add_f32 v[74:75], v[80:81], v[74:75]
	v_sub_f32_e32 v160, 1.0, v60
	v_mul_f32_e32 v60, 0x3fb8aa3b, v105
	v_cndmask_b32_e64 v75, v121, v75, s[42:43]
	v_cndmask_b32_e64 v74, v120, v74, s[42:43]
	v_cndmask_b32_e64 v73, v119, v73, s[42:43]
	v_cndmask_b32_e64 v72, v118, v72, s[42:43]
	v_sub_f32_e32 v96, 1.0, v96
	v_exp_f32_e32 v60, v60
	global_store_dwordx4 v[58:59], v[72:75], off
	v_sub_f32_e32 v161, 1.0, v60
	s_nop 0
	v_cvt_pk_bf16_f32 v72, v96, v166
	v_cvt_pk_bf16_f32 v73, v167, v172
	global_store_dwordx2 v[56:57], v[72:73], off
	v_pk_add_f32 v[72:73], v[122:123], v[102:103] neg_lo:[0,1] neg_hi:[0,1]
	v_pk_add_f32 v[74:75], v[106:107], v[124:125] neg_lo:[0,1] neg_hi:[0,1]
	v_pk_add_f32 v[72:73], v[82:83], v[72:73]
	v_pk_add_f32 v[74:75], v[104:105], v[74:75]
	v_cndmask_b32_e64 v73, v103, v73, s[42:43]
	v_cndmask_b32_e64 v75, v125, v75, s[42:43]
	v_cndmask_b32_e64 v74, v124, v74, s[42:43]
	v_cndmask_b32_e64 v72, v102, v72, s[42:43]
	v_lshl_add_u64 v[60:61], v[132:133], 0, v[48:49]
	global_store_dwordx4 v[62:63], v[72:75], off
	s_nop 1
	v_cvt_pk_bf16_f32 v72, v158, v159
	v_cvt_pk_bf16_f32 v73, v160, v161
	global_store_dwordx2 v[60:61], v[72:73], off
	v_mul_f32_e32 v72, 0x3fb8aa3b, v112
	v_exp_f32_e32 v72, v72
	v_pk_add_f32 v[74:75], v[106:107], v[114:115] neg_lo:[0,1] neg_hi:[0,1]
	v_sub_f32_e32 v78, 1.0, v72
	v_pk_add_f32 v[72:73], v[122:123], v[110:111] neg_lo:[0,1] neg_hi:[0,1]
	v_pk_add_f32 v[74:75], v[112:113], v[74:75]
	v_pk_add_f32 v[72:73], v[108:109], v[72:73]
	v_cndmask_b32_e64 v76, v114, v74, s[42:43]
	v_cndmask_b32_e64 v74, v110, v72, s[42:43]
	v_mul_f32_e32 v72, 0x3fb8aa3b, v113
	v_exp_f32_e32 v72, v72
	v_cndmask_b32_e64 v77, v115, v75, s[42:43]
	v_cndmask_b32_e64 v75, v111, v73, s[42:43]
	v_sub_f32_e32 v114, 1.0, v64
	v_sub_f32_e32 v79, 1.0, v72
	v_lshl_add_u64 v[72:73], v[134:135], 0, v[50:51]
	global_store_dwordx4 v[72:73], v[74:77], off
	v_sub_f32_e32 v113, 1.0, v65
	v_sub_f32_e32 v112, 1.0, v66
	v_cvt_pk_bf16_f32 v76, v130, v131
	v_cvt_pk_bf16_f32 v77, v78, v79
	v_lshl_add_u64 v[74:75], v[136:137], 0, v[48:49]
	global_store_dwordx2 v[74:75], v[76:77], off
	v_mul_f32_e32 v44, 0xbfb8aa3b, v44
	v_exp_f32_e32 v44, v44
	s_nop 0
	v_add_f32_e32 v44, 1.0, v44
	s_nop 0
	s_nop 1
	v_div_scale_f32 v77, s[2:3], v44, v44, v114
	v_rcp_f32_e32 v79, v77
	s_nop 0
	v_fma_f32 v80, -v77, v79, 1.0
	v_fmac_f32_e32 v79, v80, v79
	v_div_scale_f32 v80, vcc, v114, v44, v114
	v_mul_f32_e32 v81, v80, v79
	v_fma_f32 v82, -v77, v81, v80
	v_fmac_f32_e32 v81, v82, v79
	v_fma_f32 v77, -v77, v81, v80
	v_div_fmas_f32 v77, v77, v79, v81
	v_div_fixup_f32 v44, v77, v44, v114
	v_add_f32_e32 v44, v64, v44
	v_cmp_gt_f32_e32 vcc, s37, v44
; __device__ __forceinline__ float log_forget(float z, float lb) {
;   const float r0 = fminf(z, 0.f) - __logf(1.f + __expf(-fabsf(z)));
;   const float r1 = __logf(lb + (1.f - lb) / (1.f + __expf(-z)));
;   return lb <= 0.f ? r0 : r1;
; }
;   __device__ __forceinline__ void operator()(const f32x4 (&acc)[2][2][4][2], const pg8::Unit& u, int wr, int wc, int fr, int fq) const {
;     ...
;           for (int qh = 0; qh < 2; ++qh) { float g[4][4], cs[4][4], carry[4];
;             const f32x4 lq = qh == 0 ? l0 : l1;
; #pragma unroll
;             for (int q = 0; q < 4; ++q) carry[q] = 0.f;
; #pragma unroll
;             for (int m = 0; m < 4; ++m)
; #pragma unroll
;               for (int q = 0; q < 4; ++q) { const float gv = log_forget(acc[ai][bj][m][qh][q], lq[q]); g[m][q] = gv;
	s_nop 1
	v_cndmask_b32_e64 v77, 0, 32, vcc
	v_ldexp_f32 v44, v44, v77
	v_log_f32_e32 v44, v44
	s_nop 0
	v_mul_f32_e32 v77, 0x3f317217, v44
	v_fma_f32 v77, v44, s33, -v77
	v_fmac_f32_e32 v77, 0x3377d1cf, v44
	v_fmac_f32_e32 v77, 0x3f317217, v44
	v_cmp_lt_f32_e64 s[48:49], |v44|, s36
	s_nop 1
	v_cndmask_b32_e64 v44, v44, v77, s[48:49]
	v_cndmask_b32_e32 v77, 0, v216, vcc
	v_sub_f32_e32 v115, v44, v77
	s_nop 0
	s_nop 1
	s_nop 0
	s_nop 1
	v_mul_f32_e32 v44, 0xbfb8aa3b, v45
	v_exp_f32_e32 v44, v44
	s_nop 0
	v_add_f32_e32 v44, 1.0, v44
	v_div_scale_f32 v45, s[2:3], v44, v44, v113
	v_rcp_f32_e32 v80, v45
	s_nop 0
	v_fma_f32 v81, -v45, v80, 1.0
	v_fmac_f32_e32 v80, v81, v80
	v_div_scale_f32 v81, vcc, v113, v44, v113
	v_mul_f32_e32 v82, v81, v80
	v_fma_f32 v83, -v45, v82, v81
	v_fmac_f32_e32 v82, v83, v80
	v_fma_f32 v45, -v45, v82, v81
	v_div_fmas_f32 v45, v45, v80, v82
	v_div_fixup_f32 v44, v45, v44, v113
	v_add_f32_e32 v44, v65, v44
	v_cmp_gt_f32_e32 vcc, s37, v44
	s_nop 1
	v_cndmask_b32_e64 v45, 0, 32, vcc
	v_ldexp_f32 v44, v44, v45
	v_log_f32_e32 v44, v44
	s_nop 0
	v_mul_f32_e32 v45, 0x3f317217, v44
	v_fma_f32 v45, v44, s33, -v45
	v_fmac_f32_e32 v45, 0x3377d1cf, v44
	v_fmac_f32_e32 v45, 0x3f317217, v44
	v_cmp_lt_f32_e64 s[48:49], |v44|, s36
	s_nop 1
	v_cndmask_b32_e64 v44, v44, v45, s[48:49]
	v_cndmask_b32_e32 v45, 0, v216, vcc
	v_sub_f32_e32 v116, v44, v45
	s_nop 1
	s_nop 0
	s_nop 1
	v_mul_f32_e32 v45, 0xbfb8aa3b, v46
	v_exp_f32_e32 v45, v45
	s_nop 0
	v_add_f32_e32 v45, 1.0, v45
	v_div_scale_f32 v46, s[2:3], v45, v45, v112
	v_rcp_f32_e32 v81, v46
	s_nop 0
	v_fma_f32 v82, -v46, v81, 1.0
	v_fmac_f32_e32 v81, v82, v81
	v_div_scale_f32 v82, vcc, v112, v45, v112
	v_mul_f32_e32 v83, v82, v81
	v_fma_f32 v96, -v46, v83, v82
	v_fmac_f32_e32 v83, v96, v81
	v_fma_f32 v46, -v46, v83, v82
	v_div_fmas_f32 v46, v46, v81, v83
	v_div_fixup_f32 v45, v46, v45, v112
	v_add_f32_e32 v45, v66, v45
	v_cmp_gt_f32_e32 vcc, s37, v45
	v_sub_f32_e32 v96, 1.0, v67
	s_nop 0
	v_cndmask_b32_e64 v46, 0, 32, vcc
	v_ldexp_f32 v45, v45, v46
	v_log_f32_e32 v45, v45
	s_nop 0
	v_mul_f32_e32 v46, 0x3f317217, v45
	v_fma_f32 v46, v45, s33, -v46
	v_fmac_f32_e32 v46, 0x3377d1cf, v45
	v_fmac_f32_e32 v46, 0x3f317217, v45
	v_cmp_lt_f32_e64 s[48:49], |v45|, s36
	s_nop 1
	v_cndmask_b32_e64 v45, v45, v46, s[48:49]
	v_cndmask_b32_e32 v46, 0, v216, vcc
	v_sub_f32_e32 v117, v45, v46
	s_nop 1
	s_nop 0
	s_nop 1
	v_mul_f32_e32 v46, 0xbfb8aa3b, v47
	v_exp_f32_e32 v46, v46
	s_nop 0
	v_add_f32_e32 v46, 1.0, v46
	v_div_scale_f32 v47, s[2:3], v46, v46, v96
	v_rcp_f32_e32 v82, v47
	v_mov_b32_e32 v44, v117
	v_fma_f32 v83, -v47, v82, 1.0
	v_fmac_f32_e32 v82, v83, v82
	v_div_scale_f32 v83, vcc, v96, v46, v96
	v_mul_f32_e32 v102, v83, v82
	v_fma_f32 v103, -v47, v102, v83
	v_fmac_f32_e32 v102, v103, v82
	v_fma_f32 v47, -v47, v102, v83
	v_div_fmas_f32 v47, v47, v82, v102
	v_div_fixup_f32 v46, v47, v46, v96
	v_add_f32_e32 v46, v67, v46
	v_cmp_gt_f32_e32 vcc, s37, v46
	s_nop 1
	v_cndmask_b32_e64 v47, 0, 32, vcc
	v_ldexp_f32 v46, v46, v47
	v_log_f32_e32 v46, v46
	s_nop 0
	v_mul_f32_e32 v47, 0x3f317217, v46
	v_fma_f32 v47, v46, s33, -v47
	v_fmac_f32_e32 v47, 0x3377d1cf, v46
	v_fmac_f32_e32 v47, 0x3f317217, v46
	v_cmp_lt_f32_e64 s[48:49], |v46|, s36
	s_nop 1
	v_cndmask_b32_e64 v46, v46, v47, s[48:49]
	v_cndmask_b32_e32 v47, 0, v216, vcc
	v_sub_f32_e32 v118, v46, v47
	v_mul_f32_e32 v40, 0xbfb8aa3b, v40
	v_exp_f32_e32 v40, v40
	v_mov_b32_e32 v45, v118
	v_add_f32_e32 v40, 1.0, v40
	s_nop 1
	v_div_scale_f32 v47, s[2:3], v40, v40, v114
	v_rcp_f32_e32 v83, v47
	s_nop 0
	v_fma_f32 v102, -v47, v83, 1.0
	v_fmac_f32_e32 v83, v102, v83
	v_div_scale_f32 v102, vcc, v114, v40, v114
	v_mul_f32_e32 v103, v102, v83
	v_fma_f32 v104, -v47, v103, v102
	v_fmac_f32_e32 v103, v104, v83
	v_fma_f32 v47, -v47, v103, v102
	v_div_fmas_f32 v47, v47, v83, v103
	v_div_fixup_f32 v40, v47, v40, v114
	v_add_f32_e32 v40, v64, v40
	v_cmp_gt_f32_e32 vcc, s37, v40
	s_nop 1
	v_cndmask_b32_e64 v47, 0, 32, vcc
	v_ldexp_f32 v40, v40, v47
	v_log_f32_e32 v40, v40
	s_nop 0
	v_mul_f32_e32 v47, 0x3f317217, v40
	v_fma_f32 v47, v40, s33, -v47
	v_fmac_f32_e32 v47, 0x3377d1cf, v40
	v_fmac_f32_e32 v47, 0x3f317217, v40
	v_cmp_lt_f32_e64 s[48:49], |v40|, s36
	s_nop 1
	v_cndmask_b32_e64 v40, v40, v47, s[48:49]
	v_cndmask_b32_e32 v47, 0, v216, vcc
	v_sub_f32_e32 v119, v40, v47
	s_nop 0
	s_nop 1
	s_nop 0
	s_nop 1
	v_mul_f32_e32 v40, 0xbfb8aa3b, v41
	v_exp_f32_e32 v40, v40
	s_nop 0
	v_add_f32_e32 v40, 1.0, v40
	v_div_scale_f32 v41, s[2:3], v40, v40, v113
	v_rcp_f32_e32 v102, v41
	s_nop 0
	v_fma_f32 v103, -v41, v102, 1.0
	v_fmac_f32_e32 v102, v103, v102
	v_div_scale_f32 v103, vcc, v113, v40, v113
	v_mul_f32_e32 v104, v103, v102
	v_fma_f32 v105, -v41, v104, v103
	v_fmac_f32_e32 v104, v105, v102
	v_fma_f32 v41, -v41, v104, v103
	v_div_fmas_f32 v41, v41, v102, v104
	v_div_fixup_f32 v40, v41, v40, v113
	v_add_f32_e32 v40, v65, v40
	v_cmp_gt_f32_e32 vcc, s37, v40
	s_nop 1
	v_cndmask_b32_e64 v41, 0, 32, vcc
	v_ldexp_f32 v40, v40, v41
	v_log_f32_e32 v40, v40
	s_nop 0
	v_mul_f32_e32 v41, 0x3f317217, v40
	v_fma_f32 v41, v40, s33, -v41
	v_fmac_f32_e32 v41, 0x3377d1cf, v40
	v_fmac_f32_e32 v41, 0x3f317217, v40
	v_cmp_lt_f32_e64 s[48:49], |v40|, s36
	s_nop 1
	v_cndmask_b32_e64 v40, v40, v41, s[48:49]
	v_cndmask_b32_e32 v41, 0, v216, vcc
	v_sub_f32_e32 v120, v40, v41
	v_mov_b32_e32 v47, v120
	s_nop 1
	s_nop 0
	s_nop 1
	v_mul_f32_e32 v41, 0xbfb8aa3b, v42
	v_exp_f32_e32 v41, v41
	s_nop 0
	v_add_f32_e32 v41, 1.0, v41
	v_div_scale_f32 v42, s[2:3], v41, v41, v112
	v_rcp_f32_e32 v103, v42
	s_nop 0
	v_fma_f32 v104, -v42, v103, 1.0
	v_fmac_f32_e32 v103, v104, v103
	v_div_scale_f32 v104, vcc, v112, v41, v112
; __device__ __forceinline__ float log_forget(float z, float lb) {
;   const float r0 = fminf(z, 0.f) - __logf(1.f + __expf(-fabsf(z)));
;   const float r1 = __logf(lb + (1.f - lb) / (1.f + __expf(-z)));
;   return lb <= 0.f ? r0 : r1;
; }
;   __device__ __forceinline__ void operator()(const f32x4 (&acc)[2][2][4][2], const pg8::Unit& u, int wr, int wc, int fr, int fq) const {
;     ...
;           for (int qh = 0; qh < 2; ++qh) { float g[4][4], cs[4][4], carry[4];
;             const f32x4 lq = qh == 0 ? l0 : l1;
; #pragma unroll
;             for (int q = 0; q < 4; ++q) carry[q] = 0.f;
; #pragma unroll
;             for (int m = 0; m < 4; ++m)
; #pragma unroll
;               for (int q = 0; q < 4; ++q) { const float gv = log_forget(acc[ai][bj][m][qh][q], lq[q]); g[m][q] = gv;
	v_mul_f32_e32 v105, v104, v103
	v_fma_f32 v106, -v42, v105, v104
	v_fmac_f32_e32 v105, v106, v103
	v_fma_f32 v42, -v42, v105, v104
	v_div_fmas_f32 v42, v42, v103, v105
	v_div_fixup_f32 v41, v42, v41, v112
	v_add_f32_e32 v41, v66, v41
	v_cmp_gt_f32_e32 vcc, s37, v41
	s_nop 1
	v_cndmask_b32_e64 v42, 0, 32, vcc
	v_ldexp_f32 v41, v41, v42
	v_log_f32_e32 v41, v41
	s_nop 0
	v_mul_f32_e32 v42, 0x3f317217, v41
	v_fma_f32 v42, v41, s33, -v42
	v_fmac_f32_e32 v42, 0x3377d1cf, v41
	v_fmac_f32_e32 v42, 0x3f317217, v41
	v_cmp_lt_f32_e64 s[48:49], |v41|, s36
	s_nop 1
	v_cndmask_b32_e64 v41, v41, v42, s[48:49]
	v_cndmask_b32_e32 v42, 0, v216, vcc
	v_sub_f32_e32 v121, v41, v42
	s_nop 1
	s_nop 0
	s_nop 1
	v_mul_f32_e32 v42, 0xbfb8aa3b, v43
	v_exp_f32_e32 v42, v42
	s_nop 0
	v_add_f32_e32 v42, 1.0, v42
	v_div_scale_f32 v43, s[2:3], v42, v42, v96
	v_rcp_f32_e32 v104, v43
	v_mov_b32_e32 v40, v121
	v_fma_f32 v105, -v43, v104, 1.0
	v_fmac_f32_e32 v104, v105, v104
	v_div_scale_f32 v105, vcc, v96, v42, v96
	v_mul_f32_e32 v106, v105, v104
	v_fma_f32 v107, -v43, v106, v105
	v_fmac_f32_e32 v106, v107, v104
	v_fma_f32 v43, -v43, v106, v105
	v_div_fmas_f32 v43, v43, v104, v106
	v_div_fixup_f32 v42, v43, v42, v96
	v_add_f32_e32 v42, v67, v42
	v_cmp_gt_f32_e32 vcc, s37, v42
	s_nop 1
	v_cndmask_b32_e64 v43, 0, 32, vcc
	v_ldexp_f32 v42, v42, v43
	v_log_f32_e32 v42, v42
	s_nop 0
	v_mul_f32_e32 v43, 0x3f317217, v42
	v_fma_f32 v43, v42, s33, -v43
	v_fmac_f32_e32 v43, 0x3377d1cf, v42
	v_fmac_f32_e32 v43, 0x3f317217, v42
	v_cmp_lt_f32_e64 s[48:49], |v42|, s36
	s_nop 1
	v_cndmask_b32_e64 v42, v42, v43, s[48:49]
	v_cndmask_b32_e32 v43, 0, v216, vcc
	v_sub_f32_e32 v122, v42, v43
	v_mul_f32_e32 v36, 0xbfb8aa3b, v36
	v_exp_f32_e32 v36, v36
	v_mov_b32_e32 v41, v122
	v_add_f32_e32 v36, 1.0, v36
	s_nop 1
	v_div_scale_f32 v43, s[2:3], v36, v36, v114
	v_rcp_f32_e32 v105, v43
	s_nop 0
	v_fma_f32 v106, -v43, v105, 1.0
	v_fmac_f32_e32 v105, v106, v105
	v_div_scale_f32 v106, vcc, v114, v36, v114
	v_mul_f32_e32 v107, v106, v105
	v_fma_f32 v108, -v43, v107, v106
	v_fmac_f32_e32 v107, v108, v105
	v_fma_f32 v43, -v43, v107, v106
	v_div_fmas_f32 v43, v43, v105, v107
	v_div_fixup_f32 v36, v43, v36, v114
	v_add_f32_e32 v36, v64, v36
	v_cmp_gt_f32_e32 vcc, s37, v36
	s_nop 1
	v_cndmask_b32_e64 v43, 0, 32, vcc
	v_ldexp_f32 v36, v36, v43
	v_log_f32_e32 v36, v36
	s_nop 0
	v_mul_f32_e32 v43, 0x3f317217, v36
	v_fma_f32 v43, v36, s33, -v43
	v_fmac_f32_e32 v43, 0x3377d1cf, v36
	v_fmac_f32_e32 v43, 0x3f317217, v36
	v_cmp_lt_f32_e64 s[48:49], |v36|, s36
	s_nop 1
	v_cndmask_b32_e64 v36, v36, v43, s[48:49]
	v_cndmask_b32_e32 v43, 0, v216, vcc
	v_sub_f32_e32 v123, v36, v43
	s_nop 0
	s_nop 1
	s_nop 0
	s_nop 1
	v_mul_f32_e32 v36, 0xbfb8aa3b, v37
	v_exp_f32_e32 v36, v36
	s_nop 0
	v_add_f32_e32 v36, 1.0, v36
	v_div_scale_f32 v37, s[2:3], v36, v36, v113
	v_rcp_f32_e32 v106, v37
	s_nop 0
	v_fma_f32 v107, -v37, v106, 1.0
	v_fmac_f32_e32 v106, v107, v106
	v_div_scale_f32 v107, vcc, v113, v36, v113
	v_mul_f32_e32 v108, v107, v106
	v_fma_f32 v109, -v37, v108, v107
	v_fmac_f32_e32 v108, v109, v106
	v_fma_f32 v37, -v37, v108, v107
	v_div_fmas_f32 v37, v37, v106, v108
	v_div_fixup_f32 v36, v37, v36, v113
	v_add_f32_e32 v36, v65, v36
	v_cmp_gt_f32_e32 vcc, s37, v36
	s_nop 1
	v_cndmask_b32_e64 v37, 0, 32, vcc
	v_ldexp_f32 v36, v36, v37
	v_log_f32_e32 v36, v36
	s_nop 0
	v_mul_f32_e32 v37, 0x3f317217, v36
	v_fma_f32 v37, v36, s33, -v37
	v_fmac_f32_e32 v37, 0x3377d1cf, v36
	v_fmac_f32_e32 v37, 0x3f317217, v36
	v_cmp_lt_f32_e64 s[48:49], |v36|, s36
	s_nop 1
	v_cndmask_b32_e64 v36, v36, v37, s[48:49]
	v_cndmask_b32_e32 v37, 0, v216, vcc
	v_sub_f32_e32 v124, v36, v37
	v_mov_b32_e32 v43, v124
	s_nop 1
	v_mov_b32_dpp v105, v43 row_shr:1 row_mask:0xf bank_mask:0xf bound_ctrl:1
	s_nop 0
	s_nop 0
	s_nop 1
	v_mul_f32_e32 v37, 0xbfb8aa3b, v38
	v_exp_f32_e32 v37, v37
	s_nop 0
	v_add_f32_e32 v37, 1.0, v37
	v_div_scale_f32 v38, s[2:3], v37, v37, v112
	v_rcp_f32_e32 v107, v38
	s_nop 0
	v_fma_f32 v108, -v38, v107, 1.0
	v_fmac_f32_e32 v107, v108, v107
	v_div_scale_f32 v108, vcc, v112, v37, v112
	v_mul_f32_e32 v109, v108, v107
	v_fma_f32 v110, -v38, v109, v108
	v_fmac_f32_e32 v109, v110, v107
	v_fma_f32 v38, -v38, v109, v108
	v_div_fmas_f32 v38, v38, v107, v109
	v_div_fixup_f32 v37, v38, v37, v112
	v_add_f32_e32 v37, v66, v37
	v_cmp_gt_f32_e32 vcc, s37, v37
	s_nop 1
	v_cndmask_b32_e64 v38, 0, 32, vcc
	v_ldexp_f32 v37, v37, v38
	v_log_f32_e32 v37, v37
	s_nop 0
	v_mul_f32_e32 v38, 0x3f317217, v37
	v_fma_f32 v38, v37, s33, -v38
	v_fmac_f32_e32 v38, 0x3377d1cf, v37
	v_fmac_f32_e32 v38, 0x3f317217, v37
	v_cmp_lt_f32_e64 s[48:49], |v37|, s36
	s_nop 1
	v_cndmask_b32_e64 v37, v37, v38, s[48:49]
	v_cndmask_b32_e32 v38, 0, v216, vcc
	v_sub_f32_e32 v125, v37, v38
	s_nop 1
	s_nop 0
	s_nop 1
	v_mul_f32_e32 v38, 0xbfb8aa3b, v39
	v_exp_f32_e32 v38, v38
	s_nop 0
	v_add_f32_e32 v38, 1.0, v38
	v_div_scale_f32 v39, s[2:3], v38, v38, v96
	v_rcp_f32_e32 v108, v39
	v_mov_b32_e32 v36, v125
	v_fma_f32 v109, -v39, v108, 1.0
	v_fmac_f32_e32 v108, v109, v108
	v_div_scale_f32 v109, vcc, v96, v38, v96
	v_mul_f32_e32 v110, v109, v108
	v_fma_f32 v111, -v39, v110, v109
	v_fmac_f32_e32 v110, v111, v108
	v_fma_f32 v39, -v39, v110, v109
	v_div_fmas_f32 v39, v39, v108, v110
	v_div_fixup_f32 v38, v39, v38, v96
	v_add_f32_e32 v38, v67, v38
	v_cmp_gt_f32_e32 vcc, s37, v38
	v_mov_b32_dpp v106, v36 row_shr:1 row_mask:0xf bank_mask:0xf bound_ctrl:1
	s_nop 0
	v_cndmask_b32_e64 v39, 0, 32, vcc
	v_ldexp_f32 v38, v38, v39
	v_log_f32_e32 v38, v38
	s_nop 0
	v_mul_f32_e32 v39, 0x3f317217, v38
	v_fma_f32 v39, v38, s33, -v39
	v_fmac_f32_e32 v39, 0x3377d1cf, v38
	v_fmac_f32_e32 v39, 0x3f317217, v38
; template <int CTRL> __device__ __forceinline__ float dppx(float v) { return __int_as_float(__builtin_amdgcn_update_dpp(0, __float_as_int(v), CTRL, 0xf, 0xf, true)); }
; __device__ __forceinline__ float log_forget(float z, float lb) {
;   const float r0 = fminf(z, 0.f) - __logf(1.f + __expf(-fabsf(z)));
;   const float r1 = __logf(lb + (1.f - lb) / (1.f + __expf(-z)));
;   return lb <= 0.f ? r0 : r1;
; }
;   __device__ __forceinline__ void operator()(const f32x4 (&acc)[2][2][4][2], const pg8::Unit& u, int wr, int wc, int fr, int fq) const {
;     ...
;           for (int qh = 0; qh < 2; ++qh) { float g[4][4], cs[4][4], carry[4];
;             const f32x4 lq = qh == 0 ? l0 : l1;
; #pragma unroll
;             for (int q = 0; q < 4; ++q) carry[q] = 0.f;
; #pragma unroll
;             for (int m = 0; m < 4; ++m)
; #pragma unroll
;               for (int q = 0; q < 4; ++q) { const float gv = log_forget(acc[ai][bj][m][qh][q], lq[q]); g[m][q] = gv;
;                 float sc = gv; sc += dppx<0x111>(sc); sc += dppx<0x112>(sc); sc += dppx<0x114>(sc); sc += dppx<0x118>(sc);
;                 const float tot16 = __int_as_float(__builtin_amdgcn_ds_swizzle(__float_as_int(sc), 0x1F0));
	v_cmp_lt_f32_e64 s[48:49], |v38|, s36
	s_nop 1
	v_cndmask_b32_e64 v38, v38, v39, s[48:49]
	v_cndmask_b32_e32 v39, 0, v216, vcc
	v_sub_f32_e32 v126, v38, v39
	v_mul_f32_e32 v32, 0xbfb8aa3b, v32
	v_exp_f32_e32 v32, v32
	v_mov_b32_e32 v37, v126
	v_add_f32_e32 v32, 1.0, v32
	s_nop 0
	v_mov_b32_dpp v107, v37 row_shr:1 row_mask:0xf bank_mask:0xf bound_ctrl:1
	v_pk_add_f32 v[106:107], v[36:37], v[106:107]
	s_nop 1
	v_div_scale_f32 v39, s[2:3], v32, v32, v114
	v_rcp_f32_e32 v109, v39
	s_nop 0
	v_fma_f32 v110, -v39, v109, 1.0
	v_fmac_f32_e32 v109, v110, v109
	v_div_scale_f32 v110, vcc, v114, v32, v114
	v_mul_f32_e32 v111, v110, v109
	v_fma_f32 v127, -v39, v111, v110
	v_fmac_f32_e32 v111, v127, v109
	v_fma_f32 v39, -v39, v111, v110
	v_div_fmas_f32 v39, v39, v109, v111
	v_div_fixup_f32 v32, v39, v32, v114
	v_add_f32_e32 v32, v64, v32
	v_cmp_gt_f32_e32 vcc, s37, v32
	s_nop 1
	v_cndmask_b32_e64 v39, 0, 32, vcc
	v_ldexp_f32 v32, v32, v39
	v_log_f32_e32 v32, v32
	s_nop 0
	v_mul_f32_e32 v39, 0x3f317217, v32
	v_fma_f32 v39, v32, s33, -v39
	v_fmac_f32_e32 v39, 0x3377d1cf, v32
	v_fmac_f32_e32 v39, 0x3f317217, v32
	v_cmp_lt_f32_e64 s[48:49], |v32|, s36
	s_nop 1
	v_cndmask_b32_e64 v32, v32, v39, s[48:49]
	v_cndmask_b32_e32 v39, 0, v216, vcc
	v_sub_f32_e32 v127, v32, v39
	s_nop 0
	s_nop 1
	s_nop 0
	s_nop 1
	v_mul_f32_e32 v32, 0xbfb8aa3b, v33
	v_exp_f32_e32 v32, v32
	s_nop 0
	v_add_f32_e32 v32, 1.0, v32
	v_div_scale_f32 v33, s[2:3], v32, v32, v113
	v_rcp_f32_e32 v110, v33
	s_nop 0
	v_fma_f32 v111, -v33, v110, 1.0
	v_fmac_f32_e32 v110, v111, v110
	v_div_scale_f32 v111, vcc, v113, v32, v113
	v_mul_f32_e32 v128, v111, v110
	v_fma_f32 v129, -v33, v128, v111
	v_fmac_f32_e32 v128, v129, v110
	v_fma_f32 v33, -v33, v128, v111
	v_div_fmas_f32 v33, v33, v110, v128
	v_div_fixup_f32 v32, v33, v32, v113
	v_add_f32_e32 v32, v65, v32
	v_cmp_gt_f32_e32 vcc, s37, v32
	s_nop 1
	v_cndmask_b32_e64 v33, 0, 32, vcc
	v_ldexp_f32 v32, v32, v33
	v_log_f32_e32 v32, v32
	s_nop 0
	v_mul_f32_e32 v33, 0x3f317217, v32
	v_fma_f32 v33, v32, s33, -v33
	v_fmac_f32_e32 v33, 0x3377d1cf, v32
	v_fmac_f32_e32 v33, 0x3f317217, v32
	v_cmp_lt_f32_e64 s[48:49], |v32|, s36
	s_nop 1
	v_cndmask_b32_e64 v32, v32, v33, s[48:49]
	v_cndmask_b32_e32 v33, 0, v216, vcc
	v_sub_f32_e32 v128, v32, v33
	v_mov_b32_e32 v39, v128
	s_nop 1
	v_mov_b32_dpp v109, v39 row_shr:1 row_mask:0xf bank_mask:0xf bound_ctrl:1
	s_nop 0
	s_nop 0
	s_nop 1
	v_mul_f32_e32 v33, 0xbfb8aa3b, v34
	v_exp_f32_e32 v33, v33
	s_nop 0
	v_add_f32_e32 v33, 1.0, v33
	v_div_scale_f32 v34, s[2:3], v33, v33, v112
	v_rcp_f32_e32 v111, v34
	s_nop 0
	v_fma_f32 v129, -v34, v111, 1.0
	v_fmac_f32_e32 v111, v129, v111
	v_div_scale_f32 v129, vcc, v112, v33, v112
	v_mul_f32_e32 v130, v129, v111
	v_fma_f32 v131, -v34, v130, v129
	v_fmac_f32_e32 v130, v131, v111
	v_fma_f32 v34, -v34, v130, v129
	v_div_fmas_f32 v34, v34, v111, v130
	v_div_fixup_f32 v33, v34, v33, v112
	v_add_f32_e32 v33, v66, v33
	v_cmp_gt_f32_e32 vcc, s37, v33
	s_nop 1
	v_cndmask_b32_e64 v34, 0, 32, vcc
	v_ldexp_f32 v33, v33, v34
	v_log_f32_e32 v33, v33
	s_nop 0
	v_mul_f32_e32 v34, 0x3f317217, v33
	v_fma_f32 v34, v33, s33, -v34
	v_fmac_f32_e32 v34, 0x3377d1cf, v33
	v_fmac_f32_e32 v34, 0x3f317217, v33
	v_cmp_lt_f32_e64 s[48:49], |v33|, s36
	s_nop 1
	v_cndmask_b32_e64 v33, v33, v34, s[48:49]
	v_cndmask_b32_e32 v34, 0, v216, vcc
	v_sub_f32_e32 v129, v33, v34
	s_nop 1
	s_nop 0
	s_nop 1
	v_mul_f32_e32 v34, 0xbfb8aa3b, v35
	v_exp_f32_e32 v34, v34
	s_nop 0
	v_add_f32_e32 v34, 1.0, v34
	v_div_scale_f32 v35, s[2:3], v34, v34, v96
	v_rcp_f32_e32 v130, v35
	v_mov_b32_e32 v110, v129
	v_fma_f32 v131, -v35, v130, 1.0
	v_fmac_f32_e32 v130, v131, v130
	v_div_scale_f32 v131, vcc, v96, v34, v96
	v_mul_f32_e32 v132, v131, v130
	v_fma_f32 v133, -v35, v132, v131
	v_fmac_f32_e32 v132, v133, v130
	v_fma_f32 v35, -v35, v132, v131
	v_div_fmas_f32 v35, v35, v130, v132
	v_div_fixup_f32 v34, v35, v34, v96
	v_add_f32_e32 v34, v67, v34
	v_cmp_gt_f32_e32 vcc, s37, v34
	v_mov_b32_dpp v32, v110 row_shr:1 row_mask:0xf bank_mask:0xf bound_ctrl:1
	s_nop 0
	v_cndmask_b32_e64 v35, 0, 32, vcc
	v_ldexp_f32 v34, v34, v35
	v_log_f32_e32 v34, v34
	s_nop 0
	v_mul_f32_e32 v35, 0x3f317217, v34
	v_fma_f32 v35, v34, s33, -v35
	v_fmac_f32_e32 v35, 0x3377d1cf, v34
	v_fmac_f32_e32 v35, 0x3f317217, v34
	v_cmp_lt_f32_e64 s[48:49], |v34|, s36
	s_nop 1
	v_cndmask_b32_e64 v34, v34, v35, s[48:49]
	v_cndmask_b32_e32 v35, 0, v216, vcc
	v_sub_f32_e32 v132, v34, v35
	v_mov_b32_e32 v35, v116
	v_mov_b32_e32 v111, v132
	v_mov_b32_e32 v34, v115
	v_mov_b32_dpp v77, v35 row_shr:1 row_mask:0xf bank_mask:0xf bound_ctrl:1
	v_mov_b32_e32 v46, v119
	v_mov_b32_dpp v76, v34 row_shr:1 row_mask:0xf bank_mask:0xf bound_ctrl:1
	v_pk_add_f32 v[76:77], v[34:35], v[76:77]
	v_mov_b32_e32 v42, v123
	v_mov_b32_e32 v38, v127
	v_mov_b32_dpp v78, v76 row_shr:2 row_mask:0xf bank_mask:0xf bound_ctrl:1
	v_mov_b32_dpp v79, v77 row_shr:2 row_mask:0xf bank_mask:0xf bound_ctrl:1
	v_pk_add_f32 v[76:77], v[76:77], v[78:79]
	v_mov_b32_dpp v104, v42 row_shr:1 row_mask:0xf bank_mask:0xf bound_ctrl:1
	v_pk_add_f32 v[104:105], v[42:43], v[104:105]
	v_mov_b32_dpp v78, v76 row_shr:4 row_mask:0xf bank_mask:0xf bound_ctrl:1
	v_mov_b32_dpp v79, v77 row_shr:4 row_mask:0xf bank_mask:0xf bound_ctrl:1
	v_pk_add_f32 v[76:77], v[76:77], v[78:79]
	v_mov_b32_dpp v108, v38 row_shr:1 row_mask:0xf bank_mask:0xf bound_ctrl:1
	v_pk_add_f32 v[108:109], v[38:39], v[108:109]
	v_mov_b32_dpp v78, v76 row_shr:8 row_mask:0xf bank_mask:0xf bound_ctrl:1
	v_mov_b32_dpp v79, v77 row_shr:8 row_mask:0xf bank_mask:0xf bound_ctrl:1
	v_pk_add_f32 v[76:77], v[76:77], v[78:79]
	ds_swizzle_b32 v78, v76 offset:swizzle(BROADCAST,16,15)
	ds_swizzle_b32 v79, v77 offset:swizzle(BROADCAST,16,15)
	v_mov_b32_dpp v33, v111 row_shr:1 row_mask:0xf bank_mask:0xf bound_ctrl:1
	v_pk_add_f32 v[32:33], v[110:111], v[32:33]
	v_pk_add_f32 v[76:77], v[76:77], 0 op_sel_hi:[1,0]
	s_waitcnt lgkmcnt(0)
; template <int CTRL> __device__ __forceinline__ float dppx(float v) { return __int_as_float(__builtin_amdgcn_update_dpp(0, __float_as_int(v), CTRL, 0xf, 0xf, true)); }
;   __device__ __forceinline__ void operator()(const f32x4 (&acc)[2][2][4][2], const pg8::Unit& u, int wr, int wc, int fr, int fq) const {
;     ...
;               for (int q = 0; q < 4; ++q) { const float gv = log_forget(acc[ai][bj][m][qh][q], lq[q]); g[m][q] = gv;
;                 float sc = gv; sc += dppx<0x111>(sc); sc += dppx<0x112>(sc); sc += dppx<0x114>(sc); sc += dppx<0x118>(sc);
;                 const float tot16 = __int_as_float(__builtin_amdgcn_ds_swizzle(__float_as_int(sc), 0x1F0));
;                 cs[m][q] = sc + carry[q]; carry[q] += tot16; }
; #pragma unroll
;             for (int m = 0; m < 4; ++m) { const int r = row0 + ai * 128 + m * 16; float bq[4], kq[4];
; #pragma unroll
;               for (int q = 0; q < 4; ++q) { bq[q] = bwd ? (carry[q] - cs[m][q]) + g[m][q] : cs[m][q]; kq[q] = 1.f - __expf(g[m][q]); }
	v_pk_add_f32 v[130:131], v[78:79], 0 op_sel_hi:[1,0]
	v_mul_f32_e32 v78, 0x3fb8aa3b, v34
	v_exp_f32_e32 v78, v78
	v_mov_b32_dpp v79, v45 row_shr:1 row_mask:0xf bank_mask:0xf bound_ctrl:1
	v_sub_f32_e32 v115, 1.0, v78
	v_mul_f32_e32 v78, 0x3fb8aa3b, v35
	v_exp_f32_e32 v78, v78
	s_nop 0
	v_sub_f32_e32 v133, 1.0, v78
	v_mov_b32_dpp v78, v44 row_shr:1 row_mask:0xf bank_mask:0xf bound_ctrl:1
	v_pk_add_f32 v[78:79], v[44:45], v[78:79]
	s_nop 1
	v_mov_b32_dpp v80, v78 row_shr:2 row_mask:0xf bank_mask:0xf bound_ctrl:1
	v_mov_b32_dpp v81, v79 row_shr:2 row_mask:0xf bank_mask:0xf bound_ctrl:1
	v_pk_add_f32 v[78:79], v[78:79], v[80:81]
	s_nop 1
	v_mov_b32_dpp v80, v78 row_shr:4 row_mask:0xf bank_mask:0xf bound_ctrl:1
	v_mov_b32_dpp v81, v79 row_shr:4 row_mask:0xf bank_mask:0xf bound_ctrl:1
	v_pk_add_f32 v[78:79], v[78:79], v[80:81]
	s_nop 1
	v_mov_b32_dpp v80, v78 row_shr:8 row_mask:0xf bank_mask:0xf bound_ctrl:1
	v_mov_b32_dpp v81, v79 row_shr:8 row_mask:0xf bank_mask:0xf bound_ctrl:1
	v_pk_add_f32 v[78:79], v[78:79], v[80:81]
	ds_swizzle_b32 v80, v78 offset:swizzle(BROADCAST,16,15)
	ds_swizzle_b32 v81, v79 offset:swizzle(BROADCAST,16,15)
	v_pk_add_f32 v[78:79], v[78:79], 0 op_sel_hi:[1,0]
	s_waitcnt lgkmcnt(0)
	v_pk_add_f32 v[116:117], v[80:81], 0 op_sel_hi:[1,0]
	v_mul_f32_e32 v80, 0x3fb8aa3b, v44
	v_exp_f32_e32 v80, v80
	v_mov_b32_dpp v81, v47 row_shr:1 row_mask:0xf bank_mask:0xf bound_ctrl:1
	v_sub_f32_e32 v134, 1.0, v80
	v_mul_f32_e32 v80, 0x3fb8aa3b, v45
	v_exp_f32_e32 v80, v80
	s_nop 0
	v_sub_f32_e32 v135, 1.0, v80
	v_mov_b32_dpp v80, v46 row_shr:1 row_mask:0xf bank_mask:0xf bound_ctrl:1
	v_pk_add_f32 v[80:81], v[46:47], v[80:81]
	s_nop 1
	v_mov_b32_dpp v82, v80 row_shr:2 row_mask:0xf bank_mask:0xf bound_ctrl:1
	v_mov_b32_dpp v83, v81 row_shr:2 row_mask:0xf bank_mask:0xf bound_ctrl:1
	v_pk_add_f32 v[80:81], v[80:81], v[82:83]
	s_nop 1
	v_mov_b32_dpp v82, v80 row_shr:4 row_mask:0xf bank_mask:0xf bound_ctrl:1
	v_mov_b32_dpp v83, v81 row_shr:4 row_mask:0xf bank_mask:0xf bound_ctrl:1
	v_pk_add_f32 v[80:81], v[80:81], v[82:83]
	s_nop 1
	v_mov_b32_dpp v82, v80 row_shr:8 row_mask:0xf bank_mask:0xf bound_ctrl:1
	v_mov_b32_dpp v83, v81 row_shr:8 row_mask:0xf bank_mask:0xf bound_ctrl:1
	v_pk_add_f32 v[80:81], v[80:81], v[82:83]
	ds_swizzle_b32 v82, v80 offset:swizzle(BROADCAST,16,15)
	ds_swizzle_b32 v83, v81 offset:swizzle(BROADCAST,16,15)
	v_pk_add_f32 v[80:81], v[130:131], v[80:81]
	s_waitcnt lgkmcnt(0)
	v_pk_add_f32 v[118:119], v[130:131], v[82:83]
	v_mul_f32_e32 v82, 0x3fb8aa3b, v46
	v_exp_f32_e32 v82, v82
	v_mov_b32_dpp v83, v41 row_shr:1 row_mask:0xf bank_mask:0xf bound_ctrl:1
	v_sub_f32_e32 v130, 1.0, v82
	v_mul_f32_e32 v82, 0x3fb8aa3b, v47
	v_exp_f32_e32 v82, v82
	s_nop 0
	v_sub_f32_e32 v131, 1.0, v82
	v_mov_b32_dpp v82, v40 row_shr:1 row_mask:0xf bank_mask:0xf bound_ctrl:1
	v_pk_add_f32 v[82:83], v[40:41], v[82:83]
	s_nop 1
	v_mov_b32_dpp v102, v82 row_shr:2 row_mask:0xf bank_mask:0xf bound_ctrl:1
	v_mov_b32_dpp v103, v83 row_shr:2 row_mask:0xf bank_mask:0xf bound_ctrl:1
	v_pk_add_f32 v[82:83], v[82:83], v[102:103]
	s_nop 1
	v_mov_b32_dpp v102, v82 row_shr:4 row_mask:0xf bank_mask:0xf bound_ctrl:1
	v_mov_b32_dpp v103, v83 row_shr:4 row_mask:0xf bank_mask:0xf bound_ctrl:1
	v_pk_add_f32 v[82:83], v[82:83], v[102:103]
	s_nop 1
	v_mov_b32_dpp v102, v82 row_shr:8 row_mask:0xf bank_mask:0xf bound_ctrl:1
	v_mov_b32_dpp v103, v83 row_shr:8 row_mask:0xf bank_mask:0xf bound_ctrl:1
	v_pk_add_f32 v[82:83], v[82:83], v[102:103]
	ds_swizzle_b32 v102, v82 offset:swizzle(BROADCAST,16,15)
	ds_swizzle_b32 v103, v83 offset:swizzle(BROADCAST,16,15)
	v_pk_add_f32 v[82:83], v[116:117], v[82:83]
	s_waitcnt lgkmcnt(0)
	v_pk_add_f32 v[102:103], v[116:117], v[102:103]
	v_mul_f32_e32 v116, 0x3fb8aa3b, v40
	v_exp_f32_e32 v116, v116
	v_mov_b32_dpp v117, v105 row_shr:2 row_mask:0xf bank_mask:0xf bound_ctrl:1
	v_sub_f32_e32 v122, 1.0, v116
	v_mul_f32_e32 v116, 0x3fb8aa3b, v41
	v_exp_f32_e32 v116, v116
	s_nop 0
	v_sub_f32_e32 v136, 1.0, v116
	v_mov_b32_dpp v116, v104 row_shr:2 row_mask:0xf bank_mask:0xf bound_ctrl:1
	v_pk_add_f32 v[104:105], v[104:105], v[116:117]
	s_nop 1
	v_mov_b32_dpp v116, v104 row_shr:4 row_mask:0xf bank_mask:0xf bound_ctrl:1
	v_mov_b32_dpp v117, v105 row_shr:4 row_mask:0xf bank_mask:0xf bound_ctrl:1
	v_pk_add_f32 v[104:105], v[104:105], v[116:117]
	s_nop 1
	v_mov_b32_dpp v116, v104 row_shr:8 row_mask:0xf bank_mask:0xf bound_ctrl:1
	v_mov_b32_dpp v117, v105 row_shr:8 row_mask:0xf bank_mask:0xf bound_ctrl:1
	v_pk_add_f32 v[104:105], v[104:105], v[116:117]
	ds_swizzle_b32 v116, v104 offset:swizzle(BROADCAST,16,15)
	ds_swizzle_b32 v117, v105 offset:swizzle(BROADCAST,16,15)
	v_pk_add_f32 v[104:105], v[118:119], v[104:105]
	s_waitcnt lgkmcnt(0)
	v_pk_add_f32 v[116:117], v[118:119], v[116:117]
	v_mul_f32_e32 v118, 0x3fb8aa3b, v42
	v_exp_f32_e32 v118, v118
	v_mov_b32_dpp v119, v107 row_shr:2 row_mask:0xf bank_mask:0xf bound_ctrl:1
	v_sub_f32_e32 v123, 1.0, v118
	v_mul_f32_e32 v118, 0x3fb8aa3b, v43
	v_exp_f32_e32 v118, v118
	s_nop 0
	v_sub_f32_e32 v124, 1.0, v118
	v_mov_b32_dpp v118, v106 row_shr:2 row_mask:0xf bank_mask:0xf bound_ctrl:1
	v_pk_add_f32 v[106:107], v[106:107], v[118:119]
	s_nop 1
	v_mov_b32_dpp v118, v106 row_shr:4 row_mask:0xf bank_mask:0xf bound_ctrl:1
	v_mov_b32_dpp v119, v107 row_shr:4 row_mask:0xf bank_mask:0xf bound_ctrl:1
	v_pk_add_f32 v[106:107], v[106:107], v[118:119]
	s_nop 1
	v_mov_b32_dpp v118, v106 row_shr:8 row_mask:0xf bank_mask:0xf bound_ctrl:1
	v_mov_b32_dpp v119, v107 row_shr:8 row_mask:0xf bank_mask:0xf bound_ctrl:1
	v_pk_add_f32 v[106:107], v[106:107], v[118:119]
	ds_swizzle_b32 v118, v106 offset:swizzle(BROADCAST,16,15)
	ds_swizzle_b32 v119, v107 offset:swizzle(BROADCAST,16,15)
	v_pk_add_f32 v[106:107], v[102:103], v[106:107]
	s_waitcnt lgkmcnt(0)
; template <int CTRL> __device__ __forceinline__ float dppx(float v) { return __int_as_float(__builtin_amdgcn_update_dpp(0, __float_as_int(v), CTRL, 0xf, 0xf, true)); }
; __device__ __forceinline__ unsigned cvt_pk_bf16(float lo, float hi) { unsigned r; asm volatile("v_cvt_pk_bf16_f32 %0, %1, %2" : "=v"(r) : "v"(lo), "v"(hi)); return r; }
; __device__ __forceinline__ float log_forget(float z, float lb) {
;   const float r0 = fminf(z, 0.f) - __logf(1.f + __expf(-fabsf(z)));
;   const float r1 = __logf(lb + (1.f - lb) / (1.f + __expf(-z)));
;   return lb <= 0.f ? r0 : r1;
; }
;   __device__ __forceinline__ void operator()(const f32x4 (&acc)[2][2][4][2], const pg8::Unit& u, int wr, int wc, int fr, int fq) const {
;     ...
;               for (int q = 0; q < 4; ++q) { const float gv = log_forget(acc[ai][bj][m][qh][q], lq[q]); g[m][q] = gv;
;                 float sc = gv; sc += dppx<0x111>(sc); sc += dppx<0x112>(sc); sc += dppx<0x114>(sc); sc += dppx<0x118>(sc);
;                 const float tot16 = __int_as_float(__builtin_amdgcn_ds_swizzle(__float_as_int(sc), 0x1F0));
;                 cs[m][q] = sc + carry[q]; carry[q] += tot16; }
; #pragma unroll
;             for (int m = 0; m < 4; ++m) { const int r = row0 + ai * 128 + m * 16; float bq[4], kq[4];
; #pragma unroll
;               for (int q = 0; q < 4; ++q) { bq[q] = bwd ? (carry[q] - cs[m][q]) + g[m][q] : cs[m][q]; kq[q] = 1.f - __expf(g[m][q]); }
;               *(f32x4*)(logfp + (size_t)r * 1024 + c + 4 * qh) = (f32x4){bq[0], bq[1], bq[2], bq[3]};
;               u32x2 w; w.x = pg8::cvt_pk_bf16(kq[0], kq[1]); w.y = pg8::cvt_pk_bf16(kq[2], kq[3]);
;               *(u32x2*)(km + (size_t)r * 1024 + c + 4 * qh) = w; } } }
	v_pk_add_f32 v[102:103], v[102:103], v[118:119]
	v_mul_f32_e32 v118, 0x3fb8aa3b, v36
	v_exp_f32_e32 v118, v118
	v_mov_b32_dpp v119, v109 row_shr:2 row_mask:0xf bank_mask:0xf bound_ctrl:1
	v_sub_f32_e32 v125, 1.0, v118
	v_mul_f32_e32 v118, 0x3fb8aa3b, v37
	v_exp_f32_e32 v118, v118
	s_nop 0
	v_sub_f32_e32 v126, 1.0, v118
	v_mov_b32_dpp v118, v108 row_shr:2 row_mask:0xf bank_mask:0xf bound_ctrl:1
	v_pk_add_f32 v[108:109], v[108:109], v[118:119]
	s_nop 1
	v_mov_b32_dpp v118, v108 row_shr:4 row_mask:0xf bank_mask:0xf bound_ctrl:1
	v_mov_b32_dpp v119, v109 row_shr:4 row_mask:0xf bank_mask:0xf bound_ctrl:1
	v_pk_add_f32 v[108:109], v[108:109], v[118:119]
	s_nop 1
	v_mov_b32_dpp v118, v108 row_shr:8 row_mask:0xf bank_mask:0xf bound_ctrl:1
	v_mov_b32_dpp v119, v109 row_shr:8 row_mask:0xf bank_mask:0xf bound_ctrl:1
	v_pk_add_f32 v[108:109], v[108:109], v[118:119]
	ds_swizzle_b32 v118, v108 offset:swizzle(BROADCAST,16,15)
	ds_swizzle_b32 v119, v109 offset:swizzle(BROADCAST,16,15)
	v_pk_add_f32 v[108:109], v[116:117], v[108:109]
	s_waitcnt lgkmcnt(0)
	v_pk_add_f32 v[116:117], v[116:117], v[118:119]
	v_mul_f32_e32 v118, 0x3fb8aa3b, v38
	v_exp_f32_e32 v118, v118
	v_mov_b32_dpp v119, v33 row_shr:2 row_mask:0xf bank_mask:0xf bound_ctrl:1
	v_sub_f32_e32 v127, 1.0, v118
	v_mul_f32_e32 v118, 0x3fb8aa3b, v39
	v_exp_f32_e32 v118, v118
	s_nop 0
	v_sub_f32_e32 v128, 1.0, v118
	v_mov_b32_dpp v118, v32 row_shr:2 row_mask:0xf bank_mask:0xf bound_ctrl:1
	v_pk_add_f32 v[32:33], v[32:33], v[118:119]
	s_nop 1
	v_mov_b32_dpp v118, v32 row_shr:4 row_mask:0xf bank_mask:0xf bound_ctrl:1
	v_mov_b32_dpp v119, v33 row_shr:4 row_mask:0xf bank_mask:0xf bound_ctrl:1
	v_pk_add_f32 v[32:33], v[32:33], v[118:119]
	s_nop 1
	v_mov_b32_dpp v118, v32 row_shr:8 row_mask:0xf bank_mask:0xf bound_ctrl:1
	v_mov_b32_dpp v119, v33 row_shr:8 row_mask:0xf bank_mask:0xf bound_ctrl:1
	v_pk_add_f32 v[32:33], v[32:33], v[118:119]
	ds_swizzle_b32 v118, v32 offset:swizzle(BROADCAST,16,15)
	ds_swizzle_b32 v119, v33 offset:swizzle(BROADCAST,16,15)
	v_pk_add_f32 v[120:121], v[102:103], v[32:33]
	v_pk_add_f32 v[32:33], v[116:117], v[76:77] neg_lo:[0,1] neg_hi:[0,1]
	s_waitcnt lgkmcnt(0)
	v_pk_add_f32 v[102:103], v[102:103], v[118:119]
	s_nop 0
	v_pk_add_f32 v[118:119], v[102:103], v[78:79] neg_lo:[0,1] neg_hi:[0,1]
	v_pk_add_f32 v[32:33], v[34:35], v[32:33]
	v_pk_add_f32 v[34:35], v[44:45], v[118:119]
	v_cndmask_b32_e64 v33, v77, v33, s[42:43]
	v_cndmask_b32_e64 v35, v79, v35, s[42:43]
	v_cndmask_b32_e64 v34, v78, v34, s[42:43]
	v_cndmask_b32_e64 v32, v76, v32, s[42:43]
	global_store_dwordx4 v[54:55], v[32:35], off offset:16
	s_nop 1
	v_cvt_pk_bf16_f32 v32, v115, v133
	v_cvt_pk_bf16_f32 v33, v134, v135
	global_store_dwordx2 v[52:53], v[32:33], off offset:8
	v_pk_add_f32 v[32:33], v[116:117], v[80:81] neg_lo:[0,1] neg_hi:[0,1]
	v_pk_add_f32 v[34:35], v[102:103], v[82:83] neg_lo:[0,1] neg_hi:[0,1]
	v_pk_add_f32 v[32:33], v[46:47], v[32:33]
	v_pk_add_f32 v[34:35], v[40:41], v[34:35]
	v_cndmask_b32_e64 v33, v81, v33, s[42:43]
	v_cndmask_b32_e64 v35, v83, v35, s[42:43]
	v_cndmask_b32_e64 v34, v82, v34, s[42:43]
	v_cndmask_b32_e64 v32, v80, v32, s[42:43]
	global_store_dwordx4 v[58:59], v[32:35], off offset:16
	s_nop 1
	v_cvt_pk_bf16_f32 v32, v130, v131
	v_cvt_pk_bf16_f32 v33, v122, v136
	global_store_dwordx2 v[56:57], v[32:33], off offset:8
	v_pk_add_f32 v[32:33], v[116:117], v[104:105] neg_lo:[0,1] neg_hi:[0,1]
	v_pk_add_f32 v[34:35], v[102:103], v[106:107] neg_lo:[0,1] neg_hi:[0,1]
	v_pk_add_f32 v[32:33], v[42:43], v[32:33]
	v_pk_add_f32 v[34:35], v[36:37], v[34:35]
	v_cndmask_b32_e64 v33, v105, v33, s[42:43]
	v_cndmask_b32_e64 v35, v107, v35, s[42:43]
	v_cndmask_b32_e64 v34, v106, v34, s[42:43]
	v_cndmask_b32_e64 v32, v104, v32, s[42:43]
	global_store_dwordx4 v[62:63], v[32:35], off offset:16
	v_mul_f32_e32 v37, 0x3fb8aa3b, v111
	v_exp_f32_e32 v37, v37
	v_cvt_pk_bf16_f32 v32, v123, v124
	v_cvt_pk_bf16_f32 v33, v125, v126
	global_store_dwordx2 v[60:61], v[32:33], off offset:8
	v_mul_f32_e32 v32, 0x3fb8aa3b, v110
	v_exp_f32_e32 v32, v32
	v_pk_add_f32 v[34:35], v[102:103], v[120:121] neg_lo:[0,1] neg_hi:[0,1]
	v_sub_f32_e32 v37, 1.0, v37
	v_pk_add_f32 v[34:35], v[110:111], v[34:35]
	v_sub_f32_e32 v36, 1.0, v32
	v_pk_add_f32 v[32:33], v[116:117], v[108:109] neg_lo:[0,1] neg_hi:[0,1]
	v_cndmask_b32_e64 v35, v121, v35, s[42:43]
	v_pk_add_f32 v[32:33], v[38:39], v[32:33]
	v_cndmask_b32_e64 v34, v120, v34, s[42:43]
	v_cndmask_b32_e64 v33, v109, v33, s[42:43]
	v_cndmask_b32_e64 v32, v108, v32, s[42:43]
	global_store_dwordx4 v[72:73], v[32:35], off offset:16
	s_nop 1
	v_cvt_pk_bf16_f32 v32, v127, v128
	v_cvt_pk_bf16_f32 v33, v36, v37
	global_store_dwordx2 v[74:75], v[32:33], off offset:8
	v_mul_f32_e32 v28, 0xbfb8aa3b, v28
	v_exp_f32_e32 v28, v28
	s_nop 0
	v_add_f32_e32 v28, 1.0, v28
	s_nop 0
	s_nop 1
	v_div_scale_f32 v33, s[2:3], v28, v28, v157
	v_rcp_f32_e32 v35, v33
	s_nop 0
	v_fma_f32 v36, -v33, v35, 1.0
	v_fmac_f32_e32 v35, v36, v35
	v_div_scale_f32 v36, vcc, v157, v28, v157
	v_mul_f32_e32 v37, v36, v35
	v_fma_f32 v38, -v33, v37, v36
	v_fmac_f32_e32 v37, v38, v35
	v_fma_f32 v33, -v33, v37, v36
	v_div_fmas_f32 v33, v33, v35, v37
	v_div_fixup_f32 v28, v33, v28, v157
	v_add_f32_e32 v28, v68, v28
	v_cmp_gt_f32_e32 vcc, s37, v28
	s_nop 1
	v_cndmask_b32_e64 v33, 0, 32, vcc
	v_ldexp_f32 v28, v28, v33
	v_log_f32_e32 v28, v28
	s_nop 0
	v_mul_f32_e32 v33, 0x3f317217, v28
	v_fma_f32 v33, v28, s33, -v33
	v_fmac_f32_e32 v33, 0x3377d1cf, v28
	v_fmac_f32_e32 v33, 0x3f317217, v28
	v_cmp_lt_f32_e64 s[60:61], |v28|, s36
	s_nop 1
	v_cndmask_b32_e64 v28, v28, v33, s[60:61]
	v_cndmask_b32_e32 v33, 0, v216, vcc
	v_sub_f32_e32 v60, v28, v33
; __device__ __forceinline__ float log_forget(float z, float lb) {
;   const float r0 = fminf(z, 0.f) - __logf(1.f + __expf(-fabsf(z)));
;   const float r1 = __logf(lb + (1.f - lb) / (1.f + __expf(-z)));
;   return lb <= 0.f ? r0 : r1;
; }
;   __device__ __forceinline__ void operator()(const f32x4 (&acc)[2][2][4][2], const pg8::Unit& u, int wr, int wc, int fr, int fq) const {
;     ...
;           for (int qh = 0; qh < 2; ++qh) { float g[4][4], cs[4][4], carry[4];
;             const f32x4 lq = qh == 0 ? l0 : l1;
; #pragma unroll
;             for (int q = 0; q < 4; ++q) carry[q] = 0.f;
; #pragma unroll
;             for (int m = 0; m < 4; ++m)
; #pragma unroll
;               for (int q = 0; q < 4; ++q) { const float gv = log_forget(acc[ai][bj][m][qh][q], lq[q]); g[m][q] = gv;
	s_nop 0
	s_nop 1
	s_nop 0
	s_nop 1
	v_mul_f32_e32 v28, 0xbfb8aa3b, v29
	v_exp_f32_e32 v28, v28
	s_nop 0
	v_add_f32_e32 v28, 1.0, v28
	v_div_scale_f32 v29, s[2:3], v28, v28, v156
	v_rcp_f32_e32 v36, v29
	s_nop 0
	v_fma_f32 v37, -v29, v36, 1.0
	v_fmac_f32_e32 v36, v37, v36
	v_div_scale_f32 v37, vcc, v156, v28, v156
	v_mul_f32_e32 v38, v37, v36
	v_fma_f32 v39, -v29, v38, v37
	v_fmac_f32_e32 v38, v39, v36
	v_fma_f32 v29, -v29, v38, v37
	v_div_fmas_f32 v29, v29, v36, v38
	v_div_fixup_f32 v28, v29, v28, v156
	v_add_f32_e32 v28, v69, v28
	v_cmp_gt_f32_e32 vcc, s37, v28
	s_nop 1
	v_cndmask_b32_e64 v29, 0, 32, vcc
	v_ldexp_f32 v28, v28, v29
	v_log_f32_e32 v28, v28
	s_nop 0
	v_mul_f32_e32 v29, 0x3f317217, v28
	v_fma_f32 v29, v28, s33, -v29
	v_fmac_f32_e32 v29, 0x3377d1cf, v28
	v_fmac_f32_e32 v29, 0x3f317217, v28
	v_cmp_lt_f32_e64 s[60:61], |v28|, s36
	s_nop 1
	v_cndmask_b32_e64 v28, v28, v29, s[60:61]
	v_cndmask_b32_e32 v29, 0, v216, vcc
	v_sub_f32_e32 v61, v28, v29
	s_nop 1
	s_nop 0
	s_nop 1
	v_mul_f32_e32 v29, 0xbfb8aa3b, v30
	v_exp_f32_e32 v29, v29
	s_nop 0
	v_add_f32_e32 v29, 1.0, v29
	v_div_scale_f32 v30, s[2:3], v29, v29, v155
	v_rcp_f32_e32 v37, v30
	s_nop 0
	v_fma_f32 v38, -v30, v37, 1.0
	v_fmac_f32_e32 v37, v38, v37
	v_div_scale_f32 v38, vcc, v155, v29, v155
	v_mul_f32_e32 v39, v38, v37
	v_fma_f32 v40, -v30, v39, v38
	v_fmac_f32_e32 v39, v40, v37
	v_fma_f32 v30, -v30, v39, v38
	v_div_fmas_f32 v30, v30, v37, v39
	v_div_fixup_f32 v29, v30, v29, v155
	v_add_f32_e32 v29, v70, v29
	v_cmp_gt_f32_e32 vcc, s37, v29
	s_nop 1
	v_cndmask_b32_e64 v30, 0, 32, vcc
	v_ldexp_f32 v29, v29, v30
	v_log_f32_e32 v29, v29
	s_nop 0
	v_mul_f32_e32 v30, 0x3f317217, v29
	v_fma_f32 v30, v29, s33, -v30
	v_fmac_f32_e32 v30, 0x3377d1cf, v29
	v_fmac_f32_e32 v30, 0x3f317217, v29
	v_cmp_lt_f32_e64 s[60:61], |v29|, s36
	s_nop 1
	v_cndmask_b32_e64 v29, v29, v30, s[60:61]
	v_cndmask_b32_e32 v30, 0, v216, vcc
	v_sub_f32_e32 v62, v29, v30
	s_nop 1
	s_nop 0
	s_nop 1
	v_mul_f32_e32 v30, 0xbfb8aa3b, v31
	v_exp_f32_e32 v30, v30
	s_nop 0
	v_add_f32_e32 v30, 1.0, v30
	v_div_scale_f32 v31, s[2:3], v30, v30, v154
	v_rcp_f32_e32 v38, v31
	s_nop 0
	v_fma_f32 v39, -v31, v38, 1.0
	v_fmac_f32_e32 v38, v39, v38
	v_div_scale_f32 v39, vcc, v154, v30, v154
	v_mul_f32_e32 v40, v39, v38
	v_fma_f32 v41, -v31, v40, v39
	v_fmac_f32_e32 v40, v41, v38
	v_fma_f32 v31, -v31, v40, v39
	v_div_fmas_f32 v31, v31, v38, v40
	v_div_fixup_f32 v30, v31, v30, v154
	v_add_f32_e32 v30, v71, v30
	v_cmp_gt_f32_e32 vcc, s37, v30
	s_nop 1
	v_cndmask_b32_e64 v31, 0, 32, vcc
	v_ldexp_f32 v30, v30, v31
	v_log_f32_e32 v30, v30
	s_nop 0
	v_mul_f32_e32 v31, 0x3f317217, v30
	v_fma_f32 v31, v30, s33, -v31
	v_fmac_f32_e32 v31, 0x3377d1cf, v30
	v_fmac_f32_e32 v31, 0x3f317217, v30
	v_cmp_lt_f32_e64 s[60:61], |v30|, s36
	s_nop 1
	v_cndmask_b32_e64 v30, v30, v31, s[60:61]
	v_cndmask_b32_e32 v31, 0, v216, vcc
	v_sub_f32_e32 v63, v30, v31
	v_mul_f32_e32 v24, 0xbfb8aa3b, v24
	v_exp_f32_e32 v24, v24
	s_nop 0
	v_add_f32_e32 v24, 1.0, v24
	s_nop 0
	s_nop 1
	v_div_scale_f32 v31, s[2:3], v24, v24, v157
	v_rcp_f32_e32 v39, v31
	s_nop 0
	v_fma_f32 v40, -v31, v39, 1.0
	v_fmac_f32_e32 v39, v40, v39
	v_div_scale_f32 v40, vcc, v157, v24, v157
	v_mul_f32_e32 v41, v40, v39
	v_fma_f32 v42, -v31, v41, v40
	v_fmac_f32_e32 v41, v42, v39
	v_fma_f32 v31, -v31, v41, v40
	v_div_fmas_f32 v31, v31, v39, v41
	v_div_fixup_f32 v24, v31, v24, v157
	v_add_f32_e32 v24, v68, v24
	v_cmp_gt_f32_e32 vcc, s37, v24
	s_nop 1
	v_cndmask_b32_e64 v31, 0, 32, vcc
	v_ldexp_f32 v24, v24, v31
	v_log_f32_e32 v24, v24
	s_nop 0
	v_mul_f32_e32 v31, 0x3f317217, v24
	v_fma_f32 v31, v24, s33, -v31
	v_fmac_f32_e32 v31, 0x3377d1cf, v24
	v_fmac_f32_e32 v31, 0x3f317217, v24
	v_cmp_lt_f32_e64 s[60:61], |v24|, s36
	s_nop 1
	v_cndmask_b32_e64 v24, v24, v31, s[60:61]
	v_cndmask_b32_e32 v31, 0, v216, vcc
	v_sub_f32_e32 v72, v24, v31
	s_nop 0
	s_nop 1
	s_nop 0
	s_nop 1
	v_mul_f32_e32 v24, 0xbfb8aa3b, v25
	v_exp_f32_e32 v24, v24
	s_nop 0
	v_add_f32_e32 v24, 1.0, v24
	v_div_scale_f32 v25, s[2:3], v24, v24, v156
	v_rcp_f32_e32 v40, v25
	v_mov_b32_e32 v30, v72
	v_fma_f32 v41, -v25, v40, 1.0
	v_fmac_f32_e32 v40, v41, v40
	v_div_scale_f32 v41, vcc, v156, v24, v156
	v_mul_f32_e32 v42, v41, v40
	v_fma_f32 v43, -v25, v42, v41
	v_fmac_f32_e32 v42, v43, v40
	v_fma_f32 v25, -v25, v42, v41
	v_div_fmas_f32 v25, v25, v40, v42
	v_div_fixup_f32 v24, v25, v24, v156
	v_add_f32_e32 v24, v69, v24
	v_cmp_gt_f32_e32 vcc, s37, v24
	v_mov_b32_dpp v38, v30 row_shr:1 row_mask:0xf bank_mask:0xf bound_ctrl:1
	s_nop 0
	v_cndmask_b32_e64 v25, 0, 32, vcc
	v_ldexp_f32 v24, v24, v25
	v_log_f32_e32 v24, v24
	s_nop 0
	v_mul_f32_e32 v25, 0x3f317217, v24
	v_fma_f32 v25, v24, s33, -v25
	v_fmac_f32_e32 v25, 0x3377d1cf, v24
	v_fmac_f32_e32 v25, 0x3f317217, v24
	v_cmp_lt_f32_e64 s[60:61], |v24|, s36
	s_nop 1
	v_cndmask_b32_e64 v24, v24, v25, s[60:61]
	v_cndmask_b32_e32 v25, 0, v216, vcc
	v_sub_f32_e32 v73, v24, v25
	v_mov_b32_e32 v31, v73
	s_nop 1
	v_mov_b32_dpp v39, v31 row_shr:1 row_mask:0xf bank_mask:0xf bound_ctrl:1
	v_pk_add_f32 v[38:39], v[30:31], v[38:39]
	s_nop 0
	s_nop 1
	v_mul_f32_e32 v25, 0xbfb8aa3b, v26
	v_exp_f32_e32 v25, v25
	s_nop 0
	v_add_f32_e32 v25, 1.0, v25
	v_div_scale_f32 v26, s[2:3], v25, v25, v155
	v_rcp_f32_e32 v41, v26
	s_nop 0
	v_fma_f32 v42, -v26, v41, 1.0
	v_fmac_f32_e32 v41, v42, v41
	v_div_scale_f32 v42, vcc, v155, v25, v155
	v_mul_f32_e32 v43, v42, v41
	v_fma_f32 v44, -v26, v43, v42
	v_fmac_f32_e32 v43, v44, v41
	v_fma_f32 v26, -v26, v43, v42
	v_div_fmas_f32 v26, v26, v41, v43
	v_div_fixup_f32 v25, v26, v25, v155
	v_add_f32_e32 v25, v70, v25
	v_cmp_gt_f32_e32 vcc, s37, v25
	s_nop 1
; template <int CTRL> __device__ __forceinline__ float dppx(float v) { return __int_as_float(__builtin_amdgcn_update_dpp(0, __float_as_int(v), CTRL, 0xf, 0xf, true)); }
; __device__ __forceinline__ float log_forget(float z, float lb) {
;   const float r0 = fminf(z, 0.f) - __logf(1.f + __expf(-fabsf(z)));
;   const float r1 = __logf(lb + (1.f - lb) / (1.f + __expf(-z)));
;   return lb <= 0.f ? r0 : r1;
; }
;   __device__ __forceinline__ void operator()(const f32x4 (&acc)[2][2][4][2], const pg8::Unit& u, int wr, int wc, int fr, int fq) const {
;     ...
;           for (int qh = 0; qh < 2; ++qh) { float g[4][4], cs[4][4], carry[4];
;             const f32x4 lq = qh == 0 ? l0 : l1;
; #pragma unroll
;             for (int q = 0; q < 4; ++q) carry[q] = 0.f;
; #pragma unroll
;             for (int m = 0; m < 4; ++m)
; #pragma unroll
;               for (int q = 0; q < 4; ++q) { const float gv = log_forget(acc[ai][bj][m][qh][q], lq[q]); g[m][q] = gv;
;                 float sc = gv; sc += dppx<0x111>(sc); sc += dppx<0x112>(sc); sc += dppx<0x114>(sc); sc += dppx<0x118>(sc);
;                 const float tot16 = __int_as_float(__builtin_amdgcn_ds_swizzle(__float_as_int(sc), 0x1F0));
	v_cndmask_b32_e64 v26, 0, 32, vcc
	v_ldexp_f32 v25, v25, v26
	v_log_f32_e32 v25, v25
	s_nop 0
	v_mul_f32_e32 v26, 0x3f317217, v25
	v_fma_f32 v26, v25, s33, -v26
	v_fmac_f32_e32 v26, 0x3377d1cf, v25
	v_fmac_f32_e32 v26, 0x3f317217, v25
	v_cmp_lt_f32_e64 s[60:61], |v25|, s36
	s_nop 1
	v_cndmask_b32_e64 v25, v25, v26, s[60:61]
	v_cndmask_b32_e32 v26, 0, v216, vcc
	v_sub_f32_e32 v74, v25, v26
	s_nop 1
	s_nop 0
	s_nop 1
	v_mul_f32_e32 v26, 0xbfb8aa3b, v27
	v_exp_f32_e32 v26, v26
	s_nop 0
	v_add_f32_e32 v26, 1.0, v26
	v_div_scale_f32 v27, s[2:3], v26, v26, v154
	v_rcp_f32_e32 v42, v27
	s_nop 0
	v_fma_f32 v43, -v27, v42, 1.0
	v_fmac_f32_e32 v42, v43, v42
	v_div_scale_f32 v43, vcc, v154, v26, v154
	v_mul_f32_e32 v44, v43, v42
	v_fma_f32 v45, -v27, v44, v43
	v_fmac_f32_e32 v44, v45, v42
	v_fma_f32 v27, -v27, v44, v43
	v_div_fmas_f32 v27, v27, v42, v44
	v_div_fixup_f32 v26, v27, v26, v154
	v_add_f32_e32 v26, v71, v26
	v_cmp_gt_f32_e32 vcc, s37, v26
	s_nop 1
	v_cndmask_b32_e64 v27, 0, 32, vcc
	v_ldexp_f32 v26, v26, v27
	v_log_f32_e32 v26, v26
	s_nop 0
	v_mul_f32_e32 v27, 0x3f317217, v26
	v_fma_f32 v27, v26, s33, -v27
	v_fmac_f32_e32 v27, 0x3377d1cf, v26
	v_fmac_f32_e32 v27, 0x3f317217, v26
	v_cmp_lt_f32_e64 s[60:61], |v26|, s36
	s_nop 1
	v_cndmask_b32_e64 v26, v26, v27, s[60:61]
	v_cndmask_b32_e32 v27, 0, v216, vcc
	v_sub_f32_e32 v75, v26, v27
	v_mul_f32_e32 v20, 0xbfb8aa3b, v20
	v_exp_f32_e32 v20, v20
	s_nop 0
	v_add_f32_e32 v20, 1.0, v20
	s_nop 0
	s_nop 1
	v_div_scale_f32 v27, s[2:3], v20, v20, v157
	v_rcp_f32_e32 v43, v27
	s_nop 0
	v_fma_f32 v44, -v27, v43, 1.0
	v_fmac_f32_e32 v43, v44, v43
	v_div_scale_f32 v44, vcc, v157, v20, v157
	v_mul_f32_e32 v45, v44, v43
	v_fma_f32 v46, -v27, v45, v44
	v_fmac_f32_e32 v45, v46, v43
	v_fma_f32 v27, -v27, v45, v44
	v_div_fmas_f32 v27, v27, v43, v45
	v_div_fixup_f32 v20, v27, v20, v157
	v_add_f32_e32 v20, v68, v20
	v_cmp_gt_f32_e32 vcc, s37, v20
	s_nop 1
	v_cndmask_b32_e64 v27, 0, 32, vcc
	v_ldexp_f32 v20, v20, v27
	v_log_f32_e32 v20, v20
	s_nop 0
	v_mul_f32_e32 v27, 0x3f317217, v20
	v_fma_f32 v27, v20, s33, -v27
	v_fmac_f32_e32 v27, 0x3377d1cf, v20
	v_fmac_f32_e32 v27, 0x3f317217, v20
	v_cmp_lt_f32_e64 s[60:61], |v20|, s36
	s_nop 1
	v_cndmask_b32_e64 v20, v20, v27, s[60:61]
	v_cndmask_b32_e32 v27, 0, v216, vcc
	v_sub_f32_e32 v76, v20, v27
	s_nop 0
	s_nop 1
	s_nop 0
	s_nop 1
	v_mul_f32_e32 v20, 0xbfb8aa3b, v21
	v_exp_f32_e32 v20, v20
	s_nop 0
	v_add_f32_e32 v20, 1.0, v20
	v_div_scale_f32 v21, s[2:3], v20, v20, v156
	v_rcp_f32_e32 v44, v21
	v_mov_b32_e32 v42, v76
	v_fma_f32 v45, -v21, v44, 1.0
	v_fmac_f32_e32 v44, v45, v44
	v_div_scale_f32 v45, vcc, v156, v20, v156
	v_mul_f32_e32 v46, v45, v44
	v_fma_f32 v47, -v21, v46, v45
	v_fmac_f32_e32 v46, v47, v44
	v_fma_f32 v21, -v21, v46, v45
	v_div_fmas_f32 v21, v21, v44, v46
	v_div_fixup_f32 v20, v21, v20, v156
	v_add_f32_e32 v20, v69, v20
	v_cmp_gt_f32_e32 vcc, s37, v20
	v_mov_b32_dpp v26, v42 row_shr:1 row_mask:0xf bank_mask:0xf bound_ctrl:1
	s_nop 0
	v_cndmask_b32_e64 v21, 0, 32, vcc
	v_ldexp_f32 v20, v20, v21
	v_log_f32_e32 v20, v20
	s_nop 0
	v_mul_f32_e32 v21, 0x3f317217, v20
	v_fma_f32 v21, v20, s33, -v21
	v_fmac_f32_e32 v21, 0x3377d1cf, v20
	v_fmac_f32_e32 v21, 0x3f317217, v20
	v_cmp_lt_f32_e64 s[60:61], |v20|, s36
	s_nop 1
	v_cndmask_b32_e64 v20, v20, v21, s[60:61]
	v_cndmask_b32_e32 v21, 0, v216, vcc
	v_sub_f32_e32 v77, v20, v21
	v_mov_b32_e32 v43, v77
	s_nop 1
	v_mov_b32_dpp v27, v43 row_shr:1 row_mask:0xf bank_mask:0xf bound_ctrl:1
	v_pk_add_f32 v[26:27], v[42:43], v[26:27]
	s_nop 1
	v_mov_b32_dpp v72, v26 row_shr:2 row_mask:0xf bank_mask:0xf bound_ctrl:1
	v_mov_b32_dpp v73, v27 row_shr:2 row_mask:0xf bank_mask:0xf bound_ctrl:1
	v_pk_add_f32 v[26:27], v[26:27], v[72:73]
	s_nop 1
	v_mov_b32_dpp v72, v26 row_shr:4 row_mask:0xf bank_mask:0xf bound_ctrl:1
	v_mov_b32_dpp v73, v27 row_shr:4 row_mask:0xf bank_mask:0xf bound_ctrl:1
	v_mul_f32_e32 v20, 0xbfb8aa3b, v22
	v_exp_f32_e32 v20, v20
	v_pk_add_f32 v[26:27], v[26:27], v[72:73]
	v_add_f32_e32 v20, 1.0, v20
	v_div_scale_f32 v21, s[2:3], v20, v20, v155
	v_rcp_f32_e32 v22, v21
	v_mov_b32_dpp v72, v26 row_shr:8 row_mask:0xf bank_mask:0xf bound_ctrl:1
	v_mov_b32_dpp v73, v27 row_shr:8 row_mask:0xf bank_mask:0xf bound_ctrl:1
	v_pk_add_f32 v[26:27], v[26:27], v[72:73]
	v_fma_f32 v45, -v21, v22, 1.0
	v_fmac_f32_e32 v22, v45, v22
	v_div_scale_f32 v45, vcc, v155, v20, v155
	v_mul_f32_e32 v47, v45, v22
	v_fma_f32 v52, -v21, v47, v45
	v_fmac_f32_e32 v47, v52, v22
	v_fma_f32 v21, -v21, v47, v45
	v_div_fmas_f32 v21, v21, v22, v47
	v_div_fixup_f32 v20, v21, v20, v155
	v_add_f32_e32 v20, v70, v20
	v_cmp_gt_f32_e32 vcc, s37, v20
	ds_swizzle_b32 v72, v26 offset:swizzle(BROADCAST,16,15)
	ds_swizzle_b32 v73, v27 offset:swizzle(BROADCAST,16,15)
	v_cndmask_b32_e64 v21, 0, 32, vcc
	v_ldexp_f32 v20, v20, v21
	v_log_f32_e32 v20, v20
	s_nop 0
	v_mul_f32_e32 v21, 0x3f317217, v20
	v_fma_f32 v21, v20, s33, -v21
	v_fmac_f32_e32 v21, 0x3377d1cf, v20
	v_fmac_f32_e32 v21, 0x3f317217, v20
	v_cmp_lt_f32_e64 s[60:61], |v20|, s36
	s_nop 1
	v_cndmask_b32_e64 v20, v20, v21, s[60:61]
	v_cndmask_b32_e32 v21, 0, v216, vcc
	v_sub_f32_e32 v78, v20, v21
	s_nop 0
	s_nop 1
	s_nop 0
	s_nop 1
	v_mul_f32_e32 v20, 0xbfb8aa3b, v23
	v_exp_f32_e32 v20, v20
	s_nop 0
	v_add_f32_e32 v20, 1.0, v20
	v_div_scale_f32 v21, s[2:3], v20, v20, v154
	v_rcp_f32_e32 v22, v21
	s_nop 0
	v_fma_f32 v23, -v21, v22, 1.0
	v_fmac_f32_e32 v22, v23, v22
	v_div_scale_f32 v23, vcc, v154, v20, v154
	v_mul_f32_e32 v52, v23, v22
	v_fma_f32 v53, -v21, v52, v23
	v_fmac_f32_e32 v52, v53, v22
	v_fma_f32 v21, -v21, v52, v23
	v_div_fmas_f32 v21, v21, v22, v52
	v_div_fixup_f32 v20, v21, v20, v154
; template <int CTRL> __device__ __forceinline__ float dppx(float v) { return __int_as_float(__builtin_amdgcn_update_dpp(0, __float_as_int(v), CTRL, 0xf, 0xf, true)); }
; __device__ __forceinline__ float log_forget(float z, float lb) {
;   const float r0 = fminf(z, 0.f) - __logf(1.f + __expf(-fabsf(z)));
;   const float r1 = __logf(lb + (1.f - lb) / (1.f + __expf(-z)));
;   return lb <= 0.f ? r0 : r1;
; }
;   __device__ __forceinline__ void operator()(const f32x4 (&acc)[2][2][4][2], const pg8::Unit& u, int wr, int wc, int fr, int fq) const {
;     ...
;           for (int qh = 0; qh < 2; ++qh) { float g[4][4], cs[4][4], carry[4];
;             const f32x4 lq = qh == 0 ? l0 : l1;
; #pragma unroll
;             for (int q = 0; q < 4; ++q) carry[q] = 0.f;
; #pragma unroll
;             for (int m = 0; m < 4; ++m)
; #pragma unroll
;               for (int q = 0; q < 4; ++q) { const float gv = log_forget(acc[ai][bj][m][qh][q], lq[q]); g[m][q] = gv;
;                 float sc = gv; sc += dppx<0x111>(sc); sc += dppx<0x112>(sc); sc += dppx<0x114>(sc); sc += dppx<0x118>(sc);
;                 const float tot16 = __int_as_float(__builtin_amdgcn_ds_swizzle(__float_as_int(sc), 0x1F0));
	v_add_f32_e32 v20, v71, v20
	v_cmp_gt_f32_e32 vcc, s37, v20
	s_nop 1
	v_cndmask_b32_e64 v21, 0, 32, vcc
	v_ldexp_f32 v20, v20, v21
	v_log_f32_e32 v20, v20
	s_nop 0
	v_mul_f32_e32 v21, 0x3f317217, v20
	v_fma_f32 v21, v20, s33, -v21
	v_fmac_f32_e32 v21, 0x3377d1cf, v20
	v_fmac_f32_e32 v21, 0x3f317217, v20
	v_cmp_lt_f32_e64 s[60:61], |v20|, s36
	s_nop 1
	v_cndmask_b32_e64 v20, v20, v21, s[60:61]
	v_cndmask_b32_e32 v21, 0, v216, vcc
	v_sub_f32_e32 v79, v20, v21
	v_mul_f32_e32 v16, 0xbfb8aa3b, v16
	v_exp_f32_e32 v16, v16
	s_nop 0
	v_add_f32_e32 v16, 1.0, v16
	s_nop 0
	s_nop 0
	s_nop 1
	v_div_scale_f32 v20, s[2:3], v16, v16, v157
	v_rcp_f32_e32 v21, v20
	s_nop 0
	v_fma_f32 v22, -v20, v21, 1.0
	v_fmac_f32_e32 v21, v22, v21
	v_div_scale_f32 v22, vcc, v157, v16, v157
	v_mul_f32_e32 v23, v22, v21
	v_fma_f32 v53, -v20, v23, v22
	v_fmac_f32_e32 v23, v53, v21
	v_fma_f32 v20, -v20, v23, v22
	v_div_fmas_f32 v20, v20, v21, v23
	v_div_fixup_f32 v16, v20, v16, v157
	v_add_f32_e32 v16, v68, v16
	v_cmp_gt_f32_e32 vcc, s37, v16
	s_nop 1
	v_cndmask_b32_e64 v20, 0, 32, vcc
	v_ldexp_f32 v16, v16, v20
	v_log_f32_e32 v16, v16
	s_nop 0
	v_mul_f32_e32 v20, 0x3f317217, v16
	v_fma_f32 v20, v16, s33, -v20
	v_fmac_f32_e32 v20, 0x3377d1cf, v16
	v_fmac_f32_e32 v20, 0x3f317217, v16
	v_cmp_lt_f32_e64 s[60:61], |v16|, s36
	s_nop 1
	v_cndmask_b32_e64 v16, v16, v20, s[60:61]
	v_cndmask_b32_e32 v20, 0, v216, vcc
	v_sub_f32_e32 v68, v16, v20
	s_nop 0
	s_nop 1
	s_nop 0
	s_nop 1
	v_mul_f32_e32 v16, 0xbfb8aa3b, v17
	v_exp_f32_e32 v16, v16
	s_nop 0
	v_add_f32_e32 v16, 1.0, v16
	v_div_scale_f32 v17, s[2:3], v16, v16, v156
	v_rcp_f32_e32 v20, v17
	v_mov_b32_e32 v52, v68
	v_fma_f32 v21, -v17, v20, 1.0
	v_fmac_f32_e32 v20, v21, v20
	v_div_scale_f32 v21, vcc, v156, v16, v156
	v_mul_f32_e32 v22, v21, v20
	v_fma_f32 v23, -v17, v22, v21
	v_fmac_f32_e32 v22, v23, v20
	v_fma_f32 v17, -v17, v22, v21
	v_div_fmas_f32 v17, v17, v20, v22
	v_div_fixup_f32 v16, v17, v16, v156
	v_add_f32_e32 v16, v69, v16
	v_cmp_gt_f32_e32 vcc, s37, v16
	v_mov_b32_dpp v54, v52 row_shr:1 row_mask:0xf bank_mask:0xf bound_ctrl:1
	s_nop 0
	v_cndmask_b32_e64 v17, 0, 32, vcc
	v_ldexp_f32 v16, v16, v17
	v_log_f32_e32 v16, v16
	s_nop 0
	v_mul_f32_e32 v17, 0x3f317217, v16
	v_fma_f32 v17, v16, s33, -v17
	v_fmac_f32_e32 v17, 0x3377d1cf, v16
	v_fmac_f32_e32 v17, 0x3f317217, v16
	v_cmp_lt_f32_e64 s[60:61], |v16|, s36
	s_nop 1
	v_cndmask_b32_e64 v16, v16, v17, s[60:61]
	v_cndmask_b32_e32 v17, 0, v216, vcc
	v_sub_f32_e32 v69, v16, v17
	v_mov_b32_e32 v53, v69
	s_nop 1
	v_mov_b32_dpp v55, v53 row_shr:1 row_mask:0xf bank_mask:0xf bound_ctrl:1
	v_pk_add_f32 v[54:55], v[52:53], v[54:55]
	s_nop 1
	v_mov_b32_dpp v68, v54 row_shr:2 row_mask:0xf bank_mask:0xf bound_ctrl:1
	v_mov_b32_dpp v69, v55 row_shr:2 row_mask:0xf bank_mask:0xf bound_ctrl:1
	v_pk_add_f32 v[54:55], v[54:55], v[68:69]
	s_nop 1
	v_mov_b32_dpp v68, v54 row_shr:4 row_mask:0xf bank_mask:0xf bound_ctrl:1
	v_mov_b32_dpp v69, v55 row_shr:4 row_mask:0xf bank_mask:0xf bound_ctrl:1
	v_mul_f32_e32 v16, 0xbfb8aa3b, v18
	v_exp_f32_e32 v16, v16
	v_pk_add_f32 v[54:55], v[54:55], v[68:69]
	v_add_f32_e32 v16, 1.0, v16
	v_div_scale_f32 v17, s[2:3], v16, v16, v155
	v_rcp_f32_e32 v18, v17
	v_mov_b32_dpp v68, v54 row_shr:8 row_mask:0xf bank_mask:0xf bound_ctrl:1
	v_mov_b32_dpp v69, v55 row_shr:8 row_mask:0xf bank_mask:0xf bound_ctrl:1
	v_pk_add_f32 v[54:55], v[54:55], v[68:69]
	v_fma_f32 v20, -v17, v18, 1.0
	v_fmac_f32_e32 v18, v20, v18
	v_div_scale_f32 v20, vcc, v155, v16, v155
	v_mul_f32_e32 v21, v20, v18
	v_fma_f32 v22, -v17, v21, v20
	v_fmac_f32_e32 v21, v22, v18
	v_fma_f32 v17, -v17, v21, v20
	v_div_fmas_f32 v17, v17, v18, v21
	v_div_fixup_f32 v16, v17, v16, v155
	v_add_f32_e32 v16, v70, v16
	v_cmp_gt_f32_e32 vcc, s37, v16
	ds_swizzle_b32 v68, v54 offset:swizzle(BROADCAST,16,15)
	ds_swizzle_b32 v69, v55 offset:swizzle(BROADCAST,16,15)
	v_cndmask_b32_e64 v17, 0, 32, vcc
	v_ldexp_f32 v16, v16, v17
	v_log_f32_e32 v16, v16
	s_nop 0
	v_mul_f32_e32 v17, 0x3f317217, v16
	v_fma_f32 v17, v16, s33, -v17
	v_fmac_f32_e32 v17, 0x3377d1cf, v16
	v_fmac_f32_e32 v17, 0x3f317217, v16
	v_cmp_lt_f32_e64 s[60:61], |v16|, s36
	s_nop 1
	v_cndmask_b32_e64 v16, v16, v17, s[60:61]
	v_cndmask_b32_e32 v17, 0, v216, vcc
	v_sub_f32_e32 v70, v16, v17
	s_nop 0
	s_nop 1
	s_nop 0
	s_nop 1
	v_mul_f32_e32 v16, 0xbfb8aa3b, v19
	v_exp_f32_e32 v16, v16
	s_nop 0
	v_add_f32_e32 v16, 1.0, v16
	v_div_scale_f32 v17, s[2:3], v16, v16, v154
	v_rcp_f32_e32 v18, v17
	v_mov_b32_e32 v56, v70
	v_fma_f32 v19, -v17, v18, 1.0
	v_fmac_f32_e32 v18, v19, v18
	v_div_scale_f32 v19, vcc, v154, v16, v154
	v_mul_f32_e32 v20, v19, v18
	v_fma_f32 v21, -v17, v20, v19
	v_fmac_f32_e32 v20, v21, v18
	v_fma_f32 v17, -v17, v20, v19
	v_div_fmas_f32 v17, v17, v18, v20
	v_div_fixup_f32 v16, v17, v16, v154
	v_add_f32_e32 v16, v71, v16
	v_cmp_gt_f32_e32 vcc, s37, v16
	v_mov_b32_dpp v58, v56 row_shr:1 row_mask:0xf bank_mask:0xf bound_ctrl:1
	s_nop 0
	v_cndmask_b32_e64 v17, 0, 32, vcc
	v_ldexp_f32 v16, v16, v17
	v_log_f32_e32 v16, v16
	s_nop 0
	v_mul_f32_e32 v17, 0x3f317217, v16
	v_fma_f32 v17, v16, s33, -v17
	v_fmac_f32_e32 v17, 0x3377d1cf, v16
	v_fmac_f32_e32 v17, 0x3f317217, v16
	v_cmp_lt_f32_e64 s[60:61], |v16|, s36
	s_nop 1
	v_cndmask_b32_e64 v16, v16, v17, s[60:61]
	v_cndmask_b32_e32 v17, 0, v216, vcc
	v_sub_f32_e32 v71, v16, v17
	v_mov_b32_e32 v57, v71
	v_mov_b32_e32 v33, v61
	v_mov_b32_e32 v32, v60
	v_mov_b32_dpp v60, v38 row_shr:2 row_mask:0xf bank_mask:0xf bound_ctrl:1
	v_mov_b32_dpp v17, v33 row_shr:1 row_mask:0xf bank_mask:0xf bound_ctrl:1
	v_mov_b32_dpp v16, v32 row_shr:1 row_mask:0xf bank_mask:0xf bound_ctrl:1
	v_pk_add_f32 v[16:17], v[32:33], v[16:17]
; template <int CTRL> __device__ __forceinline__ float dppx(float v) { return __int_as_float(__builtin_amdgcn_update_dpp(0, __float_as_int(v), CTRL, 0xf, 0xf, true)); }
;   __device__ __forceinline__ void operator()(const f32x4 (&acc)[2][2][4][2], const pg8::Unit& u, int wr, int wc, int fr, int fq) const {
;     ...
;               for (int q = 0; q < 4; ++q) { const float gv = log_forget(acc[ai][bj][m][qh][q], lq[q]); g[m][q] = gv;
;                 float sc = gv; sc += dppx<0x111>(sc); sc += dppx<0x112>(sc); sc += dppx<0x114>(sc); sc += dppx<0x118>(sc);
;                 const float tot16 = __int_as_float(__builtin_amdgcn_ds_swizzle(__float_as_int(sc), 0x1F0));
;                 cs[m][q] = sc + carry[q]; carry[q] += tot16; }
; #pragma unroll
;             for (int m = 0; m < 4; ++m) { const int r = row0 + ai * 128 + m * 16; float bq[4], kq[4];
; #pragma unroll
;               for (int q = 0; q < 4; ++q) { bq[q] = bwd ? (carry[q] - cs[m][q]) + g[m][q] : cs[m][q]; kq[q] = 1.f - __expf(g[m][q]); }
;               *(f32x4*)(logfp + (size_t)r * 1024 + c + 4 * qh) = (f32x4){bq[0], bq[1], bq[2], bq[3]};
	v_mov_b32_dpp v61, v39 row_shr:2 row_mask:0xf bank_mask:0xf bound_ctrl:1
	v_pk_add_f32 v[38:39], v[38:39], v[60:61]
	v_mov_b32_dpp v18, v16 row_shr:2 row_mask:0xf bank_mask:0xf bound_ctrl:1
	v_mov_b32_dpp v19, v17 row_shr:2 row_mask:0xf bank_mask:0xf bound_ctrl:1
	v_pk_add_f32 v[16:17], v[16:17], v[18:19]
	v_mov_b32_dpp v60, v38 row_shr:4 row_mask:0xf bank_mask:0xf bound_ctrl:1
	v_mov_b32_dpp v61, v39 row_shr:4 row_mask:0xf bank_mask:0xf bound_ctrl:1
	v_mov_b32_dpp v18, v16 row_shr:4 row_mask:0xf bank_mask:0xf bound_ctrl:1
	v_mov_b32_dpp v19, v17 row_shr:4 row_mask:0xf bank_mask:0xf bound_ctrl:1
	v_pk_add_f32 v[16:17], v[16:17], v[18:19]
	v_pk_add_f32 v[38:39], v[38:39], v[60:61]
	v_mov_b32_dpp v59, v57 row_shr:1 row_mask:0xf bank_mask:0xf bound_ctrl:1
	v_mov_b32_dpp v18, v16 row_shr:8 row_mask:0xf bank_mask:0xf bound_ctrl:1
	v_mov_b32_dpp v19, v17 row_shr:8 row_mask:0xf bank_mask:0xf bound_ctrl:1
	v_pk_add_f32 v[16:17], v[16:17], v[18:19]
	ds_swizzle_b32 v18, v16 offset:swizzle(BROADCAST,16,15)
	v_pk_add_f32 v[34:35], v[16:17], 0 op_sel_hi:[1,0]
	v_mul_f32_e32 v16, 0x3fb8aa3b, v32
	v_exp_f32_e32 v16, v16
	ds_swizzle_b32 v19, v17 offset:swizzle(BROADCAST,16,15)
	v_mov_b32_dpp v60, v38 row_shr:8 row_mask:0xf bank_mask:0xf bound_ctrl:1
	v_mov_b32_dpp v61, v39 row_shr:8 row_mask:0xf bank_mask:0xf bound_ctrl:1
	v_sub_f32_e32 v80, 1.0, v16
	v_mul_f32_e32 v16, 0x3fb8aa3b, v33
	v_exp_f32_e32 v16, v16
	s_waitcnt lgkmcnt(0)
	v_pk_add_f32 v[20:21], v[18:19], 0 op_sel_hi:[1,0]
	v_pk_add_f32 v[38:39], v[38:39], v[60:61]
	ds_swizzle_b32 v60, v38 offset:swizzle(BROADCAST,16,15)
	v_sub_f32_e32 v81, 1.0, v16
	ds_swizzle_b32 v61, v39 offset:swizzle(BROADCAST,16,15)
	v_mov_b32_e32 v29, v63
	v_mov_b32_e32 v28, v62
	v_pk_add_f32 v[38:39], v[20:21], v[38:39]
	v_mov_b32_dpp v17, v29 row_shr:1 row_mask:0xf bank_mask:0xf bound_ctrl:1
	v_mov_b32_dpp v16, v28 row_shr:1 row_mask:0xf bank_mask:0xf bound_ctrl:1
	v_pk_add_f32 v[16:17], v[28:29], v[16:17]
	s_waitcnt lgkmcnt(0)
	v_pk_add_f32 v[62:63], v[20:21], v[60:61]
	v_mul_f32_e32 v20, 0x3fb8aa3b, v30
	v_mov_b32_dpp v18, v16 row_shr:2 row_mask:0xf bank_mask:0xf bound_ctrl:1
	v_mov_b32_dpp v19, v17 row_shr:2 row_mask:0xf bank_mask:0xf bound_ctrl:1
	v_pk_add_f32 v[16:17], v[16:17], v[18:19]
	v_exp_f32_e32 v20, v20
	v_pk_add_f32 v[58:59], v[56:57], v[58:59]
	v_mov_b32_dpp v18, v16 row_shr:4 row_mask:0xf bank_mask:0xf bound_ctrl:1
	v_mov_b32_dpp v19, v17 row_shr:4 row_mask:0xf bank_mask:0xf bound_ctrl:1
	v_pk_add_f32 v[16:17], v[16:17], v[18:19]
	s_nop 1
	v_mov_b32_dpp v18, v16 row_shr:8 row_mask:0xf bank_mask:0xf bound_ctrl:1
	v_mov_b32_dpp v19, v17 row_shr:8 row_mask:0xf bank_mask:0xf bound_ctrl:1
	v_pk_add_f32 v[16:17], v[16:17], v[18:19]
	ds_swizzle_b32 v18, v16 offset:swizzle(BROADCAST,16,15)
	ds_swizzle_b32 v19, v17 offset:swizzle(BROADCAST,16,15)
	v_pk_add_f32 v[36:37], v[16:17], 0 op_sel_hi:[1,0]
	v_mul_f32_e32 v16, 0x3fb8aa3b, v28
	v_exp_f32_e32 v16, v16
	s_waitcnt lgkmcnt(0)
	v_pk_add_f32 v[22:23], v[18:19], 0 op_sel_hi:[1,0]
	v_lshl_add_u64 v[18:19], v[84:85], 0, v[50:51]
	v_sub_f32_e32 v84, 1.0, v20
	v_mul_f32_e32 v20, 0x3fb8aa3b, v31
	v_exp_f32_e32 v20, v20
	v_sub_f32_e32 v82, 1.0, v16
	v_mul_f32_e32 v16, 0x3fb8aa3b, v29
	v_exp_f32_e32 v16, v16
	v_sub_f32_e32 v85, 1.0, v20
	v_sub_f32_e32 v83, 1.0, v16
	v_mov_b32_e32 v41, v75
	v_mov_b32_e32 v40, v74
	v_pk_add_f32 v[74:75], v[62:63], v[26:27]
	v_mov_b32_dpp v21, v41 row_shr:1 row_mask:0xf bank_mask:0xf bound_ctrl:1
	v_mov_b32_dpp v20, v40 row_shr:1 row_mask:0xf bank_mask:0xf bound_ctrl:1
	v_pk_add_f32 v[20:21], v[40:41], v[20:21]
	v_mul_f32_e32 v26, 0x3fb8aa3b, v42
	v_exp_f32_e32 v26, v26
	v_mov_b32_dpp v24, v20 row_shr:2 row_mask:0xf bank_mask:0xf bound_ctrl:1
	v_mov_b32_dpp v25, v21 row_shr:2 row_mask:0xf bank_mask:0xf bound_ctrl:1
	v_pk_add_f32 v[20:21], v[20:21], v[24:25]
	v_pk_add_f32 v[62:63], v[62:63], v[72:73]
	v_sub_f32_e32 v76, 1.0, v26
	v_mov_b32_dpp v24, v20 row_shr:4 row_mask:0xf bank_mask:0xf bound_ctrl:1
	v_mov_b32_dpp v25, v21 row_shr:4 row_mask:0xf bank_mask:0xf bound_ctrl:1
	v_pk_add_f32 v[20:21], v[20:21], v[24:25]
	v_mul_f32_e32 v26, 0x3fb8aa3b, v43
	v_pk_add_f32 v[54:55], v[62:63], v[54:55]
	v_mov_b32_dpp v24, v20 row_shr:8 row_mask:0xf bank_mask:0xf bound_ctrl:1
	v_mov_b32_dpp v25, v21 row_shr:8 row_mask:0xf bank_mask:0xf bound_ctrl:1
	v_pk_add_f32 v[20:21], v[20:21], v[24:25]
	ds_swizzle_b32 v24, v20 offset:swizzle(BROADCAST,16,15)
	ds_swizzle_b32 v25, v21 offset:swizzle(BROADCAST,16,15)
	v_pk_add_f32 v[62:63], v[62:63], v[68:69]
	v_mul_f32_e32 v68, 0x3fb8aa3b, v52
	v_exp_f32_e32 v26, v26
	v_exp_f32_e32 v68, v68
	v_pk_add_f32 v[60:61], v[22:23], v[20:21]
	s_waitcnt lgkmcnt(0)
	v_pk_add_f32 v[24:25], v[22:23], v[24:25]
	v_lshl_add_u64 v[22:23], v[88:89], 0, v[50:51]
	v_sub_f32_e32 v77, 1.0, v26
	v_sub_f32_e32 v88, 1.0, v68
	v_mul_f32_e32 v68, 0x3fb8aa3b, v53
	v_mov_b32_e32 v45, v79
	v_mov_b32_e32 v44, v78
	v_exp_f32_e32 v68, v68
	v_mov_b32_dpp v27, v45 row_shr:1 row_mask:0xf bank_mask:0xf bound_ctrl:1
	v_mov_b32_dpp v26, v44 row_shr:1 row_mask:0xf bank_mask:0xf bound_ctrl:1
	v_pk_add_f32 v[26:27], v[44:45], v[26:27]
	v_sub_f32_e32 v89, 1.0, v68
	v_mov_b32_dpp v68, v58 row_shr:2 row_mask:0xf bank_mask:0xf bound_ctrl:1
	v_mov_b32_dpp v46, v26 row_shr:2 row_mask:0xf bank_mask:0xf bound_ctrl:1
	v_mov_b32_dpp v47, v27 row_shr:2 row_mask:0xf bank_mask:0xf bound_ctrl:1
	v_pk_add_f32 v[26:27], v[26:27], v[46:47]
	v_mov_b32_dpp v69, v59 row_shr:2 row_mask:0xf bank_mask:0xf bound_ctrl:1
	v_pk_add_f32 v[58:59], v[58:59], v[68:69]
	v_mov_b32_dpp v46, v26 row_shr:4 row_mask:0xf bank_mask:0xf bound_ctrl:1
	v_mov_b32_dpp v47, v27 row_shr:4 row_mask:0xf bank_mask:0xf bound_ctrl:1
	v_pk_add_f32 v[26:27], v[26:27], v[46:47]
	v_mov_b32_dpp v68, v58 row_shr:4 row_mask:0xf bank_mask:0xf bound_ctrl:1
	v_mov_b32_dpp v69, v59 row_shr:4 row_mask:0xf bank_mask:0xf bound_ctrl:1
	v_mov_b32_dpp v46, v26 row_shr:8 row_mask:0xf bank_mask:0xf bound_ctrl:1
	v_mov_b32_dpp v47, v27 row_shr:8 row_mask:0xf bank_mask:0xf bound_ctrl:1
	v_pk_add_f32 v[58:59], v[58:59], v[68:69]
	v_pk_add_f32 v[26:27], v[26:27], v[46:47]
	ds_swizzle_b32 v46, v26 offset:swizzle(BROADCAST,16,15)
	v_mov_b32_dpp v68, v58 row_shr:8 row_mask:0xf bank_mask:0xf bound_ctrl:1
	v_mov_b32_dpp v69, v59 row_shr:8 row_mask:0xf bank_mask:0xf bound_ctrl:1
	ds_swizzle_b32 v47, v27 offset:swizzle(BROADCAST,16,15)
	v_pk_add_f32 v[58:59], v[58:59], v[68:69]
	ds_swizzle_b32 v68, v58 offset:swizzle(BROADCAST,16,15)
	ds_swizzle_b32 v69, v59 offset:swizzle(BROADCAST,16,15)
	v_mul_f32_e32 v20, 0x3fb8aa3b, v40
	v_exp_f32_e32 v20, v20
	s_waitcnt lgkmcnt(2)
; template <int CTRL> __device__ __forceinline__ float dppx(float v) { return __int_as_float(__builtin_amdgcn_update_dpp(0, __float_as_int(v), CTRL, 0xf, 0xf, true)); }
; __device__ __forceinline__ unsigned cvt_pk_bf16(float lo, float hi) { unsigned r; asm volatile("v_cvt_pk_bf16_f32 %0, %1, %2" : "=v"(r) : "v"(lo), "v"(hi)); return r; }
; __device__ __forceinline__ float log_forget(float z, float lb) {
;   const float r0 = fminf(z, 0.f) - __logf(1.f + __expf(-fabsf(z)));
;   const float r1 = __logf(lb + (1.f - lb) / (1.f + __expf(-z)));
;   return lb <= 0.f ? r0 : r1;
; }
;   __device__ __forceinline__ void operator()(const f32x4 (&acc)[2][2][4][2], const pg8::Unit& u, int wr, int wc, int fr, int fq) const {
;     ...
;               for (int q = 0; q < 4; ++q) { const float gv = log_forget(acc[ai][bj][m][qh][q], lq[q]); g[m][q] = gv;
;                 float sc = gv; sc += dppx<0x111>(sc); sc += dppx<0x112>(sc); sc += dppx<0x114>(sc); sc += dppx<0x118>(sc);
;                 const float tot16 = __int_as_float(__builtin_amdgcn_ds_swizzle(__float_as_int(sc), 0x1F0));
;                 cs[m][q] = sc + carry[q]; carry[q] += tot16; }
; #pragma unroll
;             for (int m = 0; m < 4; ++m) { const int r = row0 + ai * 128 + m * 16; float bq[4], kq[4];
; #pragma unroll
;               for (int q = 0; q < 4; ++q) { bq[q] = bwd ? (carry[q] - cs[m][q]) + g[m][q] : cs[m][q]; kq[q] = 1.f - __expf(g[m][q]); }
;               *(f32x4*)(logfp + (size_t)r * 1024 + c + 4 * qh) = (f32x4){bq[0], bq[1], bq[2], bq[3]};
;               u32x2 w; w.x = pg8::cvt_pk_bf16(kq[0], kq[1]); w.y = pg8::cvt_pk_bf16(kq[2], kq[3]);
;               *(u32x2*)(km + (size_t)r * 1024 + c + 4 * qh) = w; } } }
	v_pk_add_f32 v[46:47], v[24:25], v[46:47]
	v_pk_add_f32 v[72:73], v[24:25], v[26:27]
	v_pk_add_f32 v[58:59], v[46:47], v[58:59]
	s_waitcnt lgkmcnt(0)
	v_pk_add_f32 v[46:47], v[46:47], v[68:69]
	v_pk_add_f32 v[68:69], v[62:63], v[34:35] neg_lo:[0,1] neg_hi:[0,1]
	v_pk_add_f32 v[70:71], v[46:47], v[36:37] neg_lo:[0,1] neg_hi:[0,1]
	v_mul_f32_e32 v24, 0x3fb8aa3b, v44
	v_pk_add_f32 v[32:33], v[32:33], v[68:69]
	v_pk_add_f32 v[28:29], v[28:29], v[70:71]
	v_lshl_add_u64 v[16:17], v[86:87], 0, v[48:49]
	v_sub_f32_e32 v86, 1.0, v20
	v_mul_f32_e32 v20, 0x3fb8aa3b, v41
	v_exp_f32_e32 v24, v24
	v_cndmask_b32_e64 v37, v37, v29, s[42:43]
	v_cndmask_b32_e64 v36, v36, v28, s[42:43]
	v_cndmask_b32_e64 v35, v35, v33, s[42:43]
	v_cndmask_b32_e64 v34, v34, v32, s[42:43]
	v_exp_f32_e32 v20, v20
	global_store_dwordx4 v[18:19], v[34:37], off
	v_cvt_pk_bf16_f32 v28, v80, v81
	v_cvt_pk_bf16_f32 v29, v82, v83
	global_store_dwordx2 v[16:17], v[28:29], off
	v_pk_add_f32 v[28:29], v[62:63], v[38:39] neg_lo:[0,1] neg_hi:[0,1]
	v_pk_add_f32 v[32:33], v[46:47], v[60:61] neg_lo:[0,1] neg_hi:[0,1]
	v_pk_add_f32 v[28:29], v[30:31], v[28:29]
	v_pk_add_f32 v[30:31], v[40:41], v[32:33]
	v_sub_f32_e32 v78, 1.0, v24
	v_mul_f32_e32 v24, 0x3fb8aa3b, v45
	v_cndmask_b32_e64 v31, v61, v31, s[42:43]
	v_cndmask_b32_e64 v30, v60, v30, s[42:43]
	v_cndmask_b32_e64 v29, v39, v29, s[42:43]
	v_cndmask_b32_e64 v28, v38, v28, s[42:43]
	v_sub_f32_e32 v87, 1.0, v20
	v_lshl_add_u64 v[20:21], v[90:91], 0, v[48:49]
	v_exp_f32_e32 v24, v24
	global_store_dwordx4 v[22:23], v[28:31], off
	v_lshl_add_u64 v[26:27], v[92:93], 0, v[50:51]
	v_sub_f32_e32 v79, 1.0, v24
	v_cvt_pk_bf16_f32 v28, v84, v85
	v_cvt_pk_bf16_f32 v29, v86, v87
	global_store_dwordx2 v[20:21], v[28:29], off
	v_pk_add_f32 v[28:29], v[62:63], v[74:75] neg_lo:[0,1] neg_hi:[0,1]
	v_pk_add_f32 v[30:31], v[46:47], v[72:73] neg_lo:[0,1] neg_hi:[0,1]
	v_pk_add_f32 v[28:29], v[42:43], v[28:29]
	v_pk_add_f32 v[30:31], v[44:45], v[30:31]
	v_cndmask_b32_e64 v29, v75, v29, s[42:43]
	v_cndmask_b32_e64 v31, v73, v31, s[42:43]
	v_cndmask_b32_e64 v30, v72, v30, s[42:43]
	v_cndmask_b32_e64 v28, v74, v28, s[42:43]
	v_lshl_add_u64 v[24:25], v[94:95], 0, v[48:49]
	global_store_dwordx4 v[26:27], v[28:31], off
	s_nop 1
	v_cvt_pk_bf16_f32 v28, v76, v77
	v_cvt_pk_bf16_f32 v29, v78, v79
	global_store_dwordx2 v[24:25], v[28:29], off
	v_mul_f32_e32 v28, 0x3fb8aa3b, v56
	v_exp_f32_e32 v28, v28
	v_pk_add_f32 v[30:31], v[46:47], v[58:59] neg_lo:[0,1] neg_hi:[0,1]
	v_sub_f32_e32 v34, 1.0, v28
	v_pk_add_f32 v[28:29], v[62:63], v[54:55] neg_lo:[0,1] neg_hi:[0,1]
	v_pk_add_f32 v[30:31], v[56:57], v[30:31]
	v_pk_add_f32 v[28:29], v[52:53], v[28:29]
	v_cndmask_b32_e64 v32, v58, v30, s[42:43]
	v_cndmask_b32_e64 v30, v54, v28, s[42:43]
	v_mul_f32_e32 v28, 0x3fb8aa3b, v57
	v_exp_f32_e32 v28, v28
	v_cndmask_b32_e64 v33, v59, v31, s[42:43]
	v_cndmask_b32_e64 v31, v55, v29, s[42:43]
	v_sub_f32_e32 v35, 1.0, v28
	v_lshl_add_u64 v[28:29], v[98:99], 0, v[50:51]
	global_store_dwordx4 v[28:29], v[30:33], off
	s_nop 1
	v_cvt_pk_bf16_f32 v32, v88, v89
	v_cvt_pk_bf16_f32 v33, v34, v35
	v_lshl_add_u64 v[30:31], v[100:101], 0, v[48:49]
	global_store_dwordx2 v[30:31], v[32:33], off
	v_mul_f32_e32 v12, 0xbfb8aa3b, v12
	v_exp_f32_e32 v12, v12
	s_nop 0
	v_add_f32_e32 v12, 1.0, v12
	s_nop 0
	s_nop 1
	v_div_scale_f32 v33, s[2:3], v12, v12, v114
	v_rcp_f32_e32 v35, v33
	s_nop 0
	v_fma_f32 v36, -v33, v35, 1.0
	v_fmac_f32_e32 v35, v36, v35
	v_div_scale_f32 v36, vcc, v114, v12, v114
	v_mul_f32_e32 v37, v36, v35
	v_fma_f32 v38, -v33, v37, v36
	v_fmac_f32_e32 v37, v38, v35
	v_fma_f32 v33, -v33, v37, v36
	v_div_fmas_f32 v33, v33, v35, v37
	v_div_fixup_f32 v12, v33, v12, v114
	v_add_f32_e32 v12, v64, v12
	v_cmp_gt_f32_e32 vcc, s37, v12
	s_nop 1
	v_cndmask_b32_e64 v33, 0, 32, vcc
	v_ldexp_f32 v12, v12, v33
	v_log_f32_e32 v12, v12
	s_nop 0
	v_mul_f32_e32 v33, 0x3f317217, v12
	v_fma_f32 v33, v12, s33, -v33
	v_fmac_f32_e32 v33, 0x3377d1cf, v12
	v_fmac_f32_e32 v33, 0x3f317217, v12
	v_cmp_lt_f32_e64 s[44:45], |v12|, s36
	s_nop 1
	v_cndmask_b32_e64 v12, v12, v33, s[44:45]
	v_cndmask_b32_e32 v33, 0, v216, vcc
	v_sub_f32_e32 v50, v12, v33
	s_nop 0
	s_nop 1
	s_nop 0
	s_nop 1
	v_mul_f32_e32 v12, 0xbfb8aa3b, v13
	v_exp_f32_e32 v12, v12
	s_nop 0
	v_add_f32_e32 v12, 1.0, v12
	v_div_scale_f32 v13, s[2:3], v12, v12, v113
	v_rcp_f32_e32 v36, v13
	s_nop 0
	v_fma_f32 v37, -v13, v36, 1.0
	v_fmac_f32_e32 v36, v37, v36
	v_div_scale_f32 v37, vcc, v113, v12, v113
	v_mul_f32_e32 v38, v37, v36
	v_fma_f32 v39, -v13, v38, v37
	v_fmac_f32_e32 v38, v39, v36
	v_fma_f32 v13, -v13, v38, v37
	v_div_fmas_f32 v13, v13, v36, v38
	v_div_fixup_f32 v12, v13, v12, v113
	v_add_f32_e32 v12, v65, v12
	v_cmp_gt_f32_e32 vcc, s37, v12
	s_nop 1
	v_cndmask_b32_e64 v13, 0, 32, vcc
	v_ldexp_f32 v12, v12, v13
	v_log_f32_e32 v12, v12
	s_nop 0
	v_mul_f32_e32 v13, 0x3f317217, v12
	v_fma_f32 v13, v12, s33, -v13
	v_fmac_f32_e32 v13, 0x3377d1cf, v12
	v_fmac_f32_e32 v13, 0x3f317217, v12
	v_cmp_lt_f32_e64 s[44:45], |v12|, s36
	s_nop 1
	v_cndmask_b32_e64 v12, v12, v13, s[44:45]
	v_cndmask_b32_e32 v13, 0, v216, vcc
	v_sub_f32_e32 v51, v12, v13
	s_nop 1
	s_nop 0
	s_nop 1
	v_mul_f32_e32 v13, 0xbfb8aa3b, v14
	v_exp_f32_e32 v13, v13
	s_nop 0
	v_add_f32_e32 v13, 1.0, v13
	v_div_scale_f32 v14, s[2:3], v13, v13, v112
	v_rcp_f32_e32 v37, v14
	s_nop 0
	v_fma_f32 v38, -v14, v37, 1.0
	v_fmac_f32_e32 v37, v38, v37
	v_div_scale_f32 v38, vcc, v112, v13, v112
	v_mul_f32_e32 v39, v38, v37
	v_fma_f32 v40, -v14, v39, v38
	v_fmac_f32_e32 v39, v40, v37
	v_fma_f32 v14, -v14, v39, v38
	v_div_fmas_f32 v14, v14, v37, v39
	v_div_fixup_f32 v13, v14, v13, v112
	v_add_f32_e32 v13, v66, v13
; __device__ __forceinline__ float log_forget(float z, float lb) {
;   const float r0 = fminf(z, 0.f) - __logf(1.f + __expf(-fabsf(z)));
;   const float r1 = __logf(lb + (1.f - lb) / (1.f + __expf(-z)));
;   return lb <= 0.f ? r0 : r1;
; }
;   __device__ __forceinline__ void operator()(const f32x4 (&acc)[2][2][4][2], const pg8::Unit& u, int wr, int wc, int fr, int fq) const {
;     ...
;               for (int q = 0; q < 4; ++q) { const float gv = log_forget(acc[ai][bj][m][qh][q], lq[q]); g[m][q] = gv;
	v_cmp_gt_f32_e32 vcc, s37, v13
	s_nop 1
	v_cndmask_b32_e64 v14, 0, 32, vcc
	v_ldexp_f32 v13, v13, v14
	v_log_f32_e32 v13, v13
	s_nop 0
	v_mul_f32_e32 v14, 0x3f317217, v13
	v_fma_f32 v14, v13, s33, -v14
	v_fmac_f32_e32 v14, 0x3377d1cf, v13
	v_fmac_f32_e32 v14, 0x3f317217, v13
	v_cmp_lt_f32_e64 s[44:45], |v13|, s36
	s_nop 1
	v_cndmask_b32_e64 v13, v13, v14, s[44:45]
	v_cndmask_b32_e32 v14, 0, v216, vcc
	v_sub_f32_e32 v52, v13, v14
	s_nop 1
	s_nop 0
	s_nop 1
	v_mul_f32_e32 v14, 0xbfb8aa3b, v15
	v_exp_f32_e32 v14, v14
	s_nop 0
	v_add_f32_e32 v14, 1.0, v14
	v_div_scale_f32 v15, s[2:3], v14, v14, v96
	v_rcp_f32_e32 v38, v15
	v_mov_b32_e32 v12, v52
	v_fma_f32 v39, -v15, v38, 1.0
	v_fmac_f32_e32 v38, v39, v38
	v_div_scale_f32 v39, vcc, v96, v14, v96
	v_mul_f32_e32 v40, v39, v38
	v_fma_f32 v41, -v15, v40, v39
	v_fmac_f32_e32 v40, v41, v38
	v_fma_f32 v15, -v15, v40, v39
	v_div_fmas_f32 v15, v15, v38, v40
	v_div_fixup_f32 v14, v15, v14, v96
	v_add_f32_e32 v14, v67, v14
	v_cmp_gt_f32_e32 vcc, s37, v14
	s_nop 1
	v_cndmask_b32_e64 v15, 0, 32, vcc
	v_ldexp_f32 v14, v14, v15
	v_log_f32_e32 v14, v14
	s_nop 0
	v_mul_f32_e32 v15, 0x3f317217, v14
	v_fma_f32 v15, v14, s33, -v15
	v_fmac_f32_e32 v15, 0x3377d1cf, v14
	v_fmac_f32_e32 v15, 0x3f317217, v14
	v_cmp_lt_f32_e64 s[44:45], |v14|, s36
	s_nop 1
	v_cndmask_b32_e64 v14, v14, v15, s[44:45]
	v_cndmask_b32_e32 v15, 0, v216, vcc
	v_sub_f32_e32 v53, v14, v15
	v_mul_f32_e32 v8, 0xbfb8aa3b, v8
	v_exp_f32_e32 v8, v8
	v_mov_b32_e32 v13, v53
	v_add_f32_e32 v8, 1.0, v8
	s_nop 1
	v_div_scale_f32 v15, s[2:3], v8, v8, v114
	v_rcp_f32_e32 v39, v15
	s_nop 0
	v_fma_f32 v40, -v15, v39, 1.0
	v_fmac_f32_e32 v39, v40, v39
	v_div_scale_f32 v40, vcc, v114, v8, v114
	v_mul_f32_e32 v41, v40, v39
	v_fma_f32 v42, -v15, v41, v40
	v_fmac_f32_e32 v41, v42, v39
	v_fma_f32 v15, -v15, v41, v40
	v_div_fmas_f32 v15, v15, v39, v41
	v_div_fixup_f32 v8, v15, v8, v114
	v_add_f32_e32 v8, v64, v8
	v_cmp_gt_f32_e32 vcc, s37, v8
	s_nop 1
	v_cndmask_b32_e64 v15, 0, 32, vcc
	v_ldexp_f32 v8, v8, v15
	v_log_f32_e32 v8, v8
	s_nop 0
	v_mul_f32_e32 v15, 0x3f317217, v8
	v_fma_f32 v15, v8, s33, -v15
	v_fmac_f32_e32 v15, 0x3377d1cf, v8
	v_fmac_f32_e32 v15, 0x3f317217, v8
	v_cmp_lt_f32_e64 s[44:45], |v8|, s36
	s_nop 1
	v_cndmask_b32_e64 v8, v8, v15, s[44:45]
	v_cndmask_b32_e32 v15, 0, v216, vcc
	v_sub_f32_e32 v54, v8, v15
	s_nop 0
	s_nop 1
	s_nop 0
	s_nop 1
	v_mul_f32_e32 v8, 0xbfb8aa3b, v9
	v_exp_f32_e32 v8, v8
	s_nop 0
	v_add_f32_e32 v8, 1.0, v8
	v_div_scale_f32 v9, s[2:3], v8, v8, v113
	v_rcp_f32_e32 v40, v9
	v_mov_b32_e32 v14, v54
	v_fma_f32 v41, -v9, v40, 1.0
	v_fmac_f32_e32 v40, v41, v40
	v_div_scale_f32 v41, vcc, v113, v8, v113
	v_mul_f32_e32 v42, v41, v40
	v_fma_f32 v43, -v9, v42, v41
	v_fmac_f32_e32 v42, v43, v40
	v_fma_f32 v9, -v9, v42, v41
	v_div_fmas_f32 v9, v9, v40, v42
	v_div_fixup_f32 v8, v9, v8, v113
	v_add_f32_e32 v8, v65, v8
	v_cmp_gt_f32_e32 vcc, s37, v8
	s_nop 1
	v_cndmask_b32_e64 v9, 0, 32, vcc
	v_ldexp_f32 v8, v8, v9
	v_log_f32_e32 v8, v8
	s_nop 0
	v_mul_f32_e32 v9, 0x3f317217, v8
	v_fma_f32 v9, v8, s33, -v9
	v_fmac_f32_e32 v9, 0x3377d1cf, v8
	v_fmac_f32_e32 v9, 0x3f317217, v8
	v_cmp_lt_f32_e64 s[44:45], |v8|, s36
	s_nop 1
	v_cndmask_b32_e64 v8, v8, v9, s[44:45]
	v_cndmask_b32_e32 v9, 0, v216, vcc
	v_sub_f32_e32 v55, v8, v9
	v_mov_b32_e32 v15, v55
	s_nop 1
	s_nop 0
	s_nop 1
	v_mul_f32_e32 v9, 0xbfb8aa3b, v10
	v_exp_f32_e32 v9, v9
	s_nop 0
	v_add_f32_e32 v9, 1.0, v9
	v_div_scale_f32 v10, s[2:3], v9, v9, v112
	v_rcp_f32_e32 v41, v10
	s_nop 0
	v_fma_f32 v42, -v10, v41, 1.0
	v_fmac_f32_e32 v41, v42, v41
	v_div_scale_f32 v42, vcc, v112, v9, v112
	v_mul_f32_e32 v43, v42, v41
	v_fma_f32 v44, -v10, v43, v42
	v_fmac_f32_e32 v43, v44, v41
	v_fma_f32 v10, -v10, v43, v42
	v_div_fmas_f32 v10, v10, v41, v43
	v_div_fixup_f32 v9, v10, v9, v112
	v_add_f32_e32 v9, v66, v9
	v_cmp_gt_f32_e32 vcc, s37, v9
	s_nop 1
	v_cndmask_b32_e64 v10, 0, 32, vcc
	v_ldexp_f32 v9, v9, v10
	v_log_f32_e32 v9, v9
	s_nop 0
	v_mul_f32_e32 v10, 0x3f317217, v9
	v_fma_f32 v10, v9, s33, -v10
	v_fmac_f32_e32 v10, 0x3377d1cf, v9
	v_fmac_f32_e32 v10, 0x3f317217, v9
	v_cmp_lt_f32_e64 s[44:45], |v9|, s36
	s_nop 1
	v_cndmask_b32_e64 v9, v9, v10, s[44:45]
	v_cndmask_b32_e32 v10, 0, v216, vcc
	v_sub_f32_e32 v56, v9, v10
	s_nop 1
	s_nop 0
	s_nop 1
	v_mul_f32_e32 v10, 0xbfb8aa3b, v11
	v_exp_f32_e32 v10, v10
	s_nop 0
	v_add_f32_e32 v10, 1.0, v10
	v_div_scale_f32 v11, s[2:3], v10, v10, v96
	v_rcp_f32_e32 v42, v11
	v_mov_b32_e32 v8, v56
	v_fma_f32 v43, -v11, v42, 1.0
	v_fmac_f32_e32 v42, v43, v42
	v_div_scale_f32 v43, vcc, v96, v10, v96
	v_mul_f32_e32 v44, v43, v42
	v_fma_f32 v45, -v11, v44, v43
	v_fmac_f32_e32 v44, v45, v42
	v_fma_f32 v11, -v11, v44, v43
	v_div_fmas_f32 v11, v11, v42, v44
	v_div_fixup_f32 v10, v11, v10, v96
	v_add_f32_e32 v10, v67, v10
	v_cmp_gt_f32_e32 vcc, s37, v10
	s_nop 1
	v_cndmask_b32_e64 v11, 0, 32, vcc
	v_ldexp_f32 v10, v10, v11
	v_log_f32_e32 v10, v10
	s_nop 0
	v_mul_f32_e32 v11, 0x3f317217, v10
	v_fma_f32 v11, v10, s33, -v11
	v_fmac_f32_e32 v11, 0x3377d1cf, v10
	v_fmac_f32_e32 v11, 0x3f317217, v10
	v_cmp_lt_f32_e64 s[44:45], |v10|, s36
	s_nop 1
	v_cndmask_b32_e64 v10, v10, v11, s[44:45]
	v_cndmask_b32_e32 v11, 0, v216, vcc
	v_sub_f32_e32 v57, v10, v11
	v_mul_f32_e32 v4, 0xbfb8aa3b, v4
	v_exp_f32_e32 v4, v4
	v_mov_b32_e32 v9, v57
	v_add_f32_e32 v4, 1.0, v4
	s_nop 1
	v_div_scale_f32 v11, s[2:3], v4, v4, v114
	v_rcp_f32_e32 v43, v11
	s_nop 0
	v_fma_f32 v44, -v11, v43, 1.0
	v_fmac_f32_e32 v43, v44, v43
	v_div_scale_f32 v44, vcc, v114, v4, v114
	v_mul_f32_e32 v45, v44, v43
	v_fma_f32 v46, -v11, v45, v44
	v_fmac_f32_e32 v45, v46, v43
	v_fma_f32 v11, -v11, v45, v44
; template <int CTRL> __device__ __forceinline__ float dppx(float v) { return __int_as_float(__builtin_amdgcn_update_dpp(0, __float_as_int(v), CTRL, 0xf, 0xf, true)); }
; __device__ __forceinline__ float log_forget(float z, float lb) {
;   const float r0 = fminf(z, 0.f) - __logf(1.f + __expf(-fabsf(z)));
;   const float r1 = __logf(lb + (1.f - lb) / (1.f + __expf(-z)));
;   return lb <= 0.f ? r0 : r1;
; }
;   __device__ __forceinline__ void operator()(const f32x4 (&acc)[2][2][4][2], const pg8::Unit& u, int wr, int wc, int fr, int fq) const {
;     ...
;               for (int q = 0; q < 4; ++q) { const float gv = log_forget(acc[ai][bj][m][qh][q], lq[q]); g[m][q] = gv;
;                 float sc = gv; sc += dppx<0x111>(sc); sc += dppx<0x112>(sc); sc += dppx<0x114>(sc); sc += dppx<0x118>(sc);
	v_div_fmas_f32 v11, v11, v43, v45
	v_div_fixup_f32 v4, v11, v4, v114
	v_add_f32_e32 v4, v64, v4
	v_cmp_gt_f32_e32 vcc, s37, v4
	s_nop 1
	v_cndmask_b32_e64 v11, 0, 32, vcc
	v_ldexp_f32 v4, v4, v11
	v_log_f32_e32 v4, v4
	s_nop 0
	v_mul_f32_e32 v11, 0x3f317217, v4
	v_fma_f32 v11, v4, s33, -v11
	v_fmac_f32_e32 v11, 0x3377d1cf, v4
	v_fmac_f32_e32 v11, 0x3f317217, v4
	v_cmp_lt_f32_e64 s[44:45], |v4|, s36
	s_nop 1
	v_cndmask_b32_e64 v4, v4, v11, s[44:45]
	v_cndmask_b32_e32 v11, 0, v216, vcc
	v_sub_f32_e32 v58, v4, v11
	s_nop 0
	s_nop 1
	s_nop 0
	s_nop 1
	v_mul_f32_e32 v4, 0xbfb8aa3b, v5
	v_exp_f32_e32 v4, v4
	s_nop 0
	v_add_f32_e32 v4, 1.0, v4
	v_div_scale_f32 v5, s[2:3], v4, v4, v113
	v_rcp_f32_e32 v44, v5
	v_mov_b32_e32 v10, v58
	v_fma_f32 v45, -v5, v44, 1.0
	v_fmac_f32_e32 v44, v45, v44
	v_div_scale_f32 v45, vcc, v113, v4, v113
	v_mul_f32_e32 v46, v45, v44
	v_fma_f32 v47, -v5, v46, v45
	v_fmac_f32_e32 v46, v47, v44
	v_fma_f32 v5, -v5, v46, v45
	v_div_fmas_f32 v5, v5, v44, v46
	v_div_fixup_f32 v4, v5, v4, v113
	v_add_f32_e32 v4, v65, v4
	v_cmp_gt_f32_e32 vcc, s37, v4
	v_mov_b32_dpp v42, v10 row_shr:1 row_mask:0xf bank_mask:0xf bound_ctrl:1
	s_nop 0
	v_cndmask_b32_e64 v5, 0, 32, vcc
	v_ldexp_f32 v4, v4, v5
	v_log_f32_e32 v4, v4
	s_nop 0
	v_mul_f32_e32 v5, 0x3f317217, v4
	v_fma_f32 v5, v4, s33, -v5
	v_fmac_f32_e32 v5, 0x3377d1cf, v4
	v_fmac_f32_e32 v5, 0x3f317217, v4
	v_cmp_lt_f32_e64 s[44:45], |v4|, s36
	s_nop 1
	v_cndmask_b32_e64 v4, v4, v5, s[44:45]
	v_cndmask_b32_e32 v5, 0, v216, vcc
	v_sub_f32_e32 v59, v4, v5
	v_mov_b32_e32 v11, v59
	s_nop 1
	v_mov_b32_dpp v43, v11 row_shr:1 row_mask:0xf bank_mask:0xf bound_ctrl:1
	v_pk_add_f32 v[42:43], v[10:11], v[42:43]
	s_nop 0
	s_nop 1
	v_mul_f32_e32 v5, 0xbfb8aa3b, v6
	v_exp_f32_e32 v5, v5
	s_nop 0
	v_add_f32_e32 v5, 1.0, v5
	v_div_scale_f32 v6, s[2:3], v5, v5, v112
	v_rcp_f32_e32 v45, v6
	s_nop 0
	v_fma_f32 v46, -v6, v45, 1.0
	v_fmac_f32_e32 v45, v46, v45
	v_div_scale_f32 v46, vcc, v112, v5, v112
	v_mul_f32_e32 v47, v46, v45
	v_fma_f32 v48, -v6, v47, v46
	v_fmac_f32_e32 v47, v48, v45
	v_fma_f32 v6, -v6, v47, v46
	v_div_fmas_f32 v6, v6, v45, v47
	v_div_fixup_f32 v5, v6, v5, v112
	v_add_f32_e32 v5, v66, v5
	v_cmp_gt_f32_e32 vcc, s37, v5
	s_nop 1
	v_cndmask_b32_e64 v6, 0, 32, vcc
	v_ldexp_f32 v5, v5, v6
	v_log_f32_e32 v5, v5
	s_nop 0
	v_mul_f32_e32 v6, 0x3f317217, v5
	v_fma_f32 v6, v5, s33, -v6
	v_fmac_f32_e32 v6, 0x3377d1cf, v5
	v_fmac_f32_e32 v6, 0x3f317217, v5
	v_cmp_lt_f32_e64 s[44:45], |v5|, s36
	s_nop 1
	v_cndmask_b32_e64 v5, v5, v6, s[44:45]
	v_cndmask_b32_e32 v6, 0, v216, vcc
	v_sub_f32_e32 v60, v5, v6
	s_nop 1
	s_nop 0
	s_nop 1
	v_mul_f32_e32 v6, 0xbfb8aa3b, v7
	v_exp_f32_e32 v6, v6
	s_nop 0
	v_add_f32_e32 v6, 1.0, v6
	v_div_scale_f32 v7, s[2:3], v6, v6, v96
	v_rcp_f32_e32 v46, v7
	v_mov_b32_e32 v4, v60
	v_fma_f32 v47, -v7, v46, 1.0
	v_fmac_f32_e32 v46, v47, v46
	v_div_scale_f32 v47, vcc, v96, v6, v96
	v_mul_f32_e32 v48, v47, v46
	v_fma_f32 v49, -v7, v48, v47
	v_fmac_f32_e32 v48, v49, v46
	v_fma_f32 v7, -v7, v48, v47
	v_div_fmas_f32 v7, v7, v46, v48
	v_div_fixup_f32 v6, v7, v6, v96
	v_add_f32_e32 v6, v67, v6
	v_cmp_gt_f32_e32 vcc, s37, v6
	v_mov_b32_dpp v44, v4 row_shr:1 row_mask:0xf bank_mask:0xf bound_ctrl:1
	s_nop 0
	v_cndmask_b32_e64 v7, 0, 32, vcc
	v_ldexp_f32 v6, v6, v7
	v_log_f32_e32 v6, v6
	s_nop 0
	v_mul_f32_e32 v7, 0x3f317217, v6
	v_fma_f32 v7, v6, s33, -v7
	v_fmac_f32_e32 v7, 0x3377d1cf, v6
	v_fmac_f32_e32 v7, 0x3f317217, v6
	v_cmp_lt_f32_e64 s[44:45], |v6|, s36
	s_nop 1
	v_cndmask_b32_e64 v6, v6, v7, s[44:45]
	v_cndmask_b32_e32 v7, 0, v216, vcc
	v_sub_f32_e32 v61, v6, v7
	v_mul_f32_e32 v0, 0xbfb8aa3b, v0
	v_exp_f32_e32 v0, v0
	v_mov_b32_e32 v5, v61
	v_add_f32_e32 v0, 1.0, v0
	s_nop 0
	v_mov_b32_dpp v45, v5 row_shr:1 row_mask:0xf bank_mask:0xf bound_ctrl:1
	v_pk_add_f32 v[44:45], v[4:5], v[44:45]
	s_nop 1
	v_div_scale_f32 v7, s[2:3], v0, v0, v114
	v_rcp_f32_e32 v47, v7
	s_nop 0
	v_fma_f32 v48, -v7, v47, 1.0
	v_fmac_f32_e32 v47, v48, v47
	v_div_scale_f32 v48, vcc, v114, v0, v114
	v_mul_f32_e32 v49, v48, v47
	v_fma_f32 v62, -v7, v49, v48
	v_fmac_f32_e32 v49, v62, v47
	v_fma_f32 v7, -v7, v49, v48
	v_div_fmas_f32 v7, v7, v47, v49
	v_div_fixup_f32 v0, v7, v0, v114
	v_add_f32_e32 v0, v64, v0
	v_cmp_gt_f32_e32 vcc, s37, v0
	s_nop 1
	v_cndmask_b32_e64 v7, 0, 32, vcc
	v_ldexp_f32 v0, v0, v7
	v_log_f32_e32 v0, v0
	s_nop 0
	v_mul_f32_e32 v7, 0x3f317217, v0
	v_fma_f32 v7, v0, s33, -v7
	v_fmac_f32_e32 v7, 0x3377d1cf, v0
	v_fmac_f32_e32 v7, 0x3f317217, v0
	v_cmp_lt_f32_e64 s[44:45], |v0|, s36
	s_nop 1
	v_cndmask_b32_e64 v0, v0, v7, s[44:45]
	v_cndmask_b32_e32 v7, 0, v216, vcc
	v_sub_f32_e32 v62, v0, v7
	s_nop 0
	s_nop 1
	s_nop 0
	s_nop 1
	v_mul_f32_e32 v0, 0xbfb8aa3b, v1
	v_exp_f32_e32 v0, v0
	s_nop 0
	v_add_f32_e32 v0, 1.0, v0
	v_div_scale_f32 v1, s[2:3], v0, v0, v113
	v_rcp_f32_e32 v48, v1
	v_mov_b32_e32 v6, v62
	v_fma_f32 v49, -v1, v48, 1.0
	v_fmac_f32_e32 v48, v49, v48
	v_div_scale_f32 v49, vcc, v113, v0, v113
	v_mul_f32_e32 v63, v49, v48
	v_fma_f32 v64, -v1, v63, v49
	v_fmac_f32_e32 v63, v64, v48
	v_fma_f32 v1, -v1, v63, v49
	v_div_fmas_f32 v1, v1, v48, v63
	v_div_fixup_f32 v0, v1, v0, v113
	v_add_f32_e32 v0, v65, v0
	v_cmp_gt_f32_e32 vcc, s37, v0
	v_mov_b32_dpp v46, v6 row_shr:1 row_mask:0xf bank_mask:0xf bound_ctrl:1
	s_nop 0
	v_cndmask_b32_e64 v1, 0, 32, vcc
	v_ldexp_f32 v0, v0, v1
	v_log_f32_e32 v0, v0
	s_nop 0
	v_mul_f32_e32 v1, 0x3f317217, v0
	v_fma_f32 v1, v0, s33, -v1
	v_fmac_f32_e32 v1, 0x3377d1cf, v0
	v_fmac_f32_e32 v1, 0x3f317217, v0
	v_cmp_lt_f32_e64 s[44:45], |v0|, s36
	s_nop 1
	v_cndmask_b32_e64 v0, v0, v1, s[44:45]
	v_cndmask_b32_e32 v1, 0, v216, vcc
	v_sub_f32_e32 v63, v0, v1
; template <int CTRL> __device__ __forceinline__ float dppx(float v) { return __int_as_float(__builtin_amdgcn_update_dpp(0, __float_as_int(v), CTRL, 0xf, 0xf, true)); }
;   __device__ __forceinline__ void operator()(const f32x4 (&acc)[2][2][4][2], const pg8::Unit& u, int wr, int wc, int fr, int fq) const {
;     ...
;             for (int m = 0; m < 4; ++m)
; #pragma unroll
;               for (int q = 0; q < 4; ++q) { const float gv = log_forget(acc[ai][bj][m][qh][q], lq[q]); g[m][q] = gv;
;                 float sc = gv; sc += dppx<0x111>(sc); sc += dppx<0x112>(sc); sc += dppx<0x114>(sc); sc += dppx<0x118>(sc);
;                 const float tot16 = __int_as_float(__builtin_amdgcn_ds_swizzle(__float_as_int(sc), 0x1F0));
;                 cs[m][q] = sc + carry[q]; carry[q] += tot16; }
; #pragma unroll
;             for (int m = 0; m < 4; ++m) { const int r = row0 + ai * 128 + m * 16; float bq[4], kq[4];
; #pragma unroll
;               for (int q = 0; q < 4; ++q) { bq[q] = bwd ? (carry[q] - cs[m][q]) + g[m][q] : cs[m][q]; kq[q] = 1.f - __expf(g[m][q]); }
	v_mov_b32_e32 v7, v63
	s_nop 1
	v_mov_b32_dpp v47, v7 row_shr:1 row_mask:0xf bank_mask:0xf bound_ctrl:1
	v_pk_add_f32 v[46:47], v[6:7], v[46:47]
	s_nop 0
	s_nop 1
	v_mul_f32_e32 v1, 0xbfb8aa3b, v2
	v_exp_f32_e32 v1, v1
	s_nop 0
	v_add_f32_e32 v1, 1.0, v1
	v_div_scale_f32 v2, s[2:3], v1, v1, v112
	v_rcp_f32_e32 v49, v2
	s_nop 0
	v_fma_f32 v64, -v2, v49, 1.0
	v_fmac_f32_e32 v49, v64, v49
	v_div_scale_f32 v64, vcc, v112, v1, v112
	v_mul_f32_e32 v65, v64, v49
	v_fma_f32 v68, -v2, v65, v64
	v_fmac_f32_e32 v65, v68, v49
	v_fma_f32 v2, -v2, v65, v64
	v_div_fmas_f32 v2, v2, v49, v65
	v_div_fixup_f32 v1, v2, v1, v112
	v_add_f32_e32 v1, v66, v1
	v_cmp_gt_f32_e32 vcc, s37, v1
	s_nop 1
	v_cndmask_b32_e64 v2, 0, 32, vcc
	v_ldexp_f32 v1, v1, v2
	v_log_f32_e32 v1, v1
	s_nop 0
	v_mul_f32_e32 v2, 0x3f317217, v1
	v_fma_f32 v2, v1, s33, -v2
	v_fmac_f32_e32 v2, 0x3377d1cf, v1
	v_fmac_f32_e32 v2, 0x3f317217, v1
	v_cmp_lt_f32_e64 s[44:45], |v1|, s36
	s_nop 1
	v_cndmask_b32_e64 v1, v1, v2, s[44:45]
	v_cndmask_b32_e32 v2, 0, v216, vcc
	v_sub_f32_e32 v64, v1, v2
	s_nop 1
	s_nop 0
	s_nop 1
	v_mul_f32_e32 v2, 0xbfb8aa3b, v3
	v_exp_f32_e32 v2, v2
	s_nop 0
	v_add_f32_e32 v2, 1.0, v2
	v_div_scale_f32 v3, s[2:3], v2, v2, v96
	v_rcp_f32_e32 v65, v3
	v_mov_b32_e32 v48, v64
	v_fma_f32 v66, -v3, v65, 1.0
	v_fmac_f32_e32 v65, v66, v65
	v_div_scale_f32 v66, vcc, v96, v2, v96
	v_mul_f32_e32 v68, v66, v65
	v_fma_f32 v69, -v3, v68, v66
	v_fmac_f32_e32 v68, v69, v65
	v_fma_f32 v3, -v3, v68, v66
	v_div_fmas_f32 v3, v3, v65, v68
	v_div_fixup_f32 v2, v3, v2, v96
	v_add_f32_e32 v2, v67, v2
	v_cmp_gt_f32_e32 vcc, s37, v2
	v_mov_b32_dpp v0, v48 row_shr:1 row_mask:0xf bank_mask:0xf bound_ctrl:1
	s_nop 0
	v_cndmask_b32_e64 v3, 0, 32, vcc
	v_ldexp_f32 v2, v2, v3
	v_log_f32_e32 v2, v2
	s_nop 0
	v_mul_f32_e32 v3, 0x3f317217, v2
	v_fma_f32 v3, v2, s33, -v3
	v_fmac_f32_e32 v3, 0x3377d1cf, v2
	v_fmac_f32_e32 v3, 0x3f317217, v2
	v_cmp_lt_f32_e64 s[44:45], |v2|, s36
	s_nop 1
	v_cndmask_b32_e64 v2, v2, v3, s[44:45]
	v_cndmask_b32_e32 v3, 0, v216, vcc
	v_sub_f32_e32 v65, v2, v3
	v_mov_b32_e32 v49, v65
	v_mov_b32_e32 v3, v51
	v_mov_b32_e32 v2, v50
	v_mov_b32_dpp v1, v49 row_shr:1 row_mask:0xf bank_mask:0xf bound_ctrl:1
	v_mov_b32_dpp v33, v3 row_shr:1 row_mask:0xf bank_mask:0xf bound_ctrl:1
	v_mov_b32_dpp v32, v2 row_shr:1 row_mask:0xf bank_mask:0xf bound_ctrl:1
	v_pk_add_f32 v[32:33], v[2:3], v[32:33]
	v_pk_add_f32 v[0:1], v[48:49], v[0:1]
	s_nop 0
	v_mov_b32_dpp v34, v32 row_shr:2 row_mask:0xf bank_mask:0xf bound_ctrl:1
	v_mov_b32_dpp v35, v33 row_shr:2 row_mask:0xf bank_mask:0xf bound_ctrl:1
	v_pk_add_f32 v[32:33], v[32:33], v[34:35]
	s_nop 1
	v_mov_b32_dpp v34, v32 row_shr:4 row_mask:0xf bank_mask:0xf bound_ctrl:1
	v_mov_b32_dpp v35, v33 row_shr:4 row_mask:0xf bank_mask:0xf bound_ctrl:1
	v_pk_add_f32 v[32:33], v[32:33], v[34:35]
	s_nop 1
	v_mov_b32_dpp v34, v32 row_shr:8 row_mask:0xf bank_mask:0xf bound_ctrl:1
	v_mov_b32_dpp v35, v33 row_shr:8 row_mask:0xf bank_mask:0xf bound_ctrl:1
	v_pk_add_f32 v[32:33], v[32:33], v[34:35]
	ds_swizzle_b32 v34, v32 offset:swizzle(BROADCAST,16,15)
	ds_swizzle_b32 v35, v33 offset:swizzle(BROADCAST,16,15)
	v_pk_add_f32 v[32:33], v[32:33], 0 op_sel_hi:[1,0]
	s_waitcnt lgkmcnt(0)
	v_pk_add_f32 v[50:51], v[34:35], 0 op_sel_hi:[1,0]
	v_mul_f32_e32 v34, 0x3fb8aa3b, v2
	v_exp_f32_e32 v34, v34
	v_mov_b32_dpp v35, v13 row_shr:1 row_mask:0xf bank_mask:0xf bound_ctrl:1
	v_sub_f32_e32 v66, 1.0, v34
	v_mul_f32_e32 v34, 0x3fb8aa3b, v3
	v_exp_f32_e32 v34, v34
	s_nop 0
	v_sub_f32_e32 v67, 1.0, v34
	v_mov_b32_dpp v34, v12 row_shr:1 row_mask:0xf bank_mask:0xf bound_ctrl:1
	v_pk_add_f32 v[34:35], v[12:13], v[34:35]
	s_nop 1
	v_mov_b32_dpp v36, v34 row_shr:2 row_mask:0xf bank_mask:0xf bound_ctrl:1
	v_mov_b32_dpp v37, v35 row_shr:2 row_mask:0xf bank_mask:0xf bound_ctrl:1
	v_pk_add_f32 v[34:35], v[34:35], v[36:37]
	s_nop 1
	v_mov_b32_dpp v36, v34 row_shr:4 row_mask:0xf bank_mask:0xf bound_ctrl:1
	v_mov_b32_dpp v37, v35 row_shr:4 row_mask:0xf bank_mask:0xf bound_ctrl:1
	v_pk_add_f32 v[34:35], v[34:35], v[36:37]
	s_nop 1
	v_mov_b32_dpp v36, v34 row_shr:8 row_mask:0xf bank_mask:0xf bound_ctrl:1
	v_mov_b32_dpp v37, v35 row_shr:8 row_mask:0xf bank_mask:0xf bound_ctrl:1
	v_pk_add_f32 v[34:35], v[34:35], v[36:37]
	ds_swizzle_b32 v36, v34 offset:swizzle(BROADCAST,16,15)
	ds_swizzle_b32 v37, v35 offset:swizzle(BROADCAST,16,15)
	v_pk_add_f32 v[34:35], v[34:35], 0 op_sel_hi:[1,0]
	s_waitcnt lgkmcnt(0)
	v_pk_add_f32 v[52:53], v[36:37], 0 op_sel_hi:[1,0]
	v_mul_f32_e32 v36, 0x3fb8aa3b, v12
	v_exp_f32_e32 v36, v36
	v_mov_b32_dpp v37, v15 row_shr:1 row_mask:0xf bank_mask:0xf bound_ctrl:1
	v_sub_f32_e32 v68, 1.0, v36
	v_mul_f32_e32 v36, 0x3fb8aa3b, v13
	v_exp_f32_e32 v36, v36
	s_nop 0
	v_sub_f32_e32 v69, 1.0, v36
	v_mov_b32_dpp v36, v14 row_shr:1 row_mask:0xf bank_mask:0xf bound_ctrl:1
	v_pk_add_f32 v[36:37], v[14:15], v[36:37]
	s_nop 1
	v_mov_b32_dpp v38, v36 row_shr:2 row_mask:0xf bank_mask:0xf bound_ctrl:1
	v_mov_b32_dpp v39, v37 row_shr:2 row_mask:0xf bank_mask:0xf bound_ctrl:1
	v_pk_add_f32 v[36:37], v[36:37], v[38:39]
	s_nop 1
	v_mov_b32_dpp v38, v36 row_shr:4 row_mask:0xf bank_mask:0xf bound_ctrl:1
	v_mov_b32_dpp v39, v37 row_shr:4 row_mask:0xf bank_mask:0xf bound_ctrl:1
	v_pk_add_f32 v[36:37], v[36:37], v[38:39]
	s_nop 1
	v_mov_b32_dpp v38, v36 row_shr:8 row_mask:0xf bank_mask:0xf bound_ctrl:1
	v_mov_b32_dpp v39, v37 row_shr:8 row_mask:0xf bank_mask:0xf bound_ctrl:1
	v_pk_add_f32 v[36:37], v[36:37], v[38:39]
	ds_swizzle_b32 v38, v36 offset:swizzle(BROADCAST,16,15)
	ds_swizzle_b32 v39, v37 offset:swizzle(BROADCAST,16,15)
	v_pk_add_f32 v[36:37], v[50:51], v[36:37]
	s_waitcnt lgkmcnt(0)
; template <int CTRL> __device__ __forceinline__ float dppx(float v) { return __int_as_float(__builtin_amdgcn_update_dpp(0, __float_as_int(v), CTRL, 0xf, 0xf, true)); }
;   __device__ __forceinline__ void operator()(const f32x4 (&acc)[2][2][4][2], const pg8::Unit& u, int wr, int wc, int fr, int fq) const {
;     ...
;             for (int m = 0; m < 4; ++m)
; #pragma unroll
;               for (int q = 0; q < 4; ++q) { const float gv = log_forget(acc[ai][bj][m][qh][q], lq[q]); g[m][q] = gv;
;                 float sc = gv; sc += dppx<0x111>(sc); sc += dppx<0x112>(sc); sc += dppx<0x114>(sc); sc += dppx<0x118>(sc);
;                 const float tot16 = __int_as_float(__builtin_amdgcn_ds_swizzle(__float_as_int(sc), 0x1F0));
;                 cs[m][q] = sc + carry[q]; carry[q] += tot16; }
; #pragma unroll
;             for (int m = 0; m < 4; ++m) { const int r = row0 + ai * 128 + m * 16; float bq[4], kq[4];
; #pragma unroll
;               for (int q = 0; q < 4; ++q) { bq[q] = bwd ? (carry[q] - cs[m][q]) + g[m][q] : cs[m][q]; kq[q] = 1.f - __expf(g[m][q]); }
	v_pk_add_f32 v[50:51], v[50:51], v[38:39]
	v_mul_f32_e32 v38, 0x3fb8aa3b, v14
	v_exp_f32_e32 v38, v38
	v_mov_b32_dpp v39, v9 row_shr:1 row_mask:0xf bank_mask:0xf bound_ctrl:1
	v_sub_f32_e32 v70, 1.0, v38
	v_mul_f32_e32 v38, 0x3fb8aa3b, v15
	v_exp_f32_e32 v38, v38
	s_nop 0
	v_sub_f32_e32 v71, 1.0, v38
	v_mov_b32_dpp v38, v8 row_shr:1 row_mask:0xf bank_mask:0xf bound_ctrl:1
	v_pk_add_f32 v[38:39], v[8:9], v[38:39]
	s_nop 1
	v_mov_b32_dpp v40, v38 row_shr:2 row_mask:0xf bank_mask:0xf bound_ctrl:1
	v_mov_b32_dpp v41, v39 row_shr:2 row_mask:0xf bank_mask:0xf bound_ctrl:1
	v_pk_add_f32 v[38:39], v[38:39], v[40:41]
	s_nop 1
	v_mov_b32_dpp v40, v38 row_shr:4 row_mask:0xf bank_mask:0xf bound_ctrl:1
	v_mov_b32_dpp v41, v39 row_shr:4 row_mask:0xf bank_mask:0xf bound_ctrl:1
	v_pk_add_f32 v[38:39], v[38:39], v[40:41]
	s_nop 1
	v_mov_b32_dpp v40, v38 row_shr:8 row_mask:0xf bank_mask:0xf bound_ctrl:1
	v_mov_b32_dpp v41, v39 row_shr:8 row_mask:0xf bank_mask:0xf bound_ctrl:1
	v_pk_add_f32 v[38:39], v[38:39], v[40:41]
	ds_swizzle_b32 v40, v38 offset:swizzle(BROADCAST,16,15)
	ds_swizzle_b32 v41, v39 offset:swizzle(BROADCAST,16,15)
	v_pk_add_f32 v[38:39], v[52:53], v[38:39]
	s_waitcnt lgkmcnt(0)
	v_pk_add_f32 v[40:41], v[52:53], v[40:41]
	v_mul_f32_e32 v52, 0x3fb8aa3b, v8
	v_exp_f32_e32 v52, v52
	v_mov_b32_dpp v53, v43 row_shr:2 row_mask:0xf bank_mask:0xf bound_ctrl:1
	v_sub_f32_e32 v56, 1.0, v52
	v_mul_f32_e32 v52, 0x3fb8aa3b, v9
	v_exp_f32_e32 v52, v52
	s_nop 0
	v_sub_f32_e32 v57, 1.0, v52
	v_mov_b32_dpp v52, v42 row_shr:2 row_mask:0xf bank_mask:0xf bound_ctrl:1
	v_pk_add_f32 v[42:43], v[42:43], v[52:53]
	s_nop 1
	v_mov_b32_dpp v52, v42 row_shr:4 row_mask:0xf bank_mask:0xf bound_ctrl:1
	v_mov_b32_dpp v53, v43 row_shr:4 row_mask:0xf bank_mask:0xf bound_ctrl:1
	v_pk_add_f32 v[42:43], v[42:43], v[52:53]
	s_nop 1
	v_mov_b32_dpp v52, v42 row_shr:8 row_mask:0xf bank_mask:0xf bound_ctrl:1
	v_mov_b32_dpp v53, v43 row_shr:8 row_mask:0xf bank_mask:0xf bound_ctrl:1
	v_pk_add_f32 v[42:43], v[42:43], v[52:53]
	ds_swizzle_b32 v52, v42 offset:swizzle(BROADCAST,16,15)
	ds_swizzle_b32 v53, v43 offset:swizzle(BROADCAST,16,15)
	v_pk_add_f32 v[42:43], v[50:51], v[42:43]
	s_waitcnt lgkmcnt(0)
	v_pk_add_f32 v[50:51], v[50:51], v[52:53]
	v_mul_f32_e32 v52, 0x3fb8aa3b, v10
	v_exp_f32_e32 v52, v52
	v_mov_b32_dpp v53, v45 row_shr:2 row_mask:0xf bank_mask:0xf bound_ctrl:1
	v_sub_f32_e32 v58, 1.0, v52
	v_mul_f32_e32 v52, 0x3fb8aa3b, v11
	v_exp_f32_e32 v52, v52
	s_nop 0
	v_sub_f32_e32 v59, 1.0, v52
	v_mov_b32_dpp v52, v44 row_shr:2 row_mask:0xf bank_mask:0xf bound_ctrl:1
	v_pk_add_f32 v[44:45], v[44:45], v[52:53]
	s_nop 1
	v_mov_b32_dpp v52, v44 row_shr:4 row_mask:0xf bank_mask:0xf bound_ctrl:1
	v_mov_b32_dpp v53, v45 row_shr:4 row_mask:0xf bank_mask:0xf bound_ctrl:1
	v_pk_add_f32 v[44:45], v[44:45], v[52:53]
	s_nop 1
	v_mov_b32_dpp v52, v44 row_shr:8 row_mask:0xf bank_mask:0xf bound_ctrl:1
	v_mov_b32_dpp v53, v45 row_shr:8 row_mask:0xf bank_mask:0xf bound_ctrl:1
	v_pk_add_f32 v[44:45], v[44:45], v[52:53]
	ds_swizzle_b32 v52, v44 offset:swizzle(BROADCAST,16,15)
	ds_swizzle_b32 v53, v45 offset:swizzle(BROADCAST,16,15)
	v_pk_add_f32 v[44:45], v[40:41], v[44:45]
	s_waitcnt lgkmcnt(0)
	v_pk_add_f32 v[40:41], v[40:41], v[52:53]
	v_mul_f32_e32 v52, 0x3fb8aa3b, v4
	v_exp_f32_e32 v52, v52
	v_mov_b32_dpp v53, v47 row_shr:2 row_mask:0xf bank_mask:0xf bound_ctrl:1
	v_sub_f32_e32 v60, 1.0, v52
	v_mul_f32_e32 v52, 0x3fb8aa3b, v5
	v_exp_f32_e32 v52, v52
	s_nop 0
	v_sub_f32_e32 v61, 1.0, v52
	v_mov_b32_dpp v52, v46 row_shr:2 row_mask:0xf bank_mask:0xf bound_ctrl:1
	v_pk_add_f32 v[46:47], v[46:47], v[52:53]
	s_nop 1
	v_mov_b32_dpp v52, v46 row_shr:4 row_mask:0xf bank_mask:0xf bound_ctrl:1
	v_mov_b32_dpp v53, v47 row_shr:4 row_mask:0xf bank_mask:0xf bound_ctrl:1
	v_pk_add_f32 v[46:47], v[46:47], v[52:53]
	s_nop 1
	v_mov_b32_dpp v52, v46 row_shr:8 row_mask:0xf bank_mask:0xf bound_ctrl:1
	v_mov_b32_dpp v53, v47 row_shr:8 row_mask:0xf bank_mask:0xf bound_ctrl:1
	v_pk_add_f32 v[46:47], v[46:47], v[52:53]
	ds_swizzle_b32 v52, v46 offset:swizzle(BROADCAST,16,15)
	ds_swizzle_b32 v53, v47 offset:swizzle(BROADCAST,16,15)
	v_pk_add_f32 v[46:47], v[50:51], v[46:47]
	s_waitcnt lgkmcnt(0)
	v_pk_add_f32 v[50:51], v[50:51], v[52:53]
	v_mul_f32_e32 v52, 0x3fb8aa3b, v6
	v_exp_f32_e32 v52, v52
	v_mov_b32_dpp v53, v1 row_shr:2 row_mask:0xf bank_mask:0xf bound_ctrl:1
	v_sub_f32_e32 v62, 1.0, v52
	v_mul_f32_e32 v52, 0x3fb8aa3b, v7
	v_exp_f32_e32 v52, v52
	s_nop 0
	v_sub_f32_e32 v63, 1.0, v52
	v_mov_b32_dpp v52, v0 row_shr:2 row_mask:0xf bank_mask:0xf bound_ctrl:1
	v_pk_add_f32 v[0:1], v[0:1], v[52:53]
	s_nop 1
	v_mov_b32_dpp v52, v0 row_shr:4 row_mask:0xf bank_mask:0xf bound_ctrl:1
	v_mov_b32_dpp v53, v1 row_shr:4 row_mask:0xf bank_mask:0xf bound_ctrl:1
	v_pk_add_f32 v[0:1], v[0:1], v[52:53]
	s_nop 1
	v_mov_b32_dpp v52, v0 row_shr:8 row_mask:0xf bank_mask:0xf bound_ctrl:1
	v_mov_b32_dpp v53, v1 row_shr:8 row_mask:0xf bank_mask:0xf bound_ctrl:1
	v_pk_add_f32 v[0:1], v[0:1], v[52:53]
	ds_swizzle_b32 v52, v0 offset:swizzle(BROADCAST,16,15)
	ds_swizzle_b32 v53, v1 offset:swizzle(BROADCAST,16,15)
	v_pk_add_f32 v[54:55], v[40:41], v[0:1]
	v_pk_add_f32 v[0:1], v[50:51], v[32:33] neg_lo:[0,1] neg_hi:[0,1]
	s_waitcnt lgkmcnt(0)
; __device__ __forceinline__ unsigned cvt_pk_bf16(float lo, float hi) { unsigned r; asm volatile("v_cvt_pk_bf16_f32 %0, %1, %2" : "=v"(r) : "v"(lo), "v"(hi)); return r; }
; __device__ __forceinline__ float log_forget(float z, float lb) {
;   const float r0 = fminf(z, 0.f) - __logf(1.f + __expf(-fabsf(z)));
;   const float r1 = __logf(lb + (1.f - lb) / (1.f + __expf(-z)));
;   return lb <= 0.f ? r0 : r1;
; }
;   __device__ __forceinline__ void operator()(const f32x4 (&acc)[2][2][4][2], const pg8::Unit& u, int wr, int wc, int fr, int fq) const {
;     ...
;             for (int m = 0; m < 4; ++m) { const int r = row0 + ai * 128 + m * 16; float bq[4], kq[4];
; #pragma unroll
;               for (int q = 0; q < 4; ++q) { bq[q] = bwd ? (carry[q] - cs[m][q]) + g[m][q] : cs[m][q]; kq[q] = 1.f - __expf(g[m][q]); }
;               *(f32x4*)(logfp + (size_t)r * 1024 + c + 4 * qh) = (f32x4){bq[0], bq[1], bq[2], bq[3]};
;               u32x2 w; w.x = pg8::cvt_pk_bf16(kq[0], kq[1]); w.y = pg8::cvt_pk_bf16(kq[2], kq[3]);
;               *(u32x2*)(km + (size_t)r * 1024 + c + 4 * qh) = w; } } }
	v_pk_add_f32 v[40:41], v[40:41], v[52:53]
	s_nop 0
	v_pk_add_f32 v[52:53], v[40:41], v[34:35] neg_lo:[0,1] neg_hi:[0,1]
	v_pk_add_f32 v[0:1], v[2:3], v[0:1]
	v_pk_add_f32 v[2:3], v[12:13], v[52:53]
	v_cndmask_b32_e64 v1, v33, v1, s[42:43]
	v_cndmask_b32_e64 v3, v35, v3, s[42:43]
	v_cndmask_b32_e64 v2, v34, v2, s[42:43]
	v_cndmask_b32_e64 v0, v32, v0, s[42:43]
	global_store_dwordx4 v[18:19], v[0:3], off offset:16
	s_nop 1
	v_cvt_pk_bf16_f32 v0, v66, v67
	v_cvt_pk_bf16_f32 v1, v68, v69
	global_store_dwordx2 v[16:17], v[0:1], off offset:8
	v_pk_add_f32 v[0:1], v[50:51], v[36:37] neg_lo:[0,1] neg_hi:[0,1]
	v_pk_add_f32 v[2:3], v[40:41], v[38:39] neg_lo:[0,1] neg_hi:[0,1]
	v_pk_add_f32 v[0:1], v[14:15], v[0:1]
	v_pk_add_f32 v[2:3], v[8:9], v[2:3]
	v_cndmask_b32_e64 v1, v37, v1, s[42:43]
	v_cndmask_b32_e64 v3, v39, v3, s[42:43]
	v_cndmask_b32_e64 v2, v38, v2, s[42:43]
	v_cndmask_b32_e64 v0, v36, v0, s[42:43]
	global_store_dwordx4 v[22:23], v[0:3], off offset:16
	s_nop 1
	v_cvt_pk_bf16_f32 v0, v70, v71
	v_cvt_pk_bf16_f32 v1, v56, v57
	global_store_dwordx2 v[20:21], v[0:1], off offset:8
	v_pk_add_f32 v[0:1], v[50:51], v[42:43] neg_lo:[0,1] neg_hi:[0,1]
	v_pk_add_f32 v[2:3], v[40:41], v[44:45] neg_lo:[0,1] neg_hi:[0,1]
	v_pk_add_f32 v[0:1], v[10:11], v[0:1]
	v_pk_add_f32 v[2:3], v[4:5], v[2:3]
	v_cndmask_b32_e64 v1, v43, v1, s[42:43]
	v_cndmask_b32_e64 v3, v45, v3, s[42:43]
	v_cndmask_b32_e64 v2, v44, v2, s[42:43]
	v_cndmask_b32_e64 v0, v42, v0, s[42:43]
	global_store_dwordx4 v[26:27], v[0:3], off offset:16
	v_mul_f32_e32 v5, 0x3fb8aa3b, v49
	v_exp_f32_e32 v5, v5
	v_cvt_pk_bf16_f32 v0, v58, v59
	v_cvt_pk_bf16_f32 v1, v60, v61
	global_store_dwordx2 v[24:25], v[0:1], off offset:8
	v_mul_f32_e32 v0, 0x3fb8aa3b, v48
	v_exp_f32_e32 v0, v0
	v_pk_add_f32 v[2:3], v[40:41], v[54:55] neg_lo:[0,1] neg_hi:[0,1]
	v_sub_f32_e32 v5, 1.0, v5
	v_pk_add_f32 v[2:3], v[48:49], v[2:3]
	v_sub_f32_e32 v4, 1.0, v0
	v_pk_add_f32 v[0:1], v[50:51], v[46:47] neg_lo:[0,1] neg_hi:[0,1]
	v_cndmask_b32_e64 v3, v55, v3, s[42:43]
	v_pk_add_f32 v[0:1], v[6:7], v[0:1]
	v_cndmask_b32_e64 v2, v54, v2, s[42:43]
	v_cndmask_b32_e64 v1, v47, v1, s[42:43]
	v_cndmask_b32_e64 v0, v46, v0, s[42:43]
	global_store_dwordx4 v[28:29], v[0:3], off offset:16
	s_nop 1
	v_cvt_pk_bf16_f32 v0, v62, v63
	v_cvt_pk_bf16_f32 v1, v4, v5
	global_store_dwordx2 v[30:31], v[0:1], off offset:8
	s_and_b64 vcc, exec, s[40:41]
	s_mov_b64 s[6:7], -1
	s_cbranch_vccnz .LBB0_189
	s_branch .LBB0_203
.Lep1_A:
	s_nop 0
	v_and_b32_e32 v72, 0x178, v154
	v_lshlrev_b32_e32 v155, 2, v72
	global_load_dwordx4 v[72:75], v155, s[66:67] offset:16
	global_load_dwordx4 v[92:95], v155, s[66:67]
	v_max_f32_e32 v157, v134, v134
	v_min_f32_e32 v166, 0, v157
	v_mul_f32_e64 v157, |v134|, s8
	v_exp_f32_e32 v157, v157
	s_cmp_gt_u32 s2, 5
	v_add_f32_e32 v157, 1.0, v157
	v_cmp_gt_f32_e32 vcc, s37, v157
	v_add_u32_e32 v96, 0xfffffc00, v154
	s_nop 0
	v_cndmask_b32_e64 v159, 0, 32, vcc
	v_ldexp_f32 v157, v157, v159
	v_log_f32_e32 v157, v157
	s_cselect_b64 s[42:43], -1, 0
	v_mul_f32_e32 v159, 0x3f317217, v157
	v_fma_f32 v159, v157, s33, -v159
	v_fmac_f32_e32 v159, 0x3377d1cf, v157
	v_fmac_f32_e32 v159, 0x3f317217, v157
	v_cmp_lt_f32_e64 s[44:45], |v157|, s36
	s_waitcnt vmcnt(0)
	s_nop 0
	v_cndmask_b32_e64 v157, v157, v159, s[44:45]
	v_cndmask_b32_e32 v159, 0, v216, vcc
	v_sub_f32_e32 v174, v157, v159
	s_nop 0
	s_nop 1
	v_max_f32_e32 v134, v135, v135
	v_min_f32_e32 v167, 0, v134
	v_mul_f32_e64 v134, |v135|, s8
	v_exp_f32_e32 v134, v134
	s_nop 0
	v_add_f32_e32 v134, 1.0, v134
	v_cmp_gt_f32_e32 vcc, s37, v134
	s_nop 1
	v_cndmask_b32_e64 v159, 0, 32, vcc
	v_ldexp_f32 v134, v134, v159
	v_log_f32_e32 v134, v134
	s_nop 0
	v_mul_f32_e32 v159, 0x3f317217, v134
	v_fma_f32 v159, v134, s33, -v159
	v_fmac_f32_e32 v159, 0x3377d1cf, v134
	v_fmac_f32_e32 v159, 0x3f317217, v134
	v_cmp_lt_f32_e64 s[44:45], |v134|, s36
	s_nop 1
	v_cndmask_b32_e64 v134, v134, v159, s[44:45]
	v_cndmask_b32_e32 v159, 0, v216, vcc
	v_sub_f32_e32 v175, v134, v159
	s_nop 0
	s_nop 1
	s_nop 0
	s_nop 1
	v_mul_f32_e64 v135, |v136|, s8
	v_exp_f32_e32 v135, v135
	v_max_f32_e32 v134, v136, v136
	v_min_f32_e32 v134, 0, v134
	v_add_f32_e32 v135, 1.0, v135
	v_cmp_gt_f32_e32 vcc, s37, v135
	s_nop 1
	v_cndmask_b32_e64 v161, 0, 32, vcc
	v_ldexp_f32 v135, v135, v161
	v_log_f32_e32 v135, v135
	s_nop 0
	v_mul_f32_e32 v161, 0x3f317217, v135
	v_fma_f32 v161, v135, s33, -v161
	v_fmac_f32_e32 v161, 0x3377d1cf, v135
	v_fmac_f32_e32 v161, 0x3f317217, v135
	v_cmp_lt_f32_e64 s[44:45], |v135|, s36
	s_nop 1
	v_cndmask_b32_e64 v135, v135, v161, s[44:45]
	v_cndmask_b32_e32 v161, 0, v216, vcc
	v_sub_f32_e32 v176, v135, v161
	s_nop 0
	s_nop 1
	s_nop 0
	s_nop 1
	v_mul_f32_e64 v136, |v137|, s8
	v_exp_f32_e32 v136, v136
	v_max_f32_e32 v135, v137, v137
	v_min_f32_e32 v135, 0, v135
	v_add_f32_e32 v136, 1.0, v136
	v_cmp_gt_f32_e32 vcc, s37, v136
	s_nop 1
	v_cndmask_b32_e64 v163, 0, 32, vcc
	v_ldexp_f32 v136, v136, v163
	v_log_f32_e32 v136, v136
	s_nop 0
	v_mul_f32_e32 v163, 0x3f317217, v136
	v_fma_f32 v163, v136, s33, -v163
	v_fmac_f32_e32 v163, 0x3377d1cf, v136
	v_fmac_f32_e32 v163, 0x3f317217, v136
	v_cmp_lt_f32_e64 s[44:45], |v136|, s36
	s_nop 1
	v_cndmask_b32_e64 v136, v136, v163, s[44:45]
	v_cndmask_b32_e32 v163, 0, v216, vcc
	v_sub_f32_e32 v177, v136, v163
	s_nop 0
	s_nop 1
	s_nop 0
	s_nop 1
	v_mul_f32_e64 v137, |v130|, s8
	v_exp_f32_e32 v137, v137
	v_max_f32_e32 v136, v130, v130
	v_add_f32_e32 v137, 1.0, v137
	v_cmp_gt_f32_e32 vcc, s37, v137
	v_min_f32_e32 v136, 0, v136
	s_nop 0
	v_cndmask_b32_e64 v180, 0, 32, vcc
	v_ldexp_f32 v137, v137, v180
	v_log_f32_e32 v137, v137
	s_nop 0
	v_mul_f32_e32 v180, 0x3f317217, v137
; template <int CTRL> __device__ __forceinline__ float dppx(float v) { return __int_as_float(__builtin_amdgcn_update_dpp(0, __float_as_int(v), CTRL, 0xf, 0xf, true)); }
; __device__ __forceinline__ float log_forget(float z, float lb) {
;   const float r0 = fminf(z, 0.f) - __logf(1.f + __expf(-fabsf(z)));
;   __device__ __forceinline__ void operator()(const f32x4 (&acc)[2][2][4][2], const pg8::Unit& u, int wr, int wc, int fr, int fq) const {
;     ...
;               for (int q = 0; q < 4; ++q) { const float gv = log_forget(acc[ai][bj][m][qh][q], lq[q]); g[m][q] = gv;
;                 float sc = gv; sc += dppx<0x111>(sc); sc += dppx<0x112>(sc); sc += dppx<0x114>(sc); sc += dppx<0x118>(sc);
	v_fma_f32 v180, v137, s33, -v180
	v_fmac_f32_e32 v180, 0x3377d1cf, v137
	v_fmac_f32_e32 v180, 0x3f317217, v137
	v_cmp_lt_f32_e64 s[44:45], |v137|, s36
	s_nop 1
	v_cndmask_b32_e64 v137, v137, v180, s[44:45]
	v_cndmask_b32_e32 v180, 0, v216, vcc
	v_sub_f32_e32 v180, v137, v180
	s_nop 0
	s_nop 1
	s_nop 0
	s_nop 1
	v_max_f32_e32 v130, v131, v131
	v_min_f32_e32 v137, 0, v130
	v_mul_f32_e64 v130, |v131|, s8
	v_exp_f32_e32 v130, v130
	s_nop 0
	v_add_f32_e32 v130, 1.0, v130
	v_cmp_gt_f32_e32 vcc, s37, v130
	s_nop 1
	v_cndmask_b32_e64 v181, 0, 32, vcc
	v_ldexp_f32 v130, v130, v181
	v_log_f32_e32 v130, v130
	s_nop 0
	v_mul_f32_e32 v181, 0x3f317217, v130
	v_fma_f32 v181, v130, s33, -v181
	v_fmac_f32_e32 v181, 0x3377d1cf, v130
	v_fmac_f32_e32 v181, 0x3f317217, v130
	v_cmp_lt_f32_e64 s[44:45], |v130|, s36
	s_nop 1
	v_cndmask_b32_e64 v130, v130, v181, s[44:45]
	v_cndmask_b32_e32 v181, 0, v216, vcc
	v_sub_f32_e32 v181, v130, v181
	v_pk_add_f32 v[136:137], v[136:137], v[180:181] neg_lo:[0,1] neg_hi:[0,1]
	s_nop 0
	s_nop 1
	s_nop 0
	s_nop 1
	v_mul_f32_e64 v131, |v132|, s8
	v_exp_f32_e32 v131, v131
	v_max_f32_e32 v130, v132, v132
	v_mov_b32_e32 v137, v137
	v_min_f32_e32 v130, 0, v130
	v_add_f32_e32 v131, 1.0, v131
	v_cmp_gt_f32_e32 vcc, s37, v131
	v_mov_b32_dpp v181, v137 row_shr:1 row_mask:0xf bank_mask:0xf bound_ctrl:1
	s_nop 0
	v_cndmask_b32_e64 v182, 0, 32, vcc
	v_ldexp_f32 v131, v131, v182
	v_log_f32_e32 v131, v131
	s_nop 0
	v_mul_f32_e32 v182, 0x3f317217, v131
	v_fma_f32 v182, v131, s33, -v182
	v_fmac_f32_e32 v182, 0x3377d1cf, v131
	v_fmac_f32_e32 v182, 0x3f317217, v131
	v_cmp_lt_f32_e64 s[44:45], |v131|, s36
	s_nop 1
	v_cndmask_b32_e64 v131, v131, v182, s[44:45]
	v_cndmask_b32_e32 v182, 0, v216, vcc
	v_sub_f32_e32 v182, v131, v182
	s_nop 0
	s_nop 0
	s_nop 1
	s_nop 0
	s_nop 1
	v_mul_f32_e64 v132, |v133|, s8
	v_exp_f32_e32 v132, v132
	v_max_f32_e32 v131, v133, v133
	v_min_f32_e32 v131, 0, v131
	v_add_f32_e32 v132, 1.0, v132
	v_cmp_gt_f32_e32 vcc, s37, v132
	s_nop 1
	v_cndmask_b32_e64 v183, 0, 32, vcc
	v_ldexp_f32 v132, v132, v183
	v_log_f32_e32 v132, v132
	s_nop 0
	v_mul_f32_e32 v183, 0x3f317217, v132
	v_fma_f32 v183, v132, s33, -v183
	v_fmac_f32_e32 v183, 0x3377d1cf, v132
	v_fmac_f32_e32 v183, 0x3f317217, v132
	v_cmp_lt_f32_e64 s[44:45], |v132|, s36
	s_nop 1
	v_cndmask_b32_e64 v132, v132, v183, s[44:45]
	v_cndmask_b32_e32 v183, 0, v216, vcc
	v_sub_f32_e32 v183, v132, v183
	s_nop 0
	s_nop 0
	s_nop 1
	s_nop 0
	s_nop 1
	v_mul_f32_e64 v133, |v126|, s8
	v_exp_f32_e32 v133, v133
	v_max_f32_e32 v132, v126, v126
	v_add_f32_e32 v133, 1.0, v133
	v_cmp_gt_f32_e32 vcc, s37, v133
	v_min_f32_e32 v132, 0, v132
	s_nop 0
	v_cndmask_b32_e64 v184, 0, 32, vcc
	v_ldexp_f32 v133, v133, v184
	v_log_f32_e32 v133, v133
	s_nop 0
	v_mul_f32_e32 v184, 0x3f317217, v133
	v_fma_f32 v184, v133, s33, -v184
	v_fmac_f32_e32 v184, 0x3377d1cf, v133
	v_fmac_f32_e32 v184, 0x3f317217, v133
	v_cmp_lt_f32_e64 s[44:45], |v133|, s36
	s_nop 1
	v_cndmask_b32_e64 v133, v133, v184, s[44:45]
	v_cndmask_b32_e32 v184, 0, v216, vcc
	v_sub_f32_e32 v184, v133, v184
	s_nop 0
	s_nop 1
	s_nop 0
	s_nop 1
	v_max_f32_e32 v126, v127, v127
	v_min_f32_e32 v133, 0, v126
	v_mul_f32_e64 v126, |v127|, s8
	v_exp_f32_e32 v126, v126
	s_nop 0
	v_add_f32_e32 v126, 1.0, v126
	v_cmp_gt_f32_e32 vcc, s37, v126
	s_nop 1
	v_cndmask_b32_e64 v185, 0, 32, vcc
	v_ldexp_f32 v126, v126, v185
	v_log_f32_e32 v126, v126
	s_nop 0
	v_mul_f32_e32 v185, 0x3f317217, v126
	v_fma_f32 v185, v126, s33, -v185
	v_fmac_f32_e32 v185, 0x3377d1cf, v126
	v_fmac_f32_e32 v185, 0x3f317217, v126
	v_cmp_lt_f32_e64 s[44:45], |v126|, s36
	s_nop 1
	v_cndmask_b32_e64 v126, v126, v185, s[44:45]
	v_cndmask_b32_e32 v185, 0, v216, vcc
	v_sub_f32_e32 v185, v126, v185
	v_pk_add_f32 v[132:133], v[132:133], v[184:185] neg_lo:[0,1] neg_hi:[0,1]
	s_nop 0
	s_nop 1
	s_nop 0
	s_nop 1
	v_max_f32_e32 v126, v128, v128
	v_min_f32_e32 v186, 0, v126
	v_mul_f32_e64 v126, |v128|, s8
	v_exp_f32_e32 v126, v126
	v_mov_b32_e32 v185, v133
	v_add_f32_e32 v126, 1.0, v126
	v_cmp_gt_f32_e32 vcc, s37, v126
	v_mov_b32_dpp v133, v185 row_shr:1 row_mask:0xf bank_mask:0xf bound_ctrl:1
	s_nop 0
	v_cndmask_b32_e64 v127, 0, 32, vcc
	v_ldexp_f32 v126, v126, v127
	v_log_f32_e32 v126, v126
	s_nop 0
	v_mul_f32_e32 v127, 0x3f317217, v126
	v_fma_f32 v127, v126, s33, -v127
	v_fmac_f32_e32 v127, 0x3377d1cf, v126
	v_fmac_f32_e32 v127, 0x3f317217, v126
	v_cmp_lt_f32_e64 s[44:45], |v126|, s36
	s_nop 1
	v_cndmask_b32_e64 v126, v126, v127, s[44:45]
	v_cndmask_b32_e32 v127, 0, v216, vcc
	v_sub_f32_e32 v188, v126, v127
	s_nop 0
	s_nop 0
	s_nop 1
	s_nop 0
	s_nop 1
	v_max_f32_e32 v126, v129, v129
	v_min_f32_e32 v187, 0, v126
	v_mul_f32_e64 v126, |v129|, s8
	v_exp_f32_e32 v126, v126
	s_nop 0
	v_add_f32_e32 v126, 1.0, v126
	v_cmp_gt_f32_e32 vcc, s37, v126
	s_nop 1
	v_cndmask_b32_e64 v127, 0, 32, vcc
	v_ldexp_f32 v126, v126, v127
	v_log_f32_e32 v126, v126
	s_nop 0
	v_mul_f32_e32 v127, 0x3f317217, v126
	v_fma_f32 v127, v126, s33, -v127
	v_fmac_f32_e32 v127, 0x3377d1cf, v126
	v_fmac_f32_e32 v127, 0x3f317217, v126
	v_cmp_lt_f32_e64 s[44:45], |v126|, s36
	s_nop 1
	v_cndmask_b32_e64 v126, v126, v127, s[44:45]
	v_cndmask_b32_e32 v127, 0, v216, vcc
	v_sub_f32_e32 v189, v126, v127
	s_nop 0
	s_nop 0
	s_nop 1
	s_nop 0
	s_nop 1
	v_max_f32_e32 v126, v122, v122
	v_min_f32_e32 v190, 0, v126
	v_mul_f32_e64 v126, |v122|, s8
	v_exp_f32_e32 v126, v126
	s_nop 0
	v_add_f32_e32 v126, 1.0, v126
	v_cmp_gt_f32_e32 vcc, s37, v126
	s_nop 0
	s_nop 0
	v_cndmask_b32_e64 v127, 0, 32, vcc
	v_ldexp_f32 v126, v126, v127
	v_log_f32_e32 v126, v126
	s_nop 0
	v_mul_f32_e32 v127, 0x3f317217, v126
	v_fma_f32 v127, v126, s33, -v127
; template <int CTRL> __device__ __forceinline__ float dppx(float v) { return __int_as_float(__builtin_amdgcn_update_dpp(0, __float_as_int(v), CTRL, 0xf, 0xf, true)); }
; __device__ __forceinline__ float log_forget(float z, float lb) {
;   const float r0 = fminf(z, 0.f) - __logf(1.f + __expf(-fabsf(z)));
;   __device__ __forceinline__ void operator()(const f32x4 (&acc)[2][2][4][2], const pg8::Unit& u, int wr, int wc, int fr, int fq) const {
;     ...
;             for (int m = 0; m < 4; ++m)
; #pragma unroll
;               for (int q = 0; q < 4; ++q) { const float gv = log_forget(acc[ai][bj][m][qh][q], lq[q]); g[m][q] = gv;
;                 float sc = gv; sc += dppx<0x111>(sc); sc += dppx<0x112>(sc); sc += dppx<0x114>(sc); sc += dppx<0x118>(sc);
;                 const float tot16 = __int_as_float(__builtin_amdgcn_ds_swizzle(__float_as_int(sc), 0x1F0));
;                 cs[m][q] = sc + carry[q]; carry[q] += tot16; }
; #pragma unroll
;             for (int m = 0; m < 4; ++m) { const int r = row0 + ai * 128 + m * 16; float bq[4], kq[4];
; #pragma unroll
;               for (int q = 0; q < 4; ++q) { bq[q] = bwd ? (carry[q] - cs[m][q]) + g[m][q] : cs[m][q]; kq[q] = 1.f - __expf(g[m][q]); }
	v_fmac_f32_e32 v127, 0x3377d1cf, v126
	v_fmac_f32_e32 v127, 0x3f317217, v126
	v_cmp_lt_f32_e64 s[44:45], |v126|, s36
	s_nop 1
	v_cndmask_b32_e64 v126, v126, v127, s[44:45]
	v_cndmask_b32_e32 v127, 0, v216, vcc
	v_sub_f32_e32 v192, v126, v127
	s_nop 0
	s_nop 1
	s_nop 0
	s_nop 1
	v_max_f32_e32 v122, v123, v123
	v_min_f32_e32 v191, 0, v122
	v_mul_f32_e64 v122, |v123|, s8
	v_exp_f32_e32 v122, v122
	s_nop 0
	v_add_f32_e32 v122, 1.0, v122
	v_cmp_gt_f32_e32 vcc, s37, v122
	s_nop 1
	v_cndmask_b32_e64 v126, 0, 32, vcc
	v_ldexp_f32 v122, v122, v126
	v_log_f32_e32 v122, v122
	s_nop 0
	v_mul_f32_e32 v126, 0x3f317217, v122
	v_fma_f32 v126, v122, s33, -v126
	v_fmac_f32_e32 v126, 0x3377d1cf, v122
	v_fmac_f32_e32 v126, 0x3f317217, v122
	v_cmp_lt_f32_e64 s[44:45], |v122|, s36
	s_nop 1
	v_cndmask_b32_e64 v122, v122, v126, s[44:45]
	v_cndmask_b32_e32 v126, 0, v216, vcc
	v_sub_f32_e32 v193, v122, v126
	s_nop 0
	s_nop 0
	s_nop 1
	s_nop 0
	s_nop 1
	v_max_f32_e32 v122, v124, v124
	v_min_f32_e32 v194, 0, v122
	v_mul_f32_e64 v122, |v124|, s8
	v_exp_f32_e32 v122, v122
	s_nop 0
	v_add_f32_e32 v122, 1.0, v122
	v_cmp_gt_f32_e32 vcc, s37, v122
	s_nop 1
	v_cndmask_b32_e64 v123, 0, 32, vcc
	v_ldexp_f32 v122, v122, v123
	v_log_f32_e32 v122, v122
	s_nop 0
	v_mul_f32_e32 v123, 0x3f317217, v122
	v_fma_f32 v123, v122, s33, -v123
	v_fmac_f32_e32 v123, 0x3377d1cf, v122
	v_fmac_f32_e32 v123, 0x3f317217, v122
	v_cmp_lt_f32_e64 s[44:45], |v122|, s36
	s_nop 1
	v_cndmask_b32_e64 v122, v122, v123, s[44:45]
	v_cndmask_b32_e32 v123, 0, v216, vcc
	v_sub_f32_e32 v196, v122, v123
	s_nop 0
	s_nop 0
	s_nop 1
	s_nop 0
	s_nop 1
	v_max_f32_e32 v122, v125, v125
	v_min_f32_e32 v195, 0, v122
	v_mul_f32_e64 v122, |v125|, s8
	v_exp_f32_e32 v122, v122
	s_nop 0
	v_add_f32_e32 v122, 1.0, v122
	v_cmp_gt_f32_e32 vcc, s37, v122
	s_nop 1
	v_cndmask_b32_e64 v123, 0, 32, vcc
	v_ldexp_f32 v122, v122, v123
	v_log_f32_e32 v122, v122
	s_nop 0
	v_mul_f32_e32 v123, 0x3f317217, v122
	v_fma_f32 v123, v122, s33, -v123
	v_fmac_f32_e32 v123, 0x3377d1cf, v122
	v_fmac_f32_e32 v123, 0x3f317217, v122
	v_cmp_lt_f32_e64 s[44:45], |v122|, s36
	s_nop 1
	v_cndmask_b32_e64 v122, v122, v123, s[44:45]
	v_cndmask_b32_e32 v123, 0, v216, vcc
	v_sub_f32_e32 v197, v122, v123
	s_nop 0
	s_nop 0
	s_nop 1
	s_nop 0
	s_nop 1
	v_pk_add_f32 v[122:123], v[166:167], v[174:175] neg_lo:[0,1] neg_hi:[0,1]
	v_mov_b32_e32 v199, v123
	v_lshlrev_b64 v[166:167], 2, v[96:97]
	v_mov_b32_e32 v198, v122
	v_mov_b32_dpp v123, v199 row_shr:1 row_mask:0xf bank_mask:0xf bound_ctrl:1
	v_mov_b32_e32 v136, v136
	v_mov_b32_dpp v122, v198 row_shr:1 row_mask:0xf bank_mask:0xf bound_ctrl:1
	v_pk_add_f32 v[122:123], v[198:199], v[122:123]
	v_mov_b32_dpp v180, v136 row_shr:1 row_mask:0xf bank_mask:0xf bound_ctrl:1
	v_pk_add_f32 v[180:181], v[136:137], v[180:181]
	v_mov_b32_dpp v124, v122 row_shr:2 row_mask:0xf bank_mask:0xf bound_ctrl:1
	v_mov_b32_dpp v125, v123 row_shr:2 row_mask:0xf bank_mask:0xf bound_ctrl:1
	v_pk_add_f32 v[122:123], v[122:123], v[124:125]
	v_mov_b32_dpp v204, v180 row_shr:2 row_mask:0xf bank_mask:0xf bound_ctrl:1
	v_mov_b32_dpp v205, v181 row_shr:2 row_mask:0xf bank_mask:0xf bound_ctrl:1
	v_mov_b32_dpp v124, v122 row_shr:4 row_mask:0xf bank_mask:0xf bound_ctrl:1
	v_mov_b32_dpp v125, v123 row_shr:4 row_mask:0xf bank_mask:0xf bound_ctrl:1
	v_pk_add_f32 v[180:181], v[180:181], v[204:205]
	v_pk_add_f32 v[122:123], v[122:123], v[124:125]
	v_mov_b32_e32 v184, v132
	v_mov_b32_dpp v204, v180 row_shr:4 row_mask:0xf bank_mask:0xf bound_ctrl:1
	v_mov_b32_dpp v205, v181 row_shr:4 row_mask:0xf bank_mask:0xf bound_ctrl:1
	v_mov_b32_dpp v124, v122 row_shr:8 row_mask:0xf bank_mask:0xf bound_ctrl:1
	v_mov_b32_dpp v125, v123 row_shr:8 row_mask:0xf bank_mask:0xf bound_ctrl:1
	v_pk_add_f32 v[180:181], v[180:181], v[204:205]
	v_pk_add_f32 v[122:123], v[122:123], v[124:125]
	ds_swizzle_b32 v124, v122 offset:swizzle(BROADCAST,16,15)
	v_mov_b32_dpp v204, v180 row_shr:8 row_mask:0xf bank_mask:0xf bound_ctrl:1
	v_mov_b32_dpp v205, v181 row_shr:8 row_mask:0xf bank_mask:0xf bound_ctrl:1
	ds_swizzle_b32 v125, v123 offset:swizzle(BROADCAST,16,15)
	v_pk_add_f32 v[180:181], v[180:181], v[204:205]
	ds_swizzle_b32 v208, v180 offset:swizzle(BROADCAST,16,15)
	ds_swizzle_b32 v209, v181 offset:swizzle(BROADCAST,16,15)
	v_mov_b32_dpp v132, v184 row_shr:1 row_mask:0xf bank_mask:0xf bound_ctrl:1
	s_waitcnt lgkmcnt(2)
	v_pk_add_f32 v[126:127], v[124:125], 0 op_sel_hi:[1,0]
	v_pk_add_f32 v[132:133], v[184:185], v[132:133]
	v_pk_add_f32 v[204:205], v[126:127], v[180:181]
	s_waitcnt lgkmcnt(0)
	v_pk_add_f32 v[212:213], v[126:127], v[208:209]
	v_mul_f32_e32 v126, 0x3fb8aa3b, v137
	v_exp_f32_e32 v126, v126
	v_pk_add_f32 v[200:201], v[122:123], 0 op_sel_hi:[1,0]
	v_mul_f32_e32 v122, 0x3fb8aa3b, v198
	v_exp_f32_e32 v122, v122
	v_sub_f32_e32 v235, 1.0, v126
	v_pk_add_f32 v[126:127], v[130:131], v[182:183] neg_lo:[0,1] neg_hi:[0,1]
	v_mov_b32_dpp v182, v132 row_shr:2 row_mask:0xf bank_mask:0xf bound_ctrl:1
	v_mov_b32_dpp v183, v133 row_shr:2 row_mask:0xf bank_mask:0xf bound_ctrl:1
	v_pk_add_f32 v[132:133], v[132:133], v[182:183]
	v_sub_f32_e32 v169, 1.0, v122
	v_mul_f32_e32 v122, 0x3fb8aa3b, v199
	v_mov_b32_dpp v182, v132 row_shr:4 row_mask:0xf bank_mask:0xf bound_ctrl:1
	v_mov_b32_dpp v183, v133 row_shr:4 row_mask:0xf bank_mask:0xf bound_ctrl:1
	v_pk_add_f32 v[132:133], v[132:133], v[182:183]
	v_exp_f32_e32 v122, v122
	v_mov_b32_e32 v207, v127
	v_mov_b32_dpp v182, v132 row_shr:8 row_mask:0xf bank_mask:0xf bound_ctrl:1
	v_mov_b32_dpp v183, v133 row_shr:8 row_mask:0xf bank_mask:0xf bound_ctrl:1
	v_pk_add_f32 v[132:133], v[132:133], v[182:183]
	ds_swizzle_b32 v182, v132 offset:swizzle(BROADCAST,16,15)
	v_pk_add_f32 v[210:211], v[212:213], v[132:133]
	v_mul_f32_e32 v132, 0x3fb8aa3b, v184
	v_exp_f32_e32 v132, v132
	ds_swizzle_b32 v183, v133 offset:swizzle(BROADCAST,16,15)
	v_sub_f32_e32 v232, 1.0, v122
	v_pk_add_f32 v[122:123], v[134:135], v[176:177] neg_lo:[0,1] neg_hi:[0,1]
	v_sub_f32_e32 v238, 1.0, v132
	v_mul_f32_e32 v132, 0x3fb8aa3b, v185
	v_exp_f32_e32 v132, v132
	s_waitcnt lgkmcnt(0)
; template <int CTRL> __device__ __forceinline__ float dppx(float v) { return __int_as_float(__builtin_amdgcn_update_dpp(0, __float_as_int(v), CTRL, 0xf, 0xf, true)); }
;   __device__ __forceinline__ void operator()(const f32x4 (&acc)[2][2][4][2], const pg8::Unit& u, int wr, int wc, int fr, int fq) const {
;     ...
;             for (int m = 0; m < 4; ++m)
; #pragma unroll
;               for (int q = 0; q < 4; ++q) { const float gv = log_forget(acc[ai][bj][m][qh][q], lq[q]); g[m][q] = gv;
;                 float sc = gv; sc += dppx<0x111>(sc); sc += dppx<0x112>(sc); sc += dppx<0x114>(sc); sc += dppx<0x118>(sc);
;                 const float tot16 = __int_as_float(__builtin_amdgcn_ds_swizzle(__float_as_int(sc), 0x1F0));
;                 cs[m][q] = sc + carry[q]; carry[q] += tot16; }
; #pragma unroll
;             for (int m = 0; m < 4; ++m) { const int r = row0 + ai * 128 + m * 16; float bq[4], kq[4];
; #pragma unroll
;               for (int q = 0; q < 4; ++q) { bq[q] = bwd ? (carry[q] - cs[m][q]) + g[m][q] : cs[m][q]; kq[q] = 1.f - __expf(g[m][q]); }
	v_pk_add_f32 v[212:213], v[212:213], v[182:183]
	v_mov_b32_e32 v135, v123
	v_mov_b32_e32 v134, v122
	v_sub_f32_e32 v239, 1.0, v132
	v_pk_add_f32 v[132:133], v[186:187], v[188:189] neg_lo:[0,1] neg_hi:[0,1]
	v_pk_add_f32 v[188:189], v[190:191], v[192:193] neg_lo:[0,1] neg_hi:[0,1]
	v_mov_b32_dpp v122, v134 row_shr:1 row_mask:0xf bank_mask:0xf bound_ctrl:1
	v_mov_b32_e32 v191, v189
	v_mov_b32_e32 v190, v188
	v_mov_b32_dpp v123, v135 row_shr:1 row_mask:0xf bank_mask:0xf bound_ctrl:1
	v_mov_b32_dpp v189, v191 row_shr:1 row_mask:0xf bank_mask:0xf bound_ctrl:1
	v_mov_b32_dpp v188, v190 row_shr:1 row_mask:0xf bank_mask:0xf bound_ctrl:1
	v_pk_add_f32 v[188:189], v[190:191], v[188:189]
	v_pk_add_f32 v[122:123], v[134:135], v[122:123]
	v_mov_b32_e32 v206, v126
	v_mov_b32_dpp v192, v188 row_shr:2 row_mask:0xf bank_mask:0xf bound_ctrl:1
	v_mov_b32_dpp v193, v189 row_shr:2 row_mask:0xf bank_mask:0xf bound_ctrl:1
	v_pk_add_f32 v[188:189], v[188:189], v[192:193]
	v_mov_b32_dpp v124, v122 row_shr:2 row_mask:0xf bank_mask:0xf bound_ctrl:1
	v_mov_b32_dpp v125, v123 row_shr:2 row_mask:0xf bank_mask:0xf bound_ctrl:1
	v_mov_b32_dpp v192, v188 row_shr:4 row_mask:0xf bank_mask:0xf bound_ctrl:1
	v_mov_b32_dpp v193, v189 row_shr:4 row_mask:0xf bank_mask:0xf bound_ctrl:1
	v_pk_add_f32 v[188:189], v[188:189], v[192:193]
	v_pk_add_f32 v[122:123], v[122:123], v[124:125]
	v_mov_b32_dpp v126, v206 row_shr:1 row_mask:0xf bank_mask:0xf bound_ctrl:1
	v_mov_b32_dpp v192, v188 row_shr:8 row_mask:0xf bank_mask:0xf bound_ctrl:1
	v_mov_b32_dpp v193, v189 row_shr:8 row_mask:0xf bank_mask:0xf bound_ctrl:1
	v_pk_add_f32 v[188:189], v[188:189], v[192:193]
	ds_swizzle_b32 v192, v188 offset:swizzle(BROADCAST,16,15)
	v_pk_add_f32 v[228:229], v[212:213], v[188:189]
	v_mul_f32_e32 v188, 0x3fb8aa3b, v190
	v_exp_f32_e32 v188, v188
	v_mov_b32_dpp v124, v122 row_shr:4 row_mask:0xf bank_mask:0xf bound_ctrl:1
	v_mov_b32_dpp v125, v123 row_shr:4 row_mask:0xf bank_mask:0xf bound_ctrl:1
	v_mov_b32_dpp v127, v207 row_shr:1 row_mask:0xf bank_mask:0xf bound_ctrl:1
	v_sub_f32_e32 v242, 1.0, v188
	v_mul_f32_e32 v188, 0x3fb8aa3b, v191
	v_exp_f32_e32 v188, v188
	v_mov_b32_e32 v215, v133
	v_mov_b32_e32 v214, v132
	ds_swizzle_b32 v193, v189 offset:swizzle(BROADCAST,16,15)
	v_sub_f32_e32 v243, 1.0, v188
	v_pk_add_f32 v[188:189], v[194:195], v[196:197] neg_lo:[0,1] neg_hi:[0,1]
	v_pk_add_f32 v[122:123], v[122:123], v[124:125]
	v_pk_add_f32 v[126:127], v[206:207], v[126:127]
	v_mov_b32_dpp v132, v214 row_shr:1 row_mask:0xf bank_mask:0xf bound_ctrl:1
	v_mov_b32_dpp v133, v215 row_shr:1 row_mask:0xf bank_mask:0xf bound_ctrl:1
	v_mov_b32_e32 v195, v189
	v_mov_b32_e32 v194, v188
	v_mov_b32_dpp v124, v122 row_shr:8 row_mask:0xf bank_mask:0xf bound_ctrl:1
	v_mov_b32_dpp v125, v123 row_shr:8 row_mask:0xf bank_mask:0xf bound_ctrl:1
	v_mov_b32_dpp v130, v126 row_shr:2 row_mask:0xf bank_mask:0xf bound_ctrl:1
	v_mov_b32_dpp v131, v127 row_shr:2 row_mask:0xf bank_mask:0xf bound_ctrl:1
	v_pk_add_f32 v[132:133], v[214:215], v[132:133]
	v_mov_b32_dpp v188, v194 row_shr:1 row_mask:0xf bank_mask:0xf bound_ctrl:1
	v_mov_b32_dpp v189, v195 row_shr:1 row_mask:0xf bank_mask:0xf bound_ctrl:1
	v_pk_add_f32 v[122:123], v[122:123], v[124:125]
	v_pk_add_f32 v[126:127], v[126:127], v[130:131]
	v_mov_b32_dpp v182, v132 row_shr:2 row_mask:0xf bank_mask:0xf bound_ctrl:1
	v_mov_b32_dpp v183, v133 row_shr:2 row_mask:0xf bank_mask:0xf bound_ctrl:1
	v_pk_add_f32 v[188:189], v[194:195], v[188:189]
	ds_swizzle_b32 v124, v122 offset:swizzle(BROADCAST,16,15)
	ds_swizzle_b32 v125, v123 offset:swizzle(BROADCAST,16,15)
	v_mov_b32_dpp v130, v126 row_shr:4 row_mask:0xf bank_mask:0xf bound_ctrl:1
	v_mov_b32_dpp v131, v127 row_shr:4 row_mask:0xf bank_mask:0xf bound_ctrl:1
	v_pk_add_f32 v[132:133], v[132:133], v[182:183]
	v_mov_b32_dpp v196, v188 row_shr:2 row_mask:0xf bank_mask:0xf bound_ctrl:1
	v_mov_b32_dpp v197, v189 row_shr:2 row_mask:0xf bank_mask:0xf bound_ctrl:1
	v_pk_add_f32 v[126:127], v[126:127], v[130:131]
	v_mov_b32_dpp v182, v132 row_shr:4 row_mask:0xf bank_mask:0xf bound_ctrl:1
	v_mov_b32_dpp v183, v133 row_shr:4 row_mask:0xf bank_mask:0xf bound_ctrl:1
	v_pk_add_f32 v[188:189], v[188:189], v[196:197]
	v_pk_add_f32 v[202:203], v[122:123], 0 op_sel_hi:[1,0]
	v_mul_f32_e32 v122, 0x3fb8aa3b, v134
	v_mov_b32_dpp v130, v126 row_shr:8 row_mask:0xf bank_mask:0xf bound_ctrl:1
	v_mov_b32_dpp v131, v127 row_shr:8 row_mask:0xf bank_mask:0xf bound_ctrl:1
	v_pk_add_f32 v[132:133], v[132:133], v[182:183]
	v_mov_b32_dpp v196, v188 row_shr:4 row_mask:0xf bank_mask:0xf bound_ctrl:1
	v_mov_b32_dpp v197, v189 row_shr:4 row_mask:0xf bank_mask:0xf bound_ctrl:1
	v_exp_f32_e32 v122, v122
	v_pk_add_f32 v[126:127], v[126:127], v[130:131]
	v_mov_b32_dpp v182, v132 row_shr:8 row_mask:0xf bank_mask:0xf bound_ctrl:1
	v_mov_b32_dpp v183, v133 row_shr:8 row_mask:0xf bank_mask:0xf bound_ctrl:1
	v_pk_add_f32 v[188:189], v[188:189], v[196:197]
	ds_swizzle_b32 v130, v126 offset:swizzle(BROADCAST,16,15)
	ds_swizzle_b32 v131, v127 offset:swizzle(BROADCAST,16,15)
	v_pk_add_f32 v[132:133], v[132:133], v[182:183]
	v_mov_b32_dpp v196, v188 row_shr:8 row_mask:0xf bank_mask:0xf bound_ctrl:1
	v_mov_b32_dpp v197, v189 row_shr:8 row_mask:0xf bank_mask:0xf bound_ctrl:1
	s_waitcnt lgkmcnt(2)
	v_pk_add_f32 v[128:129], v[124:125], 0 op_sel_hi:[1,0]
	ds_swizzle_b32 v182, v132 offset:swizzle(BROADCAST,16,15)
	ds_swizzle_b32 v183, v133 offset:swizzle(BROADCAST,16,15)
	v_pk_add_f32 v[188:189], v[188:189], v[196:197]
	v_pk_add_f32 v[208:209], v[128:129], v[126:127]
	v_mul_f32_e32 v126, 0x3fb8aa3b, v206
	ds_swizzle_b32 v196, v188 offset:swizzle(BROADCAST,16,15)
	ds_swizzle_b32 v197, v189 offset:swizzle(BROADCAST,16,15)
	v_sub_f32_e32 v233, 1.0, v122
	v_mul_f32_e32 v122, 0x3fb8aa3b, v135
	v_exp_f32_e32 v126, v126
	v_exp_f32_e32 v122, v122
	s_waitcnt lgkmcnt(4)
; __device__ __forceinline__ unsigned cvt_pk_bf16(float lo, float hi) { unsigned r; asm volatile("v_cvt_pk_bf16_f32 %0, %1, %2" : "=v"(r) : "v"(lo), "v"(hi)); return r; }
; __device__ __forceinline__ float log_forget(float z, float lb) {
;   const float r0 = fminf(z, 0.f) - __logf(1.f + __expf(-fabsf(z)));
;   __device__ __forceinline__ void operator()(const f32x4 (&acc)[2][2][4][2], const pg8::Unit& u, int wr, int wc, int fr, int fq) const {
;     ...
;             for (int m = 0; m < 4; ++m) { const int r = row0 + ai * 128 + m * 16; float bq[4], kq[4];
; #pragma unroll
;               for (int q = 0; q < 4; ++q) { bq[q] = bwd ? (carry[q] - cs[m][q]) + g[m][q] : cs[m][q]; kq[q] = 1.f - __expf(g[m][q]); }
;               *(f32x4*)(logfp + (size_t)r * 1024 + c + 4 * qh) = (f32x4){bq[0], bq[1], bq[2], bq[3]};
;               u32x2 w; w.x = pg8::cvt_pk_bf16(kq[0], kq[1]); w.y = pg8::cvt_pk_bf16(kq[2], kq[3]);
;               *(u32x2*)(km + (size_t)r * 1024 + c + 4 * qh) = w; } } }
	v_pk_add_f32 v[130:131], v[128:129], v[130:131]
	v_ashrrev_i32_e32 v165, 31, v164
	v_pk_add_f32 v[226:227], v[130:131], v[132:133]
	s_waitcnt lgkmcnt(2)
	v_pk_add_f32 v[186:187], v[130:131], v[182:183]
	v_mul_f32_e32 v130, 0x3fb8aa3b, v214
	v_sub_f32_e32 v236, 1.0, v126
	v_mul_f32_e32 v126, 0x3fb8aa3b, v207
	v_exp_f32_e32 v130, v130
	v_pk_add_f32 v[192:193], v[212:213], v[192:193]
	s_waitcnt lgkmcnt(0)
	v_pk_add_f32 v[196:197], v[186:187], v[196:197]
	v_sub_f32_e32 v234, 1.0, v122
	v_lshlrev_b64 v[122:123], 12, v[164:165]
	v_exp_f32_e32 v126, v126
	v_pk_add_f32 v[212:213], v[186:187], v[188:189]
	v_pk_add_f32 v[186:187], v[192:193], v[200:201] neg_lo:[0,1] neg_hi:[0,1]
	v_pk_add_f32 v[188:189], v[196:197], v[202:203] neg_lo:[0,1] neg_hi:[0,1]
	v_lshl_add_u64 v[122:123], s[22:23], 0, v[122:123]
	v_lshlrev_b64 v[124:125], 11, v[164:165]
	v_pk_add_f32 v[186:187], v[198:199], v[186:187]
	v_pk_add_f32 v[134:135], v[134:135], v[188:189]
	v_lshl_add_u64 v[176:177], v[122:123], 0, v[166:167]
	v_lshl_add_u64 v[124:125], s[0:1], 0, v[124:125]
	v_lshlrev_b64 v[164:165], 1, v[96:97]
	v_mul_f32_e32 v96, 0x3fb8aa3b, v136
	v_cndmask_b32_e64 v189, v203, v135, s[42:43]
	v_cndmask_b32_e64 v188, v202, v134, s[42:43]
	v_cndmask_b32_e64 v187, v201, v187, s[42:43]
	v_cndmask_b32_e64 v186, v200, v186, s[42:43]
	v_lshl_add_u64 v[174:175], v[124:125], 0, v[164:165]
	v_exp_f32_e32 v96, v96
	v_ashrrev_i32_e32 v173, 31, v172
	v_sub_f32_e32 v240, 1.0, v130
	v_mul_f32_e32 v130, 0x3fb8aa3b, v215
	global_store_dwordx4 v[176:177], v[186:189], off
	v_cvt_pk_bf16_f32 v134, v169, v232
	v_cvt_pk_bf16_f32 v135, v233, v234
	v_sub_f32_e32 v237, 1.0, v126
	v_lshlrev_b64 v[126:127], 12, v[172:173]
	v_exp_f32_e32 v130, v130
	global_store_dwordx2 v[174:175], v[134:135], off
	v_pk_add_f32 v[134:135], v[192:193], v[204:205] neg_lo:[0,1] neg_hi:[0,1]
	v_pk_add_f32 v[186:187], v[196:197], v[208:209] neg_lo:[0,1] neg_hi:[0,1]
	v_lshl_add_u64 v[126:127], s[22:23], 0, v[126:127]
	v_lshlrev_b64 v[128:129], 11, v[172:173]
	v_pk_add_f32 v[134:135], v[136:137], v[134:135]
	v_pk_add_f32 v[136:137], v[206:207], v[186:187]
	v_lshl_add_u64 v[180:181], v[126:127], 0, v[166:167]
	v_lshl_add_u64 v[128:129], s[0:1], 0, v[128:129]
	v_cndmask_b32_e64 v137, v209, v137, s[42:43]
	v_cndmask_b32_e64 v136, v208, v136, s[42:43]
	v_cndmask_b32_e64 v135, v205, v135, s[42:43]
	v_cndmask_b32_e64 v134, v204, v134, s[42:43]
	v_sub_f32_e32 v96, 1.0, v96
	v_lshl_add_u64 v[172:173], v[128:129], 0, v[164:165]
	v_ashrrev_i32_e32 v171, 31, v170
	global_store_dwordx4 v[180:181], v[134:137], off
	v_sub_f32_e32 v241, 1.0, v130
	v_lshlrev_b64 v[130:131], 12, v[170:171]
	v_cvt_pk_bf16_f32 v134, v96, v235
	v_cvt_pk_bf16_f32 v135, v236, v237
	global_store_dwordx2 v[172:173], v[134:135], off
	v_pk_add_f32 v[134:135], v[192:193], v[210:211] neg_lo:[0,1] neg_hi:[0,1]
	v_pk_add_f32 v[136:137], v[196:197], v[226:227] neg_lo:[0,1] neg_hi:[0,1]
	v_lshl_add_u64 v[130:131], s[22:23], 0, v[130:131]
	v_lshlrev_b64 v[132:133], 11, v[170:171]
	v_pk_add_f32 v[134:135], v[184:185], v[134:135]
	v_pk_add_f32 v[136:137], v[214:215], v[136:137]
	v_lshl_add_u64 v[182:183], v[130:131], 0, v[166:167]
	v_lshl_add_u64 v[132:133], s[0:1], 0, v[132:133]
	v_cndmask_b32_e64 v137, v227, v137, s[42:43]
	v_cndmask_b32_e64 v136, v226, v136, s[42:43]
	v_cndmask_b32_e64 v135, v211, v135, s[42:43]
	v_cndmask_b32_e64 v134, v210, v134, s[42:43]
	v_lshl_add_u64 v[170:171], v[132:133], 0, v[164:165]
	global_store_dwordx4 v[182:183], v[134:137], off
	v_mul_f32_e32 v96, 0x3fb8aa3b, v194
	v_exp_f32_e32 v96, v96
	v_cvt_pk_bf16_f32 v134, v238, v239
	v_cvt_pk_bf16_f32 v135, v240, v241
	global_store_dwordx2 v[170:171], v[134:135], off
	v_pk_add_f32 v[134:135], v[192:193], v[228:229] neg_lo:[0,1] neg_hi:[0,1]
	v_pk_add_f32 v[136:137], v[196:197], v[212:213] neg_lo:[0,1] neg_hi:[0,1]
	v_pk_add_f32 v[134:135], v[190:191], v[134:135]
	v_pk_add_f32 v[136:137], v[194:195], v[136:137]
	v_cndmask_b32_e64 v186, v228, v134, s[42:43]
	v_mul_f32_e32 v134, 0x3fb8aa3b, v195
	v_exp_f32_e32 v134, v134
	v_ashrrev_i32_e32 v169, 31, v168
	v_cndmask_b32_e64 v188, v212, v136, s[42:43]
	v_cndmask_b32_e64 v187, v229, v135, s[42:43]
	v_sub_f32_e32 v136, 1.0, v134
	v_lshlrev_b64 v[134:135], 12, v[168:169]
	v_lshl_add_u64 v[134:135], s[22:23], 0, v[134:135]
	v_cndmask_b32_e64 v189, v213, v137, s[42:43]
	v_lshl_add_u64 v[184:185], v[134:135], 0, v[166:167]
	v_sub_f32_e32 v96, 1.0, v96
	global_store_dwordx4 v[184:185], v[186:189], off
	s_nop 1
	v_cvt_pk_bf16_f32 v186, v242, v243
	v_cvt_pk_bf16_f32 v187, v96, v136
	v_lshlrev_b64 v[136:137], 11, v[168:169]
	v_lshl_add_u64 v[136:137], s[0:1], 0, v[136:137]
	v_lshl_add_u64 v[168:169], v[136:137], 0, v[164:165]
	v_max_f32_e32 v96, v118, v118
	global_store_dwordx2 v[168:169], v[186:187], off
	v_min_f32_e32 v186, 0, v96
	v_mul_f32_e64 v96, |v118|, s8
	v_exp_f32_e32 v96, v96
	s_nop 0
	v_add_f32_e32 v96, 1.0, v96
	v_cmp_gt_f32_e32 vcc, s37, v96
	s_nop 1
	v_cndmask_b32_e64 v187, 0, 32, vcc
	v_ldexp_f32 v96, v96, v187
	v_log_f32_e32 v96, v96
	s_nop 0
	v_mul_f32_e32 v187, 0x3f317217, v96
	v_fma_f32 v187, v96, s33, -v187
	v_fmac_f32_e32 v187, 0x3377d1cf, v96
	v_fmac_f32_e32 v187, 0x3f317217, v96
	v_cmp_lt_f32_e64 s[52:53], |v96|, s36
	s_nop 1
	v_cndmask_b32_e64 v96, v96, v187, s[52:53]
	v_cndmask_b32_e32 v187, 0, v216, vcc
	v_sub_f32_e32 v188, v96, v187
	s_nop 0
	s_nop 0
	s_nop 1
	s_nop 0
	s_nop 1
	v_max_f32_e32 v96, v119, v119
	v_min_f32_e32 v187, 0, v96
	v_mul_f32_e64 v96, |v119|, s8
	v_exp_f32_e32 v96, v96
	s_nop 0
	v_add_f32_e32 v96, 1.0, v96
	v_cmp_gt_f32_e32 vcc, s37, v96
	s_nop 1
	v_cndmask_b32_e64 v118, 0, 32, vcc
	v_ldexp_f32 v96, v96, v118
; __device__ __forceinline__ float log_forget(float z, float lb) {
;   const float r0 = fminf(z, 0.f) - __logf(1.f + __expf(-fabsf(z)));
;   __device__ __forceinline__ void operator()(const f32x4 (&acc)[2][2][4][2], const pg8::Unit& u, int wr, int wc, int fr, int fq) const {
;     ...
;               for (int q = 0; q < 4; ++q) { const float gv = log_forget(acc[ai][bj][m][qh][q], lq[q]); g[m][q] = gv;
	v_log_f32_e32 v96, v96
	s_nop 0
	v_mul_f32_e32 v118, 0x3f317217, v96
	v_fma_f32 v118, v96, s33, -v118
	v_fmac_f32_e32 v118, 0x3377d1cf, v96
	v_fmac_f32_e32 v118, 0x3f317217, v96
	v_cmp_lt_f32_e64 s[52:53], |v96|, s36
	s_nop 1
	v_cndmask_b32_e64 v96, v96, v118, s[52:53]
	v_cndmask_b32_e32 v118, 0, v216, vcc
	v_sub_f32_e32 v189, v96, v118
	s_nop 0
	s_nop 0
	s_nop 1
	s_nop 0
	s_nop 1
	v_max_f32_e32 v96, v120, v120
	v_min_f32_e32 v118, 0, v96
	v_mul_f32_e64 v96, |v120|, s8
	v_exp_f32_e32 v96, v96
	s_nop 0
	v_add_f32_e32 v96, 1.0, v96
	v_cmp_gt_f32_e32 vcc, s37, v96
	s_nop 1
	v_cndmask_b32_e64 v119, 0, 32, vcc
	v_ldexp_f32 v96, v96, v119
	v_log_f32_e32 v96, v96
	s_nop 0
	v_mul_f32_e32 v119, 0x3f317217, v96
	v_fma_f32 v119, v96, s33, -v119
	v_fmac_f32_e32 v119, 0x3377d1cf, v96
	v_fmac_f32_e32 v119, 0x3f317217, v96
	v_cmp_lt_f32_e64 s[52:53], |v96|, s36
	s_nop 1
	v_cndmask_b32_e64 v96, v96, v119, s[52:53]
	v_cndmask_b32_e32 v119, 0, v216, vcc
	v_sub_f32_e32 v190, v96, v119
	s_nop 0
	s_nop 0
	s_nop 1
	s_nop 0
	s_nop 1
	v_max_f32_e32 v96, v121, v121
	v_min_f32_e32 v119, 0, v96
	v_mul_f32_e64 v96, |v121|, s8
	v_exp_f32_e32 v96, v96
	s_nop 0
	v_add_f32_e32 v96, 1.0, v96
	v_cmp_gt_f32_e32 vcc, s37, v96
	s_nop 1
	v_cndmask_b32_e64 v120, 0, 32, vcc
	v_ldexp_f32 v96, v96, v120
	v_log_f32_e32 v96, v96
	s_nop 0
	v_mul_f32_e32 v120, 0x3f317217, v96
	v_fma_f32 v120, v96, s33, -v120
	v_fmac_f32_e32 v120, 0x3377d1cf, v96
	v_fmac_f32_e32 v120, 0x3f317217, v96
	v_cmp_lt_f32_e64 s[52:53], |v96|, s36
	s_nop 1
	v_cndmask_b32_e64 v96, v96, v120, s[52:53]
	v_cndmask_b32_e32 v120, 0, v216, vcc
	v_sub_f32_e32 v191, v96, v120
	v_pk_add_f32 v[118:119], v[118:119], v[190:191] neg_lo:[0,1] neg_hi:[0,1]
	v_mov_b32_e32 v118, v118
	s_nop 1
	s_nop 0
	s_nop 1
	v_mul_f32_e64 v121, |v114|, s8
	v_exp_f32_e32 v121, v121
	v_max_f32_e32 v120, v114, v114
	v_add_f32_e32 v121, 1.0, v121
	v_cmp_gt_f32_e32 vcc, s37, v121
	v_mov_b32_e32 v119, v119
	s_nop 0
	v_cndmask_b32_e64 v192, 0, 32, vcc
	v_ldexp_f32 v121, v121, v192
	v_log_f32_e32 v121, v121
	v_min_f32_e32 v120, 0, v120
	v_mul_f32_e32 v192, 0x3f317217, v121
	v_fma_f32 v192, v121, s33, -v192
	v_fmac_f32_e32 v192, 0x3377d1cf, v121
	v_fmac_f32_e32 v192, 0x3f317217, v121
	v_cmp_lt_f32_e64 s[52:53], |v121|, s36
	s_nop 1
	v_cndmask_b32_e64 v121, v121, v192, s[52:53]
	v_cndmask_b32_e32 v192, 0, v216, vcc
	v_sub_f32_e32 v192, v121, v192
	s_nop 0
	s_nop 1
	s_nop 0
	s_nop 1
	v_max_f32_e32 v114, v115, v115
	v_min_f32_e32 v121, 0, v114
	v_mul_f32_e64 v114, |v115|, s8
	v_exp_f32_e32 v114, v114
	s_nop 0
	v_add_f32_e32 v114, 1.0, v114
	v_cmp_gt_f32_e32 vcc, s37, v114
	s_nop 1
	v_cndmask_b32_e64 v193, 0, 32, vcc
	v_ldexp_f32 v114, v114, v193
	v_log_f32_e32 v114, v114
	s_nop 0
	v_mul_f32_e32 v193, 0x3f317217, v114
	v_fma_f32 v193, v114, s33, -v193
	v_fmac_f32_e32 v193, 0x3377d1cf, v114
	v_fmac_f32_e32 v193, 0x3f317217, v114
	v_cmp_lt_f32_e64 s[52:53], |v114|, s36
	s_nop 1
	v_cndmask_b32_e64 v114, v114, v193, s[52:53]
	v_cndmask_b32_e32 v193, 0, v216, vcc
	v_sub_f32_e32 v193, v114, v193
	v_pk_add_f32 v[120:121], v[120:121], v[192:193] neg_lo:[0,1] neg_hi:[0,1]
	s_nop 0
	s_nop 1
	s_nop 0
	s_nop 1
	v_mul_f32_e64 v115, |v116|, s8
	v_exp_f32_e32 v115, v115
	v_max_f32_e32 v114, v116, v116
	v_mov_b32_e32 v121, v121
	v_min_f32_e32 v114, 0, v114
	v_add_f32_e32 v115, 1.0, v115
	v_cmp_gt_f32_e32 vcc, s37, v115
	s_nop 1
	v_cndmask_b32_e64 v194, 0, 32, vcc
	v_ldexp_f32 v115, v115, v194
	v_log_f32_e32 v115, v115
	s_nop 0
	v_mul_f32_e32 v194, 0x3f317217, v115
	v_fma_f32 v194, v115, s33, -v194
	v_fmac_f32_e32 v194, 0x3377d1cf, v115
	v_fmac_f32_e32 v194, 0x3f317217, v115
	v_cmp_lt_f32_e64 s[52:53], |v115|, s36
	s_nop 1
	v_cndmask_b32_e64 v115, v115, v194, s[52:53]
	v_cndmask_b32_e32 v194, 0, v216, vcc
	v_sub_f32_e32 v194, v115, v194
	s_nop 0
	s_nop 0
	s_nop 1
	s_nop 0
	s_nop 1
	v_mul_f32_e64 v116, |v117|, s8
	v_exp_f32_e32 v116, v116
	v_max_f32_e32 v115, v117, v117
	v_min_f32_e32 v115, 0, v115
	v_add_f32_e32 v116, 1.0, v116
	v_cmp_gt_f32_e32 vcc, s37, v116
	s_nop 1
	v_cndmask_b32_e64 v195, 0, 32, vcc
	v_ldexp_f32 v116, v116, v195
	v_log_f32_e32 v116, v116
	s_nop 0
	v_mul_f32_e32 v195, 0x3f317217, v116
	v_fma_f32 v195, v116, s33, -v195
	v_fmac_f32_e32 v195, 0x3377d1cf, v116
	v_fmac_f32_e32 v195, 0x3f317217, v116
	v_cmp_lt_f32_e64 s[52:53], |v116|, s36
	s_nop 1
	v_cndmask_b32_e64 v116, v116, v195, s[52:53]
	v_cndmask_b32_e32 v195, 0, v216, vcc
	v_sub_f32_e32 v195, v116, v195
	v_pk_add_f32 v[114:115], v[114:115], v[194:195] neg_lo:[0,1] neg_hi:[0,1]
	v_mov_b32_e32 v114, v114
	s_nop 1
	s_nop 0
	s_nop 1
	v_mul_f32_e64 v117, |v110|, s8
	v_exp_f32_e32 v117, v117
	v_max_f32_e32 v116, v110, v110
	v_add_f32_e32 v117, 1.0, v117
	v_cmp_gt_f32_e32 vcc, s37, v117
	v_mov_b32_e32 v115, v115
	s_nop 0
	v_cndmask_b32_e64 v196, 0, 32, vcc
	v_ldexp_f32 v117, v117, v196
	v_log_f32_e32 v117, v117
	v_min_f32_e32 v116, 0, v116
	v_mul_f32_e32 v196, 0x3f317217, v117
	v_fma_f32 v196, v117, s33, -v196
	v_fmac_f32_e32 v196, 0x3377d1cf, v117
	v_fmac_f32_e32 v196, 0x3f317217, v117
	v_cmp_lt_f32_e64 s[52:53], |v117|, s36
	s_nop 1
	v_cndmask_b32_e64 v117, v117, v196, s[52:53]
	v_cndmask_b32_e32 v196, 0, v216, vcc
	v_sub_f32_e32 v196, v117, v196
	s_nop 0
	s_nop 1
	s_nop 0
	s_nop 1
	v_max_f32_e32 v110, v111, v111
	v_min_f32_e32 v117, 0, v110
	v_mul_f32_e64 v110, |v111|, s8
	v_exp_f32_e32 v110, v110
	s_nop 0
	v_add_f32_e32 v110, 1.0, v110
	v_cmp_gt_f32_e32 vcc, s37, v110
	s_nop 1
	v_cndmask_b32_e64 v197, 0, 32, vcc
	v_ldexp_f32 v110, v110, v197
	v_log_f32_e32 v110, v110
	s_nop 0
	v_mul_f32_e32 v197, 0x3f317217, v110
	v_fma_f32 v197, v110, s33, -v197
	v_fmac_f32_e32 v197, 0x3377d1cf, v110
; template <int CTRL> __device__ __forceinline__ float dppx(float v) { return __int_as_float(__builtin_amdgcn_update_dpp(0, __float_as_int(v), CTRL, 0xf, 0xf, true)); }
; __device__ __forceinline__ float log_forget(float z, float lb) {
;   const float r0 = fminf(z, 0.f) - __logf(1.f + __expf(-fabsf(z)));
;   __device__ __forceinline__ void operator()(const f32x4 (&acc)[2][2][4][2], const pg8::Unit& u, int wr, int wc, int fr, int fq) const {
;     ...
;             for (int m = 0; m < 4; ++m)
; #pragma unroll
;               for (int q = 0; q < 4; ++q) { const float gv = log_forget(acc[ai][bj][m][qh][q], lq[q]); g[m][q] = gv;
;                 float sc = gv; sc += dppx<0x111>(sc); sc += dppx<0x112>(sc); sc += dppx<0x114>(sc); sc += dppx<0x118>(sc);
;                 const float tot16 = __int_as_float(__builtin_amdgcn_ds_swizzle(__float_as_int(sc), 0x1F0));
	v_fmac_f32_e32 v197, 0x3f317217, v110
	v_cmp_lt_f32_e64 s[52:53], |v110|, s36
	s_nop 1
	v_cndmask_b32_e64 v110, v110, v197, s[52:53]
	v_cndmask_b32_e32 v197, 0, v216, vcc
	v_sub_f32_e32 v197, v110, v197
	v_pk_add_f32 v[116:117], v[116:117], v[196:197] neg_lo:[0,1] neg_hi:[0,1]
	s_nop 0
	s_nop 1
	s_nop 0
	s_nop 1
	v_mul_f32_e64 v111, |v112|, s8
	v_exp_f32_e32 v111, v111
	v_max_f32_e32 v110, v112, v112
	v_mov_b32_e32 v117, v117
	v_min_f32_e32 v110, 0, v110
	v_add_f32_e32 v111, 1.0, v111
	v_cmp_gt_f32_e32 vcc, s37, v111
	v_mov_b32_dpp v197, v117 row_shr:1 row_mask:0xf bank_mask:0xf bound_ctrl:1
	s_nop 0
	v_cndmask_b32_e64 v198, 0, 32, vcc
	v_ldexp_f32 v111, v111, v198
	v_log_f32_e32 v111, v111
	s_nop 0
	v_mul_f32_e32 v198, 0x3f317217, v111
	v_fma_f32 v198, v111, s33, -v198
	v_fmac_f32_e32 v198, 0x3377d1cf, v111
	v_fmac_f32_e32 v198, 0x3f317217, v111
	v_cmp_lt_f32_e64 s[52:53], |v111|, s36
	s_nop 1
	v_cndmask_b32_e64 v111, v111, v198, s[52:53]
	v_cndmask_b32_e32 v198, 0, v216, vcc
	v_sub_f32_e32 v198, v111, v198
	s_nop 0
	s_nop 0
	s_nop 1
	s_nop 0
	s_nop 1
	v_mul_f32_e64 v112, |v113|, s8
	v_exp_f32_e32 v112, v112
	v_max_f32_e32 v111, v113, v113
	v_min_f32_e32 v111, 0, v111
	v_add_f32_e32 v112, 1.0, v112
	v_cmp_gt_f32_e32 vcc, s37, v112
	s_nop 1
	v_cndmask_b32_e64 v199, 0, 32, vcc
	v_ldexp_f32 v112, v112, v199
	v_log_f32_e32 v112, v112
	s_nop 0
	v_mul_f32_e32 v199, 0x3f317217, v112
	v_fma_f32 v199, v112, s33, -v199
	v_fmac_f32_e32 v199, 0x3377d1cf, v112
	v_fmac_f32_e32 v199, 0x3f317217, v112
	v_cmp_lt_f32_e64 s[52:53], |v112|, s36
	s_nop 1
	v_cndmask_b32_e64 v112, v112, v199, s[52:53]
	v_cndmask_b32_e32 v199, 0, v216, vcc
	v_sub_f32_e32 v199, v112, v199
	v_pk_add_f32 v[110:111], v[110:111], v[198:199] neg_lo:[0,1] neg_hi:[0,1]
	v_mov_b32_e32 v110, v110
	s_nop 1
	v_mov_b32_dpp v198, v110 row_shr:1 row_mask:0xf bank_mask:0xf bound_ctrl:1
	s_nop 0
	s_nop 0
	s_nop 1
	v_mul_f32_e64 v113, |v106|, s8
	v_exp_f32_e32 v113, v113
	v_max_f32_e32 v112, v106, v106
	v_add_f32_e32 v113, 1.0, v113
	v_cmp_gt_f32_e32 vcc, s37, v113
	v_mov_b32_e32 v111, v111
	s_nop 0
	v_cndmask_b32_e64 v200, 0, 32, vcc
	v_ldexp_f32 v113, v113, v200
	v_log_f32_e32 v113, v113
	v_mov_b32_dpp v199, v111 row_shr:1 row_mask:0xf bank_mask:0xf bound_ctrl:1
	v_pk_add_f32 v[198:199], v[110:111], v[198:199]
	v_min_f32_e32 v112, 0, v112
	v_mul_f32_e32 v200, 0x3f317217, v113
	v_fma_f32 v200, v113, s33, -v200
	v_fmac_f32_e32 v200, 0x3377d1cf, v113
	v_fmac_f32_e32 v200, 0x3f317217, v113
	v_cmp_lt_f32_e64 s[52:53], |v113|, s36
	s_nop 1
	v_cndmask_b32_e64 v113, v113, v200, s[52:53]
	v_cndmask_b32_e32 v200, 0, v216, vcc
	v_sub_f32_e32 v200, v113, v200
	s_nop 0
	s_nop 1
	s_nop 0
	s_nop 1
	v_max_f32_e32 v106, v107, v107
	v_min_f32_e32 v113, 0, v106
	v_mul_f32_e64 v106, |v107|, s8
	v_exp_f32_e32 v106, v106
	s_nop 0
	v_add_f32_e32 v106, 1.0, v106
	v_cmp_gt_f32_e32 vcc, s37, v106
	s_nop 1
	v_cndmask_b32_e64 v201, 0, 32, vcc
	v_ldexp_f32 v106, v106, v201
	v_log_f32_e32 v106, v106
	s_nop 0
	v_mul_f32_e32 v201, 0x3f317217, v106
	v_fma_f32 v201, v106, s33, -v201
	v_fmac_f32_e32 v201, 0x3377d1cf, v106
	v_fmac_f32_e32 v201, 0x3f317217, v106
	v_cmp_lt_f32_e64 s[52:53], |v106|, s36
	s_nop 1
	v_cndmask_b32_e64 v106, v106, v201, s[52:53]
	v_cndmask_b32_e32 v201, 0, v216, vcc
	v_sub_f32_e32 v201, v106, v201
	v_pk_add_f32 v[112:113], v[112:113], v[200:201] neg_lo:[0,1] neg_hi:[0,1]
	s_nop 0
	s_nop 1
	s_nop 0
	s_nop 1
	v_mul_f32_e64 v107, |v108|, s8
	v_exp_f32_e32 v107, v107
	v_max_f32_e32 v106, v108, v108
	v_mov_b32_e32 v113, v113
	v_min_f32_e32 v106, 0, v106
	v_add_f32_e32 v107, 1.0, v107
	v_cmp_gt_f32_e32 vcc, s37, v107
	v_mov_b32_dpp v201, v113 row_shr:1 row_mask:0xf bank_mask:0xf bound_ctrl:1
	s_nop 0
	v_cndmask_b32_e64 v202, 0, 32, vcc
	v_ldexp_f32 v107, v107, v202
	v_log_f32_e32 v107, v107
	s_nop 0
	v_mul_f32_e32 v202, 0x3f317217, v107
	v_fma_f32 v202, v107, s33, -v202
	v_fmac_f32_e32 v202, 0x3377d1cf, v107
	v_fmac_f32_e32 v202, 0x3f317217, v107
	v_cmp_lt_f32_e64 s[52:53], |v107|, s36
	s_nop 1
	v_cndmask_b32_e64 v107, v107, v202, s[52:53]
	v_cndmask_b32_e32 v202, 0, v216, vcc
	v_sub_f32_e32 v202, v107, v202
	s_nop 0
	s_nop 0
	s_nop 1
	s_nop 0
	s_nop 1
	v_mul_f32_e64 v108, |v109|, s8
	v_exp_f32_e32 v108, v108
	v_max_f32_e32 v107, v109, v109
	v_min_f32_e32 v107, 0, v107
	v_add_f32_e32 v108, 1.0, v108
	v_cmp_gt_f32_e32 vcc, s37, v108
	s_nop 1
	v_cndmask_b32_e64 v203, 0, 32, vcc
	v_ldexp_f32 v108, v108, v203
	v_log_f32_e32 v108, v108
	s_nop 0
	v_mul_f32_e32 v203, 0x3f317217, v108
	v_fma_f32 v203, v108, s33, -v203
	v_fmac_f32_e32 v203, 0x3377d1cf, v108
	v_fmac_f32_e32 v203, 0x3f317217, v108
	v_cmp_lt_f32_e64 s[52:53], |v108|, s36
	s_nop 1
	v_cndmask_b32_e64 v108, v108, v203, s[52:53]
	v_cndmask_b32_e32 v203, 0, v216, vcc
	v_sub_f32_e32 v203, v108, v203
	v_pk_add_f32 v[106:107], v[106:107], v[202:203] neg_lo:[0,1] neg_hi:[0,1]
	v_mov_b32_e32 v202, v106
	s_nop 1
	v_mov_b32_dpp v106, v202 row_shr:1 row_mask:0xf bank_mask:0xf bound_ctrl:1
	s_nop 0
	s_nop 0
	s_nop 1
	v_pk_add_f32 v[108:109], v[186:187], v[188:189] neg_lo:[0,1] neg_hi:[0,1]
	v_mov_b32_e32 v109, v109
	v_mov_b32_e32 v203, v107
	v_mov_b32_e32 v108, v108
	v_mov_b32_dpp v187, v109 row_shr:1 row_mask:0xf bank_mask:0xf bound_ctrl:1
	v_mov_b32_e32 v120, v120
	v_mov_b32_dpp v186, v108 row_shr:1 row_mask:0xf bank_mask:0xf bound_ctrl:1
	v_pk_add_f32 v[186:187], v[108:109], v[186:187]
	v_mov_b32_e32 v116, v116
	v_mov_b32_e32 v112, v112
	v_mov_b32_dpp v188, v186 row_shr:2 row_mask:0xf bank_mask:0xf bound_ctrl:1
	v_mov_b32_dpp v189, v187 row_shr:2 row_mask:0xf bank_mask:0xf bound_ctrl:1
	v_pk_add_f32 v[186:187], v[186:187], v[188:189]
	v_mov_b32_dpp v196, v116 row_shr:1 row_mask:0xf bank_mask:0xf bound_ctrl:1
	v_pk_add_f32 v[196:197], v[116:117], v[196:197]
	v_mov_b32_dpp v188, v186 row_shr:4 row_mask:0xf bank_mask:0xf bound_ctrl:1
	v_mov_b32_dpp v189, v187 row_shr:4 row_mask:0xf bank_mask:0xf bound_ctrl:1
	v_pk_add_f32 v[186:187], v[186:187], v[188:189]
	v_mov_b32_dpp v200, v112 row_shr:1 row_mask:0xf bank_mask:0xf bound_ctrl:1
	v_pk_add_f32 v[200:201], v[112:113], v[200:201]
	v_mov_b32_dpp v188, v186 row_shr:8 row_mask:0xf bank_mask:0xf bound_ctrl:1
	v_mov_b32_dpp v189, v187 row_shr:8 row_mask:0xf bank_mask:0xf bound_ctrl:1
	v_pk_add_f32 v[186:187], v[186:187], v[188:189]
	ds_swizzle_b32 v188, v186 offset:swizzle(BROADCAST,16,15)
	ds_swizzle_b32 v189, v187 offset:swizzle(BROADCAST,16,15)
	v_mov_b32_dpp v107, v203 row_shr:1 row_mask:0xf bank_mask:0xf bound_ctrl:1
	v_pk_add_f32 v[106:107], v[202:203], v[106:107]
	v_pk_add_f32 v[186:187], v[186:187], 0 op_sel_hi:[1,0]
	s_waitcnt lgkmcnt(0)
; template <int CTRL> __device__ __forceinline__ float dppx(float v) { return __int_as_float(__builtin_amdgcn_update_dpp(0, __float_as_int(v), CTRL, 0xf, 0xf, true)); }
;   __device__ __forceinline__ void operator()(const f32x4 (&acc)[2][2][4][2], const pg8::Unit& u, int wr, int wc, int fr, int fq) const {
;     ...
;             for (int m = 0; m < 4; ++m)
; #pragma unroll
;               for (int q = 0; q < 4; ++q) { const float gv = log_forget(acc[ai][bj][m][qh][q], lq[q]); g[m][q] = gv;
;                 float sc = gv; sc += dppx<0x111>(sc); sc += dppx<0x112>(sc); sc += dppx<0x114>(sc); sc += dppx<0x118>(sc);
;                 const float tot16 = __int_as_float(__builtin_amdgcn_ds_swizzle(__float_as_int(sc), 0x1F0));
;                 cs[m][q] = sc + carry[q]; carry[q] += tot16; }
; #pragma unroll
;             for (int m = 0; m < 4; ++m) { const int r = row0 + ai * 128 + m * 16; float bq[4], kq[4];
; #pragma unroll
;               for (int q = 0; q < 4; ++q) { bq[q] = bwd ? (carry[q] - cs[m][q]) + g[m][q] : cs[m][q]; kq[q] = 1.f - __expf(g[m][q]); }
	v_pk_add_f32 v[212:213], v[188:189], 0 op_sel_hi:[1,0]
	v_mul_f32_e32 v188, 0x3fb8aa3b, v108
	v_exp_f32_e32 v188, v188
	v_mov_b32_dpp v189, v119 row_shr:1 row_mask:0xf bank_mask:0xf bound_ctrl:1
	v_sub_f32_e32 v207, 1.0, v188
	v_mul_f32_e32 v188, 0x3fb8aa3b, v109
	v_exp_f32_e32 v188, v188
	s_nop 0
	v_sub_f32_e32 v215, 1.0, v188
	v_mov_b32_dpp v188, v118 row_shr:1 row_mask:0xf bank_mask:0xf bound_ctrl:1
	v_pk_add_f32 v[188:189], v[118:119], v[188:189]
	s_nop 1
	v_mov_b32_dpp v190, v188 row_shr:2 row_mask:0xf bank_mask:0xf bound_ctrl:1
	v_mov_b32_dpp v191, v189 row_shr:2 row_mask:0xf bank_mask:0xf bound_ctrl:1
	v_pk_add_f32 v[188:189], v[188:189], v[190:191]
	s_nop 1
	v_mov_b32_dpp v190, v188 row_shr:4 row_mask:0xf bank_mask:0xf bound_ctrl:1
	v_mov_b32_dpp v191, v189 row_shr:4 row_mask:0xf bank_mask:0xf bound_ctrl:1
	v_pk_add_f32 v[188:189], v[188:189], v[190:191]
	s_nop 1
	v_mov_b32_dpp v190, v188 row_shr:8 row_mask:0xf bank_mask:0xf bound_ctrl:1
	v_mov_b32_dpp v191, v189 row_shr:8 row_mask:0xf bank_mask:0xf bound_ctrl:1
	v_pk_add_f32 v[188:189], v[188:189], v[190:191]
	ds_swizzle_b32 v190, v188 offset:swizzle(BROADCAST,16,15)
	ds_swizzle_b32 v191, v189 offset:swizzle(BROADCAST,16,15)
	v_pk_add_f32 v[188:189], v[188:189], 0 op_sel_hi:[1,0]
	s_waitcnt lgkmcnt(0)
	v_pk_add_f32 v[208:209], v[190:191], 0 op_sel_hi:[1,0]
	v_mul_f32_e32 v190, 0x3fb8aa3b, v118
	v_exp_f32_e32 v190, v190
	v_mov_b32_dpp v191, v121 row_shr:1 row_mask:0xf bank_mask:0xf bound_ctrl:1
	v_sub_f32_e32 v236, 1.0, v190
	v_mul_f32_e32 v190, 0x3fb8aa3b, v119
	v_exp_f32_e32 v190, v190
	s_nop 0
	v_sub_f32_e32 v237, 1.0, v190
	v_mov_b32_dpp v190, v120 row_shr:1 row_mask:0xf bank_mask:0xf bound_ctrl:1
	v_pk_add_f32 v[190:191], v[120:121], v[190:191]
	s_nop 1
	v_mov_b32_dpp v192, v190 row_shr:2 row_mask:0xf bank_mask:0xf bound_ctrl:1
	v_mov_b32_dpp v193, v191 row_shr:2 row_mask:0xf bank_mask:0xf bound_ctrl:1
	v_pk_add_f32 v[190:191], v[190:191], v[192:193]
	s_nop 1
	v_mov_b32_dpp v192, v190 row_shr:4 row_mask:0xf bank_mask:0xf bound_ctrl:1
	v_mov_b32_dpp v193, v191 row_shr:4 row_mask:0xf bank_mask:0xf bound_ctrl:1
	v_pk_add_f32 v[190:191], v[190:191], v[192:193]
	s_nop 1
	v_mov_b32_dpp v192, v190 row_shr:8 row_mask:0xf bank_mask:0xf bound_ctrl:1
	v_mov_b32_dpp v193, v191 row_shr:8 row_mask:0xf bank_mask:0xf bound_ctrl:1
	v_pk_add_f32 v[190:191], v[190:191], v[192:193]
	ds_swizzle_b32 v192, v190 offset:swizzle(BROADCAST,16,15)
	ds_swizzle_b32 v193, v191 offset:swizzle(BROADCAST,16,15)
	v_pk_add_f32 v[190:191], v[212:213], v[190:191]
	s_waitcnt lgkmcnt(0)
	v_pk_add_f32 v[210:211], v[212:213], v[192:193]
	v_mul_f32_e32 v192, 0x3fb8aa3b, v120
	v_exp_f32_e32 v192, v192
	v_mov_b32_dpp v193, v115 row_shr:1 row_mask:0xf bank_mask:0xf bound_ctrl:1
	v_sub_f32_e32 v226, 1.0, v192
	v_mul_f32_e32 v192, 0x3fb8aa3b, v121
	v_exp_f32_e32 v192, v192
	s_nop 0
	v_sub_f32_e32 v238, 1.0, v192
	v_mov_b32_dpp v192, v114 row_shr:1 row_mask:0xf bank_mask:0xf bound_ctrl:1
	v_pk_add_f32 v[192:193], v[114:115], v[192:193]
	s_nop 1
	v_mov_b32_dpp v194, v192 row_shr:2 row_mask:0xf bank_mask:0xf bound_ctrl:1
	v_mov_b32_dpp v195, v193 row_shr:2 row_mask:0xf bank_mask:0xf bound_ctrl:1
	v_pk_add_f32 v[192:193], v[192:193], v[194:195]
	s_nop 1
	v_mov_b32_dpp v194, v192 row_shr:4 row_mask:0xf bank_mask:0xf bound_ctrl:1
	v_mov_b32_dpp v195, v193 row_shr:4 row_mask:0xf bank_mask:0xf bound_ctrl:1
	v_pk_add_f32 v[192:193], v[192:193], v[194:195]
	s_nop 1
	v_mov_b32_dpp v194, v192 row_shr:8 row_mask:0xf bank_mask:0xf bound_ctrl:1
	v_mov_b32_dpp v195, v193 row_shr:8 row_mask:0xf bank_mask:0xf bound_ctrl:1
	v_pk_add_f32 v[192:193], v[192:193], v[194:195]
	ds_swizzle_b32 v194, v192 offset:swizzle(BROADCAST,16,15)
	ds_swizzle_b32 v195, v193 offset:swizzle(BROADCAST,16,15)
	v_pk_add_f32 v[192:193], v[208:209], v[192:193]
	s_waitcnt lgkmcnt(0)
	v_pk_add_f32 v[194:195], v[208:209], v[194:195]
	v_mul_f32_e32 v208, 0x3fb8aa3b, v114
	v_exp_f32_e32 v208, v208
	v_mov_b32_dpp v209, v197 row_shr:2 row_mask:0xf bank_mask:0xf bound_ctrl:1
	v_sub_f32_e32 v227, 1.0, v208
	v_mul_f32_e32 v208, 0x3fb8aa3b, v115
	v_exp_f32_e32 v208, v208
	s_nop 0
	v_sub_f32_e32 v228, 1.0, v208
	v_mov_b32_dpp v208, v196 row_shr:2 row_mask:0xf bank_mask:0xf bound_ctrl:1
	v_pk_add_f32 v[196:197], v[196:197], v[208:209]
	s_nop 1
	v_mov_b32_dpp v208, v196 row_shr:4 row_mask:0xf bank_mask:0xf bound_ctrl:1
	v_mov_b32_dpp v209, v197 row_shr:4 row_mask:0xf bank_mask:0xf bound_ctrl:1
	v_pk_add_f32 v[196:197], v[196:197], v[208:209]
	s_nop 1
	v_mov_b32_dpp v208, v196 row_shr:8 row_mask:0xf bank_mask:0xf bound_ctrl:1
	v_mov_b32_dpp v209, v197 row_shr:8 row_mask:0xf bank_mask:0xf bound_ctrl:1
	v_pk_add_f32 v[196:197], v[196:197], v[208:209]
	ds_swizzle_b32 v208, v196 offset:swizzle(BROADCAST,16,15)
	ds_swizzle_b32 v209, v197 offset:swizzle(BROADCAST,16,15)
	v_pk_add_f32 v[196:197], v[210:211], v[196:197]
	s_waitcnt lgkmcnt(0)
	v_pk_add_f32 v[208:209], v[210:211], v[208:209]
	v_mul_f32_e32 v210, 0x3fb8aa3b, v116
	v_exp_f32_e32 v210, v210
	v_mov_b32_dpp v211, v199 row_shr:2 row_mask:0xf bank_mask:0xf bound_ctrl:1
	v_sub_f32_e32 v229, 1.0, v210
	v_mul_f32_e32 v210, 0x3fb8aa3b, v117
	v_exp_f32_e32 v210, v210
	s_nop 0
	v_sub_f32_e32 v230, 1.0, v210
	v_mov_b32_dpp v210, v198 row_shr:2 row_mask:0xf bank_mask:0xf bound_ctrl:1
	v_pk_add_f32 v[198:199], v[198:199], v[210:211]
	s_nop 1
	v_mov_b32_dpp v210, v198 row_shr:4 row_mask:0xf bank_mask:0xf bound_ctrl:1
	v_mov_b32_dpp v211, v199 row_shr:4 row_mask:0xf bank_mask:0xf bound_ctrl:1
	v_pk_add_f32 v[198:199], v[198:199], v[210:211]
	s_nop 1
	v_mov_b32_dpp v210, v198 row_shr:8 row_mask:0xf bank_mask:0xf bound_ctrl:1
	v_mov_b32_dpp v211, v199 row_shr:8 row_mask:0xf bank_mask:0xf bound_ctrl:1
	v_pk_add_f32 v[198:199], v[198:199], v[210:211]
	ds_swizzle_b32 v210, v198 offset:swizzle(BROADCAST,16,15)
	ds_swizzle_b32 v211, v199 offset:swizzle(BROADCAST,16,15)
	v_pk_add_f32 v[198:199], v[194:195], v[198:199]
	s_waitcnt lgkmcnt(0)
; __device__ __forceinline__ unsigned cvt_pk_bf16(float lo, float hi) { unsigned r; asm volatile("v_cvt_pk_bf16_f32 %0, %1, %2" : "=v"(r) : "v"(lo), "v"(hi)); return r; }
; __device__ __forceinline__ float log_forget(float z, float lb) {
;   const float r0 = fminf(z, 0.f) - __logf(1.f + __expf(-fabsf(z)));
;   __device__ __forceinline__ void operator()(const f32x4 (&acc)[2][2][4][2], const pg8::Unit& u, int wr, int wc, int fr, int fq) const {
;     ...
;             for (int m = 0; m < 4; ++m) { const int r = row0 + ai * 128 + m * 16; float bq[4], kq[4];
; #pragma unroll
;               for (int q = 0; q < 4; ++q) { bq[q] = bwd ? (carry[q] - cs[m][q]) + g[m][q] : cs[m][q]; kq[q] = 1.f - __expf(g[m][q]); }
;               *(f32x4*)(logfp + (size_t)r * 1024 + c + 4 * qh) = (f32x4){bq[0], bq[1], bq[2], bq[3]};
;               u32x2 w; w.x = pg8::cvt_pk_bf16(kq[0], kq[1]); w.y = pg8::cvt_pk_bf16(kq[2], kq[3]);
;               *(u32x2*)(km + (size_t)r * 1024 + c + 4 * qh) = w; } } }
	v_pk_add_f32 v[194:195], v[194:195], v[210:211]
	v_mul_f32_e32 v210, 0x3fb8aa3b, v110
	v_exp_f32_e32 v210, v210
	v_mov_b32_dpp v211, v201 row_shr:2 row_mask:0xf bank_mask:0xf bound_ctrl:1
	v_sub_f32_e32 v231, 1.0, v210
	v_mul_f32_e32 v210, 0x3fb8aa3b, v111
	v_exp_f32_e32 v210, v210
	s_nop 0
	v_sub_f32_e32 v232, 1.0, v210
	v_mov_b32_dpp v210, v200 row_shr:2 row_mask:0xf bank_mask:0xf bound_ctrl:1
	v_pk_add_f32 v[200:201], v[200:201], v[210:211]
	s_nop 1
	v_mov_b32_dpp v210, v200 row_shr:4 row_mask:0xf bank_mask:0xf bound_ctrl:1
	v_mov_b32_dpp v211, v201 row_shr:4 row_mask:0xf bank_mask:0xf bound_ctrl:1
	v_pk_add_f32 v[200:201], v[200:201], v[210:211]
	s_nop 1
	v_mov_b32_dpp v210, v200 row_shr:8 row_mask:0xf bank_mask:0xf bound_ctrl:1
	v_mov_b32_dpp v211, v201 row_shr:8 row_mask:0xf bank_mask:0xf bound_ctrl:1
	v_pk_add_f32 v[200:201], v[200:201], v[210:211]
	ds_swizzle_b32 v210, v200 offset:swizzle(BROADCAST,16,15)
	ds_swizzle_b32 v211, v201 offset:swizzle(BROADCAST,16,15)
	v_pk_add_f32 v[200:201], v[208:209], v[200:201]
	s_waitcnt lgkmcnt(0)
	v_pk_add_f32 v[208:209], v[208:209], v[210:211]
	v_mul_f32_e32 v210, 0x3fb8aa3b, v112
	v_exp_f32_e32 v210, v210
	v_mov_b32_dpp v211, v107 row_shr:2 row_mask:0xf bank_mask:0xf bound_ctrl:1
	v_sub_f32_e32 v233, 1.0, v210
	v_mul_f32_e32 v210, 0x3fb8aa3b, v113
	v_exp_f32_e32 v210, v210
	s_nop 0
	v_sub_f32_e32 v234, 1.0, v210
	v_mov_b32_dpp v210, v106 row_shr:2 row_mask:0xf bank_mask:0xf bound_ctrl:1
	v_pk_add_f32 v[106:107], v[106:107], v[210:211]
	s_nop 1
	v_mov_b32_dpp v210, v106 row_shr:4 row_mask:0xf bank_mask:0xf bound_ctrl:1
	v_mov_b32_dpp v211, v107 row_shr:4 row_mask:0xf bank_mask:0xf bound_ctrl:1
	v_pk_add_f32 v[106:107], v[106:107], v[210:211]
	s_nop 1
	v_mov_b32_dpp v210, v106 row_shr:8 row_mask:0xf bank_mask:0xf bound_ctrl:1
	v_mov_b32_dpp v211, v107 row_shr:8 row_mask:0xf bank_mask:0xf bound_ctrl:1
	v_pk_add_f32 v[106:107], v[106:107], v[210:211]
	ds_swizzle_b32 v210, v106 offset:swizzle(BROADCAST,16,15)
	ds_swizzle_b32 v211, v107 offset:swizzle(BROADCAST,16,15)
	v_pk_add_f32 v[212:213], v[194:195], v[106:107]
	v_pk_add_f32 v[106:107], v[208:209], v[186:187] neg_lo:[0,1] neg_hi:[0,1]
	s_waitcnt lgkmcnt(0)
	v_pk_add_f32 v[194:195], v[194:195], v[210:211]
	s_nop 0
	v_pk_add_f32 v[210:211], v[194:195], v[188:189] neg_lo:[0,1] neg_hi:[0,1]
	v_pk_add_f32 v[106:107], v[108:109], v[106:107]
	v_pk_add_f32 v[108:109], v[118:119], v[210:211]
	v_cndmask_b32_e64 v107, v187, v107, s[42:43]
	v_cndmask_b32_e64 v109, v189, v109, s[42:43]
	v_cndmask_b32_e64 v108, v188, v108, s[42:43]
	v_cndmask_b32_e64 v106, v186, v106, s[42:43]
	global_store_dwordx4 v[176:177], v[106:109], off offset:16
	s_nop 1
	v_cvt_pk_bf16_f32 v106, v207, v215
	v_cvt_pk_bf16_f32 v107, v236, v237
	global_store_dwordx2 v[174:175], v[106:107], off offset:8
	v_pk_add_f32 v[106:107], v[208:209], v[190:191] neg_lo:[0,1] neg_hi:[0,1]
	v_pk_add_f32 v[108:109], v[194:195], v[192:193] neg_lo:[0,1] neg_hi:[0,1]
	v_pk_add_f32 v[106:107], v[120:121], v[106:107]
	v_pk_add_f32 v[108:109], v[114:115], v[108:109]
	v_cndmask_b32_e64 v107, v191, v107, s[42:43]
	v_cndmask_b32_e64 v109, v193, v109, s[42:43]
	v_cndmask_b32_e64 v108, v192, v108, s[42:43]
	v_cndmask_b32_e64 v106, v190, v106, s[42:43]
	global_store_dwordx4 v[180:181], v[106:109], off offset:16
	s_nop 1
	v_cvt_pk_bf16_f32 v106, v226, v238
	v_cvt_pk_bf16_f32 v107, v227, v228
	global_store_dwordx2 v[172:173], v[106:107], off offset:8
	v_pk_add_f32 v[106:107], v[208:209], v[196:197] neg_lo:[0,1] neg_hi:[0,1]
	v_pk_add_f32 v[108:109], v[194:195], v[198:199] neg_lo:[0,1] neg_hi:[0,1]
	v_pk_add_f32 v[106:107], v[116:117], v[106:107]
	v_pk_add_f32 v[108:109], v[110:111], v[108:109]
	v_cndmask_b32_e64 v107, v197, v107, s[42:43]
	v_cndmask_b32_e64 v109, v199, v109, s[42:43]
	v_cndmask_b32_e64 v108, v198, v108, s[42:43]
	v_cndmask_b32_e64 v106, v196, v106, s[42:43]
	global_store_dwordx4 v[182:183], v[106:109], off offset:16
	v_mul_f32_e32 v111, 0x3fb8aa3b, v203
	v_exp_f32_e32 v111, v111
	v_cvt_pk_bf16_f32 v106, v229, v230
	v_cvt_pk_bf16_f32 v107, v231, v232
	global_store_dwordx2 v[170:171], v[106:107], off offset:8
	v_mul_f32_e32 v106, 0x3fb8aa3b, v202
	v_exp_f32_e32 v106, v106
	v_pk_add_f32 v[108:109], v[194:195], v[212:213] neg_lo:[0,1] neg_hi:[0,1]
	v_sub_f32_e32 v111, 1.0, v111
	v_pk_add_f32 v[108:109], v[202:203], v[108:109]
	v_sub_f32_e32 v110, 1.0, v106
	v_pk_add_f32 v[106:107], v[208:209], v[200:201] neg_lo:[0,1] neg_hi:[0,1]
	v_cndmask_b32_e64 v109, v213, v109, s[42:43]
	v_pk_add_f32 v[106:107], v[112:113], v[106:107]
	v_cndmask_b32_e64 v108, v212, v108, s[42:43]
	v_cndmask_b32_e64 v107, v201, v107, s[42:43]
	v_cndmask_b32_e64 v106, v200, v106, s[42:43]
	global_store_dwordx4 v[184:185], v[106:109], off offset:16
	s_nop 1
	v_cvt_pk_bf16_f32 v106, v233, v234
	v_cvt_pk_bf16_f32 v107, v110, v111
	global_store_dwordx2 v[168:169], v[106:107], off offset:8
	v_mul_f32_e64 v107, |v102|, s8
	v_exp_f32_e32 v107, v107
	v_max_f32_e32 v106, v102, v102
	v_add_f32_e32 v107, 1.0, v107
	v_cmp_gt_f32_e32 vcc, s37, v107
	v_min_f32_e32 v106, 0, v106
	s_nop 0
	v_cndmask_b32_e64 v108, 0, 32, vcc
	v_ldexp_f32 v107, v107, v108
	v_log_f32_e32 v107, v107
	s_nop 0
	v_mul_f32_e32 v108, 0x3f317217, v107
	v_fma_f32 v108, v107, s33, -v108
	v_fmac_f32_e32 v108, 0x3377d1cf, v107
	v_fmac_f32_e32 v108, 0x3f317217, v107
	v_cmp_lt_f32_e64 s[60:61], |v107|, s36
	s_nop 1
	v_cndmask_b32_e64 v107, v107, v108, s[60:61]
	v_cndmask_b32_e32 v108, 0, v216, vcc
	v_sub_f32_e32 v108, v107, v108
	s_nop 0
	s_nop 1
	s_nop 0
	s_nop 1
	v_max_f32_e32 v102, v103, v103
	v_min_f32_e32 v107, 0, v102
	v_mul_f32_e64 v102, |v103|, s8
	v_exp_f32_e32 v102, v102
; __device__ __forceinline__ float log_forget(float z, float lb) {
;   const float r0 = fminf(z, 0.f) - __logf(1.f + __expf(-fabsf(z)));
;   __device__ __forceinline__ void operator()(const f32x4 (&acc)[2][2][4][2], const pg8::Unit& u, int wr, int wc, int fr, int fq) const {
;     ...
;               for (int q = 0; q < 4; ++q) { const float gv = log_forget(acc[ai][bj][m][qh][q], lq[q]); g[m][q] = gv;
	s_nop 0
	v_add_f32_e32 v102, 1.0, v102
	v_cmp_gt_f32_e32 vcc, s37, v102
	s_nop 1
	v_cndmask_b32_e64 v109, 0, 32, vcc
	v_ldexp_f32 v102, v102, v109
	v_log_f32_e32 v102, v102
	s_nop 0
	v_mul_f32_e32 v109, 0x3f317217, v102
	v_fma_f32 v109, v102, s33, -v109
	v_fmac_f32_e32 v109, 0x3377d1cf, v102
	v_fmac_f32_e32 v109, 0x3f317217, v102
	v_cmp_lt_f32_e64 s[60:61], |v102|, s36
	s_nop 1
	v_cndmask_b32_e64 v102, v102, v109, s[60:61]
	v_cndmask_b32_e32 v109, 0, v216, vcc
	v_sub_f32_e32 v109, v102, v109
	s_nop 0
	s_nop 0
	s_nop 1
	s_nop 0
	s_nop 1
	v_mul_f32_e64 v103, |v104|, s8
	v_exp_f32_e32 v103, v103
	v_max_f32_e32 v102, v104, v104
	v_min_f32_e32 v102, 0, v102
	v_add_f32_e32 v103, 1.0, v103
	v_cmp_gt_f32_e32 vcc, s37, v103
	s_nop 1
	v_cndmask_b32_e64 v110, 0, 32, vcc
	v_ldexp_f32 v103, v103, v110
	v_log_f32_e32 v103, v103
	s_nop 0
	v_mul_f32_e32 v110, 0x3f317217, v103
	v_fma_f32 v110, v103, s33, -v110
	v_fmac_f32_e32 v110, 0x3377d1cf, v103
	v_fmac_f32_e32 v110, 0x3f317217, v103
	v_cmp_lt_f32_e64 s[60:61], |v103|, s36
	s_nop 1
	v_cndmask_b32_e64 v103, v103, v110, s[60:61]
	v_cndmask_b32_e32 v110, 0, v216, vcc
	v_sub_f32_e32 v110, v103, v110
	s_nop 0
	s_nop 0
	v_mul_f32_e64 v111, |v105|, s8
	v_exp_f32_e32 v111, v111
	s_nop 0
	v_add_f32_e32 v111, 1.0, v111
	s_nop 1
	v_cmp_gt_f32_e32 vcc, s37, v111
	v_max_f32_e32 v103, v105, v105
	s_nop 0
	v_cndmask_b32_e64 v112, 0, 32, vcc
	v_ldexp_f32 v111, v111, v112
	v_log_f32_e32 v111, v111
	v_min_f32_e32 v103, 0, v103
	v_mul_f32_e32 v112, 0x3f317217, v111
	v_fma_f32 v112, v111, s33, -v112
	v_fmac_f32_e32 v112, 0x3377d1cf, v111
	v_fmac_f32_e32 v112, 0x3f317217, v111
	v_cmp_lt_f32_e64 s[60:61], |v111|, s36
	s_nop 0
	s_nop 0
	v_cndmask_b32_e64 v111, v111, v112, s[60:61]
	v_cndmask_b32_e32 v112, 0, v216, vcc
	v_sub_f32_e32 v111, v111, v112
	s_nop 0
	v_mul_f32_e64 v113, |v98|, s8
	v_exp_f32_e32 v113, v113
	s_nop 0
	v_add_f32_e32 v113, 1.0, v113
	s_nop 1
	v_cmp_gt_f32_e32 vcc, s37, v113
	v_max_f32_e32 v112, v98, v98
	s_nop 0
	v_cndmask_b32_e64 v114, 0, 32, vcc
	v_ldexp_f32 v113, v113, v114
	v_log_f32_e32 v113, v113
	v_min_f32_e32 v112, 0, v112
	v_mul_f32_e32 v114, 0x3f317217, v113
	v_fma_f32 v114, v113, s33, -v114
	v_fmac_f32_e32 v114, 0x3377d1cf, v113
	v_fmac_f32_e32 v114, 0x3f317217, v113
	v_cmp_lt_f32_e64 s[60:61], |v113|, s36
	s_nop 0
	s_nop 0
	v_cndmask_b32_e64 v113, v113, v114, s[60:61]
	v_cndmask_b32_e32 v114, 0, v216, vcc
	v_sub_f32_e32 v114, v113, v114
	s_nop 0
	s_nop 1
	s_nop 0
	s_nop 1
	v_max_f32_e32 v98, v99, v99
	v_min_f32_e32 v113, 0, v98
	v_mul_f32_e64 v98, |v99|, s8
	v_exp_f32_e32 v98, v98
	s_nop 0
	v_add_f32_e32 v98, 1.0, v98
	v_cmp_gt_f32_e32 vcc, s37, v98
	s_nop 1
	v_cndmask_b32_e64 v115, 0, 32, vcc
	v_ldexp_f32 v98, v98, v115
	v_log_f32_e32 v98, v98
	s_nop 0
	v_mul_f32_e32 v115, 0x3f317217, v98
	v_fma_f32 v115, v98, s33, -v115
	v_fmac_f32_e32 v115, 0x3377d1cf, v98
	v_fmac_f32_e32 v115, 0x3f317217, v98
	v_cmp_lt_f32_e64 s[60:61], |v98|, s36
	s_nop 1
	v_cndmask_b32_e64 v98, v98, v115, s[60:61]
	v_cndmask_b32_e32 v115, 0, v216, vcc
	v_sub_f32_e32 v115, v98, v115
	s_nop 0
	s_nop 0
	s_nop 1
	s_nop 0
	s_nop 1
	v_mul_f32_e64 v99, |v100|, s8
	v_exp_f32_e32 v99, v99
	v_max_f32_e32 v98, v100, v100
	v_min_f32_e32 v98, 0, v98
	v_add_f32_e32 v99, 1.0, v99
	v_cmp_gt_f32_e32 vcc, s37, v99
	s_nop 1
	v_cndmask_b32_e64 v116, 0, 32, vcc
	v_ldexp_f32 v99, v99, v116
	v_log_f32_e32 v99, v99
	s_nop 0
	v_mul_f32_e32 v116, 0x3f317217, v99
	v_fma_f32 v116, v99, s33, -v116
	v_fmac_f32_e32 v116, 0x3377d1cf, v99
	v_fmac_f32_e32 v116, 0x3f317217, v99
	v_cmp_lt_f32_e64 s[60:61], |v99|, s36
	s_nop 1
	v_cndmask_b32_e64 v99, v99, v116, s[60:61]
	v_cndmask_b32_e32 v116, 0, v216, vcc
	v_sub_f32_e32 v116, v99, v116
	s_nop 0
	s_nop 0
	s_nop 1
	s_nop 0
	s_nop 1
	v_mul_f32_e64 v100, |v101|, s8
	v_exp_f32_e32 v100, v100
	v_max_f32_e32 v99, v101, v101
	v_min_f32_e32 v99, 0, v99
	v_add_f32_e32 v100, 1.0, v100
	v_cmp_gt_f32_e32 vcc, s37, v100
	s_nop 1
	v_cndmask_b32_e64 v117, 0, 32, vcc
	v_ldexp_f32 v100, v100, v117
	v_log_f32_e32 v100, v100
	s_nop 0
	v_mul_f32_e32 v117, 0x3f317217, v100
	v_fma_f32 v117, v100, s33, -v117
	v_fmac_f32_e32 v117, 0x3377d1cf, v100
	v_fmac_f32_e32 v117, 0x3f317217, v100
	v_cmp_lt_f32_e64 s[60:61], |v100|, s36
	s_nop 1
	v_cndmask_b32_e64 v100, v100, v117, s[60:61]
	v_cndmask_b32_e32 v117, 0, v216, vcc
	v_sub_f32_e32 v117, v100, v117
	s_nop 0
	s_nop 0
	s_nop 1
	s_nop 0
	s_nop 1
	v_mul_f32_e64 v101, |v88|, s8
	v_exp_f32_e32 v101, v101
	v_max_f32_e32 v100, v88, v88
	v_add_f32_e32 v101, 1.0, v101
	v_cmp_gt_f32_e32 vcc, s37, v101
	v_min_f32_e32 v100, 0, v100
	s_nop 0
	v_cndmask_b32_e64 v118, 0, 32, vcc
	v_ldexp_f32 v101, v101, v118
	v_log_f32_e32 v101, v101
	s_nop 0
	v_mul_f32_e32 v118, 0x3f317217, v101
	v_fma_f32 v118, v101, s33, -v118
	v_fmac_f32_e32 v118, 0x3377d1cf, v101
	v_fmac_f32_e32 v118, 0x3f317217, v101
	v_cmp_lt_f32_e64 s[60:61], |v101|, s36
	s_nop 1
	v_cndmask_b32_e64 v101, v101, v118, s[60:61]
	v_cndmask_b32_e32 v118, 0, v216, vcc
	v_sub_f32_e32 v118, v101, v118
	s_nop 0
	s_nop 1
	s_nop 0
	s_nop 1
	v_max_f32_e32 v88, v89, v89
	v_min_f32_e32 v101, 0, v88
	v_mul_f32_e64 v88, |v89|, s8
	v_exp_f32_e32 v88, v88
	s_nop 0
	v_add_f32_e32 v88, 1.0, v88
	v_cmp_gt_f32_e32 vcc, s37, v88
	s_nop 1
	v_cndmask_b32_e64 v119, 0, 32, vcc
	v_ldexp_f32 v88, v88, v119
	v_log_f32_e32 v88, v88
	s_nop 0
	v_mul_f32_e32 v119, 0x3f317217, v88
	v_fma_f32 v119, v88, s33, -v119
	v_fmac_f32_e32 v119, 0x3377d1cf, v88
	v_fmac_f32_e32 v119, 0x3f317217, v88
	v_cmp_lt_f32_e64 s[60:61], |v88|, s36
	s_nop 1
	v_cndmask_b32_e64 v88, v88, v119, s[60:61]
	v_cndmask_b32_e32 v119, 0, v216, vcc
	v_sub_f32_e32 v119, v88, v119
; template <int CTRL> __device__ __forceinline__ float dppx(float v) { return __int_as_float(__builtin_amdgcn_update_dpp(0, __float_as_int(v), CTRL, 0xf, 0xf, true)); }
; __device__ __forceinline__ float log_forget(float z, float lb) {
;   const float r0 = fminf(z, 0.f) - __logf(1.f + __expf(-fabsf(z)));
;   __device__ __forceinline__ void operator()(const f32x4 (&acc)[2][2][4][2], const pg8::Unit& u, int wr, int wc, int fr, int fq) const {
;     ...
;             for (int m = 0; m < 4; ++m)
; #pragma unroll
;               for (int q = 0; q < 4; ++q) { const float gv = log_forget(acc[ai][bj][m][qh][q], lq[q]); g[m][q] = gv;
;                 float sc = gv; sc += dppx<0x111>(sc); sc += dppx<0x112>(sc); sc += dppx<0x114>(sc); sc += dppx<0x118>(sc);
;                 const float tot16 = __int_as_float(__builtin_amdgcn_ds_swizzle(__float_as_int(sc), 0x1F0));
	v_pk_add_f32 v[100:101], v[100:101], v[118:119] neg_lo:[0,1] neg_hi:[0,1]
	v_mov_b32_e32 v100, v100
	s_nop 1
	s_nop 0
	s_nop 1
	v_max_f32_e32 v88, v90, v90
	v_min_f32_e32 v120, 0, v88
	v_mul_f32_e64 v88, |v90|, s8
	v_exp_f32_e32 v88, v88
	v_mov_b32_e32 v101, v101
	v_add_f32_e32 v88, 1.0, v88
	v_cmp_gt_f32_e32 vcc, s37, v88
	s_nop 1
	v_cndmask_b32_e64 v89, 0, 32, vcc
	v_ldexp_f32 v88, v88, v89
	v_log_f32_e32 v88, v88
	s_nop 0
	v_mul_f32_e32 v89, 0x3f317217, v88
	v_fma_f32 v89, v88, s33, -v89
	v_fmac_f32_e32 v89, 0x3377d1cf, v88
	v_fmac_f32_e32 v89, 0x3f317217, v88
	v_cmp_lt_f32_e64 s[60:61], |v88|, s36
	s_nop 1
	v_cndmask_b32_e64 v88, v88, v89, s[60:61]
	v_cndmask_b32_e32 v89, 0, v216, vcc
	v_sub_f32_e32 v168, v88, v89
	s_nop 0
	s_nop 0
	s_nop 1
	s_nop 0
	s_nop 1
	v_max_f32_e32 v88, v91, v91
	v_min_f32_e32 v121, 0, v88
	v_mul_f32_e64 v88, |v91|, s8
	v_exp_f32_e32 v88, v88
	s_nop 0
	v_add_f32_e32 v88, 1.0, v88
	v_cmp_gt_f32_e32 vcc, s37, v88
	s_nop 1
	v_cndmask_b32_e64 v89, 0, 32, vcc
	v_ldexp_f32 v88, v88, v89
	v_log_f32_e32 v88, v88
	s_nop 0
	v_mul_f32_e32 v89, 0x3f317217, v88
	v_fma_f32 v89, v88, s33, -v89
	v_fmac_f32_e32 v89, 0x3377d1cf, v88
	v_fmac_f32_e32 v89, 0x3f317217, v88
	v_cmp_lt_f32_e64 s[60:61], |v88|, s36
	s_nop 1
	v_cndmask_b32_e64 v88, v88, v89, s[60:61]
	v_cndmask_b32_e32 v89, 0, v216, vcc
	v_sub_f32_e32 v169, v88, v89
	s_nop 0
	s_nop 0
	s_nop 1
	s_nop 0
	s_nop 1
	v_max_f32_e32 v88, v84, v84
	v_min_f32_e32 v170, 0, v88
	v_mul_f32_e64 v88, |v84|, s8
	v_exp_f32_e32 v88, v88
	s_nop 0
	v_add_f32_e32 v88, 1.0, v88
	v_cmp_gt_f32_e32 vcc, s37, v88
	s_nop 0
	s_nop 0
	v_cndmask_b32_e64 v89, 0, 32, vcc
	v_ldexp_f32 v88, v88, v89
	v_log_f32_e32 v88, v88
	s_nop 0
	v_mul_f32_e32 v89, 0x3f317217, v88
	v_fma_f32 v89, v88, s33, -v89
	v_fmac_f32_e32 v89, 0x3377d1cf, v88
	v_fmac_f32_e32 v89, 0x3f317217, v88
	v_cmp_lt_f32_e64 s[60:61], |v88|, s36
	s_nop 1
	v_cndmask_b32_e64 v88, v88, v89, s[60:61]
	v_cndmask_b32_e32 v89, 0, v216, vcc
	v_sub_f32_e32 v172, v88, v89
	s_nop 0
	s_nop 1
	s_nop 0
	s_nop 1
	v_max_f32_e32 v84, v85, v85
	v_min_f32_e32 v171, 0, v84
	v_mul_f32_e64 v84, |v85|, s8
	v_exp_f32_e32 v84, v84
	s_nop 0
	v_add_f32_e32 v84, 1.0, v84
	v_cmp_gt_f32_e32 vcc, s37, v84
	s_nop 1
	v_cndmask_b32_e64 v88, 0, 32, vcc
	v_ldexp_f32 v84, v84, v88
	v_log_f32_e32 v84, v84
	s_nop 0
	v_mul_f32_e32 v88, 0x3f317217, v84
	v_fma_f32 v88, v84, s33, -v88
	v_fmac_f32_e32 v88, 0x3377d1cf, v84
	v_fmac_f32_e32 v88, 0x3f317217, v84
	v_cmp_lt_f32_e64 s[60:61], |v84|, s36
	s_nop 1
	v_cndmask_b32_e64 v84, v84, v88, s[60:61]
	v_cndmask_b32_e32 v88, 0, v216, vcc
	v_sub_f32_e32 v173, v84, v88
	s_nop 0
	s_nop 0
	v_pk_add_f32 v[92:93], v[112:113], v[114:115] neg_lo:[0,1] neg_hi:[0,1]
	v_ashrrev_i32_e32 v159, 31, v158
	v_mov_b32_e32 v115, v93
	v_mov_b32_e32 v114, v92
	s_nop 1
	v_mov_b32_dpp v92, v114 row_shr:1 row_mask:0xf bank_mask:0xf bound_ctrl:1
	v_mov_b32_dpp v93, v115 row_shr:1 row_mask:0xf bank_mask:0xf bound_ctrl:1
	v_max_f32_e32 v84, v86, v86
	v_min_f32_e32 v174, 0, v84
	v_mul_f32_e64 v84, |v86|, s8
	v_exp_f32_e32 v84, v84
	v_pk_add_f32 v[92:93], v[114:115], v[92:93]
	v_add_f32_e32 v84, 1.0, v84
	v_cmp_gt_f32_e32 vcc, s37, v84
	s_nop 1
	v_cndmask_b32_e64 v85, 0, 32, vcc
	v_ldexp_f32 v84, v84, v85
	v_log_f32_e32 v84, v84
	s_nop 0
	v_mul_f32_e32 v85, 0x3f317217, v84
	v_fma_f32 v85, v84, s33, -v85
	v_fmac_f32_e32 v85, 0x3377d1cf, v84
	v_fmac_f32_e32 v85, 0x3f317217, v84
	v_cmp_lt_f32_e64 s[60:61], |v84|, s36
	s_nop 1
	v_cndmask_b32_e64 v84, v84, v85, s[60:61]
	v_cndmask_b32_e32 v85, 0, v216, vcc
	v_sub_f32_e32 v176, v84, v85
	s_nop 0
	s_nop 0
	v_mov_b32_dpp v94, v92 row_shr:2 row_mask:0xf bank_mask:0xf bound_ctrl:1
	v_ashrrev_i32_e32 v161, 31, v160
	s_nop 0
	s_nop 1
	v_max_f32_e32 v84, v87, v87
	v_min_f32_e32 v175, 0, v84
	v_mul_f32_e64 v84, |v87|, s8
	v_exp_f32_e32 v84, v84
	s_nop 0
	v_add_f32_e32 v84, 1.0, v84
	v_cmp_gt_f32_e32 vcc, s37, v84
	s_nop 1
	v_cndmask_b32_e64 v85, 0, 32, vcc
	v_ldexp_f32 v84, v84, v85
	v_log_f32_e32 v84, v84
	s_nop 0
	v_mul_f32_e32 v85, 0x3f317217, v84
	v_fma_f32 v85, v84, s33, -v85
	v_fmac_f32_e32 v85, 0x3377d1cf, v84
	v_fmac_f32_e32 v85, 0x3f317217, v84
	v_cmp_lt_f32_e64 s[60:61], |v84|, s36
	s_nop 1
	v_cndmask_b32_e64 v84, v84, v85, s[60:61]
	v_cndmask_b32_e32 v85, 0, v216, vcc
	v_sub_f32_e32 v177, v84, v85
	s_nop 0
	s_nop 0
	v_mov_b32_dpp v95, v93 row_shr:2 row_mask:0xf bank_mask:0xf bound_ctrl:1
	v_pk_add_f32 v[92:93], v[92:93], v[94:95]
	s_nop 1
	v_mov_b32_dpp v94, v92 row_shr:4 row_mask:0xf bank_mask:0xf bound_ctrl:1
	v_mov_b32_dpp v95, v93 row_shr:4 row_mask:0xf bank_mask:0xf bound_ctrl:1
	v_pk_add_f32 v[92:93], v[92:93], v[94:95]
	s_nop 1
	v_mov_b32_dpp v94, v92 row_shr:8 row_mask:0xf bank_mask:0xf bound_ctrl:1
	v_mov_b32_dpp v95, v93 row_shr:8 row_mask:0xf bank_mask:0xf bound_ctrl:1
	v_pk_add_f32 v[84:85], v[106:107], v[108:109] neg_lo:[0,1] neg_hi:[0,1]
	v_pk_add_f32 v[92:93], v[92:93], v[94:95]
	v_mov_b32_e32 v181, v85
	v_mov_b32_e32 v180, v84
	ds_swizzle_b32 v94, v92 offset:swizzle(BROADCAST,16,15)
	v_mov_b32_dpp v85, v181 row_shr:1 row_mask:0xf bank_mask:0xf bound_ctrl:1
	v_mov_b32_dpp v84, v180 row_shr:1 row_mask:0xf bank_mask:0xf bound_ctrl:1
	v_pk_add_f32 v[84:85], v[180:181], v[84:85]
	ds_swizzle_b32 v95, v93 offset:swizzle(BROADCAST,16,15)
	v_ashrrev_i32_e32 v163, 31, v162
	v_mov_b32_dpp v86, v84 row_shr:2 row_mask:0xf bank_mask:0xf bound_ctrl:1
	v_mov_b32_dpp v87, v85 row_shr:2 row_mask:0xf bank_mask:0xf bound_ctrl:1
	v_pk_add_f32 v[84:85], v[84:85], v[86:87]
	s_nop 1
	v_mov_b32_dpp v86, v84 row_shr:4 row_mask:0xf bank_mask:0xf bound_ctrl:1
	v_mov_b32_dpp v87, v85 row_shr:4 row_mask:0xf bank_mask:0xf bound_ctrl:1
	v_pk_add_f32 v[84:85], v[84:85], v[86:87]
	s_nop 1
	v_mov_b32_dpp v86, v84 row_shr:8 row_mask:0xf bank_mask:0xf bound_ctrl:1
	v_mov_b32_dpp v87, v85 row_shr:8 row_mask:0xf bank_mask:0xf bound_ctrl:1
	v_pk_add_f32 v[84:85], v[84:85], v[86:87]
	ds_swizzle_b32 v86, v84 offset:swizzle(BROADCAST,16,15)
	v_pk_add_f32 v[182:183], v[84:85], 0 op_sel_hi:[1,0]
	v_mul_f32_e32 v84, 0x3fb8aa3b, v180
	v_exp_f32_e32 v84, v84
	ds_swizzle_b32 v87, v85 offset:swizzle(BROADCAST,16,15)
	v_sub_f32_e32 v199, 1.0, v84
	v_mul_f32_e32 v84, 0x3fb8aa3b, v181
	v_exp_f32_e32 v84, v84
	s_waitcnt lgkmcnt(0)
; template <int CTRL> __device__ __forceinline__ float dppx(float v) { return __int_as_float(__builtin_amdgcn_update_dpp(0, __float_as_int(v), CTRL, 0xf, 0xf, true)); }
; __device__ __forceinline__ unsigned cvt_pk_bf16(float lo, float hi) { unsigned r; asm volatile("v_cvt_pk_bf16_f32 %0, %1, %2" : "=v"(r) : "v"(lo), "v"(hi)); return r; }
;   __device__ __forceinline__ void operator()(const f32x4 (&acc)[2][2][4][2], const pg8::Unit& u, int wr, int wc, int fr, int fq) const {
;     ...
;             for (int m = 0; m < 4; ++m)
; #pragma unroll
;               for (int q = 0; q < 4; ++q) { const float gv = log_forget(acc[ai][bj][m][qh][q], lq[q]); g[m][q] = gv;
;                 float sc = gv; sc += dppx<0x111>(sc); sc += dppx<0x112>(sc); sc += dppx<0x114>(sc); sc += dppx<0x118>(sc);
;                 const float tot16 = __int_as_float(__builtin_amdgcn_ds_swizzle(__float_as_int(sc), 0x1F0));
;                 cs[m][q] = sc + carry[q]; carry[q] += tot16; }
; #pragma unroll
;             for (int m = 0; m < 4; ++m) { const int r = row0 + ai * 128 + m * 16; float bq[4], kq[4];
; #pragma unroll
;               for (int q = 0; q < 4; ++q) { bq[q] = bwd ? (carry[q] - cs[m][q]) + g[m][q] : cs[m][q]; kq[q] = 1.f - __expf(g[m][q]); }
;               *(f32x4*)(logfp + (size_t)r * 1024 + c + 4 * qh) = (f32x4){bq[0], bq[1], bq[2], bq[3]};
;               u32x2 w; w.x = pg8::cvt_pk_bf16(kq[0], kq[1]); w.y = pg8::cvt_pk_bf16(kq[2], kq[3]);
;               *(u32x2*)(km + (size_t)r * 1024 + c + 4 * qh) = w; } } }
	v_pk_add_f32 v[88:89], v[86:87], 0 op_sel_hi:[1,0]
	v_sub_f32_e32 v200, 1.0, v84
	v_pk_add_f32 v[84:85], v[102:103], v[110:111] neg_lo:[0,1] neg_hi:[0,1]
	v_mov_b32_dpp v110, v100 row_shr:1 row_mask:0xf bank_mask:0xf bound_ctrl:1
	v_mov_b32_e32 v185, v85
	v_mov_b32_e32 v184, v84
	v_mov_b32_dpp v111, v101 row_shr:1 row_mask:0xf bank_mask:0xf bound_ctrl:1
	v_mov_b32_dpp v85, v185 row_shr:1 row_mask:0xf bank_mask:0xf bound_ctrl:1
	v_mov_b32_dpp v84, v184 row_shr:1 row_mask:0xf bank_mask:0xf bound_ctrl:1
	v_pk_add_f32 v[84:85], v[184:185], v[84:85]
	v_pk_add_f32 v[110:111], v[100:101], v[110:111]
	s_nop 0
	v_mov_b32_dpp v86, v84 row_shr:2 row_mask:0xf bank_mask:0xf bound_ctrl:1
	v_mov_b32_dpp v87, v85 row_shr:2 row_mask:0xf bank_mask:0xf bound_ctrl:1
	v_pk_add_f32 v[84:85], v[84:85], v[86:87]
	v_mov_b32_dpp v112, v110 row_shr:2 row_mask:0xf bank_mask:0xf bound_ctrl:1
	v_mov_b32_dpp v113, v111 row_shr:2 row_mask:0xf bank_mask:0xf bound_ctrl:1
	v_mov_b32_dpp v86, v84 row_shr:4 row_mask:0xf bank_mask:0xf bound_ctrl:1
	v_mov_b32_dpp v87, v85 row_shr:4 row_mask:0xf bank_mask:0xf bound_ctrl:1
	v_pk_add_f32 v[84:85], v[84:85], v[86:87]
	v_pk_add_f32 v[110:111], v[110:111], v[112:113]
	s_nop 0
	v_mov_b32_dpp v86, v84 row_shr:8 row_mask:0xf bank_mask:0xf bound_ctrl:1
	v_mov_b32_dpp v87, v85 row_shr:8 row_mask:0xf bank_mask:0xf bound_ctrl:1
	v_pk_add_f32 v[84:85], v[84:85], v[86:87]
	ds_swizzle_b32 v86, v84 offset:swizzle(BROADCAST,16,15)
	v_pk_add_f32 v[186:187], v[84:85], 0 op_sel_hi:[1,0]
	v_mul_f32_e32 v84, 0x3fb8aa3b, v184
	v_exp_f32_e32 v84, v84
	ds_swizzle_b32 v87, v85 offset:swizzle(BROADCAST,16,15)
	v_mov_b32_dpp v112, v110 row_shr:4 row_mask:0xf bank_mask:0xf bound_ctrl:1
	v_mov_b32_dpp v113, v111 row_shr:4 row_mask:0xf bank_mask:0xf bound_ctrl:1
	v_sub_f32_e32 v201, 1.0, v84
	v_mul_f32_e32 v84, 0x3fb8aa3b, v185
	v_exp_f32_e32 v84, v84
	s_waitcnt lgkmcnt(0)
	v_pk_add_f32 v[90:91], v[86:87], 0 op_sel_hi:[1,0]
	v_lshlrev_b64 v[86:87], 11, v[162:163]
	v_pk_add_f32 v[110:111], v[110:111], v[112:113]
	v_sub_f32_e32 v202, 1.0, v84
	v_lshlrev_b64 v[84:85], 12, v[162:163]
	v_pk_add_f32 v[162:163], v[88:89], v[92:93]
	v_pk_add_f32 v[92:93], v[88:89], v[94:95]
	v_mul_f32_e32 v88, 0x3fb8aa3b, v114
	v_exp_f32_e32 v88, v88
	v_mov_b32_dpp v112, v110 row_shr:8 row_mask:0xf bank_mask:0xf bound_ctrl:1
	v_mov_b32_dpp v113, v111 row_shr:8 row_mask:0xf bank_mask:0xf bound_ctrl:1
	v_pk_add_f32 v[110:111], v[110:111], v[112:113]
	v_sub_f32_e32 v203, 1.0, v88
	v_mul_f32_e32 v88, 0x3fb8aa3b, v115
	v_exp_f32_e32 v88, v88
	ds_swizzle_b32 v112, v110 offset:swizzle(BROADCAST,16,15)
	ds_swizzle_b32 v113, v111 offset:swizzle(BROADCAST,16,15)
	v_lshl_add_u64 v[84:85], s[22:23], 0, v[84:85]
	v_sub_f32_e32 v207, 1.0, v88
	v_pk_add_f32 v[88:89], v[98:99], v[116:117] neg_lo:[0,1] neg_hi:[0,1]
	v_lshl_add_u64 v[104:105], v[84:85], 0, v[166:167]
	v_mov_b32_e32 v99, v89
	v_mov_b32_e32 v98, v88
	s_waitcnt lgkmcnt(0)
	v_pk_add_f32 v[118:119], v[92:93], v[112:113]
	v_mov_b32_dpp v89, v99 row_shr:1 row_mask:0xf bank_mask:0xf bound_ctrl:1
	v_mov_b32_dpp v88, v98 row_shr:1 row_mask:0xf bank_mask:0xf bound_ctrl:1
	v_pk_add_f32 v[88:89], v[98:99], v[88:89]
	v_lshl_add_u64 v[86:87], s[0:1], 0, v[86:87]
	v_lshl_add_u64 v[102:103], v[86:87], 0, v[164:165]
	v_mov_b32_dpp v94, v88 row_shr:2 row_mask:0xf bank_mask:0xf bound_ctrl:1
	v_mov_b32_dpp v95, v89 row_shr:2 row_mask:0xf bank_mask:0xf bound_ctrl:1
	v_pk_add_f32 v[88:89], v[88:89], v[94:95]
	s_nop 1
	v_mov_b32_dpp v94, v88 row_shr:4 row_mask:0xf bank_mask:0xf bound_ctrl:1
	v_mov_b32_dpp v95, v89 row_shr:4 row_mask:0xf bank_mask:0xf bound_ctrl:1
	v_pk_add_f32 v[88:89], v[88:89], v[94:95]
	s_nop 1
	v_mov_b32_dpp v94, v88 row_shr:8 row_mask:0xf bank_mask:0xf bound_ctrl:1
	v_mov_b32_dpp v95, v89 row_shr:8 row_mask:0xf bank_mask:0xf bound_ctrl:1
	v_pk_add_f32 v[88:89], v[88:89], v[94:95]
	ds_swizzle_b32 v94, v88 offset:swizzle(BROADCAST,16,15)
	v_pk_add_f32 v[116:117], v[90:91], v[88:89]
	v_mul_f32_e32 v88, 0x3fb8aa3b, v98
	v_exp_f32_e32 v88, v88
	ds_swizzle_b32 v95, v89 offset:swizzle(BROADCAST,16,15)
	v_sub_f32_e32 v208, 1.0, v88
	v_mul_f32_e32 v88, 0x3fb8aa3b, v99
	v_exp_f32_e32 v88, v88
	s_waitcnt lgkmcnt(0)
	v_pk_add_f32 v[94:95], v[90:91], v[94:95]
	v_lshlrev_b64 v[90:91], 11, v[160:161]
	v_lshl_add_u64 v[90:91], s[0:1], 0, v[90:91]
	v_sub_f32_e32 v209, 1.0, v88
	v_lshlrev_b64 v[88:89], 12, v[160:161]
	v_pk_add_f32 v[160:161], v[92:93], v[110:111]
	v_mul_f32_e32 v92, 0x3fb8aa3b, v100
	v_exp_f32_e32 v92, v92
	v_lshl_add_u64 v[88:89], s[22:23], 0, v[88:89]
	v_lshl_add_u64 v[108:109], v[88:89], 0, v[166:167]
	v_lshl_add_u64 v[106:107], v[90:91], 0, v[164:165]
	v_sub_f32_e32 v192, 1.0, v92
	v_mul_f32_e32 v92, 0x3fb8aa3b, v101
	v_exp_f32_e32 v92, v92
	s_nop 0
	v_sub_f32_e32 v193, 1.0, v92
	v_pk_add_f32 v[92:93], v[120:121], v[168:169] neg_lo:[0,1] neg_hi:[0,1]
	s_nop 0
	v_mov_b32_e32 v169, v93
	v_mov_b32_e32 v168, v92
	s_nop 0
	v_mov_b32_dpp v93, v169 row_shr:1 row_mask:0xf bank_mask:0xf bound_ctrl:1
	v_mov_b32_dpp v92, v168 row_shr:1 row_mask:0xf bank_mask:0xf bound_ctrl:1
	v_pk_add_f32 v[92:93], v[168:169], v[92:93]
	s_nop 1
	v_mov_b32_dpp v110, v92 row_shr:2 row_mask:0xf bank_mask:0xf bound_ctrl:1
	v_mov_b32_dpp v111, v93 row_shr:2 row_mask:0xf bank_mask:0xf bound_ctrl:1
	v_pk_add_f32 v[92:93], v[92:93], v[110:111]
	s_nop 1
	v_mov_b32_dpp v110, v92 row_shr:4 row_mask:0xf bank_mask:0xf bound_ctrl:1
	v_mov_b32_dpp v111, v93 row_shr:4 row_mask:0xf bank_mask:0xf bound_ctrl:1
	v_pk_add_f32 v[92:93], v[92:93], v[110:111]
	s_nop 1
	v_mov_b32_dpp v110, v92 row_shr:8 row_mask:0xf bank_mask:0xf bound_ctrl:1
	v_mov_b32_dpp v111, v93 row_shr:8 row_mask:0xf bank_mask:0xf bound_ctrl:1
	v_pk_add_f32 v[92:93], v[92:93], v[110:111]
	ds_swizzle_b32 v110, v92 offset:swizzle(BROADCAST,16,15)
	v_pk_add_f32 v[188:189], v[94:95], v[92:93]
	v_mul_f32_e32 v92, 0x3fb8aa3b, v168
	v_exp_f32_e32 v92, v92
	ds_swizzle_b32 v111, v93 offset:swizzle(BROADCAST,16,15)
	v_sub_f32_e32 v194, 1.0, v92
	v_mul_f32_e32 v92, 0x3fb8aa3b, v169
	v_exp_f32_e32 v92, v92
	s_waitcnt lgkmcnt(0)
; __device__ __forceinline__ unsigned cvt_pk_bf16(float lo, float hi) { unsigned r; asm volatile("v_cvt_pk_bf16_f32 %0, %1, %2" : "=v"(r) : "v"(lo), "v"(hi)); return r; }
;   __device__ __forceinline__ void operator()(const f32x4 (&acc)[2][2][4][2], const pg8::Unit& u, int wr, int wc, int fr, int fq) const {
;     ...
;             for (int m = 0; m < 4; ++m) { const int r = row0 + ai * 128 + m * 16; float bq[4], kq[4];
; #pragma unroll
;               for (int q = 0; q < 4; ++q) { bq[q] = bwd ? (carry[q] - cs[m][q]) + g[m][q] : cs[m][q]; kq[q] = 1.f - __expf(g[m][q]); }
;               *(f32x4*)(logfp + (size_t)r * 1024 + c + 4 * qh) = (f32x4){bq[0], bq[1], bq[2], bq[3]};
;               u32x2 w; w.x = pg8::cvt_pk_bf16(kq[0], kq[1]); w.y = pg8::cvt_pk_bf16(kq[2], kq[3]);
;               *(u32x2*)(km + (size_t)r * 1024 + c + 4 * qh) = w; } } }
	v_pk_add_f32 v[120:121], v[94:95], v[110:111]
	v_lshlrev_b64 v[94:95], 11, v[158:159]
	v_lshl_add_u64 v[94:95], s[0:1], 0, v[94:95]
	v_sub_f32_e32 v195, 1.0, v92
	v_lshlrev_b64 v[92:93], 12, v[158:159]
	v_pk_add_f32 v[158:159], v[170:171], v[172:173] neg_lo:[0,1] neg_hi:[0,1]
	v_lshl_add_u64 v[92:93], s[22:23], 0, v[92:93]
	v_mov_b32_e32 v159, v159
	v_mov_b32_e32 v158, v158
	v_lshl_add_u64 v[110:111], v[92:93], 0, v[166:167]
	v_mov_b32_dpp v171, v159 row_shr:1 row_mask:0xf bank_mask:0xf bound_ctrl:1
	v_mov_b32_dpp v170, v158 row_shr:1 row_mask:0xf bank_mask:0xf bound_ctrl:1
	v_pk_add_f32 v[170:171], v[158:159], v[170:171]
	v_lshl_add_u64 v[112:113], v[94:95], 0, v[164:165]
	v_ashrrev_i32_e32 v157, 31, v156
	v_mov_b32_dpp v172, v170 row_shr:2 row_mask:0xf bank_mask:0xf bound_ctrl:1
	v_mov_b32_dpp v173, v171 row_shr:2 row_mask:0xf bank_mask:0xf bound_ctrl:1
	v_pk_add_f32 v[170:171], v[170:171], v[172:173]
	s_nop 1
	v_mov_b32_dpp v172, v170 row_shr:4 row_mask:0xf bank_mask:0xf bound_ctrl:1
	v_mov_b32_dpp v173, v171 row_shr:4 row_mask:0xf bank_mask:0xf bound_ctrl:1
	v_pk_add_f32 v[170:171], v[170:171], v[172:173]
	s_nop 1
	v_mov_b32_dpp v172, v170 row_shr:8 row_mask:0xf bank_mask:0xf bound_ctrl:1
	v_mov_b32_dpp v173, v171 row_shr:8 row_mask:0xf bank_mask:0xf bound_ctrl:1
	v_pk_add_f32 v[170:171], v[170:171], v[172:173]
	ds_swizzle_b32 v172, v170 offset:swizzle(BROADCAST,16,15)
	ds_swizzle_b32 v173, v171 offset:swizzle(BROADCAST,16,15)
	v_pk_add_f32 v[170:171], v[118:119], v[170:171]
	s_waitcnt lgkmcnt(0)
	v_pk_add_f32 v[172:173], v[118:119], v[172:173]
	v_mul_f32_e32 v118, 0x3fb8aa3b, v158
	v_exp_f32_e32 v118, v118
	s_nop 0
	v_sub_f32_e32 v196, 1.0, v118
	v_mul_f32_e32 v118, 0x3fb8aa3b, v159
	v_exp_f32_e32 v118, v118
	s_nop 0
	v_sub_f32_e32 v210, 1.0, v118
	v_pk_add_f32 v[118:119], v[174:175], v[176:177] neg_lo:[0,1] neg_hi:[0,1]
	s_nop 0
	v_mov_b32_e32 v175, v119
	v_mov_b32_e32 v174, v118
	s_nop 0
	v_mov_b32_dpp v119, v175 row_shr:1 row_mask:0xf bank_mask:0xf bound_ctrl:1
	v_mov_b32_dpp v118, v174 row_shr:1 row_mask:0xf bank_mask:0xf bound_ctrl:1
	v_pk_add_f32 v[118:119], v[174:175], v[118:119]
	s_nop 1
	v_mov_b32_dpp v176, v118 row_shr:2 row_mask:0xf bank_mask:0xf bound_ctrl:1
	v_mov_b32_dpp v177, v119 row_shr:2 row_mask:0xf bank_mask:0xf bound_ctrl:1
	v_pk_add_f32 v[118:119], v[118:119], v[176:177]
	s_nop 1
	v_mov_b32_dpp v176, v118 row_shr:4 row_mask:0xf bank_mask:0xf bound_ctrl:1
	v_mov_b32_dpp v177, v119 row_shr:4 row_mask:0xf bank_mask:0xf bound_ctrl:1
	v_pk_add_f32 v[118:119], v[118:119], v[176:177]
	s_nop 1
	v_mov_b32_dpp v176, v118 row_shr:8 row_mask:0xf bank_mask:0xf bound_ctrl:1
	v_mov_b32_dpp v177, v119 row_shr:8 row_mask:0xf bank_mask:0xf bound_ctrl:1
	v_pk_add_f32 v[118:119], v[118:119], v[176:177]
	ds_swizzle_b32 v176, v118 offset:swizzle(BROADCAST,16,15)
	ds_swizzle_b32 v177, v119 offset:swizzle(BROADCAST,16,15)
	v_pk_add_f32 v[190:191], v[120:121], v[118:119]
	v_pk_add_f32 v[118:119], v[172:173], v[182:183] neg_lo:[0,1] neg_hi:[0,1]
	s_waitcnt lgkmcnt(0)
	v_pk_add_f32 v[176:177], v[120:121], v[176:177]
	s_nop 0
	v_pk_add_f32 v[120:121], v[176:177], v[186:187] neg_lo:[0,1] neg_hi:[0,1]
	v_pk_add_f32 v[118:119], v[180:181], v[118:119]
	v_pk_add_f32 v[120:121], v[184:185], v[120:121]
	v_cndmask_b32_e64 v119, v183, v119, s[42:43]
	v_cndmask_b32_e64 v121, v187, v121, s[42:43]
	v_cndmask_b32_e64 v120, v186, v120, s[42:43]
	v_cndmask_b32_e64 v118, v182, v118, s[42:43]
	global_store_dwordx4 v[104:105], v[118:121], off
	s_nop 1
	v_cvt_pk_bf16_f32 v118, v199, v200
	v_cvt_pk_bf16_f32 v119, v201, v202
	global_store_dwordx2 v[102:103], v[118:119], off
	v_pk_add_f32 v[118:119], v[172:173], v[162:163] neg_lo:[0,1] neg_hi:[0,1]
	v_pk_add_f32 v[120:121], v[176:177], v[116:117] neg_lo:[0,1] neg_hi:[0,1]
	v_pk_add_f32 v[114:115], v[114:115], v[118:119]
	v_pk_add_f32 v[98:99], v[98:99], v[120:121]
	v_cndmask_b32_e64 v115, v163, v115, s[42:43]
	v_cndmask_b32_e64 v117, v117, v99, s[42:43]
	v_cndmask_b32_e64 v116, v116, v98, s[42:43]
	v_cndmask_b32_e64 v114, v162, v114, s[42:43]
	global_store_dwordx4 v[108:109], v[114:117], off
	v_cvt_pk_bf16_f32 v98, v203, v207
	v_cvt_pk_bf16_f32 v99, v208, v209
	global_store_dwordx2 v[106:107], v[98:99], off
	v_pk_add_f32 v[98:99], v[172:173], v[160:161] neg_lo:[0,1] neg_hi:[0,1]
	v_pk_add_f32 v[114:115], v[176:177], v[188:189] neg_lo:[0,1] neg_hi:[0,1]
	v_pk_add_f32 v[98:99], v[100:101], v[98:99]
	v_pk_add_f32 v[100:101], v[168:169], v[114:115]
	v_cndmask_b32_e64 v99, v161, v99, s[42:43]
	v_cndmask_b32_e64 v101, v189, v101, s[42:43]
	v_cndmask_b32_e64 v100, v188, v100, s[42:43]
	v_cndmask_b32_e64 v98, v160, v98, s[42:43]
	global_store_dwordx4 v[110:111], v[98:101], off
	s_nop 1
	v_cvt_pk_bf16_f32 v98, v192, v193
	v_cvt_pk_bf16_f32 v99, v194, v195
	global_store_dwordx2 v[112:113], v[98:99], off
	v_mul_f32_e32 v98, 0x3fb8aa3b, v174
	v_exp_f32_e32 v98, v98
	v_pk_add_f32 v[100:101], v[176:177], v[190:191] neg_lo:[0,1] neg_hi:[0,1]
	v_sub_f32_e32 v120, 1.0, v98
	v_pk_add_f32 v[98:99], v[172:173], v[170:171] neg_lo:[0,1] neg_hi:[0,1]
	v_pk_add_f32 v[100:101], v[174:175], v[100:101]
	v_pk_add_f32 v[98:99], v[158:159], v[98:99]
	v_cndmask_b32_e64 v118, v190, v100, s[42:43]
	v_cndmask_b32_e64 v116, v170, v98, s[42:43]
	v_mul_f32_e32 v98, 0x3fb8aa3b, v175
	v_exp_f32_e32 v98, v98
	v_cndmask_b32_e64 v117, v171, v99, s[42:43]
	v_cndmask_b32_e64 v119, v191, v101, s[42:43]
	v_sub_f32_e32 v100, 1.0, v98
	v_lshlrev_b64 v[98:99], 12, v[156:157]
	v_lshl_add_u64 v[98:99], s[22:23], 0, v[98:99]
	v_lshl_add_u64 v[114:115], v[98:99], 0, v[166:167]
	global_store_dwordx4 v[114:115], v[116:119], off
	s_nop 1
	v_cvt_pk_bf16_f32 v118, v196, v210
; __device__ __forceinline__ float log_forget(float z, float lb) {
;   const float r0 = fminf(z, 0.f) - __logf(1.f + __expf(-fabsf(z)));
;   __device__ __forceinline__ void operator()(const f32x4 (&acc)[2][2][4][2], const pg8::Unit& u, int wr, int wc, int fr, int fq) const {
;     ...
;               for (int q = 0; q < 4; ++q) { const float gv = log_forget(acc[ai][bj][m][qh][q], lq[q]); g[m][q] = gv;
	v_cvt_pk_bf16_f32 v119, v120, v100
	v_lshlrev_b64 v[100:101], 11, v[156:157]
	v_lshl_add_u64 v[100:101], s[0:1], 0, v[100:101]
	v_lshl_add_u64 v[116:117], v[100:101], 0, v[164:165]
	global_store_dwordx2 v[116:117], v[118:119], off
	v_mul_f32_e64 v119, |v80|, s8
	v_exp_f32_e32 v119, v119
	v_max_f32_e32 v118, v80, v80
	v_add_f32_e32 v119, 1.0, v119
	v_cmp_gt_f32_e32 vcc, s37, v119
	v_min_f32_e32 v118, 0, v118
	s_nop 0
	v_cndmask_b32_e64 v120, 0, 32, vcc
	v_ldexp_f32 v119, v119, v120
	v_log_f32_e32 v119, v119
	s_nop 0
	v_mul_f32_e32 v120, 0x3f317217, v119
	v_fma_f32 v120, v119, s33, -v120
	v_fmac_f32_e32 v120, 0x3377d1cf, v119
	v_fmac_f32_e32 v120, 0x3f317217, v119
	v_cmp_lt_f32_e64 s[44:45], |v119|, s36
	s_nop 1
	v_cndmask_b32_e64 v119, v119, v120, s[44:45]
	v_cndmask_b32_e32 v120, 0, v216, vcc
	v_sub_f32_e32 v120, v119, v120
	s_nop 0
	s_nop 1
	s_nop 0
	s_nop 1
	v_max_f32_e32 v80, v81, v81
	v_min_f32_e32 v119, 0, v80
	v_mul_f32_e64 v80, |v81|, s8
	v_exp_f32_e32 v80, v80
	s_nop 0
	v_add_f32_e32 v80, 1.0, v80
	v_cmp_gt_f32_e32 vcc, s37, v80
	s_nop 1
	v_cndmask_b32_e64 v121, 0, 32, vcc
	v_ldexp_f32 v80, v80, v121
	v_log_f32_e32 v80, v80
	s_nop 0
	v_mul_f32_e32 v121, 0x3f317217, v80
	v_fma_f32 v121, v80, s33, -v121
	v_fmac_f32_e32 v121, 0x3377d1cf, v80
	v_fmac_f32_e32 v121, 0x3f317217, v80
	v_cmp_lt_f32_e64 s[44:45], |v80|, s36
	s_nop 1
	v_cndmask_b32_e64 v80, v80, v121, s[44:45]
	v_cndmask_b32_e32 v121, 0, v216, vcc
	v_sub_f32_e32 v121, v80, v121
	s_nop 0
	s_nop 0
	s_nop 1
	s_nop 0
	s_nop 1
	v_mul_f32_e64 v81, |v82|, s8
	v_exp_f32_e32 v81, v81
	v_max_f32_e32 v80, v82, v82
	v_min_f32_e32 v80, 0, v80
	v_add_f32_e32 v81, 1.0, v81
	v_cmp_gt_f32_e32 vcc, s37, v81
	s_nop 1
	v_cndmask_b32_e64 v156, 0, 32, vcc
	v_ldexp_f32 v81, v81, v156
	v_log_f32_e32 v81, v81
	s_nop 0
	v_mul_f32_e32 v156, 0x3f317217, v81
	v_fma_f32 v156, v81, s33, -v156
	v_fmac_f32_e32 v156, 0x3377d1cf, v81
	v_fmac_f32_e32 v156, 0x3f317217, v81
	v_cmp_lt_f32_e64 s[44:45], |v81|, s36
	s_nop 1
	v_cndmask_b32_e64 v81, v81, v156, s[44:45]
	v_cndmask_b32_e32 v156, 0, v216, vcc
	v_sub_f32_e32 v156, v81, v156
	s_nop 0
	s_nop 0
	s_nop 1
	s_nop 0
	s_nop 1
	v_mul_f32_e64 v82, |v83|, s8
	v_exp_f32_e32 v82, v82
	v_max_f32_e32 v81, v83, v83
	v_min_f32_e32 v81, 0, v81
	v_add_f32_e32 v82, 1.0, v82
	v_cmp_gt_f32_e32 vcc, s37, v82
	s_nop 1
	v_cndmask_b32_e64 v157, 0, 32, vcc
	v_ldexp_f32 v82, v82, v157
	v_log_f32_e32 v82, v82
	s_nop 0
	v_mul_f32_e32 v157, 0x3f317217, v82
	v_fma_f32 v157, v82, s33, -v157
	v_fmac_f32_e32 v157, 0x3377d1cf, v82
	v_fmac_f32_e32 v157, 0x3f317217, v82
	v_cmp_lt_f32_e64 s[44:45], |v82|, s36
	s_nop 1
	v_cndmask_b32_e64 v82, v82, v157, s[44:45]
	v_cndmask_b32_e32 v157, 0, v216, vcc
	v_sub_f32_e32 v157, v82, v157
	v_pk_add_f32 v[80:81], v[80:81], v[156:157] neg_lo:[0,1] neg_hi:[0,1]
	v_mov_b32_e32 v80, v80
	s_nop 1
	s_nop 0
	s_nop 1
	v_mul_f32_e64 v83, |v76|, s8
	v_exp_f32_e32 v83, v83
	v_max_f32_e32 v82, v76, v76
	v_add_f32_e32 v83, 1.0, v83
	v_cmp_gt_f32_e32 vcc, s37, v83
	v_mov_b32_e32 v81, v81
	s_nop 0
	v_cndmask_b32_e64 v158, 0, 32, vcc
	v_ldexp_f32 v83, v83, v158
	v_log_f32_e32 v83, v83
	v_min_f32_e32 v82, 0, v82
	v_mul_f32_e32 v158, 0x3f317217, v83
	v_fma_f32 v158, v83, s33, -v158
	v_fmac_f32_e32 v158, 0x3377d1cf, v83
	v_fmac_f32_e32 v158, 0x3f317217, v83
	v_cmp_lt_f32_e64 s[44:45], |v83|, s36
	s_nop 1
	v_cndmask_b32_e64 v83, v83, v158, s[44:45]
	v_cndmask_b32_e32 v158, 0, v216, vcc
	v_sub_f32_e32 v158, v83, v158
	s_nop 0
	s_nop 1
	s_nop 0
	s_nop 1
	v_max_f32_e32 v76, v77, v77
	v_min_f32_e32 v83, 0, v76
	v_mul_f32_e64 v76, |v77|, s8
	v_exp_f32_e32 v76, v76
	s_nop 0
	v_add_f32_e32 v76, 1.0, v76
	v_cmp_gt_f32_e32 vcc, s37, v76
	s_nop 1
	v_cndmask_b32_e64 v159, 0, 32, vcc
	v_ldexp_f32 v76, v76, v159
	v_log_f32_e32 v76, v76
	s_nop 0
	v_mul_f32_e32 v159, 0x3f317217, v76
	v_fma_f32 v159, v76, s33, -v159
	v_fmac_f32_e32 v159, 0x3377d1cf, v76
	v_fmac_f32_e32 v159, 0x3f317217, v76
	v_cmp_lt_f32_e64 s[44:45], |v76|, s36
	s_nop 1
	v_cndmask_b32_e64 v76, v76, v159, s[44:45]
	v_cndmask_b32_e32 v159, 0, v216, vcc
	v_sub_f32_e32 v159, v76, v159
	v_pk_add_f32 v[82:83], v[82:83], v[158:159] neg_lo:[0,1] neg_hi:[0,1]
	v_mov_b32_e32 v82, v82
	s_nop 1
	s_nop 0
	s_nop 1
	v_mul_f32_e64 v77, |v78|, s8
	v_exp_f32_e32 v77, v77
	v_max_f32_e32 v76, v78, v78
	v_mov_b32_e32 v83, v83
	v_min_f32_e32 v76, 0, v76
	v_add_f32_e32 v77, 1.0, v77
	v_cmp_gt_f32_e32 vcc, s37, v77
	s_nop 1
	v_cndmask_b32_e64 v160, 0, 32, vcc
	v_ldexp_f32 v77, v77, v160
	v_log_f32_e32 v77, v77
	s_nop 0
	v_mul_f32_e32 v160, 0x3f317217, v77
	v_fma_f32 v160, v77, s33, -v160
	v_fmac_f32_e32 v160, 0x3377d1cf, v77
	v_fmac_f32_e32 v160, 0x3f317217, v77
	v_cmp_lt_f32_e64 s[44:45], |v77|, s36
	s_nop 1
	v_cndmask_b32_e64 v77, v77, v160, s[44:45]
	v_cndmask_b32_e32 v160, 0, v216, vcc
	v_sub_f32_e32 v160, v77, v160
	s_nop 0
	s_nop 0
	s_nop 1
	s_nop 0
	s_nop 1
	v_mul_f32_e64 v78, |v79|, s8
	v_exp_f32_e32 v78, v78
	v_max_f32_e32 v77, v79, v79
	v_min_f32_e32 v77, 0, v77
	v_add_f32_e32 v78, 1.0, v78
	v_cmp_gt_f32_e32 vcc, s37, v78
	s_nop 1
	v_cndmask_b32_e64 v161, 0, 32, vcc
	v_ldexp_f32 v78, v78, v161
	v_log_f32_e32 v78, v78
	s_nop 0
	v_mul_f32_e32 v161, 0x3f317217, v78
	v_fma_f32 v161, v78, s33, -v161
	v_fmac_f32_e32 v161, 0x3377d1cf, v78
	v_fmac_f32_e32 v161, 0x3f317217, v78
	v_cmp_lt_f32_e64 s[44:45], |v78|, s36
	s_nop 1
	v_cndmask_b32_e64 v78, v78, v161, s[44:45]
	v_cndmask_b32_e32 v161, 0, v216, vcc
	v_sub_f32_e32 v161, v78, v161
	v_pk_add_f32 v[76:77], v[76:77], v[160:161] neg_lo:[0,1] neg_hi:[0,1]
	v_mov_b32_e32 v76, v76
	s_nop 1
	s_nop 0
	s_nop 1
	v_mul_f32_e64 v79, |v68|, s8
	v_exp_f32_e32 v79, v79
	v_max_f32_e32 v78, v68, v68
; template <int CTRL> __device__ __forceinline__ float dppx(float v) { return __int_as_float(__builtin_amdgcn_update_dpp(0, __float_as_int(v), CTRL, 0xf, 0xf, true)); }
; __device__ __forceinline__ float log_forget(float z, float lb) {
;   const float r0 = fminf(z, 0.f) - __logf(1.f + __expf(-fabsf(z)));
;   __device__ __forceinline__ void operator()(const f32x4 (&acc)[2][2][4][2], const pg8::Unit& u, int wr, int wc, int fr, int fq) const {
;     ...
;             for (int m = 0; m < 4; ++m)
; #pragma unroll
;               for (int q = 0; q < 4; ++q) { const float gv = log_forget(acc[ai][bj][m][qh][q], lq[q]); g[m][q] = gv;
;                 float sc = gv; sc += dppx<0x111>(sc); sc += dppx<0x112>(sc); sc += dppx<0x114>(sc); sc += dppx<0x118>(sc);
	v_add_f32_e32 v79, 1.0, v79
	v_cmp_gt_f32_e32 vcc, s37, v79
	v_mov_b32_e32 v77, v77
	s_nop 0
	v_cndmask_b32_e64 v162, 0, 32, vcc
	v_ldexp_f32 v79, v79, v162
	v_log_f32_e32 v79, v79
	v_min_f32_e32 v78, 0, v78
	v_mul_f32_e32 v162, 0x3f317217, v79
	v_fma_f32 v162, v79, s33, -v162
	v_fmac_f32_e32 v162, 0x3377d1cf, v79
	v_fmac_f32_e32 v162, 0x3f317217, v79
	v_cmp_lt_f32_e64 s[44:45], |v79|, s36
	s_nop 1
	v_cndmask_b32_e64 v79, v79, v162, s[44:45]
	v_cndmask_b32_e32 v162, 0, v216, vcc
	v_sub_f32_e32 v162, v79, v162
	s_nop 0
	s_nop 1
	s_nop 0
	s_nop 1
	v_max_f32_e32 v68, v69, v69
	v_min_f32_e32 v79, 0, v68
	v_mul_f32_e64 v68, |v69|, s8
	v_exp_f32_e32 v68, v68
	s_nop 0
	v_add_f32_e32 v68, 1.0, v68
	v_cmp_gt_f32_e32 vcc, s37, v68
	s_nop 1
	v_cndmask_b32_e64 v163, 0, 32, vcc
	v_ldexp_f32 v68, v68, v163
	v_log_f32_e32 v68, v68
	s_nop 0
	v_mul_f32_e32 v163, 0x3f317217, v68
	v_fma_f32 v163, v68, s33, -v163
	v_fmac_f32_e32 v163, 0x3377d1cf, v68
	v_fmac_f32_e32 v163, 0x3f317217, v68
	v_cmp_lt_f32_e64 s[44:45], |v68|, s36
	s_nop 1
	v_cndmask_b32_e64 v68, v68, v163, s[44:45]
	v_cndmask_b32_e32 v163, 0, v216, vcc
	v_sub_f32_e32 v163, v68, v163
	v_pk_add_f32 v[78:79], v[78:79], v[162:163] neg_lo:[0,1] neg_hi:[0,1]
	v_mov_b32_e32 v78, v78
	s_nop 1
	v_mov_b32_dpp v162, v78 row_shr:1 row_mask:0xf bank_mask:0xf bound_ctrl:1
	s_nop 0
	s_nop 0
	s_nop 1
	v_mul_f32_e64 v69, |v70|, s8
	v_exp_f32_e32 v69, v69
	v_max_f32_e32 v68, v70, v70
	v_mov_b32_e32 v79, v79
	v_min_f32_e32 v68, 0, v68
	v_add_f32_e32 v69, 1.0, v69
	v_cmp_gt_f32_e32 vcc, s37, v69
	v_mov_b32_dpp v163, v79 row_shr:1 row_mask:0xf bank_mask:0xf bound_ctrl:1
	v_pk_add_f32 v[162:163], v[78:79], v[162:163]
	v_cndmask_b32_e64 v164, 0, 32, vcc
	v_ldexp_f32 v69, v69, v164
	v_log_f32_e32 v69, v69
	s_nop 0
	v_mul_f32_e32 v164, 0x3f317217, v69
	v_fma_f32 v164, v69, s33, -v164
	v_fmac_f32_e32 v164, 0x3377d1cf, v69
	v_fmac_f32_e32 v164, 0x3f317217, v69
	v_cmp_lt_f32_e64 s[44:45], |v69|, s36
	s_nop 1
	v_cndmask_b32_e64 v69, v69, v164, s[44:45]
	v_cndmask_b32_e32 v164, 0, v216, vcc
	v_sub_f32_e32 v164, v69, v164
	s_nop 0
	s_nop 0
	s_nop 1
	s_nop 0
	s_nop 1
	v_mul_f32_e64 v70, |v71|, s8
	v_exp_f32_e32 v70, v70
	v_max_f32_e32 v69, v71, v71
	v_min_f32_e32 v69, 0, v69
	v_add_f32_e32 v70, 1.0, v70
	v_cmp_gt_f32_e32 vcc, s37, v70
	s_nop 1
	v_cndmask_b32_e64 v165, 0, 32, vcc
	v_ldexp_f32 v70, v70, v165
	v_log_f32_e32 v70, v70
	s_nop 0
	v_mul_f32_e32 v165, 0x3f317217, v70
	v_fma_f32 v165, v70, s33, -v165
	v_fmac_f32_e32 v165, 0x3377d1cf, v70
	v_fmac_f32_e32 v165, 0x3f317217, v70
	v_cmp_lt_f32_e64 s[44:45], |v70|, s36
	s_nop 1
	v_cndmask_b32_e64 v70, v70, v165, s[44:45]
	v_cndmask_b32_e32 v165, 0, v216, vcc
	v_sub_f32_e32 v165, v70, v165
	v_pk_add_f32 v[68:69], v[68:69], v[164:165] neg_lo:[0,1] neg_hi:[0,1]
	v_mov_b32_e32 v68, v68
	s_nop 1
	v_mov_b32_dpp v164, v68 row_shr:1 row_mask:0xf bank_mask:0xf bound_ctrl:1
	s_nop 0
	s_nop 0
	s_nop 1
	v_mul_f32_e64 v71, |v64|, s8
	v_exp_f32_e32 v71, v71
	v_max_f32_e32 v70, v64, v64
	v_add_f32_e32 v71, 1.0, v71
	v_cmp_gt_f32_e32 vcc, s37, v71
	v_mov_b32_e32 v69, v69
	s_nop 0
	v_cndmask_b32_e64 v166, 0, 32, vcc
	v_ldexp_f32 v71, v71, v166
	v_log_f32_e32 v71, v71
	v_mov_b32_dpp v165, v69 row_shr:1 row_mask:0xf bank_mask:0xf bound_ctrl:1
	v_pk_add_f32 v[164:165], v[68:69], v[164:165]
	v_min_f32_e32 v70, 0, v70
	v_mul_f32_e32 v166, 0x3f317217, v71
	v_fma_f32 v166, v71, s33, -v166
	v_fmac_f32_e32 v166, 0x3377d1cf, v71
	v_fmac_f32_e32 v166, 0x3f317217, v71
	v_cmp_lt_f32_e64 s[44:45], |v71|, s36
	s_nop 1
	v_cndmask_b32_e64 v71, v71, v166, s[44:45]
	v_cndmask_b32_e32 v166, 0, v216, vcc
	v_sub_f32_e32 v166, v71, v166
	s_nop 0
	s_nop 1
	s_nop 0
	s_nop 1
	v_max_f32_e32 v64, v65, v65
	v_min_f32_e32 v71, 0, v64
	v_mul_f32_e64 v64, |v65|, s8
	v_exp_f32_e32 v64, v64
	s_nop 0
	v_add_f32_e32 v64, 1.0, v64
	v_cmp_gt_f32_e32 vcc, s37, v64
	s_nop 1
	v_cndmask_b32_e64 v72, 0, 32, vcc
	v_ldexp_f32 v64, v64, v72
	v_log_f32_e32 v64, v64
	s_nop 0
	v_mul_f32_e32 v72, 0x3f317217, v64
	v_fma_f32 v72, v64, s33, -v72
	v_fmac_f32_e32 v72, 0x3377d1cf, v64
	v_fmac_f32_e32 v72, 0x3f317217, v64
	v_cmp_lt_f32_e64 s[44:45], |v64|, s36
	s_nop 1
	v_cndmask_b32_e64 v64, v64, v72, s[44:45]
	v_cndmask_b32_e32 v72, 0, v216, vcc
	v_sub_f32_e32 v167, v64, v72
	v_pk_add_f32 v[70:71], v[70:71], v[166:167] neg_lo:[0,1] neg_hi:[0,1]
	v_mov_b32_e32 v70, v70
	s_nop 1
	v_mov_b32_dpp v166, v70 row_shr:1 row_mask:0xf bank_mask:0xf bound_ctrl:1
	s_nop 0
	s_nop 0
	s_nop 1
	v_mul_f32_e64 v65, |v66|, s8
	v_exp_f32_e32 v65, v65
	v_max_f32_e32 v64, v66, v66
	v_mov_b32_e32 v71, v71
	v_min_f32_e32 v64, 0, v64
	v_add_f32_e32 v65, 1.0, v65
	v_cmp_gt_f32_e32 vcc, s37, v65
	v_mov_b32_dpp v167, v71 row_shr:1 row_mask:0xf bank_mask:0xf bound_ctrl:1
	v_pk_add_f32 v[166:167], v[70:71], v[166:167]
	v_cndmask_b32_e64 v72, 0, 32, vcc
	v_ldexp_f32 v65, v65, v72
	v_log_f32_e32 v65, v65
	s_nop 0
	v_mul_f32_e32 v72, 0x3f317217, v65
	v_fma_f32 v72, v65, s33, -v72
	v_fmac_f32_e32 v72, 0x3377d1cf, v65
	v_fmac_f32_e32 v72, 0x3f317217, v65
	v_cmp_lt_f32_e64 s[44:45], |v65|, s36
	s_nop 1
	v_cndmask_b32_e64 v65, v65, v72, s[44:45]
	v_cndmask_b32_e32 v72, 0, v216, vcc
	v_sub_f32_e32 v72, v65, v72
	s_nop 0
	s_nop 0
	s_nop 1
	s_nop 0
	s_nop 1
	v_mul_f32_e64 v66, |v67|, s8
	v_exp_f32_e32 v66, v66
	v_max_f32_e32 v65, v67, v67
	v_min_f32_e32 v65, 0, v65
	v_add_f32_e32 v66, 1.0, v66
	v_cmp_gt_f32_e32 vcc, s37, v66
	s_nop 1
	v_cndmask_b32_e64 v73, 0, 32, vcc
	v_ldexp_f32 v66, v66, v73
	v_log_f32_e32 v66, v66
	s_nop 0
	v_mul_f32_e32 v73, 0x3f317217, v66
	v_fma_f32 v73, v66, s33, -v73
	v_fmac_f32_e32 v73, 0x3377d1cf, v66
	v_fmac_f32_e32 v73, 0x3f317217, v66
; template <int CTRL> __device__ __forceinline__ float dppx(float v) { return __int_as_float(__builtin_amdgcn_update_dpp(0, __float_as_int(v), CTRL, 0xf, 0xf, true)); }
;   __device__ __forceinline__ void operator()(const f32x4 (&acc)[2][2][4][2], const pg8::Unit& u, int wr, int wc, int fr, int fq) const {
;     ...
;             for (int m = 0; m < 4; ++m)
; #pragma unroll
;               for (int q = 0; q < 4; ++q) { const float gv = log_forget(acc[ai][bj][m][qh][q], lq[q]); g[m][q] = gv;
;                 float sc = gv; sc += dppx<0x111>(sc); sc += dppx<0x112>(sc); sc += dppx<0x114>(sc); sc += dppx<0x118>(sc);
;                 const float tot16 = __int_as_float(__builtin_amdgcn_ds_swizzle(__float_as_int(sc), 0x1F0));
;                 cs[m][q] = sc + carry[q]; carry[q] += tot16; }
; #pragma unroll
;             for (int m = 0; m < 4; ++m) { const int r = row0 + ai * 128 + m * 16; float bq[4], kq[4];
; #pragma unroll
;               for (int q = 0; q < 4; ++q) { bq[q] = bwd ? (carry[q] - cs[m][q]) + g[m][q] : cs[m][q]; kq[q] = 1.f - __expf(g[m][q]); }
	v_cmp_lt_f32_e64 s[44:45], |v66|, s36
	s_nop 1
	v_cndmask_b32_e64 v66, v66, v73, s[44:45]
	v_cndmask_b32_e32 v73, 0, v216, vcc
	v_sub_f32_e32 v73, v66, v73
	v_pk_add_f32 v[64:65], v[64:65], v[72:73] neg_lo:[0,1] neg_hi:[0,1]
	v_mov_b32_e32 v72, v64
	s_nop 1
	v_mov_b32_dpp v64, v72 row_shr:1 row_mask:0xf bank_mask:0xf bound_ctrl:1
	s_nop 0
	s_nop 0
	s_nop 1
	v_pk_add_f32 v[66:67], v[118:119], v[120:121] neg_lo:[0,1] neg_hi:[0,1]
	v_mov_b32_e32 v73, v65
	v_mov_b32_e32 v67, v67
	v_mov_b32_e32 v66, v66
	v_mov_b32_dpp v65, v73 row_shr:1 row_mask:0xf bank_mask:0xf bound_ctrl:1
	v_mov_b32_dpp v75, v67 row_shr:1 row_mask:0xf bank_mask:0xf bound_ctrl:1
	v_mov_b32_dpp v74, v66 row_shr:1 row_mask:0xf bank_mask:0xf bound_ctrl:1
	v_pk_add_f32 v[74:75], v[66:67], v[74:75]
	v_pk_add_f32 v[64:65], v[72:73], v[64:65]
	v_add_u32_e32 v96, 0xfffffc80, v154
	v_mov_b32_dpp v118, v74 row_shr:2 row_mask:0xf bank_mask:0xf bound_ctrl:1
	v_mov_b32_dpp v119, v75 row_shr:2 row_mask:0xf bank_mask:0xf bound_ctrl:1
	v_pk_add_f32 v[74:75], v[74:75], v[118:119]
	s_nop 1
	v_mov_b32_dpp v118, v74 row_shr:4 row_mask:0xf bank_mask:0xf bound_ctrl:1
	v_mov_b32_dpp v119, v75 row_shr:4 row_mask:0xf bank_mask:0xf bound_ctrl:1
	v_pk_add_f32 v[74:75], v[74:75], v[118:119]
	s_nop 1
	v_mov_b32_dpp v118, v74 row_shr:8 row_mask:0xf bank_mask:0xf bound_ctrl:1
	v_mov_b32_dpp v119, v75 row_shr:8 row_mask:0xf bank_mask:0xf bound_ctrl:1
	v_pk_add_f32 v[74:75], v[74:75], v[118:119]
	ds_swizzle_b32 v118, v74 offset:swizzle(BROADCAST,16,15)
	ds_swizzle_b32 v119, v75 offset:swizzle(BROADCAST,16,15)
	v_pk_add_f32 v[74:75], v[74:75], 0 op_sel_hi:[1,0]
	s_waitcnt lgkmcnt(0)
	v_pk_add_f32 v[168:169], v[118:119], 0 op_sel_hi:[1,0]
	v_mul_f32_e32 v118, 0x3fb8aa3b, v66
	v_exp_f32_e32 v118, v118
	v_mov_b32_dpp v119, v81 row_shr:1 row_mask:0xf bank_mask:0xf bound_ctrl:1
	v_sub_f32_e32 v185, 1.0, v118
	v_mul_f32_e32 v118, 0x3fb8aa3b, v67
	v_exp_f32_e32 v118, v118
	s_nop 0
	v_sub_f32_e32 v186, 1.0, v118
	v_mov_b32_dpp v118, v80 row_shr:1 row_mask:0xf bank_mask:0xf bound_ctrl:1
	v_pk_add_f32 v[118:119], v[80:81], v[118:119]
	s_nop 1
	v_mov_b32_dpp v120, v118 row_shr:2 row_mask:0xf bank_mask:0xf bound_ctrl:1
	v_mov_b32_dpp v121, v119 row_shr:2 row_mask:0xf bank_mask:0xf bound_ctrl:1
	v_pk_add_f32 v[118:119], v[118:119], v[120:121]
	s_nop 1
	v_mov_b32_dpp v120, v118 row_shr:4 row_mask:0xf bank_mask:0xf bound_ctrl:1
	v_mov_b32_dpp v121, v119 row_shr:4 row_mask:0xf bank_mask:0xf bound_ctrl:1
	v_pk_add_f32 v[118:119], v[118:119], v[120:121]
	s_nop 1
	v_mov_b32_dpp v120, v118 row_shr:8 row_mask:0xf bank_mask:0xf bound_ctrl:1
	v_mov_b32_dpp v121, v119 row_shr:8 row_mask:0xf bank_mask:0xf bound_ctrl:1
	v_pk_add_f32 v[118:119], v[118:119], v[120:121]
	ds_swizzle_b32 v120, v118 offset:swizzle(BROADCAST,16,15)
	ds_swizzle_b32 v121, v119 offset:swizzle(BROADCAST,16,15)
	v_pk_add_f32 v[118:119], v[118:119], 0 op_sel_hi:[1,0]
	s_waitcnt lgkmcnt(0)
	v_pk_add_f32 v[170:171], v[120:121], 0 op_sel_hi:[1,0]
	v_mul_f32_e32 v120, 0x3fb8aa3b, v80
	v_exp_f32_e32 v120, v120
	v_mov_b32_dpp v121, v83 row_shr:1 row_mask:0xf bank_mask:0xf bound_ctrl:1
	v_sub_f32_e32 v187, 1.0, v120
	v_mul_f32_e32 v120, 0x3fb8aa3b, v81
	v_exp_f32_e32 v120, v120
	s_nop 0
	v_sub_f32_e32 v188, 1.0, v120
	v_mov_b32_dpp v120, v82 row_shr:1 row_mask:0xf bank_mask:0xf bound_ctrl:1
	v_pk_add_f32 v[120:121], v[82:83], v[120:121]
	s_nop 1
	v_mov_b32_dpp v156, v120 row_shr:2 row_mask:0xf bank_mask:0xf bound_ctrl:1
	v_mov_b32_dpp v157, v121 row_shr:2 row_mask:0xf bank_mask:0xf bound_ctrl:1
	v_pk_add_f32 v[120:121], v[120:121], v[156:157]
	s_nop 1
	v_mov_b32_dpp v156, v120 row_shr:4 row_mask:0xf bank_mask:0xf bound_ctrl:1
	v_mov_b32_dpp v157, v121 row_shr:4 row_mask:0xf bank_mask:0xf bound_ctrl:1
	v_pk_add_f32 v[120:121], v[120:121], v[156:157]
	s_nop 1
	v_mov_b32_dpp v156, v120 row_shr:8 row_mask:0xf bank_mask:0xf bound_ctrl:1
	v_mov_b32_dpp v157, v121 row_shr:8 row_mask:0xf bank_mask:0xf bound_ctrl:1
	v_pk_add_f32 v[120:121], v[120:121], v[156:157]
	ds_swizzle_b32 v156, v120 offset:swizzle(BROADCAST,16,15)
	ds_swizzle_b32 v157, v121 offset:swizzle(BROADCAST,16,15)
	v_pk_add_f32 v[120:121], v[168:169], v[120:121]
	s_waitcnt lgkmcnt(0)
	v_pk_add_f32 v[158:159], v[168:169], v[156:157]
	v_mul_f32_e32 v168, 0x3fb8aa3b, v76
	v_exp_f32_e32 v168, v168
	v_mov_b32_dpp v169, v163 row_shr:2 row_mask:0xf bank_mask:0xf bound_ctrl:1
	v_mul_f32_e32 v156, 0x3fb8aa3b, v82
	v_exp_f32_e32 v156, v156
	v_sub_f32_e32 v174, 1.0, v168
	v_mul_f32_e32 v168, 0x3fb8aa3b, v77
	v_exp_f32_e32 v168, v168
	v_sub_f32_e32 v172, 1.0, v156
	v_mul_f32_e32 v156, 0x3fb8aa3b, v83
	v_exp_f32_e32 v156, v156
	v_sub_f32_e32 v175, 1.0, v168
	v_mov_b32_dpp v168, v162 row_shr:2 row_mask:0xf bank_mask:0xf bound_ctrl:1
	v_pk_add_f32 v[162:163], v[162:163], v[168:169]
	v_sub_f32_e32 v173, 1.0, v156
	v_mov_b32_dpp v156, v76 row_shr:1 row_mask:0xf bank_mask:0xf bound_ctrl:1
	v_mov_b32_dpp v168, v162 row_shr:4 row_mask:0xf bank_mask:0xf bound_ctrl:1
	v_mov_b32_dpp v169, v163 row_shr:4 row_mask:0xf bank_mask:0xf bound_ctrl:1
	v_pk_add_f32 v[162:163], v[162:163], v[168:169]
	v_mov_b32_dpp v157, v77 row_shr:1 row_mask:0xf bank_mask:0xf bound_ctrl:1
	v_pk_add_f32 v[156:157], v[76:77], v[156:157]
	v_mov_b32_dpp v168, v162 row_shr:8 row_mask:0xf bank_mask:0xf bound_ctrl:1
	v_mov_b32_dpp v169, v163 row_shr:8 row_mask:0xf bank_mask:0xf bound_ctrl:1
	v_pk_add_f32 v[162:163], v[162:163], v[168:169]
	ds_swizzle_b32 v168, v162 offset:swizzle(BROADCAST,16,15)
	ds_swizzle_b32 v169, v163 offset:swizzle(BROADCAST,16,15)
	v_pk_add_f32 v[162:163], v[158:159], v[162:163]
	v_mov_b32_dpp v160, v156 row_shr:2 row_mask:0xf bank_mask:0xf bound_ctrl:1
	v_mov_b32_dpp v161, v157 row_shr:2 row_mask:0xf bank_mask:0xf bound_ctrl:1
	v_pk_add_f32 v[156:157], v[156:157], v[160:161]
	s_waitcnt lgkmcnt(0)
; template <int CTRL> __device__ __forceinline__ float dppx(float v) { return __int_as_float(__builtin_amdgcn_update_dpp(0, __float_as_int(v), CTRL, 0xf, 0xf, true)); }
; __device__ __forceinline__ unsigned cvt_pk_bf16(float lo, float hi) { unsigned r; asm volatile("v_cvt_pk_bf16_f32 %0, %1, %2" : "=v"(r) : "v"(lo), "v"(hi)); return r; }
;   __device__ __forceinline__ void operator()(const f32x4 (&acc)[2][2][4][2], const pg8::Unit& u, int wr, int wc, int fr, int fq) const {
;     ...
;             for (int m = 0; m < 4; ++m)
; #pragma unroll
;               for (int q = 0; q < 4; ++q) { const float gv = log_forget(acc[ai][bj][m][qh][q], lq[q]); g[m][q] = gv;
;                 float sc = gv; sc += dppx<0x111>(sc); sc += dppx<0x112>(sc); sc += dppx<0x114>(sc); sc += dppx<0x118>(sc);
;                 const float tot16 = __int_as_float(__builtin_amdgcn_ds_swizzle(__float_as_int(sc), 0x1F0));
;                 cs[m][q] = sc + carry[q]; carry[q] += tot16; }
; #pragma unroll
;             for (int m = 0; m < 4; ++m) { const int r = row0 + ai * 128 + m * 16; float bq[4], kq[4];
; #pragma unroll
;               for (int q = 0; q < 4; ++q) { bq[q] = bwd ? (carry[q] - cs[m][q]) + g[m][q] : cs[m][q]; kq[q] = 1.f - __expf(g[m][q]); }
;               *(f32x4*)(logfp + (size_t)r * 1024 + c + 4 * qh) = (f32x4){bq[0], bq[1], bq[2], bq[3]};
;               u32x2 w; w.x = pg8::cvt_pk_bf16(kq[0], kq[1]); w.y = pg8::cvt_pk_bf16(kq[2], kq[3]);
;               *(u32x2*)(km + (size_t)r * 1024 + c + 4 * qh) = w; } } }
	v_pk_add_f32 v[158:159], v[158:159], v[168:169]
	v_mul_f32_e32 v168, 0x3fb8aa3b, v78
	v_exp_f32_e32 v168, v168
	v_mov_b32_dpp v169, v165 row_shr:2 row_mask:0xf bank_mask:0xf bound_ctrl:1
	v_mov_b32_dpp v160, v156 row_shr:4 row_mask:0xf bank_mask:0xf bound_ctrl:1
	v_mov_b32_dpp v161, v157 row_shr:4 row_mask:0xf bank_mask:0xf bound_ctrl:1
	v_sub_f32_e32 v176, 1.0, v168
	v_mul_f32_e32 v168, 0x3fb8aa3b, v79
	v_exp_f32_e32 v168, v168
	v_pk_add_f32 v[156:157], v[156:157], v[160:161]
	v_sub_f32_e32 v177, 1.0, v168
	v_mov_b32_dpp v168, v164 row_shr:2 row_mask:0xf bank_mask:0xf bound_ctrl:1
	v_pk_add_f32 v[164:165], v[164:165], v[168:169]
	v_mov_b32_dpp v160, v156 row_shr:8 row_mask:0xf bank_mask:0xf bound_ctrl:1
	v_mov_b32_dpp v161, v157 row_shr:8 row_mask:0xf bank_mask:0xf bound_ctrl:1
	v_mov_b32_dpp v168, v164 row_shr:4 row_mask:0xf bank_mask:0xf bound_ctrl:1
	v_mov_b32_dpp v169, v165 row_shr:4 row_mask:0xf bank_mask:0xf bound_ctrl:1
	v_pk_add_f32 v[164:165], v[164:165], v[168:169]
	v_pk_add_f32 v[156:157], v[156:157], v[160:161]
	ds_swizzle_b32 v160, v156 offset:swizzle(BROADCAST,16,15)
	v_mov_b32_dpp v168, v164 row_shr:8 row_mask:0xf bank_mask:0xf bound_ctrl:1
	v_mov_b32_dpp v169, v165 row_shr:8 row_mask:0xf bank_mask:0xf bound_ctrl:1
	ds_swizzle_b32 v161, v157 offset:swizzle(BROADCAST,16,15)
	v_pk_add_f32 v[164:165], v[164:165], v[168:169]
	ds_swizzle_b32 v168, v164 offset:swizzle(BROADCAST,16,15)
	ds_swizzle_b32 v169, v165 offset:swizzle(BROADCAST,16,15)
	v_pk_add_f32 v[156:157], v[170:171], v[156:157]
	s_waitcnt lgkmcnt(2)
	v_pk_add_f32 v[160:161], v[170:171], v[160:161]
	s_nop 0
	v_pk_add_f32 v[164:165], v[160:161], v[164:165]
	s_waitcnt lgkmcnt(0)
	v_pk_add_f32 v[160:161], v[160:161], v[168:169]
	v_mul_f32_e32 v168, 0x3fb8aa3b, v68
	v_exp_f32_e32 v168, v168
	v_mov_b32_dpp v169, v167 row_shr:2 row_mask:0xf bank_mask:0xf bound_ctrl:1
	v_sub_f32_e32 v180, 1.0, v168
	v_mul_f32_e32 v168, 0x3fb8aa3b, v69
	v_exp_f32_e32 v168, v168
	s_nop 0
	v_sub_f32_e32 v181, 1.0, v168
	v_mov_b32_dpp v168, v166 row_shr:2 row_mask:0xf bank_mask:0xf bound_ctrl:1
	v_pk_add_f32 v[166:167], v[166:167], v[168:169]
	s_nop 1
	v_mov_b32_dpp v168, v166 row_shr:4 row_mask:0xf bank_mask:0xf bound_ctrl:1
	v_mov_b32_dpp v169, v167 row_shr:4 row_mask:0xf bank_mask:0xf bound_ctrl:1
	v_pk_add_f32 v[166:167], v[166:167], v[168:169]
	s_nop 1
	v_mov_b32_dpp v168, v166 row_shr:8 row_mask:0xf bank_mask:0xf bound_ctrl:1
	v_mov_b32_dpp v169, v167 row_shr:8 row_mask:0xf bank_mask:0xf bound_ctrl:1
	v_pk_add_f32 v[166:167], v[166:167], v[168:169]
	ds_swizzle_b32 v168, v166 offset:swizzle(BROADCAST,16,15)
	ds_swizzle_b32 v169, v167 offset:swizzle(BROADCAST,16,15)
	v_pk_add_f32 v[166:167], v[158:159], v[166:167]
	s_waitcnt lgkmcnt(0)
	v_pk_add_f32 v[158:159], v[158:159], v[168:169]
	v_mul_f32_e32 v168, 0x3fb8aa3b, v70
	v_exp_f32_e32 v168, v168
	v_mov_b32_dpp v169, v65 row_shr:2 row_mask:0xf bank_mask:0xf bound_ctrl:1
	v_sub_f32_e32 v182, 1.0, v168
	v_mul_f32_e32 v168, 0x3fb8aa3b, v71
	v_exp_f32_e32 v168, v168
	s_nop 0
	v_sub_f32_e32 v183, 1.0, v168
	v_mov_b32_dpp v168, v64 row_shr:2 row_mask:0xf bank_mask:0xf bound_ctrl:1
	v_pk_add_f32 v[64:65], v[64:65], v[168:169]
	s_nop 1
	v_mov_b32_dpp v168, v64 row_shr:4 row_mask:0xf bank_mask:0xf bound_ctrl:1
	v_mov_b32_dpp v169, v65 row_shr:4 row_mask:0xf bank_mask:0xf bound_ctrl:1
	v_pk_add_f32 v[64:65], v[64:65], v[168:169]
	s_nop 1
	v_mov_b32_dpp v168, v64 row_shr:8 row_mask:0xf bank_mask:0xf bound_ctrl:1
	v_mov_b32_dpp v169, v65 row_shr:8 row_mask:0xf bank_mask:0xf bound_ctrl:1
	v_pk_add_f32 v[64:65], v[64:65], v[168:169]
	ds_swizzle_b32 v168, v64 offset:swizzle(BROADCAST,16,15)
	ds_swizzle_b32 v169, v65 offset:swizzle(BROADCAST,16,15)
	v_pk_add_f32 v[170:171], v[160:161], v[64:65]
	v_pk_add_f32 v[64:65], v[158:159], v[74:75] neg_lo:[0,1] neg_hi:[0,1]
	s_waitcnt lgkmcnt(0)
	v_pk_add_f32 v[160:161], v[160:161], v[168:169]
	s_nop 0
	v_pk_add_f32 v[168:169], v[160:161], v[118:119] neg_lo:[0,1] neg_hi:[0,1]
	v_pk_add_f32 v[64:65], v[66:67], v[64:65]
	v_pk_add_f32 v[66:67], v[80:81], v[168:169]
	v_cndmask_b32_e64 v65, v75, v65, s[42:43]
	v_cndmask_b32_e64 v67, v119, v67, s[42:43]
	v_cndmask_b32_e64 v66, v118, v66, s[42:43]
	v_cndmask_b32_e64 v64, v74, v64, s[42:43]
	global_store_dwordx4 v[104:105], v[64:67], off offset:16
	s_nop 1
	v_cvt_pk_bf16_f32 v64, v185, v186
	v_cvt_pk_bf16_f32 v65, v187, v188
	global_store_dwordx2 v[102:103], v[64:65], off offset:8
	v_pk_add_f32 v[64:65], v[158:159], v[120:121] neg_lo:[0,1] neg_hi:[0,1]
	v_pk_add_f32 v[66:67], v[160:161], v[156:157] neg_lo:[0,1] neg_hi:[0,1]
	v_pk_add_f32 v[64:65], v[82:83], v[64:65]
	v_pk_add_f32 v[66:67], v[76:77], v[66:67]
	v_cndmask_b32_e64 v65, v121, v65, s[42:43]
	v_cndmask_b32_e64 v67, v157, v67, s[42:43]
	v_cndmask_b32_e64 v66, v156, v66, s[42:43]
	v_cndmask_b32_e64 v64, v120, v64, s[42:43]
	global_store_dwordx4 v[108:109], v[64:67], off offset:16
	s_nop 1
	v_cvt_pk_bf16_f32 v64, v172, v173
	v_cvt_pk_bf16_f32 v65, v174, v175
	global_store_dwordx2 v[106:107], v[64:65], off offset:8
	v_pk_add_f32 v[64:65], v[158:159], v[162:163] neg_lo:[0,1] neg_hi:[0,1]
	v_pk_add_f32 v[66:67], v[160:161], v[164:165] neg_lo:[0,1] neg_hi:[0,1]
	v_pk_add_f32 v[64:65], v[78:79], v[64:65]
	v_pk_add_f32 v[66:67], v[68:69], v[66:67]
	v_cndmask_b32_e64 v65, v163, v65, s[42:43]
	v_cndmask_b32_e64 v67, v165, v67, s[42:43]
	v_cndmask_b32_e64 v66, v164, v66, s[42:43]
	v_cndmask_b32_e64 v64, v162, v64, s[42:43]
	global_store_dwordx4 v[110:111], v[64:67], off offset:16
	v_mul_f32_e32 v69, 0x3fb8aa3b, v73
	v_exp_f32_e32 v69, v69
	v_cvt_pk_bf16_f32 v64, v176, v177
	v_cvt_pk_bf16_f32 v65, v180, v181
	global_store_dwordx2 v[112:113], v[64:65], off offset:8
	v_mul_f32_e32 v64, 0x3fb8aa3b, v72
	v_exp_f32_e32 v64, v64
	v_pk_add_f32 v[66:67], v[160:161], v[170:171] neg_lo:[0,1] neg_hi:[0,1]
	v_sub_f32_e32 v69, 1.0, v69
	v_pk_add_f32 v[66:67], v[72:73], v[66:67]
	v_sub_f32_e32 v68, 1.0, v64
	v_pk_add_f32 v[64:65], v[158:159], v[166:167] neg_lo:[0,1] neg_hi:[0,1]
	v_cndmask_b32_e64 v67, v171, v67, s[42:43]
	v_pk_add_f32 v[64:65], v[70:71], v[64:65]
	v_cndmask_b32_e64 v66, v170, v66, s[42:43]
	v_cndmask_b32_e64 v65, v167, v65, s[42:43]
	v_cndmask_b32_e64 v64, v166, v64, s[42:43]
	global_store_dwordx4 v[114:115], v[64:67], off offset:16
	v_mul_f32_e64 v73, |v60|, s8
	v_exp_f32_e32 v73, v73
	v_cvt_pk_bf16_f32 v64, v182, v183
	v_cvt_pk_bf16_f32 v65, v68, v69
	global_store_dwordx2 v[116:117], v[64:65], off offset:8
	global_load_dwordx4 v[64:67], v155, s[66:67] offset:528
	s_nop 0
	global_load_dwordx4 v[68:71], v155, s[66:67] offset:512
	v_add_f32_e32 v73, 1.0, v73
	v_cmp_gt_f32_e32 vcc, s37, v73
	v_max_f32_e32 v72, v60, v60
	s_nop 0
	v_cndmask_b32_e64 v74, 0, 32, vcc
	v_ldexp_f32 v73, v73, v74
	v_log_f32_e32 v73, v73
	v_min_f32_e32 v72, 0, v72
	v_mul_f32_e32 v74, 0x3f317217, v73
	v_fma_f32 v74, v73, s33, -v74
	v_fmac_f32_e32 v74, 0x3377d1cf, v73
	v_fmac_f32_e32 v74, 0x3f317217, v73
	v_cmp_lt_f32_e64 s[44:45], |v73|, s36
	s_waitcnt vmcnt(1)
; template <int CTRL> __device__ __forceinline__ float dppx(float v) { return __int_as_float(__builtin_amdgcn_update_dpp(0, __float_as_int(v), CTRL, 0xf, 0xf, true)); }
; __device__ __forceinline__ float log_forget(float z, float lb) {
;   const float r0 = fminf(z, 0.f) - __logf(1.f + __expf(-fabsf(z)));
;   __device__ __forceinline__ void operator()(const f32x4 (&acc)[2][2][4][2], const pg8::Unit& u, int wr, int wc, int fr, int fq) const {
;     ...
;             for (int m = 0; m < 4; ++m)
; #pragma unroll
;               for (int q = 0; q < 4; ++q) { const float gv = log_forget(acc[ai][bj][m][qh][q], lq[q]); g[m][q] = gv;
;                 float sc = gv; sc += dppx<0x111>(sc); sc += dppx<0x112>(sc); sc += dppx<0x114>(sc); sc += dppx<0x118>(sc);
;                 const float tot16 = __int_as_float(__builtin_amdgcn_ds_swizzle(__float_as_int(sc), 0x1F0));
;                 cs[m][q] = sc + carry[q]; carry[q] += tot16; }
	s_nop 0
	v_cndmask_b32_e64 v73, v73, v74, s[44:45]
	v_cndmask_b32_e32 v74, 0, v216, vcc
	s_waitcnt vmcnt(0)
	v_sub_f32_e32 v74, v73, v74
	v_sub_f32_e32 v154, 1.0, v71
	v_cmp_ge_f32_e64 s[46:47], 0, v69
	v_cmp_ge_f32_e64 s[56:57], 0, v66
	v_cmp_ge_f32_e64 s[58:59], 0, v67
	s_nop 1
	v_max_f32_e32 v60, v61, v61
	v_min_f32_e32 v73, 0, v60
	v_mul_f32_e64 v60, |v61|, s8
	v_exp_f32_e32 v60, v60
	s_nop 0
	v_add_f32_e32 v60, 1.0, v60
	v_cmp_gt_f32_e32 vcc, s37, v60
	s_nop 1
	v_cndmask_b32_e64 v75, 0, 32, vcc
	v_ldexp_f32 v60, v60, v75
	v_log_f32_e32 v60, v60
	s_nop 0
	v_mul_f32_e32 v75, 0x3f317217, v60
	v_fma_f32 v75, v60, s33, -v75
	v_fmac_f32_e32 v75, 0x3377d1cf, v60
	v_fmac_f32_e32 v75, 0x3f317217, v60
	v_cmp_lt_f32_e64 s[44:45], |v60|, s36
	s_nop 1
	v_cndmask_b32_e64 v60, v60, v75, s[44:45]
	v_cndmask_b32_e32 v75, 0, v216, vcc
	v_sub_f32_e32 v75, v60, v75
	s_nop 0
	s_nop 0
	s_nop 1
	s_nop 0
	s_nop 1
	v_mul_f32_e64 v61, |v62|, s8
	v_exp_f32_e32 v61, v61
	v_max_f32_e32 v60, v62, v62
	v_min_f32_e32 v60, 0, v60
	v_add_f32_e32 v61, 1.0, v61
	v_cmp_gt_f32_e32 vcc, s37, v61
	s_nop 1
	v_cndmask_b32_e64 v76, 0, 32, vcc
	v_ldexp_f32 v61, v61, v76
	v_log_f32_e32 v61, v61
	s_nop 0
	v_mul_f32_e32 v76, 0x3f317217, v61
	v_fma_f32 v76, v61, s33, -v76
	v_fmac_f32_e32 v76, 0x3377d1cf, v61
	v_fmac_f32_e32 v76, 0x3f317217, v61
	v_cmp_lt_f32_e64 s[44:45], |v61|, s36
	s_nop 1
	v_cndmask_b32_e64 v61, v61, v76, s[44:45]
	v_cndmask_b32_e32 v76, 0, v216, vcc
	v_sub_f32_e32 v76, v61, v76
	s_nop 0
	s_nop 0
	s_nop 1
	s_nop 0
	s_nop 1
	v_mul_f32_e64 v62, |v63|, s8
	v_exp_f32_e32 v62, v62
	v_max_f32_e32 v61, v63, v63
	v_min_f32_e32 v61, 0, v61
	v_add_f32_e32 v62, 1.0, v62
	v_cmp_gt_f32_e32 vcc, s37, v62
	s_nop 1
	v_cndmask_b32_e64 v77, 0, 32, vcc
	v_ldexp_f32 v62, v62, v77
	v_log_f32_e32 v62, v62
	s_nop 0
	v_mul_f32_e32 v77, 0x3f317217, v62
	v_fma_f32 v77, v62, s33, -v77
	v_fmac_f32_e32 v77, 0x3377d1cf, v62
	v_fmac_f32_e32 v77, 0x3f317217, v62
	v_cmp_lt_f32_e64 s[44:45], |v62|, s36
	s_nop 1
	v_cndmask_b32_e64 v62, v62, v77, s[44:45]
	v_cndmask_b32_e32 v77, 0, v216, vcc
	v_sub_f32_e32 v77, v62, v77
	s_nop 0
	s_nop 0
	s_nop 1
	s_nop 0
	s_nop 1
	v_mul_f32_e64 v63, |v56|, s8
	v_exp_f32_e32 v63, v63
	v_max_f32_e32 v62, v56, v56
	v_add_f32_e32 v63, 1.0, v63
	v_cmp_gt_f32_e32 vcc, s37, v63
	v_min_f32_e32 v62, 0, v62
	s_nop 0
	v_cndmask_b32_e64 v78, 0, 32, vcc
	v_ldexp_f32 v63, v63, v78
	v_log_f32_e32 v63, v63
	s_nop 0
	v_mul_f32_e32 v78, 0x3f317217, v63
	v_fma_f32 v78, v63, s33, -v78
	v_fmac_f32_e32 v78, 0x3377d1cf, v63
	v_fmac_f32_e32 v78, 0x3f317217, v63
	v_cmp_lt_f32_e64 s[44:45], |v63|, s36
	s_nop 1
	v_cndmask_b32_e64 v63, v63, v78, s[44:45]
	v_cndmask_b32_e32 v78, 0, v216, vcc
	v_sub_f32_e32 v78, v63, v78
	s_nop 0
	s_nop 1
	s_nop 0
	s_nop 1
	v_max_f32_e32 v56, v57, v57
	v_min_f32_e32 v63, 0, v56
	v_mul_f32_e64 v56, |v57|, s8
	v_exp_f32_e32 v56, v56
	s_nop 0
	v_add_f32_e32 v56, 1.0, v56
	v_cmp_gt_f32_e32 vcc, s37, v56
	s_nop 1
	v_cndmask_b32_e64 v79, 0, 32, vcc
	v_ldexp_f32 v56, v56, v79
	v_log_f32_e32 v56, v56
	s_nop 0
	v_mul_f32_e32 v79, 0x3f317217, v56
	v_fma_f32 v79, v56, s33, -v79
	v_fmac_f32_e32 v79, 0x3377d1cf, v56
	v_fmac_f32_e32 v79, 0x3f317217, v56
	v_cmp_lt_f32_e64 s[44:45], |v56|, s36
	s_nop 1
	v_cndmask_b32_e64 v56, v56, v79, s[44:45]
	v_cndmask_b32_e32 v79, 0, v216, vcc
	v_sub_f32_e32 v79, v56, v79
	v_pk_add_f32 v[62:63], v[62:63], v[78:79] neg_lo:[0,1] neg_hi:[0,1]
	s_nop 0
	s_nop 1
	s_nop 0
	s_nop 1
	v_mul_f32_e64 v57, |v58|, s8
	v_exp_f32_e32 v57, v57
	v_max_f32_e32 v56, v58, v58
	v_mov_b32_e32 v79, v63
	v_min_f32_e32 v56, 0, v56
	v_add_f32_e32 v57, 1.0, v57
	v_cmp_gt_f32_e32 vcc, s37, v57
	v_mov_b32_dpp v63, v79 row_shr:1 row_mask:0xf bank_mask:0xf bound_ctrl:1
	s_nop 0
	v_cndmask_b32_e64 v80, 0, 32, vcc
	v_ldexp_f32 v57, v57, v80
	v_log_f32_e32 v57, v57
	s_nop 0
	v_mul_f32_e32 v80, 0x3f317217, v57
	v_fma_f32 v80, v57, s33, -v80
	v_fmac_f32_e32 v80, 0x3377d1cf, v57
	v_fmac_f32_e32 v80, 0x3f317217, v57
	v_cmp_lt_f32_e64 s[44:45], |v57|, s36
	s_nop 1
	v_cndmask_b32_e64 v57, v57, v80, s[44:45]
	v_cndmask_b32_e32 v80, 0, v216, vcc
	v_sub_f32_e32 v80, v57, v80
	s_nop 0
	s_nop 0
	v_mul_f32_e64 v81, |v59|, s8
	v_exp_f32_e32 v81, v81
	s_nop 0
	v_add_f32_e32 v81, 1.0, v81
	s_nop 1
	v_cmp_gt_f32_e32 vcc, s37, v81
	v_max_f32_e32 v57, v59, v59
	s_nop 0
	v_cndmask_b32_e64 v82, 0, 32, vcc
	v_ldexp_f32 v81, v81, v82
	v_log_f32_e32 v81, v81
	v_min_f32_e32 v57, 0, v57
	v_mul_f32_e32 v82, 0x3f317217, v81
	v_fma_f32 v82, v81, s33, -v82
	v_fmac_f32_e32 v82, 0x3377d1cf, v81
	v_fmac_f32_e32 v82, 0x3f317217, v81
	v_cmp_lt_f32_e64 s[44:45], |v81|, s36
	s_nop 0
	s_nop 0
	v_cndmask_b32_e64 v81, v81, v82, s[44:45]
	v_cndmask_b32_e32 v82, 0, v216, vcc
	v_sub_f32_e32 v81, v81, v82
	v_pk_add_f32 v[56:57], v[56:57], v[80:81] neg_lo:[0,1] neg_hi:[0,1]
	v_mul_f32_e64 v83, |v52|, s8
	v_exp_f32_e32 v83, v83
	s_nop 0
	v_add_f32_e32 v83, 1.0, v83
	v_mov_b32_e32 v80, v56
	s_nop 1
	v_mov_b32_dpp v56, v80 row_shr:1 row_mask:0xf bank_mask:0xf bound_ctrl:1
	s_nop 0
	v_cmp_gt_f32_e32 vcc, s37, v83
	v_max_f32_e32 v82, v52, v52
	s_nop 0
	v_cndmask_b32_e64 v102, 0, 32, vcc
	v_ldexp_f32 v83, v83, v102
	v_log_f32_e32 v83, v83
	v_min_f32_e32 v82, 0, v82
	v_mul_f32_e32 v102, 0x3f317217, v83
	v_fma_f32 v102, v83, s33, -v102
	v_fmac_f32_e32 v102, 0x3377d1cf, v83
	v_fmac_f32_e32 v102, 0x3f317217, v83
	v_cmp_lt_f32_e64 s[44:45], |v83|, s36
	v_mov_b32_e32 v81, v57
	s_nop 0
	v_cndmask_b32_e64 v83, v83, v102, s[44:45]
	v_cndmask_b32_e32 v102, 0, v216, vcc
	v_sub_f32_e32 v102, v83, v102
	v_mov_b32_dpp v57, v81 row_shr:1 row_mask:0xf bank_mask:0xf bound_ctrl:1
	v_pk_add_f32 v[56:57], v[80:81], v[56:57]
	s_nop 1
; template <int CTRL> __device__ __forceinline__ float dppx(float v) { return __int_as_float(__builtin_amdgcn_update_dpp(0, __float_as_int(v), CTRL, 0xf, 0xf, true)); }
; __device__ __forceinline__ float log_forget(float z, float lb) {
;   const float r0 = fminf(z, 0.f) - __logf(1.f + __expf(-fabsf(z)));
;   __device__ __forceinline__ void operator()(const f32x4 (&acc)[2][2][4][2], const pg8::Unit& u, int wr, int wc, int fr, int fq) const {
;     ...
;             for (int m = 0; m < 4; ++m)
; #pragma unroll
;               for (int q = 0; q < 4; ++q) { const float gv = log_forget(acc[ai][bj][m][qh][q], lq[q]); g[m][q] = gv;
;                 float sc = gv; sc += dppx<0x111>(sc); sc += dppx<0x112>(sc); sc += dppx<0x114>(sc); sc += dppx<0x118>(sc);
;                 const float tot16 = __int_as_float(__builtin_amdgcn_ds_swizzle(__float_as_int(sc), 0x1F0));
;                 cs[m][q] = sc + carry[q]; carry[q] += tot16; }
	v_mov_b32_dpp v58, v56 row_shr:2 row_mask:0xf bank_mask:0xf bound_ctrl:1
	v_mov_b32_dpp v59, v57 row_shr:2 row_mask:0xf bank_mask:0xf bound_ctrl:1
	v_pk_add_f32 v[56:57], v[56:57], v[58:59]
	s_nop 1
	v_mov_b32_dpp v58, v56 row_shr:4 row_mask:0xf bank_mask:0xf bound_ctrl:1
	v_mov_b32_dpp v59, v57 row_shr:4 row_mask:0xf bank_mask:0xf bound_ctrl:1
	v_max_f32_e32 v52, v53, v53
	v_min_f32_e32 v83, 0, v52
	v_mul_f32_e64 v52, |v53|, s8
	v_exp_f32_e32 v52, v52
	v_pk_add_f32 v[56:57], v[56:57], v[58:59]
	v_add_f32_e32 v52, 1.0, v52
	v_cmp_gt_f32_e32 vcc, s37, v52
	v_mov_b32_dpp v58, v56 row_shr:8 row_mask:0xf bank_mask:0xf bound_ctrl:1
	v_mov_b32_dpp v59, v57 row_shr:8 row_mask:0xf bank_mask:0xf bound_ctrl:1
	v_cndmask_b32_e64 v103, 0, 32, vcc
	v_ldexp_f32 v52, v52, v103
	v_log_f32_e32 v52, v52
	v_pk_add_f32 v[56:57], v[56:57], v[58:59]
	ds_swizzle_b32 v58, v56 offset:swizzle(BROADCAST,16,15)
	ds_swizzle_b32 v59, v57 offset:swizzle(BROADCAST,16,15)
	v_mul_f32_e32 v103, 0x3f317217, v52
	v_fma_f32 v103, v52, s33, -v103
	v_fmac_f32_e32 v103, 0x3377d1cf, v52
	v_fmac_f32_e32 v103, 0x3f317217, v52
	v_cmp_lt_f32_e64 s[44:45], |v52|, s36
	s_nop 1
	v_cndmask_b32_e64 v52, v52, v103, s[44:45]
	v_cndmask_b32_e32 v103, 0, v216, vcc
	v_sub_f32_e32 v103, v52, v103
	v_pk_add_f32 v[82:83], v[82:83], v[102:103] neg_lo:[0,1] neg_hi:[0,1]
	s_nop 0
	s_nop 1
	s_nop 0
	s_nop 1
	v_max_f32_e32 v52, v54, v54
	v_min_f32_e32 v104, 0, v52
	v_mul_f32_e64 v52, |v54|, s8
	v_exp_f32_e32 v52, v52
	v_mov_b32_e32 v83, v83
	v_add_f32_e32 v52, 1.0, v52
	v_cmp_gt_f32_e32 vcc, s37, v52
	v_mov_b32_dpp v103, v83 row_shr:1 row_mask:0xf bank_mask:0xf bound_ctrl:1
	s_nop 0
	v_cndmask_b32_e64 v53, 0, 32, vcc
	v_ldexp_f32 v52, v52, v53
	v_log_f32_e32 v52, v52
	s_nop 0
	v_mul_f32_e32 v53, 0x3f317217, v52
	v_fma_f32 v53, v52, s33, -v53
	v_fmac_f32_e32 v53, 0x3377d1cf, v52
	v_fmac_f32_e32 v53, 0x3f317217, v52
	v_cmp_lt_f32_e64 s[44:45], |v52|, s36
	s_nop 1
	v_cndmask_b32_e64 v52, v52, v53, s[44:45]
	v_cndmask_b32_e32 v53, 0, v216, vcc
	v_sub_f32_e32 v106, v52, v53
	s_nop 0
	s_nop 0
	s_nop 1
	s_nop 0
	s_nop 1
	v_max_f32_e32 v52, v55, v55
	v_min_f32_e32 v105, 0, v52
	v_mul_f32_e64 v52, |v55|, s8
	v_exp_f32_e32 v52, v52
	s_nop 0
	v_add_f32_e32 v52, 1.0, v52
	v_cmp_gt_f32_e32 vcc, s37, v52
	s_nop 1
	v_cndmask_b32_e64 v53, 0, 32, vcc
	v_ldexp_f32 v52, v52, v53
	v_log_f32_e32 v52, v52
	s_nop 0
	v_mul_f32_e32 v53, 0x3f317217, v52
	v_fma_f32 v53, v52, s33, -v53
	v_fmac_f32_e32 v53, 0x3377d1cf, v52
	v_fmac_f32_e32 v53, 0x3f317217, v52
	v_cmp_lt_f32_e64 s[44:45], |v52|, s36
	s_nop 1
	v_cndmask_b32_e64 v52, v52, v53, s[44:45]
	v_cndmask_b32_e32 v53, 0, v216, vcc
	v_sub_f32_e32 v107, v52, v53
	s_nop 0
	s_nop 0
	s_nop 1
	s_nop 0
	s_nop 1
	v_max_f32_e32 v52, v48, v48
	v_min_f32_e32 v108, 0, v52
	v_mul_f32_e64 v52, |v48|, s8
	v_exp_f32_e32 v52, v52
	s_nop 0
	v_add_f32_e32 v52, 1.0, v52
	v_cmp_gt_f32_e32 vcc, s37, v52
	s_nop 0
	s_nop 0
	v_cndmask_b32_e64 v53, 0, 32, vcc
	v_ldexp_f32 v52, v52, v53
	v_log_f32_e32 v52, v52
	s_nop 0
	v_mul_f32_e32 v53, 0x3f317217, v52
	v_fma_f32 v53, v52, s33, -v53
	v_fmac_f32_e32 v53, 0x3377d1cf, v52
	v_fmac_f32_e32 v53, 0x3f317217, v52
	v_cmp_lt_f32_e64 s[44:45], |v52|, s36
	s_nop 1
	v_cndmask_b32_e64 v52, v52, v53, s[44:45]
	v_cndmask_b32_e32 v53, 0, v216, vcc
	v_sub_f32_e32 v110, v52, v53
	s_nop 0
	s_nop 1
	s_nop 0
	s_nop 1
	v_max_f32_e32 v48, v49, v49
	v_min_f32_e32 v109, 0, v48
	v_mul_f32_e64 v48, |v49|, s8
	v_exp_f32_e32 v48, v48
	s_nop 0
	v_add_f32_e32 v48, 1.0, v48
	v_cmp_gt_f32_e32 vcc, s37, v48
	s_nop 1
	v_cndmask_b32_e64 v52, 0, 32, vcc
	v_ldexp_f32 v48, v48, v52
	v_log_f32_e32 v48, v48
	s_nop 0
	v_mul_f32_e32 v52, 0x3f317217, v48
	v_fma_f32 v52, v48, s33, -v52
	v_fmac_f32_e32 v52, 0x3377d1cf, v48
	v_fmac_f32_e32 v52, 0x3f317217, v48
	v_cmp_lt_f32_e64 s[44:45], |v48|, s36
	s_nop 1
	v_cndmask_b32_e64 v48, v48, v52, s[44:45]
	v_cndmask_b32_e32 v52, 0, v216, vcc
	v_sub_f32_e32 v111, v48, v52
	v_pk_add_f32 v[108:109], v[108:109], v[110:111] neg_lo:[0,1] neg_hi:[0,1]
	s_nop 0
	s_nop 1
	s_nop 0
	s_nop 1
	v_max_f32_e32 v48, v50, v50
	v_min_f32_e32 v112, 0, v48
	v_mul_f32_e64 v48, |v50|, s8
	v_exp_f32_e32 v48, v48
	v_mov_b32_e32 v109, v109
	v_add_f32_e32 v48, 1.0, v48
	v_cmp_gt_f32_e32 vcc, s37, v48
	v_mov_b32_dpp v111, v109 row_shr:1 row_mask:0xf bank_mask:0xf bound_ctrl:1
	s_nop 0
	v_cndmask_b32_e64 v49, 0, 32, vcc
	v_ldexp_f32 v48, v48, v49
	v_log_f32_e32 v48, v48
	s_nop 0
	v_mul_f32_e32 v49, 0x3f317217, v48
	v_fma_f32 v49, v48, s33, -v49
	v_fmac_f32_e32 v49, 0x3377d1cf, v48
	v_fmac_f32_e32 v49, 0x3f317217, v48
	v_cmp_lt_f32_e64 s[44:45], |v48|, s36
	s_nop 1
	v_cndmask_b32_e64 v48, v48, v49, s[44:45]
	v_cndmask_b32_e32 v49, 0, v216, vcc
	v_sub_f32_e32 v114, v48, v49
	s_nop 0
	s_nop 0
	s_nop 1
	s_nop 0
	s_nop 1
	v_max_f32_e32 v48, v51, v51
	v_min_f32_e32 v113, 0, v48
	v_mul_f32_e64 v48, |v51|, s8
	v_exp_f32_e32 v48, v48
	s_nop 0
	v_add_f32_e32 v48, 1.0, v48
	v_cmp_gt_f32_e32 vcc, s37, v48
	s_nop 1
	v_cndmask_b32_e64 v49, 0, 32, vcc
	v_ldexp_f32 v48, v48, v49
	v_log_f32_e32 v48, v48
	s_nop 0
	v_mul_f32_e32 v49, 0x3f317217, v48
	v_fma_f32 v49, v48, s33, -v49
	v_fmac_f32_e32 v49, 0x3377d1cf, v48
	v_fmac_f32_e32 v49, 0x3f317217, v48
	v_cmp_lt_f32_e64 s[44:45], |v48|, s36
	s_nop 1
	v_cndmask_b32_e64 v48, v48, v49, s[44:45]
	v_cndmask_b32_e32 v49, 0, v216, vcc
	v_sub_f32_e32 v115, v48, v49
	v_pk_add_f32 v[112:113], v[112:113], v[114:115] neg_lo:[0,1] neg_hi:[0,1]
	v_mov_b32_e32 v112, v112
	s_nop 1
	v_mov_b32_dpp v114, v112 row_shr:1 row_mask:0xf bank_mask:0xf bound_ctrl:1
	s_nop 0
	s_nop 0
	s_nop 1
	v_pk_add_f32 v[48:49], v[72:73], v[74:75] neg_lo:[0,1] neg_hi:[0,1]
; template <int CTRL> __device__ __forceinline__ float dppx(float v) { return __int_as_float(__builtin_amdgcn_update_dpp(0, __float_as_int(v), CTRL, 0xf, 0xf, true)); }
;   __device__ __forceinline__ void operator()(const f32x4 (&acc)[2][2][4][2], const pg8::Unit& u, int wr, int wc, int fr, int fq) const {
;     ...
;             for (int m = 0; m < 4; ++m)
; #pragma unroll
;               for (int q = 0; q < 4; ++q) { const float gv = log_forget(acc[ai][bj][m][qh][q], lq[q]); g[m][q] = gv;
;                 float sc = gv; sc += dppx<0x111>(sc); sc += dppx<0x112>(sc); sc += dppx<0x114>(sc); sc += dppx<0x118>(sc);
;                 const float tot16 = __int_as_float(__builtin_amdgcn_ds_swizzle(__float_as_int(sc), 0x1F0));
;                 cs[m][q] = sc + carry[q]; carry[q] += tot16; }
; #pragma unroll
;             for (int m = 0; m < 4; ++m) { const int r = row0 + ai * 128 + m * 16; float bq[4], kq[4];
; #pragma unroll
;               for (int q = 0; q < 4; ++q) { bq[q] = bwd ? (carry[q] - cs[m][q]) + g[m][q] : cs[m][q]; kq[q] = 1.f - __expf(g[m][q]); }
	v_mov_b32_e32 v73, v49
	v_mov_b32_e32 v113, v113
	v_mov_b32_e32 v72, v48
	v_mov_b32_dpp v49, v73 row_shr:1 row_mask:0xf bank_mask:0xf bound_ctrl:1
	v_mov_b32_e32 v78, v62
	v_mov_b32_dpp v48, v72 row_shr:1 row_mask:0xf bank_mask:0xf bound_ctrl:1
	v_pk_add_f32 v[48:49], v[72:73], v[48:49]
	v_mov_b32_dpp v62, v78 row_shr:1 row_mask:0xf bank_mask:0xf bound_ctrl:1
	v_mov_b32_e32 v82, v82
	v_mov_b32_dpp v50, v48 row_shr:2 row_mask:0xf bank_mask:0xf bound_ctrl:1
	v_mov_b32_dpp v51, v49 row_shr:2 row_mask:0xf bank_mask:0xf bound_ctrl:1
	v_pk_add_f32 v[48:49], v[48:49], v[50:51]
	v_pk_add_f32 v[62:63], v[78:79], v[62:63]
	v_mov_b32_dpp v102, v82 row_shr:1 row_mask:0xf bank_mask:0xf bound_ctrl:1
	v_mov_b32_dpp v50, v48 row_shr:4 row_mask:0xf bank_mask:0xf bound_ctrl:1
	v_mov_b32_dpp v51, v49 row_shr:4 row_mask:0xf bank_mask:0xf bound_ctrl:1
	v_pk_add_f32 v[48:49], v[48:49], v[50:51]
	v_pk_add_f32 v[102:103], v[82:83], v[102:103]
	v_mov_b32_e32 v108, v108
	v_mov_b32_dpp v50, v48 row_shr:8 row_mask:0xf bank_mask:0xf bound_ctrl:1
	v_mov_b32_dpp v51, v49 row_shr:8 row_mask:0xf bank_mask:0xf bound_ctrl:1
	v_pk_add_f32 v[48:49], v[48:49], v[50:51]
	ds_swizzle_b32 v50, v48 offset:swizzle(BROADCAST,16,15)
	v_pk_add_f32 v[74:75], v[48:49], 0 op_sel_hi:[1,0]
	v_mul_f32_e32 v48, 0x3fb8aa3b, v72
	v_exp_f32_e32 v48, v48
	ds_swizzle_b32 v51, v49 offset:swizzle(BROADCAST,16,15)
	v_mov_b32_dpp v110, v108 row_shr:1 row_mask:0xf bank_mask:0xf bound_ctrl:1
	v_pk_add_f32 v[110:111], v[108:109], v[110:111]
	v_sub_f32_e32 v168, 1.0, v48
	v_mul_f32_e32 v48, 0x3fb8aa3b, v73
	v_exp_f32_e32 v48, v48
	s_waitcnt lgkmcnt(0)
	v_pk_add_f32 v[166:167], v[50:51], 0 op_sel_hi:[1,0]
	v_mov_b32_dpp v115, v113 row_shr:1 row_mask:0xf bank_mask:0xf bound_ctrl:1
	v_pk_add_f32 v[114:115], v[112:113], v[114:115]
	v_sub_f32_e32 v169, 1.0, v48
	v_pk_add_f32 v[48:49], v[60:61], v[76:77] neg_lo:[0,1] neg_hi:[0,1]
	s_nop 0
	v_mov_b32_e32 v77, v49
	v_mov_b32_e32 v76, v48
	v_mov_b32_dpp v118, v62 row_shr:2 row_mask:0xf bank_mask:0xf bound_ctrl:1
	v_mov_b32_dpp v49, v77 row_shr:1 row_mask:0xf bank_mask:0xf bound_ctrl:1
	v_mov_b32_dpp v48, v76 row_shr:1 row_mask:0xf bank_mask:0xf bound_ctrl:1
	v_pk_add_f32 v[48:49], v[76:77], v[48:49]
	v_mov_b32_dpp v119, v63 row_shr:2 row_mask:0xf bank_mask:0xf bound_ctrl:1
	v_pk_add_f32 v[62:63], v[62:63], v[118:119]
	v_mov_b32_dpp v50, v48 row_shr:2 row_mask:0xf bank_mask:0xf bound_ctrl:1
	v_mov_b32_dpp v51, v49 row_shr:2 row_mask:0xf bank_mask:0xf bound_ctrl:1
	v_pk_add_f32 v[48:49], v[48:49], v[50:51]
	v_mov_b32_dpp v118, v62 row_shr:4 row_mask:0xf bank_mask:0xf bound_ctrl:1
	v_mov_b32_dpp v119, v63 row_shr:4 row_mask:0xf bank_mask:0xf bound_ctrl:1
	v_mov_b32_dpp v50, v48 row_shr:4 row_mask:0xf bank_mask:0xf bound_ctrl:1
	v_mov_b32_dpp v51, v49 row_shr:4 row_mask:0xf bank_mask:0xf bound_ctrl:1
	v_pk_add_f32 v[48:49], v[48:49], v[50:51]
	v_pk_add_f32 v[62:63], v[62:63], v[118:119]
	s_nop 0
	v_mov_b32_dpp v50, v48 row_shr:8 row_mask:0xf bank_mask:0xf bound_ctrl:1
	v_mov_b32_dpp v51, v49 row_shr:8 row_mask:0xf bank_mask:0xf bound_ctrl:1
	v_pk_add_f32 v[48:49], v[48:49], v[50:51]
	ds_swizzle_b32 v50, v48 offset:swizzle(BROADCAST,16,15)
	ds_swizzle_b32 v51, v49 offset:swizzle(BROADCAST,16,15)
	v_mov_b32_dpp v118, v62 row_shr:8 row_mask:0xf bank_mask:0xf bound_ctrl:1
	v_mov_b32_dpp v119, v63 row_shr:8 row_mask:0xf bank_mask:0xf bound_ctrl:1
	v_pk_add_f32 v[62:63], v[62:63], v[118:119]
	ds_swizzle_b32 v120, v62 offset:swizzle(BROADCAST,16,15)
	s_waitcnt lgkmcnt(1)
	v_pk_add_f32 v[60:61], v[50:51], 0 op_sel_hi:[1,0]
	v_lshlrev_b64 v[50:51], 2, v[96:97]
	v_lshl_add_u64 v[54:55], v[122:123], 0, v[50:51]
	v_mov_b32_dpp v122, v102 row_shr:2 row_mask:0xf bank_mask:0xf bound_ctrl:1
	v_mov_b32_dpp v123, v103 row_shr:2 row_mask:0xf bank_mask:0xf bound_ctrl:1
	v_pk_add_f32 v[102:103], v[102:103], v[122:123]
	ds_swizzle_b32 v121, v63 offset:swizzle(BROADCAST,16,15)
	v_pk_add_f32 v[118:119], v[166:167], v[62:63]
	v_mov_b32_dpp v122, v102 row_shr:4 row_mask:0xf bank_mask:0xf bound_ctrl:1
	v_mov_b32_dpp v123, v103 row_shr:4 row_mask:0xf bank_mask:0xf bound_ctrl:1
	v_pk_add_f32 v[102:103], v[102:103], v[122:123]
	s_waitcnt lgkmcnt(0)
	v_pk_add_f32 v[62:63], v[166:167], v[120:121]
	v_mul_f32_e32 v120, 0x3fb8aa3b, v79
	v_mov_b32_dpp v122, v102 row_shr:8 row_mask:0xf bank_mask:0xf bound_ctrl:1
	v_mov_b32_dpp v123, v103 row_shr:8 row_mask:0xf bank_mask:0xf bound_ctrl:1
	v_pk_add_f32 v[102:103], v[102:103], v[122:123]
	ds_swizzle_b32 v122, v102 offset:swizzle(BROADCAST,16,15)
	ds_swizzle_b32 v123, v103 offset:swizzle(BROADCAST,16,15)
	v_exp_f32_e32 v120, v120
	v_pk_add_f32 v[102:103], v[62:63], v[102:103]
	v_pk_add_f32 v[116:117], v[48:49], 0 op_sel_hi:[1,0]
	v_mul_f32_e32 v48, 0x3fb8aa3b, v76
	s_waitcnt lgkmcnt(0)
; __device__ __forceinline__ unsigned cvt_pk_bf16(float lo, float hi) { unsigned r; asm volatile("v_cvt_pk_bf16_f32 %0, %1, %2" : "=v"(r) : "v"(lo), "v"(hi)); return r; }
;   __device__ __forceinline__ void operator()(const f32x4 (&acc)[2][2][4][2], const pg8::Unit& u, int wr, int wc, int fr, int fq) const {
;     ...
;             for (int m = 0; m < 4; ++m) { const int r = row0 + ai * 128 + m * 16; float bq[4], kq[4];
; #pragma unroll
;               for (int q = 0; q < 4; ++q) { bq[q] = bwd ? (carry[q] - cs[m][q]) + g[m][q] : cs[m][q]; kq[q] = 1.f - __expf(g[m][q]); }
;               *(f32x4*)(logfp + (size_t)r * 1024 + c + 4 * qh) = (f32x4){bq[0], bq[1], bq[2], bq[3]};
;               u32x2 w; w.x = pg8::cvt_pk_bf16(kq[0], kq[1]); w.y = pg8::cvt_pk_bf16(kq[2], kq[3]);
;               *(u32x2*)(km + (size_t)r * 1024 + c + 4 * qh) = w; } } }
	v_pk_add_f32 v[122:123], v[62:63], v[122:123]
	v_mul_f32_e32 v62, 0x3fb8aa3b, v82
	v_exp_f32_e32 v62, v62
	v_sub_f32_e32 v166, 1.0, v120
	v_pk_add_f32 v[120:121], v[60:61], v[56:57]
	v_pk_add_f32 v[60:61], v[60:61], v[58:59]
	v_lshl_add_u64 v[58:59], v[126:127], 0, v[50:51]
	v_mov_b32_dpp v126, v110 row_shr:2 row_mask:0xf bank_mask:0xf bound_ctrl:1
	v_mov_b32_dpp v127, v111 row_shr:2 row_mask:0xf bank_mask:0xf bound_ctrl:1
	v_sub_f32_e32 v158, 1.0, v62
	v_mul_f32_e32 v62, 0x3fb8aa3b, v83
	v_pk_add_f32 v[110:111], v[110:111], v[126:127]
	v_exp_f32_e32 v62, v62
	v_exp_f32_e32 v48, v48
	v_mov_b32_dpp v126, v110 row_shr:4 row_mask:0xf bank_mask:0xf bound_ctrl:1
	v_mov_b32_dpp v127, v111 row_shr:4 row_mask:0xf bank_mask:0xf bound_ctrl:1
	v_pk_add_f32 v[110:111], v[110:111], v[126:127]
	v_sub_f32_e32 v159, 1.0, v62
	v_pk_add_f32 v[62:63], v[104:105], v[106:107] neg_lo:[0,1] neg_hi:[0,1]
	v_mov_b32_dpp v126, v110 row_shr:8 row_mask:0xf bank_mask:0xf bound_ctrl:1
	v_mov_b32_dpp v127, v111 row_shr:8 row_mask:0xf bank_mask:0xf bound_ctrl:1
	v_pk_add_f32 v[110:111], v[110:111], v[126:127]
	ds_swizzle_b32 v126, v110 offset:swizzle(BROADCAST,16,15)
	ds_swizzle_b32 v127, v111 offset:swizzle(BROADCAST,16,15)
	v_mov_b32_e32 v105, v63
	v_mov_b32_e32 v104, v62
	v_sub_f32_e32 v170, 1.0, v48
	v_mov_b32_dpp v63, v105 row_shr:1 row_mask:0xf bank_mask:0xf bound_ctrl:1
	v_mov_b32_dpp v62, v104 row_shr:1 row_mask:0xf bank_mask:0xf bound_ctrl:1
	v_pk_add_f32 v[62:63], v[104:105], v[62:63]
	v_mul_f32_e32 v48, 0x3fb8aa3b, v77
	v_exp_f32_e32 v48, v48
	v_mov_b32_dpp v106, v62 row_shr:2 row_mask:0xf bank_mask:0xf bound_ctrl:1
	v_mov_b32_dpp v107, v63 row_shr:2 row_mask:0xf bank_mask:0xf bound_ctrl:1
	v_pk_add_f32 v[62:63], v[62:63], v[106:107]
	v_pk_add_f32 v[110:111], v[122:123], v[110:111]
	s_waitcnt lgkmcnt(0)
	v_pk_add_f32 v[122:123], v[122:123], v[126:127]
	v_mul_f32_e32 v126, 0x3fb8aa3b, v108
	v_mov_b32_dpp v106, v62 row_shr:4 row_mask:0xf bank_mask:0xf bound_ctrl:1
	v_mov_b32_dpp v107, v63 row_shr:4 row_mask:0xf bank_mask:0xf bound_ctrl:1
	v_exp_f32_e32 v126, v126
	v_pk_add_f32 v[62:63], v[62:63], v[106:107]
	v_sub_f32_e32 v171, 1.0, v48
	v_lshlrev_b64 v[48:49], 1, v[96:97]
	v_mov_b32_dpp v106, v62 row_shr:8 row_mask:0xf bank_mask:0xf bound_ctrl:1
	v_mov_b32_dpp v107, v63 row_shr:8 row_mask:0xf bank_mask:0xf bound_ctrl:1
	v_pk_add_f32 v[62:63], v[62:63], v[106:107]
	v_lshl_add_u64 v[52:53], v[124:125], 0, v[48:49]
	ds_swizzle_b32 v106, v62 offset:swizzle(BROADCAST,16,15)
	ds_swizzle_b32 v107, v63 offset:swizzle(BROADCAST,16,15)
	v_pk_add_f32 v[124:125], v[60:61], v[62:63]
	v_lshl_add_u64 v[62:63], v[130:131], 0, v[50:51]
	v_sub_f32_e32 v130, 1.0, v126
	v_mul_f32_e32 v126, 0x3fb8aa3b, v109
	v_exp_f32_e32 v126, v126
	v_mov_b32_dpp v127, v115 row_shr:2 row_mask:0xf bank_mask:0xf bound_ctrl:1
	v_mul_f32_e32 v56, 0x3fb8aa3b, v80
	v_exp_f32_e32 v56, v56
	v_sub_f32_e32 v131, 1.0, v126
	v_mov_b32_dpp v126, v114 row_shr:2 row_mask:0xf bank_mask:0xf bound_ctrl:1
	v_pk_add_f32 v[114:115], v[114:115], v[126:127]
	v_sub_f32_e32 v167, 1.0, v56
	v_mul_f32_e32 v56, 0x3fb8aa3b, v81
	v_mov_b32_dpp v126, v114 row_shr:4 row_mask:0xf bank_mask:0xf bound_ctrl:1
	v_mov_b32_dpp v127, v115 row_shr:4 row_mask:0xf bank_mask:0xf bound_ctrl:1
	v_pk_add_f32 v[114:115], v[114:115], v[126:127]
	v_exp_f32_e32 v56, v56
	s_waitcnt lgkmcnt(0)
	v_pk_add_f32 v[106:107], v[60:61], v[106:107]
	v_mov_b32_dpp v126, v114 row_shr:8 row_mask:0xf bank_mask:0xf bound_ctrl:1
	v_mov_b32_dpp v127, v115 row_shr:8 row_mask:0xf bank_mask:0xf bound_ctrl:1
	v_pk_add_f32 v[114:115], v[114:115], v[126:127]
	ds_swizzle_b32 v126, v114 offset:swizzle(BROADCAST,16,15)
	ds_swizzle_b32 v127, v115 offset:swizzle(BROADCAST,16,15)
	v_pk_add_f32 v[114:115], v[106:107], v[114:115]
	v_sub_f32_e32 v172, 1.0, v56
	v_lshl_add_u64 v[56:57], v[128:129], 0, v[48:49]
	v_mul_f32_e32 v60, 0x3fb8aa3b, v104
	s_waitcnt lgkmcnt(0)
	v_pk_add_f32 v[106:107], v[106:107], v[126:127]
	v_pk_add_f32 v[126:127], v[122:123], v[74:75] neg_lo:[0,1] neg_hi:[0,1]
	v_pk_add_f32 v[128:129], v[106:107], v[116:117] neg_lo:[0,1] neg_hi:[0,1]
	v_pk_add_f32 v[72:73], v[72:73], v[126:127]
	v_pk_add_f32 v[76:77], v[76:77], v[128:129]
	v_mul_f32_e32 v96, 0x3fb8aa3b, v78
	v_exp_f32_e32 v60, v60
	v_cndmask_b32_e64 v77, v117, v77, s[42:43]
	v_cndmask_b32_e64 v76, v116, v76, s[42:43]
	v_cndmask_b32_e64 v75, v75, v73, s[42:43]
	v_cndmask_b32_e64 v74, v74, v72, s[42:43]
	v_exp_f32_e32 v96, v96
	global_store_dwordx4 v[54:55], v[74:77], off
	v_cvt_pk_bf16_f32 v72, v168, v169
	v_cvt_pk_bf16_f32 v73, v170, v171
	global_store_dwordx2 v[52:53], v[72:73], off
	v_pk_add_f32 v[72:73], v[122:123], v[118:119] neg_lo:[0,1] neg_hi:[0,1]
	v_pk_add_f32 v[74:75], v[106:107], v[120:121] neg_lo:[0,1] neg_hi:[0,1]
	v_pk_add_f32 v[72:73], v[78:79], v[72:73]
	v_pk_add_f32 v[74:75], v[80:81], v[74:75]
	v_sub_f32_e32 v160, 1.0, v60
	v_mul_f32_e32 v60, 0x3fb8aa3b, v105
	v_cndmask_b32_e64 v75, v121, v75, s[42:43]
	v_cndmask_b32_e64 v74, v120, v74, s[42:43]
	v_cndmask_b32_e64 v73, v119, v73, s[42:43]
	v_cndmask_b32_e64 v72, v118, v72, s[42:43]
	v_sub_f32_e32 v96, 1.0, v96
	v_exp_f32_e32 v60, v60
	global_store_dwordx4 v[58:59], v[72:75], off
	v_sub_f32_e32 v161, 1.0, v60
	s_nop 0
	v_cvt_pk_bf16_f32 v72, v96, v166
	v_cvt_pk_bf16_f32 v73, v167, v172
	global_store_dwordx2 v[56:57], v[72:73], off
	v_pk_add_f32 v[72:73], v[122:123], v[102:103] neg_lo:[0,1] neg_hi:[0,1]
	v_pk_add_f32 v[74:75], v[106:107], v[124:125] neg_lo:[0,1] neg_hi:[0,1]
	v_pk_add_f32 v[72:73], v[82:83], v[72:73]
	v_pk_add_f32 v[74:75], v[104:105], v[74:75]
	v_cndmask_b32_e64 v73, v103, v73, s[42:43]
	v_cndmask_b32_e64 v75, v125, v75, s[42:43]
; template <int CTRL> __device__ __forceinline__ float dppx(float v) { return __int_as_float(__builtin_amdgcn_update_dpp(0, __float_as_int(v), CTRL, 0xf, 0xf, true)); }
; __device__ __forceinline__ unsigned cvt_pk_bf16(float lo, float hi) { unsigned r; asm volatile("v_cvt_pk_bf16_f32 %0, %1, %2" : "=v"(r) : "v"(lo), "v"(hi)); return r; }
; __device__ __forceinline__ float log_forget(float z, float lb) {
;   const float r0 = fminf(z, 0.f) - __logf(1.f + __expf(-fabsf(z)));
;   __device__ __forceinline__ void operator()(const f32x4 (&acc)[2][2][4][2], const pg8::Unit& u, int wr, int wc, int fr, int fq) const {
;     ...
;               for (int q = 0; q < 4; ++q) { const float gv = log_forget(acc[ai][bj][m][qh][q], lq[q]); g[m][q] = gv;
;                 float sc = gv; sc += dppx<0x111>(sc); sc += dppx<0x112>(sc); sc += dppx<0x114>(sc); sc += dppx<0x118>(sc);
;                 const float tot16 = __int_as_float(__builtin_amdgcn_ds_swizzle(__float_as_int(sc), 0x1F0));
;                 cs[m][q] = sc + carry[q]; carry[q] += tot16; }
; #pragma unroll
;             for (int m = 0; m < 4; ++m) { const int r = row0 + ai * 128 + m * 16; float bq[4], kq[4];
; #pragma unroll
;               for (int q = 0; q < 4; ++q) { bq[q] = bwd ? (carry[q] - cs[m][q]) + g[m][q] : cs[m][q]; kq[q] = 1.f - __expf(g[m][q]); }
;               *(f32x4*)(logfp + (size_t)r * 1024 + c + 4 * qh) = (f32x4){bq[0], bq[1], bq[2], bq[3]};
;               u32x2 w; w.x = pg8::cvt_pk_bf16(kq[0], kq[1]); w.y = pg8::cvt_pk_bf16(kq[2], kq[3]);
;               *(u32x2*)(km + (size_t)r * 1024 + c + 4 * qh) = w; } } }
	v_cndmask_b32_e64 v74, v124, v74, s[42:43]
	v_cndmask_b32_e64 v72, v102, v72, s[42:43]
	v_lshl_add_u64 v[60:61], v[132:133], 0, v[48:49]
	global_store_dwordx4 v[62:63], v[72:75], off
	s_nop 1
	v_cvt_pk_bf16_f32 v72, v158, v159
	v_cvt_pk_bf16_f32 v73, v160, v161
	global_store_dwordx2 v[60:61], v[72:73], off
	v_mul_f32_e32 v72, 0x3fb8aa3b, v112
	v_exp_f32_e32 v72, v72
	v_pk_add_f32 v[74:75], v[106:107], v[114:115] neg_lo:[0,1] neg_hi:[0,1]
	v_sub_f32_e32 v78, 1.0, v72
	v_pk_add_f32 v[72:73], v[122:123], v[110:111] neg_lo:[0,1] neg_hi:[0,1]
	v_pk_add_f32 v[74:75], v[112:113], v[74:75]
	v_pk_add_f32 v[72:73], v[108:109], v[72:73]
	v_cndmask_b32_e64 v76, v114, v74, s[42:43]
	v_cndmask_b32_e64 v74, v110, v72, s[42:43]
	v_mul_f32_e32 v72, 0x3fb8aa3b, v113
	v_exp_f32_e32 v72, v72
	v_cndmask_b32_e64 v77, v115, v75, s[42:43]
	v_cndmask_b32_e64 v75, v111, v73, s[42:43]
	v_sub_f32_e32 v79, 1.0, v72
	v_lshl_add_u64 v[72:73], v[134:135], 0, v[50:51]
	global_store_dwordx4 v[72:73], v[74:77], off
	s_nop 1
	v_cvt_pk_bf16_f32 v76, v130, v131
	v_cvt_pk_bf16_f32 v77, v78, v79
	v_lshl_add_u64 v[74:75], v[136:137], 0, v[48:49]
	global_store_dwordx2 v[74:75], v[76:77], off
	v_mul_f32_e64 v77, |v44|, s8
	v_exp_f32_e32 v77, v77
	v_max_f32_e32 v76, v44, v44
	v_add_f32_e32 v77, 1.0, v77
	v_cmp_gt_f32_e32 vcc, s37, v77
	v_min_f32_e32 v76, 0, v76
	s_nop 0
	v_cndmask_b32_e64 v78, 0, 32, vcc
	v_ldexp_f32 v77, v77, v78
	v_log_f32_e32 v77, v77
	s_nop 0
	v_mul_f32_e32 v78, 0x3f317217, v77
	v_fma_f32 v78, v77, s33, -v78
	v_fmac_f32_e32 v78, 0x3377d1cf, v77
	v_fmac_f32_e32 v78, 0x3f317217, v77
	v_cmp_lt_f32_e64 s[48:49], |v77|, s36
	s_nop 1
	v_cndmask_b32_e64 v77, v77, v78, s[48:49]
	v_cndmask_b32_e32 v78, 0, v216, vcc
	v_sub_f32_e32 v78, v77, v78
	s_nop 0
	s_nop 1
	s_nop 0
	s_nop 1
	v_max_f32_e32 v44, v45, v45
	v_min_f32_e32 v77, 0, v44
	v_mul_f32_e64 v44, |v45|, s8
	v_exp_f32_e32 v44, v44
	s_nop 0
	v_add_f32_e32 v44, 1.0, v44
	v_cmp_gt_f32_e32 vcc, s37, v44
	s_nop 1
	v_cndmask_b32_e64 v79, 0, 32, vcc
	v_ldexp_f32 v44, v44, v79
	v_log_f32_e32 v44, v44
	s_nop 0
	v_mul_f32_e32 v79, 0x3f317217, v44
	v_fma_f32 v79, v44, s33, -v79
	v_fmac_f32_e32 v79, 0x3377d1cf, v44
	v_fmac_f32_e32 v79, 0x3f317217, v44
	v_cmp_lt_f32_e64 s[48:49], |v44|, s36
	s_nop 1
	v_cndmask_b32_e64 v44, v44, v79, s[48:49]
	v_cndmask_b32_e32 v79, 0, v216, vcc
	v_sub_f32_e32 v79, v44, v79
	s_nop 0
	s_nop 0
	s_nop 1
	s_nop 0
	s_nop 1
	v_mul_f32_e64 v45, |v46|, s8
	v_exp_f32_e32 v45, v45
	v_max_f32_e32 v44, v46, v46
	v_min_f32_e32 v44, 0, v44
	v_add_f32_e32 v45, 1.0, v45
	v_cmp_gt_f32_e32 vcc, s37, v45
	s_nop 1
	v_cndmask_b32_e64 v80, 0, 32, vcc
	v_ldexp_f32 v45, v45, v80
	v_log_f32_e32 v45, v45
	s_nop 0
	v_mul_f32_e32 v80, 0x3f317217, v45
	v_fma_f32 v80, v45, s33, -v80
	v_fmac_f32_e32 v80, 0x3377d1cf, v45
	v_fmac_f32_e32 v80, 0x3f317217, v45
	v_cmp_lt_f32_e64 s[48:49], |v45|, s36
	s_nop 1
	v_cndmask_b32_e64 v45, v45, v80, s[48:49]
	v_cndmask_b32_e32 v80, 0, v216, vcc
	v_sub_f32_e32 v80, v45, v80
	s_nop 0
	s_nop 0
	s_nop 0
	s_nop 0
	s_nop 1
	v_mul_f32_e64 v46, |v47|, s8
	v_exp_f32_e32 v46, v46
	v_max_f32_e32 v45, v47, v47
	v_min_f32_e32 v45, 0, v45
	v_add_f32_e32 v46, 1.0, v46
	v_cmp_gt_f32_e32 vcc, s37, v46
	s_nop 1
	v_cndmask_b32_e64 v81, 0, 32, vcc
	v_ldexp_f32 v46, v46, v81
	v_log_f32_e32 v46, v46
	s_nop 0
	v_mul_f32_e32 v81, 0x3f317217, v46
	v_fma_f32 v81, v46, s33, -v81
	v_fmac_f32_e32 v81, 0x3377d1cf, v46
	v_fmac_f32_e32 v81, 0x3f317217, v46
	v_cmp_lt_f32_e64 s[48:49], |v46|, s36
	s_nop 1
	v_cndmask_b32_e64 v46, v46, v81, s[48:49]
	v_cndmask_b32_e32 v81, 0, v216, vcc
	v_sub_f32_e32 v81, v46, v81
	v_pk_add_f32 v[44:45], v[44:45], v[80:81] neg_lo:[0,1] neg_hi:[0,1]
	v_mov_b32_e32 v44, v44
	s_nop 1
	s_nop 0
	s_nop 1
	v_mul_f32_e64 v47, |v40|, s8
	v_exp_f32_e32 v47, v47
	v_max_f32_e32 v46, v40, v40
	v_add_f32_e32 v47, 1.0, v47
	v_cmp_gt_f32_e32 vcc, s37, v47
	v_mov_b32_e32 v45, v45
	s_nop 0
	v_cndmask_b32_e64 v82, 0, 32, vcc
	v_ldexp_f32 v47, v47, v82
	v_log_f32_e32 v47, v47
	v_min_f32_e32 v46, 0, v46
	v_mul_f32_e32 v82, 0x3f317217, v47
	v_fma_f32 v82, v47, s33, -v82
	v_fmac_f32_e32 v82, 0x3377d1cf, v47
	v_fmac_f32_e32 v82, 0x3f317217, v47
	v_cmp_lt_f32_e64 s[48:49], |v47|, s36
	s_nop 1
	v_cndmask_b32_e64 v47, v47, v82, s[48:49]
	v_cndmask_b32_e32 v82, 0, v216, vcc
	v_sub_f32_e32 v82, v47, v82
	s_nop 0
	s_nop 1
	s_nop 0
	s_nop 1
	v_max_f32_e32 v40, v41, v41
	v_min_f32_e32 v47, 0, v40
	v_mul_f32_e64 v40, |v41|, s8
	v_exp_f32_e32 v40, v40
	s_nop 0
	v_add_f32_e32 v40, 1.0, v40
	v_cmp_gt_f32_e32 vcc, s37, v40
	s_nop 1
	v_cndmask_b32_e64 v83, 0, 32, vcc
	v_ldexp_f32 v40, v40, v83
	v_log_f32_e32 v40, v40
	s_nop 0
	v_mul_f32_e32 v83, 0x3f317217, v40
	v_fma_f32 v83, v40, s33, -v83
	v_fmac_f32_e32 v83, 0x3377d1cf, v40
	v_fmac_f32_e32 v83, 0x3f317217, v40
	v_cmp_lt_f32_e64 s[48:49], |v40|, s36
	s_nop 1
	v_cndmask_b32_e64 v40, v40, v83, s[48:49]
	v_cndmask_b32_e32 v83, 0, v216, vcc
	v_sub_f32_e32 v83, v40, v83
	v_pk_add_f32 v[46:47], v[46:47], v[82:83] neg_lo:[0,1] neg_hi:[0,1]
	s_nop 0
	s_nop 1
	s_nop 0
	s_nop 1
	v_mul_f32_e64 v41, |v42|, s8
	v_exp_f32_e32 v41, v41
	v_max_f32_e32 v40, v42, v42
	v_mov_b32_e32 v47, v47
	v_min_f32_e32 v40, 0, v40
	v_add_f32_e32 v41, 1.0, v41
	v_cmp_gt_f32_e32 vcc, s37, v41
	s_nop 1
	v_cndmask_b32_e64 v102, 0, 32, vcc
	v_ldexp_f32 v41, v41, v102
	v_log_f32_e32 v41, v41
	s_nop 0
	v_mul_f32_e32 v102, 0x3f317217, v41
	v_fma_f32 v102, v41, s33, -v102
	v_fmac_f32_e32 v102, 0x3377d1cf, v41
	v_fmac_f32_e32 v102, 0x3f317217, v41
	v_cmp_lt_f32_e64 s[48:49], |v41|, s36
	s_nop 1
	v_cndmask_b32_e64 v41, v41, v102, s[48:49]
	v_cndmask_b32_e32 v102, 0, v216, vcc
	v_sub_f32_e32 v102, v41, v102
; template <int CTRL> __device__ __forceinline__ float dppx(float v) { return __int_as_float(__builtin_amdgcn_update_dpp(0, __float_as_int(v), CTRL, 0xf, 0xf, true)); }
; __device__ __forceinline__ float log_forget(float z, float lb) {
;   const float r0 = fminf(z, 0.f) - __logf(1.f + __expf(-fabsf(z)));
;   __device__ __forceinline__ void operator()(const f32x4 (&acc)[2][2][4][2], const pg8::Unit& u, int wr, int wc, int fr, int fq) const {
;     ...
;               for (int q = 0; q < 4; ++q) { const float gv = log_forget(acc[ai][bj][m][qh][q], lq[q]); g[m][q] = gv;
;                 float sc = gv; sc += dppx<0x111>(sc); sc += dppx<0x112>(sc); sc += dppx<0x114>(sc); sc += dppx<0x118>(sc);
	s_nop 0
	s_nop 0
	s_nop 1
	s_nop 0
	s_nop 1
	v_mul_f32_e64 v42, |v43|, s8
	v_exp_f32_e32 v42, v42
	v_max_f32_e32 v41, v43, v43
	v_min_f32_e32 v41, 0, v41
	v_add_f32_e32 v42, 1.0, v42
	v_cmp_gt_f32_e32 vcc, s37, v42
	s_nop 1
	v_cndmask_b32_e64 v103, 0, 32, vcc
	v_ldexp_f32 v42, v42, v103
	v_log_f32_e32 v42, v42
	s_nop 0
	v_mul_f32_e32 v103, 0x3f317217, v42
	v_fma_f32 v103, v42, s33, -v103
	v_fmac_f32_e32 v103, 0x3377d1cf, v42
	v_fmac_f32_e32 v103, 0x3f317217, v42
	v_cmp_lt_f32_e64 s[48:49], |v42|, s36
	s_nop 1
	v_cndmask_b32_e64 v42, v42, v103, s[48:49]
	v_cndmask_b32_e32 v103, 0, v216, vcc
	v_sub_f32_e32 v103, v42, v103
	v_pk_add_f32 v[40:41], v[40:41], v[102:103] neg_lo:[0,1] neg_hi:[0,1]
	v_mov_b32_e32 v40, v40
	s_nop 1
	s_nop 0
	s_nop 1
	v_mul_f32_e64 v43, |v36|, s8
	v_exp_f32_e32 v43, v43
	v_max_f32_e32 v42, v36, v36
	v_add_f32_e32 v43, 1.0, v43
	v_cmp_gt_f32_e32 vcc, s37, v43
	v_mov_b32_e32 v41, v41
	s_nop 0
	v_cndmask_b32_e64 v104, 0, 32, vcc
	v_ldexp_f32 v43, v43, v104
	v_log_f32_e32 v43, v43
	v_min_f32_e32 v42, 0, v42
	v_mul_f32_e32 v104, 0x3f317217, v43
	v_fma_f32 v104, v43, s33, -v104
	v_fmac_f32_e32 v104, 0x3377d1cf, v43
	v_fmac_f32_e32 v104, 0x3f317217, v43
	v_cmp_lt_f32_e64 s[48:49], |v43|, s36
	s_nop 1
	v_cndmask_b32_e64 v43, v43, v104, s[48:49]
	v_cndmask_b32_e32 v104, 0, v216, vcc
	v_sub_f32_e32 v104, v43, v104
	s_nop 0
	s_nop 1
	s_nop 0
	s_nop 1
	v_max_f32_e32 v36, v37, v37
	v_min_f32_e32 v43, 0, v36
	v_mul_f32_e64 v36, |v37|, s8
	v_exp_f32_e32 v36, v36
	s_nop 0
	v_add_f32_e32 v36, 1.0, v36
	v_cmp_gt_f32_e32 vcc, s37, v36
	s_nop 1
	v_cndmask_b32_e64 v105, 0, 32, vcc
	v_ldexp_f32 v36, v36, v105
	v_log_f32_e32 v36, v36
	s_nop 0
	v_mul_f32_e32 v105, 0x3f317217, v36
	v_fma_f32 v105, v36, s33, -v105
	v_fmac_f32_e32 v105, 0x3377d1cf, v36
	v_fmac_f32_e32 v105, 0x3f317217, v36
	v_cmp_lt_f32_e64 s[48:49], |v36|, s36
	s_nop 1
	v_cndmask_b32_e64 v36, v36, v105, s[48:49]
	v_cndmask_b32_e32 v105, 0, v216, vcc
	v_sub_f32_e32 v105, v36, v105
	v_pk_add_f32 v[42:43], v[42:43], v[104:105] neg_lo:[0,1] neg_hi:[0,1]
	s_nop 0
	s_nop 1
	s_nop 0
	s_nop 1
	v_mul_f32_e64 v37, |v38|, s8
	v_exp_f32_e32 v37, v37
	v_max_f32_e32 v36, v38, v38
	v_mov_b32_e32 v43, v43
	v_min_f32_e32 v36, 0, v36
	v_add_f32_e32 v37, 1.0, v37
	v_cmp_gt_f32_e32 vcc, s37, v37
	v_mov_b32_dpp v105, v43 row_shr:1 row_mask:0xf bank_mask:0xf bound_ctrl:1
	s_nop 0
	v_cndmask_b32_e64 v106, 0, 32, vcc
	v_ldexp_f32 v37, v37, v106
	v_log_f32_e32 v37, v37
	s_nop 0
	v_mul_f32_e32 v106, 0x3f317217, v37
	v_fma_f32 v106, v37, s33, -v106
	v_fmac_f32_e32 v106, 0x3377d1cf, v37
	v_fmac_f32_e32 v106, 0x3f317217, v37
	v_cmp_lt_f32_e64 s[48:49], |v37|, s36
	s_nop 1
	v_cndmask_b32_e64 v37, v37, v106, s[48:49]
	v_cndmask_b32_e32 v106, 0, v216, vcc
	v_sub_f32_e32 v106, v37, v106
	s_nop 0
	s_nop 0
	s_nop 1
	s_nop 0
	s_nop 1
	v_mul_f32_e64 v38, |v39|, s8
	v_exp_f32_e32 v38, v38
	v_max_f32_e32 v37, v39, v39
	v_min_f32_e32 v37, 0, v37
	v_add_f32_e32 v38, 1.0, v38
	v_cmp_gt_f32_e32 vcc, s37, v38
	s_nop 1
	v_cndmask_b32_e64 v107, 0, 32, vcc
	v_ldexp_f32 v38, v38, v107
	v_log_f32_e32 v38, v38
	s_nop 0
	v_mul_f32_e32 v107, 0x3f317217, v38
	v_fma_f32 v107, v38, s33, -v107
	v_fmac_f32_e32 v107, 0x3377d1cf, v38
	v_fmac_f32_e32 v107, 0x3f317217, v38
	v_cmp_lt_f32_e64 s[48:49], |v38|, s36
	s_nop 1
	v_cndmask_b32_e64 v38, v38, v107, s[48:49]
	v_cndmask_b32_e32 v107, 0, v216, vcc
	v_sub_f32_e32 v107, v38, v107
	v_pk_add_f32 v[36:37], v[36:37], v[106:107] neg_lo:[0,1] neg_hi:[0,1]
	v_mov_b32_e32 v36, v36
	s_nop 1
	v_mov_b32_dpp v106, v36 row_shr:1 row_mask:0xf bank_mask:0xf bound_ctrl:1
	s_nop 0
	s_nop 0
	s_nop 1
	v_mul_f32_e64 v39, |v32|, s8
	v_exp_f32_e32 v39, v39
	v_max_f32_e32 v38, v32, v32
	v_add_f32_e32 v39, 1.0, v39
	v_cmp_gt_f32_e32 vcc, s37, v39
	v_mov_b32_e32 v37, v37
	s_nop 0
	v_cndmask_b32_e64 v108, 0, 32, vcc
	v_ldexp_f32 v39, v39, v108
	v_log_f32_e32 v39, v39
	v_mov_b32_dpp v107, v37 row_shr:1 row_mask:0xf bank_mask:0xf bound_ctrl:1
	v_pk_add_f32 v[106:107], v[36:37], v[106:107]
	v_min_f32_e32 v38, 0, v38
	v_mul_f32_e32 v108, 0x3f317217, v39
	v_fma_f32 v108, v39, s33, -v108
	v_fmac_f32_e32 v108, 0x3377d1cf, v39
	v_fmac_f32_e32 v108, 0x3f317217, v39
	v_cmp_lt_f32_e64 s[48:49], |v39|, s36
	s_nop 1
	v_cndmask_b32_e64 v39, v39, v108, s[48:49]
	v_cndmask_b32_e32 v108, 0, v216, vcc
	v_sub_f32_e32 v108, v39, v108
	s_nop 0
	s_nop 1
	s_nop 0
	s_nop 1
	v_max_f32_e32 v32, v33, v33
	v_min_f32_e32 v39, 0, v32
	v_mul_f32_e64 v32, |v33|, s8
	v_exp_f32_e32 v32, v32
	s_nop 0
	v_add_f32_e32 v32, 1.0, v32
	v_cmp_gt_f32_e32 vcc, s37, v32
	s_nop 1
	v_cndmask_b32_e64 v109, 0, 32, vcc
	v_ldexp_f32 v32, v32, v109
	v_log_f32_e32 v32, v32
	s_nop 0
	v_mul_f32_e32 v109, 0x3f317217, v32
	v_fma_f32 v109, v32, s33, -v109
	v_fmac_f32_e32 v109, 0x3377d1cf, v32
	v_fmac_f32_e32 v109, 0x3f317217, v32
	v_cmp_lt_f32_e64 s[48:49], |v32|, s36
	s_nop 1
	v_cndmask_b32_e64 v32, v32, v109, s[48:49]
	v_cndmask_b32_e32 v109, 0, v216, vcc
	v_sub_f32_e32 v109, v32, v109
	v_pk_add_f32 v[38:39], v[38:39], v[108:109] neg_lo:[0,1] neg_hi:[0,1]
	s_nop 0
	s_nop 1
	s_nop 0
	s_nop 1
	v_mul_f32_e64 v33, |v34|, s8
	v_exp_f32_e32 v33, v33
	v_max_f32_e32 v32, v34, v34
	v_mov_b32_e32 v39, v39
	v_min_f32_e32 v32, 0, v32
	v_add_f32_e32 v33, 1.0, v33
	v_cmp_gt_f32_e32 vcc, s37, v33
	v_mov_b32_dpp v109, v39 row_shr:1 row_mask:0xf bank_mask:0xf bound_ctrl:1
	s_nop 0
	v_cndmask_b32_e64 v110, 0, 32, vcc
	v_ldexp_f32 v33, v33, v110
	v_log_f32_e32 v33, v33
	s_nop 0
	v_mul_f32_e32 v110, 0x3f317217, v33
	v_fma_f32 v110, v33, s33, -v110
	v_fmac_f32_e32 v110, 0x3377d1cf, v33
	v_fmac_f32_e32 v110, 0x3f317217, v33
	v_cmp_lt_f32_e64 s[48:49], |v33|, s36
	s_nop 1
; template <int CTRL> __device__ __forceinline__ float dppx(float v) { return __int_as_float(__builtin_amdgcn_update_dpp(0, __float_as_int(v), CTRL, 0xf, 0xf, true)); }
;   __device__ __forceinline__ void operator()(const f32x4 (&acc)[2][2][4][2], const pg8::Unit& u, int wr, int wc, int fr, int fq) const {
;     ...
;               for (int q = 0; q < 4; ++q) { const float gv = log_forget(acc[ai][bj][m][qh][q], lq[q]); g[m][q] = gv;
;                 float sc = gv; sc += dppx<0x111>(sc); sc += dppx<0x112>(sc); sc += dppx<0x114>(sc); sc += dppx<0x118>(sc);
;                 const float tot16 = __int_as_float(__builtin_amdgcn_ds_swizzle(__float_as_int(sc), 0x1F0));
;                 cs[m][q] = sc + carry[q]; carry[q] += tot16; }
; #pragma unroll
;             for (int m = 0; m < 4; ++m) { const int r = row0 + ai * 128 + m * 16; float bq[4], kq[4];
; #pragma unroll
;               for (int q = 0; q < 4; ++q) { bq[q] = bwd ? (carry[q] - cs[m][q]) + g[m][q] : cs[m][q]; kq[q] = 1.f - __expf(g[m][q]); }
	v_cndmask_b32_e64 v33, v33, v110, s[48:49]
	v_cndmask_b32_e32 v110, 0, v216, vcc
	v_sub_f32_e32 v110, v33, v110
	s_nop 0
	s_nop 0
	s_nop 1
	s_nop 0
	s_nop 1
	v_mul_f32_e64 v34, |v35|, s8
	v_exp_f32_e32 v34, v34
	v_max_f32_e32 v33, v35, v35
	v_min_f32_e32 v33, 0, v33
	v_add_f32_e32 v34, 1.0, v34
	v_cmp_gt_f32_e32 vcc, s37, v34
	s_nop 1
	v_cndmask_b32_e64 v111, 0, 32, vcc
	v_ldexp_f32 v34, v34, v111
	v_log_f32_e32 v34, v34
	s_nop 0
	v_mul_f32_e32 v111, 0x3f317217, v34
	v_fma_f32 v111, v34, s33, -v111
	v_fmac_f32_e32 v111, 0x3377d1cf, v34
	v_fmac_f32_e32 v111, 0x3f317217, v34
	v_cmp_lt_f32_e64 s[48:49], |v34|, s36
	s_nop 1
	v_cndmask_b32_e64 v34, v34, v111, s[48:49]
	v_cndmask_b32_e32 v111, 0, v216, vcc
	v_sub_f32_e32 v111, v34, v111
	v_pk_add_f32 v[32:33], v[32:33], v[110:111] neg_lo:[0,1] neg_hi:[0,1]
	v_mov_b32_e32 v110, v32
	s_nop 1
	v_mov_b32_dpp v32, v110 row_shr:1 row_mask:0xf bank_mask:0xf bound_ctrl:1
	s_nop 0
	s_nop 0
	s_nop 1
	v_pk_add_f32 v[34:35], v[76:77], v[78:79] neg_lo:[0,1] neg_hi:[0,1]
	v_mov_b32_e32 v35, v35
	v_mov_b32_e32 v111, v33
	v_mov_b32_e32 v34, v34
	v_mov_b32_dpp v77, v35 row_shr:1 row_mask:0xf bank_mask:0xf bound_ctrl:1
	v_mov_b32_e32 v46, v46
	v_mov_b32_dpp v76, v34 row_shr:1 row_mask:0xf bank_mask:0xf bound_ctrl:1
	v_pk_add_f32 v[76:77], v[34:35], v[76:77]
	v_mov_b32_e32 v42, v42
	v_mov_b32_e32 v38, v38
	v_mov_b32_dpp v78, v76 row_shr:2 row_mask:0xf bank_mask:0xf bound_ctrl:1
	v_mov_b32_dpp v79, v77 row_shr:2 row_mask:0xf bank_mask:0xf bound_ctrl:1
	v_pk_add_f32 v[76:77], v[76:77], v[78:79]
	v_mov_b32_dpp v104, v42 row_shr:1 row_mask:0xf bank_mask:0xf bound_ctrl:1
	v_pk_add_f32 v[104:105], v[42:43], v[104:105]
	v_mov_b32_dpp v78, v76 row_shr:4 row_mask:0xf bank_mask:0xf bound_ctrl:1
	v_mov_b32_dpp v79, v77 row_shr:4 row_mask:0xf bank_mask:0xf bound_ctrl:1
	v_pk_add_f32 v[76:77], v[76:77], v[78:79]
	v_mov_b32_dpp v108, v38 row_shr:1 row_mask:0xf bank_mask:0xf bound_ctrl:1
	v_pk_add_f32 v[108:109], v[38:39], v[108:109]
	v_mov_b32_dpp v78, v76 row_shr:8 row_mask:0xf bank_mask:0xf bound_ctrl:1
	v_mov_b32_dpp v79, v77 row_shr:8 row_mask:0xf bank_mask:0xf bound_ctrl:1
	v_pk_add_f32 v[76:77], v[76:77], v[78:79]
	ds_swizzle_b32 v78, v76 offset:swizzle(BROADCAST,16,15)
	ds_swizzle_b32 v79, v77 offset:swizzle(BROADCAST,16,15)
	v_mov_b32_dpp v33, v111 row_shr:1 row_mask:0xf bank_mask:0xf bound_ctrl:1
	v_pk_add_f32 v[32:33], v[110:111], v[32:33]
	v_pk_add_f32 v[76:77], v[76:77], 0 op_sel_hi:[1,0]
	s_waitcnt lgkmcnt(0)
	v_pk_add_f32 v[130:131], v[78:79], 0 op_sel_hi:[1,0]
	v_mul_f32_e32 v78, 0x3fb8aa3b, v34
	v_exp_f32_e32 v78, v78
	v_mov_b32_dpp v79, v45 row_shr:1 row_mask:0xf bank_mask:0xf bound_ctrl:1
	v_sub_f32_e32 v115, 1.0, v78
	v_mul_f32_e32 v78, 0x3fb8aa3b, v35
	v_exp_f32_e32 v78, v78
	s_nop 0
	v_sub_f32_e32 v133, 1.0, v78
	v_mov_b32_dpp v78, v44 row_shr:1 row_mask:0xf bank_mask:0xf bound_ctrl:1
	v_pk_add_f32 v[78:79], v[44:45], v[78:79]
	s_nop 1
	v_mov_b32_dpp v80, v78 row_shr:2 row_mask:0xf bank_mask:0xf bound_ctrl:1
	v_mov_b32_dpp v81, v79 row_shr:2 row_mask:0xf bank_mask:0xf bound_ctrl:1
	v_pk_add_f32 v[78:79], v[78:79], v[80:81]
	s_nop 1
	v_mov_b32_dpp v80, v78 row_shr:4 row_mask:0xf bank_mask:0xf bound_ctrl:1
	v_mov_b32_dpp v81, v79 row_shr:4 row_mask:0xf bank_mask:0xf bound_ctrl:1
	v_pk_add_f32 v[78:79], v[78:79], v[80:81]
	s_nop 1
	v_mov_b32_dpp v80, v78 row_shr:8 row_mask:0xf bank_mask:0xf bound_ctrl:1
	v_mov_b32_dpp v81, v79 row_shr:8 row_mask:0xf bank_mask:0xf bound_ctrl:1
	v_pk_add_f32 v[78:79], v[78:79], v[80:81]
	ds_swizzle_b32 v80, v78 offset:swizzle(BROADCAST,16,15)
	ds_swizzle_b32 v81, v79 offset:swizzle(BROADCAST,16,15)
	v_pk_add_f32 v[78:79], v[78:79], 0 op_sel_hi:[1,0]
	s_waitcnt lgkmcnt(0)
	v_pk_add_f32 v[116:117], v[80:81], 0 op_sel_hi:[1,0]
	v_mul_f32_e32 v80, 0x3fb8aa3b, v44
	v_exp_f32_e32 v80, v80
	v_mov_b32_dpp v81, v47 row_shr:1 row_mask:0xf bank_mask:0xf bound_ctrl:1
	v_sub_f32_e32 v134, 1.0, v80
	v_mul_f32_e32 v80, 0x3fb8aa3b, v45
	v_exp_f32_e32 v80, v80
	s_nop 0
	v_sub_f32_e32 v135, 1.0, v80
	v_mov_b32_dpp v80, v46 row_shr:1 row_mask:0xf bank_mask:0xf bound_ctrl:1
	v_pk_add_f32 v[80:81], v[46:47], v[80:81]
	s_nop 1
	v_mov_b32_dpp v82, v80 row_shr:2 row_mask:0xf bank_mask:0xf bound_ctrl:1
	v_mov_b32_dpp v83, v81 row_shr:2 row_mask:0xf bank_mask:0xf bound_ctrl:1
	v_pk_add_f32 v[80:81], v[80:81], v[82:83]
	s_nop 1
	v_mov_b32_dpp v82, v80 row_shr:4 row_mask:0xf bank_mask:0xf bound_ctrl:1
	v_mov_b32_dpp v83, v81 row_shr:4 row_mask:0xf bank_mask:0xf bound_ctrl:1
	v_pk_add_f32 v[80:81], v[80:81], v[82:83]
	s_nop 1
	v_mov_b32_dpp v82, v80 row_shr:8 row_mask:0xf bank_mask:0xf bound_ctrl:1
	v_mov_b32_dpp v83, v81 row_shr:8 row_mask:0xf bank_mask:0xf bound_ctrl:1
	v_pk_add_f32 v[80:81], v[80:81], v[82:83]
	ds_swizzle_b32 v82, v80 offset:swizzle(BROADCAST,16,15)
	ds_swizzle_b32 v83, v81 offset:swizzle(BROADCAST,16,15)
	v_pk_add_f32 v[80:81], v[130:131], v[80:81]
	s_waitcnt lgkmcnt(0)
	v_pk_add_f32 v[118:119], v[130:131], v[82:83]
	v_mul_f32_e32 v82, 0x3fb8aa3b, v46
	v_exp_f32_e32 v82, v82
	v_mov_b32_dpp v83, v41 row_shr:1 row_mask:0xf bank_mask:0xf bound_ctrl:1
	v_sub_f32_e32 v130, 1.0, v82
	v_mul_f32_e32 v82, 0x3fb8aa3b, v47
	v_exp_f32_e32 v82, v82
	s_nop 0
	v_sub_f32_e32 v131, 1.0, v82
	v_mov_b32_dpp v82, v40 row_shr:1 row_mask:0xf bank_mask:0xf bound_ctrl:1
	v_pk_add_f32 v[82:83], v[40:41], v[82:83]
	s_nop 1
	v_mov_b32_dpp v102, v82 row_shr:2 row_mask:0xf bank_mask:0xf bound_ctrl:1
	v_mov_b32_dpp v103, v83 row_shr:2 row_mask:0xf bank_mask:0xf bound_ctrl:1
	v_pk_add_f32 v[82:83], v[82:83], v[102:103]
	s_nop 1
	v_mov_b32_dpp v102, v82 row_shr:4 row_mask:0xf bank_mask:0xf bound_ctrl:1
	v_mov_b32_dpp v103, v83 row_shr:4 row_mask:0xf bank_mask:0xf bound_ctrl:1
	v_pk_add_f32 v[82:83], v[82:83], v[102:103]
	s_nop 1
	v_mov_b32_dpp v102, v82 row_shr:8 row_mask:0xf bank_mask:0xf bound_ctrl:1
	v_mov_b32_dpp v103, v83 row_shr:8 row_mask:0xf bank_mask:0xf bound_ctrl:1
	v_pk_add_f32 v[82:83], v[82:83], v[102:103]
	ds_swizzle_b32 v102, v82 offset:swizzle(BROADCAST,16,15)
	ds_swizzle_b32 v103, v83 offset:swizzle(BROADCAST,16,15)
	v_pk_add_f32 v[82:83], v[116:117], v[82:83]
	s_waitcnt lgkmcnt(0)
; template <int CTRL> __device__ __forceinline__ float dppx(float v) { return __int_as_float(__builtin_amdgcn_update_dpp(0, __float_as_int(v), CTRL, 0xf, 0xf, true)); }
;   __device__ __forceinline__ void operator()(const f32x4 (&acc)[2][2][4][2], const pg8::Unit& u, int wr, int wc, int fr, int fq) const {
;     ...
;                 float sc = gv; sc += dppx<0x111>(sc); sc += dppx<0x112>(sc); sc += dppx<0x114>(sc); sc += dppx<0x118>(sc);
;                 const float tot16 = __int_as_float(__builtin_amdgcn_ds_swizzle(__float_as_int(sc), 0x1F0));
;                 cs[m][q] = sc + carry[q]; carry[q] += tot16; }
; #pragma unroll
;             for (int m = 0; m < 4; ++m) { const int r = row0 + ai * 128 + m * 16; float bq[4], kq[4];
; #pragma unroll
;               for (int q = 0; q < 4; ++q) { bq[q] = bwd ? (carry[q] - cs[m][q]) + g[m][q] : cs[m][q]; kq[q] = 1.f - __expf(g[m][q]); }
	v_pk_add_f32 v[102:103], v[116:117], v[102:103]
	v_mul_f32_e32 v116, 0x3fb8aa3b, v40
	v_exp_f32_e32 v116, v116
	v_mov_b32_dpp v117, v105 row_shr:2 row_mask:0xf bank_mask:0xf bound_ctrl:1
	v_sub_f32_e32 v122, 1.0, v116
	v_mul_f32_e32 v116, 0x3fb8aa3b, v41
	v_exp_f32_e32 v116, v116
	s_nop 0
	v_sub_f32_e32 v136, 1.0, v116
	v_mov_b32_dpp v116, v104 row_shr:2 row_mask:0xf bank_mask:0xf bound_ctrl:1
	v_pk_add_f32 v[104:105], v[104:105], v[116:117]
	s_nop 1
	v_mov_b32_dpp v116, v104 row_shr:4 row_mask:0xf bank_mask:0xf bound_ctrl:1
	v_mov_b32_dpp v117, v105 row_shr:4 row_mask:0xf bank_mask:0xf bound_ctrl:1
	v_pk_add_f32 v[104:105], v[104:105], v[116:117]
	s_nop 1
	v_mov_b32_dpp v116, v104 row_shr:8 row_mask:0xf bank_mask:0xf bound_ctrl:1
	v_mov_b32_dpp v117, v105 row_shr:8 row_mask:0xf bank_mask:0xf bound_ctrl:1
	v_pk_add_f32 v[104:105], v[104:105], v[116:117]
	ds_swizzle_b32 v116, v104 offset:swizzle(BROADCAST,16,15)
	ds_swizzle_b32 v117, v105 offset:swizzle(BROADCAST,16,15)
	v_pk_add_f32 v[104:105], v[118:119], v[104:105]
	s_waitcnt lgkmcnt(0)
	v_pk_add_f32 v[116:117], v[118:119], v[116:117]
	v_mul_f32_e32 v118, 0x3fb8aa3b, v42
	v_exp_f32_e32 v118, v118
	v_mov_b32_dpp v119, v107 row_shr:2 row_mask:0xf bank_mask:0xf bound_ctrl:1
	v_sub_f32_e32 v123, 1.0, v118
	v_mul_f32_e32 v118, 0x3fb8aa3b, v43
	v_exp_f32_e32 v118, v118
	s_nop 0
	v_sub_f32_e32 v124, 1.0, v118
	v_mov_b32_dpp v118, v106 row_shr:2 row_mask:0xf bank_mask:0xf bound_ctrl:1
	v_pk_add_f32 v[106:107], v[106:107], v[118:119]
	s_nop 1
	v_mov_b32_dpp v118, v106 row_shr:4 row_mask:0xf bank_mask:0xf bound_ctrl:1
	v_mov_b32_dpp v119, v107 row_shr:4 row_mask:0xf bank_mask:0xf bound_ctrl:1
	v_pk_add_f32 v[106:107], v[106:107], v[118:119]
	s_nop 1
	v_mov_b32_dpp v118, v106 row_shr:8 row_mask:0xf bank_mask:0xf bound_ctrl:1
	v_mov_b32_dpp v119, v107 row_shr:8 row_mask:0xf bank_mask:0xf bound_ctrl:1
	v_pk_add_f32 v[106:107], v[106:107], v[118:119]
	ds_swizzle_b32 v118, v106 offset:swizzle(BROADCAST,16,15)
	ds_swizzle_b32 v119, v107 offset:swizzle(BROADCAST,16,15)
	v_pk_add_f32 v[106:107], v[102:103], v[106:107]
	s_waitcnt lgkmcnt(0)
	v_pk_add_f32 v[102:103], v[102:103], v[118:119]
	v_mul_f32_e32 v118, 0x3fb8aa3b, v36
	v_exp_f32_e32 v118, v118
	v_mov_b32_dpp v119, v109 row_shr:2 row_mask:0xf bank_mask:0xf bound_ctrl:1
	v_sub_f32_e32 v125, 1.0, v118
	v_mul_f32_e32 v118, 0x3fb8aa3b, v37
	v_exp_f32_e32 v118, v118
	s_nop 0
	v_sub_f32_e32 v126, 1.0, v118
	v_mov_b32_dpp v118, v108 row_shr:2 row_mask:0xf bank_mask:0xf bound_ctrl:1
	v_pk_add_f32 v[108:109], v[108:109], v[118:119]
	s_nop 1
	v_mov_b32_dpp v118, v108 row_shr:4 row_mask:0xf bank_mask:0xf bound_ctrl:1
	v_mov_b32_dpp v119, v109 row_shr:4 row_mask:0xf bank_mask:0xf bound_ctrl:1
	v_pk_add_f32 v[108:109], v[108:109], v[118:119]
	s_nop 1
	v_mov_b32_dpp v118, v108 row_shr:8 row_mask:0xf bank_mask:0xf bound_ctrl:1
	v_mov_b32_dpp v119, v109 row_shr:8 row_mask:0xf bank_mask:0xf bound_ctrl:1
	v_pk_add_f32 v[108:109], v[108:109], v[118:119]
	ds_swizzle_b32 v118, v108 offset:swizzle(BROADCAST,16,15)
	ds_swizzle_b32 v119, v109 offset:swizzle(BROADCAST,16,15)
	v_pk_add_f32 v[108:109], v[116:117], v[108:109]
	s_waitcnt lgkmcnt(0)
	v_pk_add_f32 v[116:117], v[116:117], v[118:119]
	v_mul_f32_e32 v118, 0x3fb8aa3b, v38
	v_exp_f32_e32 v118, v118
	v_mov_b32_dpp v119, v33 row_shr:2 row_mask:0xf bank_mask:0xf bound_ctrl:1
	v_sub_f32_e32 v127, 1.0, v118
	v_mul_f32_e32 v118, 0x3fb8aa3b, v39
	v_exp_f32_e32 v118, v118
	s_nop 0
	v_sub_f32_e32 v128, 1.0, v118
	v_mov_b32_dpp v118, v32 row_shr:2 row_mask:0xf bank_mask:0xf bound_ctrl:1
	v_pk_add_f32 v[32:33], v[32:33], v[118:119]
	s_nop 1
	v_mov_b32_dpp v118, v32 row_shr:4 row_mask:0xf bank_mask:0xf bound_ctrl:1
	v_mov_b32_dpp v119, v33 row_shr:4 row_mask:0xf bank_mask:0xf bound_ctrl:1
	v_pk_add_f32 v[32:33], v[32:33], v[118:119]
	s_nop 1
	v_mov_b32_dpp v118, v32 row_shr:8 row_mask:0xf bank_mask:0xf bound_ctrl:1
	v_mov_b32_dpp v119, v33 row_shr:8 row_mask:0xf bank_mask:0xf bound_ctrl:1
	v_pk_add_f32 v[32:33], v[32:33], v[118:119]
	ds_swizzle_b32 v118, v32 offset:swizzle(BROADCAST,16,15)
	ds_swizzle_b32 v119, v33 offset:swizzle(BROADCAST,16,15)
	v_pk_add_f32 v[120:121], v[102:103], v[32:33]
	v_pk_add_f32 v[32:33], v[116:117], v[76:77] neg_lo:[0,1] neg_hi:[0,1]
	s_waitcnt lgkmcnt(0)
; __device__ __forceinline__ unsigned cvt_pk_bf16(float lo, float hi) { unsigned r; asm volatile("v_cvt_pk_bf16_f32 %0, %1, %2" : "=v"(r) : "v"(lo), "v"(hi)); return r; }
; __device__ __forceinline__ float log_forget(float z, float lb) {
;   const float r0 = fminf(z, 0.f) - __logf(1.f + __expf(-fabsf(z)));
;   __device__ __forceinline__ void operator()(const f32x4 (&acc)[2][2][4][2], const pg8::Unit& u, int wr, int wc, int fr, int fq) const {
;     ...
;             for (int m = 0; m < 4; ++m) { const int r = row0 + ai * 128 + m * 16; float bq[4], kq[4];
; #pragma unroll
;               for (int q = 0; q < 4; ++q) { bq[q] = bwd ? (carry[q] - cs[m][q]) + g[m][q] : cs[m][q]; kq[q] = 1.f - __expf(g[m][q]); }
;               *(f32x4*)(logfp + (size_t)r * 1024 + c + 4 * qh) = (f32x4){bq[0], bq[1], bq[2], bq[3]};
;               u32x2 w; w.x = pg8::cvt_pk_bf16(kq[0], kq[1]); w.y = pg8::cvt_pk_bf16(kq[2], kq[3]);
;               *(u32x2*)(km + (size_t)r * 1024 + c + 4 * qh) = w; } } }
	v_pk_add_f32 v[102:103], v[102:103], v[118:119]
	s_nop 0
	v_pk_add_f32 v[118:119], v[102:103], v[78:79] neg_lo:[0,1] neg_hi:[0,1]
	v_pk_add_f32 v[32:33], v[34:35], v[32:33]
	v_pk_add_f32 v[34:35], v[44:45], v[118:119]
	v_cndmask_b32_e64 v33, v77, v33, s[42:43]
	v_cndmask_b32_e64 v35, v79, v35, s[42:43]
	v_cndmask_b32_e64 v34, v78, v34, s[42:43]
	v_cndmask_b32_e64 v32, v76, v32, s[42:43]
	global_store_dwordx4 v[54:55], v[32:35], off offset:16
	s_nop 1
	v_cvt_pk_bf16_f32 v32, v115, v133
	v_cvt_pk_bf16_f32 v33, v134, v135
	global_store_dwordx2 v[52:53], v[32:33], off offset:8
	v_pk_add_f32 v[32:33], v[116:117], v[80:81] neg_lo:[0,1] neg_hi:[0,1]
	v_pk_add_f32 v[34:35], v[102:103], v[82:83] neg_lo:[0,1] neg_hi:[0,1]
	v_pk_add_f32 v[32:33], v[46:47], v[32:33]
	v_pk_add_f32 v[34:35], v[40:41], v[34:35]
	v_cndmask_b32_e64 v33, v81, v33, s[42:43]
	v_cndmask_b32_e64 v35, v83, v35, s[42:43]
	v_cndmask_b32_e64 v34, v82, v34, s[42:43]
	v_cndmask_b32_e64 v32, v80, v32, s[42:43]
	global_store_dwordx4 v[58:59], v[32:35], off offset:16
	s_nop 1
	v_cvt_pk_bf16_f32 v32, v130, v131
	v_cvt_pk_bf16_f32 v33, v122, v136
	global_store_dwordx2 v[56:57], v[32:33], off offset:8
	v_pk_add_f32 v[32:33], v[116:117], v[104:105] neg_lo:[0,1] neg_hi:[0,1]
	v_pk_add_f32 v[34:35], v[102:103], v[106:107] neg_lo:[0,1] neg_hi:[0,1]
	v_pk_add_f32 v[32:33], v[42:43], v[32:33]
	v_pk_add_f32 v[34:35], v[36:37], v[34:35]
	v_cndmask_b32_e64 v33, v105, v33, s[42:43]
	v_cndmask_b32_e64 v35, v107, v35, s[42:43]
	v_cndmask_b32_e64 v34, v106, v34, s[42:43]
	v_cndmask_b32_e64 v32, v104, v32, s[42:43]
	global_store_dwordx4 v[62:63], v[32:35], off offset:16
	v_mul_f32_e32 v37, 0x3fb8aa3b, v111
	v_exp_f32_e32 v37, v37
	v_cvt_pk_bf16_f32 v32, v123, v124
	v_cvt_pk_bf16_f32 v33, v125, v126
	global_store_dwordx2 v[60:61], v[32:33], off offset:8
	v_mul_f32_e32 v32, 0x3fb8aa3b, v110
	v_exp_f32_e32 v32, v32
	v_pk_add_f32 v[34:35], v[102:103], v[120:121] neg_lo:[0,1] neg_hi:[0,1]
	v_sub_f32_e32 v37, 1.0, v37
	v_pk_add_f32 v[34:35], v[110:111], v[34:35]
	v_sub_f32_e32 v36, 1.0, v32
	v_pk_add_f32 v[32:33], v[116:117], v[108:109] neg_lo:[0,1] neg_hi:[0,1]
	v_cndmask_b32_e64 v35, v121, v35, s[42:43]
	v_pk_add_f32 v[32:33], v[38:39], v[32:33]
	v_cndmask_b32_e64 v34, v120, v34, s[42:43]
	v_cndmask_b32_e64 v33, v109, v33, s[42:43]
	v_cndmask_b32_e64 v32, v108, v32, s[42:43]
	global_store_dwordx4 v[72:73], v[32:35], off offset:16
	s_nop 1
	v_cvt_pk_bf16_f32 v32, v127, v128
	v_cvt_pk_bf16_f32 v33, v36, v37
	global_store_dwordx2 v[74:75], v[32:33], off offset:8
	v_mul_f32_e64 v33, |v28|, s8
	v_exp_f32_e32 v33, v33
	v_max_f32_e32 v32, v28, v28
	v_add_f32_e32 v33, 1.0, v33
	v_cmp_gt_f32_e32 vcc, s37, v33
	v_min_f32_e32 v32, 0, v32
	s_nop 0
	v_cndmask_b32_e64 v34, 0, 32, vcc
	v_ldexp_f32 v33, v33, v34
	v_log_f32_e32 v33, v33
	s_nop 0
	v_mul_f32_e32 v34, 0x3f317217, v33
	v_fma_f32 v34, v33, s33, -v34
	v_fmac_f32_e32 v34, 0x3377d1cf, v33
	v_fmac_f32_e32 v34, 0x3f317217, v33
	v_cmp_lt_f32_e64 s[60:61], |v33|, s36
	s_nop 1
	v_cndmask_b32_e64 v33, v33, v34, s[60:61]
	v_cndmask_b32_e32 v34, 0, v216, vcc
	v_sub_f32_e32 v34, v33, v34
	s_nop 0
	s_nop 1
	s_nop 0
	s_nop 1
	v_max_f32_e32 v28, v29, v29
	v_min_f32_e32 v33, 0, v28
	v_mul_f32_e64 v28, |v29|, s8
	v_exp_f32_e32 v28, v28
	s_nop 0
	v_add_f32_e32 v28, 1.0, v28
	v_cmp_gt_f32_e32 vcc, s37, v28
	s_nop 1
	v_cndmask_b32_e64 v35, 0, 32, vcc
	v_ldexp_f32 v28, v28, v35
	v_log_f32_e32 v28, v28
	s_nop 0
	v_mul_f32_e32 v35, 0x3f317217, v28
	v_fma_f32 v35, v28, s33, -v35
	v_fmac_f32_e32 v35, 0x3377d1cf, v28
	v_fmac_f32_e32 v35, 0x3f317217, v28
	v_cmp_lt_f32_e64 s[60:61], |v28|, s36
	s_nop 1
	v_cndmask_b32_e64 v28, v28, v35, s[60:61]
	v_cndmask_b32_e32 v35, 0, v216, vcc
	v_sub_f32_e32 v35, v28, v35
	s_nop 0
	s_nop 0
	s_nop 1
	s_nop 0
	s_nop 1
	v_mul_f32_e64 v29, |v30|, s8
	v_exp_f32_e32 v29, v29
	v_max_f32_e32 v28, v30, v30
	v_min_f32_e32 v28, 0, v28
	v_add_f32_e32 v29, 1.0, v29
	v_cmp_gt_f32_e32 vcc, s37, v29
	s_nop 1
	v_cndmask_b32_e64 v36, 0, 32, vcc
	v_ldexp_f32 v29, v29, v36
	v_log_f32_e32 v29, v29
	s_nop 0
	v_mul_f32_e32 v36, 0x3f317217, v29
	v_fma_f32 v36, v29, s33, -v36
	v_fmac_f32_e32 v36, 0x3377d1cf, v29
	v_fmac_f32_e32 v36, 0x3f317217, v29
	v_cmp_lt_f32_e64 s[60:61], |v29|, s36
	s_nop 1
	v_cndmask_b32_e64 v29, v29, v36, s[60:61]
	v_cndmask_b32_e32 v36, 0, v216, vcc
	v_sub_f32_e32 v36, v29, v36
	s_nop 0
	s_nop 0
	s_nop 1
	s_nop 0
	s_nop 1
	v_mul_f32_e64 v30, |v31|, s8
	v_exp_f32_e32 v30, v30
	v_max_f32_e32 v29, v31, v31
	v_min_f32_e32 v29, 0, v29
	v_add_f32_e32 v30, 1.0, v30
	v_cmp_gt_f32_e32 vcc, s37, v30
	s_nop 1
	v_cndmask_b32_e64 v37, 0, 32, vcc
	v_ldexp_f32 v30, v30, v37
	v_log_f32_e32 v30, v30
	s_nop 0
	v_mul_f32_e32 v37, 0x3f317217, v30
	v_fma_f32 v37, v30, s33, -v37
	v_fmac_f32_e32 v37, 0x3377d1cf, v30
	v_fmac_f32_e32 v37, 0x3f317217, v30
	v_cmp_lt_f32_e64 s[60:61], |v30|, s36
	s_nop 1
	v_cndmask_b32_e64 v30, v30, v37, s[60:61]
	v_cndmask_b32_e32 v37, 0, v216, vcc
	v_sub_f32_e32 v37, v30, v37
	s_nop 0
	s_nop 0
	s_nop 1
	s_nop 0
	s_nop 1
	v_mul_f32_e64 v31, |v24|, s8
	v_exp_f32_e32 v31, v31
	v_max_f32_e32 v30, v24, v24
	v_add_f32_e32 v31, 1.0, v31
	v_cmp_gt_f32_e32 vcc, s37, v31
	v_min_f32_e32 v30, 0, v30
	s_nop 0
	v_cndmask_b32_e64 v38, 0, 32, vcc
	v_ldexp_f32 v31, v31, v38
	v_log_f32_e32 v31, v31
	s_nop 0
	v_mul_f32_e32 v38, 0x3f317217, v31
	v_fma_f32 v38, v31, s33, -v38
	v_fmac_f32_e32 v38, 0x3377d1cf, v31
	v_fmac_f32_e32 v38, 0x3f317217, v31
	v_cmp_lt_f32_e64 s[60:61], |v31|, s36
	s_nop 1
	v_cndmask_b32_e64 v31, v31, v38, s[60:61]
	v_cndmask_b32_e32 v38, 0, v216, vcc
	v_sub_f32_e32 v38, v31, v38
	s_nop 0
	s_nop 1
	s_nop 0
	s_nop 1
	v_max_f32_e32 v24, v25, v25
; template <int CTRL> __device__ __forceinline__ float dppx(float v) { return __int_as_float(__builtin_amdgcn_update_dpp(0, __float_as_int(v), CTRL, 0xf, 0xf, true)); }
; __device__ __forceinline__ float log_forget(float z, float lb) {
;   const float r0 = fminf(z, 0.f) - __logf(1.f + __expf(-fabsf(z)));
;   __device__ __forceinline__ void operator()(const f32x4 (&acc)[2][2][4][2], const pg8::Unit& u, int wr, int wc, int fr, int fq) const {
;     ...
;               for (int q = 0; q < 4; ++q) { const float gv = log_forget(acc[ai][bj][m][qh][q], lq[q]); g[m][q] = gv;
;                 float sc = gv; sc += dppx<0x111>(sc); sc += dppx<0x112>(sc); sc += dppx<0x114>(sc); sc += dppx<0x118>(sc);
;                 const float tot16 = __int_as_float(__builtin_amdgcn_ds_swizzle(__float_as_int(sc), 0x1F0));
	v_min_f32_e32 v31, 0, v24
	v_mul_f32_e64 v24, |v25|, s8
	v_exp_f32_e32 v24, v24
	s_nop 0
	v_add_f32_e32 v24, 1.0, v24
	v_cmp_gt_f32_e32 vcc, s37, v24
	s_nop 1
	v_cndmask_b32_e64 v39, 0, 32, vcc
	v_ldexp_f32 v24, v24, v39
	v_log_f32_e32 v24, v24
	s_nop 0
	v_mul_f32_e32 v39, 0x3f317217, v24
	v_fma_f32 v39, v24, s33, -v39
	v_fmac_f32_e32 v39, 0x3377d1cf, v24
	v_fmac_f32_e32 v39, 0x3f317217, v24
	v_cmp_lt_f32_e64 s[60:61], |v24|, s36
	s_nop 1
	v_cndmask_b32_e64 v24, v24, v39, s[60:61]
	v_cndmask_b32_e32 v39, 0, v216, vcc
	v_sub_f32_e32 v39, v24, v39
	v_pk_add_f32 v[30:31], v[30:31], v[38:39] neg_lo:[0,1] neg_hi:[0,1]
	v_mov_b32_e32 v30, v30
	s_nop 1
	v_mov_b32_dpp v38, v30 row_shr:1 row_mask:0xf bank_mask:0xf bound_ctrl:1
	s_nop 0
	s_nop 0
	s_nop 1
	v_mul_f32_e64 v25, |v26|, s8
	v_exp_f32_e32 v25, v25
	v_max_f32_e32 v24, v26, v26
	v_mov_b32_e32 v31, v31
	v_min_f32_e32 v24, 0, v24
	v_add_f32_e32 v25, 1.0, v25
	v_cmp_gt_f32_e32 vcc, s37, v25
	v_mov_b32_dpp v39, v31 row_shr:1 row_mask:0xf bank_mask:0xf bound_ctrl:1
	v_pk_add_f32 v[38:39], v[30:31], v[38:39]
	v_cndmask_b32_e64 v40, 0, 32, vcc
	v_ldexp_f32 v25, v25, v40
	v_log_f32_e32 v25, v25
	s_nop 0
	v_mul_f32_e32 v40, 0x3f317217, v25
	v_fma_f32 v40, v25, s33, -v40
	v_fmac_f32_e32 v40, 0x3377d1cf, v25
	v_fmac_f32_e32 v40, 0x3f317217, v25
	v_cmp_lt_f32_e64 s[60:61], |v25|, s36
	s_nop 1
	v_cndmask_b32_e64 v25, v25, v40, s[60:61]
	v_cndmask_b32_e32 v40, 0, v216, vcc
	v_sub_f32_e32 v40, v25, v40
	s_nop 0
	s_nop 0
	s_nop 1
	s_nop 0
	s_nop 1
	v_mul_f32_e64 v26, |v27|, s8
	v_exp_f32_e32 v26, v26
	v_max_f32_e32 v25, v27, v27
	v_min_f32_e32 v25, 0, v25
	v_add_f32_e32 v26, 1.0, v26
	v_cmp_gt_f32_e32 vcc, s37, v26
	s_nop 1
	v_cndmask_b32_e64 v41, 0, 32, vcc
	v_ldexp_f32 v26, v26, v41
	v_log_f32_e32 v26, v26
	s_nop 0
	v_mul_f32_e32 v41, 0x3f317217, v26
	v_fma_f32 v41, v26, s33, -v41
	v_fmac_f32_e32 v41, 0x3377d1cf, v26
	v_fmac_f32_e32 v41, 0x3f317217, v26
	v_cmp_lt_f32_e64 s[60:61], |v26|, s36
	s_nop 1
	v_cndmask_b32_e64 v26, v26, v41, s[60:61]
	v_cndmask_b32_e32 v41, 0, v216, vcc
	v_sub_f32_e32 v41, v26, v41
	s_nop 0
	s_nop 0
	s_nop 1
	s_nop 0
	s_nop 1
	v_mul_f32_e64 v27, |v20|, s8
	v_exp_f32_e32 v27, v27
	v_max_f32_e32 v26, v20, v20
	v_add_f32_e32 v27, 1.0, v27
	v_cmp_gt_f32_e32 vcc, s37, v27
	v_min_f32_e32 v26, 0, v26
	s_nop 0
	v_cndmask_b32_e64 v42, 0, 32, vcc
	v_ldexp_f32 v27, v27, v42
	v_log_f32_e32 v27, v27
	s_nop 0
	v_mul_f32_e32 v42, 0x3f317217, v27
	v_fma_f32 v42, v27, s33, -v42
	v_fmac_f32_e32 v42, 0x3377d1cf, v27
	v_fmac_f32_e32 v42, 0x3f317217, v27
	v_cmp_lt_f32_e64 s[60:61], |v27|, s36
	s_nop 1
	v_cndmask_b32_e64 v27, v27, v42, s[60:61]
	v_cndmask_b32_e32 v42, 0, v216, vcc
	v_sub_f32_e32 v42, v27, v42
	s_nop 0
	s_nop 1
	s_nop 0
	s_nop 1
	v_max_f32_e32 v20, v21, v21
	v_min_f32_e32 v27, 0, v20
	v_mul_f32_e64 v20, |v21|, s8
	v_exp_f32_e32 v20, v20
	s_nop 0
	v_add_f32_e32 v20, 1.0, v20
	v_cmp_gt_f32_e32 vcc, s37, v20
	s_nop 1
	v_cndmask_b32_e64 v43, 0, 32, vcc
	v_ldexp_f32 v20, v20, v43
	v_log_f32_e32 v20, v20
	s_nop 0
	v_mul_f32_e32 v43, 0x3f317217, v20
	v_fma_f32 v43, v20, s33, -v43
	v_fmac_f32_e32 v43, 0x3377d1cf, v20
	v_fmac_f32_e32 v43, 0x3f317217, v20
	v_cmp_lt_f32_e64 s[60:61], |v20|, s36
	s_nop 1
	v_cndmask_b32_e64 v20, v20, v43, s[60:61]
	v_cndmask_b32_e32 v43, 0, v216, vcc
	v_sub_f32_e32 v43, v20, v43
	v_pk_add_f32 v[26:27], v[26:27], v[42:43] neg_lo:[0,1] neg_hi:[0,1]
	v_mov_b32_e32 v42, v26
	s_nop 1
	v_mov_b32_dpp v26, v42 row_shr:1 row_mask:0xf bank_mask:0xf bound_ctrl:1
	s_nop 0
	s_nop 0
	s_nop 1
	v_max_f32_e32 v20, v22, v22
	v_min_f32_e32 v44, 0, v20
	v_mul_f32_e64 v20, |v22|, s8
	v_exp_f32_e32 v20, v20
	v_mov_b32_e32 v43, v27
	v_add_f32_e32 v20, 1.0, v20
	v_cmp_gt_f32_e32 vcc, s37, v20
	v_mov_b32_dpp v27, v43 row_shr:1 row_mask:0xf bank_mask:0xf bound_ctrl:1
	v_pk_add_f32 v[26:27], v[42:43], v[26:27]
	v_cndmask_b32_e64 v21, 0, 32, vcc
	v_ldexp_f32 v20, v20, v21
	v_log_f32_e32 v20, v20
	v_mov_b32_dpp v72, v26 row_shr:2 row_mask:0xf bank_mask:0xf bound_ctrl:1
	v_mov_b32_dpp v73, v27 row_shr:2 row_mask:0xf bank_mask:0xf bound_ctrl:1
	v_pk_add_f32 v[26:27], v[26:27], v[72:73]
	v_mul_f32_e32 v21, 0x3f317217, v20
	v_fma_f32 v21, v20, s33, -v21
	v_fmac_f32_e32 v21, 0x3377d1cf, v20
	v_fmac_f32_e32 v21, 0x3f317217, v20
	v_cmp_lt_f32_e64 s[60:61], |v20|, s36
	v_mov_b32_dpp v72, v26 row_shr:4 row_mask:0xf bank_mask:0xf bound_ctrl:1
	v_mov_b32_dpp v73, v27 row_shr:4 row_mask:0xf bank_mask:0xf bound_ctrl:1
	v_cndmask_b32_e64 v20, v20, v21, s[60:61]
	v_cndmask_b32_e32 v21, 0, v216, vcc
	v_sub_f32_e32 v46, v20, v21
	v_pk_add_f32 v[26:27], v[26:27], v[72:73]
	s_nop 1
	v_mov_b32_dpp v72, v26 row_shr:8 row_mask:0xf bank_mask:0xf bound_ctrl:1
	v_mov_b32_dpp v73, v27 row_shr:8 row_mask:0xf bank_mask:0xf bound_ctrl:1
	v_pk_add_f32 v[26:27], v[26:27], v[72:73]
	ds_swizzle_b32 v72, v26 offset:swizzle(BROADCAST,16,15)
	ds_swizzle_b32 v73, v27 offset:swizzle(BROADCAST,16,15)
	s_nop 0
	s_nop 1
	v_max_f32_e32 v20, v23, v23
	v_min_f32_e32 v45, 0, v20
	v_mul_f32_e64 v20, |v23|, s8
	v_exp_f32_e32 v20, v20
	s_nop 0
	v_add_f32_e32 v20, 1.0, v20
	v_cmp_gt_f32_e32 vcc, s37, v20
	s_nop 1
	v_cndmask_b32_e64 v21, 0, 32, vcc
	v_ldexp_f32 v20, v20, v21
	v_log_f32_e32 v20, v20
	s_nop 0
	v_mul_f32_e32 v21, 0x3f317217, v20
	v_fma_f32 v21, v20, s33, -v21
	v_fmac_f32_e32 v21, 0x3377d1cf, v20
	v_fmac_f32_e32 v21, 0x3f317217, v20
	v_cmp_lt_f32_e64 s[60:61], |v20|, s36
	s_nop 1
	v_cndmask_b32_e64 v20, v20, v21, s[60:61]
	v_cndmask_b32_e32 v21, 0, v216, vcc
	v_sub_f32_e32 v47, v20, v21
	s_nop 0
	s_nop 0
	s_nop 1
	s_nop 0
	s_nop 1
	v_max_f32_e32 v20, v16, v16
	v_min_f32_e32 v52, 0, v20
	v_mul_f32_e64 v20, |v16|, s8
; template <int CTRL> __device__ __forceinline__ float dppx(float v) { return __int_as_float(__builtin_amdgcn_update_dpp(0, __float_as_int(v), CTRL, 0xf, 0xf, true)); }
; __device__ __forceinline__ float log_forget(float z, float lb) {
;   const float r0 = fminf(z, 0.f) - __logf(1.f + __expf(-fabsf(z)));
;   const float r1 = __logf(lb + (1.f - lb) / (1.f + __expf(-z)));
;   return lb <= 0.f ? r0 : r1;
; }
;   __device__ __forceinline__ void operator()(const f32x4 (&acc)[2][2][4][2], const pg8::Unit& u, int wr, int wc, int fr, int fq) const {
;     ...
;               for (int q = 0; q < 4; ++q) { const float gv = log_forget(acc[ai][bj][m][qh][q], lq[q]); g[m][q] = gv;
;                 float sc = gv; sc += dppx<0x111>(sc); sc += dppx<0x112>(sc); sc += dppx<0x114>(sc); sc += dppx<0x118>(sc);
;                 const float tot16 = __int_as_float(__builtin_amdgcn_ds_swizzle(__float_as_int(sc), 0x1F0));
;                 cs[m][q] = sc + carry[q]; carry[q] += tot16; }
	v_exp_f32_e32 v20, v20
	s_nop 0
	v_add_f32_e32 v20, 1.0, v20
	v_cmp_gt_f32_e32 vcc, s37, v20
	s_nop 0
	s_nop 0
	v_cndmask_b32_e64 v21, 0, 32, vcc
	v_ldexp_f32 v20, v20, v21
	v_log_f32_e32 v20, v20
	s_nop 0
	v_mul_f32_e32 v21, 0x3f317217, v20
	v_fma_f32 v21, v20, s33, -v21
	v_fmac_f32_e32 v21, 0x3377d1cf, v20
	v_fmac_f32_e32 v21, 0x3f317217, v20
	v_cmp_lt_f32_e64 s[60:61], |v20|, s36
	s_nop 1
	v_cndmask_b32_e64 v20, v20, v21, s[60:61]
	v_cndmask_b32_e32 v21, 0, v216, vcc
	v_sub_f32_e32 v54, v20, v21
	s_nop 0
	s_nop 1
	s_nop 0
	s_nop 1
	v_max_f32_e32 v16, v17, v17
	v_min_f32_e32 v53, 0, v16
	v_mul_f32_e64 v16, |v17|, s8
	v_exp_f32_e32 v16, v16
	s_nop 0
	v_add_f32_e32 v16, 1.0, v16
	v_cmp_gt_f32_e32 vcc, s37, v16
	s_nop 1
	v_cndmask_b32_e64 v20, 0, 32, vcc
	v_ldexp_f32 v16, v16, v20
	v_log_f32_e32 v16, v16
	s_nop 0
	v_mul_f32_e32 v20, 0x3f317217, v16
	v_fma_f32 v20, v16, s33, -v20
	v_fmac_f32_e32 v20, 0x3377d1cf, v16
	v_fmac_f32_e32 v20, 0x3f317217, v16
	v_cmp_lt_f32_e64 s[60:61], |v16|, s36
	s_nop 1
	v_cndmask_b32_e64 v16, v16, v20, s[60:61]
	v_cndmask_b32_e32 v20, 0, v216, vcc
	v_sub_f32_e32 v55, v16, v20
	v_pk_add_f32 v[52:53], v[52:53], v[54:55] neg_lo:[0,1] neg_hi:[0,1]
	v_mov_b32_e32 v52, v52
	s_nop 1
	v_mov_b32_dpp v54, v52 row_shr:1 row_mask:0xf bank_mask:0xf bound_ctrl:1
	s_nop 0
	s_nop 0
	s_nop 1
	v_max_f32_e32 v16, v18, v18
	v_min_f32_e32 v56, 0, v16
	v_mul_f32_e64 v16, |v18|, s8
	v_exp_f32_e32 v16, v16
	v_mov_b32_e32 v53, v53
	v_add_f32_e32 v16, 1.0, v16
	v_cmp_gt_f32_e32 vcc, s37, v16
	v_mov_b32_dpp v55, v53 row_shr:1 row_mask:0xf bank_mask:0xf bound_ctrl:1
	v_pk_add_f32 v[54:55], v[52:53], v[54:55]
	v_cndmask_b32_e64 v17, 0, 32, vcc
	v_ldexp_f32 v16, v16, v17
	v_log_f32_e32 v16, v16
	v_mov_b32_dpp v68, v54 row_shr:2 row_mask:0xf bank_mask:0xf bound_ctrl:1
	v_mov_b32_dpp v69, v55 row_shr:2 row_mask:0xf bank_mask:0xf bound_ctrl:1
	v_pk_add_f32 v[54:55], v[54:55], v[68:69]
	v_mul_f32_e32 v17, 0x3f317217, v16
	v_fma_f32 v17, v16, s33, -v17
	v_fmac_f32_e32 v17, 0x3377d1cf, v16
	v_fmac_f32_e32 v17, 0x3f317217, v16
	v_cmp_lt_f32_e64 s[60:61], |v16|, s36
	v_mov_b32_dpp v68, v54 row_shr:4 row_mask:0xf bank_mask:0xf bound_ctrl:1
	v_mov_b32_dpp v69, v55 row_shr:4 row_mask:0xf bank_mask:0xf bound_ctrl:1
	v_cndmask_b32_e64 v16, v16, v17, s[60:61]
	v_cndmask_b32_e32 v17, 0, v216, vcc
	v_sub_f32_e32 v58, v16, v17
	v_pk_add_f32 v[54:55], v[54:55], v[68:69]
	s_nop 1
	v_mov_b32_dpp v68, v54 row_shr:8 row_mask:0xf bank_mask:0xf bound_ctrl:1
	v_mov_b32_dpp v69, v55 row_shr:8 row_mask:0xf bank_mask:0xf bound_ctrl:1
	v_pk_add_f32 v[54:55], v[54:55], v[68:69]
	ds_swizzle_b32 v68, v54 offset:swizzle(BROADCAST,16,15)
	ds_swizzle_b32 v69, v55 offset:swizzle(BROADCAST,16,15)
	s_nop 0
	s_nop 1
	v_max_f32_e32 v16, v19, v19
	v_min_f32_e32 v57, 0, v16
	v_mul_f32_e64 v16, |v19|, s8
	v_exp_f32_e32 v16, v16
	s_nop 0
	v_add_f32_e32 v16, 1.0, v16
	v_cmp_gt_f32_e32 vcc, s37, v16
	s_nop 1
	v_cndmask_b32_e64 v17, 0, 32, vcc
	v_ldexp_f32 v16, v16, v17
	v_log_f32_e32 v16, v16
	s_nop 0
	v_mul_f32_e32 v17, 0x3f317217, v16
	v_fma_f32 v17, v16, s33, -v17
	v_fmac_f32_e32 v17, 0x3377d1cf, v16
	v_fmac_f32_e32 v17, 0x3f317217, v16
	v_cmp_lt_f32_e64 s[60:61], |v16|, s36
	s_nop 1
	v_cndmask_b32_e64 v16, v16, v17, s[60:61]
	v_cndmask_b32_e32 v17, 0, v216, vcc
	v_sub_f32_e32 v59, v16, v17
	v_mul_f32_e32 v16, 0xbfb8aa3b, v19
	v_exp_f32_e32 v16, v16
	v_pk_add_f32 v[56:57], v[56:57], v[58:59] neg_lo:[0,1] neg_hi:[0,1]
	v_add_f32_e32 v16, 1.0, v16
	v_div_scale_f32 v17, s[2:3], v16, v16, v154
	v_rcp_f32_e32 v18, v17
	v_mov_b32_e32 v56, v56
	v_fma_f32 v19, -v17, v18, 1.0
	v_fmac_f32_e32 v18, v19, v18
	v_div_scale_f32 v19, vcc, v154, v16, v154
	v_mul_f32_e32 v20, v19, v18
	v_fma_f32 v21, -v17, v20, v19
	v_fmac_f32_e32 v20, v21, v18
	v_fma_f32 v17, -v17, v20, v19
	v_div_fmas_f32 v17, v17, v18, v20
	v_div_fixup_f32 v16, v17, v16, v154
	v_add_f32_e32 v16, v71, v16
	v_cmp_gt_f32_e32 vcc, s37, v16
	v_mov_b32_dpp v58, v56 row_shr:1 row_mask:0xf bank_mask:0xf bound_ctrl:1
	s_nop 0
	v_cndmask_b32_e64 v17, 0, 32, vcc
	v_ldexp_f32 v16, v16, v17
	v_log_f32_e32 v16, v16
	s_nop 0
	v_cmp_lt_f32_e64 s[60:61], |v16|, s36
	s_nop 1
	v_pk_add_f32 v[16:17], v[32:33], v[34:35] neg_lo:[0,1] neg_hi:[0,1]
	v_mov_b32_e32 v57, v57
	v_mov_b32_e32 v33, v17
	v_mov_b32_e32 v32, v16
	v_mov_b32_dpp v60, v38 row_shr:2 row_mask:0xf bank_mask:0xf bound_ctrl:1
	v_mov_b32_dpp v17, v33 row_shr:1 row_mask:0xf bank_mask:0xf bound_ctrl:1
	v_mov_b32_dpp v16, v32 row_shr:1 row_mask:0xf bank_mask:0xf bound_ctrl:1
	v_pk_add_f32 v[16:17], v[32:33], v[16:17]
	v_mov_b32_dpp v61, v39 row_shr:2 row_mask:0xf bank_mask:0xf bound_ctrl:1
	v_pk_add_f32 v[38:39], v[38:39], v[60:61]
	v_mov_b32_dpp v18, v16 row_shr:2 row_mask:0xf bank_mask:0xf bound_ctrl:1
	v_mov_b32_dpp v19, v17 row_shr:2 row_mask:0xf bank_mask:0xf bound_ctrl:1
	v_pk_add_f32 v[16:17], v[16:17], v[18:19]
	v_mov_b32_dpp v60, v38 row_shr:4 row_mask:0xf bank_mask:0xf bound_ctrl:1
	v_mov_b32_dpp v61, v39 row_shr:4 row_mask:0xf bank_mask:0xf bound_ctrl:1
	v_mov_b32_dpp v18, v16 row_shr:4 row_mask:0xf bank_mask:0xf bound_ctrl:1
	v_mov_b32_dpp v19, v17 row_shr:4 row_mask:0xf bank_mask:0xf bound_ctrl:1
	v_pk_add_f32 v[16:17], v[16:17], v[18:19]
	v_pk_add_f32 v[38:39], v[38:39], v[60:61]
	v_mov_b32_dpp v59, v57 row_shr:1 row_mask:0xf bank_mask:0xf bound_ctrl:1
	v_mov_b32_dpp v18, v16 row_shr:8 row_mask:0xf bank_mask:0xf bound_ctrl:1
	v_mov_b32_dpp v19, v17 row_shr:8 row_mask:0xf bank_mask:0xf bound_ctrl:1
	v_pk_add_f32 v[16:17], v[16:17], v[18:19]
	ds_swizzle_b32 v18, v16 offset:swizzle(BROADCAST,16,15)
	v_pk_add_f32 v[34:35], v[16:17], 0 op_sel_hi:[1,0]
	v_mul_f32_e32 v16, 0x3fb8aa3b, v32
	v_exp_f32_e32 v16, v16
	ds_swizzle_b32 v19, v17 offset:swizzle(BROADCAST,16,15)
	v_mov_b32_dpp v60, v38 row_shr:8 row_mask:0xf bank_mask:0xf bound_ctrl:1
	v_mov_b32_dpp v61, v39 row_shr:8 row_mask:0xf bank_mask:0xf bound_ctrl:1
	v_sub_f32_e32 v80, 1.0, v16
	v_mul_f32_e32 v16, 0x3fb8aa3b, v33
	v_exp_f32_e32 v16, v16
	s_waitcnt lgkmcnt(0)
; template <int CTRL> __device__ __forceinline__ float dppx(float v) { return __int_as_float(__builtin_amdgcn_update_dpp(0, __float_as_int(v), CTRL, 0xf, 0xf, true)); }
;   __device__ __forceinline__ void operator()(const f32x4 (&acc)[2][2][4][2], const pg8::Unit& u, int wr, int wc, int fr, int fq) const {
;     ...
;                 float sc = gv; sc += dppx<0x111>(sc); sc += dppx<0x112>(sc); sc += dppx<0x114>(sc); sc += dppx<0x118>(sc);
;                 const float tot16 = __int_as_float(__builtin_amdgcn_ds_swizzle(__float_as_int(sc), 0x1F0));
;                 cs[m][q] = sc + carry[q]; carry[q] += tot16; }
; #pragma unroll
;             for (int m = 0; m < 4; ++m) { const int r = row0 + ai * 128 + m * 16; float bq[4], kq[4];
; #pragma unroll
;               for (int q = 0; q < 4; ++q) { bq[q] = bwd ? (carry[q] - cs[m][q]) + g[m][q] : cs[m][q]; kq[q] = 1.f - __expf(g[m][q]); }
	v_pk_add_f32 v[20:21], v[18:19], 0 op_sel_hi:[1,0]
	v_pk_add_f32 v[38:39], v[38:39], v[60:61]
	ds_swizzle_b32 v60, v38 offset:swizzle(BROADCAST,16,15)
	v_sub_f32_e32 v81, 1.0, v16
	v_pk_add_f32 v[16:17], v[28:29], v[36:37] neg_lo:[0,1] neg_hi:[0,1]
	ds_swizzle_b32 v61, v39 offset:swizzle(BROADCAST,16,15)
	v_mov_b32_e32 v29, v17
	v_mov_b32_e32 v28, v16
	v_pk_add_f32 v[38:39], v[20:21], v[38:39]
	v_mov_b32_dpp v17, v29 row_shr:1 row_mask:0xf bank_mask:0xf bound_ctrl:1
	v_mov_b32_dpp v16, v28 row_shr:1 row_mask:0xf bank_mask:0xf bound_ctrl:1
	v_pk_add_f32 v[16:17], v[28:29], v[16:17]
	s_waitcnt lgkmcnt(0)
	v_pk_add_f32 v[62:63], v[20:21], v[60:61]
	v_mul_f32_e32 v20, 0x3fb8aa3b, v30
	v_mov_b32_dpp v18, v16 row_shr:2 row_mask:0xf bank_mask:0xf bound_ctrl:1
	v_mov_b32_dpp v19, v17 row_shr:2 row_mask:0xf bank_mask:0xf bound_ctrl:1
	v_pk_add_f32 v[16:17], v[16:17], v[18:19]
	v_exp_f32_e32 v20, v20
	v_pk_add_f32 v[58:59], v[56:57], v[58:59]
	v_mov_b32_dpp v18, v16 row_shr:4 row_mask:0xf bank_mask:0xf bound_ctrl:1
	v_mov_b32_dpp v19, v17 row_shr:4 row_mask:0xf bank_mask:0xf bound_ctrl:1
	v_pk_add_f32 v[16:17], v[16:17], v[18:19]
	s_nop 1
	v_mov_b32_dpp v18, v16 row_shr:8 row_mask:0xf bank_mask:0xf bound_ctrl:1
	v_mov_b32_dpp v19, v17 row_shr:8 row_mask:0xf bank_mask:0xf bound_ctrl:1
	v_pk_add_f32 v[16:17], v[16:17], v[18:19]
	ds_swizzle_b32 v18, v16 offset:swizzle(BROADCAST,16,15)
	ds_swizzle_b32 v19, v17 offset:swizzle(BROADCAST,16,15)
	v_pk_add_f32 v[36:37], v[16:17], 0 op_sel_hi:[1,0]
	v_mul_f32_e32 v16, 0x3fb8aa3b, v28
	v_exp_f32_e32 v16, v16
	s_waitcnt lgkmcnt(0)
	v_pk_add_f32 v[22:23], v[18:19], 0 op_sel_hi:[1,0]
	v_lshl_add_u64 v[18:19], v[84:85], 0, v[50:51]
	v_sub_f32_e32 v84, 1.0, v20
	v_mul_f32_e32 v20, 0x3fb8aa3b, v31
	v_exp_f32_e32 v20, v20
	v_sub_f32_e32 v82, 1.0, v16
	v_mul_f32_e32 v16, 0x3fb8aa3b, v29
	v_exp_f32_e32 v16, v16
	v_sub_f32_e32 v85, 1.0, v20
	v_pk_add_f32 v[20:21], v[24:25], v[40:41] neg_lo:[0,1] neg_hi:[0,1]
	v_sub_f32_e32 v83, 1.0, v16
	v_mov_b32_e32 v41, v21
	v_mov_b32_e32 v40, v20
	v_pk_add_f32 v[74:75], v[62:63], v[26:27]
	v_mov_b32_dpp v21, v41 row_shr:1 row_mask:0xf bank_mask:0xf bound_ctrl:1
	v_mov_b32_dpp v20, v40 row_shr:1 row_mask:0xf bank_mask:0xf bound_ctrl:1
	v_pk_add_f32 v[20:21], v[40:41], v[20:21]
	v_mul_f32_e32 v26, 0x3fb8aa3b, v42
	v_exp_f32_e32 v26, v26
	v_mov_b32_dpp v24, v20 row_shr:2 row_mask:0xf bank_mask:0xf bound_ctrl:1
	v_mov_b32_dpp v25, v21 row_shr:2 row_mask:0xf bank_mask:0xf bound_ctrl:1
	v_pk_add_f32 v[20:21], v[20:21], v[24:25]
	v_pk_add_f32 v[62:63], v[62:63], v[72:73]
	v_sub_f32_e32 v76, 1.0, v26
	v_mov_b32_dpp v24, v20 row_shr:4 row_mask:0xf bank_mask:0xf bound_ctrl:1
	v_mov_b32_dpp v25, v21 row_shr:4 row_mask:0xf bank_mask:0xf bound_ctrl:1
	v_pk_add_f32 v[20:21], v[20:21], v[24:25]
	v_mul_f32_e32 v26, 0x3fb8aa3b, v43
	v_pk_add_f32 v[54:55], v[62:63], v[54:55]
	v_mov_b32_dpp v24, v20 row_shr:8 row_mask:0xf bank_mask:0xf bound_ctrl:1
	v_mov_b32_dpp v25, v21 row_shr:8 row_mask:0xf bank_mask:0xf bound_ctrl:1
	v_pk_add_f32 v[20:21], v[20:21], v[24:25]
	ds_swizzle_b32 v24, v20 offset:swizzle(BROADCAST,16,15)
	ds_swizzle_b32 v25, v21 offset:swizzle(BROADCAST,16,15)
	v_pk_add_f32 v[62:63], v[62:63], v[68:69]
	v_mul_f32_e32 v68, 0x3fb8aa3b, v52
	v_exp_f32_e32 v26, v26
	v_exp_f32_e32 v68, v68
	v_pk_add_f32 v[60:61], v[22:23], v[20:21]
	s_waitcnt lgkmcnt(0)
	v_pk_add_f32 v[24:25], v[22:23], v[24:25]
	v_lshl_add_u64 v[22:23], v[88:89], 0, v[50:51]
	v_sub_f32_e32 v77, 1.0, v26
	v_pk_add_f32 v[26:27], v[44:45], v[46:47] neg_lo:[0,1] neg_hi:[0,1]
	v_sub_f32_e32 v88, 1.0, v68
	v_mul_f32_e32 v68, 0x3fb8aa3b, v53
	v_mov_b32_e32 v45, v27
	v_mov_b32_e32 v44, v26
	v_exp_f32_e32 v68, v68
	v_mov_b32_dpp v27, v45 row_shr:1 row_mask:0xf bank_mask:0xf bound_ctrl:1
	v_mov_b32_dpp v26, v44 row_shr:1 row_mask:0xf bank_mask:0xf bound_ctrl:1
	v_pk_add_f32 v[26:27], v[44:45], v[26:27]
	v_sub_f32_e32 v89, 1.0, v68
	v_mov_b32_dpp v68, v58 row_shr:2 row_mask:0xf bank_mask:0xf bound_ctrl:1
	v_mov_b32_dpp v46, v26 row_shr:2 row_mask:0xf bank_mask:0xf bound_ctrl:1
	v_mov_b32_dpp v47, v27 row_shr:2 row_mask:0xf bank_mask:0xf bound_ctrl:1
	v_pk_add_f32 v[26:27], v[26:27], v[46:47]
	v_mov_b32_dpp v69, v59 row_shr:2 row_mask:0xf bank_mask:0xf bound_ctrl:1
	v_pk_add_f32 v[58:59], v[58:59], v[68:69]
	v_mov_b32_dpp v46, v26 row_shr:4 row_mask:0xf bank_mask:0xf bound_ctrl:1
	v_mov_b32_dpp v47, v27 row_shr:4 row_mask:0xf bank_mask:0xf bound_ctrl:1
	v_pk_add_f32 v[26:27], v[26:27], v[46:47]
	v_mov_b32_dpp v68, v58 row_shr:4 row_mask:0xf bank_mask:0xf bound_ctrl:1
	v_mov_b32_dpp v69, v59 row_shr:4 row_mask:0xf bank_mask:0xf bound_ctrl:1
	v_mov_b32_dpp v46, v26 row_shr:8 row_mask:0xf bank_mask:0xf bound_ctrl:1
	v_mov_b32_dpp v47, v27 row_shr:8 row_mask:0xf bank_mask:0xf bound_ctrl:1
	v_pk_add_f32 v[58:59], v[58:59], v[68:69]
	v_pk_add_f32 v[26:27], v[26:27], v[46:47]
	ds_swizzle_b32 v46, v26 offset:swizzle(BROADCAST,16,15)
	v_mov_b32_dpp v68, v58 row_shr:8 row_mask:0xf bank_mask:0xf bound_ctrl:1
	v_mov_b32_dpp v69, v59 row_shr:8 row_mask:0xf bank_mask:0xf bound_ctrl:1
	ds_swizzle_b32 v47, v27 offset:swizzle(BROADCAST,16,15)
	v_pk_add_f32 v[58:59], v[58:59], v[68:69]
	ds_swizzle_b32 v68, v58 offset:swizzle(BROADCAST,16,15)
	ds_swizzle_b32 v69, v59 offset:swizzle(BROADCAST,16,15)
	v_mul_f32_e32 v20, 0x3fb8aa3b, v40
	v_exp_f32_e32 v20, v20
	s_waitcnt lgkmcnt(2)
	v_pk_add_f32 v[46:47], v[24:25], v[46:47]
	v_pk_add_f32 v[72:73], v[24:25], v[26:27]
	v_pk_add_f32 v[58:59], v[46:47], v[58:59]
	s_waitcnt lgkmcnt(0)
; __device__ __forceinline__ unsigned cvt_pk_bf16(float lo, float hi) { unsigned r; asm volatile("v_cvt_pk_bf16_f32 %0, %1, %2" : "=v"(r) : "v"(lo), "v"(hi)); return r; }
; __device__ __forceinline__ float log_forget(float z, float lb) {
;   const float r0 = fminf(z, 0.f) - __logf(1.f + __expf(-fabsf(z)));
;   __device__ __forceinline__ void operator()(const f32x4 (&acc)[2][2][4][2], const pg8::Unit& u, int wr, int wc, int fr, int fq) const {
;     ...
;             for (int m = 0; m < 4; ++m) { const int r = row0 + ai * 128 + m * 16; float bq[4], kq[4];
; #pragma unroll
;               for (int q = 0; q < 4; ++q) { bq[q] = bwd ? (carry[q] - cs[m][q]) + g[m][q] : cs[m][q]; kq[q] = 1.f - __expf(g[m][q]); }
;               *(f32x4*)(logfp + (size_t)r * 1024 + c + 4 * qh) = (f32x4){bq[0], bq[1], bq[2], bq[3]};
;               u32x2 w; w.x = pg8::cvt_pk_bf16(kq[0], kq[1]); w.y = pg8::cvt_pk_bf16(kq[2], kq[3]);
;               *(u32x2*)(km + (size_t)r * 1024 + c + 4 * qh) = w; } } }
	v_pk_add_f32 v[46:47], v[46:47], v[68:69]
	v_pk_add_f32 v[68:69], v[62:63], v[34:35] neg_lo:[0,1] neg_hi:[0,1]
	v_pk_add_f32 v[70:71], v[46:47], v[36:37] neg_lo:[0,1] neg_hi:[0,1]
	v_mul_f32_e32 v24, 0x3fb8aa3b, v44
	v_pk_add_f32 v[32:33], v[32:33], v[68:69]
	v_pk_add_f32 v[28:29], v[28:29], v[70:71]
	v_lshl_add_u64 v[16:17], v[86:87], 0, v[48:49]
	v_sub_f32_e32 v86, 1.0, v20
	v_mul_f32_e32 v20, 0x3fb8aa3b, v41
	v_exp_f32_e32 v24, v24
	v_cndmask_b32_e64 v37, v37, v29, s[42:43]
	v_cndmask_b32_e64 v36, v36, v28, s[42:43]
	v_cndmask_b32_e64 v35, v35, v33, s[42:43]
	v_cndmask_b32_e64 v34, v34, v32, s[42:43]
	v_exp_f32_e32 v20, v20
	global_store_dwordx4 v[18:19], v[34:37], off
	v_cvt_pk_bf16_f32 v28, v80, v81
	v_cvt_pk_bf16_f32 v29, v82, v83
	global_store_dwordx2 v[16:17], v[28:29], off
	v_pk_add_f32 v[28:29], v[62:63], v[38:39] neg_lo:[0,1] neg_hi:[0,1]
	v_pk_add_f32 v[32:33], v[46:47], v[60:61] neg_lo:[0,1] neg_hi:[0,1]
	v_pk_add_f32 v[28:29], v[30:31], v[28:29]
	v_pk_add_f32 v[30:31], v[40:41], v[32:33]
	v_sub_f32_e32 v78, 1.0, v24
	v_mul_f32_e32 v24, 0x3fb8aa3b, v45
	v_cndmask_b32_e64 v31, v61, v31, s[42:43]
	v_cndmask_b32_e64 v30, v60, v30, s[42:43]
	v_cndmask_b32_e64 v29, v39, v29, s[42:43]
	v_cndmask_b32_e64 v28, v38, v28, s[42:43]
	v_sub_f32_e32 v87, 1.0, v20
	v_lshl_add_u64 v[20:21], v[90:91], 0, v[48:49]
	v_exp_f32_e32 v24, v24
	global_store_dwordx4 v[22:23], v[28:31], off
	v_lshl_add_u64 v[26:27], v[92:93], 0, v[50:51]
	v_sub_f32_e32 v79, 1.0, v24
	v_cvt_pk_bf16_f32 v28, v84, v85
	v_cvt_pk_bf16_f32 v29, v86, v87
	global_store_dwordx2 v[20:21], v[28:29], off
	v_pk_add_f32 v[28:29], v[62:63], v[74:75] neg_lo:[0,1] neg_hi:[0,1]
	v_pk_add_f32 v[30:31], v[46:47], v[72:73] neg_lo:[0,1] neg_hi:[0,1]
	v_pk_add_f32 v[28:29], v[42:43], v[28:29]
	v_pk_add_f32 v[30:31], v[44:45], v[30:31]
	v_cndmask_b32_e64 v29, v75, v29, s[42:43]
	v_cndmask_b32_e64 v31, v73, v31, s[42:43]
	v_cndmask_b32_e64 v30, v72, v30, s[42:43]
	v_cndmask_b32_e64 v28, v74, v28, s[42:43]
	v_lshl_add_u64 v[24:25], v[94:95], 0, v[48:49]
	global_store_dwordx4 v[26:27], v[28:31], off
	s_nop 1
	v_cvt_pk_bf16_f32 v28, v76, v77
	v_cvt_pk_bf16_f32 v29, v78, v79
	global_store_dwordx2 v[24:25], v[28:29], off
	v_mul_f32_e32 v28, 0x3fb8aa3b, v56
	v_exp_f32_e32 v28, v28
	v_pk_add_f32 v[30:31], v[46:47], v[58:59] neg_lo:[0,1] neg_hi:[0,1]
	v_sub_f32_e32 v34, 1.0, v28
	v_pk_add_f32 v[28:29], v[62:63], v[54:55] neg_lo:[0,1] neg_hi:[0,1]
	v_pk_add_f32 v[30:31], v[56:57], v[30:31]
	v_pk_add_f32 v[28:29], v[52:53], v[28:29]
	v_cndmask_b32_e64 v32, v58, v30, s[42:43]
	v_cndmask_b32_e64 v30, v54, v28, s[42:43]
	v_mul_f32_e32 v28, 0x3fb8aa3b, v57
	v_exp_f32_e32 v28, v28
	v_cndmask_b32_e64 v33, v59, v31, s[42:43]
	v_cndmask_b32_e64 v31, v55, v29, s[42:43]
	v_sub_f32_e32 v35, 1.0, v28
	v_lshl_add_u64 v[28:29], v[98:99], 0, v[50:51]
	global_store_dwordx4 v[28:29], v[30:33], off
	s_nop 1
	v_cvt_pk_bf16_f32 v32, v88, v89
	v_cvt_pk_bf16_f32 v33, v34, v35
	v_lshl_add_u64 v[30:31], v[100:101], 0, v[48:49]
	global_store_dwordx2 v[30:31], v[32:33], off
	v_mul_f32_e64 v33, |v12|, s8
	v_exp_f32_e32 v33, v33
	v_max_f32_e32 v32, v12, v12
	v_add_f32_e32 v33, 1.0, v33
	v_cmp_gt_f32_e32 vcc, s37, v33
	v_min_f32_e32 v32, 0, v32
	s_nop 0
	v_cndmask_b32_e64 v34, 0, 32, vcc
	v_ldexp_f32 v33, v33, v34
	v_log_f32_e32 v33, v33
	s_nop 0
	v_mul_f32_e32 v34, 0x3f317217, v33
	v_fma_f32 v34, v33, s33, -v34
	v_fmac_f32_e32 v34, 0x3377d1cf, v33
	v_fmac_f32_e32 v34, 0x3f317217, v33
	v_cmp_lt_f32_e64 s[44:45], |v33|, s36
	s_nop 1
	v_cndmask_b32_e64 v33, v33, v34, s[44:45]
	v_cndmask_b32_e32 v34, 0, v216, vcc
	v_sub_f32_e32 v34, v33, v34
	s_nop 0
	s_nop 1
	s_nop 0
	s_nop 1
	v_max_f32_e32 v12, v13, v13
	v_min_f32_e32 v33, 0, v12
	v_mul_f32_e64 v12, |v13|, s8
	v_exp_f32_e32 v12, v12
	s_nop 0
	v_add_f32_e32 v12, 1.0, v12
	v_cmp_gt_f32_e32 vcc, s37, v12
	s_nop 1
	v_cndmask_b32_e64 v35, 0, 32, vcc
	v_ldexp_f32 v12, v12, v35
	v_log_f32_e32 v12, v12
	s_nop 0
	v_mul_f32_e32 v35, 0x3f317217, v12
	v_fma_f32 v35, v12, s33, -v35
	v_fmac_f32_e32 v35, 0x3377d1cf, v12
	v_fmac_f32_e32 v35, 0x3f317217, v12
	v_cmp_lt_f32_e64 s[44:45], |v12|, s36
	s_nop 1
	v_cndmask_b32_e64 v12, v12, v35, s[44:45]
	v_cndmask_b32_e32 v35, 0, v216, vcc
	v_sub_f32_e32 v35, v12, v35
	s_nop 0
	s_nop 0
	s_nop 1
	s_nop 0
	s_nop 1
	v_mul_f32_e64 v13, |v14|, s8
	v_exp_f32_e32 v13, v13
	v_max_f32_e32 v12, v14, v14
	v_min_f32_e32 v12, 0, v12
	v_add_f32_e32 v13, 1.0, v13
	v_cmp_gt_f32_e32 vcc, s37, v13
	s_nop 1
	v_cndmask_b32_e64 v36, 0, 32, vcc
	v_ldexp_f32 v13, v13, v36
	v_log_f32_e32 v13, v13
	s_nop 0
	v_mul_f32_e32 v36, 0x3f317217, v13
	v_fma_f32 v36, v13, s33, -v36
	v_fmac_f32_e32 v36, 0x3377d1cf, v13
	v_fmac_f32_e32 v36, 0x3f317217, v13
	v_cmp_lt_f32_e64 s[44:45], |v13|, s36
	s_nop 1
	v_cndmask_b32_e64 v13, v13, v36, s[44:45]
	v_cndmask_b32_e32 v36, 0, v216, vcc
	v_sub_f32_e32 v36, v13, v36
	s_nop 0
	s_nop 0
	s_nop 1
	s_nop 0
	s_nop 1
	v_mul_f32_e64 v14, |v15|, s8
	v_exp_f32_e32 v14, v14
	v_max_f32_e32 v13, v15, v15
	v_min_f32_e32 v13, 0, v13
	v_add_f32_e32 v14, 1.0, v14
	v_cmp_gt_f32_e32 vcc, s37, v14
	s_nop 1
	v_cndmask_b32_e64 v37, 0, 32, vcc
	v_ldexp_f32 v14, v14, v37
	v_log_f32_e32 v14, v14
	s_nop 0
	v_mul_f32_e32 v37, 0x3f317217, v14
	v_fma_f32 v37, v14, s33, -v37
	v_fmac_f32_e32 v37, 0x3377d1cf, v14
	v_fmac_f32_e32 v37, 0x3f317217, v14
	v_cmp_lt_f32_e64 s[44:45], |v14|, s36
	s_nop 1
	v_cndmask_b32_e64 v14, v14, v37, s[44:45]
	v_cndmask_b32_e32 v37, 0, v216, vcc
	v_sub_f32_e32 v37, v14, v37
	v_pk_add_f32 v[12:13], v[12:13], v[36:37] neg_lo:[0,1] neg_hi:[0,1]
	v_mov_b32_e32 v12, v12
	s_nop 1
	s_nop 0
	s_nop 1
	v_mul_f32_e64 v15, |v8|, s8
	v_exp_f32_e32 v15, v15
; template <int CTRL> __device__ __forceinline__ float dppx(float v) { return __int_as_float(__builtin_amdgcn_update_dpp(0, __float_as_int(v), CTRL, 0xf, 0xf, true)); }
; __device__ __forceinline__ float log_forget(float z, float lb) {
;   const float r0 = fminf(z, 0.f) - __logf(1.f + __expf(-fabsf(z)));
;   __device__ __forceinline__ void operator()(const f32x4 (&acc)[2][2][4][2], const pg8::Unit& u, int wr, int wc, int fr, int fq) const {
;     ...
;               for (int q = 0; q < 4; ++q) { const float gv = log_forget(acc[ai][bj][m][qh][q], lq[q]); g[m][q] = gv;
;                 float sc = gv; sc += dppx<0x111>(sc); sc += dppx<0x112>(sc); sc += dppx<0x114>(sc); sc += dppx<0x118>(sc);
	v_max_f32_e32 v14, v8, v8
	v_add_f32_e32 v15, 1.0, v15
	v_cmp_gt_f32_e32 vcc, s37, v15
	v_mov_b32_e32 v13, v13
	s_nop 0
	v_cndmask_b32_e64 v38, 0, 32, vcc
	v_ldexp_f32 v15, v15, v38
	v_log_f32_e32 v15, v15
	v_min_f32_e32 v14, 0, v14
	v_mul_f32_e32 v38, 0x3f317217, v15
	v_fma_f32 v38, v15, s33, -v38
	v_fmac_f32_e32 v38, 0x3377d1cf, v15
	v_fmac_f32_e32 v38, 0x3f317217, v15
	v_cmp_lt_f32_e64 s[44:45], |v15|, s36
	s_nop 1
	v_cndmask_b32_e64 v15, v15, v38, s[44:45]
	v_cndmask_b32_e32 v38, 0, v216, vcc
	v_sub_f32_e32 v38, v15, v38
	s_nop 0
	s_nop 1
	s_nop 0
	s_nop 1
	v_max_f32_e32 v8, v9, v9
	v_min_f32_e32 v15, 0, v8
	v_mul_f32_e64 v8, |v9|, s8
	v_exp_f32_e32 v8, v8
	s_nop 0
	v_add_f32_e32 v8, 1.0, v8
	v_cmp_gt_f32_e32 vcc, s37, v8
	s_nop 1
	v_cndmask_b32_e64 v39, 0, 32, vcc
	v_ldexp_f32 v8, v8, v39
	v_log_f32_e32 v8, v8
	s_nop 0
	v_mul_f32_e32 v39, 0x3f317217, v8
	v_fma_f32 v39, v8, s33, -v39
	v_fmac_f32_e32 v39, 0x3377d1cf, v8
	v_fmac_f32_e32 v39, 0x3f317217, v8
	v_cmp_lt_f32_e64 s[44:45], |v8|, s36
	s_nop 1
	v_cndmask_b32_e64 v8, v8, v39, s[44:45]
	v_cndmask_b32_e32 v39, 0, v216, vcc
	v_sub_f32_e32 v39, v8, v39
	v_pk_add_f32 v[14:15], v[14:15], v[38:39] neg_lo:[0,1] neg_hi:[0,1]
	v_mov_b32_e32 v14, v14
	s_nop 1
	s_nop 0
	s_nop 1
	v_mul_f32_e64 v9, |v10|, s8
	v_exp_f32_e32 v9, v9
	v_max_f32_e32 v8, v10, v10
	v_mov_b32_e32 v15, v15
	v_min_f32_e32 v8, 0, v8
	v_add_f32_e32 v9, 1.0, v9
	v_cmp_gt_f32_e32 vcc, s37, v9
	s_nop 1
	v_cndmask_b32_e64 v40, 0, 32, vcc
	v_ldexp_f32 v9, v9, v40
	v_log_f32_e32 v9, v9
	s_nop 0
	v_mul_f32_e32 v40, 0x3f317217, v9
	v_fma_f32 v40, v9, s33, -v40
	v_fmac_f32_e32 v40, 0x3377d1cf, v9
	v_fmac_f32_e32 v40, 0x3f317217, v9
	v_cmp_lt_f32_e64 s[44:45], |v9|, s36
	s_nop 1
	v_cndmask_b32_e64 v9, v9, v40, s[44:45]
	v_cndmask_b32_e32 v40, 0, v216, vcc
	v_sub_f32_e32 v40, v9, v40
	s_nop 0
	s_nop 0
	s_nop 1
	s_nop 0
	s_nop 1
	v_mul_f32_e64 v10, |v11|, s8
	v_exp_f32_e32 v10, v10
	v_max_f32_e32 v9, v11, v11
	v_min_f32_e32 v9, 0, v9
	v_add_f32_e32 v10, 1.0, v10
	v_cmp_gt_f32_e32 vcc, s37, v10
	s_nop 1
	v_cndmask_b32_e64 v41, 0, 32, vcc
	v_ldexp_f32 v10, v10, v41
	v_log_f32_e32 v10, v10
	s_nop 0
	v_mul_f32_e32 v41, 0x3f317217, v10
	v_fma_f32 v41, v10, s33, -v41
	v_fmac_f32_e32 v41, 0x3377d1cf, v10
	v_fmac_f32_e32 v41, 0x3f317217, v10
	v_cmp_lt_f32_e64 s[44:45], |v10|, s36
	s_nop 1
	v_cndmask_b32_e64 v10, v10, v41, s[44:45]
	v_cndmask_b32_e32 v41, 0, v216, vcc
	v_sub_f32_e32 v41, v10, v41
	v_pk_add_f32 v[8:9], v[8:9], v[40:41] neg_lo:[0,1] neg_hi:[0,1]
	v_mov_b32_e32 v8, v8
	s_nop 1
	s_nop 0
	s_nop 1
	v_mul_f32_e64 v11, |v4|, s8
	v_exp_f32_e32 v11, v11
	v_max_f32_e32 v10, v4, v4
	v_add_f32_e32 v11, 1.0, v11
	v_cmp_gt_f32_e32 vcc, s37, v11
	v_mov_b32_e32 v9, v9
	s_nop 0
	v_cndmask_b32_e64 v42, 0, 32, vcc
	v_ldexp_f32 v11, v11, v42
	v_log_f32_e32 v11, v11
	v_min_f32_e32 v10, 0, v10
	v_mul_f32_e32 v42, 0x3f317217, v11
	v_fma_f32 v42, v11, s33, -v42
	v_fmac_f32_e32 v42, 0x3377d1cf, v11
	v_fmac_f32_e32 v42, 0x3f317217, v11
	v_cmp_lt_f32_e64 s[44:45], |v11|, s36
	s_nop 1
	v_cndmask_b32_e64 v11, v11, v42, s[44:45]
	v_cndmask_b32_e32 v42, 0, v216, vcc
	v_sub_f32_e32 v42, v11, v42
	s_nop 0
	s_nop 1
	s_nop 0
	s_nop 1
	v_max_f32_e32 v4, v5, v5
	v_min_f32_e32 v11, 0, v4
	v_mul_f32_e64 v4, |v5|, s8
	v_exp_f32_e32 v4, v4
	s_nop 0
	v_add_f32_e32 v4, 1.0, v4
	v_cmp_gt_f32_e32 vcc, s37, v4
	s_nop 1
	v_cndmask_b32_e64 v43, 0, 32, vcc
	v_ldexp_f32 v4, v4, v43
	v_log_f32_e32 v4, v4
	s_nop 0
	v_mul_f32_e32 v43, 0x3f317217, v4
	v_fma_f32 v43, v4, s33, -v43
	v_fmac_f32_e32 v43, 0x3377d1cf, v4
	v_fmac_f32_e32 v43, 0x3f317217, v4
	v_cmp_lt_f32_e64 s[44:45], |v4|, s36
	s_nop 1
	v_cndmask_b32_e64 v4, v4, v43, s[44:45]
	v_cndmask_b32_e32 v43, 0, v216, vcc
	v_sub_f32_e32 v43, v4, v43
	v_pk_add_f32 v[10:11], v[10:11], v[42:43] neg_lo:[0,1] neg_hi:[0,1]
	v_mov_b32_e32 v10, v10
	s_nop 1
	v_mov_b32_dpp v42, v10 row_shr:1 row_mask:0xf bank_mask:0xf bound_ctrl:1
	s_nop 0
	s_nop 0
	s_nop 1
	v_mul_f32_e64 v5, |v6|, s8
	v_exp_f32_e32 v5, v5
	v_max_f32_e32 v4, v6, v6
	v_mov_b32_e32 v11, v11
	v_min_f32_e32 v4, 0, v4
	v_add_f32_e32 v5, 1.0, v5
	v_cmp_gt_f32_e32 vcc, s37, v5
	v_mov_b32_dpp v43, v11 row_shr:1 row_mask:0xf bank_mask:0xf bound_ctrl:1
	v_pk_add_f32 v[42:43], v[10:11], v[42:43]
	v_cndmask_b32_e64 v44, 0, 32, vcc
	v_ldexp_f32 v5, v5, v44
	v_log_f32_e32 v5, v5
	s_nop 0
	v_mul_f32_e32 v44, 0x3f317217, v5
	v_fma_f32 v44, v5, s33, -v44
	v_fmac_f32_e32 v44, 0x3377d1cf, v5
	v_fmac_f32_e32 v44, 0x3f317217, v5
	v_cmp_lt_f32_e64 s[44:45], |v5|, s36
	s_nop 1
	v_cndmask_b32_e64 v5, v5, v44, s[44:45]
	v_cndmask_b32_e32 v44, 0, v216, vcc
	v_sub_f32_e32 v44, v5, v44
	s_nop 0
	s_nop 0
	s_nop 1
	s_nop 0
	s_nop 1
	v_mul_f32_e64 v6, |v7|, s8
	v_exp_f32_e32 v6, v6
	v_max_f32_e32 v5, v7, v7
	v_min_f32_e32 v5, 0, v5
	v_add_f32_e32 v6, 1.0, v6
	v_cmp_gt_f32_e32 vcc, s37, v6
	s_nop 1
	v_cndmask_b32_e64 v45, 0, 32, vcc
	v_ldexp_f32 v6, v6, v45
	v_log_f32_e32 v6, v6
	s_nop 0
	v_mul_f32_e32 v45, 0x3f317217, v6
	v_fma_f32 v45, v6, s33, -v45
	v_fmac_f32_e32 v45, 0x3377d1cf, v6
	v_fmac_f32_e32 v45, 0x3f317217, v6
	v_cmp_lt_f32_e64 s[44:45], |v6|, s36
	s_nop 1
	v_cndmask_b32_e64 v6, v6, v45, s[44:45]
	v_cndmask_b32_e32 v45, 0, v216, vcc
	v_sub_f32_e32 v45, v6, v45
	v_pk_add_f32 v[4:5], v[4:5], v[44:45] neg_lo:[0,1] neg_hi:[0,1]
	v_mov_b32_e32 v4, v4
	s_nop 1
	v_mov_b32_dpp v44, v4 row_shr:1 row_mask:0xf bank_mask:0xf bound_ctrl:1
	s_nop 0
	s_nop 0
	s_nop 1
	v_mul_f32_e64 v7, |v0|, s8
	v_exp_f32_e32 v7, v7
	v_max_f32_e32 v6, v0, v0
	v_add_f32_e32 v7, 1.0, v7
	v_cmp_gt_f32_e32 vcc, s37, v7
	v_mov_b32_e32 v5, v5
	s_nop 0
	v_cndmask_b32_e64 v46, 0, 32, vcc
	v_ldexp_f32 v7, v7, v46
; template <int CTRL> __device__ __forceinline__ float dppx(float v) { return __int_as_float(__builtin_amdgcn_update_dpp(0, __float_as_int(v), CTRL, 0xf, 0xf, true)); }
;   __device__ __forceinline__ void operator()(const f32x4 (&acc)[2][2][4][2], const pg8::Unit& u, int wr, int wc, int fr, int fq) const {
;     ...
;               for (int q = 0; q < 4; ++q) { const float gv = log_forget(acc[ai][bj][m][qh][q], lq[q]); g[m][q] = gv;
;                 float sc = gv; sc += dppx<0x111>(sc); sc += dppx<0x112>(sc); sc += dppx<0x114>(sc); sc += dppx<0x118>(sc);
;                 const float tot16 = __int_as_float(__builtin_amdgcn_ds_swizzle(__float_as_int(sc), 0x1F0));
;                 cs[m][q] = sc + carry[q]; carry[q] += tot16; }
; #pragma unroll
;             for (int m = 0; m < 4; ++m) { const int r = row0 + ai * 128 + m * 16; float bq[4], kq[4];
; #pragma unroll
;               for (int q = 0; q < 4; ++q) { bq[q] = bwd ? (carry[q] - cs[m][q]) + g[m][q] : cs[m][q]; kq[q] = 1.f - __expf(g[m][q]); }
	v_log_f32_e32 v7, v7
	v_mov_b32_dpp v45, v5 row_shr:1 row_mask:0xf bank_mask:0xf bound_ctrl:1
	v_pk_add_f32 v[44:45], v[4:5], v[44:45]
	v_min_f32_e32 v6, 0, v6
	v_mul_f32_e32 v46, 0x3f317217, v7
	v_fma_f32 v46, v7, s33, -v46
	v_fmac_f32_e32 v46, 0x3377d1cf, v7
	v_fmac_f32_e32 v46, 0x3f317217, v7
	v_cmp_lt_f32_e64 s[44:45], |v7|, s36
	s_nop 1
	v_cndmask_b32_e64 v7, v7, v46, s[44:45]
	v_cndmask_b32_e32 v46, 0, v216, vcc
	v_sub_f32_e32 v46, v7, v46
	s_nop 0
	s_nop 1
	s_nop 0
	s_nop 1
	v_max_f32_e32 v0, v1, v1
	v_min_f32_e32 v7, 0, v0
	v_mul_f32_e64 v0, |v1|, s8
	v_exp_f32_e32 v0, v0
	s_nop 0
	v_add_f32_e32 v0, 1.0, v0
	v_cmp_gt_f32_e32 vcc, s37, v0
	s_nop 1
	v_cndmask_b32_e64 v47, 0, 32, vcc
	v_ldexp_f32 v0, v0, v47
	v_log_f32_e32 v0, v0
	s_nop 0
	v_mul_f32_e32 v47, 0x3f317217, v0
	v_fma_f32 v47, v0, s33, -v47
	v_fmac_f32_e32 v47, 0x3377d1cf, v0
	v_fmac_f32_e32 v47, 0x3f317217, v0
	v_cmp_lt_f32_e64 s[44:45], |v0|, s36
	s_nop 1
	v_cndmask_b32_e64 v0, v0, v47, s[44:45]
	v_cndmask_b32_e32 v47, 0, v216, vcc
	v_sub_f32_e32 v47, v0, v47
	v_pk_add_f32 v[6:7], v[6:7], v[46:47] neg_lo:[0,1] neg_hi:[0,1]
	v_mov_b32_e32 v6, v6
	s_nop 1
	v_mov_b32_dpp v46, v6 row_shr:1 row_mask:0xf bank_mask:0xf bound_ctrl:1
	s_nop 0
	s_nop 0
	s_nop 1
	v_mul_f32_e64 v1, |v2|, s8
	v_exp_f32_e32 v1, v1
	v_max_f32_e32 v0, v2, v2
	v_mov_b32_e32 v7, v7
	v_min_f32_e32 v0, 0, v0
	v_add_f32_e32 v1, 1.0, v1
	v_cmp_gt_f32_e32 vcc, s37, v1
	v_mov_b32_dpp v47, v7 row_shr:1 row_mask:0xf bank_mask:0xf bound_ctrl:1
	v_pk_add_f32 v[46:47], v[6:7], v[46:47]
	v_cndmask_b32_e64 v48, 0, 32, vcc
	v_ldexp_f32 v1, v1, v48
	v_log_f32_e32 v1, v1
	s_nop 0
	v_mul_f32_e32 v48, 0x3f317217, v1
	v_fma_f32 v48, v1, s33, -v48
	v_fmac_f32_e32 v48, 0x3377d1cf, v1
	v_fmac_f32_e32 v48, 0x3f317217, v1
	v_cmp_lt_f32_e64 s[44:45], |v1|, s36
	s_nop 1
	v_cndmask_b32_e64 v1, v1, v48, s[44:45]
	v_cndmask_b32_e32 v48, 0, v216, vcc
	v_sub_f32_e32 v48, v1, v48
	s_nop 0
	s_nop 0
	s_nop 1
	s_nop 0
	s_nop 1
	v_mul_f32_e64 v2, |v3|, s8
	v_exp_f32_e32 v2, v2
	v_max_f32_e32 v1, v3, v3
	v_min_f32_e32 v1, 0, v1
	v_add_f32_e32 v2, 1.0, v2
	v_cmp_gt_f32_e32 vcc, s37, v2
	s_nop 1
	v_cndmask_b32_e64 v49, 0, 32, vcc
	v_ldexp_f32 v2, v2, v49
	v_log_f32_e32 v2, v2
	s_nop 0
	v_mul_f32_e32 v49, 0x3f317217, v2
	v_fma_f32 v49, v2, s33, -v49
	v_fmac_f32_e32 v49, 0x3377d1cf, v2
	v_fmac_f32_e32 v49, 0x3f317217, v2
	v_cmp_lt_f32_e64 s[44:45], |v2|, s36
	s_nop 1
	v_cndmask_b32_e64 v2, v2, v49, s[44:45]
	v_cndmask_b32_e32 v49, 0, v216, vcc
	v_sub_f32_e32 v49, v2, v49
	v_pk_add_f32 v[0:1], v[0:1], v[48:49] neg_lo:[0,1] neg_hi:[0,1]
	v_mov_b32_e32 v48, v0
	s_nop 1
	v_mov_b32_dpp v0, v48 row_shr:1 row_mask:0xf bank_mask:0xf bound_ctrl:1
	s_nop 0
	s_nop 0
	s_nop 1
	v_pk_add_f32 v[2:3], v[32:33], v[34:35] neg_lo:[0,1] neg_hi:[0,1]
	v_mov_b32_e32 v49, v1
	v_mov_b32_e32 v3, v3
	v_mov_b32_e32 v2, v2
	v_mov_b32_dpp v1, v49 row_shr:1 row_mask:0xf bank_mask:0xf bound_ctrl:1
	v_mov_b32_dpp v33, v3 row_shr:1 row_mask:0xf bank_mask:0xf bound_ctrl:1
	v_mov_b32_dpp v32, v2 row_shr:1 row_mask:0xf bank_mask:0xf bound_ctrl:1
	v_pk_add_f32 v[32:33], v[2:3], v[32:33]
	v_pk_add_f32 v[0:1], v[48:49], v[0:1]
	s_nop 0
	v_mov_b32_dpp v34, v32 row_shr:2 row_mask:0xf bank_mask:0xf bound_ctrl:1
	v_mov_b32_dpp v35, v33 row_shr:2 row_mask:0xf bank_mask:0xf bound_ctrl:1
	v_pk_add_f32 v[32:33], v[32:33], v[34:35]
	s_nop 1
	v_mov_b32_dpp v34, v32 row_shr:4 row_mask:0xf bank_mask:0xf bound_ctrl:1
	v_mov_b32_dpp v35, v33 row_shr:4 row_mask:0xf bank_mask:0xf bound_ctrl:1
	v_pk_add_f32 v[32:33], v[32:33], v[34:35]
	s_nop 1
	v_mov_b32_dpp v34, v32 row_shr:8 row_mask:0xf bank_mask:0xf bound_ctrl:1
	v_mov_b32_dpp v35, v33 row_shr:8 row_mask:0xf bank_mask:0xf bound_ctrl:1
	v_pk_add_f32 v[32:33], v[32:33], v[34:35]
	ds_swizzle_b32 v34, v32 offset:swizzle(BROADCAST,16,15)
	ds_swizzle_b32 v35, v33 offset:swizzle(BROADCAST,16,15)
	v_pk_add_f32 v[32:33], v[32:33], 0 op_sel_hi:[1,0]
	s_waitcnt lgkmcnt(0)
	v_pk_add_f32 v[50:51], v[34:35], 0 op_sel_hi:[1,0]
	v_mul_f32_e32 v34, 0x3fb8aa3b, v2
	v_exp_f32_e32 v34, v34
	v_mov_b32_dpp v35, v13 row_shr:1 row_mask:0xf bank_mask:0xf bound_ctrl:1
	v_sub_f32_e32 v66, 1.0, v34
	v_mul_f32_e32 v34, 0x3fb8aa3b, v3
	v_exp_f32_e32 v34, v34
	s_nop 0
	v_sub_f32_e32 v67, 1.0, v34
	v_mov_b32_dpp v34, v12 row_shr:1 row_mask:0xf bank_mask:0xf bound_ctrl:1
	v_pk_add_f32 v[34:35], v[12:13], v[34:35]
	s_nop 1
	v_mov_b32_dpp v36, v34 row_shr:2 row_mask:0xf bank_mask:0xf bound_ctrl:1
	v_mov_b32_dpp v37, v35 row_shr:2 row_mask:0xf bank_mask:0xf bound_ctrl:1
	v_pk_add_f32 v[34:35], v[34:35], v[36:37]
	s_nop 1
	v_mov_b32_dpp v36, v34 row_shr:4 row_mask:0xf bank_mask:0xf bound_ctrl:1
	v_mov_b32_dpp v37, v35 row_shr:4 row_mask:0xf bank_mask:0xf bound_ctrl:1
	v_pk_add_f32 v[34:35], v[34:35], v[36:37]
	s_nop 1
	v_mov_b32_dpp v36, v34 row_shr:8 row_mask:0xf bank_mask:0xf bound_ctrl:1
	v_mov_b32_dpp v37, v35 row_shr:8 row_mask:0xf bank_mask:0xf bound_ctrl:1
	v_pk_add_f32 v[34:35], v[34:35], v[36:37]
	ds_swizzle_b32 v36, v34 offset:swizzle(BROADCAST,16,15)
	ds_swizzle_b32 v37, v35 offset:swizzle(BROADCAST,16,15)
	v_pk_add_f32 v[34:35], v[34:35], 0 op_sel_hi:[1,0]
	s_waitcnt lgkmcnt(0)
; template <int CTRL> __device__ __forceinline__ float dppx(float v) { return __int_as_float(__builtin_amdgcn_update_dpp(0, __float_as_int(v), CTRL, 0xf, 0xf, true)); }
;   __device__ __forceinline__ void operator()(const f32x4 (&acc)[2][2][4][2], const pg8::Unit& u, int wr, int wc, int fr, int fq) const {
;     ...
;                 float sc = gv; sc += dppx<0x111>(sc); sc += dppx<0x112>(sc); sc += dppx<0x114>(sc); sc += dppx<0x118>(sc);
;                 const float tot16 = __int_as_float(__builtin_amdgcn_ds_swizzle(__float_as_int(sc), 0x1F0));
;                 cs[m][q] = sc + carry[q]; carry[q] += tot16; }
; #pragma unroll
;             for (int m = 0; m < 4; ++m) { const int r = row0 + ai * 128 + m * 16; float bq[4], kq[4];
; #pragma unroll
;               for (int q = 0; q < 4; ++q) { bq[q] = bwd ? (carry[q] - cs[m][q]) + g[m][q] : cs[m][q]; kq[q] = 1.f - __expf(g[m][q]); }
	v_pk_add_f32 v[52:53], v[36:37], 0 op_sel_hi:[1,0]
	v_mul_f32_e32 v36, 0x3fb8aa3b, v12
	v_exp_f32_e32 v36, v36
	v_mov_b32_dpp v37, v15 row_shr:1 row_mask:0xf bank_mask:0xf bound_ctrl:1
	v_sub_f32_e32 v68, 1.0, v36
	v_mul_f32_e32 v36, 0x3fb8aa3b, v13
	v_exp_f32_e32 v36, v36
	s_nop 0
	v_sub_f32_e32 v69, 1.0, v36
	v_mov_b32_dpp v36, v14 row_shr:1 row_mask:0xf bank_mask:0xf bound_ctrl:1
	v_pk_add_f32 v[36:37], v[14:15], v[36:37]
	s_nop 1
	v_mov_b32_dpp v38, v36 row_shr:2 row_mask:0xf bank_mask:0xf bound_ctrl:1
	v_mov_b32_dpp v39, v37 row_shr:2 row_mask:0xf bank_mask:0xf bound_ctrl:1
	v_pk_add_f32 v[36:37], v[36:37], v[38:39]
	s_nop 1
	v_mov_b32_dpp v38, v36 row_shr:4 row_mask:0xf bank_mask:0xf bound_ctrl:1
	v_mov_b32_dpp v39, v37 row_shr:4 row_mask:0xf bank_mask:0xf bound_ctrl:1
	v_pk_add_f32 v[36:37], v[36:37], v[38:39]
	s_nop 1
	v_mov_b32_dpp v38, v36 row_shr:8 row_mask:0xf bank_mask:0xf bound_ctrl:1
	v_mov_b32_dpp v39, v37 row_shr:8 row_mask:0xf bank_mask:0xf bound_ctrl:1
	v_pk_add_f32 v[36:37], v[36:37], v[38:39]
	ds_swizzle_b32 v38, v36 offset:swizzle(BROADCAST,16,15)
	ds_swizzle_b32 v39, v37 offset:swizzle(BROADCAST,16,15)
	v_pk_add_f32 v[36:37], v[50:51], v[36:37]
	s_waitcnt lgkmcnt(0)
	v_pk_add_f32 v[50:51], v[50:51], v[38:39]
	v_mul_f32_e32 v38, 0x3fb8aa3b, v14
	v_exp_f32_e32 v38, v38
	v_mov_b32_dpp v39, v9 row_shr:1 row_mask:0xf bank_mask:0xf bound_ctrl:1
	v_sub_f32_e32 v70, 1.0, v38
	v_mul_f32_e32 v38, 0x3fb8aa3b, v15
	v_exp_f32_e32 v38, v38
	s_nop 0
	v_sub_f32_e32 v71, 1.0, v38
	v_mov_b32_dpp v38, v8 row_shr:1 row_mask:0xf bank_mask:0xf bound_ctrl:1
	v_pk_add_f32 v[38:39], v[8:9], v[38:39]
	s_nop 1
	v_mov_b32_dpp v40, v38 row_shr:2 row_mask:0xf bank_mask:0xf bound_ctrl:1
	v_mov_b32_dpp v41, v39 row_shr:2 row_mask:0xf bank_mask:0xf bound_ctrl:1
	v_pk_add_f32 v[38:39], v[38:39], v[40:41]
	s_nop 1
	v_mov_b32_dpp v40, v38 row_shr:4 row_mask:0xf bank_mask:0xf bound_ctrl:1
	v_mov_b32_dpp v41, v39 row_shr:4 row_mask:0xf bank_mask:0xf bound_ctrl:1
	v_pk_add_f32 v[38:39], v[38:39], v[40:41]
	s_nop 1
	v_mov_b32_dpp v40, v38 row_shr:8 row_mask:0xf bank_mask:0xf bound_ctrl:1
	v_mov_b32_dpp v41, v39 row_shr:8 row_mask:0xf bank_mask:0xf bound_ctrl:1
	v_pk_add_f32 v[38:39], v[38:39], v[40:41]
	ds_swizzle_b32 v40, v38 offset:swizzle(BROADCAST,16,15)
	ds_swizzle_b32 v41, v39 offset:swizzle(BROADCAST,16,15)
	v_pk_add_f32 v[38:39], v[52:53], v[38:39]
	s_waitcnt lgkmcnt(0)
	v_pk_add_f32 v[40:41], v[52:53], v[40:41]
	v_mul_f32_e32 v52, 0x3fb8aa3b, v8
	v_exp_f32_e32 v52, v52
	v_mov_b32_dpp v53, v43 row_shr:2 row_mask:0xf bank_mask:0xf bound_ctrl:1
	v_sub_f32_e32 v56, 1.0, v52
	v_mul_f32_e32 v52, 0x3fb8aa3b, v9
	v_exp_f32_e32 v52, v52
	s_nop 0
	v_sub_f32_e32 v57, 1.0, v52
	v_mov_b32_dpp v52, v42 row_shr:2 row_mask:0xf bank_mask:0xf bound_ctrl:1
	v_pk_add_f32 v[42:43], v[42:43], v[52:53]
	s_nop 1
	v_mov_b32_dpp v52, v42 row_shr:4 row_mask:0xf bank_mask:0xf bound_ctrl:1
	v_mov_b32_dpp v53, v43 row_shr:4 row_mask:0xf bank_mask:0xf bound_ctrl:1
	v_pk_add_f32 v[42:43], v[42:43], v[52:53]
	s_nop 1
	v_mov_b32_dpp v52, v42 row_shr:8 row_mask:0xf bank_mask:0xf bound_ctrl:1
	v_mov_b32_dpp v53, v43 row_shr:8 row_mask:0xf bank_mask:0xf bound_ctrl:1
	v_pk_add_f32 v[42:43], v[42:43], v[52:53]
	ds_swizzle_b32 v52, v42 offset:swizzle(BROADCAST,16,15)
	ds_swizzle_b32 v53, v43 offset:swizzle(BROADCAST,16,15)
	v_pk_add_f32 v[42:43], v[50:51], v[42:43]
	s_waitcnt lgkmcnt(0)
	v_pk_add_f32 v[50:51], v[50:51], v[52:53]
	v_mul_f32_e32 v52, 0x3fb8aa3b, v10
	v_exp_f32_e32 v52, v52
	v_mov_b32_dpp v53, v45 row_shr:2 row_mask:0xf bank_mask:0xf bound_ctrl:1
	v_sub_f32_e32 v58, 1.0, v52
	v_mul_f32_e32 v52, 0x3fb8aa3b, v11
	v_exp_f32_e32 v52, v52
	s_nop 0
	v_sub_f32_e32 v59, 1.0, v52
	v_mov_b32_dpp v52, v44 row_shr:2 row_mask:0xf bank_mask:0xf bound_ctrl:1
	v_pk_add_f32 v[44:45], v[44:45], v[52:53]
	s_nop 1
	v_mov_b32_dpp v52, v44 row_shr:4 row_mask:0xf bank_mask:0xf bound_ctrl:1
	v_mov_b32_dpp v53, v45 row_shr:4 row_mask:0xf bank_mask:0xf bound_ctrl:1
	v_pk_add_f32 v[44:45], v[44:45], v[52:53]
	s_nop 1
	v_mov_b32_dpp v52, v44 row_shr:8 row_mask:0xf bank_mask:0xf bound_ctrl:1
	v_mov_b32_dpp v53, v45 row_shr:8 row_mask:0xf bank_mask:0xf bound_ctrl:1
	v_pk_add_f32 v[44:45], v[44:45], v[52:53]
	ds_swizzle_b32 v52, v44 offset:swizzle(BROADCAST,16,15)
	ds_swizzle_b32 v53, v45 offset:swizzle(BROADCAST,16,15)
	v_pk_add_f32 v[44:45], v[40:41], v[44:45]
	s_waitcnt lgkmcnt(0)
; __device__ __forceinline__ unsigned cvt_pk_bf16(float lo, float hi) { unsigned r; asm volatile("v_cvt_pk_bf16_f32 %0, %1, %2" : "=v"(r) : "v"(lo), "v"(hi)); return r; }
;   __device__ __forceinline__ void operator()(const f32x4 (&acc)[2][2][4][2], const pg8::Unit& u, int wr, int wc, int fr, int fq) const {
;     ...
;             for (int m = 0; m < 4; ++m) { const int r = row0 + ai * 128 + m * 16; float bq[4], kq[4];
; #pragma unroll
;               for (int q = 0; q < 4; ++q) { bq[q] = bwd ? (carry[q] - cs[m][q]) + g[m][q] : cs[m][q]; kq[q] = 1.f - __expf(g[m][q]); }
;               *(f32x4*)(logfp + (size_t)r * 1024 + c + 4 * qh) = (f32x4){bq[0], bq[1], bq[2], bq[3]};
;               u32x2 w; w.x = pg8::cvt_pk_bf16(kq[0], kq[1]); w.y = pg8::cvt_pk_bf16(kq[2], kq[3]);
;               *(u32x2*)(km + (size_t)r * 1024 + c + 4 * qh) = w; } } }
	v_pk_add_f32 v[40:41], v[40:41], v[52:53]
	v_mul_f32_e32 v52, 0x3fb8aa3b, v4
	v_exp_f32_e32 v52, v52
	v_mov_b32_dpp v53, v47 row_shr:2 row_mask:0xf bank_mask:0xf bound_ctrl:1
	v_sub_f32_e32 v60, 1.0, v52
	v_mul_f32_e32 v52, 0x3fb8aa3b, v5
	v_exp_f32_e32 v52, v52
	s_nop 0
	v_sub_f32_e32 v61, 1.0, v52
	v_mov_b32_dpp v52, v46 row_shr:2 row_mask:0xf bank_mask:0xf bound_ctrl:1
	v_pk_add_f32 v[46:47], v[46:47], v[52:53]
	s_nop 1
	v_mov_b32_dpp v52, v46 row_shr:4 row_mask:0xf bank_mask:0xf bound_ctrl:1
	v_mov_b32_dpp v53, v47 row_shr:4 row_mask:0xf bank_mask:0xf bound_ctrl:1
	v_pk_add_f32 v[46:47], v[46:47], v[52:53]
	s_nop 1
	v_mov_b32_dpp v52, v46 row_shr:8 row_mask:0xf bank_mask:0xf bound_ctrl:1
	v_mov_b32_dpp v53, v47 row_shr:8 row_mask:0xf bank_mask:0xf bound_ctrl:1
	v_pk_add_f32 v[46:47], v[46:47], v[52:53]
	ds_swizzle_b32 v52, v46 offset:swizzle(BROADCAST,16,15)
	ds_swizzle_b32 v53, v47 offset:swizzle(BROADCAST,16,15)
	v_pk_add_f32 v[46:47], v[50:51], v[46:47]
	s_waitcnt lgkmcnt(0)
	v_pk_add_f32 v[50:51], v[50:51], v[52:53]
	v_mul_f32_e32 v52, 0x3fb8aa3b, v6
	v_exp_f32_e32 v52, v52
	v_mov_b32_dpp v53, v1 row_shr:2 row_mask:0xf bank_mask:0xf bound_ctrl:1
	v_sub_f32_e32 v62, 1.0, v52
	v_mul_f32_e32 v52, 0x3fb8aa3b, v7
	v_exp_f32_e32 v52, v52
	s_nop 0
	v_sub_f32_e32 v63, 1.0, v52
	v_mov_b32_dpp v52, v0 row_shr:2 row_mask:0xf bank_mask:0xf bound_ctrl:1
	v_pk_add_f32 v[0:1], v[0:1], v[52:53]
	s_nop 1
	v_mov_b32_dpp v52, v0 row_shr:4 row_mask:0xf bank_mask:0xf bound_ctrl:1
	v_mov_b32_dpp v53, v1 row_shr:4 row_mask:0xf bank_mask:0xf bound_ctrl:1
	v_pk_add_f32 v[0:1], v[0:1], v[52:53]
	s_nop 1
	v_mov_b32_dpp v52, v0 row_shr:8 row_mask:0xf bank_mask:0xf bound_ctrl:1
	v_mov_b32_dpp v53, v1 row_shr:8 row_mask:0xf bank_mask:0xf bound_ctrl:1
	v_pk_add_f32 v[0:1], v[0:1], v[52:53]
	ds_swizzle_b32 v52, v0 offset:swizzle(BROADCAST,16,15)
	ds_swizzle_b32 v53, v1 offset:swizzle(BROADCAST,16,15)
	v_pk_add_f32 v[54:55], v[40:41], v[0:1]
	v_pk_add_f32 v[0:1], v[50:51], v[32:33] neg_lo:[0,1] neg_hi:[0,1]
	s_waitcnt lgkmcnt(0)
	v_pk_add_f32 v[40:41], v[40:41], v[52:53]
	s_nop 0
	v_pk_add_f32 v[52:53], v[40:41], v[34:35] neg_lo:[0,1] neg_hi:[0,1]
	v_pk_add_f32 v[0:1], v[2:3], v[0:1]
	v_pk_add_f32 v[2:3], v[12:13], v[52:53]
	v_cndmask_b32_e64 v1, v33, v1, s[42:43]
	v_cndmask_b32_e64 v3, v35, v3, s[42:43]
	v_cndmask_b32_e64 v2, v34, v2, s[42:43]
	v_cndmask_b32_e64 v0, v32, v0, s[42:43]
	global_store_dwordx4 v[18:19], v[0:3], off offset:16
	s_nop 1
	v_cvt_pk_bf16_f32 v0, v66, v67
	v_cvt_pk_bf16_f32 v1, v68, v69
	global_store_dwordx2 v[16:17], v[0:1], off offset:8
	v_pk_add_f32 v[0:1], v[50:51], v[36:37] neg_lo:[0,1] neg_hi:[0,1]
	v_pk_add_f32 v[2:3], v[40:41], v[38:39] neg_lo:[0,1] neg_hi:[0,1]
	v_pk_add_f32 v[0:1], v[14:15], v[0:1]
	v_pk_add_f32 v[2:3], v[8:9], v[2:3]
	v_cndmask_b32_e64 v1, v37, v1, s[42:43]
	v_cndmask_b32_e64 v3, v39, v3, s[42:43]
	v_cndmask_b32_e64 v2, v38, v2, s[42:43]
	v_cndmask_b32_e64 v0, v36, v0, s[42:43]
	global_store_dwordx4 v[22:23], v[0:3], off offset:16
	s_nop 1
	v_cvt_pk_bf16_f32 v0, v70, v71
	v_cvt_pk_bf16_f32 v1, v56, v57
	global_store_dwordx2 v[20:21], v[0:1], off offset:8
	v_pk_add_f32 v[0:1], v[50:51], v[42:43] neg_lo:[0,1] neg_hi:[0,1]
	v_pk_add_f32 v[2:3], v[40:41], v[44:45] neg_lo:[0,1] neg_hi:[0,1]
	v_pk_add_f32 v[0:1], v[10:11], v[0:1]
	v_pk_add_f32 v[2:3], v[4:5], v[2:3]
	v_cndmask_b32_e64 v1, v43, v1, s[42:43]
	v_cndmask_b32_e64 v3, v45, v3, s[42:43]
	v_cndmask_b32_e64 v2, v44, v2, s[42:43]
	v_cndmask_b32_e64 v0, v42, v0, s[42:43]
	global_store_dwordx4 v[26:27], v[0:3], off offset:16
	v_mul_f32_e32 v5, 0x3fb8aa3b, v49
	v_exp_f32_e32 v5, v5
	v_cvt_pk_bf16_f32 v0, v58, v59
	v_cvt_pk_bf16_f32 v1, v60, v61
	global_store_dwordx2 v[24:25], v[0:1], off offset:8
	v_mul_f32_e32 v0, 0x3fb8aa3b, v48
	v_exp_f32_e32 v0, v0
	v_pk_add_f32 v[2:3], v[40:41], v[54:55] neg_lo:[0,1] neg_hi:[0,1]
	v_sub_f32_e32 v5, 1.0, v5
	v_pk_add_f32 v[2:3], v[48:49], v[2:3]
	v_sub_f32_e32 v4, 1.0, v0
	v_pk_add_f32 v[0:1], v[50:51], v[46:47] neg_lo:[0,1] neg_hi:[0,1]
	v_cndmask_b32_e64 v3, v55, v3, s[42:43]
	v_pk_add_f32 v[0:1], v[6:7], v[0:1]
	v_cndmask_b32_e64 v2, v54, v2, s[42:43]
	v_cndmask_b32_e64 v1, v47, v1, s[42:43]
	v_cndmask_b32_e64 v0, v46, v0, s[42:43]
	global_store_dwordx4 v[28:29], v[0:3], off offset:16
	s_nop 1
	v_cvt_pk_bf16_f32 v0, v62, v63
	v_cvt_pk_bf16_f32 v1, v4, v5
	global_store_dwordx2 v[30:31], v[0:1], off offset:8
	s_and_b64 vcc, exec, s[40:41]
	s_mov_b64 s[6:7], -1
	s_cbranch_vccnz .LBB0_189
	s_branch .LBB0_203
.Lep1_isl_309:
	s_branch .LBB0_309

; __device__ __forceinline__ float log_forget(float z, float lb) {
;   const float r0 = fminf(z, 0.f) - __logf(1.f + __expf(-fabsf(z)));
;   const float r1 = __logf(lb + (1.f - lb) / (1.f + __expf(-z)));
;   return lb <= 0.f ? r0 : r1;
; }
;   __device__ __forceinline__ void operator()(const f32x4 (&acc)[2][2][4][2], const pg8::Unit& u, int wr, int wc, int fr, int fq) const {
;     ...
;     if (colt >= C_HF && colt < C_HI) {
;       const bool bwd = colt >= C_HF + 512;
; #pragma unroll
;       for (int bj = 0; bj < 2; ++bj) { const int c = col0 + bj * 128 - C_HF; const f32x4 l0 = *(const f32x4*)(lb + (c & 511)), l1 = *(const f32x4*)(lb + (c & 511) + 4);
.LBB0_202:
	v_and_b32_e32 v196, 0x178, v154
	v_lshlrev_b32_e32 v196, 2, v196
	global_load_dwordx4 v[180:183], v196, s[66:67]
	global_load_dwordx4 v[184:187], v196, s[66:67] offset:16
	global_load_dwordx4 v[188:191], v196, s[66:67] offset:512
	global_load_dwordx4 v[192:195], v196, s[66:67] offset:528
	s_waitcnt vmcnt(0)
	s_mov_b64 s[44:45], exec
	s_mov_b64 s[46:47], 0
	v_cmp_ge_f32_e64 s[48:49], 0, v180
	s_and_b64 s[44:45], s[44:45], s[48:49]
	s_or_b64 s[46:47], s[46:47], s[48:49]
	v_cmp_ge_f32_e64 s[48:49], 0, v181
	s_and_b64 s[44:45], s[44:45], s[48:49]
	s_or_b64 s[46:47], s[46:47], s[48:49]
	v_cmp_ge_f32_e64 s[48:49], 0, v182
	s_and_b64 s[44:45], s[44:45], s[48:49]
	s_or_b64 s[46:47], s[46:47], s[48:49]
	v_cmp_ge_f32_e64 s[48:49], 0, v183
	s_and_b64 s[44:45], s[44:45], s[48:49]
	s_or_b64 s[46:47], s[46:47], s[48:49]
	v_cmp_ge_f32_e64 s[48:49], 0, v184
	s_and_b64 s[44:45], s[44:45], s[48:49]
	s_or_b64 s[46:47], s[46:47], s[48:49]
	v_cmp_ge_f32_e64 s[48:49], 0, v185
	s_and_b64 s[44:45], s[44:45], s[48:49]
	s_or_b64 s[46:47], s[46:47], s[48:49]
	v_cmp_ge_f32_e64 s[48:49], 0, v186
	s_and_b64 s[44:45], s[44:45], s[48:49]
	s_or_b64 s[46:47], s[46:47], s[48:49]
	v_cmp_ge_f32_e64 s[48:49], 0, v187
	s_and_b64 s[44:45], s[44:45], s[48:49]
	s_or_b64 s[46:47], s[46:47], s[48:49]
	v_cmp_ge_f32_e64 s[48:49], 0, v188
	s_and_b64 s[44:45], s[44:45], s[48:49]
	s_or_b64 s[46:47], s[46:47], s[48:49]
	v_cmp_ge_f32_e64 s[48:49], 0, v189
	s_and_b64 s[44:45], s[44:45], s[48:49]
	s_or_b64 s[46:47], s[46:47], s[48:49]
	v_cmp_ge_f32_e64 s[48:49], 0, v190
	s_and_b64 s[44:45], s[44:45], s[48:49]
	s_or_b64 s[46:47], s[46:47], s[48:49]
	v_cmp_ge_f32_e64 s[48:49], 0, v191
	s_and_b64 s[44:45], s[44:45], s[48:49]
	s_or_b64 s[46:47], s[46:47], s[48:49]
	v_cmp_ge_f32_e64 s[48:49], 0, v192
	s_and_b64 s[44:45], s[44:45], s[48:49]
	s_or_b64 s[46:47], s[46:47], s[48:49]
	v_cmp_ge_f32_e64 s[48:49], 0, v193
	s_and_b64 s[44:45], s[44:45], s[48:49]
	s_or_b64 s[46:47], s[46:47], s[48:49]
	v_cmp_ge_f32_e64 s[48:49], 0, v194
	s_and_b64 s[44:45], s[44:45], s[48:49]
	s_or_b64 s[46:47], s[46:47], s[48:49]
	v_cmp_ge_f32_e64 s[48:49], 0, v195
	s_and_b64 s[44:45], s[44:45], s[48:49]
	s_or_b64 s[46:47], s[46:47], s[48:49]
	s_cmp_eq_u64 s[44:45], exec
	s_cbranch_scc1 .Lep1_A
	s_cmp_eq_u64 s[46:47], 0
	s_cbranch_scc1 .Lep1_B
	s_nop 0
	v_and_b32_e32 v72, 0x178, v154
	v_lshlrev_b32_e32 v155, 2, v72
	global_load_dwordx4 v[72:75], v155, s[66:67] offset:16
	global_load_dwordx4 v[92:95], v155, s[66:67]
	v_max_f32_e32 v157, v134, v134
	v_min_f32_e32 v166, 0, v157
	v_mul_f32_e64 v157, |v134|, s8
	v_exp_f32_e32 v157, v157
	v_mul_f32_e32 v134, 0xbfb8aa3b, v134
	v_exp_f32_e32 v134, v134
	s_cmp_gt_u32 s2, 5
	v_add_f32_e32 v157, 1.0, v157
	v_cmp_gt_f32_e32 vcc, s37, v157
	v_add_f32_e32 v134, 1.0, v134
	v_add_u32_e32 v96, 0xfffffc00, v154
	v_cndmask_b32_e64 v159, 0, 32, vcc
	v_ldexp_f32 v157, v157, v159
	v_log_f32_e32 v157, v157
	s_cselect_b64 s[42:43], -1, 0
	v_mul_f32_e32 v159, 0x3f317217, v157
	v_fma_f32 v159, v157, s33, -v159
	v_fmac_f32_e32 v159, 0x3377d1cf, v157
	v_fmac_f32_e32 v159, 0x3f317217, v157
	v_cmp_lt_f32_e64 s[44:45], |v157|, s36
	s_waitcnt vmcnt(0)
	v_cmp_ge_f32_e64 s[54:55], 0, v73
	v_cndmask_b32_e64 v157, v157, v159, s[44:45]
	v_cndmask_b32_e32 v159, 0, v216, vcc
	v_sub_f32_e32 v174, v157, v159
	v_sub_f32_e32 v157, 1.0, v92
	v_div_scale_f32 v159, s[2:3], v134, v134, v157
	v_rcp_f32_e32 v161, v159
	v_cmp_ge_f32_e64 s[46:47], 0, v93
	v_cmp_ge_f32_e64 s[48:49], 0, v94
	v_cmp_ge_f32_e64 s[50:51], 0, v95
	v_fma_f32 v163, -v159, v161, 1.0
	v_fmac_f32_e32 v161, v163, v161
	v_div_scale_f32 v163, vcc, v157, v134, v157
	v_mul_f32_e32 v165, v163, v161
	v_fma_f32 v167, -v159, v165, v163
	v_fmac_f32_e32 v165, v167, v161
	v_fma_f32 v159, -v159, v165, v163
	v_div_fmas_f32 v159, v159, v161, v165
	v_div_fixup_f32 v134, v159, v134, v157
	v_add_f32_e32 v134, v92, v134
	v_cmp_gt_f32_e32 vcc, s37, v134
	v_cmp_ge_f32_e64 s[56:57], 0, v74
	v_cmp_ge_f32_e64 s[58:59], 0, v75
	v_cndmask_b32_e64 v159, 0, 32, vcc
	v_ldexp_f32 v134, v134, v159
	v_log_f32_e32 v134, v134
	s_nop 0
	v_mul_f32_e32 v159, 0x3f317217, v134
	v_fma_f32 v159, v134, s33, -v159
	v_fmac_f32_e32 v159, 0x3377d1cf, v134
	v_fmac_f32_e32 v159, 0x3f317217, v134
	v_cmp_lt_f32_e64 s[44:45], |v134|, s36
	s_nop 1
	v_cndmask_b32_e64 v134, v134, v159, s[44:45]
	v_cndmask_b32_e32 v159, 0, v216, vcc
	v_sub_f32_e32 v165, v134, v159
	v_max_f32_e32 v134, v135, v135
	v_min_f32_e32 v167, 0, v134
	v_mul_f32_e64 v134, |v135|, s8
	v_exp_f32_e32 v134, v134
	s_nop 0
	v_add_f32_e32 v134, 1.0, v134
	v_cmp_gt_f32_e32 vcc, s37, v134
	s_nop 1
	v_cndmask_b32_e64 v159, 0, 32, vcc
	v_ldexp_f32 v134, v134, v159
	v_log_f32_e32 v134, v134
	s_nop 0
	v_mul_f32_e32 v159, 0x3f317217, v134
	v_fma_f32 v159, v134, s33, -v159
	v_fmac_f32_e32 v159, 0x3377d1cf, v134
	v_fmac_f32_e32 v159, 0x3f317217, v134
	v_cmp_lt_f32_e64 s[44:45], |v134|, s36
	s_nop 1
	v_cndmask_b32_e64 v134, v134, v159, s[44:45]
	v_cndmask_b32_e32 v159, 0, v216, vcc
	v_sub_f32_e32 v175, v134, v159
	v_mul_f32_e32 v134, 0xbfb8aa3b, v135
	v_exp_f32_e32 v134, v134
	v_sub_f32_e32 v159, 1.0, v93
	v_add_f32_e32 v134, 1.0, v134
	v_div_scale_f32 v135, s[2:3], v134, v134, v159
	v_rcp_f32_e32 v161, v135
	s_nop 0
	v_fma_f32 v163, -v135, v161, 1.0
	v_fmac_f32_e32 v161, v163, v161
	v_div_scale_f32 v163, vcc, v159, v134, v159
	v_mul_f32_e32 v169, v163, v161
	v_fma_f32 v171, -v135, v169, v163
	v_fmac_f32_e32 v169, v171, v161
	v_fma_f32 v135, -v135, v169, v163
	v_div_fmas_f32 v135, v135, v161, v169
	v_div_fixup_f32 v134, v135, v134, v159
	v_add_f32_e32 v134, v93, v134
	v_cmp_gt_f32_e32 vcc, s37, v134
	s_nop 1
	v_cndmask_b32_e64 v135, 0, 32, vcc
; __device__ __forceinline__ float log_forget(float z, float lb) {
;   const float r0 = fminf(z, 0.f) - __logf(1.f + __expf(-fabsf(z)));
;   const float r1 = __logf(lb + (1.f - lb) / (1.f + __expf(-z)));
;   return lb <= 0.f ? r0 : r1;
; }
	v_ldexp_f32 v134, v134, v135
	v_log_f32_e32 v134, v134
	s_nop 0
	v_mul_f32_e32 v135, 0x3f317217, v134
	v_fma_f32 v135, v134, s33, -v135
	v_fmac_f32_e32 v135, 0x3377d1cf, v134
	v_fmac_f32_e32 v135, 0x3f317217, v134
	v_cmp_lt_f32_e64 s[44:45], |v134|, s36
	s_nop 1
	v_cndmask_b32_e64 v134, v134, v135, s[44:45]
	v_cndmask_b32_e32 v135, 0, v216, vcc
	v_sub_f32_e32 v169, v134, v135
	v_mul_f32_e64 v135, |v136|, s8
	v_exp_f32_e32 v135, v135
	v_max_f32_e32 v134, v136, v136
	v_min_f32_e32 v134, 0, v134
	v_add_f32_e32 v135, 1.0, v135
	v_cmp_gt_f32_e32 vcc, s37, v135
	s_nop 1
	v_cndmask_b32_e64 v161, 0, 32, vcc
	v_ldexp_f32 v135, v135, v161
	v_log_f32_e32 v135, v135
	s_nop 0
	v_mul_f32_e32 v161, 0x3f317217, v135
	v_fma_f32 v161, v135, s33, -v161
	v_fmac_f32_e32 v161, 0x3377d1cf, v135
	v_fmac_f32_e32 v161, 0x3f317217, v135
	v_cmp_lt_f32_e64 s[44:45], |v135|, s36
	s_nop 1
	v_cndmask_b32_e64 v135, v135, v161, s[44:45]
	v_cndmask_b32_e32 v161, 0, v216, vcc
	v_sub_f32_e32 v176, v135, v161
	v_mul_f32_e32 v135, 0xbfb8aa3b, v136
	v_exp_f32_e32 v135, v135
	v_sub_f32_e32 v161, 1.0, v94
	v_add_f32_e32 v135, 1.0, v135
	v_div_scale_f32 v136, s[2:3], v135, v135, v161
	v_rcp_f32_e32 v163, v136
	s_nop 0
	v_fma_f32 v171, -v136, v163, 1.0
	v_fmac_f32_e32 v163, v171, v163
	v_div_scale_f32 v171, vcc, v161, v135, v161
	v_mul_f32_e32 v173, v171, v163
	v_fma_f32 v177, -v136, v173, v171
	v_fmac_f32_e32 v173, v177, v163
	v_fma_f32 v136, -v136, v173, v171
	v_div_fmas_f32 v136, v136, v163, v173
	v_div_fixup_f32 v135, v136, v135, v161
	v_add_f32_e32 v135, v94, v135
	v_cmp_gt_f32_e32 vcc, s37, v135
	s_nop 1
	v_cndmask_b32_e64 v136, 0, 32, vcc
	v_ldexp_f32 v135, v135, v136
	v_log_f32_e32 v135, v135
	s_nop 0
	v_mul_f32_e32 v136, 0x3f317217, v135
	v_fma_f32 v136, v135, s33, -v136
	v_fmac_f32_e32 v136, 0x3377d1cf, v135
	v_fmac_f32_e32 v136, 0x3f317217, v135
	v_cmp_lt_f32_e64 s[44:45], |v135|, s36
	s_nop 1
	v_cndmask_b32_e64 v135, v135, v136, s[44:45]
	v_cndmask_b32_e32 v136, 0, v216, vcc
	v_sub_f32_e32 v171, v135, v136
	v_mul_f32_e64 v136, |v137|, s8
	v_exp_f32_e32 v136, v136
	v_max_f32_e32 v135, v137, v137
	v_min_f32_e32 v135, 0, v135
	v_add_f32_e32 v136, 1.0, v136
	v_cmp_gt_f32_e32 vcc, s37, v136
	s_nop 1
	v_cndmask_b32_e64 v163, 0, 32, vcc
	v_ldexp_f32 v136, v136, v163
	v_log_f32_e32 v136, v136
	s_nop 0
	v_mul_f32_e32 v163, 0x3f317217, v136
	v_fma_f32 v163, v136, s33, -v163
	v_fmac_f32_e32 v163, 0x3377d1cf, v136
	v_fmac_f32_e32 v163, 0x3f317217, v136
	v_cmp_lt_f32_e64 s[44:45], |v136|, s36
	s_nop 1
	v_cndmask_b32_e64 v136, v136, v163, s[44:45]
	v_cndmask_b32_e32 v163, 0, v216, vcc
	v_sub_f32_e32 v177, v136, v163
	v_mul_f32_e32 v136, 0xbfb8aa3b, v137
	v_exp_f32_e32 v136, v136
	v_sub_f32_e32 v163, 1.0, v95
	v_add_f32_e32 v136, 1.0, v136
	v_div_scale_f32 v137, s[2:3], v136, v136, v163
	v_rcp_f32_e32 v173, v137
	s_nop 0
	v_fma_f32 v180, -v137, v173, 1.0
	v_fmac_f32_e32 v173, v180, v173
	v_div_scale_f32 v180, vcc, v163, v136, v163
	v_mul_f32_e32 v181, v180, v173
	v_fma_f32 v182, -v137, v181, v180
	v_fmac_f32_e32 v181, v182, v173
	v_fma_f32 v137, -v137, v181, v180
	v_div_fmas_f32 v137, v137, v173, v181
	v_div_fixup_f32 v136, v137, v136, v163
	v_add_f32_e32 v136, v95, v136
	v_cmp_gt_f32_e32 vcc, s37, v136
	s_nop 1
	v_cndmask_b32_e64 v137, 0, 32, vcc
	v_ldexp_f32 v136, v136, v137
	v_log_f32_e32 v136, v136
	s_nop 0
	v_mul_f32_e32 v137, 0x3f317217, v136
	v_fma_f32 v137, v136, s33, -v137
	v_fmac_f32_e32 v137, 0x3377d1cf, v136
	v_fmac_f32_e32 v137, 0x3f317217, v136
	v_cmp_lt_f32_e64 s[44:45], |v136|, s36
	s_nop 1
	v_cndmask_b32_e64 v136, v136, v137, s[44:45]
	v_cndmask_b32_e32 v137, 0, v216, vcc
	v_sub_f32_e32 v173, v136, v137
	v_mul_f32_e64 v137, |v130|, s8
	v_exp_f32_e32 v137, v137
	v_max_f32_e32 v136, v130, v130
	v_mul_f32_e32 v130, 0xbfb8aa3b, v130
	v_exp_f32_e32 v130, v130
	v_add_f32_e32 v137, 1.0, v137
	v_cmp_gt_f32_e32 vcc, s37, v137
	v_min_f32_e32 v136, 0, v136
	v_add_f32_e32 v130, 1.0, v130
	v_cndmask_b32_e64 v180, 0, 32, vcc
	v_ldexp_f32 v137, v137, v180
	v_log_f32_e32 v137, v137
	s_nop 0
	v_mul_f32_e32 v180, 0x3f317217, v137
	v_fma_f32 v180, v137, s33, -v180
	v_fmac_f32_e32 v180, 0x3377d1cf, v137
	v_fmac_f32_e32 v180, 0x3f317217, v137
	v_cmp_lt_f32_e64 s[44:45], |v137|, s36
	s_nop 1
	v_cndmask_b32_e64 v137, v137, v180, s[44:45]
	v_cndmask_b32_e32 v180, 0, v216, vcc
	v_sub_f32_e32 v180, v137, v180
	v_div_scale_f32 v137, s[2:3], v130, v130, v157
	v_rcp_f32_e32 v181, v137
	s_nop 0
	v_fma_f32 v182, -v137, v181, 1.0
	v_fmac_f32_e32 v181, v182, v181
	v_div_scale_f32 v182, vcc, v157, v130, v157
	v_mul_f32_e32 v183, v182, v181
	v_fma_f32 v184, -v137, v183, v182
	v_fmac_f32_e32 v183, v184, v181
	v_fma_f32 v137, -v137, v183, v182
	v_div_fmas_f32 v137, v137, v181, v183
	v_div_fixup_f32 v130, v137, v130, v157
	v_add_f32_e32 v130, v92, v130
	v_cmp_gt_f32_e32 vcc, s37, v130
	s_nop 1
	v_cndmask_b32_e64 v137, 0, 32, vcc
	v_ldexp_f32 v130, v130, v137
	v_log_f32_e32 v130, v130
	s_nop 0
	v_mul_f32_e32 v137, 0x3f317217, v130
	v_fma_f32 v137, v130, s33, -v137
	v_fmac_f32_e32 v137, 0x3377d1cf, v130
	v_fmac_f32_e32 v137, 0x3f317217, v130
	v_cmp_lt_f32_e64 s[44:45], |v130|, s36
	s_nop 1
	v_cndmask_b32_e64 v130, v130, v137, s[44:45]
	v_cndmask_b32_e32 v137, 0, v216, vcc
	v_sub_f32_e32 v204, v130, v137
	v_max_f32_e32 v130, v131, v131
	v_min_f32_e32 v137, 0, v130
	v_mul_f32_e64 v130, |v131|, s8
	v_exp_f32_e32 v130, v130
	s_nop 0
	v_add_f32_e32 v130, 1.0, v130
	v_cmp_gt_f32_e32 vcc, s37, v130
	s_nop 1
	v_cndmask_b32_e64 v181, 0, 32, vcc
	v_ldexp_f32 v130, v130, v181
	v_log_f32_e32 v130, v130
	s_nop 0
	v_mul_f32_e32 v181, 0x3f317217, v130
	v_fma_f32 v181, v130, s33, -v181
	v_fmac_f32_e32 v181, 0x3377d1cf, v130
; template <int CTRL> __device__ __forceinline__ float dppx(float v) { return __int_as_float(__builtin_amdgcn_update_dpp(0, __float_as_int(v), CTRL, 0xf, 0xf, true)); }
; __device__ __forceinline__ float log_forget(float z, float lb) {
;   const float r0 = fminf(z, 0.f) - __logf(1.f + __expf(-fabsf(z)));
;   const float r1 = __logf(lb + (1.f - lb) / (1.f + __expf(-z)));
;   return lb <= 0.f ? r0 : r1;
; }
;   __device__ __forceinline__ void operator()(const f32x4 (&acc)[2][2][4][2], const pg8::Unit& u, int wr, int wc, int fr, int fq) const {
;     ...
;               for (int q = 0; q < 4; ++q) { const float gv = log_forget(acc[ai][bj][m][qh][q], lq[q]); g[m][q] = gv;
;                 float sc = gv; sc += dppx<0x111>(sc); sc += dppx<0x112>(sc); sc += dppx<0x114>(sc); sc += dppx<0x118>(sc);
	v_fmac_f32_e32 v181, 0x3f317217, v130
	v_cmp_lt_f32_e64 s[44:45], |v130|, s36
	s_nop 1
	v_cndmask_b32_e64 v130, v130, v181, s[44:45]
	v_cndmask_b32_e32 v181, 0, v216, vcc
	v_sub_f32_e32 v181, v130, v181
	v_mul_f32_e32 v130, 0xbfb8aa3b, v131
	v_exp_f32_e32 v130, v130
	v_pk_add_f32 v[136:137], v[136:137], v[180:181] neg_lo:[0,1] neg_hi:[0,1]
	v_add_f32_e32 v130, 1.0, v130
	v_div_scale_f32 v131, s[2:3], v130, v130, v159
	v_rcp_f32_e32 v182, v131
	s_nop 0
	v_fma_f32 v183, -v131, v182, 1.0
	v_fmac_f32_e32 v182, v183, v182
	v_div_scale_f32 v183, vcc, v159, v130, v159
	v_mul_f32_e32 v184, v183, v182
	v_fma_f32 v185, -v131, v184, v183
	v_fmac_f32_e32 v184, v185, v182
	v_fma_f32 v131, -v131, v184, v183
	v_div_fmas_f32 v131, v131, v182, v184
	v_div_fixup_f32 v130, v131, v130, v159
	v_add_f32_e32 v130, v93, v130
	v_cmp_gt_f32_e32 vcc, s37, v130
	s_nop 1
	v_cndmask_b32_e64 v131, 0, 32, vcc
	v_ldexp_f32 v130, v130, v131
	v_log_f32_e32 v130, v130
	s_nop 0
	v_mul_f32_e32 v131, 0x3f317217, v130
	v_fma_f32 v131, v130, s33, -v131
	v_fmac_f32_e32 v131, 0x3377d1cf, v130
	v_fmac_f32_e32 v131, 0x3f317217, v130
	v_cmp_lt_f32_e64 s[44:45], |v130|, s36
	s_nop 1
	v_cndmask_b32_e64 v130, v130, v131, s[44:45]
	v_cndmask_b32_e32 v131, 0, v216, vcc
	v_sub_f32_e32 v205, v130, v131
	v_mul_f32_e64 v131, |v132|, s8
	v_exp_f32_e32 v131, v131
	v_max_f32_e32 v130, v132, v132
	v_cndmask_b32_e64 v137, v205, v137, s[46:47]
	v_min_f32_e32 v130, 0, v130
	v_add_f32_e32 v131, 1.0, v131
	v_cmp_gt_f32_e32 vcc, s37, v131
	v_mov_b32_dpp v181, v137 row_shr:1 row_mask:0xf bank_mask:0xf bound_ctrl:1
	s_nop 0
	v_cndmask_b32_e64 v182, 0, 32, vcc
	v_ldexp_f32 v131, v131, v182
	v_log_f32_e32 v131, v131
	s_nop 0
	v_mul_f32_e32 v182, 0x3f317217, v131
	v_fma_f32 v182, v131, s33, -v182
	v_fmac_f32_e32 v182, 0x3377d1cf, v131
	v_fmac_f32_e32 v182, 0x3f317217, v131
	v_cmp_lt_f32_e64 s[44:45], |v131|, s36
	s_nop 1
	v_cndmask_b32_e64 v131, v131, v182, s[44:45]
	v_cndmask_b32_e32 v182, 0, v216, vcc
	v_sub_f32_e32 v182, v131, v182
	v_mul_f32_e32 v131, 0xbfb8aa3b, v132
	v_exp_f32_e32 v131, v131
	s_nop 0
	v_add_f32_e32 v131, 1.0, v131
	v_div_scale_f32 v132, s[2:3], v131, v131, v161
	v_rcp_f32_e32 v183, v132
	s_nop 0
	v_fma_f32 v184, -v132, v183, 1.0
	v_fmac_f32_e32 v183, v184, v183
	v_div_scale_f32 v184, vcc, v161, v131, v161
	v_mul_f32_e32 v185, v184, v183
	v_fma_f32 v186, -v132, v185, v184
	v_fmac_f32_e32 v185, v186, v183
	v_fma_f32 v132, -v132, v185, v184
	v_div_fmas_f32 v132, v132, v183, v185
	v_div_fixup_f32 v131, v132, v131, v161
	v_add_f32_e32 v131, v94, v131
	v_cmp_gt_f32_e32 vcc, s37, v131
	s_nop 1
	v_cndmask_b32_e64 v132, 0, 32, vcc
	v_ldexp_f32 v131, v131, v132
	v_log_f32_e32 v131, v131
	s_nop 0
	v_mul_f32_e32 v132, 0x3f317217, v131
	v_fma_f32 v132, v131, s33, -v132
	v_fmac_f32_e32 v132, 0x3377d1cf, v131
	v_fmac_f32_e32 v132, 0x3f317217, v131
	v_cmp_lt_f32_e64 s[44:45], |v131|, s36
	s_nop 1
	v_cndmask_b32_e64 v131, v131, v132, s[44:45]
	v_cndmask_b32_e32 v132, 0, v216, vcc
	v_sub_f32_e32 v206, v131, v132
	v_mul_f32_e64 v132, |v133|, s8
	v_exp_f32_e32 v132, v132
	v_max_f32_e32 v131, v133, v133
	v_min_f32_e32 v131, 0, v131
	v_add_f32_e32 v132, 1.0, v132
	v_cmp_gt_f32_e32 vcc, s37, v132
	s_nop 1
	v_cndmask_b32_e64 v183, 0, 32, vcc
	v_ldexp_f32 v132, v132, v183
	v_log_f32_e32 v132, v132
	s_nop 0
	v_mul_f32_e32 v183, 0x3f317217, v132
	v_fma_f32 v183, v132, s33, -v183
	v_fmac_f32_e32 v183, 0x3377d1cf, v132
	v_fmac_f32_e32 v183, 0x3f317217, v132
	v_cmp_lt_f32_e64 s[44:45], |v132|, s36
	s_nop 1
	v_cndmask_b32_e64 v132, v132, v183, s[44:45]
	v_cndmask_b32_e32 v183, 0, v216, vcc
	v_sub_f32_e32 v183, v132, v183
	v_mul_f32_e32 v132, 0xbfb8aa3b, v133
	v_exp_f32_e32 v132, v132
	s_nop 0
	v_add_f32_e32 v132, 1.0, v132
	v_div_scale_f32 v133, s[2:3], v132, v132, v163
	v_rcp_f32_e32 v184, v133
	s_nop 0
	v_fma_f32 v185, -v133, v184, 1.0
	v_fmac_f32_e32 v184, v185, v184
	v_div_scale_f32 v185, vcc, v163, v132, v163
	v_mul_f32_e32 v186, v185, v184
	v_fma_f32 v187, -v133, v186, v185
	v_fmac_f32_e32 v186, v187, v184
	v_fma_f32 v133, -v133, v186, v185
	v_div_fmas_f32 v133, v133, v184, v186
	v_div_fixup_f32 v132, v133, v132, v163
	v_add_f32_e32 v132, v95, v132
	v_cmp_gt_f32_e32 vcc, s37, v132
	s_nop 1
	v_cndmask_b32_e64 v133, 0, 32, vcc
	v_ldexp_f32 v132, v132, v133
	v_log_f32_e32 v132, v132
	s_nop 0
	v_mul_f32_e32 v133, 0x3f317217, v132
	v_fma_f32 v133, v132, s33, -v133
	v_fmac_f32_e32 v133, 0x3377d1cf, v132
	v_fmac_f32_e32 v133, 0x3f317217, v132
	v_cmp_lt_f32_e64 s[44:45], |v132|, s36
	s_nop 1
	v_cndmask_b32_e64 v132, v132, v133, s[44:45]
	v_cndmask_b32_e32 v133, 0, v216, vcc
	v_sub_f32_e32 v207, v132, v133
	v_mul_f32_e64 v133, |v126|, s8
	v_exp_f32_e32 v133, v133
	v_max_f32_e32 v132, v126, v126
	v_mul_f32_e32 v126, 0xbfb8aa3b, v126
	v_exp_f32_e32 v126, v126
	v_add_f32_e32 v133, 1.0, v133
	v_cmp_gt_f32_e32 vcc, s37, v133
	v_min_f32_e32 v132, 0, v132
	v_add_f32_e32 v126, 1.0, v126
	v_cndmask_b32_e64 v184, 0, 32, vcc
	v_ldexp_f32 v133, v133, v184
	v_log_f32_e32 v133, v133
	s_nop 0
	v_mul_f32_e32 v184, 0x3f317217, v133
	v_fma_f32 v184, v133, s33, -v184
	v_fmac_f32_e32 v184, 0x3377d1cf, v133
	v_fmac_f32_e32 v184, 0x3f317217, v133
	v_cmp_lt_f32_e64 s[44:45], |v133|, s36
	s_nop 1
	v_cndmask_b32_e64 v133, v133, v184, s[44:45]
	v_cndmask_b32_e32 v184, 0, v216, vcc
	v_sub_f32_e32 v184, v133, v184
	v_div_scale_f32 v133, s[2:3], v126, v126, v157
	v_rcp_f32_e32 v185, v133
	s_nop 0
	v_fma_f32 v186, -v133, v185, 1.0
	v_fmac_f32_e32 v185, v186, v185
	v_div_scale_f32 v186, vcc, v157, v126, v157
	v_mul_f32_e32 v187, v186, v185
	v_fma_f32 v188, -v133, v187, v186
	v_fmac_f32_e32 v187, v188, v185
	v_fma_f32 v133, -v133, v187, v186
; template <int CTRL> __device__ __forceinline__ float dppx(float v) { return __int_as_float(__builtin_amdgcn_update_dpp(0, __float_as_int(v), CTRL, 0xf, 0xf, true)); }
; __device__ __forceinline__ float log_forget(float z, float lb) {
;   const float r0 = fminf(z, 0.f) - __logf(1.f + __expf(-fabsf(z)));
;   const float r1 = __logf(lb + (1.f - lb) / (1.f + __expf(-z)));
;   return lb <= 0.f ? r0 : r1;
; }
;   __device__ __forceinline__ void operator()(const f32x4 (&acc)[2][2][4][2], const pg8::Unit& u, int wr, int wc, int fr, int fq) const {
;     ...
;               for (int q = 0; q < 4; ++q) { const float gv = log_forget(acc[ai][bj][m][qh][q], lq[q]); g[m][q] = gv;
;                 float sc = gv; sc += dppx<0x111>(sc); sc += dppx<0x112>(sc); sc += dppx<0x114>(sc); sc += dppx<0x118>(sc);
	v_div_fmas_f32 v133, v133, v185, v187
	v_div_fixup_f32 v126, v133, v126, v157
	v_add_f32_e32 v126, v92, v126
	v_cmp_gt_f32_e32 vcc, s37, v126
	s_nop 1
	v_cndmask_b32_e64 v133, 0, 32, vcc
	v_ldexp_f32 v126, v126, v133
	v_log_f32_e32 v126, v126
	s_nop 0
	v_mul_f32_e32 v133, 0x3f317217, v126
	v_fma_f32 v133, v126, s33, -v133
	v_fmac_f32_e32 v133, 0x3377d1cf, v126
	v_fmac_f32_e32 v133, 0x3f317217, v126
	v_cmp_lt_f32_e64 s[44:45], |v126|, s36
	s_nop 1
	v_cndmask_b32_e64 v126, v126, v133, s[44:45]
	v_cndmask_b32_e32 v133, 0, v216, vcc
	v_sub_f32_e32 v210, v126, v133
	v_max_f32_e32 v126, v127, v127
	v_min_f32_e32 v133, 0, v126
	v_mul_f32_e64 v126, |v127|, s8
	v_exp_f32_e32 v126, v126
	s_nop 0
	v_add_f32_e32 v126, 1.0, v126
	v_cmp_gt_f32_e32 vcc, s37, v126
	s_nop 1
	v_cndmask_b32_e64 v185, 0, 32, vcc
	v_ldexp_f32 v126, v126, v185
	v_log_f32_e32 v126, v126
	s_nop 0
	v_mul_f32_e32 v185, 0x3f317217, v126
	v_fma_f32 v185, v126, s33, -v185
	v_fmac_f32_e32 v185, 0x3377d1cf, v126
	v_fmac_f32_e32 v185, 0x3f317217, v126
	v_cmp_lt_f32_e64 s[44:45], |v126|, s36
	s_nop 1
	v_cndmask_b32_e64 v126, v126, v185, s[44:45]
	v_cndmask_b32_e32 v185, 0, v216, vcc
	v_sub_f32_e32 v185, v126, v185
	v_mul_f32_e32 v126, 0xbfb8aa3b, v127
	v_exp_f32_e32 v126, v126
	v_pk_add_f32 v[132:133], v[132:133], v[184:185] neg_lo:[0,1] neg_hi:[0,1]
	v_add_f32_e32 v126, 1.0, v126
	v_div_scale_f32 v127, s[2:3], v126, v126, v159
	v_rcp_f32_e32 v186, v127
	s_nop 0
	v_fma_f32 v187, -v127, v186, 1.0
	v_fmac_f32_e32 v186, v187, v186
	v_div_scale_f32 v187, vcc, v159, v126, v159
	v_mul_f32_e32 v188, v187, v186
	v_fma_f32 v189, -v127, v188, v187
	v_fmac_f32_e32 v188, v189, v186
	v_fma_f32 v127, -v127, v188, v187
	v_div_fmas_f32 v127, v127, v186, v188
	v_div_fixup_f32 v126, v127, v126, v159
	v_add_f32_e32 v126, v93, v126
	v_cmp_gt_f32_e32 vcc, s37, v126
	s_nop 1
	v_cndmask_b32_e64 v127, 0, 32, vcc
	v_ldexp_f32 v126, v126, v127
	v_log_f32_e32 v126, v126
	s_nop 0
	v_mul_f32_e32 v127, 0x3f317217, v126
	v_fma_f32 v127, v126, s33, -v127
	v_fmac_f32_e32 v127, 0x3377d1cf, v126
	v_fmac_f32_e32 v127, 0x3f317217, v126
	v_cmp_lt_f32_e64 s[44:45], |v126|, s36
	s_nop 1
	v_cndmask_b32_e64 v126, v126, v127, s[44:45]
	v_cndmask_b32_e32 v127, 0, v216, vcc
	v_sub_f32_e32 v211, v126, v127
	v_max_f32_e32 v126, v128, v128
	v_min_f32_e32 v186, 0, v126
	v_mul_f32_e64 v126, |v128|, s8
	v_exp_f32_e32 v126, v126
	v_cndmask_b32_e64 v185, v211, v133, s[46:47]
	v_add_f32_e32 v126, 1.0, v126
	v_cmp_gt_f32_e32 vcc, s37, v126
	v_mov_b32_dpp v133, v185 row_shr:1 row_mask:0xf bank_mask:0xf bound_ctrl:1
	s_nop 0
	v_cndmask_b32_e64 v127, 0, 32, vcc
	v_ldexp_f32 v126, v126, v127
	v_log_f32_e32 v126, v126
	s_nop 0
	v_mul_f32_e32 v127, 0x3f317217, v126
	v_fma_f32 v127, v126, s33, -v127
	v_fmac_f32_e32 v127, 0x3377d1cf, v126
	v_fmac_f32_e32 v127, 0x3f317217, v126
	v_cmp_lt_f32_e64 s[44:45], |v126|, s36
	s_nop 1
	v_cndmask_b32_e64 v126, v126, v127, s[44:45]
	v_cndmask_b32_e32 v127, 0, v216, vcc
	v_sub_f32_e32 v188, v126, v127
	v_mul_f32_e32 v126, 0xbfb8aa3b, v128
	v_exp_f32_e32 v126, v126
	s_nop 0
	v_add_f32_e32 v126, 1.0, v126
	v_div_scale_f32 v127, s[2:3], v126, v126, v161
	v_rcp_f32_e32 v128, v127
	s_nop 0
	v_fma_f32 v187, -v127, v128, 1.0
	v_fmac_f32_e32 v128, v187, v128
	v_div_scale_f32 v187, vcc, v161, v126, v161
	v_mul_f32_e32 v189, v187, v128
	v_fma_f32 v190, -v127, v189, v187
	v_fmac_f32_e32 v189, v190, v128
	v_fma_f32 v127, -v127, v189, v187
	v_div_fmas_f32 v127, v127, v128, v189
	v_div_fixup_f32 v126, v127, v126, v161
	v_add_f32_e32 v126, v94, v126
	v_cmp_gt_f32_e32 vcc, s37, v126
	s_nop 1
	v_cndmask_b32_e64 v127, 0, 32, vcc
	v_ldexp_f32 v126, v126, v127
	v_log_f32_e32 v126, v126
	s_nop 0
	v_mul_f32_e32 v127, 0x3f317217, v126
	v_fma_f32 v127, v126, s33, -v127
	v_fmac_f32_e32 v127, 0x3377d1cf, v126
	v_fmac_f32_e32 v127, 0x3f317217, v126
	v_cmp_lt_f32_e64 s[44:45], |v126|, s36
	s_nop 1
	v_cndmask_b32_e64 v126, v126, v127, s[44:45]
	v_cndmask_b32_e32 v127, 0, v216, vcc
	v_sub_f32_e32 v226, v126, v127
	v_max_f32_e32 v126, v129, v129
	v_min_f32_e32 v187, 0, v126
	v_mul_f32_e64 v126, |v129|, s8
	v_exp_f32_e32 v126, v126
	s_nop 0
	v_add_f32_e32 v126, 1.0, v126
	v_cmp_gt_f32_e32 vcc, s37, v126
	s_nop 1
	v_cndmask_b32_e64 v127, 0, 32, vcc
	v_ldexp_f32 v126, v126, v127
	v_log_f32_e32 v126, v126
	s_nop 0
	v_mul_f32_e32 v127, 0x3f317217, v126
	v_fma_f32 v127, v126, s33, -v127
	v_fmac_f32_e32 v127, 0x3377d1cf, v126
	v_fmac_f32_e32 v127, 0x3f317217, v126
	v_cmp_lt_f32_e64 s[44:45], |v126|, s36
	s_nop 1
	v_cndmask_b32_e64 v126, v126, v127, s[44:45]
	v_cndmask_b32_e32 v127, 0, v216, vcc
	v_sub_f32_e32 v189, v126, v127
	v_mul_f32_e32 v126, 0xbfb8aa3b, v129
	v_exp_f32_e32 v126, v126
	s_nop 0
	v_add_f32_e32 v126, 1.0, v126
	v_div_scale_f32 v127, s[2:3], v126, v126, v163
	v_rcp_f32_e32 v128, v127
	s_nop 0
	v_fma_f32 v129, -v127, v128, 1.0
	v_fmac_f32_e32 v128, v129, v128
	v_div_scale_f32 v129, vcc, v163, v126, v163
	v_mul_f32_e32 v190, v129, v128
	v_fma_f32 v191, -v127, v190, v129
	v_fmac_f32_e32 v190, v191, v128
	v_fma_f32 v127, -v127, v190, v129
	v_div_fmas_f32 v127, v127, v128, v190
	v_div_fixup_f32 v126, v127, v126, v163
	v_add_f32_e32 v126, v95, v126
	v_cmp_gt_f32_e32 vcc, s37, v126
	s_nop 1
	v_cndmask_b32_e64 v127, 0, 32, vcc
	v_ldexp_f32 v126, v126, v127
	v_log_f32_e32 v126, v126
	s_nop 0
	v_mul_f32_e32 v127, 0x3f317217, v126
	v_fma_f32 v127, v126, s33, -v127
	v_fmac_f32_e32 v127, 0x3377d1cf, v126
	v_fmac_f32_e32 v127, 0x3f317217, v126
	v_cmp_lt_f32_e64 s[44:45], |v126|, s36
	s_nop 1
	v_cndmask_b32_e64 v126, v126, v127, s[44:45]
	v_cndmask_b32_e32 v127, 0, v216, vcc
	v_sub_f32_e32 v227, v126, v127
	v_max_f32_e32 v126, v122, v122
; __device__ __forceinline__ float log_forget(float z, float lb) {
;   const float r0 = fminf(z, 0.f) - __logf(1.f + __expf(-fabsf(z)));
;   const float r1 = __logf(lb + (1.f - lb) / (1.f + __expf(-z)));
;   return lb <= 0.f ? r0 : r1;
; }
	v_min_f32_e32 v190, 0, v126
	v_mul_f32_e64 v126, |v122|, s8
	v_exp_f32_e32 v126, v126
	v_mul_f32_e32 v122, 0xbfb8aa3b, v122
	v_exp_f32_e32 v122, v122
	v_add_f32_e32 v126, 1.0, v126
	v_cmp_gt_f32_e32 vcc, s37, v126
	v_add_f32_e32 v122, 1.0, v122
	s_nop 0
	v_cndmask_b32_e64 v127, 0, 32, vcc
	v_ldexp_f32 v126, v126, v127
	v_log_f32_e32 v126, v126
	s_nop 0
	v_mul_f32_e32 v127, 0x3f317217, v126
	v_fma_f32 v127, v126, s33, -v127
	v_fmac_f32_e32 v127, 0x3377d1cf, v126
	v_fmac_f32_e32 v127, 0x3f317217, v126
	v_cmp_lt_f32_e64 s[44:45], |v126|, s36
	s_nop 1
	v_cndmask_b32_e64 v126, v126, v127, s[44:45]
	v_cndmask_b32_e32 v127, 0, v216, vcc
	v_sub_f32_e32 v192, v126, v127
	v_div_scale_f32 v126, s[2:3], v122, v122, v157
	v_rcp_f32_e32 v127, v126
	s_nop 0
	v_fma_f32 v128, -v126, v127, 1.0
	v_fmac_f32_e32 v127, v128, v127
	v_div_scale_f32 v128, vcc, v157, v122, v157
	v_mul_f32_e32 v129, v128, v127
	v_fma_f32 v191, -v126, v129, v128
	v_fmac_f32_e32 v129, v191, v127
	v_fma_f32 v126, -v126, v129, v128
	v_div_fmas_f32 v126, v126, v127, v129
	v_div_fixup_f32 v122, v126, v122, v157
	v_add_f32_e32 v122, v92, v122
	v_cmp_gt_f32_e32 vcc, s37, v122
	s_nop 1
	v_cndmask_b32_e64 v126, 0, 32, vcc
	v_ldexp_f32 v122, v122, v126
	v_log_f32_e32 v122, v122
	s_nop 0
	v_mul_f32_e32 v126, 0x3f317217, v122
	v_fma_f32 v126, v122, s33, -v126
	v_fmac_f32_e32 v126, 0x3377d1cf, v122
	v_fmac_f32_e32 v126, 0x3f317217, v122
	v_cmp_lt_f32_e64 s[44:45], |v122|, s36
	s_nop 1
	v_cndmask_b32_e64 v122, v122, v126, s[44:45]
	v_cndmask_b32_e32 v126, 0, v216, vcc
	v_sub_f32_e32 v228, v122, v126
	v_max_f32_e32 v122, v123, v123
	v_min_f32_e32 v191, 0, v122
	v_mul_f32_e64 v122, |v123|, s8
	v_exp_f32_e32 v122, v122
	s_nop 0
	v_add_f32_e32 v122, 1.0, v122
	v_cmp_gt_f32_e32 vcc, s37, v122
	s_nop 1
	v_cndmask_b32_e64 v126, 0, 32, vcc
	v_ldexp_f32 v122, v122, v126
	v_log_f32_e32 v122, v122
	s_nop 0
	v_mul_f32_e32 v126, 0x3f317217, v122
	v_fma_f32 v126, v122, s33, -v126
	v_fmac_f32_e32 v126, 0x3377d1cf, v122
	v_fmac_f32_e32 v126, 0x3f317217, v122
	v_cmp_lt_f32_e64 s[44:45], |v122|, s36
	s_nop 1
	v_cndmask_b32_e64 v122, v122, v126, s[44:45]
	v_cndmask_b32_e32 v126, 0, v216, vcc
	v_sub_f32_e32 v193, v122, v126
	v_mul_f32_e32 v122, 0xbfb8aa3b, v123
	v_exp_f32_e32 v122, v122
	s_nop 0
	v_add_f32_e32 v122, 1.0, v122
	v_div_scale_f32 v123, s[2:3], v122, v122, v159
	v_rcp_f32_e32 v126, v123
	s_nop 0
	v_fma_f32 v127, -v123, v126, 1.0
	v_fmac_f32_e32 v126, v127, v126
	v_div_scale_f32 v127, vcc, v159, v122, v159
	v_mul_f32_e32 v128, v127, v126
	v_fma_f32 v129, -v123, v128, v127
	v_fmac_f32_e32 v128, v129, v126
	v_fma_f32 v123, -v123, v128, v127
	v_div_fmas_f32 v123, v123, v126, v128
	v_div_fixup_f32 v122, v123, v122, v159
	v_add_f32_e32 v122, v93, v122
	v_cmp_gt_f32_e32 vcc, s37, v122
	s_nop 1
	v_cndmask_b32_e64 v123, 0, 32, vcc
	v_ldexp_f32 v122, v122, v123
	v_log_f32_e32 v122, v122
	s_nop 0
	v_mul_f32_e32 v123, 0x3f317217, v122
	v_fma_f32 v123, v122, s33, -v123
	v_fmac_f32_e32 v123, 0x3377d1cf, v122
	v_fmac_f32_e32 v123, 0x3f317217, v122
	v_cmp_lt_f32_e64 s[44:45], |v122|, s36
	s_nop 1
	v_cndmask_b32_e64 v122, v122, v123, s[44:45]
	v_cndmask_b32_e32 v123, 0, v216, vcc
	v_sub_f32_e32 v229, v122, v123
	v_max_f32_e32 v122, v124, v124
	v_min_f32_e32 v194, 0, v122
	v_mul_f32_e64 v122, |v124|, s8
	v_exp_f32_e32 v122, v122
	s_nop 0
	v_add_f32_e32 v122, 1.0, v122
	v_cmp_gt_f32_e32 vcc, s37, v122
	s_nop 1
	v_cndmask_b32_e64 v123, 0, 32, vcc
	v_ldexp_f32 v122, v122, v123
	v_log_f32_e32 v122, v122
	s_nop 0
	v_mul_f32_e32 v123, 0x3f317217, v122
	v_fma_f32 v123, v122, s33, -v123
	v_fmac_f32_e32 v123, 0x3377d1cf, v122
	v_fmac_f32_e32 v123, 0x3f317217, v122
	v_cmp_lt_f32_e64 s[44:45], |v122|, s36
	s_nop 1
	v_cndmask_b32_e64 v122, v122, v123, s[44:45]
	v_cndmask_b32_e32 v123, 0, v216, vcc
	v_sub_f32_e32 v196, v122, v123
	v_mul_f32_e32 v122, 0xbfb8aa3b, v124
	v_exp_f32_e32 v122, v122
	s_nop 0
	v_add_f32_e32 v122, 1.0, v122
	v_div_scale_f32 v123, s[2:3], v122, v122, v161
	v_rcp_f32_e32 v124, v123
	s_nop 0
	v_fma_f32 v126, -v123, v124, 1.0
	v_fmac_f32_e32 v124, v126, v124
	v_div_scale_f32 v126, vcc, v161, v122, v161
	v_mul_f32_e32 v127, v126, v124
	v_fma_f32 v128, -v123, v127, v126
	v_fmac_f32_e32 v127, v128, v124
	v_fma_f32 v123, -v123, v127, v126
	v_div_fmas_f32 v123, v123, v124, v127
	v_div_fixup_f32 v122, v123, v122, v161
	v_add_f32_e32 v122, v94, v122
	v_cmp_gt_f32_e32 vcc, s37, v122
	s_nop 1
	v_cndmask_b32_e64 v123, 0, 32, vcc
	v_ldexp_f32 v122, v122, v123
	v_log_f32_e32 v122, v122
	s_nop 0
	v_mul_f32_e32 v123, 0x3f317217, v122
	v_fma_f32 v123, v122, s33, -v123
	v_fmac_f32_e32 v123, 0x3377d1cf, v122
	v_fmac_f32_e32 v123, 0x3f317217, v122
	v_cmp_lt_f32_e64 s[44:45], |v122|, s36
	s_nop 1
	v_cndmask_b32_e64 v122, v122, v123, s[44:45]
	v_cndmask_b32_e32 v123, 0, v216, vcc
	v_sub_f32_e32 v230, v122, v123
	v_max_f32_e32 v122, v125, v125
	v_min_f32_e32 v195, 0, v122
	v_mul_f32_e64 v122, |v125|, s8
	v_exp_f32_e32 v122, v122
	s_nop 0
	v_add_f32_e32 v122, 1.0, v122
	v_cmp_gt_f32_e32 vcc, s37, v122
	s_nop 1
	v_cndmask_b32_e64 v123, 0, 32, vcc
	v_ldexp_f32 v122, v122, v123
	v_log_f32_e32 v122, v122
	s_nop 0
	v_mul_f32_e32 v123, 0x3f317217, v122
	v_fma_f32 v123, v122, s33, -v123
	v_fmac_f32_e32 v123, 0x3377d1cf, v122
	v_fmac_f32_e32 v123, 0x3f317217, v122
	v_cmp_lt_f32_e64 s[44:45], |v122|, s36
	s_nop 1
	v_cndmask_b32_e64 v122, v122, v123, s[44:45]
	v_cndmask_b32_e32 v123, 0, v216, vcc
	v_sub_f32_e32 v197, v122, v123
	v_mul_f32_e32 v122, 0xbfb8aa3b, v125
	v_exp_f32_e32 v122, v122
	s_nop 0
	v_add_f32_e32 v122, 1.0, v122
	v_div_scale_f32 v123, s[2:3], v122, v122, v163
	v_rcp_f32_e32 v124, v123
	s_nop 0
	v_fma_f32 v125, -v123, v124, 1.0
; template <int CTRL> __device__ __forceinline__ float dppx(float v) { return __int_as_float(__builtin_amdgcn_update_dpp(0, __float_as_int(v), CTRL, 0xf, 0xf, true)); }
; __device__ __forceinline__ float log_forget(float z, float lb) {
;   const float r0 = fminf(z, 0.f) - __logf(1.f + __expf(-fabsf(z)));
;   const float r1 = __logf(lb + (1.f - lb) / (1.f + __expf(-z)));
;   return lb <= 0.f ? r0 : r1;
; }
;   __device__ __forceinline__ void operator()(const f32x4 (&acc)[2][2][4][2], const pg8::Unit& u, int wr, int wc, int fr, int fq) const {
;     ...
;             for (int m = 0; m < 4; ++m)
; #pragma unroll
;               for (int q = 0; q < 4; ++q) { const float gv = log_forget(acc[ai][bj][m][qh][q], lq[q]); g[m][q] = gv;
;                 float sc = gv; sc += dppx<0x111>(sc); sc += dppx<0x112>(sc); sc += dppx<0x114>(sc); sc += dppx<0x118>(sc);
;                 const float tot16 = __int_as_float(__builtin_amdgcn_ds_swizzle(__float_as_int(sc), 0x1F0));
;                 cs[m][q] = sc + carry[q]; carry[q] += tot16; }
; #pragma unroll
;             for (int m = 0; m < 4; ++m) { const int r = row0 + ai * 128 + m * 16; float bq[4], kq[4];
; #pragma unroll
;               for (int q = 0; q < 4; ++q) { bq[q] = bwd ? (carry[q] - cs[m][q]) + g[m][q] : cs[m][q]; kq[q] = 1.f - __expf(g[m][q]); }
	v_fmac_f32_e32 v124, v125, v124
	v_div_scale_f32 v125, vcc, v163, v122, v163
	v_mul_f32_e32 v126, v125, v124
	v_fma_f32 v127, -v123, v126, v125
	v_fmac_f32_e32 v126, v127, v124
	v_fma_f32 v123, -v123, v126, v125
	v_div_fmas_f32 v123, v123, v124, v126
	v_div_fixup_f32 v122, v123, v122, v163
	v_add_f32_e32 v122, v95, v122
	v_cmp_gt_f32_e32 vcc, s37, v122
	s_nop 1
	v_cndmask_b32_e64 v123, 0, 32, vcc
	v_ldexp_f32 v122, v122, v123
	v_log_f32_e32 v122, v122
	s_nop 0
	v_mul_f32_e32 v123, 0x3f317217, v122
	v_fma_f32 v123, v122, s33, -v123
	v_fmac_f32_e32 v123, 0x3377d1cf, v122
	v_fmac_f32_e32 v123, 0x3f317217, v122
	v_cmp_lt_f32_e64 s[44:45], |v122|, s36
	s_nop 1
	v_cndmask_b32_e64 v122, v122, v123, s[44:45]
	v_cndmask_b32_e32 v123, 0, v216, vcc
	v_sub_f32_e32 v231, v122, v123
	v_pk_add_f32 v[122:123], v[166:167], v[174:175] neg_lo:[0,1] neg_hi:[0,1]
	v_cmp_ge_f32_e64 s[44:45], 0, v92
	v_cndmask_b32_e64 v199, v169, v123, s[46:47]
	v_lshlrev_b64 v[166:167], 2, v[96:97]
	v_cndmask_b32_e64 v198, v165, v122, s[44:45]
	v_mov_b32_dpp v123, v199 row_shr:1 row_mask:0xf bank_mask:0xf bound_ctrl:1
	v_cndmask_b32_e64 v136, v204, v136, s[44:45]
	v_mov_b32_dpp v122, v198 row_shr:1 row_mask:0xf bank_mask:0xf bound_ctrl:1
	v_pk_add_f32 v[122:123], v[198:199], v[122:123]
	v_mov_b32_dpp v180, v136 row_shr:1 row_mask:0xf bank_mask:0xf bound_ctrl:1
	v_pk_add_f32 v[180:181], v[136:137], v[180:181]
	v_mov_b32_dpp v124, v122 row_shr:2 row_mask:0xf bank_mask:0xf bound_ctrl:1
	v_mov_b32_dpp v125, v123 row_shr:2 row_mask:0xf bank_mask:0xf bound_ctrl:1
	v_pk_add_f32 v[122:123], v[122:123], v[124:125]
	v_mov_b32_dpp v204, v180 row_shr:2 row_mask:0xf bank_mask:0xf bound_ctrl:1
	v_mov_b32_dpp v205, v181 row_shr:2 row_mask:0xf bank_mask:0xf bound_ctrl:1
	v_mov_b32_dpp v124, v122 row_shr:4 row_mask:0xf bank_mask:0xf bound_ctrl:1
	v_mov_b32_dpp v125, v123 row_shr:4 row_mask:0xf bank_mask:0xf bound_ctrl:1
	v_pk_add_f32 v[180:181], v[180:181], v[204:205]
	v_pk_add_f32 v[122:123], v[122:123], v[124:125]
	v_cndmask_b32_e64 v184, v210, v132, s[44:45]
	v_mov_b32_dpp v204, v180 row_shr:4 row_mask:0xf bank_mask:0xf bound_ctrl:1
	v_mov_b32_dpp v205, v181 row_shr:4 row_mask:0xf bank_mask:0xf bound_ctrl:1
	v_mov_b32_dpp v124, v122 row_shr:8 row_mask:0xf bank_mask:0xf bound_ctrl:1
	v_mov_b32_dpp v125, v123 row_shr:8 row_mask:0xf bank_mask:0xf bound_ctrl:1
	v_pk_add_f32 v[180:181], v[180:181], v[204:205]
	v_pk_add_f32 v[122:123], v[122:123], v[124:125]
	ds_swizzle_b32 v124, v122 offset:swizzle(BROADCAST,16,15)
	v_mov_b32_dpp v204, v180 row_shr:8 row_mask:0xf bank_mask:0xf bound_ctrl:1
	v_mov_b32_dpp v205, v181 row_shr:8 row_mask:0xf bank_mask:0xf bound_ctrl:1
	ds_swizzle_b32 v125, v123 offset:swizzle(BROADCAST,16,15)
	v_pk_add_f32 v[180:181], v[180:181], v[204:205]
	ds_swizzle_b32 v208, v180 offset:swizzle(BROADCAST,16,15)
	ds_swizzle_b32 v209, v181 offset:swizzle(BROADCAST,16,15)
	v_mov_b32_dpp v132, v184 row_shr:1 row_mask:0xf bank_mask:0xf bound_ctrl:1
	s_waitcnt lgkmcnt(2)
	v_pk_add_f32 v[126:127], v[124:125], 0 op_sel_hi:[1,0]
	v_pk_add_f32 v[132:133], v[184:185], v[132:133]
	v_pk_add_f32 v[204:205], v[126:127], v[180:181]
	s_waitcnt lgkmcnt(0)
	v_pk_add_f32 v[212:213], v[126:127], v[208:209]
	v_mul_f32_e32 v126, 0x3fb8aa3b, v137
	v_exp_f32_e32 v126, v126
	v_pk_add_f32 v[200:201], v[122:123], 0 op_sel_hi:[1,0]
	v_mul_f32_e32 v122, 0x3fb8aa3b, v198
	v_exp_f32_e32 v122, v122
	v_sub_f32_e32 v235, 1.0, v126
	v_pk_add_f32 v[126:127], v[130:131], v[182:183] neg_lo:[0,1] neg_hi:[0,1]
	v_mov_b32_dpp v182, v132 row_shr:2 row_mask:0xf bank_mask:0xf bound_ctrl:1
	v_mov_b32_dpp v183, v133 row_shr:2 row_mask:0xf bank_mask:0xf bound_ctrl:1
	v_pk_add_f32 v[132:133], v[132:133], v[182:183]
	v_sub_f32_e32 v169, 1.0, v122
	v_mul_f32_e32 v122, 0x3fb8aa3b, v199
	v_mov_b32_dpp v182, v132 row_shr:4 row_mask:0xf bank_mask:0xf bound_ctrl:1
	v_mov_b32_dpp v183, v133 row_shr:4 row_mask:0xf bank_mask:0xf bound_ctrl:1
	v_pk_add_f32 v[132:133], v[132:133], v[182:183]
	v_exp_f32_e32 v122, v122
	v_cndmask_b32_e64 v207, v207, v127, s[50:51]
	v_mov_b32_dpp v182, v132 row_shr:8 row_mask:0xf bank_mask:0xf bound_ctrl:1
	v_mov_b32_dpp v183, v133 row_shr:8 row_mask:0xf bank_mask:0xf bound_ctrl:1
	v_pk_add_f32 v[132:133], v[132:133], v[182:183]
	ds_swizzle_b32 v182, v132 offset:swizzle(BROADCAST,16,15)
	v_pk_add_f32 v[210:211], v[212:213], v[132:133]
	v_mul_f32_e32 v132, 0x3fb8aa3b, v184
	v_exp_f32_e32 v132, v132
	ds_swizzle_b32 v183, v133 offset:swizzle(BROADCAST,16,15)
	v_sub_f32_e32 v232, 1.0, v122
	v_pk_add_f32 v[122:123], v[134:135], v[176:177] neg_lo:[0,1] neg_hi:[0,1]
	v_sub_f32_e32 v238, 1.0, v132
	v_mul_f32_e32 v132, 0x3fb8aa3b, v185
	v_exp_f32_e32 v132, v132
	s_waitcnt lgkmcnt(0)
; template <int CTRL> __device__ __forceinline__ float dppx(float v) { return __int_as_float(__builtin_amdgcn_update_dpp(0, __float_as_int(v), CTRL, 0xf, 0xf, true)); }
;   __device__ __forceinline__ void operator()(const f32x4 (&acc)[2][2][4][2], const pg8::Unit& u, int wr, int wc, int fr, int fq) const {
;     ...
;             for (int m = 0; m < 4; ++m)
; #pragma unroll
;               for (int q = 0; q < 4; ++q) { const float gv = log_forget(acc[ai][bj][m][qh][q], lq[q]); g[m][q] = gv;
;                 float sc = gv; sc += dppx<0x111>(sc); sc += dppx<0x112>(sc); sc += dppx<0x114>(sc); sc += dppx<0x118>(sc);
;                 const float tot16 = __int_as_float(__builtin_amdgcn_ds_swizzle(__float_as_int(sc), 0x1F0));
;                 cs[m][q] = sc + carry[q]; carry[q] += tot16; }
; #pragma unroll
;             for (int m = 0; m < 4; ++m) { const int r = row0 + ai * 128 + m * 16; float bq[4], kq[4];
; #pragma unroll
;               for (int q = 0; q < 4; ++q) { bq[q] = bwd ? (carry[q] - cs[m][q]) + g[m][q] : cs[m][q]; kq[q] = 1.f - __expf(g[m][q]); }
	v_pk_add_f32 v[212:213], v[212:213], v[182:183]
	v_cndmask_b32_e64 v135, v173, v123, s[50:51]
	v_cndmask_b32_e64 v134, v171, v122, s[48:49]
	v_sub_f32_e32 v239, 1.0, v132
	v_pk_add_f32 v[132:133], v[186:187], v[188:189] neg_lo:[0,1] neg_hi:[0,1]
	v_pk_add_f32 v[188:189], v[190:191], v[192:193] neg_lo:[0,1] neg_hi:[0,1]
	v_mov_b32_dpp v122, v134 row_shr:1 row_mask:0xf bank_mask:0xf bound_ctrl:1
	v_cndmask_b32_e64 v191, v229, v189, s[46:47]
	v_cndmask_b32_e64 v190, v228, v188, s[44:45]
	v_mov_b32_dpp v123, v135 row_shr:1 row_mask:0xf bank_mask:0xf bound_ctrl:1
	v_mov_b32_dpp v189, v191 row_shr:1 row_mask:0xf bank_mask:0xf bound_ctrl:1
	v_mov_b32_dpp v188, v190 row_shr:1 row_mask:0xf bank_mask:0xf bound_ctrl:1
	v_pk_add_f32 v[188:189], v[190:191], v[188:189]
	v_pk_add_f32 v[122:123], v[134:135], v[122:123]
	v_cndmask_b32_e64 v206, v206, v126, s[48:49]
	v_mov_b32_dpp v192, v188 row_shr:2 row_mask:0xf bank_mask:0xf bound_ctrl:1
	v_mov_b32_dpp v193, v189 row_shr:2 row_mask:0xf bank_mask:0xf bound_ctrl:1
	v_pk_add_f32 v[188:189], v[188:189], v[192:193]
	v_mov_b32_dpp v124, v122 row_shr:2 row_mask:0xf bank_mask:0xf bound_ctrl:1
	v_mov_b32_dpp v125, v123 row_shr:2 row_mask:0xf bank_mask:0xf bound_ctrl:1
	v_mov_b32_dpp v192, v188 row_shr:4 row_mask:0xf bank_mask:0xf bound_ctrl:1
	v_mov_b32_dpp v193, v189 row_shr:4 row_mask:0xf bank_mask:0xf bound_ctrl:1
	v_pk_add_f32 v[188:189], v[188:189], v[192:193]
	v_pk_add_f32 v[122:123], v[122:123], v[124:125]
	v_mov_b32_dpp v126, v206 row_shr:1 row_mask:0xf bank_mask:0xf bound_ctrl:1
	v_mov_b32_dpp v192, v188 row_shr:8 row_mask:0xf bank_mask:0xf bound_ctrl:1
	v_mov_b32_dpp v193, v189 row_shr:8 row_mask:0xf bank_mask:0xf bound_ctrl:1
	v_pk_add_f32 v[188:189], v[188:189], v[192:193]
	ds_swizzle_b32 v192, v188 offset:swizzle(BROADCAST,16,15)
	v_pk_add_f32 v[228:229], v[212:213], v[188:189]
	v_mul_f32_e32 v188, 0x3fb8aa3b, v190
	v_exp_f32_e32 v188, v188
	v_mov_b32_dpp v124, v122 row_shr:4 row_mask:0xf bank_mask:0xf bound_ctrl:1
	v_mov_b32_dpp v125, v123 row_shr:4 row_mask:0xf bank_mask:0xf bound_ctrl:1
	v_mov_b32_dpp v127, v207 row_shr:1 row_mask:0xf bank_mask:0xf bound_ctrl:1
	v_sub_f32_e32 v242, 1.0, v188
	v_mul_f32_e32 v188, 0x3fb8aa3b, v191
	v_exp_f32_e32 v188, v188
	v_cndmask_b32_e64 v215, v227, v133, s[50:51]
	v_cndmask_b32_e64 v214, v226, v132, s[48:49]
	ds_swizzle_b32 v193, v189 offset:swizzle(BROADCAST,16,15)
	v_sub_f32_e32 v243, 1.0, v188
	v_pk_add_f32 v[188:189], v[194:195], v[196:197] neg_lo:[0,1] neg_hi:[0,1]
	v_pk_add_f32 v[122:123], v[122:123], v[124:125]
	v_pk_add_f32 v[126:127], v[206:207], v[126:127]
	v_mov_b32_dpp v132, v214 row_shr:1 row_mask:0xf bank_mask:0xf bound_ctrl:1
	v_mov_b32_dpp v133, v215 row_shr:1 row_mask:0xf bank_mask:0xf bound_ctrl:1
	v_cndmask_b32_e64 v195, v231, v189, s[50:51]
	v_cndmask_b32_e64 v194, v230, v188, s[48:49]
	v_mov_b32_dpp v124, v122 row_shr:8 row_mask:0xf bank_mask:0xf bound_ctrl:1
	v_mov_b32_dpp v125, v123 row_shr:8 row_mask:0xf bank_mask:0xf bound_ctrl:1
	v_mov_b32_dpp v130, v126 row_shr:2 row_mask:0xf bank_mask:0xf bound_ctrl:1
	v_mov_b32_dpp v131, v127 row_shr:2 row_mask:0xf bank_mask:0xf bound_ctrl:1
	v_pk_add_f32 v[132:133], v[214:215], v[132:133]
	v_mov_b32_dpp v188, v194 row_shr:1 row_mask:0xf bank_mask:0xf bound_ctrl:1
	v_mov_b32_dpp v189, v195 row_shr:1 row_mask:0xf bank_mask:0xf bound_ctrl:1
	v_pk_add_f32 v[122:123], v[122:123], v[124:125]
	v_pk_add_f32 v[126:127], v[126:127], v[130:131]
	v_mov_b32_dpp v182, v132 row_shr:2 row_mask:0xf bank_mask:0xf bound_ctrl:1
	v_mov_b32_dpp v183, v133 row_shr:2 row_mask:0xf bank_mask:0xf bound_ctrl:1
	v_pk_add_f32 v[188:189], v[194:195], v[188:189]
	ds_swizzle_b32 v124, v122 offset:swizzle(BROADCAST,16,15)
	ds_swizzle_b32 v125, v123 offset:swizzle(BROADCAST,16,15)
	v_mov_b32_dpp v130, v126 row_shr:4 row_mask:0xf bank_mask:0xf bound_ctrl:1
	v_mov_b32_dpp v131, v127 row_shr:4 row_mask:0xf bank_mask:0xf bound_ctrl:1
	v_pk_add_f32 v[132:133], v[132:133], v[182:183]
	v_mov_b32_dpp v196, v188 row_shr:2 row_mask:0xf bank_mask:0xf bound_ctrl:1
	v_mov_b32_dpp v197, v189 row_shr:2 row_mask:0xf bank_mask:0xf bound_ctrl:1
	v_pk_add_f32 v[126:127], v[126:127], v[130:131]
	v_mov_b32_dpp v182, v132 row_shr:4 row_mask:0xf bank_mask:0xf bound_ctrl:1
	v_mov_b32_dpp v183, v133 row_shr:4 row_mask:0xf bank_mask:0xf bound_ctrl:1
	v_pk_add_f32 v[188:189], v[188:189], v[196:197]
	v_pk_add_f32 v[202:203], v[122:123], 0 op_sel_hi:[1,0]
	v_mul_f32_e32 v122, 0x3fb8aa3b, v134
	v_mov_b32_dpp v130, v126 row_shr:8 row_mask:0xf bank_mask:0xf bound_ctrl:1
	v_mov_b32_dpp v131, v127 row_shr:8 row_mask:0xf bank_mask:0xf bound_ctrl:1
	v_pk_add_f32 v[132:133], v[132:133], v[182:183]
	v_mov_b32_dpp v196, v188 row_shr:4 row_mask:0xf bank_mask:0xf bound_ctrl:1
	v_mov_b32_dpp v197, v189 row_shr:4 row_mask:0xf bank_mask:0xf bound_ctrl:1
	v_exp_f32_e32 v122, v122
	v_pk_add_f32 v[126:127], v[126:127], v[130:131]
	v_mov_b32_dpp v182, v132 row_shr:8 row_mask:0xf bank_mask:0xf bound_ctrl:1
	v_mov_b32_dpp v183, v133 row_shr:8 row_mask:0xf bank_mask:0xf bound_ctrl:1
	v_pk_add_f32 v[188:189], v[188:189], v[196:197]
	ds_swizzle_b32 v130, v126 offset:swizzle(BROADCAST,16,15)
	ds_swizzle_b32 v131, v127 offset:swizzle(BROADCAST,16,15)
	v_pk_add_f32 v[132:133], v[132:133], v[182:183]
	v_mov_b32_dpp v196, v188 row_shr:8 row_mask:0xf bank_mask:0xf bound_ctrl:1
	v_mov_b32_dpp v197, v189 row_shr:8 row_mask:0xf bank_mask:0xf bound_ctrl:1
	s_waitcnt lgkmcnt(2)
; template <int CTRL> __device__ __forceinline__ float dppx(float v) { return __int_as_float(__builtin_amdgcn_update_dpp(0, __float_as_int(v), CTRL, 0xf, 0xf, true)); }
; __device__ __forceinline__ unsigned cvt_pk_bf16(float lo, float hi) { unsigned r; asm volatile("v_cvt_pk_bf16_f32 %0, %1, %2" : "=v"(r) : "v"(lo), "v"(hi)); return r; }
;   __device__ __forceinline__ void operator()(const f32x4 (&acc)[2][2][4][2], const pg8::Unit& u, int wr, int wc, int fr, int fq) const {
;     ...
;               for (int q = 0; q < 4; ++q) { const float gv = log_forget(acc[ai][bj][m][qh][q], lq[q]); g[m][q] = gv;
;                 float sc = gv; sc += dppx<0x111>(sc); sc += dppx<0x112>(sc); sc += dppx<0x114>(sc); sc += dppx<0x118>(sc);
;                 const float tot16 = __int_as_float(__builtin_amdgcn_ds_swizzle(__float_as_int(sc), 0x1F0));
;                 cs[m][q] = sc + carry[q]; carry[q] += tot16; }
; #pragma unroll
;             for (int m = 0; m < 4; ++m) { const int r = row0 + ai * 128 + m * 16; float bq[4], kq[4];
; #pragma unroll
;               for (int q = 0; q < 4; ++q) { bq[q] = bwd ? (carry[q] - cs[m][q]) + g[m][q] : cs[m][q]; kq[q] = 1.f - __expf(g[m][q]); }
;               *(f32x4*)(logfp + (size_t)r * 1024 + c + 4 * qh) = (f32x4){bq[0], bq[1], bq[2], bq[3]};
;               u32x2 w; w.x = pg8::cvt_pk_bf16(kq[0], kq[1]); w.y = pg8::cvt_pk_bf16(kq[2], kq[3]);
;               *(u32x2*)(km + (size_t)r * 1024 + c + 4 * qh) = w; } } }
	v_pk_add_f32 v[128:129], v[124:125], 0 op_sel_hi:[1,0]
	ds_swizzle_b32 v182, v132 offset:swizzle(BROADCAST,16,15)
	ds_swizzle_b32 v183, v133 offset:swizzle(BROADCAST,16,15)
	v_pk_add_f32 v[188:189], v[188:189], v[196:197]
	v_pk_add_f32 v[208:209], v[128:129], v[126:127]
	v_mul_f32_e32 v126, 0x3fb8aa3b, v206
	ds_swizzle_b32 v196, v188 offset:swizzle(BROADCAST,16,15)
	ds_swizzle_b32 v197, v189 offset:swizzle(BROADCAST,16,15)
	v_sub_f32_e32 v233, 1.0, v122
	v_mul_f32_e32 v122, 0x3fb8aa3b, v135
	v_exp_f32_e32 v126, v126
	v_exp_f32_e32 v122, v122
	s_waitcnt lgkmcnt(4)
	v_pk_add_f32 v[130:131], v[128:129], v[130:131]
	v_ashrrev_i32_e32 v165, 31, v164
	v_pk_add_f32 v[226:227], v[130:131], v[132:133]
	s_waitcnt lgkmcnt(2)
	v_pk_add_f32 v[186:187], v[130:131], v[182:183]
	v_mul_f32_e32 v130, 0x3fb8aa3b, v214
	v_sub_f32_e32 v236, 1.0, v126
	v_mul_f32_e32 v126, 0x3fb8aa3b, v207
	v_exp_f32_e32 v130, v130
	v_pk_add_f32 v[192:193], v[212:213], v[192:193]
	s_waitcnt lgkmcnt(0)
	v_pk_add_f32 v[196:197], v[186:187], v[196:197]
	v_sub_f32_e32 v234, 1.0, v122
	v_lshlrev_b64 v[122:123], 12, v[164:165]
	v_exp_f32_e32 v126, v126
	v_pk_add_f32 v[212:213], v[186:187], v[188:189]
	v_pk_add_f32 v[186:187], v[192:193], v[200:201] neg_lo:[0,1] neg_hi:[0,1]
	v_pk_add_f32 v[188:189], v[196:197], v[202:203] neg_lo:[0,1] neg_hi:[0,1]
	v_lshl_add_u64 v[122:123], s[22:23], 0, v[122:123]
	v_lshlrev_b64 v[124:125], 11, v[164:165]
	v_pk_add_f32 v[186:187], v[198:199], v[186:187]
	v_pk_add_f32 v[134:135], v[134:135], v[188:189]
	v_lshl_add_u64 v[176:177], v[122:123], 0, v[166:167]
	v_lshl_add_u64 v[124:125], s[0:1], 0, v[124:125]
	v_lshlrev_b64 v[164:165], 1, v[96:97]
	v_mul_f32_e32 v96, 0x3fb8aa3b, v136
	v_cndmask_b32_e64 v189, v203, v135, s[42:43]
	v_cndmask_b32_e64 v188, v202, v134, s[42:43]
	v_cndmask_b32_e64 v187, v201, v187, s[42:43]
	v_cndmask_b32_e64 v186, v200, v186, s[42:43]
	v_lshl_add_u64 v[174:175], v[124:125], 0, v[164:165]
	v_exp_f32_e32 v96, v96
	v_ashrrev_i32_e32 v173, 31, v172
	v_sub_f32_e32 v240, 1.0, v130
	v_mul_f32_e32 v130, 0x3fb8aa3b, v215
	global_store_dwordx4 v[176:177], v[186:189], off
	v_cvt_pk_bf16_f32 v134, v169, v232
	v_cvt_pk_bf16_f32 v135, v233, v234
	v_sub_f32_e32 v237, 1.0, v126
	v_lshlrev_b64 v[126:127], 12, v[172:173]
	v_exp_f32_e32 v130, v130
	global_store_dwordx2 v[174:175], v[134:135], off
	v_pk_add_f32 v[134:135], v[192:193], v[204:205] neg_lo:[0,1] neg_hi:[0,1]
	v_pk_add_f32 v[186:187], v[196:197], v[208:209] neg_lo:[0,1] neg_hi:[0,1]
	v_lshl_add_u64 v[126:127], s[22:23], 0, v[126:127]
	v_lshlrev_b64 v[128:129], 11, v[172:173]
	v_pk_add_f32 v[134:135], v[136:137], v[134:135]
	v_pk_add_f32 v[136:137], v[206:207], v[186:187]
	v_lshl_add_u64 v[180:181], v[126:127], 0, v[166:167]
	v_lshl_add_u64 v[128:129], s[0:1], 0, v[128:129]
	v_cndmask_b32_e64 v137, v209, v137, s[42:43]
	v_cndmask_b32_e64 v136, v208, v136, s[42:43]
	v_cndmask_b32_e64 v135, v205, v135, s[42:43]
	v_cndmask_b32_e64 v134, v204, v134, s[42:43]
	v_sub_f32_e32 v96, 1.0, v96
	v_lshl_add_u64 v[172:173], v[128:129], 0, v[164:165]
	v_ashrrev_i32_e32 v171, 31, v170
	global_store_dwordx4 v[180:181], v[134:137], off
	v_sub_f32_e32 v241, 1.0, v130
	v_lshlrev_b64 v[130:131], 12, v[170:171]
	v_cvt_pk_bf16_f32 v134, v96, v235
	v_cvt_pk_bf16_f32 v135, v236, v237
	global_store_dwordx2 v[172:173], v[134:135], off
	v_pk_add_f32 v[134:135], v[192:193], v[210:211] neg_lo:[0,1] neg_hi:[0,1]
	v_pk_add_f32 v[136:137], v[196:197], v[226:227] neg_lo:[0,1] neg_hi:[0,1]
	v_lshl_add_u64 v[130:131], s[22:23], 0, v[130:131]
	v_lshlrev_b64 v[132:133], 11, v[170:171]
	v_pk_add_f32 v[134:135], v[184:185], v[134:135]
	v_pk_add_f32 v[136:137], v[214:215], v[136:137]
	v_lshl_add_u64 v[182:183], v[130:131], 0, v[166:167]
	v_lshl_add_u64 v[132:133], s[0:1], 0, v[132:133]
	v_cndmask_b32_e64 v137, v227, v137, s[42:43]
	v_cndmask_b32_e64 v136, v226, v136, s[42:43]
	v_cndmask_b32_e64 v135, v211, v135, s[42:43]
	v_cndmask_b32_e64 v134, v210, v134, s[42:43]
	v_lshl_add_u64 v[170:171], v[132:133], 0, v[164:165]
	global_store_dwordx4 v[182:183], v[134:137], off
	v_mul_f32_e32 v96, 0x3fb8aa3b, v194
	v_exp_f32_e32 v96, v96
	v_cvt_pk_bf16_f32 v134, v238, v239
	v_cvt_pk_bf16_f32 v135, v240, v241
	global_store_dwordx2 v[170:171], v[134:135], off
	v_pk_add_f32 v[134:135], v[192:193], v[228:229] neg_lo:[0,1] neg_hi:[0,1]
	v_pk_add_f32 v[136:137], v[196:197], v[212:213] neg_lo:[0,1] neg_hi:[0,1]
	v_pk_add_f32 v[134:135], v[190:191], v[134:135]
	v_pk_add_f32 v[136:137], v[194:195], v[136:137]
	v_cndmask_b32_e64 v186, v228, v134, s[42:43]
	v_mul_f32_e32 v134, 0x3fb8aa3b, v195
	v_exp_f32_e32 v134, v134
	v_ashrrev_i32_e32 v169, 31, v168
	v_cndmask_b32_e64 v188, v212, v136, s[42:43]
	v_cndmask_b32_e64 v187, v229, v135, s[42:43]
	v_sub_f32_e32 v136, 1.0, v134
	v_lshlrev_b64 v[134:135], 12, v[168:169]
	v_lshl_add_u64 v[134:135], s[22:23], 0, v[134:135]
	v_cndmask_b32_e64 v189, v213, v137, s[42:43]
	v_lshl_add_u64 v[184:185], v[134:135], 0, v[166:167]
	v_sub_f32_e32 v96, 1.0, v96
	global_store_dwordx4 v[184:185], v[186:189], off
	v_sub_f32_e32 v206, 1.0, v72
	v_sub_f32_e32 v205, 1.0, v73
	v_cvt_pk_bf16_f32 v186, v242, v243
	v_cvt_pk_bf16_f32 v187, v96, v136
	v_lshlrev_b64 v[136:137], 11, v[168:169]
	v_lshl_add_u64 v[136:137], s[0:1], 0, v[136:137]
	v_lshl_add_u64 v[168:169], v[136:137], 0, v[164:165]
	v_max_f32_e32 v96, v118, v118
	global_store_dwordx2 v[168:169], v[186:187], off
	v_min_f32_e32 v186, 0, v96
	v_mul_f32_e64 v96, |v118|, s8
	v_exp_f32_e32 v96, v96
	v_sub_f32_e32 v204, 1.0, v74
	v_add_f32_e32 v96, 1.0, v96
	v_cmp_gt_f32_e32 vcc, s37, v96
	s_nop 1
	v_cndmask_b32_e64 v187, 0, 32, vcc
	v_ldexp_f32 v96, v96, v187
; __device__ __forceinline__ float log_forget(float z, float lb) {
;   const float r0 = fminf(z, 0.f) - __logf(1.f + __expf(-fabsf(z)));
;   const float r1 = __logf(lb + (1.f - lb) / (1.f + __expf(-z)));
;   return lb <= 0.f ? r0 : r1;
; }
	v_log_f32_e32 v96, v96
	s_nop 0
	v_mul_f32_e32 v187, 0x3f317217, v96
	v_fma_f32 v187, v96, s33, -v187
	v_fmac_f32_e32 v187, 0x3377d1cf, v96
	v_fmac_f32_e32 v187, 0x3f317217, v96
	v_cmp_lt_f32_e64 s[52:53], |v96|, s36
	s_nop 1
	v_cndmask_b32_e64 v96, v96, v187, s[52:53]
	v_cndmask_b32_e32 v187, 0, v216, vcc
	v_sub_f32_e32 v188, v96, v187
	v_mul_f32_e32 v96, 0xbfb8aa3b, v118
	v_exp_f32_e32 v96, v96
	s_nop 0
	v_add_f32_e32 v96, 1.0, v96
	v_div_scale_f32 v118, s[2:3], v96, v96, v206
	v_rcp_f32_e32 v187, v118
	s_nop 0
	v_fma_f32 v189, -v118, v187, 1.0
	v_fmac_f32_e32 v187, v189, v187
	v_div_scale_f32 v189, vcc, v206, v96, v206
	v_mul_f32_e32 v190, v189, v187
	v_fma_f32 v191, -v118, v190, v189
	v_fmac_f32_e32 v190, v191, v187
	v_fma_f32 v118, -v118, v190, v189
	v_div_fmas_f32 v118, v118, v187, v190
	v_div_fixup_f32 v96, v118, v96, v206
	v_add_f32_e32 v96, v72, v96
	v_cmp_gt_f32_e32 vcc, s37, v96
	s_nop 1
	v_cndmask_b32_e64 v118, 0, 32, vcc
	v_ldexp_f32 v96, v96, v118
	v_log_f32_e32 v96, v96
	s_nop 0
	v_mul_f32_e32 v118, 0x3f317217, v96
	v_fma_f32 v118, v96, s33, -v118
	v_fmac_f32_e32 v118, 0x3377d1cf, v96
	v_fmac_f32_e32 v118, 0x3f317217, v96
	v_cmp_lt_f32_e64 s[52:53], |v96|, s36
	s_nop 1
	v_cndmask_b32_e64 v96, v96, v118, s[52:53]
	v_cndmask_b32_e32 v118, 0, v216, vcc
	v_sub_f32_e32 v207, v96, v118
	v_max_f32_e32 v96, v119, v119
	v_min_f32_e32 v187, 0, v96
	v_mul_f32_e64 v96, |v119|, s8
	v_exp_f32_e32 v96, v96
	s_nop 0
	v_add_f32_e32 v96, 1.0, v96
	v_cmp_gt_f32_e32 vcc, s37, v96
	s_nop 1
	v_cndmask_b32_e64 v118, 0, 32, vcc
	v_ldexp_f32 v96, v96, v118
	v_log_f32_e32 v96, v96
	s_nop 0
	v_mul_f32_e32 v118, 0x3f317217, v96
	v_fma_f32 v118, v96, s33, -v118
	v_fmac_f32_e32 v118, 0x3377d1cf, v96
	v_fmac_f32_e32 v118, 0x3f317217, v96
	v_cmp_lt_f32_e64 s[52:53], |v96|, s36
	s_nop 1
	v_cndmask_b32_e64 v96, v96, v118, s[52:53]
	v_cndmask_b32_e32 v118, 0, v216, vcc
	v_sub_f32_e32 v189, v96, v118
	v_mul_f32_e32 v96, 0xbfb8aa3b, v119
	v_exp_f32_e32 v96, v96
	s_nop 0
	v_add_f32_e32 v96, 1.0, v96
	v_div_scale_f32 v118, s[2:3], v96, v96, v205
	v_rcp_f32_e32 v119, v118
	s_nop 0
	v_fma_f32 v190, -v118, v119, 1.0
	v_fmac_f32_e32 v119, v190, v119
	v_div_scale_f32 v190, vcc, v205, v96, v205
	v_mul_f32_e32 v191, v190, v119
	v_fma_f32 v192, -v118, v191, v190
	v_fmac_f32_e32 v191, v192, v119
	v_fma_f32 v118, -v118, v191, v190
	v_div_fmas_f32 v118, v118, v119, v191
	v_div_fixup_f32 v96, v118, v96, v205
	v_add_f32_e32 v96, v73, v96
	v_cmp_gt_f32_e32 vcc, s37, v96
	s_nop 1
	v_cndmask_b32_e64 v118, 0, 32, vcc
	v_ldexp_f32 v96, v96, v118
	v_log_f32_e32 v96, v96
	s_nop 0
	v_mul_f32_e32 v118, 0x3f317217, v96
	v_fma_f32 v118, v96, s33, -v118
	v_fmac_f32_e32 v118, 0x3377d1cf, v96
	v_fmac_f32_e32 v118, 0x3f317217, v96
	v_cmp_lt_f32_e64 s[52:53], |v96|, s36
	s_nop 1
	v_cndmask_b32_e64 v96, v96, v118, s[52:53]
	v_cndmask_b32_e32 v118, 0, v216, vcc
	v_sub_f32_e32 v208, v96, v118
	v_max_f32_e32 v96, v120, v120
	v_min_f32_e32 v118, 0, v96
	v_mul_f32_e64 v96, |v120|, s8
	v_exp_f32_e32 v96, v96
	s_nop 0
	v_add_f32_e32 v96, 1.0, v96
	v_cmp_gt_f32_e32 vcc, s37, v96
	s_nop 1
	v_cndmask_b32_e64 v119, 0, 32, vcc
	v_ldexp_f32 v96, v96, v119
	v_log_f32_e32 v96, v96
	s_nop 0
	v_mul_f32_e32 v119, 0x3f317217, v96
	v_fma_f32 v119, v96, s33, -v119
	v_fmac_f32_e32 v119, 0x3377d1cf, v96
	v_fmac_f32_e32 v119, 0x3f317217, v96
	v_cmp_lt_f32_e64 s[52:53], |v96|, s36
	s_nop 1
	v_cndmask_b32_e64 v96, v96, v119, s[52:53]
	v_cndmask_b32_e32 v119, 0, v216, vcc
	v_sub_f32_e32 v190, v96, v119
	v_mul_f32_e32 v96, 0xbfb8aa3b, v120
	v_exp_f32_e32 v96, v96
	s_nop 0
	v_add_f32_e32 v96, 1.0, v96
	v_div_scale_f32 v119, s[2:3], v96, v96, v204
	v_rcp_f32_e32 v120, v119
	s_nop 0
	v_fma_f32 v191, -v119, v120, 1.0
	v_fmac_f32_e32 v120, v191, v120
	v_div_scale_f32 v191, vcc, v204, v96, v204
	v_mul_f32_e32 v192, v191, v120
	v_fma_f32 v193, -v119, v192, v191
	v_fmac_f32_e32 v192, v193, v120
	v_fma_f32 v119, -v119, v192, v191
	v_div_fmas_f32 v119, v119, v120, v192
	v_div_fixup_f32 v96, v119, v96, v204
	v_add_f32_e32 v96, v74, v96
	v_cmp_gt_f32_e32 vcc, s37, v96
	s_nop 1
	v_cndmask_b32_e64 v119, 0, 32, vcc
	v_ldexp_f32 v96, v96, v119
	v_log_f32_e32 v96, v96
	s_nop 0
	v_mul_f32_e32 v119, 0x3f317217, v96
	v_fma_f32 v119, v96, s33, -v119
	v_fmac_f32_e32 v119, 0x3377d1cf, v96
	v_fmac_f32_e32 v119, 0x3f317217, v96
	v_cmp_lt_f32_e64 s[52:53], |v96|, s36
	s_nop 1
	v_cndmask_b32_e64 v96, v96, v119, s[52:53]
	v_cndmask_b32_e32 v119, 0, v216, vcc
	v_sub_f32_e32 v209, v96, v119
	v_max_f32_e32 v96, v121, v121
	v_min_f32_e32 v119, 0, v96
	v_mul_f32_e64 v96, |v121|, s8
	v_exp_f32_e32 v96, v96
	s_nop 0
	v_add_f32_e32 v96, 1.0, v96
	v_cmp_gt_f32_e32 vcc, s37, v96
	s_nop 1
	v_cndmask_b32_e64 v120, 0, 32, vcc
	v_ldexp_f32 v96, v96, v120
	v_log_f32_e32 v96, v96
	s_nop 0
	v_mul_f32_e32 v120, 0x3f317217, v96
	v_fma_f32 v120, v96, s33, -v120
	v_fmac_f32_e32 v120, 0x3377d1cf, v96
	v_fmac_f32_e32 v120, 0x3f317217, v96
	v_cmp_lt_f32_e64 s[52:53], |v96|, s36
	s_nop 1
	v_cndmask_b32_e64 v96, v96, v120, s[52:53]
	v_cndmask_b32_e32 v120, 0, v216, vcc
	v_sub_f32_e32 v191, v96, v120
	v_mul_f32_e32 v120, 0xbfb8aa3b, v121
	v_exp_f32_e32 v120, v120
	v_sub_f32_e32 v96, 1.0, v75
	v_pk_add_f32 v[118:119], v[118:119], v[190:191] neg_lo:[0,1] neg_hi:[0,1]
	v_add_f32_e32 v120, 1.0, v120
	v_div_scale_f32 v121, s[2:3], v120, v120, v96
	v_rcp_f32_e32 v192, v121
	v_cndmask_b32_e64 v118, v209, v118, s[56:57]
	v_fma_f32 v193, -v121, v192, 1.0
	v_fmac_f32_e32 v192, v193, v192
	v_div_scale_f32 v193, vcc, v96, v120, v96
	v_mul_f32_e32 v194, v193, v192
	v_fma_f32 v195, -v121, v194, v193
	v_fmac_f32_e32 v194, v195, v192
	v_fma_f32 v121, -v121, v194, v193
; __device__ __forceinline__ float log_forget(float z, float lb) {
;   const float r0 = fminf(z, 0.f) - __logf(1.f + __expf(-fabsf(z)));
;   const float r1 = __logf(lb + (1.f - lb) / (1.f + __expf(-z)));
;   return lb <= 0.f ? r0 : r1;
; }
	v_div_fmas_f32 v121, v121, v192, v194
	v_div_fixup_f32 v120, v121, v120, v96
	v_add_f32_e32 v120, v75, v120
	v_cmp_gt_f32_e32 vcc, s37, v120
	s_nop 1
	v_cndmask_b32_e64 v121, 0, 32, vcc
	v_ldexp_f32 v120, v120, v121
	v_log_f32_e32 v120, v120
	s_nop 0
	v_mul_f32_e32 v121, 0x3f317217, v120
	v_fma_f32 v121, v120, s33, -v121
	v_fmac_f32_e32 v121, 0x3377d1cf, v120
	v_fmac_f32_e32 v121, 0x3f317217, v120
	v_cmp_lt_f32_e64 s[52:53], |v120|, s36
	s_nop 1
	v_cndmask_b32_e64 v120, v120, v121, s[52:53]
	v_cndmask_b32_e32 v121, 0, v216, vcc
	v_sub_f32_e32 v210, v120, v121
	v_mul_f32_e64 v121, |v114|, s8
	v_exp_f32_e32 v121, v121
	v_max_f32_e32 v120, v114, v114
	v_mul_f32_e32 v114, 0xbfb8aa3b, v114
	v_exp_f32_e32 v114, v114
	v_add_f32_e32 v121, 1.0, v121
	v_cmp_gt_f32_e32 vcc, s37, v121
	v_cndmask_b32_e64 v119, v210, v119, s[58:59]
	v_add_f32_e32 v114, 1.0, v114
	v_cndmask_b32_e64 v192, 0, 32, vcc
	v_ldexp_f32 v121, v121, v192
	v_log_f32_e32 v121, v121
	v_min_f32_e32 v120, 0, v120
	v_mul_f32_e32 v192, 0x3f317217, v121
	v_fma_f32 v192, v121, s33, -v192
	v_fmac_f32_e32 v192, 0x3377d1cf, v121
	v_fmac_f32_e32 v192, 0x3f317217, v121
	v_cmp_lt_f32_e64 s[52:53], |v121|, s36
	s_nop 1
	v_cndmask_b32_e64 v121, v121, v192, s[52:53]
	v_cndmask_b32_e32 v192, 0, v216, vcc
	v_sub_f32_e32 v192, v121, v192
	v_div_scale_f32 v121, s[2:3], v114, v114, v206
	v_rcp_f32_e32 v193, v121
	s_nop 0
	v_fma_f32 v194, -v121, v193, 1.0
	v_fmac_f32_e32 v193, v194, v193
	v_div_scale_f32 v194, vcc, v206, v114, v206
	v_mul_f32_e32 v195, v194, v193
	v_fma_f32 v196, -v121, v195, v194
	v_fmac_f32_e32 v195, v196, v193
	v_fma_f32 v121, -v121, v195, v194
	v_div_fmas_f32 v121, v121, v193, v195
	v_div_fixup_f32 v114, v121, v114, v206
	v_add_f32_e32 v114, v72, v114
	v_cmp_gt_f32_e32 vcc, s37, v114
	s_nop 1
	v_cndmask_b32_e64 v121, 0, 32, vcc
	v_ldexp_f32 v114, v114, v121
	v_log_f32_e32 v114, v114
	s_nop 0
	v_mul_f32_e32 v121, 0x3f317217, v114
	v_fma_f32 v121, v114, s33, -v121
	v_fmac_f32_e32 v121, 0x3377d1cf, v114
	v_fmac_f32_e32 v121, 0x3f317217, v114
	v_cmp_lt_f32_e64 s[52:53], |v114|, s36
	s_nop 1
	v_cndmask_b32_e64 v114, v114, v121, s[52:53]
	v_cndmask_b32_e32 v121, 0, v216, vcc
	v_sub_f32_e32 v211, v114, v121
	v_max_f32_e32 v114, v115, v115
	v_min_f32_e32 v121, 0, v114
	v_mul_f32_e64 v114, |v115|, s8
	v_exp_f32_e32 v114, v114
	s_nop 0
	v_add_f32_e32 v114, 1.0, v114
	v_cmp_gt_f32_e32 vcc, s37, v114
	s_nop 1
	v_cndmask_b32_e64 v193, 0, 32, vcc
	v_ldexp_f32 v114, v114, v193
	v_log_f32_e32 v114, v114
	s_nop 0
	v_mul_f32_e32 v193, 0x3f317217, v114
	v_fma_f32 v193, v114, s33, -v193
	v_fmac_f32_e32 v193, 0x3377d1cf, v114
	v_fmac_f32_e32 v193, 0x3f317217, v114
	v_cmp_lt_f32_e64 s[52:53], |v114|, s36
	s_nop 1
	v_cndmask_b32_e64 v114, v114, v193, s[52:53]
	v_cndmask_b32_e32 v193, 0, v216, vcc
	v_sub_f32_e32 v193, v114, v193
	v_mul_f32_e32 v114, 0xbfb8aa3b, v115
	v_exp_f32_e32 v114, v114
	v_pk_add_f32 v[120:121], v[120:121], v[192:193] neg_lo:[0,1] neg_hi:[0,1]
	v_add_f32_e32 v114, 1.0, v114
	v_div_scale_f32 v115, s[2:3], v114, v114, v205
	v_rcp_f32_e32 v194, v115
	s_nop 0
	v_fma_f32 v195, -v115, v194, 1.0
	v_fmac_f32_e32 v194, v195, v194
	v_div_scale_f32 v195, vcc, v205, v114, v205
	v_mul_f32_e32 v196, v195, v194
	v_fma_f32 v197, -v115, v196, v195
	v_fmac_f32_e32 v196, v197, v194
	v_fma_f32 v115, -v115, v196, v195
	v_div_fmas_f32 v115, v115, v194, v196
	v_div_fixup_f32 v114, v115, v114, v205
	v_add_f32_e32 v114, v73, v114
	v_cmp_gt_f32_e32 vcc, s37, v114
	s_nop 1
	v_cndmask_b32_e64 v115, 0, 32, vcc
	v_ldexp_f32 v114, v114, v115
	v_log_f32_e32 v114, v114
	s_nop 0
	v_mul_f32_e32 v115, 0x3f317217, v114
	v_fma_f32 v115, v114, s33, -v115
	v_fmac_f32_e32 v115, 0x3377d1cf, v114
	v_fmac_f32_e32 v115, 0x3f317217, v114
	v_cmp_lt_f32_e64 s[52:53], |v114|, s36
	s_nop 1
	v_cndmask_b32_e64 v114, v114, v115, s[52:53]
	v_cndmask_b32_e32 v115, 0, v216, vcc
	v_sub_f32_e32 v226, v114, v115
	v_mul_f32_e64 v115, |v116|, s8
	v_exp_f32_e32 v115, v115
	v_max_f32_e32 v114, v116, v116
	v_cndmask_b32_e64 v121, v226, v121, s[54:55]
	v_min_f32_e32 v114, 0, v114
	v_add_f32_e32 v115, 1.0, v115
	v_cmp_gt_f32_e32 vcc, s37, v115
	s_nop 1
	v_cndmask_b32_e64 v194, 0, 32, vcc
	v_ldexp_f32 v115, v115, v194
	v_log_f32_e32 v115, v115
	s_nop 0
	v_mul_f32_e32 v194, 0x3f317217, v115
	v_fma_f32 v194, v115, s33, -v194
	v_fmac_f32_e32 v194, 0x3377d1cf, v115
	v_fmac_f32_e32 v194, 0x3f317217, v115
	v_cmp_lt_f32_e64 s[52:53], |v115|, s36
	s_nop 1
	v_cndmask_b32_e64 v115, v115, v194, s[52:53]
	v_cndmask_b32_e32 v194, 0, v216, vcc
	v_sub_f32_e32 v194, v115, v194
	v_mul_f32_e32 v115, 0xbfb8aa3b, v116
	v_exp_f32_e32 v115, v115
	s_nop 0
	v_add_f32_e32 v115, 1.0, v115
	v_div_scale_f32 v116, s[2:3], v115, v115, v204
	v_rcp_f32_e32 v195, v116
	s_nop 0
	v_fma_f32 v196, -v116, v195, 1.0
	v_fmac_f32_e32 v195, v196, v195
	v_div_scale_f32 v196, vcc, v204, v115, v204
	v_mul_f32_e32 v197, v196, v195
	v_fma_f32 v198, -v116, v197, v196
	v_fmac_f32_e32 v197, v198, v195
	v_fma_f32 v116, -v116, v197, v196
	v_div_fmas_f32 v116, v116, v195, v197
	v_div_fixup_f32 v115, v116, v115, v204
	v_add_f32_e32 v115, v74, v115
	v_cmp_gt_f32_e32 vcc, s37, v115
	s_nop 1
	v_cndmask_b32_e64 v116, 0, 32, vcc
	v_ldexp_f32 v115, v115, v116
	v_log_f32_e32 v115, v115
	s_nop 0
	v_mul_f32_e32 v116, 0x3f317217, v115
	v_fma_f32 v116, v115, s33, -v116
	v_fmac_f32_e32 v116, 0x3377d1cf, v115
	v_fmac_f32_e32 v116, 0x3f317217, v115
	v_cmp_lt_f32_e64 s[52:53], |v115|, s36
	s_nop 1
	v_cndmask_b32_e64 v115, v115, v116, s[52:53]
	v_cndmask_b32_e32 v116, 0, v216, vcc
	v_sub_f32_e32 v227, v115, v116
	v_mul_f32_e64 v116, |v117|, s8
	v_exp_f32_e32 v116, v116
	v_max_f32_e32 v115, v117, v117
; template <int CTRL> __device__ __forceinline__ float dppx(float v) { return __int_as_float(__builtin_amdgcn_update_dpp(0, __float_as_int(v), CTRL, 0xf, 0xf, true)); }
; __device__ __forceinline__ float log_forget(float z, float lb) {
;   const float r0 = fminf(z, 0.f) - __logf(1.f + __expf(-fabsf(z)));
;   const float r1 = __logf(lb + (1.f - lb) / (1.f + __expf(-z)));
;   return lb <= 0.f ? r0 : r1;
; }
;   __device__ __forceinline__ void operator()(const f32x4 (&acc)[2][2][4][2], const pg8::Unit& u, int wr, int wc, int fr, int fq) const {
;     ...
;               for (int q = 0; q < 4; ++q) { const float gv = log_forget(acc[ai][bj][m][qh][q], lq[q]); g[m][q] = gv;
;                 float sc = gv; sc += dppx<0x111>(sc); sc += dppx<0x112>(sc); sc += dppx<0x114>(sc); sc += dppx<0x118>(sc);
	v_min_f32_e32 v115, 0, v115
	v_add_f32_e32 v116, 1.0, v116
	v_cmp_gt_f32_e32 vcc, s37, v116
	s_nop 1
	v_cndmask_b32_e64 v195, 0, 32, vcc
	v_ldexp_f32 v116, v116, v195
	v_log_f32_e32 v116, v116
	s_nop 0
	v_mul_f32_e32 v195, 0x3f317217, v116
	v_fma_f32 v195, v116, s33, -v195
	v_fmac_f32_e32 v195, 0x3377d1cf, v116
	v_fmac_f32_e32 v195, 0x3f317217, v116
	v_cmp_lt_f32_e64 s[52:53], |v116|, s36
	s_nop 1
	v_cndmask_b32_e64 v116, v116, v195, s[52:53]
	v_cndmask_b32_e32 v195, 0, v216, vcc
	v_sub_f32_e32 v195, v116, v195
	v_mul_f32_e32 v116, 0xbfb8aa3b, v117
	v_exp_f32_e32 v116, v116
	v_pk_add_f32 v[114:115], v[114:115], v[194:195] neg_lo:[0,1] neg_hi:[0,1]
	v_add_f32_e32 v116, 1.0, v116
	v_div_scale_f32 v117, s[2:3], v116, v116, v96
	v_rcp_f32_e32 v196, v117
	v_cndmask_b32_e64 v114, v227, v114, s[56:57]
	v_fma_f32 v197, -v117, v196, 1.0
	v_fmac_f32_e32 v196, v197, v196
	v_div_scale_f32 v197, vcc, v96, v116, v96
	v_mul_f32_e32 v198, v197, v196
	v_fma_f32 v199, -v117, v198, v197
	v_fmac_f32_e32 v198, v199, v196
	v_fma_f32 v117, -v117, v198, v197
	v_div_fmas_f32 v117, v117, v196, v198
	v_div_fixup_f32 v116, v117, v116, v96
	v_add_f32_e32 v116, v75, v116
	v_cmp_gt_f32_e32 vcc, s37, v116
	s_nop 1
	v_cndmask_b32_e64 v117, 0, 32, vcc
	v_ldexp_f32 v116, v116, v117
	v_log_f32_e32 v116, v116
	s_nop 0
	v_mul_f32_e32 v117, 0x3f317217, v116
	v_fma_f32 v117, v116, s33, -v117
	v_fmac_f32_e32 v117, 0x3377d1cf, v116
	v_fmac_f32_e32 v117, 0x3f317217, v116
	v_cmp_lt_f32_e64 s[52:53], |v116|, s36
	s_nop 1
	v_cndmask_b32_e64 v116, v116, v117, s[52:53]
	v_cndmask_b32_e32 v117, 0, v216, vcc
	v_sub_f32_e32 v228, v116, v117
	v_mul_f32_e64 v117, |v110|, s8
	v_exp_f32_e32 v117, v117
	v_max_f32_e32 v116, v110, v110
	v_mul_f32_e32 v110, 0xbfb8aa3b, v110
	v_exp_f32_e32 v110, v110
	v_add_f32_e32 v117, 1.0, v117
	v_cmp_gt_f32_e32 vcc, s37, v117
	v_cndmask_b32_e64 v115, v228, v115, s[58:59]
	v_add_f32_e32 v110, 1.0, v110
	v_cndmask_b32_e64 v196, 0, 32, vcc
	v_ldexp_f32 v117, v117, v196
	v_log_f32_e32 v117, v117
	v_min_f32_e32 v116, 0, v116
	v_mul_f32_e32 v196, 0x3f317217, v117
	v_fma_f32 v196, v117, s33, -v196
	v_fmac_f32_e32 v196, 0x3377d1cf, v117
	v_fmac_f32_e32 v196, 0x3f317217, v117
	v_cmp_lt_f32_e64 s[52:53], |v117|, s36
	s_nop 1
	v_cndmask_b32_e64 v117, v117, v196, s[52:53]
	v_cndmask_b32_e32 v196, 0, v216, vcc
	v_sub_f32_e32 v196, v117, v196
	v_div_scale_f32 v117, s[2:3], v110, v110, v206
	v_rcp_f32_e32 v197, v117
	s_nop 0
	v_fma_f32 v198, -v117, v197, 1.0
	v_fmac_f32_e32 v197, v198, v197
	v_div_scale_f32 v198, vcc, v206, v110, v206
	v_mul_f32_e32 v199, v198, v197
	v_fma_f32 v200, -v117, v199, v198
	v_fmac_f32_e32 v199, v200, v197
	v_fma_f32 v117, -v117, v199, v198
	v_div_fmas_f32 v117, v117, v197, v199
	v_div_fixup_f32 v110, v117, v110, v206
	v_add_f32_e32 v110, v72, v110
	v_cmp_gt_f32_e32 vcc, s37, v110
	s_nop 1
	v_cndmask_b32_e64 v117, 0, 32, vcc
	v_ldexp_f32 v110, v110, v117
	v_log_f32_e32 v110, v110
	s_nop 0
	v_mul_f32_e32 v117, 0x3f317217, v110
	v_fma_f32 v117, v110, s33, -v117
	v_fmac_f32_e32 v117, 0x3377d1cf, v110
	v_fmac_f32_e32 v117, 0x3f317217, v110
	v_cmp_lt_f32_e64 s[52:53], |v110|, s36
	s_nop 1
	v_cndmask_b32_e64 v110, v110, v117, s[52:53]
	v_cndmask_b32_e32 v117, 0, v216, vcc
	v_sub_f32_e32 v229, v110, v117
	v_max_f32_e32 v110, v111, v111
	v_min_f32_e32 v117, 0, v110
	v_mul_f32_e64 v110, |v111|, s8
	v_exp_f32_e32 v110, v110
	s_nop 0
	v_add_f32_e32 v110, 1.0, v110
	v_cmp_gt_f32_e32 vcc, s37, v110
	s_nop 1
	v_cndmask_b32_e64 v197, 0, 32, vcc
	v_ldexp_f32 v110, v110, v197
	v_log_f32_e32 v110, v110
	s_nop 0
	v_mul_f32_e32 v197, 0x3f317217, v110
	v_fma_f32 v197, v110, s33, -v197
	v_fmac_f32_e32 v197, 0x3377d1cf, v110
	v_fmac_f32_e32 v197, 0x3f317217, v110
	v_cmp_lt_f32_e64 s[52:53], |v110|, s36
	s_nop 1
	v_cndmask_b32_e64 v110, v110, v197, s[52:53]
	v_cndmask_b32_e32 v197, 0, v216, vcc
	v_sub_f32_e32 v197, v110, v197
	v_mul_f32_e32 v110, 0xbfb8aa3b, v111
	v_exp_f32_e32 v110, v110
	v_pk_add_f32 v[116:117], v[116:117], v[196:197] neg_lo:[0,1] neg_hi:[0,1]
	v_add_f32_e32 v110, 1.0, v110
	v_div_scale_f32 v111, s[2:3], v110, v110, v205
	v_rcp_f32_e32 v198, v111
	s_nop 0
	v_fma_f32 v199, -v111, v198, 1.0
	v_fmac_f32_e32 v198, v199, v198
	v_div_scale_f32 v199, vcc, v205, v110, v205
	v_mul_f32_e32 v200, v199, v198
	v_fma_f32 v201, -v111, v200, v199
	v_fmac_f32_e32 v200, v201, v198
	v_fma_f32 v111, -v111, v200, v199
	v_div_fmas_f32 v111, v111, v198, v200
	v_div_fixup_f32 v110, v111, v110, v205
	v_add_f32_e32 v110, v73, v110
	v_cmp_gt_f32_e32 vcc, s37, v110
	s_nop 1
	v_cndmask_b32_e64 v111, 0, 32, vcc
	v_ldexp_f32 v110, v110, v111
	v_log_f32_e32 v110, v110
	s_nop 0
	v_mul_f32_e32 v111, 0x3f317217, v110
	v_fma_f32 v111, v110, s33, -v111
	v_fmac_f32_e32 v111, 0x3377d1cf, v110
	v_fmac_f32_e32 v111, 0x3f317217, v110
	v_cmp_lt_f32_e64 s[52:53], |v110|, s36
	s_nop 1
	v_cndmask_b32_e64 v110, v110, v111, s[52:53]
	v_cndmask_b32_e32 v111, 0, v216, vcc
	v_sub_f32_e32 v230, v110, v111
	v_mul_f32_e64 v111, |v112|, s8
	v_exp_f32_e32 v111, v111
	v_max_f32_e32 v110, v112, v112
	v_cndmask_b32_e64 v117, v230, v117, s[54:55]
	v_min_f32_e32 v110, 0, v110
	v_add_f32_e32 v111, 1.0, v111
	v_cmp_gt_f32_e32 vcc, s37, v111
	v_mov_b32_dpp v197, v117 row_shr:1 row_mask:0xf bank_mask:0xf bound_ctrl:1
	s_nop 0
	v_cndmask_b32_e64 v198, 0, 32, vcc
	v_ldexp_f32 v111, v111, v198
	v_log_f32_e32 v111, v111
	s_nop 0
	v_mul_f32_e32 v198, 0x3f317217, v111
	v_fma_f32 v198, v111, s33, -v198
	v_fmac_f32_e32 v198, 0x3377d1cf, v111
	v_fmac_f32_e32 v198, 0x3f317217, v111
	v_cmp_lt_f32_e64 s[52:53], |v111|, s36
	s_nop 1
	v_cndmask_b32_e64 v111, v111, v198, s[52:53]
	v_cndmask_b32_e32 v198, 0, v216, vcc
; template <int CTRL> __device__ __forceinline__ float dppx(float v) { return __int_as_float(__builtin_amdgcn_update_dpp(0, __float_as_int(v), CTRL, 0xf, 0xf, true)); }
; __device__ __forceinline__ float log_forget(float z, float lb) {
;   const float r0 = fminf(z, 0.f) - __logf(1.f + __expf(-fabsf(z)));
;   const float r1 = __logf(lb + (1.f - lb) / (1.f + __expf(-z)));
;   return lb <= 0.f ? r0 : r1;
; }
;   __device__ __forceinline__ void operator()(const f32x4 (&acc)[2][2][4][2], const pg8::Unit& u, int wr, int wc, int fr, int fq) const {
;     ...
;               for (int q = 0; q < 4; ++q) { const float gv = log_forget(acc[ai][bj][m][qh][q], lq[q]); g[m][q] = gv;
;                 float sc = gv; sc += dppx<0x111>(sc); sc += dppx<0x112>(sc); sc += dppx<0x114>(sc); sc += dppx<0x118>(sc);
	v_sub_f32_e32 v198, v111, v198
	v_mul_f32_e32 v111, 0xbfb8aa3b, v112
	v_exp_f32_e32 v111, v111
	s_nop 0
	v_add_f32_e32 v111, 1.0, v111
	v_div_scale_f32 v112, s[2:3], v111, v111, v204
	v_rcp_f32_e32 v199, v112
	s_nop 0
	v_fma_f32 v200, -v112, v199, 1.0
	v_fmac_f32_e32 v199, v200, v199
	v_div_scale_f32 v200, vcc, v204, v111, v204
	v_mul_f32_e32 v201, v200, v199
	v_fma_f32 v202, -v112, v201, v200
	v_fmac_f32_e32 v201, v202, v199
	v_fma_f32 v112, -v112, v201, v200
	v_div_fmas_f32 v112, v112, v199, v201
	v_div_fixup_f32 v111, v112, v111, v204
	v_add_f32_e32 v111, v74, v111
	v_cmp_gt_f32_e32 vcc, s37, v111
	s_nop 1
	v_cndmask_b32_e64 v112, 0, 32, vcc
	v_ldexp_f32 v111, v111, v112
	v_log_f32_e32 v111, v111
	s_nop 0
	v_mul_f32_e32 v112, 0x3f317217, v111
	v_fma_f32 v112, v111, s33, -v112
	v_fmac_f32_e32 v112, 0x3377d1cf, v111
	v_fmac_f32_e32 v112, 0x3f317217, v111
	v_cmp_lt_f32_e64 s[52:53], |v111|, s36
	s_nop 1
	v_cndmask_b32_e64 v111, v111, v112, s[52:53]
	v_cndmask_b32_e32 v112, 0, v216, vcc
	v_sub_f32_e32 v231, v111, v112
	v_mul_f32_e64 v112, |v113|, s8
	v_exp_f32_e32 v112, v112
	v_max_f32_e32 v111, v113, v113
	v_min_f32_e32 v111, 0, v111
	v_add_f32_e32 v112, 1.0, v112
	v_cmp_gt_f32_e32 vcc, s37, v112
	s_nop 1
	v_cndmask_b32_e64 v199, 0, 32, vcc
	v_ldexp_f32 v112, v112, v199
	v_log_f32_e32 v112, v112
	s_nop 0
	v_mul_f32_e32 v199, 0x3f317217, v112
	v_fma_f32 v199, v112, s33, -v199
	v_fmac_f32_e32 v199, 0x3377d1cf, v112
	v_fmac_f32_e32 v199, 0x3f317217, v112
	v_cmp_lt_f32_e64 s[52:53], |v112|, s36
	s_nop 1
	v_cndmask_b32_e64 v112, v112, v199, s[52:53]
	v_cndmask_b32_e32 v199, 0, v216, vcc
	v_sub_f32_e32 v199, v112, v199
	v_mul_f32_e32 v112, 0xbfb8aa3b, v113
	v_exp_f32_e32 v112, v112
	v_pk_add_f32 v[110:111], v[110:111], v[198:199] neg_lo:[0,1] neg_hi:[0,1]
	v_add_f32_e32 v112, 1.0, v112
	v_div_scale_f32 v113, s[2:3], v112, v112, v96
	v_rcp_f32_e32 v200, v113
	v_cndmask_b32_e64 v110, v231, v110, s[56:57]
	v_fma_f32 v201, -v113, v200, 1.0
	v_fmac_f32_e32 v200, v201, v200
	v_div_scale_f32 v201, vcc, v96, v112, v96
	v_mul_f32_e32 v202, v201, v200
	v_fma_f32 v203, -v113, v202, v201
	v_fmac_f32_e32 v202, v203, v200
	v_fma_f32 v113, -v113, v202, v201
	v_div_fmas_f32 v113, v113, v200, v202
	v_div_fixup_f32 v112, v113, v112, v96
	v_add_f32_e32 v112, v75, v112
	v_cmp_gt_f32_e32 vcc, s37, v112
	v_mov_b32_dpp v198, v110 row_shr:1 row_mask:0xf bank_mask:0xf bound_ctrl:1
	s_nop 0
	v_cndmask_b32_e64 v113, 0, 32, vcc
	v_ldexp_f32 v112, v112, v113
	v_log_f32_e32 v112, v112
	s_nop 0
	v_mul_f32_e32 v113, 0x3f317217, v112
	v_fma_f32 v113, v112, s33, -v113
	v_fmac_f32_e32 v113, 0x3377d1cf, v112
	v_fmac_f32_e32 v113, 0x3f317217, v112
	v_cmp_lt_f32_e64 s[52:53], |v112|, s36
	s_nop 1
	v_cndmask_b32_e64 v112, v112, v113, s[52:53]
	v_cndmask_b32_e32 v113, 0, v216, vcc
	v_sub_f32_e32 v232, v112, v113
	v_mul_f32_e64 v113, |v106|, s8
	v_exp_f32_e32 v113, v113
	v_max_f32_e32 v112, v106, v106
	v_mul_f32_e32 v106, 0xbfb8aa3b, v106
	v_exp_f32_e32 v106, v106
	v_add_f32_e32 v113, 1.0, v113
	v_cmp_gt_f32_e32 vcc, s37, v113
	v_cndmask_b32_e64 v111, v232, v111, s[58:59]
	v_add_f32_e32 v106, 1.0, v106
	v_cndmask_b32_e64 v200, 0, 32, vcc
	v_ldexp_f32 v113, v113, v200
	v_log_f32_e32 v113, v113
	v_mov_b32_dpp v199, v111 row_shr:1 row_mask:0xf bank_mask:0xf bound_ctrl:1
	v_pk_add_f32 v[198:199], v[110:111], v[198:199]
	v_min_f32_e32 v112, 0, v112
	v_mul_f32_e32 v200, 0x3f317217, v113
	v_fma_f32 v200, v113, s33, -v200
	v_fmac_f32_e32 v200, 0x3377d1cf, v113
	v_fmac_f32_e32 v200, 0x3f317217, v113
	v_cmp_lt_f32_e64 s[52:53], |v113|, s36
	s_nop 1
	v_cndmask_b32_e64 v113, v113, v200, s[52:53]
	v_cndmask_b32_e32 v200, 0, v216, vcc
	v_sub_f32_e32 v200, v113, v200
	v_div_scale_f32 v113, s[2:3], v106, v106, v206
	v_rcp_f32_e32 v201, v113
	s_nop 0
	v_fma_f32 v202, -v113, v201, 1.0
	v_fmac_f32_e32 v201, v202, v201
	v_div_scale_f32 v202, vcc, v206, v106, v206
	v_mul_f32_e32 v203, v202, v201
	v_fma_f32 v212, -v113, v203, v202
	v_fmac_f32_e32 v203, v212, v201
	v_fma_f32 v113, -v113, v203, v202
	v_div_fmas_f32 v113, v113, v201, v203
	v_div_fixup_f32 v106, v113, v106, v206
	v_add_f32_e32 v106, v72, v106
	v_cmp_gt_f32_e32 vcc, s37, v106
	s_nop 1
	v_cndmask_b32_e64 v113, 0, 32, vcc
	v_ldexp_f32 v106, v106, v113
	v_log_f32_e32 v106, v106
	s_nop 0
	v_mul_f32_e32 v113, 0x3f317217, v106
	v_fma_f32 v113, v106, s33, -v113
	v_fmac_f32_e32 v113, 0x3377d1cf, v106
	v_fmac_f32_e32 v113, 0x3f317217, v106
	v_cmp_lt_f32_e64 s[52:53], |v106|, s36
	s_nop 1
	v_cndmask_b32_e64 v106, v106, v113, s[52:53]
	v_cndmask_b32_e32 v113, 0, v216, vcc
	v_sub_f32_e32 v233, v106, v113
	v_max_f32_e32 v106, v107, v107
	v_min_f32_e32 v113, 0, v106
	v_mul_f32_e64 v106, |v107|, s8
	v_exp_f32_e32 v106, v106
	s_nop 0
	v_add_f32_e32 v106, 1.0, v106
	v_cmp_gt_f32_e32 vcc, s37, v106
	s_nop 1
	v_cndmask_b32_e64 v201, 0, 32, vcc
	v_ldexp_f32 v106, v106, v201
	v_log_f32_e32 v106, v106
	s_nop 0
	v_mul_f32_e32 v201, 0x3f317217, v106
	v_fma_f32 v201, v106, s33, -v201
	v_fmac_f32_e32 v201, 0x3377d1cf, v106
	v_fmac_f32_e32 v201, 0x3f317217, v106
	v_cmp_lt_f32_e64 s[52:53], |v106|, s36
	s_nop 1
	v_cndmask_b32_e64 v106, v106, v201, s[52:53]
	v_cndmask_b32_e32 v201, 0, v216, vcc
	v_sub_f32_e32 v201, v106, v201
	v_mul_f32_e32 v106, 0xbfb8aa3b, v107
	v_exp_f32_e32 v106, v106
	v_pk_add_f32 v[112:113], v[112:113], v[200:201] neg_lo:[0,1] neg_hi:[0,1]
	v_add_f32_e32 v106, 1.0, v106
	v_div_scale_f32 v107, s[2:3], v106, v106, v205
	v_rcp_f32_e32 v202, v107
	s_nop 0
	v_fma_f32 v203, -v107, v202, 1.0
	v_fmac_f32_e32 v202, v203, v202
	v_div_scale_f32 v203, vcc, v205, v106, v205
	v_mul_f32_e32 v212, v203, v202
	v_fma_f32 v213, -v107, v212, v203
	v_fmac_f32_e32 v212, v213, v202
; template <int CTRL> __device__ __forceinline__ float dppx(float v) { return __int_as_float(__builtin_amdgcn_update_dpp(0, __float_as_int(v), CTRL, 0xf, 0xf, true)); }
; __device__ __forceinline__ float log_forget(float z, float lb) {
;   const float r0 = fminf(z, 0.f) - __logf(1.f + __expf(-fabsf(z)));
;   const float r1 = __logf(lb + (1.f - lb) / (1.f + __expf(-z)));
;   return lb <= 0.f ? r0 : r1;
; }
;   __device__ __forceinline__ void operator()(const f32x4 (&acc)[2][2][4][2], const pg8::Unit& u, int wr, int wc, int fr, int fq) const {
;     ...
;               for (int q = 0; q < 4; ++q) { const float gv = log_forget(acc[ai][bj][m][qh][q], lq[q]); g[m][q] = gv;
;                 float sc = gv; sc += dppx<0x111>(sc); sc += dppx<0x112>(sc); sc += dppx<0x114>(sc); sc += dppx<0x118>(sc);
;                 const float tot16 = __int_as_float(__builtin_amdgcn_ds_swizzle(__float_as_int(sc), 0x1F0));
	v_fma_f32 v107, -v107, v212, v203
	v_div_fmas_f32 v107, v107, v202, v212
	v_div_fixup_f32 v106, v107, v106, v205
	v_add_f32_e32 v106, v73, v106
	v_cmp_gt_f32_e32 vcc, s37, v106
	s_nop 1
	v_cndmask_b32_e64 v107, 0, 32, vcc
	v_ldexp_f32 v106, v106, v107
	v_log_f32_e32 v106, v106
	s_nop 0
	v_mul_f32_e32 v107, 0x3f317217, v106
	v_fma_f32 v107, v106, s33, -v107
	v_fmac_f32_e32 v107, 0x3377d1cf, v106
	v_fmac_f32_e32 v107, 0x3f317217, v106
	v_cmp_lt_f32_e64 s[52:53], |v106|, s36
	s_nop 1
	v_cndmask_b32_e64 v106, v106, v107, s[52:53]
	v_cndmask_b32_e32 v107, 0, v216, vcc
	v_sub_f32_e32 v234, v106, v107
	v_mul_f32_e64 v107, |v108|, s8
	v_exp_f32_e32 v107, v107
	v_max_f32_e32 v106, v108, v108
	v_cndmask_b32_e64 v113, v234, v113, s[54:55]
	v_min_f32_e32 v106, 0, v106
	v_add_f32_e32 v107, 1.0, v107
	v_cmp_gt_f32_e32 vcc, s37, v107
	v_mov_b32_dpp v201, v113 row_shr:1 row_mask:0xf bank_mask:0xf bound_ctrl:1
	s_nop 0
	v_cndmask_b32_e64 v202, 0, 32, vcc
	v_ldexp_f32 v107, v107, v202
	v_log_f32_e32 v107, v107
	s_nop 0
	v_mul_f32_e32 v202, 0x3f317217, v107
	v_fma_f32 v202, v107, s33, -v202
	v_fmac_f32_e32 v202, 0x3377d1cf, v107
	v_fmac_f32_e32 v202, 0x3f317217, v107
	v_cmp_lt_f32_e64 s[52:53], |v107|, s36
	s_nop 1
	v_cndmask_b32_e64 v107, v107, v202, s[52:53]
	v_cndmask_b32_e32 v202, 0, v216, vcc
	v_sub_f32_e32 v202, v107, v202
	v_mul_f32_e32 v107, 0xbfb8aa3b, v108
	v_exp_f32_e32 v107, v107
	s_nop 0
	v_add_f32_e32 v107, 1.0, v107
	v_div_scale_f32 v108, s[2:3], v107, v107, v204
	v_rcp_f32_e32 v203, v108
	s_nop 0
	v_fma_f32 v212, -v108, v203, 1.0
	v_fmac_f32_e32 v203, v212, v203
	v_div_scale_f32 v212, vcc, v204, v107, v204
	v_mul_f32_e32 v213, v212, v203
	v_fma_f32 v214, -v108, v213, v212
	v_fmac_f32_e32 v213, v214, v203
	v_fma_f32 v108, -v108, v213, v212
	v_div_fmas_f32 v108, v108, v203, v213
	v_div_fixup_f32 v107, v108, v107, v204
	v_add_f32_e32 v107, v74, v107
	v_cmp_gt_f32_e32 vcc, s37, v107
	s_nop 1
	v_cndmask_b32_e64 v108, 0, 32, vcc
	v_ldexp_f32 v107, v107, v108
	v_log_f32_e32 v107, v107
	s_nop 0
	v_mul_f32_e32 v108, 0x3f317217, v107
	v_fma_f32 v108, v107, s33, -v108
	v_fmac_f32_e32 v108, 0x3377d1cf, v107
	v_fmac_f32_e32 v108, 0x3f317217, v107
	v_cmp_lt_f32_e64 s[52:53], |v107|, s36
	s_nop 1
	v_cndmask_b32_e64 v107, v107, v108, s[52:53]
	v_cndmask_b32_e32 v108, 0, v216, vcc
	v_sub_f32_e32 v235, v107, v108
	v_mul_f32_e64 v108, |v109|, s8
	v_exp_f32_e32 v108, v108
	v_max_f32_e32 v107, v109, v109
	v_min_f32_e32 v107, 0, v107
	v_add_f32_e32 v108, 1.0, v108
	v_cmp_gt_f32_e32 vcc, s37, v108
	s_nop 1
	v_cndmask_b32_e64 v203, 0, 32, vcc
	v_ldexp_f32 v108, v108, v203
	v_log_f32_e32 v108, v108
	s_nop 0
	v_mul_f32_e32 v203, 0x3f317217, v108
	v_fma_f32 v203, v108, s33, -v203
	v_fmac_f32_e32 v203, 0x3377d1cf, v108
	v_fmac_f32_e32 v203, 0x3f317217, v108
	v_cmp_lt_f32_e64 s[52:53], |v108|, s36
	s_nop 1
	v_cndmask_b32_e64 v108, v108, v203, s[52:53]
	v_cndmask_b32_e32 v203, 0, v216, vcc
	v_sub_f32_e32 v203, v108, v203
	v_mul_f32_e32 v108, 0xbfb8aa3b, v109
	v_exp_f32_e32 v108, v108
	v_pk_add_f32 v[106:107], v[106:107], v[202:203] neg_lo:[0,1] neg_hi:[0,1]
	v_add_f32_e32 v108, 1.0, v108
	v_div_scale_f32 v109, s[2:3], v108, v108, v96
	v_rcp_f32_e32 v212, v109
	v_cndmask_b32_e64 v202, v235, v106, s[56:57]
	v_fma_f32 v213, -v109, v212, 1.0
	v_fmac_f32_e32 v212, v213, v212
	v_div_scale_f32 v213, vcc, v96, v108, v96
	v_mul_f32_e32 v214, v213, v212
	v_fma_f32 v215, -v109, v214, v213
	v_fmac_f32_e32 v214, v215, v212
	v_fma_f32 v109, -v109, v214, v213
	v_div_fmas_f32 v109, v109, v212, v214
	v_div_fixup_f32 v108, v109, v108, v96
	v_add_f32_e32 v108, v75, v108
	v_cmp_gt_f32_e32 vcc, s37, v108
	v_mov_b32_dpp v106, v202 row_shr:1 row_mask:0xf bank_mask:0xf bound_ctrl:1
	s_nop 0
	v_cndmask_b32_e64 v109, 0, 32, vcc
	v_ldexp_f32 v108, v108, v109
	v_log_f32_e32 v108, v108
	s_nop 0
	v_mul_f32_e32 v109, 0x3f317217, v108
	v_fma_f32 v109, v108, s33, -v109
	v_fmac_f32_e32 v109, 0x3377d1cf, v108
	v_fmac_f32_e32 v109, 0x3f317217, v108
	v_cmp_lt_f32_e64 s[52:53], |v108|, s36
	s_nop 1
	v_cndmask_b32_e64 v108, v108, v109, s[52:53]
	v_cndmask_b32_e32 v109, 0, v216, vcc
	v_sub_f32_e32 v214, v108, v109
	v_pk_add_f32 v[108:109], v[186:187], v[188:189] neg_lo:[0,1] neg_hi:[0,1]
	v_cmp_ge_f32_e64 s[52:53], 0, v72
	v_cndmask_b32_e64 v109, v208, v109, s[54:55]
	v_cndmask_b32_e64 v203, v214, v107, s[58:59]
	v_cndmask_b32_e64 v108, v207, v108, s[52:53]
	v_mov_b32_dpp v187, v109 row_shr:1 row_mask:0xf bank_mask:0xf bound_ctrl:1
	v_cndmask_b32_e64 v120, v211, v120, s[52:53]
	v_mov_b32_dpp v186, v108 row_shr:1 row_mask:0xf bank_mask:0xf bound_ctrl:1
	v_pk_add_f32 v[186:187], v[108:109], v[186:187]
	v_cndmask_b32_e64 v116, v229, v116, s[52:53]
	v_cndmask_b32_e64 v112, v233, v112, s[52:53]
	v_mov_b32_dpp v188, v186 row_shr:2 row_mask:0xf bank_mask:0xf bound_ctrl:1
	v_mov_b32_dpp v189, v187 row_shr:2 row_mask:0xf bank_mask:0xf bound_ctrl:1
	v_pk_add_f32 v[186:187], v[186:187], v[188:189]
	v_mov_b32_dpp v196, v116 row_shr:1 row_mask:0xf bank_mask:0xf bound_ctrl:1
	v_pk_add_f32 v[196:197], v[116:117], v[196:197]
	v_mov_b32_dpp v188, v186 row_shr:4 row_mask:0xf bank_mask:0xf bound_ctrl:1
	v_mov_b32_dpp v189, v187 row_shr:4 row_mask:0xf bank_mask:0xf bound_ctrl:1
	v_pk_add_f32 v[186:187], v[186:187], v[188:189]
	v_mov_b32_dpp v200, v112 row_shr:1 row_mask:0xf bank_mask:0xf bound_ctrl:1
	v_pk_add_f32 v[200:201], v[112:113], v[200:201]
	v_mov_b32_dpp v188, v186 row_shr:8 row_mask:0xf bank_mask:0xf bound_ctrl:1
	v_mov_b32_dpp v189, v187 row_shr:8 row_mask:0xf bank_mask:0xf bound_ctrl:1
	v_pk_add_f32 v[186:187], v[186:187], v[188:189]
	ds_swizzle_b32 v188, v186 offset:swizzle(BROADCAST,16,15)
	ds_swizzle_b32 v189, v187 offset:swizzle(BROADCAST,16,15)
	v_mov_b32_dpp v107, v203 row_shr:1 row_mask:0xf bank_mask:0xf bound_ctrl:1
	v_pk_add_f32 v[106:107], v[202:203], v[106:107]
	v_pk_add_f32 v[186:187], v[186:187], 0 op_sel_hi:[1,0]
	s_waitcnt lgkmcnt(0)
; template <int CTRL> __device__ __forceinline__ float dppx(float v) { return __int_as_float(__builtin_amdgcn_update_dpp(0, __float_as_int(v), CTRL, 0xf, 0xf, true)); }
;   __device__ __forceinline__ void operator()(const f32x4 (&acc)[2][2][4][2], const pg8::Unit& u, int wr, int wc, int fr, int fq) const {
;     ...
;               for (int q = 0; q < 4; ++q) { const float gv = log_forget(acc[ai][bj][m][qh][q], lq[q]); g[m][q] = gv;
;                 float sc = gv; sc += dppx<0x111>(sc); sc += dppx<0x112>(sc); sc += dppx<0x114>(sc); sc += dppx<0x118>(sc);
;                 const float tot16 = __int_as_float(__builtin_amdgcn_ds_swizzle(__float_as_int(sc), 0x1F0));
;                 cs[m][q] = sc + carry[q]; carry[q] += tot16; }
; #pragma unroll
;             for (int m = 0; m < 4; ++m) { const int r = row0 + ai * 128 + m * 16; float bq[4], kq[4];
; #pragma unroll
;               for (int q = 0; q < 4; ++q) { bq[q] = bwd ? (carry[q] - cs[m][q]) + g[m][q] : cs[m][q]; kq[q] = 1.f - __expf(g[m][q]); }
	v_pk_add_f32 v[212:213], v[188:189], 0 op_sel_hi:[1,0]
	v_mul_f32_e32 v188, 0x3fb8aa3b, v108
	v_exp_f32_e32 v188, v188
	v_mov_b32_dpp v189, v119 row_shr:1 row_mask:0xf bank_mask:0xf bound_ctrl:1
	v_sub_f32_e32 v207, 1.0, v188
	v_mul_f32_e32 v188, 0x3fb8aa3b, v109
	v_exp_f32_e32 v188, v188
	s_nop 0
	v_sub_f32_e32 v215, 1.0, v188
	v_mov_b32_dpp v188, v118 row_shr:1 row_mask:0xf bank_mask:0xf bound_ctrl:1
	v_pk_add_f32 v[188:189], v[118:119], v[188:189]
	s_nop 1
	v_mov_b32_dpp v190, v188 row_shr:2 row_mask:0xf bank_mask:0xf bound_ctrl:1
	v_mov_b32_dpp v191, v189 row_shr:2 row_mask:0xf bank_mask:0xf bound_ctrl:1
	v_pk_add_f32 v[188:189], v[188:189], v[190:191]
	s_nop 1
	v_mov_b32_dpp v190, v188 row_shr:4 row_mask:0xf bank_mask:0xf bound_ctrl:1
	v_mov_b32_dpp v191, v189 row_shr:4 row_mask:0xf bank_mask:0xf bound_ctrl:1
	v_pk_add_f32 v[188:189], v[188:189], v[190:191]
	s_nop 1
	v_mov_b32_dpp v190, v188 row_shr:8 row_mask:0xf bank_mask:0xf bound_ctrl:1
	v_mov_b32_dpp v191, v189 row_shr:8 row_mask:0xf bank_mask:0xf bound_ctrl:1
	v_pk_add_f32 v[188:189], v[188:189], v[190:191]
	ds_swizzle_b32 v190, v188 offset:swizzle(BROADCAST,16,15)
	ds_swizzle_b32 v191, v189 offset:swizzle(BROADCAST,16,15)
	v_pk_add_f32 v[188:189], v[188:189], 0 op_sel_hi:[1,0]
	s_waitcnt lgkmcnt(0)
	v_pk_add_f32 v[208:209], v[190:191], 0 op_sel_hi:[1,0]
	v_mul_f32_e32 v190, 0x3fb8aa3b, v118
	v_exp_f32_e32 v190, v190
	v_mov_b32_dpp v191, v121 row_shr:1 row_mask:0xf bank_mask:0xf bound_ctrl:1
	v_sub_f32_e32 v236, 1.0, v190
	v_mul_f32_e32 v190, 0x3fb8aa3b, v119
	v_exp_f32_e32 v190, v190
	s_nop 0
	v_sub_f32_e32 v237, 1.0, v190
	v_mov_b32_dpp v190, v120 row_shr:1 row_mask:0xf bank_mask:0xf bound_ctrl:1
	v_pk_add_f32 v[190:191], v[120:121], v[190:191]
	s_nop 1
	v_mov_b32_dpp v192, v190 row_shr:2 row_mask:0xf bank_mask:0xf bound_ctrl:1
	v_mov_b32_dpp v193, v191 row_shr:2 row_mask:0xf bank_mask:0xf bound_ctrl:1
	v_pk_add_f32 v[190:191], v[190:191], v[192:193]
	s_nop 1
	v_mov_b32_dpp v192, v190 row_shr:4 row_mask:0xf bank_mask:0xf bound_ctrl:1
	v_mov_b32_dpp v193, v191 row_shr:4 row_mask:0xf bank_mask:0xf bound_ctrl:1
	v_pk_add_f32 v[190:191], v[190:191], v[192:193]
	s_nop 1
	v_mov_b32_dpp v192, v190 row_shr:8 row_mask:0xf bank_mask:0xf bound_ctrl:1
	v_mov_b32_dpp v193, v191 row_shr:8 row_mask:0xf bank_mask:0xf bound_ctrl:1
	v_pk_add_f32 v[190:191], v[190:191], v[192:193]
	ds_swizzle_b32 v192, v190 offset:swizzle(BROADCAST,16,15)
	ds_swizzle_b32 v193, v191 offset:swizzle(BROADCAST,16,15)
	v_pk_add_f32 v[190:191], v[212:213], v[190:191]
	s_waitcnt lgkmcnt(0)
	v_pk_add_f32 v[210:211], v[212:213], v[192:193]
	v_mul_f32_e32 v192, 0x3fb8aa3b, v120
	v_exp_f32_e32 v192, v192
	v_mov_b32_dpp v193, v115 row_shr:1 row_mask:0xf bank_mask:0xf bound_ctrl:1
	v_sub_f32_e32 v226, 1.0, v192
	v_mul_f32_e32 v192, 0x3fb8aa3b, v121
	v_exp_f32_e32 v192, v192
	s_nop 0
	v_sub_f32_e32 v238, 1.0, v192
	v_mov_b32_dpp v192, v114 row_shr:1 row_mask:0xf bank_mask:0xf bound_ctrl:1
	v_pk_add_f32 v[192:193], v[114:115], v[192:193]
	s_nop 1
	v_mov_b32_dpp v194, v192 row_shr:2 row_mask:0xf bank_mask:0xf bound_ctrl:1
	v_mov_b32_dpp v195, v193 row_shr:2 row_mask:0xf bank_mask:0xf bound_ctrl:1
	v_pk_add_f32 v[192:193], v[192:193], v[194:195]
	s_nop 1
	v_mov_b32_dpp v194, v192 row_shr:4 row_mask:0xf bank_mask:0xf bound_ctrl:1
	v_mov_b32_dpp v195, v193 row_shr:4 row_mask:0xf bank_mask:0xf bound_ctrl:1
	v_pk_add_f32 v[192:193], v[192:193], v[194:195]
	s_nop 1
	v_mov_b32_dpp v194, v192 row_shr:8 row_mask:0xf bank_mask:0xf bound_ctrl:1
	v_mov_b32_dpp v195, v193 row_shr:8 row_mask:0xf bank_mask:0xf bound_ctrl:1
	v_pk_add_f32 v[192:193], v[192:193], v[194:195]
	ds_swizzle_b32 v194, v192 offset:swizzle(BROADCAST,16,15)
	ds_swizzle_b32 v195, v193 offset:swizzle(BROADCAST,16,15)
	v_pk_add_f32 v[192:193], v[208:209], v[192:193]
	s_waitcnt lgkmcnt(0)
	v_pk_add_f32 v[194:195], v[208:209], v[194:195]
	v_mul_f32_e32 v208, 0x3fb8aa3b, v114
	v_exp_f32_e32 v208, v208
	v_mov_b32_dpp v209, v197 row_shr:2 row_mask:0xf bank_mask:0xf bound_ctrl:1
	v_sub_f32_e32 v227, 1.0, v208
	v_mul_f32_e32 v208, 0x3fb8aa3b, v115
	v_exp_f32_e32 v208, v208
	s_nop 0
	v_sub_f32_e32 v228, 1.0, v208
	v_mov_b32_dpp v208, v196 row_shr:2 row_mask:0xf bank_mask:0xf bound_ctrl:1
	v_pk_add_f32 v[196:197], v[196:197], v[208:209]
	s_nop 1
	v_mov_b32_dpp v208, v196 row_shr:4 row_mask:0xf bank_mask:0xf bound_ctrl:1
	v_mov_b32_dpp v209, v197 row_shr:4 row_mask:0xf bank_mask:0xf bound_ctrl:1
	v_pk_add_f32 v[196:197], v[196:197], v[208:209]
	s_nop 1
	v_mov_b32_dpp v208, v196 row_shr:8 row_mask:0xf bank_mask:0xf bound_ctrl:1
	v_mov_b32_dpp v209, v197 row_shr:8 row_mask:0xf bank_mask:0xf bound_ctrl:1
	v_pk_add_f32 v[196:197], v[196:197], v[208:209]
	ds_swizzle_b32 v208, v196 offset:swizzle(BROADCAST,16,15)
	ds_swizzle_b32 v209, v197 offset:swizzle(BROADCAST,16,15)
	v_pk_add_f32 v[196:197], v[210:211], v[196:197]
	s_waitcnt lgkmcnt(0)
	v_pk_add_f32 v[208:209], v[210:211], v[208:209]
	v_mul_f32_e32 v210, 0x3fb8aa3b, v116
	v_exp_f32_e32 v210, v210
	v_mov_b32_dpp v211, v199 row_shr:2 row_mask:0xf bank_mask:0xf bound_ctrl:1
	v_sub_f32_e32 v229, 1.0, v210
	v_mul_f32_e32 v210, 0x3fb8aa3b, v117
	v_exp_f32_e32 v210, v210
	s_nop 0
	v_sub_f32_e32 v230, 1.0, v210
	v_mov_b32_dpp v210, v198 row_shr:2 row_mask:0xf bank_mask:0xf bound_ctrl:1
	v_pk_add_f32 v[198:199], v[198:199], v[210:211]
	s_nop 1
	v_mov_b32_dpp v210, v198 row_shr:4 row_mask:0xf bank_mask:0xf bound_ctrl:1
	v_mov_b32_dpp v211, v199 row_shr:4 row_mask:0xf bank_mask:0xf bound_ctrl:1
	v_pk_add_f32 v[198:199], v[198:199], v[210:211]
	s_nop 1
	v_mov_b32_dpp v210, v198 row_shr:8 row_mask:0xf bank_mask:0xf bound_ctrl:1
	v_mov_b32_dpp v211, v199 row_shr:8 row_mask:0xf bank_mask:0xf bound_ctrl:1
	v_pk_add_f32 v[198:199], v[198:199], v[210:211]
	ds_swizzle_b32 v210, v198 offset:swizzle(BROADCAST,16,15)
	ds_swizzle_b32 v211, v199 offset:swizzle(BROADCAST,16,15)
	v_pk_add_f32 v[198:199], v[194:195], v[198:199]
	s_waitcnt lgkmcnt(0)
; template <int CTRL> __device__ __forceinline__ float dppx(float v) { return __int_as_float(__builtin_amdgcn_update_dpp(0, __float_as_int(v), CTRL, 0xf, 0xf, true)); }
; __device__ __forceinline__ unsigned cvt_pk_bf16(float lo, float hi) { unsigned r; asm volatile("v_cvt_pk_bf16_f32 %0, %1, %2" : "=v"(r) : "v"(lo), "v"(hi)); return r; }
; __device__ __forceinline__ float log_forget(float z, float lb) {
;   const float r0 = fminf(z, 0.f) - __logf(1.f + __expf(-fabsf(z)));
;   const float r1 = __logf(lb + (1.f - lb) / (1.f + __expf(-z)));
;   return lb <= 0.f ? r0 : r1;
; }
;   __device__ __forceinline__ void operator()(const f32x4 (&acc)[2][2][4][2], const pg8::Unit& u, int wr, int wc, int fr, int fq) const {
;     ...
;                 float sc = gv; sc += dppx<0x111>(sc); sc += dppx<0x112>(sc); sc += dppx<0x114>(sc); sc += dppx<0x118>(sc);
;                 const float tot16 = __int_as_float(__builtin_amdgcn_ds_swizzle(__float_as_int(sc), 0x1F0));
;                 cs[m][q] = sc + carry[q]; carry[q] += tot16; }
; #pragma unroll
;             for (int m = 0; m < 4; ++m) { const int r = row0 + ai * 128 + m * 16; float bq[4], kq[4];
; #pragma unroll
;               for (int q = 0; q < 4; ++q) { bq[q] = bwd ? (carry[q] - cs[m][q]) + g[m][q] : cs[m][q]; kq[q] = 1.f - __expf(g[m][q]); }
;               *(f32x4*)(logfp + (size_t)r * 1024 + c + 4 * qh) = (f32x4){bq[0], bq[1], bq[2], bq[3]};
;               u32x2 w; w.x = pg8::cvt_pk_bf16(kq[0], kq[1]); w.y = pg8::cvt_pk_bf16(kq[2], kq[3]);
;               *(u32x2*)(km + (size_t)r * 1024 + c + 4 * qh) = w; } } }
	v_pk_add_f32 v[194:195], v[194:195], v[210:211]
	v_mul_f32_e32 v210, 0x3fb8aa3b, v110
	v_exp_f32_e32 v210, v210
	v_mov_b32_dpp v211, v201 row_shr:2 row_mask:0xf bank_mask:0xf bound_ctrl:1
	v_sub_f32_e32 v231, 1.0, v210
	v_mul_f32_e32 v210, 0x3fb8aa3b, v111
	v_exp_f32_e32 v210, v210
	s_nop 0
	v_sub_f32_e32 v232, 1.0, v210
	v_mov_b32_dpp v210, v200 row_shr:2 row_mask:0xf bank_mask:0xf bound_ctrl:1
	v_pk_add_f32 v[200:201], v[200:201], v[210:211]
	s_nop 1
	v_mov_b32_dpp v210, v200 row_shr:4 row_mask:0xf bank_mask:0xf bound_ctrl:1
	v_mov_b32_dpp v211, v201 row_shr:4 row_mask:0xf bank_mask:0xf bound_ctrl:1
	v_pk_add_f32 v[200:201], v[200:201], v[210:211]
	s_nop 1
	v_mov_b32_dpp v210, v200 row_shr:8 row_mask:0xf bank_mask:0xf bound_ctrl:1
	v_mov_b32_dpp v211, v201 row_shr:8 row_mask:0xf bank_mask:0xf bound_ctrl:1
	v_pk_add_f32 v[200:201], v[200:201], v[210:211]
	ds_swizzle_b32 v210, v200 offset:swizzle(BROADCAST,16,15)
	ds_swizzle_b32 v211, v201 offset:swizzle(BROADCAST,16,15)
	v_pk_add_f32 v[200:201], v[208:209], v[200:201]
	s_waitcnt lgkmcnt(0)
	v_pk_add_f32 v[208:209], v[208:209], v[210:211]
	v_mul_f32_e32 v210, 0x3fb8aa3b, v112
	v_exp_f32_e32 v210, v210
	v_mov_b32_dpp v211, v107 row_shr:2 row_mask:0xf bank_mask:0xf bound_ctrl:1
	v_sub_f32_e32 v233, 1.0, v210
	v_mul_f32_e32 v210, 0x3fb8aa3b, v113
	v_exp_f32_e32 v210, v210
	s_nop 0
	v_sub_f32_e32 v234, 1.0, v210
	v_mov_b32_dpp v210, v106 row_shr:2 row_mask:0xf bank_mask:0xf bound_ctrl:1
	v_pk_add_f32 v[106:107], v[106:107], v[210:211]
	s_nop 1
	v_mov_b32_dpp v210, v106 row_shr:4 row_mask:0xf bank_mask:0xf bound_ctrl:1
	v_mov_b32_dpp v211, v107 row_shr:4 row_mask:0xf bank_mask:0xf bound_ctrl:1
	v_pk_add_f32 v[106:107], v[106:107], v[210:211]
	s_nop 1
	v_mov_b32_dpp v210, v106 row_shr:8 row_mask:0xf bank_mask:0xf bound_ctrl:1
	v_mov_b32_dpp v211, v107 row_shr:8 row_mask:0xf bank_mask:0xf bound_ctrl:1
	v_pk_add_f32 v[106:107], v[106:107], v[210:211]
	ds_swizzle_b32 v210, v106 offset:swizzle(BROADCAST,16,15)
	ds_swizzle_b32 v211, v107 offset:swizzle(BROADCAST,16,15)
	v_pk_add_f32 v[212:213], v[194:195], v[106:107]
	v_pk_add_f32 v[106:107], v[208:209], v[186:187] neg_lo:[0,1] neg_hi:[0,1]
	s_waitcnt lgkmcnt(0)
	v_pk_add_f32 v[194:195], v[194:195], v[210:211]
	s_nop 0
	v_pk_add_f32 v[210:211], v[194:195], v[188:189] neg_lo:[0,1] neg_hi:[0,1]
	v_pk_add_f32 v[106:107], v[108:109], v[106:107]
	v_pk_add_f32 v[108:109], v[118:119], v[210:211]
	v_cndmask_b32_e64 v107, v187, v107, s[42:43]
	v_cndmask_b32_e64 v109, v189, v109, s[42:43]
	v_cndmask_b32_e64 v108, v188, v108, s[42:43]
	v_cndmask_b32_e64 v106, v186, v106, s[42:43]
	global_store_dwordx4 v[176:177], v[106:109], off offset:16
	s_nop 1
	v_cvt_pk_bf16_f32 v106, v207, v215
	v_cvt_pk_bf16_f32 v107, v236, v237
	global_store_dwordx2 v[174:175], v[106:107], off offset:8
	v_pk_add_f32 v[106:107], v[208:209], v[190:191] neg_lo:[0,1] neg_hi:[0,1]
	v_pk_add_f32 v[108:109], v[194:195], v[192:193] neg_lo:[0,1] neg_hi:[0,1]
	v_pk_add_f32 v[106:107], v[120:121], v[106:107]
	v_pk_add_f32 v[108:109], v[114:115], v[108:109]
	v_cndmask_b32_e64 v107, v191, v107, s[42:43]
	v_cndmask_b32_e64 v109, v193, v109, s[42:43]
	v_cndmask_b32_e64 v108, v192, v108, s[42:43]
	v_cndmask_b32_e64 v106, v190, v106, s[42:43]
	global_store_dwordx4 v[180:181], v[106:109], off offset:16
	s_nop 1
	v_cvt_pk_bf16_f32 v106, v226, v238
	v_cvt_pk_bf16_f32 v107, v227, v228
	global_store_dwordx2 v[172:173], v[106:107], off offset:8
	v_pk_add_f32 v[106:107], v[208:209], v[196:197] neg_lo:[0,1] neg_hi:[0,1]
	v_pk_add_f32 v[108:109], v[194:195], v[198:199] neg_lo:[0,1] neg_hi:[0,1]
	v_pk_add_f32 v[106:107], v[116:117], v[106:107]
	v_pk_add_f32 v[108:109], v[110:111], v[108:109]
	v_cndmask_b32_e64 v107, v197, v107, s[42:43]
	v_cndmask_b32_e64 v109, v199, v109, s[42:43]
	v_cndmask_b32_e64 v108, v198, v108, s[42:43]
	v_cndmask_b32_e64 v106, v196, v106, s[42:43]
	global_store_dwordx4 v[182:183], v[106:109], off offset:16
	v_mul_f32_e32 v111, 0x3fb8aa3b, v203
	v_exp_f32_e32 v111, v111
	v_cvt_pk_bf16_f32 v106, v229, v230
	v_cvt_pk_bf16_f32 v107, v231, v232
	global_store_dwordx2 v[170:171], v[106:107], off offset:8
	v_mul_f32_e32 v106, 0x3fb8aa3b, v202
	v_exp_f32_e32 v106, v106
	v_pk_add_f32 v[108:109], v[194:195], v[212:213] neg_lo:[0,1] neg_hi:[0,1]
	v_sub_f32_e32 v111, 1.0, v111
	v_pk_add_f32 v[108:109], v[202:203], v[108:109]
	v_sub_f32_e32 v110, 1.0, v106
	v_pk_add_f32 v[106:107], v[208:209], v[200:201] neg_lo:[0,1] neg_hi:[0,1]
	v_cndmask_b32_e64 v109, v213, v109, s[42:43]
	v_pk_add_f32 v[106:107], v[112:113], v[106:107]
	v_cndmask_b32_e64 v108, v212, v108, s[42:43]
	v_cndmask_b32_e64 v107, v201, v107, s[42:43]
	v_cndmask_b32_e64 v106, v200, v106, s[42:43]
	global_store_dwordx4 v[184:185], v[106:109], off offset:16
	s_nop 1
	v_cvt_pk_bf16_f32 v106, v233, v234
	v_cvt_pk_bf16_f32 v107, v110, v111
	global_store_dwordx2 v[168:169], v[106:107], off offset:8
	v_mul_f32_e64 v107, |v102|, s8
	v_exp_f32_e32 v107, v107
	v_max_f32_e32 v106, v102, v102
	v_mul_f32_e32 v102, 0xbfb8aa3b, v102
	v_exp_f32_e32 v102, v102
	v_add_f32_e32 v107, 1.0, v107
	v_cmp_gt_f32_e32 vcc, s37, v107
	v_min_f32_e32 v106, 0, v106
	v_add_f32_e32 v102, 1.0, v102
	v_cndmask_b32_e64 v108, 0, 32, vcc
	v_ldexp_f32 v107, v107, v108
	v_log_f32_e32 v107, v107
	s_nop 0
	v_mul_f32_e32 v108, 0x3f317217, v107
	v_fma_f32 v108, v107, s33, -v108
	v_fmac_f32_e32 v108, 0x3377d1cf, v107
	v_fmac_f32_e32 v108, 0x3f317217, v107
	v_cmp_lt_f32_e64 s[60:61], |v107|, s36
	s_nop 1
	v_cndmask_b32_e64 v107, v107, v108, s[60:61]
	v_cndmask_b32_e32 v108, 0, v216, vcc
	v_sub_f32_e32 v108, v107, v108
	v_div_scale_f32 v107, s[2:3], v102, v102, v157
	v_rcp_f32_e32 v109, v107
; __device__ __forceinline__ float log_forget(float z, float lb) {
;   const float r0 = fminf(z, 0.f) - __logf(1.f + __expf(-fabsf(z)));
;   const float r1 = __logf(lb + (1.f - lb) / (1.f + __expf(-z)));
;   return lb <= 0.f ? r0 : r1;
; }
	s_nop 0
	v_fma_f32 v110, -v107, v109, 1.0
	v_fmac_f32_e32 v109, v110, v109
	v_div_scale_f32 v110, vcc, v157, v102, v157
	v_mul_f32_e32 v111, v110, v109
	v_fma_f32 v112, -v107, v111, v110
	v_fmac_f32_e32 v111, v112, v109
	v_fma_f32 v107, -v107, v111, v110
	v_div_fmas_f32 v107, v107, v109, v111
	v_div_fixup_f32 v102, v107, v102, v157
	v_add_f32_e32 v102, v92, v102
	v_cmp_gt_f32_e32 vcc, s37, v102
	s_nop 1
	v_cndmask_b32_e64 v107, 0, 32, vcc
	v_ldexp_f32 v102, v102, v107
	v_log_f32_e32 v102, v102
	s_nop 0
	v_mul_f32_e32 v107, 0x3f317217, v102
	v_fma_f32 v107, v102, s33, -v107
	v_fmac_f32_e32 v107, 0x3377d1cf, v102
	v_fmac_f32_e32 v107, 0x3f317217, v102
	v_cmp_lt_f32_e64 s[60:61], |v102|, s36
	s_nop 1
	v_cndmask_b32_e64 v102, v102, v107, s[60:61]
	v_cndmask_b32_e32 v107, 0, v216, vcc
	v_sub_f32_e32 v180, v102, v107
	v_max_f32_e32 v102, v103, v103
	v_min_f32_e32 v107, 0, v102
	v_mul_f32_e64 v102, |v103|, s8
	v_exp_f32_e32 v102, v102
	s_nop 0
	v_add_f32_e32 v102, 1.0, v102
	v_cmp_gt_f32_e32 vcc, s37, v102
	s_nop 1
	v_cndmask_b32_e64 v109, 0, 32, vcc
	v_ldexp_f32 v102, v102, v109
	v_log_f32_e32 v102, v102
	s_nop 0
	v_mul_f32_e32 v109, 0x3f317217, v102
	v_fma_f32 v109, v102, s33, -v109
	v_fmac_f32_e32 v109, 0x3377d1cf, v102
	v_fmac_f32_e32 v109, 0x3f317217, v102
	v_cmp_lt_f32_e64 s[60:61], |v102|, s36
	s_nop 1
	v_cndmask_b32_e64 v102, v102, v109, s[60:61]
	v_cndmask_b32_e32 v109, 0, v216, vcc
	v_sub_f32_e32 v109, v102, v109
	v_mul_f32_e32 v102, 0xbfb8aa3b, v103
	v_exp_f32_e32 v102, v102
	s_nop 0
	v_add_f32_e32 v102, 1.0, v102
	v_div_scale_f32 v103, s[2:3], v102, v102, v159
	v_rcp_f32_e32 v110, v103
	s_nop 0
	v_fma_f32 v111, -v103, v110, 1.0
	v_fmac_f32_e32 v110, v111, v110
	v_div_scale_f32 v111, vcc, v159, v102, v159
	v_mul_f32_e32 v112, v111, v110
	v_fma_f32 v113, -v103, v112, v111
	v_fmac_f32_e32 v112, v113, v110
	v_fma_f32 v103, -v103, v112, v111
	v_div_fmas_f32 v103, v103, v110, v112
	v_div_fixup_f32 v102, v103, v102, v159
	v_add_f32_e32 v102, v93, v102
	v_cmp_gt_f32_e32 vcc, s37, v102
	s_nop 1
	v_cndmask_b32_e64 v103, 0, 32, vcc
	v_ldexp_f32 v102, v102, v103
	v_log_f32_e32 v102, v102
	s_nop 0
	v_mul_f32_e32 v103, 0x3f317217, v102
	v_fma_f32 v103, v102, s33, -v103
	v_fmac_f32_e32 v103, 0x3377d1cf, v102
	v_fmac_f32_e32 v103, 0x3f317217, v102
	v_cmp_lt_f32_e64 s[60:61], |v102|, s36
	s_nop 1
	v_cndmask_b32_e64 v102, v102, v103, s[60:61]
	v_cndmask_b32_e32 v103, 0, v216, vcc
	v_sub_f32_e32 v181, v102, v103
	v_mul_f32_e64 v103, |v104|, s8
	v_exp_f32_e32 v103, v103
	v_max_f32_e32 v102, v104, v104
	v_min_f32_e32 v102, 0, v102
	v_add_f32_e32 v103, 1.0, v103
	v_cmp_gt_f32_e32 vcc, s37, v103
	s_nop 1
	v_cndmask_b32_e64 v110, 0, 32, vcc
	v_ldexp_f32 v103, v103, v110
	v_log_f32_e32 v103, v103
	s_nop 0
	v_mul_f32_e32 v110, 0x3f317217, v103
	v_fma_f32 v110, v103, s33, -v110
	v_fmac_f32_e32 v110, 0x3377d1cf, v103
	v_fmac_f32_e32 v110, 0x3f317217, v103
	v_cmp_lt_f32_e64 s[60:61], |v103|, s36
	s_nop 1
	v_cndmask_b32_e64 v103, v103, v110, s[60:61]
	v_cndmask_b32_e32 v110, 0, v216, vcc
	v_sub_f32_e32 v110, v103, v110
	v_mul_f32_e32 v103, 0xbfb8aa3b, v104
	v_exp_f32_e32 v103, v103
	s_nop 0
	v_add_f32_e32 v103, 1.0, v103
	v_div_scale_f32 v104, s[2:3], v103, v103, v161
	v_rcp_f32_e32 v111, v104
	s_nop 0
	v_fma_f32 v112, -v104, v111, 1.0
	v_fmac_f32_e32 v111, v112, v111
	v_div_scale_f32 v112, vcc, v161, v103, v161
	v_mul_f32_e32 v113, v112, v111
	v_fma_f32 v114, -v104, v113, v112
	v_fmac_f32_e32 v113, v114, v111
	v_fma_f32 v104, -v104, v113, v112
	v_div_fmas_f32 v104, v104, v111, v113
	v_div_fixup_f32 v103, v104, v103, v161
	v_add_f32_e32 v103, v94, v103
	v_cmp_gt_f32_e32 vcc, s37, v103
	v_mul_f32_e64 v111, |v105|, s8
	v_exp_f32_e32 v111, v111
	v_cndmask_b32_e64 v104, 0, 32, vcc
	v_ldexp_f32 v103, v103, v104
	v_log_f32_e32 v103, v103
	v_add_f32_e32 v111, 1.0, v111
	v_mul_f32_e32 v104, 0x3f317217, v103
	v_fma_f32 v104, v103, s33, -v104
	v_fmac_f32_e32 v104, 0x3377d1cf, v103
	v_fmac_f32_e32 v104, 0x3f317217, v103
	v_cmp_lt_f32_e64 s[60:61], |v103|, s36
	s_nop 1
	v_cndmask_b32_e64 v103, v103, v104, s[60:61]
	v_cndmask_b32_e32 v104, 0, v216, vcc
	v_cmp_gt_f32_e32 vcc, s37, v111
	v_sub_f32_e32 v104, v103, v104
	v_max_f32_e32 v103, v105, v105
	v_cndmask_b32_e64 v112, 0, 32, vcc
	v_ldexp_f32 v111, v111, v112
	v_log_f32_e32 v111, v111
	v_mul_f32_e32 v105, 0xbfb8aa3b, v105
	v_exp_f32_e32 v105, v105
	v_min_f32_e32 v103, 0, v103
	v_mul_f32_e32 v112, 0x3f317217, v111
	v_fma_f32 v112, v111, s33, -v112
	v_fmac_f32_e32 v112, 0x3377d1cf, v111
	v_fmac_f32_e32 v112, 0x3f317217, v111
	v_cmp_lt_f32_e64 s[60:61], |v111|, s36
	v_add_f32_e32 v105, 1.0, v105
	s_nop 0
	v_cndmask_b32_e64 v111, v111, v112, s[60:61]
	v_cndmask_b32_e32 v112, 0, v216, vcc
	v_sub_f32_e32 v111, v111, v112
	v_div_scale_f32 v112, s[2:3], v105, v105, v163
	v_rcp_f32_e32 v113, v112
	s_nop 0
	v_fma_f32 v114, -v112, v113, 1.0
	v_fmac_f32_e32 v113, v114, v113
	v_div_scale_f32 v114, vcc, v163, v105, v163
	v_mul_f32_e32 v115, v114, v113
	v_fma_f32 v116, -v112, v115, v114
	v_fmac_f32_e32 v115, v116, v113
	v_fma_f32 v112, -v112, v115, v114
	v_div_fmas_f32 v112, v112, v113, v115
	v_div_fixup_f32 v105, v112, v105, v163
	v_add_f32_e32 v105, v95, v105
	v_cmp_gt_f32_e32 vcc, s37, v105
	v_mul_f32_e64 v113, |v98|, s8
	v_exp_f32_e32 v113, v113
	v_cndmask_b32_e64 v112, 0, 32, vcc
	v_ldexp_f32 v105, v105, v112
	v_log_f32_e32 v105, v105
	v_add_f32_e32 v113, 1.0, v113
	v_mul_f32_e32 v112, 0x3f317217, v105
	v_fma_f32 v112, v105, s33, -v112
	v_fmac_f32_e32 v112, 0x3377d1cf, v105
	v_fmac_f32_e32 v112, 0x3f317217, v105
	v_cmp_lt_f32_e64 s[60:61], |v105|, s36
	s_nop 1
	v_cndmask_b32_e64 v105, v105, v112, s[60:61]
	v_cndmask_b32_e32 v112, 0, v216, vcc
; __device__ __forceinline__ float log_forget(float z, float lb) {
;   const float r0 = fminf(z, 0.f) - __logf(1.f + __expf(-fabsf(z)));
;   const float r1 = __logf(lb + (1.f - lb) / (1.f + __expf(-z)));
;   return lb <= 0.f ? r0 : r1;
; }
	v_cmp_gt_f32_e32 vcc, s37, v113
	v_sub_f32_e32 v105, v105, v112
	v_max_f32_e32 v112, v98, v98
	v_cndmask_b32_e64 v114, 0, 32, vcc
	v_ldexp_f32 v113, v113, v114
	v_log_f32_e32 v113, v113
	v_mul_f32_e32 v98, 0xbfb8aa3b, v98
	v_exp_f32_e32 v98, v98
	v_min_f32_e32 v112, 0, v112
	v_mul_f32_e32 v114, 0x3f317217, v113
	v_fma_f32 v114, v113, s33, -v114
	v_fmac_f32_e32 v114, 0x3377d1cf, v113
	v_fmac_f32_e32 v114, 0x3f317217, v113
	v_cmp_lt_f32_e64 s[60:61], |v113|, s36
	v_add_f32_e32 v98, 1.0, v98
	s_nop 0
	v_cndmask_b32_e64 v113, v113, v114, s[60:61]
	v_cndmask_b32_e32 v114, 0, v216, vcc
	v_sub_f32_e32 v114, v113, v114
	v_div_scale_f32 v113, s[2:3], v98, v98, v157
	v_rcp_f32_e32 v115, v113
	s_nop 0
	v_fma_f32 v116, -v113, v115, 1.0
	v_fmac_f32_e32 v115, v116, v115
	v_div_scale_f32 v116, vcc, v157, v98, v157
	v_mul_f32_e32 v117, v116, v115
	v_fma_f32 v118, -v113, v117, v116
	v_fmac_f32_e32 v117, v118, v115
	v_fma_f32 v113, -v113, v117, v116
	v_div_fmas_f32 v113, v113, v115, v117
	v_div_fixup_f32 v98, v113, v98, v157
	v_add_f32_e32 v98, v92, v98
	v_cmp_gt_f32_e32 vcc, s37, v98
	s_nop 1
	v_cndmask_b32_e64 v113, 0, 32, vcc
	v_ldexp_f32 v98, v98, v113
	v_log_f32_e32 v98, v98
	s_nop 0
	v_mul_f32_e32 v113, 0x3f317217, v98
	v_fma_f32 v113, v98, s33, -v113
	v_fmac_f32_e32 v113, 0x3377d1cf, v98
	v_fmac_f32_e32 v113, 0x3f317217, v98
	v_cmp_lt_f32_e64 s[60:61], |v98|, s36
	s_nop 1
	v_cndmask_b32_e64 v98, v98, v113, s[60:61]
	v_cndmask_b32_e32 v113, 0, v216, vcc
	v_sub_f32_e32 v188, v98, v113
	v_max_f32_e32 v98, v99, v99
	v_min_f32_e32 v113, 0, v98
	v_mul_f32_e64 v98, |v99|, s8
	v_exp_f32_e32 v98, v98
	s_nop 0
	v_add_f32_e32 v98, 1.0, v98
	v_cmp_gt_f32_e32 vcc, s37, v98
	s_nop 1
	v_cndmask_b32_e64 v115, 0, 32, vcc
	v_ldexp_f32 v98, v98, v115
	v_log_f32_e32 v98, v98
	s_nop 0
	v_mul_f32_e32 v115, 0x3f317217, v98
	v_fma_f32 v115, v98, s33, -v115
	v_fmac_f32_e32 v115, 0x3377d1cf, v98
	v_fmac_f32_e32 v115, 0x3f317217, v98
	v_cmp_lt_f32_e64 s[60:61], |v98|, s36
	s_nop 1
	v_cndmask_b32_e64 v98, v98, v115, s[60:61]
	v_cndmask_b32_e32 v115, 0, v216, vcc
	v_sub_f32_e32 v115, v98, v115
	v_mul_f32_e32 v98, 0xbfb8aa3b, v99
	v_exp_f32_e32 v98, v98
	s_nop 0
	v_add_f32_e32 v98, 1.0, v98
	v_div_scale_f32 v99, s[2:3], v98, v98, v159
	v_rcp_f32_e32 v116, v99
	s_nop 0
	v_fma_f32 v117, -v99, v116, 1.0
	v_fmac_f32_e32 v116, v117, v116
	v_div_scale_f32 v117, vcc, v159, v98, v159
	v_mul_f32_e32 v118, v117, v116
	v_fma_f32 v119, -v99, v118, v117
	v_fmac_f32_e32 v118, v119, v116
	v_fma_f32 v99, -v99, v118, v117
	v_div_fmas_f32 v99, v99, v116, v118
	v_div_fixup_f32 v98, v99, v98, v159
	v_add_f32_e32 v98, v93, v98
	v_cmp_gt_f32_e32 vcc, s37, v98
	s_nop 1
	v_cndmask_b32_e64 v99, 0, 32, vcc
	v_ldexp_f32 v98, v98, v99
	v_log_f32_e32 v98, v98
	s_nop 0
	v_mul_f32_e32 v99, 0x3f317217, v98
	v_fma_f32 v99, v98, s33, -v99
	v_fmac_f32_e32 v99, 0x3377d1cf, v98
	v_fmac_f32_e32 v99, 0x3f317217, v98
	v_cmp_lt_f32_e64 s[60:61], |v98|, s36
	s_nop 1
	v_cndmask_b32_e64 v98, v98, v99, s[60:61]
	v_cndmask_b32_e32 v99, 0, v216, vcc
	v_sub_f32_e32 v189, v98, v99
	v_mul_f32_e64 v99, |v100|, s8
	v_exp_f32_e32 v99, v99
	v_max_f32_e32 v98, v100, v100
	v_min_f32_e32 v98, 0, v98
	v_add_f32_e32 v99, 1.0, v99
	v_cmp_gt_f32_e32 vcc, s37, v99
	s_nop 1
	v_cndmask_b32_e64 v116, 0, 32, vcc
	v_ldexp_f32 v99, v99, v116
	v_log_f32_e32 v99, v99
	s_nop 0
	v_mul_f32_e32 v116, 0x3f317217, v99
	v_fma_f32 v116, v99, s33, -v116
	v_fmac_f32_e32 v116, 0x3377d1cf, v99
	v_fmac_f32_e32 v116, 0x3f317217, v99
	v_cmp_lt_f32_e64 s[60:61], |v99|, s36
	s_nop 1
	v_cndmask_b32_e64 v99, v99, v116, s[60:61]
	v_cndmask_b32_e32 v116, 0, v216, vcc
	v_sub_f32_e32 v116, v99, v116
	v_mul_f32_e32 v99, 0xbfb8aa3b, v100
	v_exp_f32_e32 v99, v99
	s_nop 0
	v_add_f32_e32 v99, 1.0, v99
	v_div_scale_f32 v100, s[2:3], v99, v99, v161
	v_rcp_f32_e32 v117, v100
	s_nop 0
	v_fma_f32 v118, -v100, v117, 1.0
	v_fmac_f32_e32 v117, v118, v117
	v_div_scale_f32 v118, vcc, v161, v99, v161
	v_mul_f32_e32 v119, v118, v117
	v_fma_f32 v120, -v100, v119, v118
	v_fmac_f32_e32 v119, v120, v117
	v_fma_f32 v100, -v100, v119, v118
	v_div_fmas_f32 v100, v100, v117, v119
	v_div_fixup_f32 v99, v100, v99, v161
	v_add_f32_e32 v99, v94, v99
	v_cmp_gt_f32_e32 vcc, s37, v99
	s_nop 1
	v_cndmask_b32_e64 v100, 0, 32, vcc
	v_ldexp_f32 v99, v99, v100
	v_log_f32_e32 v99, v99
	s_nop 0
	v_mul_f32_e32 v100, 0x3f317217, v99
	v_fma_f32 v100, v99, s33, -v100
	v_fmac_f32_e32 v100, 0x3377d1cf, v99
	v_fmac_f32_e32 v100, 0x3f317217, v99
	v_cmp_lt_f32_e64 s[60:61], |v99|, s36
	s_nop 1
	v_cndmask_b32_e64 v99, v99, v100, s[60:61]
	v_cndmask_b32_e32 v100, 0, v216, vcc
	v_sub_f32_e32 v190, v99, v100
	v_mul_f32_e64 v100, |v101|, s8
	v_exp_f32_e32 v100, v100
	v_max_f32_e32 v99, v101, v101
	v_min_f32_e32 v99, 0, v99
	v_add_f32_e32 v100, 1.0, v100
	v_cmp_gt_f32_e32 vcc, s37, v100
	s_nop 1
	v_cndmask_b32_e64 v117, 0, 32, vcc
	v_ldexp_f32 v100, v100, v117
	v_log_f32_e32 v100, v100
	s_nop 0
	v_mul_f32_e32 v117, 0x3f317217, v100
	v_fma_f32 v117, v100, s33, -v117
	v_fmac_f32_e32 v117, 0x3377d1cf, v100
	v_fmac_f32_e32 v117, 0x3f317217, v100
	v_cmp_lt_f32_e64 s[60:61], |v100|, s36
	s_nop 1
	v_cndmask_b32_e64 v100, v100, v117, s[60:61]
	v_cndmask_b32_e32 v117, 0, v216, vcc
	v_sub_f32_e32 v117, v100, v117
	v_mul_f32_e32 v100, 0xbfb8aa3b, v101
	v_exp_f32_e32 v100, v100
	s_nop 0
	v_add_f32_e32 v100, 1.0, v100
	v_div_scale_f32 v101, s[2:3], v100, v100, v163
	v_rcp_f32_e32 v118, v101
	s_nop 0
	v_fma_f32 v119, -v101, v118, 1.0
	v_fmac_f32_e32 v118, v119, v118
	v_div_scale_f32 v119, vcc, v163, v100, v163
	v_mul_f32_e32 v120, v119, v118
	v_fma_f32 v121, -v101, v120, v119
	v_fmac_f32_e32 v120, v121, v118
	v_fma_f32 v101, -v101, v120, v119
; __device__ __forceinline__ float log_forget(float z, float lb) {
;   const float r0 = fminf(z, 0.f) - __logf(1.f + __expf(-fabsf(z)));
;   const float r1 = __logf(lb + (1.f - lb) / (1.f + __expf(-z)));
;   return lb <= 0.f ? r0 : r1;
; }
	v_div_fmas_f32 v101, v101, v118, v120
	v_div_fixup_f32 v100, v101, v100, v163
	v_add_f32_e32 v100, v95, v100
	v_cmp_gt_f32_e32 vcc, s37, v100
	s_nop 1
	v_cndmask_b32_e64 v101, 0, 32, vcc
	v_ldexp_f32 v100, v100, v101
	v_log_f32_e32 v100, v100
	s_nop 0
	v_mul_f32_e32 v101, 0x3f317217, v100
	v_fma_f32 v101, v100, s33, -v101
	v_fmac_f32_e32 v101, 0x3377d1cf, v100
	v_fmac_f32_e32 v101, 0x3f317217, v100
	v_cmp_lt_f32_e64 s[60:61], |v100|, s36
	s_nop 1
	v_cndmask_b32_e64 v100, v100, v101, s[60:61]
	v_cndmask_b32_e32 v101, 0, v216, vcc
	v_sub_f32_e32 v191, v100, v101
	v_mul_f32_e64 v101, |v88|, s8
	v_exp_f32_e32 v101, v101
	v_max_f32_e32 v100, v88, v88
	v_mul_f32_e32 v88, 0xbfb8aa3b, v88
	v_exp_f32_e32 v88, v88
	v_add_f32_e32 v101, 1.0, v101
	v_cmp_gt_f32_e32 vcc, s37, v101
	v_min_f32_e32 v100, 0, v100
	v_add_f32_e32 v88, 1.0, v88
	v_cndmask_b32_e64 v118, 0, 32, vcc
	v_ldexp_f32 v101, v101, v118
	v_log_f32_e32 v101, v101
	s_nop 0
	v_mul_f32_e32 v118, 0x3f317217, v101
	v_fma_f32 v118, v101, s33, -v118
	v_fmac_f32_e32 v118, 0x3377d1cf, v101
	v_fmac_f32_e32 v118, 0x3f317217, v101
	v_cmp_lt_f32_e64 s[60:61], |v101|, s36
	s_nop 1
	v_cndmask_b32_e64 v101, v101, v118, s[60:61]
	v_cndmask_b32_e32 v118, 0, v216, vcc
	v_sub_f32_e32 v118, v101, v118
	v_div_scale_f32 v101, s[2:3], v88, v88, v157
	v_rcp_f32_e32 v119, v101
	s_nop 0
	v_fma_f32 v120, -v101, v119, 1.0
	v_fmac_f32_e32 v119, v120, v119
	v_div_scale_f32 v120, vcc, v157, v88, v157
	v_mul_f32_e32 v121, v120, v119
	v_fma_f32 v168, -v101, v121, v120
	v_fmac_f32_e32 v121, v168, v119
	v_fma_f32 v101, -v101, v121, v120
	v_div_fmas_f32 v101, v101, v119, v121
	v_div_fixup_f32 v88, v101, v88, v157
	v_add_f32_e32 v88, v92, v88
	v_cmp_gt_f32_e32 vcc, s37, v88
	s_nop 1
	v_cndmask_b32_e64 v101, 0, 32, vcc
	v_ldexp_f32 v88, v88, v101
	v_log_f32_e32 v88, v88
	s_nop 0
	v_mul_f32_e32 v101, 0x3f317217, v88
	v_fma_f32 v101, v88, s33, -v101
	v_fmac_f32_e32 v101, 0x3377d1cf, v88
	v_fmac_f32_e32 v101, 0x3f317217, v88
	v_cmp_lt_f32_e64 s[60:61], |v88|, s36
	s_nop 1
	v_cndmask_b32_e64 v88, v88, v101, s[60:61]
	v_cndmask_b32_e32 v101, 0, v216, vcc
	v_sub_f32_e32 v192, v88, v101
	v_max_f32_e32 v88, v89, v89
	v_min_f32_e32 v101, 0, v88
	v_mul_f32_e64 v88, |v89|, s8
	v_exp_f32_e32 v88, v88
	s_nop 0
	v_add_f32_e32 v88, 1.0, v88
	v_cmp_gt_f32_e32 vcc, s37, v88
	s_nop 1
	v_cndmask_b32_e64 v119, 0, 32, vcc
	v_ldexp_f32 v88, v88, v119
	v_log_f32_e32 v88, v88
	s_nop 0
	v_mul_f32_e32 v119, 0x3f317217, v88
	v_fma_f32 v119, v88, s33, -v119
	v_fmac_f32_e32 v119, 0x3377d1cf, v88
	v_fmac_f32_e32 v119, 0x3f317217, v88
	v_cmp_lt_f32_e64 s[60:61], |v88|, s36
	s_nop 1
	v_cndmask_b32_e64 v88, v88, v119, s[60:61]
	v_cndmask_b32_e32 v119, 0, v216, vcc
	v_sub_f32_e32 v119, v88, v119
	v_mul_f32_e32 v88, 0xbfb8aa3b, v89
	v_exp_f32_e32 v88, v88
	v_pk_add_f32 v[100:101], v[100:101], v[118:119] neg_lo:[0,1] neg_hi:[0,1]
	v_add_f32_e32 v88, 1.0, v88
	v_div_scale_f32 v89, s[2:3], v88, v88, v159
	v_rcp_f32_e32 v120, v89
	v_cndmask_b32_e64 v100, v192, v100, s[44:45]
	v_fma_f32 v121, -v89, v120, 1.0
	v_fmac_f32_e32 v120, v121, v120
	v_div_scale_f32 v121, vcc, v159, v88, v159
	v_mul_f32_e32 v168, v121, v120
	v_fma_f32 v169, -v89, v168, v121
	v_fmac_f32_e32 v168, v169, v120
	v_fma_f32 v89, -v89, v168, v121
	v_div_fmas_f32 v89, v89, v120, v168
	v_div_fixup_f32 v88, v89, v88, v159
	v_add_f32_e32 v88, v93, v88
	v_cmp_gt_f32_e32 vcc, s37, v88
	s_nop 1
	v_cndmask_b32_e64 v89, 0, 32, vcc
	v_ldexp_f32 v88, v88, v89
	v_log_f32_e32 v88, v88
	s_nop 0
	v_mul_f32_e32 v89, 0x3f317217, v88
	v_fma_f32 v89, v88, s33, -v89
	v_fmac_f32_e32 v89, 0x3377d1cf, v88
	v_fmac_f32_e32 v89, 0x3f317217, v88
	v_cmp_lt_f32_e64 s[60:61], |v88|, s36
	s_nop 1
	v_cndmask_b32_e64 v88, v88, v89, s[60:61]
	v_cndmask_b32_e32 v89, 0, v216, vcc
	v_sub_f32_e32 v193, v88, v89
	v_max_f32_e32 v88, v90, v90
	v_min_f32_e32 v120, 0, v88
	v_mul_f32_e64 v88, |v90|, s8
	v_exp_f32_e32 v88, v88
	v_cndmask_b32_e64 v101, v193, v101, s[46:47]
	v_add_f32_e32 v88, 1.0, v88
	v_cmp_gt_f32_e32 vcc, s37, v88
	s_nop 1
	v_cndmask_b32_e64 v89, 0, 32, vcc
	v_ldexp_f32 v88, v88, v89
	v_log_f32_e32 v88, v88
	s_nop 0
	v_mul_f32_e32 v89, 0x3f317217, v88
	v_fma_f32 v89, v88, s33, -v89
	v_fmac_f32_e32 v89, 0x3377d1cf, v88
	v_fmac_f32_e32 v89, 0x3f317217, v88
	v_cmp_lt_f32_e64 s[60:61], |v88|, s36
	s_nop 1
	v_cndmask_b32_e64 v88, v88, v89, s[60:61]
	v_cndmask_b32_e32 v89, 0, v216, vcc
	v_sub_f32_e32 v168, v88, v89
	v_mul_f32_e32 v88, 0xbfb8aa3b, v90
	v_exp_f32_e32 v88, v88
	s_nop 0
	v_add_f32_e32 v88, 1.0, v88
	v_div_scale_f32 v89, s[2:3], v88, v88, v161
	v_rcp_f32_e32 v90, v89
	s_nop 0
	v_fma_f32 v121, -v89, v90, 1.0
	v_fmac_f32_e32 v90, v121, v90
	v_div_scale_f32 v121, vcc, v161, v88, v161
	v_mul_f32_e32 v169, v121, v90
	v_fma_f32 v170, -v89, v169, v121
	v_fmac_f32_e32 v169, v170, v90
	v_fma_f32 v89, -v89, v169, v121
	v_div_fmas_f32 v89, v89, v90, v169
	v_div_fixup_f32 v88, v89, v88, v161
	v_add_f32_e32 v88, v94, v88
	v_cmp_gt_f32_e32 vcc, s37, v88
	s_nop 1
	v_cndmask_b32_e64 v89, 0, 32, vcc
	v_ldexp_f32 v88, v88, v89
	v_log_f32_e32 v88, v88
	s_nop 0
	v_mul_f32_e32 v89, 0x3f317217, v88
	v_fma_f32 v89, v88, s33, -v89
	v_fmac_f32_e32 v89, 0x3377d1cf, v88
	v_fmac_f32_e32 v89, 0x3f317217, v88
	v_cmp_lt_f32_e64 s[60:61], |v88|, s36
	s_nop 1
	v_cndmask_b32_e64 v88, v88, v89, s[60:61]
	v_cndmask_b32_e32 v89, 0, v216, vcc
	v_sub_f32_e32 v194, v88, v89
	v_max_f32_e32 v88, v91, v91
	v_min_f32_e32 v121, 0, v88
	v_mul_f32_e64 v88, |v91|, s8
	v_exp_f32_e32 v88, v88
	s_nop 0
	v_add_f32_e32 v88, 1.0, v88
	v_cmp_gt_f32_e32 vcc, s37, v88
	s_nop 1
	v_cndmask_b32_e64 v89, 0, 32, vcc
	v_ldexp_f32 v88, v88, v89
	v_log_f32_e32 v88, v88
	s_nop 0
; template <int CTRL> __device__ __forceinline__ float dppx(float v) { return __int_as_float(__builtin_amdgcn_update_dpp(0, __float_as_int(v), CTRL, 0xf, 0xf, true)); }
; __device__ __forceinline__ float log_forget(float z, float lb) {
;   const float r0 = fminf(z, 0.f) - __logf(1.f + __expf(-fabsf(z)));
;   const float r1 = __logf(lb + (1.f - lb) / (1.f + __expf(-z)));
;   return lb <= 0.f ? r0 : r1;
; }
;   __device__ __forceinline__ void operator()(const f32x4 (&acc)[2][2][4][2], const pg8::Unit& u, int wr, int wc, int fr, int fq) const {
;     ...
;               for (int q = 0; q < 4; ++q) { const float gv = log_forget(acc[ai][bj][m][qh][q], lq[q]); g[m][q] = gv;
;                 float sc = gv; sc += dppx<0x111>(sc); sc += dppx<0x112>(sc); sc += dppx<0x114>(sc); sc += dppx<0x118>(sc);
	v_mul_f32_e32 v89, 0x3f317217, v88
	v_fma_f32 v89, v88, s33, -v89
	v_fmac_f32_e32 v89, 0x3377d1cf, v88
	v_fmac_f32_e32 v89, 0x3f317217, v88
	v_cmp_lt_f32_e64 s[60:61], |v88|, s36
	s_nop 1
	v_cndmask_b32_e64 v88, v88, v89, s[60:61]
	v_cndmask_b32_e32 v89, 0, v216, vcc
	v_sub_f32_e32 v169, v88, v89
	v_mul_f32_e32 v88, 0xbfb8aa3b, v91
	v_exp_f32_e32 v88, v88
	s_nop 0
	v_add_f32_e32 v88, 1.0, v88
	v_div_scale_f32 v89, s[2:3], v88, v88, v163
	v_rcp_f32_e32 v90, v89
	s_nop 0
	v_fma_f32 v91, -v89, v90, 1.0
	v_fmac_f32_e32 v90, v91, v90
	v_div_scale_f32 v91, vcc, v163, v88, v163
	v_mul_f32_e32 v170, v91, v90
	v_fma_f32 v171, -v89, v170, v91
	v_fmac_f32_e32 v170, v171, v90
	v_fma_f32 v89, -v89, v170, v91
	v_div_fmas_f32 v89, v89, v90, v170
	v_div_fixup_f32 v88, v89, v88, v163
	v_add_f32_e32 v88, v95, v88
	v_cmp_gt_f32_e32 vcc, s37, v88
	s_nop 1
	v_cndmask_b32_e64 v89, 0, 32, vcc
	v_ldexp_f32 v88, v88, v89
	v_log_f32_e32 v88, v88
	s_nop 0
	v_mul_f32_e32 v89, 0x3f317217, v88
	v_fma_f32 v89, v88, s33, -v89
	v_fmac_f32_e32 v89, 0x3377d1cf, v88
	v_fmac_f32_e32 v89, 0x3f317217, v88
	v_cmp_lt_f32_e64 s[60:61], |v88|, s36
	s_nop 1
	v_cndmask_b32_e64 v88, v88, v89, s[60:61]
	v_cndmask_b32_e32 v89, 0, v216, vcc
	v_sub_f32_e32 v195, v88, v89
	v_max_f32_e32 v88, v84, v84
	v_min_f32_e32 v170, 0, v88
	v_mul_f32_e64 v88, |v84|, s8
	v_exp_f32_e32 v88, v88
	v_mul_f32_e32 v84, 0xbfb8aa3b, v84
	v_exp_f32_e32 v84, v84
	v_add_f32_e32 v88, 1.0, v88
	v_cmp_gt_f32_e32 vcc, s37, v88
	v_add_f32_e32 v84, 1.0, v84
	s_nop 0
	v_cndmask_b32_e64 v89, 0, 32, vcc
	v_ldexp_f32 v88, v88, v89
	v_log_f32_e32 v88, v88
	s_nop 0
	v_mul_f32_e32 v89, 0x3f317217, v88
	v_fma_f32 v89, v88, s33, -v89
	v_fmac_f32_e32 v89, 0x3377d1cf, v88
	v_fmac_f32_e32 v89, 0x3f317217, v88
	v_cmp_lt_f32_e64 s[60:61], |v88|, s36
	s_nop 1
	v_cndmask_b32_e64 v88, v88, v89, s[60:61]
	v_cndmask_b32_e32 v89, 0, v216, vcc
	v_sub_f32_e32 v172, v88, v89
	v_div_scale_f32 v88, s[2:3], v84, v84, v157
	v_rcp_f32_e32 v89, v88
	s_nop 0
	v_fma_f32 v90, -v88, v89, 1.0
	v_fmac_f32_e32 v89, v90, v89
	v_div_scale_f32 v90, vcc, v157, v84, v157
	v_mul_f32_e32 v91, v90, v89
	v_fma_f32 v171, -v88, v91, v90
	v_fmac_f32_e32 v91, v171, v89
	v_fma_f32 v88, -v88, v91, v90
	v_div_fmas_f32 v88, v88, v89, v91
	v_div_fixup_f32 v84, v88, v84, v157
	v_add_f32_e32 v84, v92, v84
	v_cmp_gt_f32_e32 vcc, s37, v84
	s_nop 1
	v_cndmask_b32_e64 v88, 0, 32, vcc
	v_ldexp_f32 v84, v84, v88
	v_log_f32_e32 v84, v84
	s_nop 0
	v_mul_f32_e32 v88, 0x3f317217, v84
	v_fma_f32 v88, v84, s33, -v88
	v_fmac_f32_e32 v88, 0x3377d1cf, v84
	v_fmac_f32_e32 v88, 0x3f317217, v84
	v_cmp_lt_f32_e64 s[60:61], |v84|, s36
	s_nop 1
	v_cndmask_b32_e64 v84, v84, v88, s[60:61]
	v_cndmask_b32_e32 v88, 0, v216, vcc
	v_sub_f32_e32 v157, v84, v88
	v_max_f32_e32 v84, v85, v85
	v_min_f32_e32 v171, 0, v84
	v_mul_f32_e64 v84, |v85|, s8
	v_exp_f32_e32 v84, v84
	s_nop 0
	v_add_f32_e32 v84, 1.0, v84
	v_cmp_gt_f32_e32 vcc, s37, v84
	s_nop 1
	v_cndmask_b32_e64 v88, 0, 32, vcc
	v_ldexp_f32 v84, v84, v88
	v_log_f32_e32 v84, v84
	s_nop 0
	v_mul_f32_e32 v88, 0x3f317217, v84
	v_fma_f32 v88, v84, s33, -v88
	v_fmac_f32_e32 v88, 0x3377d1cf, v84
	v_fmac_f32_e32 v88, 0x3f317217, v84
	v_cmp_lt_f32_e64 s[60:61], |v84|, s36
	s_nop 1
	v_cndmask_b32_e64 v84, v84, v88, s[60:61]
	v_cndmask_b32_e32 v88, 0, v216, vcc
	v_sub_f32_e32 v173, v84, v88
	v_mul_f32_e32 v84, 0xbfb8aa3b, v85
	v_exp_f32_e32 v84, v84
	s_nop 0
	v_add_f32_e32 v84, 1.0, v84
	v_div_scale_f32 v85, s[2:3], v84, v84, v159
	v_rcp_f32_e32 v88, v85
	s_nop 0
	v_fma_f32 v89, -v85, v88, 1.0
	v_fmac_f32_e32 v88, v89, v88
	v_div_scale_f32 v89, vcc, v159, v84, v159
	v_mul_f32_e32 v90, v89, v88
	v_fma_f32 v91, -v85, v90, v89
	v_fmac_f32_e32 v90, v91, v88
	v_fma_f32 v85, -v85, v90, v89
	v_div_fmas_f32 v85, v85, v88, v90
	v_div_fixup_f32 v84, v85, v84, v159
	v_add_f32_e32 v84, v93, v84
	v_cmp_gt_f32_e32 vcc, s37, v84
	v_pk_add_f32 v[92:93], v[112:113], v[114:115] neg_lo:[0,1] neg_hi:[0,1]
	v_ashrrev_i32_e32 v159, 31, v158
	v_cndmask_b32_e64 v85, 0, 32, vcc
	v_ldexp_f32 v84, v84, v85
	v_log_f32_e32 v84, v84
	v_cndmask_b32_e64 v115, v189, v93, s[46:47]
	v_cndmask_b32_e64 v114, v188, v92, s[44:45]
	v_mul_f32_e32 v85, 0x3f317217, v84
	v_fma_f32 v85, v84, s33, -v85
	v_fmac_f32_e32 v85, 0x3377d1cf, v84
	v_fmac_f32_e32 v85, 0x3f317217, v84
	v_cmp_lt_f32_e64 s[60:61], |v84|, s36
	v_mov_b32_dpp v92, v114 row_shr:1 row_mask:0xf bank_mask:0xf bound_ctrl:1
	v_mov_b32_dpp v93, v115 row_shr:1 row_mask:0xf bank_mask:0xf bound_ctrl:1
	v_cndmask_b32_e64 v84, v84, v85, s[60:61]
	v_cndmask_b32_e32 v85, 0, v216, vcc
	v_sub_f32_e32 v196, v84, v85
	v_max_f32_e32 v84, v86, v86
	v_min_f32_e32 v174, 0, v84
	v_mul_f32_e64 v84, |v86|, s8
	v_exp_f32_e32 v84, v84
	v_pk_add_f32 v[92:93], v[114:115], v[92:93]
	v_add_f32_e32 v84, 1.0, v84
	v_cmp_gt_f32_e32 vcc, s37, v84
	s_nop 1
	v_cndmask_b32_e64 v85, 0, 32, vcc
	v_ldexp_f32 v84, v84, v85
	v_log_f32_e32 v84, v84
	s_nop 0
	v_mul_f32_e32 v85, 0x3f317217, v84
	v_fma_f32 v85, v84, s33, -v85
	v_fmac_f32_e32 v85, 0x3377d1cf, v84
	v_fmac_f32_e32 v85, 0x3f317217, v84
	v_cmp_lt_f32_e64 s[60:61], |v84|, s36
	s_nop 1
	v_cndmask_b32_e64 v84, v84, v85, s[60:61]
	v_cndmask_b32_e32 v85, 0, v216, vcc
	v_sub_f32_e32 v176, v84, v85
	v_mul_f32_e32 v84, 0xbfb8aa3b, v86
	v_exp_f32_e32 v84, v84
	s_nop 0
	v_add_f32_e32 v84, 1.0, v84
	v_div_scale_f32 v85, s[2:3], v84, v84, v161
	v_rcp_f32_e32 v86, v85
	s_nop 0
	v_fma_f32 v88, -v85, v86, 1.0
	v_fmac_f32_e32 v86, v88, v86
	v_div_scale_f32 v88, vcc, v161, v84, v161
	v_mul_f32_e32 v89, v88, v86
	v_fma_f32 v90, -v85, v89, v88
	v_fmac_f32_e32 v89, v90, v86
	v_fma_f32 v85, -v85, v89, v88
	v_div_fmas_f32 v85, v85, v86, v89
; template <int CTRL> __device__ __forceinline__ float dppx(float v) { return __int_as_float(__builtin_amdgcn_update_dpp(0, __float_as_int(v), CTRL, 0xf, 0xf, true)); }
; __device__ __forceinline__ float log_forget(float z, float lb) {
;   const float r0 = fminf(z, 0.f) - __logf(1.f + __expf(-fabsf(z)));
;   const float r1 = __logf(lb + (1.f - lb) / (1.f + __expf(-z)));
;   return lb <= 0.f ? r0 : r1;
; }
;   __device__ __forceinline__ void operator()(const f32x4 (&acc)[2][2][4][2], const pg8::Unit& u, int wr, int wc, int fr, int fq) const {
;     ...
;               for (int q = 0; q < 4; ++q) { const float gv = log_forget(acc[ai][bj][m][qh][q], lq[q]); g[m][q] = gv;
;                 float sc = gv; sc += dppx<0x111>(sc); sc += dppx<0x112>(sc); sc += dppx<0x114>(sc); sc += dppx<0x118>(sc);
;                 const float tot16 = __int_as_float(__builtin_amdgcn_ds_swizzle(__float_as_int(sc), 0x1F0));
;                 cs[m][q] = sc + carry[q]; carry[q] += tot16; }
	v_div_fixup_f32 v84, v85, v84, v161
	v_add_f32_e32 v84, v94, v84
	v_cmp_gt_f32_e32 vcc, s37, v84
	v_mov_b32_dpp v94, v92 row_shr:2 row_mask:0xf bank_mask:0xf bound_ctrl:1
	v_ashrrev_i32_e32 v161, 31, v160
	v_cndmask_b32_e64 v85, 0, 32, vcc
	v_ldexp_f32 v84, v84, v85
	v_log_f32_e32 v84, v84
	s_nop 0
	v_mul_f32_e32 v85, 0x3f317217, v84
	v_fma_f32 v85, v84, s33, -v85
	v_fmac_f32_e32 v85, 0x3377d1cf, v84
	v_fmac_f32_e32 v85, 0x3f317217, v84
	v_cmp_lt_f32_e64 s[60:61], |v84|, s36
	s_nop 1
	v_cndmask_b32_e64 v84, v84, v85, s[60:61]
	v_cndmask_b32_e32 v85, 0, v216, vcc
	v_sub_f32_e32 v197, v84, v85
	v_max_f32_e32 v84, v87, v87
	v_min_f32_e32 v175, 0, v84
	v_mul_f32_e64 v84, |v87|, s8
	v_exp_f32_e32 v84, v84
	s_nop 0
	v_add_f32_e32 v84, 1.0, v84
	v_cmp_gt_f32_e32 vcc, s37, v84
	s_nop 1
	v_cndmask_b32_e64 v85, 0, 32, vcc
	v_ldexp_f32 v84, v84, v85
	v_log_f32_e32 v84, v84
	s_nop 0
	v_mul_f32_e32 v85, 0x3f317217, v84
	v_fma_f32 v85, v84, s33, -v85
	v_fmac_f32_e32 v85, 0x3377d1cf, v84
	v_fmac_f32_e32 v85, 0x3f317217, v84
	v_cmp_lt_f32_e64 s[60:61], |v84|, s36
	s_nop 1
	v_cndmask_b32_e64 v84, v84, v85, s[60:61]
	v_cndmask_b32_e32 v85, 0, v216, vcc
	v_sub_f32_e32 v177, v84, v85
	v_mul_f32_e32 v84, 0xbfb8aa3b, v87
	v_exp_f32_e32 v84, v84
	s_nop 0
	v_add_f32_e32 v84, 1.0, v84
	v_div_scale_f32 v85, s[2:3], v84, v84, v163
	v_rcp_f32_e32 v86, v85
	s_nop 0
	v_fma_f32 v87, -v85, v86, 1.0
	v_fmac_f32_e32 v86, v87, v86
	v_div_scale_f32 v87, vcc, v163, v84, v163
	v_mul_f32_e32 v88, v87, v86
	v_fma_f32 v89, -v85, v88, v87
	v_fmac_f32_e32 v88, v89, v86
	v_fma_f32 v85, -v85, v88, v87
	v_div_fmas_f32 v85, v85, v86, v88
	v_div_fixup_f32 v84, v85, v84, v163
	v_add_f32_e32 v84, v95, v84
	v_cmp_gt_f32_e32 vcc, s37, v84
	v_mov_b32_dpp v95, v93 row_shr:2 row_mask:0xf bank_mask:0xf bound_ctrl:1
	v_pk_add_f32 v[92:93], v[92:93], v[94:95]
	v_cndmask_b32_e64 v85, 0, 32, vcc
	v_ldexp_f32 v84, v84, v85
	v_log_f32_e32 v84, v84
	v_mov_b32_dpp v94, v92 row_shr:4 row_mask:0xf bank_mask:0xf bound_ctrl:1
	v_mov_b32_dpp v95, v93 row_shr:4 row_mask:0xf bank_mask:0xf bound_ctrl:1
	v_pk_add_f32 v[92:93], v[92:93], v[94:95]
	v_mul_f32_e32 v85, 0x3f317217, v84
	v_fma_f32 v85, v84, s33, -v85
	v_fmac_f32_e32 v85, 0x3377d1cf, v84
	v_fmac_f32_e32 v85, 0x3f317217, v84
	v_cmp_lt_f32_e64 s[60:61], |v84|, s36
	v_mov_b32_dpp v94, v92 row_shr:8 row_mask:0xf bank_mask:0xf bound_ctrl:1
	v_mov_b32_dpp v95, v93 row_shr:8 row_mask:0xf bank_mask:0xf bound_ctrl:1
	v_cndmask_b32_e64 v84, v84, v85, s[60:61]
	v_cndmask_b32_e32 v85, 0, v216, vcc
	v_sub_f32_e32 v198, v84, v85
	v_pk_add_f32 v[84:85], v[106:107], v[108:109] neg_lo:[0,1] neg_hi:[0,1]
	v_pk_add_f32 v[92:93], v[92:93], v[94:95]
	v_cndmask_b32_e64 v181, v181, v85, s[46:47]
	v_cndmask_b32_e64 v180, v180, v84, s[44:45]
	ds_swizzle_b32 v94, v92 offset:swizzle(BROADCAST,16,15)
	v_mov_b32_dpp v85, v181 row_shr:1 row_mask:0xf bank_mask:0xf bound_ctrl:1
	v_mov_b32_dpp v84, v180 row_shr:1 row_mask:0xf bank_mask:0xf bound_ctrl:1
	v_pk_add_f32 v[84:85], v[180:181], v[84:85]
	ds_swizzle_b32 v95, v93 offset:swizzle(BROADCAST,16,15)
	v_ashrrev_i32_e32 v163, 31, v162
	v_mov_b32_dpp v86, v84 row_shr:2 row_mask:0xf bank_mask:0xf bound_ctrl:1
	v_mov_b32_dpp v87, v85 row_shr:2 row_mask:0xf bank_mask:0xf bound_ctrl:1
	v_pk_add_f32 v[84:85], v[84:85], v[86:87]
	s_nop 1
	v_mov_b32_dpp v86, v84 row_shr:4 row_mask:0xf bank_mask:0xf bound_ctrl:1
	v_mov_b32_dpp v87, v85 row_shr:4 row_mask:0xf bank_mask:0xf bound_ctrl:1
	v_pk_add_f32 v[84:85], v[84:85], v[86:87]
	s_nop 1
	v_mov_b32_dpp v86, v84 row_shr:8 row_mask:0xf bank_mask:0xf bound_ctrl:1
	v_mov_b32_dpp v87, v85 row_shr:8 row_mask:0xf bank_mask:0xf bound_ctrl:1
	v_pk_add_f32 v[84:85], v[84:85], v[86:87]
	ds_swizzle_b32 v86, v84 offset:swizzle(BROADCAST,16,15)
	v_pk_add_f32 v[182:183], v[84:85], 0 op_sel_hi:[1,0]
	v_mul_f32_e32 v84, 0x3fb8aa3b, v180
	v_exp_f32_e32 v84, v84
	ds_swizzle_b32 v87, v85 offset:swizzle(BROADCAST,16,15)
	v_sub_f32_e32 v199, 1.0, v84
	v_mul_f32_e32 v84, 0x3fb8aa3b, v181
	v_exp_f32_e32 v84, v84
	s_waitcnt lgkmcnt(0)
	v_pk_add_f32 v[88:89], v[86:87], 0 op_sel_hi:[1,0]
	v_sub_f32_e32 v200, 1.0, v84
	v_pk_add_f32 v[84:85], v[102:103], v[110:111] neg_lo:[0,1] neg_hi:[0,1]
	v_mov_b32_dpp v110, v100 row_shr:1 row_mask:0xf bank_mask:0xf bound_ctrl:1
	v_cndmask_b32_e64 v185, v105, v85, s[50:51]
	v_cndmask_b32_e64 v184, v104, v84, s[48:49]
	v_mov_b32_dpp v111, v101 row_shr:1 row_mask:0xf bank_mask:0xf bound_ctrl:1
	v_mov_b32_dpp v85, v185 row_shr:1 row_mask:0xf bank_mask:0xf bound_ctrl:1
	v_mov_b32_dpp v84, v184 row_shr:1 row_mask:0xf bank_mask:0xf bound_ctrl:1
	v_pk_add_f32 v[84:85], v[184:185], v[84:85]
	v_pk_add_f32 v[110:111], v[100:101], v[110:111]
	s_nop 0
	v_mov_b32_dpp v86, v84 row_shr:2 row_mask:0xf bank_mask:0xf bound_ctrl:1
	v_mov_b32_dpp v87, v85 row_shr:2 row_mask:0xf bank_mask:0xf bound_ctrl:1
	v_pk_add_f32 v[84:85], v[84:85], v[86:87]
	v_mov_b32_dpp v112, v110 row_shr:2 row_mask:0xf bank_mask:0xf bound_ctrl:1
	v_mov_b32_dpp v113, v111 row_shr:2 row_mask:0xf bank_mask:0xf bound_ctrl:1
	v_mov_b32_dpp v86, v84 row_shr:4 row_mask:0xf bank_mask:0xf bound_ctrl:1
	v_mov_b32_dpp v87, v85 row_shr:4 row_mask:0xf bank_mask:0xf bound_ctrl:1
	v_pk_add_f32 v[84:85], v[84:85], v[86:87]
	v_pk_add_f32 v[110:111], v[110:111], v[112:113]
	s_nop 0
	v_mov_b32_dpp v86, v84 row_shr:8 row_mask:0xf bank_mask:0xf bound_ctrl:1
	v_mov_b32_dpp v87, v85 row_shr:8 row_mask:0xf bank_mask:0xf bound_ctrl:1
	v_pk_add_f32 v[84:85], v[84:85], v[86:87]
	ds_swizzle_b32 v86, v84 offset:swizzle(BROADCAST,16,15)
	v_pk_add_f32 v[186:187], v[84:85], 0 op_sel_hi:[1,0]
	v_mul_f32_e32 v84, 0x3fb8aa3b, v184
	v_exp_f32_e32 v84, v84
	ds_swizzle_b32 v87, v85 offset:swizzle(BROADCAST,16,15)
	v_mov_b32_dpp v112, v110 row_shr:4 row_mask:0xf bank_mask:0xf bound_ctrl:1
	v_mov_b32_dpp v113, v111 row_shr:4 row_mask:0xf bank_mask:0xf bound_ctrl:1
	v_sub_f32_e32 v201, 1.0, v84
	v_mul_f32_e32 v84, 0x3fb8aa3b, v185
	v_exp_f32_e32 v84, v84
	s_waitcnt lgkmcnt(0)
; template <int CTRL> __device__ __forceinline__ float dppx(float v) { return __int_as_float(__builtin_amdgcn_update_dpp(0, __float_as_int(v), CTRL, 0xf, 0xf, true)); }
;   __device__ __forceinline__ void operator()(const f32x4 (&acc)[2][2][4][2], const pg8::Unit& u, int wr, int wc, int fr, int fq) const {
;     ...
;               for (int q = 0; q < 4; ++q) { const float gv = log_forget(acc[ai][bj][m][qh][q], lq[q]); g[m][q] = gv;
;                 float sc = gv; sc += dppx<0x111>(sc); sc += dppx<0x112>(sc); sc += dppx<0x114>(sc); sc += dppx<0x118>(sc);
;                 const float tot16 = __int_as_float(__builtin_amdgcn_ds_swizzle(__float_as_int(sc), 0x1F0));
;                 cs[m][q] = sc + carry[q]; carry[q] += tot16; }
; #pragma unroll
;             for (int m = 0; m < 4; ++m) { const int r = row0 + ai * 128 + m * 16; float bq[4], kq[4];
; #pragma unroll
;               for (int q = 0; q < 4; ++q) { bq[q] = bwd ? (carry[q] - cs[m][q]) + g[m][q] : cs[m][q]; kq[q] = 1.f - __expf(g[m][q]); }
	v_pk_add_f32 v[90:91], v[86:87], 0 op_sel_hi:[1,0]
	v_lshlrev_b64 v[86:87], 11, v[162:163]
	v_pk_add_f32 v[110:111], v[110:111], v[112:113]
	v_sub_f32_e32 v202, 1.0, v84
	v_lshlrev_b64 v[84:85], 12, v[162:163]
	v_pk_add_f32 v[162:163], v[88:89], v[92:93]
	v_pk_add_f32 v[92:93], v[88:89], v[94:95]
	v_mul_f32_e32 v88, 0x3fb8aa3b, v114
	v_exp_f32_e32 v88, v88
	v_mov_b32_dpp v112, v110 row_shr:8 row_mask:0xf bank_mask:0xf bound_ctrl:1
	v_mov_b32_dpp v113, v111 row_shr:8 row_mask:0xf bank_mask:0xf bound_ctrl:1
	v_pk_add_f32 v[110:111], v[110:111], v[112:113]
	v_sub_f32_e32 v203, 1.0, v88
	v_mul_f32_e32 v88, 0x3fb8aa3b, v115
	v_exp_f32_e32 v88, v88
	ds_swizzle_b32 v112, v110 offset:swizzle(BROADCAST,16,15)
	ds_swizzle_b32 v113, v111 offset:swizzle(BROADCAST,16,15)
	v_lshl_add_u64 v[84:85], s[22:23], 0, v[84:85]
	v_sub_f32_e32 v207, 1.0, v88
	v_pk_add_f32 v[88:89], v[98:99], v[116:117] neg_lo:[0,1] neg_hi:[0,1]
	v_lshl_add_u64 v[104:105], v[84:85], 0, v[166:167]
	v_cndmask_b32_e64 v99, v191, v89, s[50:51]
	v_cndmask_b32_e64 v98, v190, v88, s[48:49]
	s_waitcnt lgkmcnt(0)
	v_pk_add_f32 v[118:119], v[92:93], v[112:113]
	v_mov_b32_dpp v89, v99 row_shr:1 row_mask:0xf bank_mask:0xf bound_ctrl:1
	v_mov_b32_dpp v88, v98 row_shr:1 row_mask:0xf bank_mask:0xf bound_ctrl:1
	v_pk_add_f32 v[88:89], v[98:99], v[88:89]
	v_lshl_add_u64 v[86:87], s[0:1], 0, v[86:87]
	v_lshl_add_u64 v[102:103], v[86:87], 0, v[164:165]
	v_mov_b32_dpp v94, v88 row_shr:2 row_mask:0xf bank_mask:0xf bound_ctrl:1
	v_mov_b32_dpp v95, v89 row_shr:2 row_mask:0xf bank_mask:0xf bound_ctrl:1
	v_pk_add_f32 v[88:89], v[88:89], v[94:95]
	s_nop 1
	v_mov_b32_dpp v94, v88 row_shr:4 row_mask:0xf bank_mask:0xf bound_ctrl:1
	v_mov_b32_dpp v95, v89 row_shr:4 row_mask:0xf bank_mask:0xf bound_ctrl:1
	v_pk_add_f32 v[88:89], v[88:89], v[94:95]
	s_nop 1
	v_mov_b32_dpp v94, v88 row_shr:8 row_mask:0xf bank_mask:0xf bound_ctrl:1
	v_mov_b32_dpp v95, v89 row_shr:8 row_mask:0xf bank_mask:0xf bound_ctrl:1
	v_pk_add_f32 v[88:89], v[88:89], v[94:95]
	ds_swizzle_b32 v94, v88 offset:swizzle(BROADCAST,16,15)
	v_pk_add_f32 v[116:117], v[90:91], v[88:89]
	v_mul_f32_e32 v88, 0x3fb8aa3b, v98
	v_exp_f32_e32 v88, v88
	ds_swizzle_b32 v95, v89 offset:swizzle(BROADCAST,16,15)
	v_sub_f32_e32 v208, 1.0, v88
	v_mul_f32_e32 v88, 0x3fb8aa3b, v99
	v_exp_f32_e32 v88, v88
	s_waitcnt lgkmcnt(0)
	v_pk_add_f32 v[94:95], v[90:91], v[94:95]
	v_lshlrev_b64 v[90:91], 11, v[160:161]
	v_lshl_add_u64 v[90:91], s[0:1], 0, v[90:91]
	v_sub_f32_e32 v209, 1.0, v88
	v_lshlrev_b64 v[88:89], 12, v[160:161]
	v_pk_add_f32 v[160:161], v[92:93], v[110:111]
	v_mul_f32_e32 v92, 0x3fb8aa3b, v100
	v_exp_f32_e32 v92, v92
	v_lshl_add_u64 v[88:89], s[22:23], 0, v[88:89]
	v_lshl_add_u64 v[108:109], v[88:89], 0, v[166:167]
	v_lshl_add_u64 v[106:107], v[90:91], 0, v[164:165]
	v_sub_f32_e32 v192, 1.0, v92
	v_mul_f32_e32 v92, 0x3fb8aa3b, v101
	v_exp_f32_e32 v92, v92
	s_nop 0
	v_sub_f32_e32 v193, 1.0, v92
	v_pk_add_f32 v[92:93], v[120:121], v[168:169] neg_lo:[0,1] neg_hi:[0,1]
	s_nop 0
	v_cndmask_b32_e64 v169, v195, v93, s[50:51]
	v_cndmask_b32_e64 v168, v194, v92, s[48:49]
	s_nop 0
	v_mov_b32_dpp v93, v169 row_shr:1 row_mask:0xf bank_mask:0xf bound_ctrl:1
	v_mov_b32_dpp v92, v168 row_shr:1 row_mask:0xf bank_mask:0xf bound_ctrl:1
	v_pk_add_f32 v[92:93], v[168:169], v[92:93]
	s_nop 1
	v_mov_b32_dpp v110, v92 row_shr:2 row_mask:0xf bank_mask:0xf bound_ctrl:1
	v_mov_b32_dpp v111, v93 row_shr:2 row_mask:0xf bank_mask:0xf bound_ctrl:1
	v_pk_add_f32 v[92:93], v[92:93], v[110:111]
	s_nop 1
	v_mov_b32_dpp v110, v92 row_shr:4 row_mask:0xf bank_mask:0xf bound_ctrl:1
	v_mov_b32_dpp v111, v93 row_shr:4 row_mask:0xf bank_mask:0xf bound_ctrl:1
	v_pk_add_f32 v[92:93], v[92:93], v[110:111]
	s_nop 1
	v_mov_b32_dpp v110, v92 row_shr:8 row_mask:0xf bank_mask:0xf bound_ctrl:1
	v_mov_b32_dpp v111, v93 row_shr:8 row_mask:0xf bank_mask:0xf bound_ctrl:1
	v_pk_add_f32 v[92:93], v[92:93], v[110:111]
	ds_swizzle_b32 v110, v92 offset:swizzle(BROADCAST,16,15)
	v_pk_add_f32 v[188:189], v[94:95], v[92:93]
	v_mul_f32_e32 v92, 0x3fb8aa3b, v168
	v_exp_f32_e32 v92, v92
	ds_swizzle_b32 v111, v93 offset:swizzle(BROADCAST,16,15)
	v_sub_f32_e32 v194, 1.0, v92
	v_mul_f32_e32 v92, 0x3fb8aa3b, v169
	v_exp_f32_e32 v92, v92
	s_waitcnt lgkmcnt(0)
	v_pk_add_f32 v[120:121], v[94:95], v[110:111]
	v_lshlrev_b64 v[94:95], 11, v[158:159]
	v_lshl_add_u64 v[94:95], s[0:1], 0, v[94:95]
	v_sub_f32_e32 v195, 1.0, v92
	v_lshlrev_b64 v[92:93], 12, v[158:159]
	v_pk_add_f32 v[158:159], v[170:171], v[172:173] neg_lo:[0,1] neg_hi:[0,1]
	v_lshl_add_u64 v[92:93], s[22:23], 0, v[92:93]
	v_cndmask_b32_e64 v159, v196, v159, s[46:47]
	v_cndmask_b32_e64 v158, v157, v158, s[44:45]
	v_lshl_add_u64 v[110:111], v[92:93], 0, v[166:167]
	v_mov_b32_dpp v171, v159 row_shr:1 row_mask:0xf bank_mask:0xf bound_ctrl:1
	v_mov_b32_dpp v170, v158 row_shr:1 row_mask:0xf bank_mask:0xf bound_ctrl:1
	v_pk_add_f32 v[170:171], v[158:159], v[170:171]
	v_lshl_add_u64 v[112:113], v[94:95], 0, v[164:165]
	v_ashrrev_i32_e32 v157, 31, v156
	v_mov_b32_dpp v172, v170 row_shr:2 row_mask:0xf bank_mask:0xf bound_ctrl:1
	v_mov_b32_dpp v173, v171 row_shr:2 row_mask:0xf bank_mask:0xf bound_ctrl:1
	v_pk_add_f32 v[170:171], v[170:171], v[172:173]
	s_nop 1
	v_mov_b32_dpp v172, v170 row_shr:4 row_mask:0xf bank_mask:0xf bound_ctrl:1
	v_mov_b32_dpp v173, v171 row_shr:4 row_mask:0xf bank_mask:0xf bound_ctrl:1
	v_pk_add_f32 v[170:171], v[170:171], v[172:173]
	s_nop 1
	v_mov_b32_dpp v172, v170 row_shr:8 row_mask:0xf bank_mask:0xf bound_ctrl:1
	v_mov_b32_dpp v173, v171 row_shr:8 row_mask:0xf bank_mask:0xf bound_ctrl:1
	v_pk_add_f32 v[170:171], v[170:171], v[172:173]
	ds_swizzle_b32 v172, v170 offset:swizzle(BROADCAST,16,15)
	ds_swizzle_b32 v173, v171 offset:swizzle(BROADCAST,16,15)
	v_pk_add_f32 v[170:171], v[118:119], v[170:171]
	s_waitcnt lgkmcnt(0)
; __device__ __forceinline__ unsigned cvt_pk_bf16(float lo, float hi) { unsigned r; asm volatile("v_cvt_pk_bf16_f32 %0, %1, %2" : "=v"(r) : "v"(lo), "v"(hi)); return r; }
; __device__ __forceinline__ float log_forget(float z, float lb) {
;   const float r0 = fminf(z, 0.f) - __logf(1.f + __expf(-fabsf(z)));
;   const float r1 = __logf(lb + (1.f - lb) / (1.f + __expf(-z)));
;   return lb <= 0.f ? r0 : r1;
; }
;   __device__ __forceinline__ void operator()(const f32x4 (&acc)[2][2][4][2], const pg8::Unit& u, int wr, int wc, int fr, int fq) const {
;     ...
;             for (int m = 0; m < 4; ++m) { const int r = row0 + ai * 128 + m * 16; float bq[4], kq[4];
; #pragma unroll
;               for (int q = 0; q < 4; ++q) { bq[q] = bwd ? (carry[q] - cs[m][q]) + g[m][q] : cs[m][q]; kq[q] = 1.f - __expf(g[m][q]); }
;               *(f32x4*)(logfp + (size_t)r * 1024 + c + 4 * qh) = (f32x4){bq[0], bq[1], bq[2], bq[3]};
;               u32x2 w; w.x = pg8::cvt_pk_bf16(kq[0], kq[1]); w.y = pg8::cvt_pk_bf16(kq[2], kq[3]);
;               *(u32x2*)(km + (size_t)r * 1024 + c + 4 * qh) = w; } } }
	v_pk_add_f32 v[172:173], v[118:119], v[172:173]
	v_mul_f32_e32 v118, 0x3fb8aa3b, v158
	v_exp_f32_e32 v118, v118
	s_nop 0
	v_sub_f32_e32 v196, 1.0, v118
	v_mul_f32_e32 v118, 0x3fb8aa3b, v159
	v_exp_f32_e32 v118, v118
	s_nop 0
	v_sub_f32_e32 v210, 1.0, v118
	v_pk_add_f32 v[118:119], v[174:175], v[176:177] neg_lo:[0,1] neg_hi:[0,1]
	s_nop 0
	v_cndmask_b32_e64 v175, v198, v119, s[50:51]
	v_cndmask_b32_e64 v174, v197, v118, s[48:49]
	s_nop 0
	v_mov_b32_dpp v119, v175 row_shr:1 row_mask:0xf bank_mask:0xf bound_ctrl:1
	v_mov_b32_dpp v118, v174 row_shr:1 row_mask:0xf bank_mask:0xf bound_ctrl:1
	v_pk_add_f32 v[118:119], v[174:175], v[118:119]
	s_nop 1
	v_mov_b32_dpp v176, v118 row_shr:2 row_mask:0xf bank_mask:0xf bound_ctrl:1
	v_mov_b32_dpp v177, v119 row_shr:2 row_mask:0xf bank_mask:0xf bound_ctrl:1
	v_pk_add_f32 v[118:119], v[118:119], v[176:177]
	s_nop 1
	v_mov_b32_dpp v176, v118 row_shr:4 row_mask:0xf bank_mask:0xf bound_ctrl:1
	v_mov_b32_dpp v177, v119 row_shr:4 row_mask:0xf bank_mask:0xf bound_ctrl:1
	v_pk_add_f32 v[118:119], v[118:119], v[176:177]
	s_nop 1
	v_mov_b32_dpp v176, v118 row_shr:8 row_mask:0xf bank_mask:0xf bound_ctrl:1
	v_mov_b32_dpp v177, v119 row_shr:8 row_mask:0xf bank_mask:0xf bound_ctrl:1
	v_pk_add_f32 v[118:119], v[118:119], v[176:177]
	ds_swizzle_b32 v176, v118 offset:swizzle(BROADCAST,16,15)
	ds_swizzle_b32 v177, v119 offset:swizzle(BROADCAST,16,15)
	v_pk_add_f32 v[190:191], v[120:121], v[118:119]
	v_pk_add_f32 v[118:119], v[172:173], v[182:183] neg_lo:[0,1] neg_hi:[0,1]
	s_waitcnt lgkmcnt(0)
	v_pk_add_f32 v[176:177], v[120:121], v[176:177]
	s_nop 0
	v_pk_add_f32 v[120:121], v[176:177], v[186:187] neg_lo:[0,1] neg_hi:[0,1]
	v_pk_add_f32 v[118:119], v[180:181], v[118:119]
	v_pk_add_f32 v[120:121], v[184:185], v[120:121]
	v_cndmask_b32_e64 v119, v183, v119, s[42:43]
	v_cndmask_b32_e64 v121, v187, v121, s[42:43]
	v_cndmask_b32_e64 v120, v186, v120, s[42:43]
	v_cndmask_b32_e64 v118, v182, v118, s[42:43]
	global_store_dwordx4 v[104:105], v[118:121], off
	s_nop 1
	v_cvt_pk_bf16_f32 v118, v199, v200
	v_cvt_pk_bf16_f32 v119, v201, v202
	global_store_dwordx2 v[102:103], v[118:119], off
	v_pk_add_f32 v[118:119], v[172:173], v[162:163] neg_lo:[0,1] neg_hi:[0,1]
	v_pk_add_f32 v[120:121], v[176:177], v[116:117] neg_lo:[0,1] neg_hi:[0,1]
	v_pk_add_f32 v[114:115], v[114:115], v[118:119]
	v_pk_add_f32 v[98:99], v[98:99], v[120:121]
	v_cndmask_b32_e64 v115, v163, v115, s[42:43]
	v_cndmask_b32_e64 v117, v117, v99, s[42:43]
	v_cndmask_b32_e64 v116, v116, v98, s[42:43]
	v_cndmask_b32_e64 v114, v162, v114, s[42:43]
	global_store_dwordx4 v[108:109], v[114:117], off
	v_cvt_pk_bf16_f32 v98, v203, v207
	v_cvt_pk_bf16_f32 v99, v208, v209
	global_store_dwordx2 v[106:107], v[98:99], off
	v_pk_add_f32 v[98:99], v[172:173], v[160:161] neg_lo:[0,1] neg_hi:[0,1]
	v_pk_add_f32 v[114:115], v[176:177], v[188:189] neg_lo:[0,1] neg_hi:[0,1]
	v_pk_add_f32 v[98:99], v[100:101], v[98:99]
	v_pk_add_f32 v[100:101], v[168:169], v[114:115]
	v_cndmask_b32_e64 v99, v161, v99, s[42:43]
	v_cndmask_b32_e64 v101, v189, v101, s[42:43]
	v_cndmask_b32_e64 v100, v188, v100, s[42:43]
	v_cndmask_b32_e64 v98, v160, v98, s[42:43]
	global_store_dwordx4 v[110:111], v[98:101], off
	s_nop 1
	v_cvt_pk_bf16_f32 v98, v192, v193
	v_cvt_pk_bf16_f32 v99, v194, v195
	global_store_dwordx2 v[112:113], v[98:99], off
	v_mul_f32_e32 v98, 0x3fb8aa3b, v174
	v_exp_f32_e32 v98, v98
	v_pk_add_f32 v[100:101], v[176:177], v[190:191] neg_lo:[0,1] neg_hi:[0,1]
	v_sub_f32_e32 v120, 1.0, v98
	v_pk_add_f32 v[98:99], v[172:173], v[170:171] neg_lo:[0,1] neg_hi:[0,1]
	v_pk_add_f32 v[100:101], v[174:175], v[100:101]
	v_pk_add_f32 v[98:99], v[158:159], v[98:99]
	v_cndmask_b32_e64 v118, v190, v100, s[42:43]
	v_cndmask_b32_e64 v116, v170, v98, s[42:43]
	v_mul_f32_e32 v98, 0x3fb8aa3b, v175
	v_exp_f32_e32 v98, v98
	v_cndmask_b32_e64 v117, v171, v99, s[42:43]
	v_cndmask_b32_e64 v119, v191, v101, s[42:43]
	v_sub_f32_e32 v100, 1.0, v98
	v_lshlrev_b64 v[98:99], 12, v[156:157]
	v_lshl_add_u64 v[98:99], s[22:23], 0, v[98:99]
	v_lshl_add_u64 v[114:115], v[98:99], 0, v[166:167]
	global_store_dwordx4 v[114:115], v[116:119], off
	s_nop 1
	v_cvt_pk_bf16_f32 v118, v196, v210
	v_cvt_pk_bf16_f32 v119, v120, v100
	v_lshlrev_b64 v[100:101], 11, v[156:157]
	v_lshl_add_u64 v[100:101], s[0:1], 0, v[100:101]
	v_lshl_add_u64 v[116:117], v[100:101], 0, v[164:165]
	global_store_dwordx2 v[116:117], v[118:119], off
	v_mul_f32_e64 v119, |v80|, s8
	v_exp_f32_e32 v119, v119
	v_max_f32_e32 v118, v80, v80
	v_mul_f32_e32 v80, 0xbfb8aa3b, v80
	v_exp_f32_e32 v80, v80
	v_add_f32_e32 v119, 1.0, v119
	v_cmp_gt_f32_e32 vcc, s37, v119
	v_min_f32_e32 v118, 0, v118
	v_add_f32_e32 v80, 1.0, v80
	v_cndmask_b32_e64 v120, 0, 32, vcc
	v_ldexp_f32 v119, v119, v120
	v_log_f32_e32 v119, v119
	s_nop 0
	v_mul_f32_e32 v120, 0x3f317217, v119
	v_fma_f32 v120, v119, s33, -v120
	v_fmac_f32_e32 v120, 0x3377d1cf, v119
	v_fmac_f32_e32 v120, 0x3f317217, v119
	v_cmp_lt_f32_e64 s[44:45], |v119|, s36
	s_nop 1
	v_cndmask_b32_e64 v119, v119, v120, s[44:45]
	v_cndmask_b32_e32 v120, 0, v216, vcc
	v_sub_f32_e32 v120, v119, v120
	v_div_scale_f32 v119, s[2:3], v80, v80, v206
	v_rcp_f32_e32 v121, v119
	s_nop 0
	v_fma_f32 v156, -v119, v121, 1.0
	v_fmac_f32_e32 v121, v156, v121
	v_div_scale_f32 v156, vcc, v206, v80, v206
	v_mul_f32_e32 v157, v156, v121
	v_fma_f32 v158, -v119, v157, v156
	v_fmac_f32_e32 v157, v158, v121
	v_fma_f32 v119, -v119, v157, v156
	v_div_fmas_f32 v119, v119, v121, v157
	v_div_fixup_f32 v80, v119, v80, v206
	v_add_f32_e32 v80, v72, v80
	v_cmp_gt_f32_e32 vcc, s37, v80
	s_nop 1
	v_cndmask_b32_e64 v119, 0, 32, vcc
	v_ldexp_f32 v80, v80, v119
	v_log_f32_e32 v80, v80
; __device__ __forceinline__ float log_forget(float z, float lb) {
;   const float r0 = fminf(z, 0.f) - __logf(1.f + __expf(-fabsf(z)));
;   const float r1 = __logf(lb + (1.f - lb) / (1.f + __expf(-z)));
;   return lb <= 0.f ? r0 : r1;
; }
	s_nop 0
	v_mul_f32_e32 v119, 0x3f317217, v80
	v_fma_f32 v119, v80, s33, -v119
	v_fmac_f32_e32 v119, 0x3377d1cf, v80
	v_fmac_f32_e32 v119, 0x3f317217, v80
	v_cmp_lt_f32_e64 s[44:45], |v80|, s36
	s_nop 1
	v_cndmask_b32_e64 v80, v80, v119, s[44:45]
	v_cndmask_b32_e32 v119, 0, v216, vcc
	v_sub_f32_e32 v168, v80, v119
	v_max_f32_e32 v80, v81, v81
	v_min_f32_e32 v119, 0, v80
	v_mul_f32_e64 v80, |v81|, s8
	v_exp_f32_e32 v80, v80
	s_nop 0
	v_add_f32_e32 v80, 1.0, v80
	v_cmp_gt_f32_e32 vcc, s37, v80
	s_nop 1
	v_cndmask_b32_e64 v121, 0, 32, vcc
	v_ldexp_f32 v80, v80, v121
	v_log_f32_e32 v80, v80
	s_nop 0
	v_mul_f32_e32 v121, 0x3f317217, v80
	v_fma_f32 v121, v80, s33, -v121
	v_fmac_f32_e32 v121, 0x3377d1cf, v80
	v_fmac_f32_e32 v121, 0x3f317217, v80
	v_cmp_lt_f32_e64 s[44:45], |v80|, s36
	s_nop 1
	v_cndmask_b32_e64 v80, v80, v121, s[44:45]
	v_cndmask_b32_e32 v121, 0, v216, vcc
	v_sub_f32_e32 v121, v80, v121
	v_mul_f32_e32 v80, 0xbfb8aa3b, v81
	v_exp_f32_e32 v80, v80
	s_nop 0
	v_add_f32_e32 v80, 1.0, v80
	v_div_scale_f32 v81, s[2:3], v80, v80, v205
	v_rcp_f32_e32 v156, v81
	s_nop 0
	v_fma_f32 v157, -v81, v156, 1.0
	v_fmac_f32_e32 v156, v157, v156
	v_div_scale_f32 v157, vcc, v205, v80, v205
	v_mul_f32_e32 v158, v157, v156
	v_fma_f32 v159, -v81, v158, v157
	v_fmac_f32_e32 v158, v159, v156
	v_fma_f32 v81, -v81, v158, v157
	v_div_fmas_f32 v81, v81, v156, v158
	v_div_fixup_f32 v80, v81, v80, v205
	v_add_f32_e32 v80, v73, v80
	v_cmp_gt_f32_e32 vcc, s37, v80
	s_nop 1
	v_cndmask_b32_e64 v81, 0, 32, vcc
	v_ldexp_f32 v80, v80, v81
	v_log_f32_e32 v80, v80
	s_nop 0
	v_mul_f32_e32 v81, 0x3f317217, v80
	v_fma_f32 v81, v80, s33, -v81
	v_fmac_f32_e32 v81, 0x3377d1cf, v80
	v_fmac_f32_e32 v81, 0x3f317217, v80
	v_cmp_lt_f32_e64 s[44:45], |v80|, s36
	s_nop 1
	v_cndmask_b32_e64 v80, v80, v81, s[44:45]
	v_cndmask_b32_e32 v81, 0, v216, vcc
	v_sub_f32_e32 v169, v80, v81
	v_mul_f32_e64 v81, |v82|, s8
	v_exp_f32_e32 v81, v81
	v_max_f32_e32 v80, v82, v82
	v_min_f32_e32 v80, 0, v80
	v_add_f32_e32 v81, 1.0, v81
	v_cmp_gt_f32_e32 vcc, s37, v81
	s_nop 1
	v_cndmask_b32_e64 v156, 0, 32, vcc
	v_ldexp_f32 v81, v81, v156
	v_log_f32_e32 v81, v81
	s_nop 0
	v_mul_f32_e32 v156, 0x3f317217, v81
	v_fma_f32 v156, v81, s33, -v156
	v_fmac_f32_e32 v156, 0x3377d1cf, v81
	v_fmac_f32_e32 v156, 0x3f317217, v81
	v_cmp_lt_f32_e64 s[44:45], |v81|, s36
	s_nop 1
	v_cndmask_b32_e64 v81, v81, v156, s[44:45]
	v_cndmask_b32_e32 v156, 0, v216, vcc
	v_sub_f32_e32 v156, v81, v156
	v_mul_f32_e32 v81, 0xbfb8aa3b, v82
	v_exp_f32_e32 v81, v81
	s_nop 0
	v_add_f32_e32 v81, 1.0, v81
	v_div_scale_f32 v82, s[2:3], v81, v81, v204
	v_rcp_f32_e32 v157, v82
	s_nop 0
	v_fma_f32 v158, -v82, v157, 1.0
	v_fmac_f32_e32 v157, v158, v157
	v_div_scale_f32 v158, vcc, v204, v81, v204
	v_mul_f32_e32 v159, v158, v157
	v_fma_f32 v160, -v82, v159, v158
	v_fmac_f32_e32 v159, v160, v157
	v_fma_f32 v82, -v82, v159, v158
	v_div_fmas_f32 v82, v82, v157, v159
	v_div_fixup_f32 v81, v82, v81, v204
	v_add_f32_e32 v81, v74, v81
	v_cmp_gt_f32_e32 vcc, s37, v81
	s_nop 1
	v_cndmask_b32_e64 v82, 0, 32, vcc
	v_ldexp_f32 v81, v81, v82
	v_log_f32_e32 v81, v81
	s_nop 0
	v_mul_f32_e32 v82, 0x3f317217, v81
	v_fma_f32 v82, v81, s33, -v82
	v_fmac_f32_e32 v82, 0x3377d1cf, v81
	v_fmac_f32_e32 v82, 0x3f317217, v81
	v_cmp_lt_f32_e64 s[44:45], |v81|, s36
	s_nop 1
	v_cndmask_b32_e64 v81, v81, v82, s[44:45]
	v_cndmask_b32_e32 v82, 0, v216, vcc
	v_sub_f32_e32 v170, v81, v82
	v_mul_f32_e64 v82, |v83|, s8
	v_exp_f32_e32 v82, v82
	v_max_f32_e32 v81, v83, v83
	v_min_f32_e32 v81, 0, v81
	v_add_f32_e32 v82, 1.0, v82
	v_cmp_gt_f32_e32 vcc, s37, v82
	s_nop 1
	v_cndmask_b32_e64 v157, 0, 32, vcc
	v_ldexp_f32 v82, v82, v157
	v_log_f32_e32 v82, v82
	s_nop 0
	v_mul_f32_e32 v157, 0x3f317217, v82
	v_fma_f32 v157, v82, s33, -v157
	v_fmac_f32_e32 v157, 0x3377d1cf, v82
	v_fmac_f32_e32 v157, 0x3f317217, v82
	v_cmp_lt_f32_e64 s[44:45], |v82|, s36
	s_nop 1
	v_cndmask_b32_e64 v82, v82, v157, s[44:45]
	v_cndmask_b32_e32 v157, 0, v216, vcc
	v_sub_f32_e32 v157, v82, v157
	v_mul_f32_e32 v82, 0xbfb8aa3b, v83
	v_exp_f32_e32 v82, v82
	v_pk_add_f32 v[80:81], v[80:81], v[156:157] neg_lo:[0,1] neg_hi:[0,1]
	v_add_f32_e32 v82, 1.0, v82
	v_div_scale_f32 v83, s[2:3], v82, v82, v96
	v_rcp_f32_e32 v158, v83
	v_cndmask_b32_e64 v80, v170, v80, s[56:57]
	v_fma_f32 v159, -v83, v158, 1.0
	v_fmac_f32_e32 v158, v159, v158
	v_div_scale_f32 v159, vcc, v96, v82, v96
	v_mul_f32_e32 v160, v159, v158
	v_fma_f32 v161, -v83, v160, v159
	v_fmac_f32_e32 v160, v161, v158
	v_fma_f32 v83, -v83, v160, v159
	v_div_fmas_f32 v83, v83, v158, v160
	v_div_fixup_f32 v82, v83, v82, v96
	v_add_f32_e32 v82, v75, v82
	v_cmp_gt_f32_e32 vcc, s37, v82
	s_nop 1
	v_cndmask_b32_e64 v83, 0, 32, vcc
	v_ldexp_f32 v82, v82, v83
	v_log_f32_e32 v82, v82
	s_nop 0
	v_mul_f32_e32 v83, 0x3f317217, v82
	v_fma_f32 v83, v82, s33, -v83
	v_fmac_f32_e32 v83, 0x3377d1cf, v82
	v_fmac_f32_e32 v83, 0x3f317217, v82
	v_cmp_lt_f32_e64 s[44:45], |v82|, s36
	s_nop 1
	v_cndmask_b32_e64 v82, v82, v83, s[44:45]
	v_cndmask_b32_e32 v83, 0, v216, vcc
	v_sub_f32_e32 v171, v82, v83
	v_mul_f32_e64 v83, |v76|, s8
	v_exp_f32_e32 v83, v83
	v_max_f32_e32 v82, v76, v76
	v_mul_f32_e32 v76, 0xbfb8aa3b, v76
	v_exp_f32_e32 v76, v76
	v_add_f32_e32 v83, 1.0, v83
	v_cmp_gt_f32_e32 vcc, s37, v83
	v_cndmask_b32_e64 v81, v171, v81, s[58:59]
	v_add_f32_e32 v76, 1.0, v76
	v_cndmask_b32_e64 v158, 0, 32, vcc
	v_ldexp_f32 v83, v83, v158
	v_log_f32_e32 v83, v83
	v_min_f32_e32 v82, 0, v82
	v_mul_f32_e32 v158, 0x3f317217, v83
	v_fma_f32 v158, v83, s33, -v158
	v_fmac_f32_e32 v158, 0x3377d1cf, v83
	v_fmac_f32_e32 v158, 0x3f317217, v83
	v_cmp_lt_f32_e64 s[44:45], |v83|, s36
	s_nop 1
; __device__ __forceinline__ float log_forget(float z, float lb) {
;   const float r0 = fminf(z, 0.f) - __logf(1.f + __expf(-fabsf(z)));
;   const float r1 = __logf(lb + (1.f - lb) / (1.f + __expf(-z)));
;   return lb <= 0.f ? r0 : r1;
; }
	v_cndmask_b32_e64 v83, v83, v158, s[44:45]
	v_cndmask_b32_e32 v158, 0, v216, vcc
	v_sub_f32_e32 v158, v83, v158
	v_div_scale_f32 v83, s[2:3], v76, v76, v206
	v_rcp_f32_e32 v159, v83
	s_nop 0
	v_fma_f32 v160, -v83, v159, 1.0
	v_fmac_f32_e32 v159, v160, v159
	v_div_scale_f32 v160, vcc, v206, v76, v206
	v_mul_f32_e32 v161, v160, v159
	v_fma_f32 v162, -v83, v161, v160
	v_fmac_f32_e32 v161, v162, v159
	v_fma_f32 v83, -v83, v161, v160
	v_div_fmas_f32 v83, v83, v159, v161
	v_div_fixup_f32 v76, v83, v76, v206
	v_add_f32_e32 v76, v72, v76
	v_cmp_gt_f32_e32 vcc, s37, v76
	s_nop 1
	v_cndmask_b32_e64 v83, 0, 32, vcc
	v_ldexp_f32 v76, v76, v83
	v_log_f32_e32 v76, v76
	s_nop 0
	v_mul_f32_e32 v83, 0x3f317217, v76
	v_fma_f32 v83, v76, s33, -v83
	v_fmac_f32_e32 v83, 0x3377d1cf, v76
	v_fmac_f32_e32 v83, 0x3f317217, v76
	v_cmp_lt_f32_e64 s[44:45], |v76|, s36
	s_nop 1
	v_cndmask_b32_e64 v76, v76, v83, s[44:45]
	v_cndmask_b32_e32 v83, 0, v216, vcc
	v_sub_f32_e32 v172, v76, v83
	v_max_f32_e32 v76, v77, v77
	v_min_f32_e32 v83, 0, v76
	v_mul_f32_e64 v76, |v77|, s8
	v_exp_f32_e32 v76, v76
	s_nop 0
	v_add_f32_e32 v76, 1.0, v76
	v_cmp_gt_f32_e32 vcc, s37, v76
	s_nop 1
	v_cndmask_b32_e64 v159, 0, 32, vcc
	v_ldexp_f32 v76, v76, v159
	v_log_f32_e32 v76, v76
	s_nop 0
	v_mul_f32_e32 v159, 0x3f317217, v76
	v_fma_f32 v159, v76, s33, -v159
	v_fmac_f32_e32 v159, 0x3377d1cf, v76
	v_fmac_f32_e32 v159, 0x3f317217, v76
	v_cmp_lt_f32_e64 s[44:45], |v76|, s36
	s_nop 1
	v_cndmask_b32_e64 v76, v76, v159, s[44:45]
	v_cndmask_b32_e32 v159, 0, v216, vcc
	v_sub_f32_e32 v159, v76, v159
	v_mul_f32_e32 v76, 0xbfb8aa3b, v77
	v_exp_f32_e32 v76, v76
	v_pk_add_f32 v[82:83], v[82:83], v[158:159] neg_lo:[0,1] neg_hi:[0,1]
	v_add_f32_e32 v76, 1.0, v76
	v_div_scale_f32 v77, s[2:3], v76, v76, v205
	v_rcp_f32_e32 v160, v77
	v_cndmask_b32_e64 v82, v172, v82, s[52:53]
	v_fma_f32 v161, -v77, v160, 1.0
	v_fmac_f32_e32 v160, v161, v160
	v_div_scale_f32 v161, vcc, v205, v76, v205
	v_mul_f32_e32 v162, v161, v160
	v_fma_f32 v163, -v77, v162, v161
	v_fmac_f32_e32 v162, v163, v160
	v_fma_f32 v77, -v77, v162, v161
	v_div_fmas_f32 v77, v77, v160, v162
	v_div_fixup_f32 v76, v77, v76, v205
	v_add_f32_e32 v76, v73, v76
	v_cmp_gt_f32_e32 vcc, s37, v76
	s_nop 1
	v_cndmask_b32_e64 v77, 0, 32, vcc
	v_ldexp_f32 v76, v76, v77
	v_log_f32_e32 v76, v76
	s_nop 0
	v_mul_f32_e32 v77, 0x3f317217, v76
	v_fma_f32 v77, v76, s33, -v77
	v_fmac_f32_e32 v77, 0x3377d1cf, v76
	v_fmac_f32_e32 v77, 0x3f317217, v76
	v_cmp_lt_f32_e64 s[44:45], |v76|, s36
	s_nop 1
	v_cndmask_b32_e64 v76, v76, v77, s[44:45]
	v_cndmask_b32_e32 v77, 0, v216, vcc
	v_sub_f32_e32 v173, v76, v77
	v_mul_f32_e64 v77, |v78|, s8
	v_exp_f32_e32 v77, v77
	v_max_f32_e32 v76, v78, v78
	v_cndmask_b32_e64 v83, v173, v83, s[54:55]
	v_min_f32_e32 v76, 0, v76
	v_add_f32_e32 v77, 1.0, v77
	v_cmp_gt_f32_e32 vcc, s37, v77
	s_nop 1
	v_cndmask_b32_e64 v160, 0, 32, vcc
	v_ldexp_f32 v77, v77, v160
	v_log_f32_e32 v77, v77
	s_nop 0
	v_mul_f32_e32 v160, 0x3f317217, v77
	v_fma_f32 v160, v77, s33, -v160
	v_fmac_f32_e32 v160, 0x3377d1cf, v77
	v_fmac_f32_e32 v160, 0x3f317217, v77
	v_cmp_lt_f32_e64 s[44:45], |v77|, s36
	s_nop 1
	v_cndmask_b32_e64 v77, v77, v160, s[44:45]
	v_cndmask_b32_e32 v160, 0, v216, vcc
	v_sub_f32_e32 v160, v77, v160
	v_mul_f32_e32 v77, 0xbfb8aa3b, v78
	v_exp_f32_e32 v77, v77
	s_nop 0
	v_add_f32_e32 v77, 1.0, v77
	v_div_scale_f32 v78, s[2:3], v77, v77, v204
	v_rcp_f32_e32 v161, v78
	s_nop 0
	v_fma_f32 v162, -v78, v161, 1.0
	v_fmac_f32_e32 v161, v162, v161
	v_div_scale_f32 v162, vcc, v204, v77, v204
	v_mul_f32_e32 v163, v162, v161
	v_fma_f32 v164, -v78, v163, v162
	v_fmac_f32_e32 v163, v164, v161
	v_fma_f32 v78, -v78, v163, v162
	v_div_fmas_f32 v78, v78, v161, v163
	v_div_fixup_f32 v77, v78, v77, v204
	v_add_f32_e32 v77, v74, v77
	v_cmp_gt_f32_e32 vcc, s37, v77
	s_nop 1
	v_cndmask_b32_e64 v78, 0, 32, vcc
	v_ldexp_f32 v77, v77, v78
	v_log_f32_e32 v77, v77
	s_nop 0
	v_mul_f32_e32 v78, 0x3f317217, v77
	v_fma_f32 v78, v77, s33, -v78
	v_fmac_f32_e32 v78, 0x3377d1cf, v77
	v_fmac_f32_e32 v78, 0x3f317217, v77
	v_cmp_lt_f32_e64 s[44:45], |v77|, s36
	s_nop 1
	v_cndmask_b32_e64 v77, v77, v78, s[44:45]
	v_cndmask_b32_e32 v78, 0, v216, vcc
	v_sub_f32_e32 v174, v77, v78
	v_mul_f32_e64 v78, |v79|, s8
	v_exp_f32_e32 v78, v78
	v_max_f32_e32 v77, v79, v79
	v_min_f32_e32 v77, 0, v77
	v_add_f32_e32 v78, 1.0, v78
	v_cmp_gt_f32_e32 vcc, s37, v78
	s_nop 1
	v_cndmask_b32_e64 v161, 0, 32, vcc
	v_ldexp_f32 v78, v78, v161
	v_log_f32_e32 v78, v78
	s_nop 0
	v_mul_f32_e32 v161, 0x3f317217, v78
	v_fma_f32 v161, v78, s33, -v161
	v_fmac_f32_e32 v161, 0x3377d1cf, v78
	v_fmac_f32_e32 v161, 0x3f317217, v78
	v_cmp_lt_f32_e64 s[44:45], |v78|, s36
	s_nop 1
	v_cndmask_b32_e64 v78, v78, v161, s[44:45]
	v_cndmask_b32_e32 v161, 0, v216, vcc
	v_sub_f32_e32 v161, v78, v161
	v_mul_f32_e32 v78, 0xbfb8aa3b, v79
	v_exp_f32_e32 v78, v78
	v_pk_add_f32 v[76:77], v[76:77], v[160:161] neg_lo:[0,1] neg_hi:[0,1]
	v_add_f32_e32 v78, 1.0, v78
	v_div_scale_f32 v79, s[2:3], v78, v78, v96
	v_rcp_f32_e32 v162, v79
	v_cndmask_b32_e64 v76, v174, v76, s[56:57]
	v_fma_f32 v163, -v79, v162, 1.0
	v_fmac_f32_e32 v162, v163, v162
	v_div_scale_f32 v163, vcc, v96, v78, v96
	v_mul_f32_e32 v164, v163, v162
	v_fma_f32 v165, -v79, v164, v163
	v_fmac_f32_e32 v164, v165, v162
	v_fma_f32 v79, -v79, v164, v163
	v_div_fmas_f32 v79, v79, v162, v164
	v_div_fixup_f32 v78, v79, v78, v96
	v_add_f32_e32 v78, v75, v78
	v_cmp_gt_f32_e32 vcc, s37, v78
	s_nop 1
	v_cndmask_b32_e64 v79, 0, 32, vcc
	v_ldexp_f32 v78, v78, v79
	v_log_f32_e32 v78, v78
	s_nop 0
	v_mul_f32_e32 v79, 0x3f317217, v78
	v_fma_f32 v79, v78, s33, -v79
	v_fmac_f32_e32 v79, 0x3377d1cf, v78
; template <int CTRL> __device__ __forceinline__ float dppx(float v) { return __int_as_float(__builtin_amdgcn_update_dpp(0, __float_as_int(v), CTRL, 0xf, 0xf, true)); }
; __device__ __forceinline__ float log_forget(float z, float lb) {
;   const float r0 = fminf(z, 0.f) - __logf(1.f + __expf(-fabsf(z)));
;   const float r1 = __logf(lb + (1.f - lb) / (1.f + __expf(-z)));
;   return lb <= 0.f ? r0 : r1;
; }
;   __device__ __forceinline__ void operator()(const f32x4 (&acc)[2][2][4][2], const pg8::Unit& u, int wr, int wc, int fr, int fq) const {
;     ...
;               for (int q = 0; q < 4; ++q) { const float gv = log_forget(acc[ai][bj][m][qh][q], lq[q]); g[m][q] = gv;
;                 float sc = gv; sc += dppx<0x111>(sc); sc += dppx<0x112>(sc); sc += dppx<0x114>(sc); sc += dppx<0x118>(sc);
	v_fmac_f32_e32 v79, 0x3f317217, v78
	v_cmp_lt_f32_e64 s[44:45], |v78|, s36
	s_nop 1
	v_cndmask_b32_e64 v78, v78, v79, s[44:45]
	v_cndmask_b32_e32 v79, 0, v216, vcc
	v_sub_f32_e32 v175, v78, v79
	v_mul_f32_e64 v79, |v68|, s8
	v_exp_f32_e32 v79, v79
	v_max_f32_e32 v78, v68, v68
	v_mul_f32_e32 v68, 0xbfb8aa3b, v68
	v_exp_f32_e32 v68, v68
	v_add_f32_e32 v79, 1.0, v79
	v_cmp_gt_f32_e32 vcc, s37, v79
	v_cndmask_b32_e64 v77, v175, v77, s[58:59]
	v_add_f32_e32 v68, 1.0, v68
	v_cndmask_b32_e64 v162, 0, 32, vcc
	v_ldexp_f32 v79, v79, v162
	v_log_f32_e32 v79, v79
	v_min_f32_e32 v78, 0, v78
	v_mul_f32_e32 v162, 0x3f317217, v79
	v_fma_f32 v162, v79, s33, -v162
	v_fmac_f32_e32 v162, 0x3377d1cf, v79
	v_fmac_f32_e32 v162, 0x3f317217, v79
	v_cmp_lt_f32_e64 s[44:45], |v79|, s36
	s_nop 1
	v_cndmask_b32_e64 v79, v79, v162, s[44:45]
	v_cndmask_b32_e32 v162, 0, v216, vcc
	v_sub_f32_e32 v162, v79, v162
	v_div_scale_f32 v79, s[2:3], v68, v68, v206
	v_rcp_f32_e32 v163, v79
	s_nop 0
	v_fma_f32 v164, -v79, v163, 1.0
	v_fmac_f32_e32 v163, v164, v163
	v_div_scale_f32 v164, vcc, v206, v68, v206
	v_mul_f32_e32 v165, v164, v163
	v_fma_f32 v166, -v79, v165, v164
	v_fmac_f32_e32 v165, v166, v163
	v_fma_f32 v79, -v79, v165, v164
	v_div_fmas_f32 v79, v79, v163, v165
	v_div_fixup_f32 v68, v79, v68, v206
	v_add_f32_e32 v68, v72, v68
	v_cmp_gt_f32_e32 vcc, s37, v68
	s_nop 1
	v_cndmask_b32_e64 v79, 0, 32, vcc
	v_ldexp_f32 v68, v68, v79
	v_log_f32_e32 v68, v68
	s_nop 0
	v_mul_f32_e32 v79, 0x3f317217, v68
	v_fma_f32 v79, v68, s33, -v79
	v_fmac_f32_e32 v79, 0x3377d1cf, v68
	v_fmac_f32_e32 v79, 0x3f317217, v68
	v_cmp_lt_f32_e64 s[44:45], |v68|, s36
	s_nop 1
	v_cndmask_b32_e64 v68, v68, v79, s[44:45]
	v_cndmask_b32_e32 v79, 0, v216, vcc
	v_sub_f32_e32 v176, v68, v79
	v_max_f32_e32 v68, v69, v69
	v_min_f32_e32 v79, 0, v68
	v_mul_f32_e64 v68, |v69|, s8
	v_exp_f32_e32 v68, v68
	s_nop 0
	v_add_f32_e32 v68, 1.0, v68
	v_cmp_gt_f32_e32 vcc, s37, v68
	s_nop 1
	v_cndmask_b32_e64 v163, 0, 32, vcc
	v_ldexp_f32 v68, v68, v163
	v_log_f32_e32 v68, v68
	s_nop 0
	v_mul_f32_e32 v163, 0x3f317217, v68
	v_fma_f32 v163, v68, s33, -v163
	v_fmac_f32_e32 v163, 0x3377d1cf, v68
	v_fmac_f32_e32 v163, 0x3f317217, v68
	v_cmp_lt_f32_e64 s[44:45], |v68|, s36
	s_nop 1
	v_cndmask_b32_e64 v68, v68, v163, s[44:45]
	v_cndmask_b32_e32 v163, 0, v216, vcc
	v_sub_f32_e32 v163, v68, v163
	v_mul_f32_e32 v68, 0xbfb8aa3b, v69
	v_exp_f32_e32 v68, v68
	v_pk_add_f32 v[78:79], v[78:79], v[162:163] neg_lo:[0,1] neg_hi:[0,1]
	v_add_f32_e32 v68, 1.0, v68
	v_div_scale_f32 v69, s[2:3], v68, v68, v205
	v_rcp_f32_e32 v164, v69
	v_cndmask_b32_e64 v78, v176, v78, s[52:53]
	v_fma_f32 v165, -v69, v164, 1.0
	v_fmac_f32_e32 v164, v165, v164
	v_div_scale_f32 v165, vcc, v205, v68, v205
	v_mul_f32_e32 v166, v165, v164
	v_fma_f32 v167, -v69, v166, v165
	v_fmac_f32_e32 v166, v167, v164
	v_fma_f32 v69, -v69, v166, v165
	v_div_fmas_f32 v69, v69, v164, v166
	v_div_fixup_f32 v68, v69, v68, v205
	v_add_f32_e32 v68, v73, v68
	v_cmp_gt_f32_e32 vcc, s37, v68
	v_mov_b32_dpp v162, v78 row_shr:1 row_mask:0xf bank_mask:0xf bound_ctrl:1
	s_nop 0
	v_cndmask_b32_e64 v69, 0, 32, vcc
	v_ldexp_f32 v68, v68, v69
	v_log_f32_e32 v68, v68
	s_nop 0
	v_mul_f32_e32 v69, 0x3f317217, v68
	v_fma_f32 v69, v68, s33, -v69
	v_fmac_f32_e32 v69, 0x3377d1cf, v68
	v_fmac_f32_e32 v69, 0x3f317217, v68
	v_cmp_lt_f32_e64 s[44:45], |v68|, s36
	s_nop 1
	v_cndmask_b32_e64 v68, v68, v69, s[44:45]
	v_cndmask_b32_e32 v69, 0, v216, vcc
	v_sub_f32_e32 v177, v68, v69
	v_mul_f32_e64 v69, |v70|, s8
	v_exp_f32_e32 v69, v69
	v_max_f32_e32 v68, v70, v70
	v_cndmask_b32_e64 v79, v177, v79, s[54:55]
	v_min_f32_e32 v68, 0, v68
	v_add_f32_e32 v69, 1.0, v69
	v_cmp_gt_f32_e32 vcc, s37, v69
	v_mov_b32_dpp v163, v79 row_shr:1 row_mask:0xf bank_mask:0xf bound_ctrl:1
	v_pk_add_f32 v[162:163], v[78:79], v[162:163]
	v_cndmask_b32_e64 v164, 0, 32, vcc
	v_ldexp_f32 v69, v69, v164
	v_log_f32_e32 v69, v69
	s_nop 0
	v_mul_f32_e32 v164, 0x3f317217, v69
	v_fma_f32 v164, v69, s33, -v164
	v_fmac_f32_e32 v164, 0x3377d1cf, v69
	v_fmac_f32_e32 v164, 0x3f317217, v69
	v_cmp_lt_f32_e64 s[44:45], |v69|, s36
	s_nop 1
	v_cndmask_b32_e64 v69, v69, v164, s[44:45]
	v_cndmask_b32_e32 v164, 0, v216, vcc
	v_sub_f32_e32 v164, v69, v164
	v_mul_f32_e32 v69, 0xbfb8aa3b, v70
	v_exp_f32_e32 v69, v69
	s_nop 0
	v_add_f32_e32 v69, 1.0, v69
	v_div_scale_f32 v70, s[2:3], v69, v69, v204
	v_rcp_f32_e32 v165, v70
	s_nop 0
	v_fma_f32 v166, -v70, v165, 1.0
	v_fmac_f32_e32 v165, v166, v165
	v_div_scale_f32 v166, vcc, v204, v69, v204
	v_mul_f32_e32 v167, v166, v165
	v_fma_f32 v180, -v70, v167, v166
	v_fmac_f32_e32 v167, v180, v165
	v_fma_f32 v70, -v70, v167, v166
	v_div_fmas_f32 v70, v70, v165, v167
	v_div_fixup_f32 v69, v70, v69, v204
	v_add_f32_e32 v69, v74, v69
	v_cmp_gt_f32_e32 vcc, s37, v69
	s_nop 1
	v_cndmask_b32_e64 v70, 0, 32, vcc
	v_ldexp_f32 v69, v69, v70
	v_log_f32_e32 v69, v69
	s_nop 0
	v_mul_f32_e32 v70, 0x3f317217, v69
	v_fma_f32 v70, v69, s33, -v70
	v_fmac_f32_e32 v70, 0x3377d1cf, v69
	v_fmac_f32_e32 v70, 0x3f317217, v69
	v_cmp_lt_f32_e64 s[44:45], |v69|, s36
	s_nop 1
	v_cndmask_b32_e64 v69, v69, v70, s[44:45]
	v_cndmask_b32_e32 v70, 0, v216, vcc
	v_sub_f32_e32 v180, v69, v70
	v_mul_f32_e64 v70, |v71|, s8
	v_exp_f32_e32 v70, v70
	v_max_f32_e32 v69, v71, v71
	v_min_f32_e32 v69, 0, v69
	v_add_f32_e32 v70, 1.0, v70
	v_cmp_gt_f32_e32 vcc, s37, v70
	s_nop 1
	v_cndmask_b32_e64 v165, 0, 32, vcc
	v_ldexp_f32 v70, v70, v165
	v_log_f32_e32 v70, v70
	s_nop 0
	v_mul_f32_e32 v165, 0x3f317217, v70
	v_fma_f32 v165, v70, s33, -v165
	v_fmac_f32_e32 v165, 0x3377d1cf, v70
	v_fmac_f32_e32 v165, 0x3f317217, v70
	v_cmp_lt_f32_e64 s[44:45], |v70|, s36
	s_nop 1
; template <int CTRL> __device__ __forceinline__ float dppx(float v) { return __int_as_float(__builtin_amdgcn_update_dpp(0, __float_as_int(v), CTRL, 0xf, 0xf, true)); }
; __device__ __forceinline__ float log_forget(float z, float lb) {
;   const float r0 = fminf(z, 0.f) - __logf(1.f + __expf(-fabsf(z)));
;   const float r1 = __logf(lb + (1.f - lb) / (1.f + __expf(-z)));
;   return lb <= 0.f ? r0 : r1;
; }
;   __device__ __forceinline__ void operator()(const f32x4 (&acc)[2][2][4][2], const pg8::Unit& u, int wr, int wc, int fr, int fq) const {
;     ...
;               for (int q = 0; q < 4; ++q) { const float gv = log_forget(acc[ai][bj][m][qh][q], lq[q]); g[m][q] = gv;
;                 float sc = gv; sc += dppx<0x111>(sc); sc += dppx<0x112>(sc); sc += dppx<0x114>(sc); sc += dppx<0x118>(sc);
	v_cndmask_b32_e64 v70, v70, v165, s[44:45]
	v_cndmask_b32_e32 v165, 0, v216, vcc
	v_sub_f32_e32 v165, v70, v165
	v_mul_f32_e32 v70, 0xbfb8aa3b, v71
	v_exp_f32_e32 v70, v70
	v_pk_add_f32 v[68:69], v[68:69], v[164:165] neg_lo:[0,1] neg_hi:[0,1]
	v_add_f32_e32 v70, 1.0, v70
	v_div_scale_f32 v71, s[2:3], v70, v70, v96
	v_rcp_f32_e32 v166, v71
	v_cndmask_b32_e64 v68, v180, v68, s[56:57]
	v_fma_f32 v167, -v71, v166, 1.0
	v_fmac_f32_e32 v166, v167, v166
	v_div_scale_f32 v167, vcc, v96, v70, v96
	v_mul_f32_e32 v181, v167, v166
	v_fma_f32 v182, -v71, v181, v167
	v_fmac_f32_e32 v181, v182, v166
	v_fma_f32 v71, -v71, v181, v167
	v_div_fmas_f32 v71, v71, v166, v181
	v_div_fixup_f32 v70, v71, v70, v96
	v_add_f32_e32 v70, v75, v70
	v_cmp_gt_f32_e32 vcc, s37, v70
	v_mov_b32_dpp v164, v68 row_shr:1 row_mask:0xf bank_mask:0xf bound_ctrl:1
	s_nop 0
	v_cndmask_b32_e64 v71, 0, 32, vcc
	v_ldexp_f32 v70, v70, v71
	v_log_f32_e32 v70, v70
	s_nop 0
	v_mul_f32_e32 v71, 0x3f317217, v70
	v_fma_f32 v71, v70, s33, -v71
	v_fmac_f32_e32 v71, 0x3377d1cf, v70
	v_fmac_f32_e32 v71, 0x3f317217, v70
	v_cmp_lt_f32_e64 s[44:45], |v70|, s36
	s_nop 1
	v_cndmask_b32_e64 v70, v70, v71, s[44:45]
	v_cndmask_b32_e32 v71, 0, v216, vcc
	v_sub_f32_e32 v181, v70, v71
	v_mul_f32_e64 v71, |v64|, s8
	v_exp_f32_e32 v71, v71
	v_max_f32_e32 v70, v64, v64
	v_mul_f32_e32 v64, 0xbfb8aa3b, v64
	v_exp_f32_e32 v64, v64
	v_add_f32_e32 v71, 1.0, v71
	v_cmp_gt_f32_e32 vcc, s37, v71
	v_cndmask_b32_e64 v69, v181, v69, s[58:59]
	v_add_f32_e32 v64, 1.0, v64
	v_cndmask_b32_e64 v166, 0, 32, vcc
	v_ldexp_f32 v71, v71, v166
	v_log_f32_e32 v71, v71
	v_mov_b32_dpp v165, v69 row_shr:1 row_mask:0xf bank_mask:0xf bound_ctrl:1
	v_pk_add_f32 v[164:165], v[68:69], v[164:165]
	v_min_f32_e32 v70, 0, v70
	v_mul_f32_e32 v166, 0x3f317217, v71
	v_fma_f32 v166, v71, s33, -v166
	v_fmac_f32_e32 v166, 0x3377d1cf, v71
	v_fmac_f32_e32 v166, 0x3f317217, v71
	v_cmp_lt_f32_e64 s[44:45], |v71|, s36
	s_nop 1
	v_cndmask_b32_e64 v71, v71, v166, s[44:45]
	v_cndmask_b32_e32 v166, 0, v216, vcc
	v_sub_f32_e32 v166, v71, v166
	v_div_scale_f32 v71, s[2:3], v64, v64, v206
	v_rcp_f32_e32 v167, v71
	s_nop 0
	v_fma_f32 v182, -v71, v167, 1.0
	v_fmac_f32_e32 v167, v182, v167
	v_div_scale_f32 v182, vcc, v206, v64, v206
	v_mul_f32_e32 v183, v182, v167
	v_fma_f32 v184, -v71, v183, v182
	v_fmac_f32_e32 v183, v184, v167
	v_fma_f32 v71, -v71, v183, v182
	v_div_fmas_f32 v71, v71, v167, v183
	v_div_fixup_f32 v64, v71, v64, v206
	v_add_f32_e32 v64, v72, v64
	v_cmp_gt_f32_e32 vcc, s37, v64
	s_nop 1
	v_cndmask_b32_e64 v71, 0, 32, vcc
	v_ldexp_f32 v64, v64, v71
	v_log_f32_e32 v64, v64
	s_nop 0
	v_mul_f32_e32 v71, 0x3f317217, v64
	v_fma_f32 v71, v64, s33, -v71
	v_fmac_f32_e32 v71, 0x3377d1cf, v64
	v_fmac_f32_e32 v71, 0x3f317217, v64
	v_cmp_lt_f32_e64 s[44:45], |v64|, s36
	s_nop 1
	v_cndmask_b32_e64 v64, v64, v71, s[44:45]
	v_cndmask_b32_e32 v71, 0, v216, vcc
	v_sub_f32_e32 v182, v64, v71
	v_max_f32_e32 v64, v65, v65
	v_min_f32_e32 v71, 0, v64
	v_mul_f32_e64 v64, |v65|, s8
	v_exp_f32_e32 v64, v64
	s_nop 0
	v_add_f32_e32 v64, 1.0, v64
	v_cmp_gt_f32_e32 vcc, s37, v64
	s_nop 1
	v_cndmask_b32_e64 v72, 0, 32, vcc
	v_ldexp_f32 v64, v64, v72
	v_log_f32_e32 v64, v64
	s_nop 0
	v_mul_f32_e32 v72, 0x3f317217, v64
	v_fma_f32 v72, v64, s33, -v72
	v_fmac_f32_e32 v72, 0x3377d1cf, v64
	v_fmac_f32_e32 v72, 0x3f317217, v64
	v_cmp_lt_f32_e64 s[44:45], |v64|, s36
	s_nop 1
	v_cndmask_b32_e64 v64, v64, v72, s[44:45]
	v_cndmask_b32_e32 v72, 0, v216, vcc
	v_sub_f32_e32 v167, v64, v72
	v_mul_f32_e32 v64, 0xbfb8aa3b, v65
	v_exp_f32_e32 v64, v64
	v_pk_add_f32 v[70:71], v[70:71], v[166:167] neg_lo:[0,1] neg_hi:[0,1]
	v_add_f32_e32 v64, 1.0, v64
	v_div_scale_f32 v65, s[2:3], v64, v64, v205
	v_rcp_f32_e32 v72, v65
	v_cndmask_b32_e64 v70, v182, v70, s[52:53]
	v_fma_f32 v183, -v65, v72, 1.0
	v_fmac_f32_e32 v72, v183, v72
	v_div_scale_f32 v183, vcc, v205, v64, v205
	v_mul_f32_e32 v184, v183, v72
	v_fma_f32 v185, -v65, v184, v183
	v_fmac_f32_e32 v184, v185, v72
	v_fma_f32 v65, -v65, v184, v183
	v_div_fmas_f32 v65, v65, v72, v184
	v_div_fixup_f32 v64, v65, v64, v205
	v_add_f32_e32 v64, v73, v64
	v_cmp_gt_f32_e32 vcc, s37, v64
	v_mov_b32_dpp v166, v70 row_shr:1 row_mask:0xf bank_mask:0xf bound_ctrl:1
	s_nop 0
	v_cndmask_b32_e64 v65, 0, 32, vcc
	v_ldexp_f32 v64, v64, v65
	v_log_f32_e32 v64, v64
	s_nop 0
	v_mul_f32_e32 v65, 0x3f317217, v64
	v_fma_f32 v65, v64, s33, -v65
	v_fmac_f32_e32 v65, 0x3377d1cf, v64
	v_fmac_f32_e32 v65, 0x3f317217, v64
	v_cmp_lt_f32_e64 s[44:45], |v64|, s36
	s_nop 1
	v_cndmask_b32_e64 v64, v64, v65, s[44:45]
	v_cndmask_b32_e32 v65, 0, v216, vcc
	v_sub_f32_e32 v183, v64, v65
	v_mul_f32_e64 v65, |v66|, s8
	v_exp_f32_e32 v65, v65
	v_max_f32_e32 v64, v66, v66
	v_cndmask_b32_e64 v71, v183, v71, s[54:55]
	v_min_f32_e32 v64, 0, v64
	v_add_f32_e32 v65, 1.0, v65
	v_cmp_gt_f32_e32 vcc, s37, v65
	v_mov_b32_dpp v167, v71 row_shr:1 row_mask:0xf bank_mask:0xf bound_ctrl:1
	v_pk_add_f32 v[166:167], v[70:71], v[166:167]
	v_cndmask_b32_e64 v72, 0, 32, vcc
	v_ldexp_f32 v65, v65, v72
	v_log_f32_e32 v65, v65
	s_nop 0
	v_mul_f32_e32 v72, 0x3f317217, v65
	v_fma_f32 v72, v65, s33, -v72
	v_fmac_f32_e32 v72, 0x3377d1cf, v65
	v_fmac_f32_e32 v72, 0x3f317217, v65
	v_cmp_lt_f32_e64 s[44:45], |v65|, s36
	s_nop 1
	v_cndmask_b32_e64 v65, v65, v72, s[44:45]
	v_cndmask_b32_e32 v72, 0, v216, vcc
	v_sub_f32_e32 v72, v65, v72
	v_mul_f32_e32 v65, 0xbfb8aa3b, v66
	v_exp_f32_e32 v65, v65
	s_nop 0
	v_add_f32_e32 v65, 1.0, v65
	v_div_scale_f32 v66, s[2:3], v65, v65, v204
	v_rcp_f32_e32 v73, v66
	s_nop 0
	v_fma_f32 v184, -v66, v73, 1.0
	v_fmac_f32_e32 v73, v184, v73
	v_div_scale_f32 v184, vcc, v204, v65, v204
; template <int CTRL> __device__ __forceinline__ float dppx(float v) { return __int_as_float(__builtin_amdgcn_update_dpp(0, __float_as_int(v), CTRL, 0xf, 0xf, true)); }
; __device__ __forceinline__ float log_forget(float z, float lb) {
;   const float r0 = fminf(z, 0.f) - __logf(1.f + __expf(-fabsf(z)));
;   const float r1 = __logf(lb + (1.f - lb) / (1.f + __expf(-z)));
;   return lb <= 0.f ? r0 : r1;
; }
;   __device__ __forceinline__ void operator()(const f32x4 (&acc)[2][2][4][2], const pg8::Unit& u, int wr, int wc, int fr, int fq) const {
;     const int row0 = u.pm * 256 + wr * 64 + fr, colt = u.pn * 256, col0 = colt + wc * 32 + 8 * fq;
;     if (colt >= C_HF && colt < C_HI) {
;       const bool bwd = colt >= C_HF + 512;
; #pragma unroll
;       for (int bj = 0; bj < 2; ++bj) { const int c = col0 + bj * 128 - C_HF; const f32x4 l0 = *(const f32x4*)(lb + (c & 511)), l1 = *(const f32x4*)(lb + (c & 511) + 4);
; #pragma unroll
;         for (int ai = 0; ai < 2; ++ai)
; #pragma unroll
;           for (int qh = 0; qh < 2; ++qh) { float g[4][4], cs[4][4], carry[4];
;             const f32x4 lq = qh == 0 ? l0 : l1;
; #pragma unroll
;             for (int q = 0; q < 4; ++q) carry[q] = 0.f;
; #pragma unroll
;             for (int m = 0; m < 4; ++m)
; #pragma unroll
;               for (int q = 0; q < 4; ++q) { const float gv = log_forget(acc[ai][bj][m][qh][q], lq[q]); g[m][q] = gv;
;                 float sc = gv; sc += dppx<0x111>(sc); sc += dppx<0x112>(sc); sc += dppx<0x114>(sc); sc += dppx<0x118>(sc);
;                 const float tot16 = __int_as_float(__builtin_amdgcn_ds_swizzle(__float_as_int(sc), 0x1F0));
;                 cs[m][q] = sc + carry[q]; carry[q] += tot16; }
	v_mul_f32_e32 v185, v184, v73
	v_fma_f32 v186, -v66, v185, v184
	v_fmac_f32_e32 v185, v186, v73
	v_fma_f32 v66, -v66, v185, v184
	v_div_fmas_f32 v66, v66, v73, v185
	v_div_fixup_f32 v65, v66, v65, v204
	v_add_f32_e32 v65, v74, v65
	v_cmp_gt_f32_e32 vcc, s37, v65
	s_nop 1
	v_cndmask_b32_e64 v66, 0, 32, vcc
	v_ldexp_f32 v65, v65, v66
	v_log_f32_e32 v65, v65
	s_nop 0
	v_mul_f32_e32 v66, 0x3f317217, v65
	v_fma_f32 v66, v65, s33, -v66
	v_fmac_f32_e32 v66, 0x3377d1cf, v65
	v_fmac_f32_e32 v66, 0x3f317217, v65
	v_cmp_lt_f32_e64 s[44:45], |v65|, s36
	s_nop 1
	v_cndmask_b32_e64 v65, v65, v66, s[44:45]
	v_cndmask_b32_e32 v66, 0, v216, vcc
	v_sub_f32_e32 v184, v65, v66
	v_mul_f32_e64 v66, |v67|, s8
	v_exp_f32_e32 v66, v66
	v_max_f32_e32 v65, v67, v67
	v_min_f32_e32 v65, 0, v65
	v_add_f32_e32 v66, 1.0, v66
	v_cmp_gt_f32_e32 vcc, s37, v66
	s_nop 1
	v_cndmask_b32_e64 v73, 0, 32, vcc
	v_ldexp_f32 v66, v66, v73
	v_log_f32_e32 v66, v66
	s_nop 0
	v_mul_f32_e32 v73, 0x3f317217, v66
	v_fma_f32 v73, v66, s33, -v73
	v_fmac_f32_e32 v73, 0x3377d1cf, v66
	v_fmac_f32_e32 v73, 0x3f317217, v66
	v_cmp_lt_f32_e64 s[44:45], |v66|, s36
	s_nop 1
	v_cndmask_b32_e64 v66, v66, v73, s[44:45]
	v_cndmask_b32_e32 v73, 0, v216, vcc
	v_sub_f32_e32 v73, v66, v73
	v_mul_f32_e32 v66, 0xbfb8aa3b, v67
	v_exp_f32_e32 v66, v66
	v_pk_add_f32 v[64:65], v[64:65], v[72:73] neg_lo:[0,1] neg_hi:[0,1]
	v_add_f32_e32 v66, 1.0, v66
	v_div_scale_f32 v67, s[2:3], v66, v66, v96
	v_rcp_f32_e32 v74, v67
	v_cndmask_b32_e64 v72, v184, v64, s[56:57]
	v_fma_f32 v185, -v67, v74, 1.0
	v_fmac_f32_e32 v74, v185, v74
	v_div_scale_f32 v185, vcc, v96, v66, v96
	v_mul_f32_e32 v186, v185, v74
	v_fma_f32 v187, -v67, v186, v185
	v_fmac_f32_e32 v186, v187, v74
	v_fma_f32 v67, -v67, v186, v185
	v_div_fmas_f32 v67, v67, v74, v186
	v_div_fixup_f32 v66, v67, v66, v96
	v_add_f32_e32 v66, v75, v66
	v_cmp_gt_f32_e32 vcc, s37, v66
	v_mov_b32_dpp v64, v72 row_shr:1 row_mask:0xf bank_mask:0xf bound_ctrl:1
	s_nop 0
	v_cndmask_b32_e64 v67, 0, 32, vcc
	v_ldexp_f32 v66, v66, v67
	v_log_f32_e32 v66, v66
	s_nop 0
	v_mul_f32_e32 v67, 0x3f317217, v66
	v_fma_f32 v67, v66, s33, -v67
	v_fmac_f32_e32 v67, 0x3377d1cf, v66
	v_fmac_f32_e32 v67, 0x3f317217, v66
	v_cmp_lt_f32_e64 s[44:45], |v66|, s36
	s_nop 1
	v_cndmask_b32_e64 v66, v66, v67, s[44:45]
	v_cndmask_b32_e32 v67, 0, v216, vcc
	v_sub_f32_e32 v96, v66, v67
	v_pk_add_f32 v[66:67], v[118:119], v[120:121] neg_lo:[0,1] neg_hi:[0,1]
	v_cndmask_b32_e64 v73, v96, v65, s[58:59]
	v_cndmask_b32_e64 v67, v169, v67, s[54:55]
	v_cndmask_b32_e64 v66, v168, v66, s[52:53]
	v_mov_b32_dpp v65, v73 row_shr:1 row_mask:0xf bank_mask:0xf bound_ctrl:1
	v_mov_b32_dpp v75, v67 row_shr:1 row_mask:0xf bank_mask:0xf bound_ctrl:1
	v_mov_b32_dpp v74, v66 row_shr:1 row_mask:0xf bank_mask:0xf bound_ctrl:1
	v_pk_add_f32 v[74:75], v[66:67], v[74:75]
	v_pk_add_f32 v[64:65], v[72:73], v[64:65]
	v_add_u32_e32 v96, 0xfffffc80, v154
	v_mov_b32_dpp v118, v74 row_shr:2 row_mask:0xf bank_mask:0xf bound_ctrl:1
	v_mov_b32_dpp v119, v75 row_shr:2 row_mask:0xf bank_mask:0xf bound_ctrl:1
	v_pk_add_f32 v[74:75], v[74:75], v[118:119]
	s_nop 1
	v_mov_b32_dpp v118, v74 row_shr:4 row_mask:0xf bank_mask:0xf bound_ctrl:1
	v_mov_b32_dpp v119, v75 row_shr:4 row_mask:0xf bank_mask:0xf bound_ctrl:1
	v_pk_add_f32 v[74:75], v[74:75], v[118:119]
	s_nop 1
	v_mov_b32_dpp v118, v74 row_shr:8 row_mask:0xf bank_mask:0xf bound_ctrl:1
	v_mov_b32_dpp v119, v75 row_shr:8 row_mask:0xf bank_mask:0xf bound_ctrl:1
	v_pk_add_f32 v[74:75], v[74:75], v[118:119]
	ds_swizzle_b32 v118, v74 offset:swizzle(BROADCAST,16,15)
	ds_swizzle_b32 v119, v75 offset:swizzle(BROADCAST,16,15)
	v_pk_add_f32 v[74:75], v[74:75], 0 op_sel_hi:[1,0]
	s_waitcnt lgkmcnt(0)
	v_pk_add_f32 v[168:169], v[118:119], 0 op_sel_hi:[1,0]
	v_mul_f32_e32 v118, 0x3fb8aa3b, v66
	v_exp_f32_e32 v118, v118
	v_mov_b32_dpp v119, v81 row_shr:1 row_mask:0xf bank_mask:0xf bound_ctrl:1
	v_sub_f32_e32 v185, 1.0, v118
	v_mul_f32_e32 v118, 0x3fb8aa3b, v67
	v_exp_f32_e32 v118, v118
	s_nop 0
	v_sub_f32_e32 v186, 1.0, v118
	v_mov_b32_dpp v118, v80 row_shr:1 row_mask:0xf bank_mask:0xf bound_ctrl:1
	v_pk_add_f32 v[118:119], v[80:81], v[118:119]
	s_nop 1
	v_mov_b32_dpp v120, v118 row_shr:2 row_mask:0xf bank_mask:0xf bound_ctrl:1
	v_mov_b32_dpp v121, v119 row_shr:2 row_mask:0xf bank_mask:0xf bound_ctrl:1
	v_pk_add_f32 v[118:119], v[118:119], v[120:121]
	s_nop 1
	v_mov_b32_dpp v120, v118 row_shr:4 row_mask:0xf bank_mask:0xf bound_ctrl:1
	v_mov_b32_dpp v121, v119 row_shr:4 row_mask:0xf bank_mask:0xf bound_ctrl:1
	v_pk_add_f32 v[118:119], v[118:119], v[120:121]
	s_nop 1
	v_mov_b32_dpp v120, v118 row_shr:8 row_mask:0xf bank_mask:0xf bound_ctrl:1
	v_mov_b32_dpp v121, v119 row_shr:8 row_mask:0xf bank_mask:0xf bound_ctrl:1
	v_pk_add_f32 v[118:119], v[118:119], v[120:121]
	ds_swizzle_b32 v120, v118 offset:swizzle(BROADCAST,16,15)
	ds_swizzle_b32 v121, v119 offset:swizzle(BROADCAST,16,15)
	v_pk_add_f32 v[118:119], v[118:119], 0 op_sel_hi:[1,0]
	s_waitcnt lgkmcnt(0)
	v_pk_add_f32 v[170:171], v[120:121], 0 op_sel_hi:[1,0]
	v_mul_f32_e32 v120, 0x3fb8aa3b, v80
	v_exp_f32_e32 v120, v120
	v_mov_b32_dpp v121, v83 row_shr:1 row_mask:0xf bank_mask:0xf bound_ctrl:1
	v_sub_f32_e32 v187, 1.0, v120
	v_mul_f32_e32 v120, 0x3fb8aa3b, v81
	v_exp_f32_e32 v120, v120
	s_nop 0
	v_sub_f32_e32 v188, 1.0, v120
	v_mov_b32_dpp v120, v82 row_shr:1 row_mask:0xf bank_mask:0xf bound_ctrl:1
	v_pk_add_f32 v[120:121], v[82:83], v[120:121]
	s_nop 1
	v_mov_b32_dpp v156, v120 row_shr:2 row_mask:0xf bank_mask:0xf bound_ctrl:1
	v_mov_b32_dpp v157, v121 row_shr:2 row_mask:0xf bank_mask:0xf bound_ctrl:1
	v_pk_add_f32 v[120:121], v[120:121], v[156:157]
	s_nop 1
	v_mov_b32_dpp v156, v120 row_shr:4 row_mask:0xf bank_mask:0xf bound_ctrl:1
	v_mov_b32_dpp v157, v121 row_shr:4 row_mask:0xf bank_mask:0xf bound_ctrl:1
	v_pk_add_f32 v[120:121], v[120:121], v[156:157]
	s_nop 1
	v_mov_b32_dpp v156, v120 row_shr:8 row_mask:0xf bank_mask:0xf bound_ctrl:1
	v_mov_b32_dpp v157, v121 row_shr:8 row_mask:0xf bank_mask:0xf bound_ctrl:1
	v_pk_add_f32 v[120:121], v[120:121], v[156:157]
	ds_swizzle_b32 v156, v120 offset:swizzle(BROADCAST,16,15)
	ds_swizzle_b32 v157, v121 offset:swizzle(BROADCAST,16,15)
	v_pk_add_f32 v[120:121], v[168:169], v[120:121]
	s_waitcnt lgkmcnt(0)
; template <int CTRL> __device__ __forceinline__ float dppx(float v) { return __int_as_float(__builtin_amdgcn_update_dpp(0, __float_as_int(v), CTRL, 0xf, 0xf, true)); }
;   __device__ __forceinline__ void operator()(const f32x4 (&acc)[2][2][4][2], const pg8::Unit& u, int wr, int wc, int fr, int fq) const {
;     ...
;           for (int qh = 0; qh < 2; ++qh) { float g[4][4], cs[4][4], carry[4];
;             const f32x4 lq = qh == 0 ? l0 : l1;
; #pragma unroll
;             for (int q = 0; q < 4; ++q) carry[q] = 0.f;
; #pragma unroll
;             for (int m = 0; m < 4; ++m)
; #pragma unroll
;               for (int q = 0; q < 4; ++q) { const float gv = log_forget(acc[ai][bj][m][qh][q], lq[q]); g[m][q] = gv;
;                 float sc = gv; sc += dppx<0x111>(sc); sc += dppx<0x112>(sc); sc += dppx<0x114>(sc); sc += dppx<0x118>(sc);
;                 const float tot16 = __int_as_float(__builtin_amdgcn_ds_swizzle(__float_as_int(sc), 0x1F0));
;                 cs[m][q] = sc + carry[q]; carry[q] += tot16; }
; #pragma unroll
;             for (int m = 0; m < 4; ++m) { const int r = row0 + ai * 128 + m * 16; float bq[4], kq[4];
; #pragma unroll
;               for (int q = 0; q < 4; ++q) { bq[q] = bwd ? (carry[q] - cs[m][q]) + g[m][q] : cs[m][q]; kq[q] = 1.f - __expf(g[m][q]); }
	v_pk_add_f32 v[158:159], v[168:169], v[156:157]
	v_mul_f32_e32 v168, 0x3fb8aa3b, v76
	v_exp_f32_e32 v168, v168
	v_mov_b32_dpp v169, v163 row_shr:2 row_mask:0xf bank_mask:0xf bound_ctrl:1
	v_mul_f32_e32 v156, 0x3fb8aa3b, v82
	v_exp_f32_e32 v156, v156
	v_sub_f32_e32 v174, 1.0, v168
	v_mul_f32_e32 v168, 0x3fb8aa3b, v77
	v_exp_f32_e32 v168, v168
	v_sub_f32_e32 v172, 1.0, v156
	v_mul_f32_e32 v156, 0x3fb8aa3b, v83
	v_exp_f32_e32 v156, v156
	v_sub_f32_e32 v175, 1.0, v168
	v_mov_b32_dpp v168, v162 row_shr:2 row_mask:0xf bank_mask:0xf bound_ctrl:1
	v_pk_add_f32 v[162:163], v[162:163], v[168:169]
	v_sub_f32_e32 v173, 1.0, v156
	v_mov_b32_dpp v156, v76 row_shr:1 row_mask:0xf bank_mask:0xf bound_ctrl:1
	v_mov_b32_dpp v168, v162 row_shr:4 row_mask:0xf bank_mask:0xf bound_ctrl:1
	v_mov_b32_dpp v169, v163 row_shr:4 row_mask:0xf bank_mask:0xf bound_ctrl:1
	v_pk_add_f32 v[162:163], v[162:163], v[168:169]
	v_mov_b32_dpp v157, v77 row_shr:1 row_mask:0xf bank_mask:0xf bound_ctrl:1
	v_pk_add_f32 v[156:157], v[76:77], v[156:157]
	v_mov_b32_dpp v168, v162 row_shr:8 row_mask:0xf bank_mask:0xf bound_ctrl:1
	v_mov_b32_dpp v169, v163 row_shr:8 row_mask:0xf bank_mask:0xf bound_ctrl:1
	v_pk_add_f32 v[162:163], v[162:163], v[168:169]
	ds_swizzle_b32 v168, v162 offset:swizzle(BROADCAST,16,15)
	ds_swizzle_b32 v169, v163 offset:swizzle(BROADCAST,16,15)
	v_pk_add_f32 v[162:163], v[158:159], v[162:163]
	v_mov_b32_dpp v160, v156 row_shr:2 row_mask:0xf bank_mask:0xf bound_ctrl:1
	v_mov_b32_dpp v161, v157 row_shr:2 row_mask:0xf bank_mask:0xf bound_ctrl:1
	v_pk_add_f32 v[156:157], v[156:157], v[160:161]
	s_waitcnt lgkmcnt(0)
	v_pk_add_f32 v[158:159], v[158:159], v[168:169]
	v_mul_f32_e32 v168, 0x3fb8aa3b, v78
	v_exp_f32_e32 v168, v168
	v_mov_b32_dpp v169, v165 row_shr:2 row_mask:0xf bank_mask:0xf bound_ctrl:1
	v_mov_b32_dpp v160, v156 row_shr:4 row_mask:0xf bank_mask:0xf bound_ctrl:1
	v_mov_b32_dpp v161, v157 row_shr:4 row_mask:0xf bank_mask:0xf bound_ctrl:1
	v_sub_f32_e32 v176, 1.0, v168
	v_mul_f32_e32 v168, 0x3fb8aa3b, v79
	v_exp_f32_e32 v168, v168
	v_pk_add_f32 v[156:157], v[156:157], v[160:161]
	v_sub_f32_e32 v177, 1.0, v168
	v_mov_b32_dpp v168, v164 row_shr:2 row_mask:0xf bank_mask:0xf bound_ctrl:1
	v_pk_add_f32 v[164:165], v[164:165], v[168:169]
	v_mov_b32_dpp v160, v156 row_shr:8 row_mask:0xf bank_mask:0xf bound_ctrl:1
	v_mov_b32_dpp v161, v157 row_shr:8 row_mask:0xf bank_mask:0xf bound_ctrl:1
	v_mov_b32_dpp v168, v164 row_shr:4 row_mask:0xf bank_mask:0xf bound_ctrl:1
	v_mov_b32_dpp v169, v165 row_shr:4 row_mask:0xf bank_mask:0xf bound_ctrl:1
	v_pk_add_f32 v[164:165], v[164:165], v[168:169]
	v_pk_add_f32 v[156:157], v[156:157], v[160:161]
	ds_swizzle_b32 v160, v156 offset:swizzle(BROADCAST,16,15)
	v_mov_b32_dpp v168, v164 row_shr:8 row_mask:0xf bank_mask:0xf bound_ctrl:1
	v_mov_b32_dpp v169, v165 row_shr:8 row_mask:0xf bank_mask:0xf bound_ctrl:1
	ds_swizzle_b32 v161, v157 offset:swizzle(BROADCAST,16,15)
	v_pk_add_f32 v[164:165], v[164:165], v[168:169]
	ds_swizzle_b32 v168, v164 offset:swizzle(BROADCAST,16,15)
	ds_swizzle_b32 v169, v165 offset:swizzle(BROADCAST,16,15)
	v_pk_add_f32 v[156:157], v[170:171], v[156:157]
	s_waitcnt lgkmcnt(2)
	v_pk_add_f32 v[160:161], v[170:171], v[160:161]
	s_nop 0
	v_pk_add_f32 v[164:165], v[160:161], v[164:165]
	s_waitcnt lgkmcnt(0)
	v_pk_add_f32 v[160:161], v[160:161], v[168:169]
	v_mul_f32_e32 v168, 0x3fb8aa3b, v68
	v_exp_f32_e32 v168, v168
	v_mov_b32_dpp v169, v167 row_shr:2 row_mask:0xf bank_mask:0xf bound_ctrl:1
	v_sub_f32_e32 v180, 1.0, v168
	v_mul_f32_e32 v168, 0x3fb8aa3b, v69
	v_exp_f32_e32 v168, v168
	s_nop 0
	v_sub_f32_e32 v181, 1.0, v168
	v_mov_b32_dpp v168, v166 row_shr:2 row_mask:0xf bank_mask:0xf bound_ctrl:1
	v_pk_add_f32 v[166:167], v[166:167], v[168:169]
	s_nop 1
	v_mov_b32_dpp v168, v166 row_shr:4 row_mask:0xf bank_mask:0xf bound_ctrl:1
	v_mov_b32_dpp v169, v167 row_shr:4 row_mask:0xf bank_mask:0xf bound_ctrl:1
	v_pk_add_f32 v[166:167], v[166:167], v[168:169]
	s_nop 1
	v_mov_b32_dpp v168, v166 row_shr:8 row_mask:0xf bank_mask:0xf bound_ctrl:1
	v_mov_b32_dpp v169, v167 row_shr:8 row_mask:0xf bank_mask:0xf bound_ctrl:1
	v_pk_add_f32 v[166:167], v[166:167], v[168:169]
	ds_swizzle_b32 v168, v166 offset:swizzle(BROADCAST,16,15)
	ds_swizzle_b32 v169, v167 offset:swizzle(BROADCAST,16,15)
	v_pk_add_f32 v[166:167], v[158:159], v[166:167]
	s_waitcnt lgkmcnt(0)
	v_pk_add_f32 v[158:159], v[158:159], v[168:169]
	v_mul_f32_e32 v168, 0x3fb8aa3b, v70
	v_exp_f32_e32 v168, v168
	v_mov_b32_dpp v169, v65 row_shr:2 row_mask:0xf bank_mask:0xf bound_ctrl:1
	v_sub_f32_e32 v182, 1.0, v168
	v_mul_f32_e32 v168, 0x3fb8aa3b, v71
	v_exp_f32_e32 v168, v168
	s_nop 0
	v_sub_f32_e32 v183, 1.0, v168
	v_mov_b32_dpp v168, v64 row_shr:2 row_mask:0xf bank_mask:0xf bound_ctrl:1
	v_pk_add_f32 v[64:65], v[64:65], v[168:169]
	s_nop 1
	v_mov_b32_dpp v168, v64 row_shr:4 row_mask:0xf bank_mask:0xf bound_ctrl:1
	v_mov_b32_dpp v169, v65 row_shr:4 row_mask:0xf bank_mask:0xf bound_ctrl:1
	v_pk_add_f32 v[64:65], v[64:65], v[168:169]
	s_nop 1
	v_mov_b32_dpp v168, v64 row_shr:8 row_mask:0xf bank_mask:0xf bound_ctrl:1
	v_mov_b32_dpp v169, v65 row_shr:8 row_mask:0xf bank_mask:0xf bound_ctrl:1
	v_pk_add_f32 v[64:65], v[64:65], v[168:169]
	ds_swizzle_b32 v168, v64 offset:swizzle(BROADCAST,16,15)
	ds_swizzle_b32 v169, v65 offset:swizzle(BROADCAST,16,15)
	v_pk_add_f32 v[170:171], v[160:161], v[64:65]
	v_pk_add_f32 v[64:65], v[158:159], v[74:75] neg_lo:[0,1] neg_hi:[0,1]
	s_waitcnt lgkmcnt(0)
; __device__ __forceinline__ unsigned cvt_pk_bf16(float lo, float hi) { unsigned r; asm volatile("v_cvt_pk_bf16_f32 %0, %1, %2" : "=v"(r) : "v"(lo), "v"(hi)); return r; }
;   __device__ __forceinline__ void operator()(const f32x4 (&acc)[2][2][4][2], const pg8::Unit& u, int wr, int wc, int fr, int fq) const {
;     ...
;       for (int bj = 0; bj < 2; ++bj) { const int c = col0 + bj * 128 - C_HF; const f32x4 l0 = *(const f32x4*)(lb + (c & 511)), l1 = *(const f32x4*)(lb + (c & 511) + 4);
; #pragma unroll
;         for (int ai = 0; ai < 2; ++ai)
; #pragma unroll
;           for (int qh = 0; qh < 2; ++qh) { float g[4][4], cs[4][4], carry[4];
;             const f32x4 lq = qh == 0 ? l0 : l1;
; #pragma unroll
;             for (int q = 0; q < 4; ++q) carry[q] = 0.f;
; #pragma unroll
;             for (int m = 0; m < 4; ++m)
; #pragma unroll
;               for (int q = 0; q < 4; ++q) { const float gv = log_forget(acc[ai][bj][m][qh][q], lq[q]); g[m][q] = gv;
;     ...
;             for (int m = 0; m < 4; ++m) { const int r = row0 + ai * 128 + m * 16; float bq[4], kq[4];
; #pragma unroll
;               for (int q = 0; q < 4; ++q) { bq[q] = bwd ? (carry[q] - cs[m][q]) + g[m][q] : cs[m][q]; kq[q] = 1.f - __expf(g[m][q]); }
;               *(f32x4*)(logfp + (size_t)r * 1024 + c + 4 * qh) = (f32x4){bq[0], bq[1], bq[2], bq[3]};
;               u32x2 w; w.x = pg8::cvt_pk_bf16(kq[0], kq[1]); w.y = pg8::cvt_pk_bf16(kq[2], kq[3]);
;               *(u32x2*)(km + (size_t)r * 1024 + c + 4 * qh) = w; } } }
	v_pk_add_f32 v[160:161], v[160:161], v[168:169]
	s_nop 0
	v_pk_add_f32 v[168:169], v[160:161], v[118:119] neg_lo:[0,1] neg_hi:[0,1]
	v_pk_add_f32 v[64:65], v[66:67], v[64:65]
	v_pk_add_f32 v[66:67], v[80:81], v[168:169]
	v_cndmask_b32_e64 v65, v75, v65, s[42:43]
	v_cndmask_b32_e64 v67, v119, v67, s[42:43]
	v_cndmask_b32_e64 v66, v118, v66, s[42:43]
	v_cndmask_b32_e64 v64, v74, v64, s[42:43]
	global_store_dwordx4 v[104:105], v[64:67], off offset:16
	s_nop 1
	v_cvt_pk_bf16_f32 v64, v185, v186
	v_cvt_pk_bf16_f32 v65, v187, v188
	global_store_dwordx2 v[102:103], v[64:65], off offset:8
	v_pk_add_f32 v[64:65], v[158:159], v[120:121] neg_lo:[0,1] neg_hi:[0,1]
	v_pk_add_f32 v[66:67], v[160:161], v[156:157] neg_lo:[0,1] neg_hi:[0,1]
	v_pk_add_f32 v[64:65], v[82:83], v[64:65]
	v_pk_add_f32 v[66:67], v[76:77], v[66:67]
	v_cndmask_b32_e64 v65, v121, v65, s[42:43]
	v_cndmask_b32_e64 v67, v157, v67, s[42:43]
	v_cndmask_b32_e64 v66, v156, v66, s[42:43]
	v_cndmask_b32_e64 v64, v120, v64, s[42:43]
	global_store_dwordx4 v[108:109], v[64:67], off offset:16
	s_nop 1
	v_cvt_pk_bf16_f32 v64, v172, v173
	v_cvt_pk_bf16_f32 v65, v174, v175
	global_store_dwordx2 v[106:107], v[64:65], off offset:8
	v_pk_add_f32 v[64:65], v[158:159], v[162:163] neg_lo:[0,1] neg_hi:[0,1]
	v_pk_add_f32 v[66:67], v[160:161], v[164:165] neg_lo:[0,1] neg_hi:[0,1]
	v_pk_add_f32 v[64:65], v[78:79], v[64:65]
	v_pk_add_f32 v[66:67], v[68:69], v[66:67]
	v_cndmask_b32_e64 v65, v163, v65, s[42:43]
	v_cndmask_b32_e64 v67, v165, v67, s[42:43]
	v_cndmask_b32_e64 v66, v164, v66, s[42:43]
	v_cndmask_b32_e64 v64, v162, v64, s[42:43]
	global_store_dwordx4 v[110:111], v[64:67], off offset:16
	v_mul_f32_e32 v69, 0x3fb8aa3b, v73
	v_exp_f32_e32 v69, v69
	v_cvt_pk_bf16_f32 v64, v176, v177
	v_cvt_pk_bf16_f32 v65, v180, v181
	global_store_dwordx2 v[112:113], v[64:65], off offset:8
	v_mul_f32_e32 v64, 0x3fb8aa3b, v72
	v_exp_f32_e32 v64, v64
	v_pk_add_f32 v[66:67], v[160:161], v[170:171] neg_lo:[0,1] neg_hi:[0,1]
	v_sub_f32_e32 v69, 1.0, v69
	v_pk_add_f32 v[66:67], v[72:73], v[66:67]
	v_sub_f32_e32 v68, 1.0, v64
	v_pk_add_f32 v[64:65], v[158:159], v[166:167] neg_lo:[0,1] neg_hi:[0,1]
	v_cndmask_b32_e64 v67, v171, v67, s[42:43]
	v_pk_add_f32 v[64:65], v[70:71], v[64:65]
	v_cndmask_b32_e64 v66, v170, v66, s[42:43]
	v_cndmask_b32_e64 v65, v167, v65, s[42:43]
	v_cndmask_b32_e64 v64, v166, v64, s[42:43]
	global_store_dwordx4 v[114:115], v[64:67], off offset:16
	v_mul_f32_e64 v73, |v60|, s8
	v_exp_f32_e32 v73, v73
	v_cvt_pk_bf16_f32 v64, v182, v183
	v_cvt_pk_bf16_f32 v65, v68, v69
	global_store_dwordx2 v[116:117], v[64:65], off offset:8
	global_load_dwordx4 v[64:67], v155, s[66:67] offset:528
	s_nop 0
	global_load_dwordx4 v[68:71], v155, s[66:67] offset:512
	v_add_f32_e32 v73, 1.0, v73
	v_cmp_gt_f32_e32 vcc, s37, v73
	v_max_f32_e32 v72, v60, v60
	v_mul_f32_e32 v60, 0xbfb8aa3b, v60
	v_cndmask_b32_e64 v74, 0, 32, vcc
	v_ldexp_f32 v73, v73, v74
	v_log_f32_e32 v73, v73
	v_exp_f32_e32 v60, v60
	v_min_f32_e32 v72, 0, v72
	v_mul_f32_e32 v74, 0x3f317217, v73
	v_fma_f32 v74, v73, s33, -v74
	v_fmac_f32_e32 v74, 0x3377d1cf, v73
	v_fmac_f32_e32 v74, 0x3f317217, v73
	v_cmp_lt_f32_e64 s[44:45], |v73|, s36
	v_add_f32_e32 v60, 1.0, v60
	s_waitcnt vmcnt(1)
	v_cmp_ge_f32_e64 s[52:53], 0, v65
	v_cndmask_b32_e64 v73, v73, v74, s[44:45]
	v_cndmask_b32_e32 v74, 0, v216, vcc
	s_waitcnt vmcnt(0)
	v_sub_f32_e32 v157, 1.0, v68
	v_sub_f32_e32 v74, v73, v74
	v_div_scale_f32 v73, s[2:3], v60, v60, v157
	v_rcp_f32_e32 v75, v73
	v_sub_f32_e32 v156, 1.0, v69
	v_sub_f32_e32 v155, 1.0, v70
	v_sub_f32_e32 v154, 1.0, v71
	v_fma_f32 v76, -v73, v75, 1.0
	v_fmac_f32_e32 v75, v76, v75
	v_div_scale_f32 v76, vcc, v157, v60, v157
	v_mul_f32_e32 v77, v76, v75
	v_fma_f32 v78, -v73, v77, v76
	v_fmac_f32_e32 v77, v78, v75
	v_fma_f32 v73, -v73, v77, v76
	v_div_fmas_f32 v73, v73, v75, v77
	v_div_fixup_f32 v60, v73, v60, v157
	v_add_f32_e32 v60, v68, v60
	v_cmp_gt_f32_e32 vcc, s37, v60
	v_cmp_ge_f32_e64 s[46:47], 0, v69
	v_cmp_ge_f32_e64 s[50:51], 0, v70
	v_cndmask_b32_e64 v73, 0, 32, vcc
	v_ldexp_f32 v60, v60, v73
	v_log_f32_e32 v60, v60
	v_cmp_ge_f32_e64 s[54:55], 0, v71
	v_cmp_ge_f32_e64 s[56:57], 0, v66
	v_cmp_ge_f32_e64 s[58:59], 0, v67
	v_mul_f32_e32 v73, 0x3f317217, v60
	v_fma_f32 v73, v60, s33, -v73
	v_fmac_f32_e32 v73, 0x3377d1cf, v60
	v_fmac_f32_e32 v73, 0x3f317217, v60
	v_cmp_lt_f32_e64 s[44:45], |v60|, s36
	s_nop 1
	v_cndmask_b32_e64 v60, v60, v73, s[44:45]
	v_cndmask_b32_e32 v73, 0, v216, vcc
	v_sub_f32_e32 v116, v60, v73
	v_max_f32_e32 v60, v61, v61
	v_min_f32_e32 v73, 0, v60
	v_mul_f32_e64 v60, |v61|, s8
	v_exp_f32_e32 v60, v60
	s_nop 0
	v_add_f32_e32 v60, 1.0, v60
	v_cmp_gt_f32_e32 vcc, s37, v60
	s_nop 1
	v_cndmask_b32_e64 v75, 0, 32, vcc
	v_ldexp_f32 v60, v60, v75
	v_log_f32_e32 v60, v60
	s_nop 0
	v_mul_f32_e32 v75, 0x3f317217, v60
	v_fma_f32 v75, v60, s33, -v75
	v_fmac_f32_e32 v75, 0x3377d1cf, v60
	v_fmac_f32_e32 v75, 0x3f317217, v60
	v_cmp_lt_f32_e64 s[44:45], |v60|, s36
	s_nop 1
	v_cndmask_b32_e64 v60, v60, v75, s[44:45]
	v_cndmask_b32_e32 v75, 0, v216, vcc
	v_sub_f32_e32 v75, v60, v75
	v_mul_f32_e32 v60, 0xbfb8aa3b, v61
	v_exp_f32_e32 v60, v60
	s_nop 0
	v_add_f32_e32 v60, 1.0, v60
	v_div_scale_f32 v61, s[2:3], v60, v60, v156
	v_rcp_f32_e32 v76, v61
	s_nop 0
	v_fma_f32 v77, -v61, v76, 1.0
	v_fmac_f32_e32 v76, v77, v76
	v_div_scale_f32 v77, vcc, v156, v60, v156
	v_mul_f32_e32 v78, v77, v76
	v_fma_f32 v79, -v61, v78, v77
	v_fmac_f32_e32 v78, v79, v76
	v_fma_f32 v61, -v61, v78, v77
	v_div_fmas_f32 v61, v61, v76, v78
	v_div_fixup_f32 v60, v61, v60, v156
	v_add_f32_e32 v60, v69, v60
	v_cmp_gt_f32_e32 vcc, s37, v60
	s_nop 1
	v_cndmask_b32_e64 v61, 0, 32, vcc
; __device__ __forceinline__ float log_forget(float z, float lb) {
;   const float r0 = fminf(z, 0.f) - __logf(1.f + __expf(-fabsf(z)));
;   const float r1 = __logf(lb + (1.f - lb) / (1.f + __expf(-z)));
;   return lb <= 0.f ? r0 : r1;
; }
	v_ldexp_f32 v60, v60, v61
	v_log_f32_e32 v60, v60
	s_nop 0
	v_mul_f32_e32 v61, 0x3f317217, v60
	v_fma_f32 v61, v60, s33, -v61
	v_fmac_f32_e32 v61, 0x3377d1cf, v60
	v_fmac_f32_e32 v61, 0x3f317217, v60
	v_cmp_lt_f32_e64 s[44:45], |v60|, s36
	s_nop 1
	v_cndmask_b32_e64 v60, v60, v61, s[44:45]
	v_cndmask_b32_e32 v61, 0, v216, vcc
	v_sub_f32_e32 v117, v60, v61
	v_mul_f32_e64 v61, |v62|, s8
	v_exp_f32_e32 v61, v61
	v_max_f32_e32 v60, v62, v62
	v_min_f32_e32 v60, 0, v60
	v_add_f32_e32 v61, 1.0, v61
	v_cmp_gt_f32_e32 vcc, s37, v61
	s_nop 1
	v_cndmask_b32_e64 v76, 0, 32, vcc
	v_ldexp_f32 v61, v61, v76
	v_log_f32_e32 v61, v61
	s_nop 0
	v_mul_f32_e32 v76, 0x3f317217, v61
	v_fma_f32 v76, v61, s33, -v76
	v_fmac_f32_e32 v76, 0x3377d1cf, v61
	v_fmac_f32_e32 v76, 0x3f317217, v61
	v_cmp_lt_f32_e64 s[44:45], |v61|, s36
	s_nop 1
	v_cndmask_b32_e64 v61, v61, v76, s[44:45]
	v_cndmask_b32_e32 v76, 0, v216, vcc
	v_sub_f32_e32 v76, v61, v76
	v_mul_f32_e32 v61, 0xbfb8aa3b, v62
	v_exp_f32_e32 v61, v61
	s_nop 0
	v_add_f32_e32 v61, 1.0, v61
	v_div_scale_f32 v62, s[2:3], v61, v61, v155
	v_rcp_f32_e32 v77, v62
	s_nop 0
	v_fma_f32 v78, -v62, v77, 1.0
	v_fmac_f32_e32 v77, v78, v77
	v_div_scale_f32 v78, vcc, v155, v61, v155
	v_mul_f32_e32 v79, v78, v77
	v_fma_f32 v80, -v62, v79, v78
	v_fmac_f32_e32 v79, v80, v77
	v_fma_f32 v62, -v62, v79, v78
	v_div_fmas_f32 v62, v62, v77, v79
	v_div_fixup_f32 v61, v62, v61, v155
	v_add_f32_e32 v61, v70, v61
	v_cmp_gt_f32_e32 vcc, s37, v61
	s_nop 1
	v_cndmask_b32_e64 v62, 0, 32, vcc
	v_ldexp_f32 v61, v61, v62
	v_log_f32_e32 v61, v61
	s_nop 0
	v_mul_f32_e32 v62, 0x3f317217, v61
	v_fma_f32 v62, v61, s33, -v62
	v_fmac_f32_e32 v62, 0x3377d1cf, v61
	v_fmac_f32_e32 v62, 0x3f317217, v61
	v_cmp_lt_f32_e64 s[44:45], |v61|, s36
	s_nop 1
	v_cndmask_b32_e64 v61, v61, v62, s[44:45]
	v_cndmask_b32_e32 v62, 0, v216, vcc
	v_sub_f32_e32 v118, v61, v62
	v_mul_f32_e64 v62, |v63|, s8
	v_exp_f32_e32 v62, v62
	v_max_f32_e32 v61, v63, v63
	v_min_f32_e32 v61, 0, v61
	v_add_f32_e32 v62, 1.0, v62
	v_cmp_gt_f32_e32 vcc, s37, v62
	s_nop 1
	v_cndmask_b32_e64 v77, 0, 32, vcc
	v_ldexp_f32 v62, v62, v77
	v_log_f32_e32 v62, v62
	s_nop 0
	v_mul_f32_e32 v77, 0x3f317217, v62
	v_fma_f32 v77, v62, s33, -v77
	v_fmac_f32_e32 v77, 0x3377d1cf, v62
	v_fmac_f32_e32 v77, 0x3f317217, v62
	v_cmp_lt_f32_e64 s[44:45], |v62|, s36
	s_nop 1
	v_cndmask_b32_e64 v62, v62, v77, s[44:45]
	v_cndmask_b32_e32 v77, 0, v216, vcc
	v_sub_f32_e32 v77, v62, v77
	v_mul_f32_e32 v62, 0xbfb8aa3b, v63
	v_exp_f32_e32 v62, v62
	s_nop 0
	v_add_f32_e32 v62, 1.0, v62
	v_div_scale_f32 v63, s[2:3], v62, v62, v154
	v_rcp_f32_e32 v78, v63
	s_nop 0
	v_fma_f32 v79, -v63, v78, 1.0
	v_fmac_f32_e32 v78, v79, v78
	v_div_scale_f32 v79, vcc, v154, v62, v154
	v_mul_f32_e32 v80, v79, v78
	v_fma_f32 v81, -v63, v80, v79
	v_fmac_f32_e32 v80, v81, v78
	v_fma_f32 v63, -v63, v80, v79
	v_div_fmas_f32 v63, v63, v78, v80
	v_div_fixup_f32 v62, v63, v62, v154
	v_add_f32_e32 v62, v71, v62
	v_cmp_gt_f32_e32 vcc, s37, v62
	s_nop 1
	v_cndmask_b32_e64 v63, 0, 32, vcc
	v_ldexp_f32 v62, v62, v63
	v_log_f32_e32 v62, v62
	s_nop 0
	v_mul_f32_e32 v63, 0x3f317217, v62
	v_fma_f32 v63, v62, s33, -v63
	v_fmac_f32_e32 v63, 0x3377d1cf, v62
	v_fmac_f32_e32 v63, 0x3f317217, v62
	v_cmp_lt_f32_e64 s[44:45], |v62|, s36
	s_nop 1
	v_cndmask_b32_e64 v62, v62, v63, s[44:45]
	v_cndmask_b32_e32 v63, 0, v216, vcc
	v_sub_f32_e32 v119, v62, v63
	v_mul_f32_e64 v63, |v56|, s8
	v_exp_f32_e32 v63, v63
	v_max_f32_e32 v62, v56, v56
	v_mul_f32_e32 v56, 0xbfb8aa3b, v56
	v_exp_f32_e32 v56, v56
	v_add_f32_e32 v63, 1.0, v63
	v_cmp_gt_f32_e32 vcc, s37, v63
	v_min_f32_e32 v62, 0, v62
	v_add_f32_e32 v56, 1.0, v56
	v_cndmask_b32_e64 v78, 0, 32, vcc
	v_ldexp_f32 v63, v63, v78
	v_log_f32_e32 v63, v63
	s_nop 0
	v_mul_f32_e32 v78, 0x3f317217, v63
	v_fma_f32 v78, v63, s33, -v78
	v_fmac_f32_e32 v78, 0x3377d1cf, v63
	v_fmac_f32_e32 v78, 0x3f317217, v63
	v_cmp_lt_f32_e64 s[44:45], |v63|, s36
	s_nop 1
	v_cndmask_b32_e64 v63, v63, v78, s[44:45]
	v_cndmask_b32_e32 v78, 0, v216, vcc
	v_sub_f32_e32 v78, v63, v78
	v_div_scale_f32 v63, s[2:3], v56, v56, v157
	v_rcp_f32_e32 v79, v63
	s_nop 0
	v_fma_f32 v80, -v63, v79, 1.0
	v_fmac_f32_e32 v79, v80, v79
	v_div_scale_f32 v80, vcc, v157, v56, v157
	v_mul_f32_e32 v81, v80, v79
	v_fma_f32 v82, -v63, v81, v80
	v_fmac_f32_e32 v81, v82, v79
	v_fma_f32 v63, -v63, v81, v80
	v_div_fmas_f32 v63, v63, v79, v81
	v_div_fixup_f32 v56, v63, v56, v157
	v_add_f32_e32 v56, v68, v56
	v_cmp_gt_f32_e32 vcc, s37, v56
	s_nop 1
	v_cndmask_b32_e64 v63, 0, 32, vcc
	v_ldexp_f32 v56, v56, v63
	v_log_f32_e32 v56, v56
	s_nop 0
	v_mul_f32_e32 v63, 0x3f317217, v56
	v_fma_f32 v63, v56, s33, -v63
	v_fmac_f32_e32 v63, 0x3377d1cf, v56
	v_fmac_f32_e32 v63, 0x3f317217, v56
	v_cmp_lt_f32_e64 s[44:45], |v56|, s36
	s_nop 1
	v_cndmask_b32_e64 v56, v56, v63, s[44:45]
	v_cndmask_b32_e32 v63, 0, v216, vcc
	v_sub_f32_e32 v120, v56, v63
	v_max_f32_e32 v56, v57, v57
	v_min_f32_e32 v63, 0, v56
	v_mul_f32_e64 v56, |v57|, s8
	v_exp_f32_e32 v56, v56
	s_nop 0
	v_add_f32_e32 v56, 1.0, v56
	v_cmp_gt_f32_e32 vcc, s37, v56
	s_nop 1
	v_cndmask_b32_e64 v79, 0, 32, vcc
	v_ldexp_f32 v56, v56, v79
	v_log_f32_e32 v56, v56
	s_nop 0
	v_mul_f32_e32 v79, 0x3f317217, v56
	v_fma_f32 v79, v56, s33, -v79
	v_fmac_f32_e32 v79, 0x3377d1cf, v56
	v_fmac_f32_e32 v79, 0x3f317217, v56
	v_cmp_lt_f32_e64 s[44:45], |v56|, s36
	s_nop 1
	v_cndmask_b32_e64 v56, v56, v79, s[44:45]
	v_cndmask_b32_e32 v79, 0, v216, vcc
	v_sub_f32_e32 v79, v56, v79
	v_mul_f32_e32 v56, 0xbfb8aa3b, v57
	v_exp_f32_e32 v56, v56
	v_pk_add_f32 v[62:63], v[62:63], v[78:79] neg_lo:[0,1] neg_hi:[0,1]
	v_add_f32_e32 v56, 1.0, v56
	v_div_scale_f32 v57, s[2:3], v56, v56, v156
; template <int CTRL> __device__ __forceinline__ float dppx(float v) { return __int_as_float(__builtin_amdgcn_update_dpp(0, __float_as_int(v), CTRL, 0xf, 0xf, true)); }
; __device__ __forceinline__ float log_forget(float z, float lb) {
;   const float r0 = fminf(z, 0.f) - __logf(1.f + __expf(-fabsf(z)));
;   const float r1 = __logf(lb + (1.f - lb) / (1.f + __expf(-z)));
;   return lb <= 0.f ? r0 : r1;
; }
;   __device__ __forceinline__ void operator()(const f32x4 (&acc)[2][2][4][2], const pg8::Unit& u, int wr, int wc, int fr, int fq) const {
;     ...
;               for (int q = 0; q < 4; ++q) { const float gv = log_forget(acc[ai][bj][m][qh][q], lq[q]); g[m][q] = gv;
;                 float sc = gv; sc += dppx<0x111>(sc); sc += dppx<0x112>(sc); sc += dppx<0x114>(sc); sc += dppx<0x118>(sc);
	v_rcp_f32_e32 v80, v57
	s_nop 0
	v_fma_f32 v81, -v57, v80, 1.0
	v_fmac_f32_e32 v80, v81, v80
	v_div_scale_f32 v81, vcc, v156, v56, v156
	v_mul_f32_e32 v82, v81, v80
	v_fma_f32 v83, -v57, v82, v81
	v_fmac_f32_e32 v82, v83, v80
	v_fma_f32 v57, -v57, v82, v81
	v_div_fmas_f32 v57, v57, v80, v82
	v_div_fixup_f32 v56, v57, v56, v156
	v_add_f32_e32 v56, v69, v56
	v_cmp_gt_f32_e32 vcc, s37, v56
	s_nop 1
	v_cndmask_b32_e64 v57, 0, 32, vcc
	v_ldexp_f32 v56, v56, v57
	v_log_f32_e32 v56, v56
	s_nop 0
	v_mul_f32_e32 v57, 0x3f317217, v56
	v_fma_f32 v57, v56, s33, -v57
	v_fmac_f32_e32 v57, 0x3377d1cf, v56
	v_fmac_f32_e32 v57, 0x3f317217, v56
	v_cmp_lt_f32_e64 s[44:45], |v56|, s36
	s_nop 1
	v_cndmask_b32_e64 v56, v56, v57, s[44:45]
	v_cndmask_b32_e32 v57, 0, v216, vcc
	v_sub_f32_e32 v121, v56, v57
	v_mul_f32_e64 v57, |v58|, s8
	v_exp_f32_e32 v57, v57
	v_max_f32_e32 v56, v58, v58
	v_cndmask_b32_e64 v79, v121, v63, s[46:47]
	v_min_f32_e32 v56, 0, v56
	v_add_f32_e32 v57, 1.0, v57
	v_cmp_gt_f32_e32 vcc, s37, v57
	v_mov_b32_dpp v63, v79 row_shr:1 row_mask:0xf bank_mask:0xf bound_ctrl:1
	s_nop 0
	v_cndmask_b32_e64 v80, 0, 32, vcc
	v_ldexp_f32 v57, v57, v80
	v_log_f32_e32 v57, v57
	s_nop 0
	v_mul_f32_e32 v80, 0x3f317217, v57
	v_fma_f32 v80, v57, s33, -v80
	v_fmac_f32_e32 v80, 0x3377d1cf, v57
	v_fmac_f32_e32 v80, 0x3f317217, v57
	v_cmp_lt_f32_e64 s[44:45], |v57|, s36
	s_nop 1
	v_cndmask_b32_e64 v57, v57, v80, s[44:45]
	v_cndmask_b32_e32 v80, 0, v216, vcc
	v_sub_f32_e32 v80, v57, v80
	v_mul_f32_e32 v57, 0xbfb8aa3b, v58
	v_exp_f32_e32 v57, v57
	s_nop 0
	v_add_f32_e32 v57, 1.0, v57
	v_div_scale_f32 v58, s[2:3], v57, v57, v155
	v_rcp_f32_e32 v81, v58
	s_nop 0
	v_fma_f32 v82, -v58, v81, 1.0
	v_fmac_f32_e32 v81, v82, v81
	v_div_scale_f32 v82, vcc, v155, v57, v155
	v_mul_f32_e32 v83, v82, v81
	v_fma_f32 v102, -v58, v83, v82
	v_fmac_f32_e32 v83, v102, v81
	v_fma_f32 v58, -v58, v83, v82
	v_div_fmas_f32 v58, v58, v81, v83
	v_div_fixup_f32 v57, v58, v57, v155
	v_add_f32_e32 v57, v70, v57
	v_cmp_gt_f32_e32 vcc, s37, v57
	v_mul_f32_e64 v81, |v59|, s8
	v_exp_f32_e32 v81, v81
	v_cndmask_b32_e64 v58, 0, 32, vcc
	v_ldexp_f32 v57, v57, v58
	v_log_f32_e32 v57, v57
	v_add_f32_e32 v81, 1.0, v81
	v_mul_f32_e32 v58, 0x3f317217, v57
	v_fma_f32 v58, v57, s33, -v58
	v_fmac_f32_e32 v58, 0x3377d1cf, v57
	v_fmac_f32_e32 v58, 0x3f317217, v57
	v_cmp_lt_f32_e64 s[44:45], |v57|, s36
	s_nop 1
	v_cndmask_b32_e64 v57, v57, v58, s[44:45]
	v_cndmask_b32_e32 v58, 0, v216, vcc
	v_cmp_gt_f32_e32 vcc, s37, v81
	v_sub_f32_e32 v58, v57, v58
	v_max_f32_e32 v57, v59, v59
	v_cndmask_b32_e64 v82, 0, 32, vcc
	v_ldexp_f32 v81, v81, v82
	v_log_f32_e32 v81, v81
	v_mul_f32_e32 v59, 0xbfb8aa3b, v59
	v_exp_f32_e32 v59, v59
	v_min_f32_e32 v57, 0, v57
	v_mul_f32_e32 v82, 0x3f317217, v81
	v_fma_f32 v82, v81, s33, -v82
	v_fmac_f32_e32 v82, 0x3377d1cf, v81
	v_fmac_f32_e32 v82, 0x3f317217, v81
	v_cmp_lt_f32_e64 s[44:45], |v81|, s36
	v_add_f32_e32 v59, 1.0, v59
	s_nop 0
	v_cndmask_b32_e64 v81, v81, v82, s[44:45]
	v_cndmask_b32_e32 v82, 0, v216, vcc
	v_sub_f32_e32 v81, v81, v82
	v_div_scale_f32 v82, s[2:3], v59, v59, v154
	v_rcp_f32_e32 v83, v82
	v_pk_add_f32 v[56:57], v[56:57], v[80:81] neg_lo:[0,1] neg_hi:[0,1]
	v_fma_f32 v102, -v82, v83, 1.0
	v_fmac_f32_e32 v83, v102, v83
	v_div_scale_f32 v102, vcc, v154, v59, v154
	v_mul_f32_e32 v103, v102, v83
	v_fma_f32 v104, -v82, v103, v102
	v_fmac_f32_e32 v103, v104, v83
	v_fma_f32 v82, -v82, v103, v102
	v_div_fmas_f32 v82, v82, v83, v103
	v_div_fixup_f32 v59, v82, v59, v154
	v_add_f32_e32 v59, v71, v59
	v_cmp_gt_f32_e32 vcc, s37, v59
	v_mul_f32_e64 v83, |v52|, s8
	v_exp_f32_e32 v83, v83
	v_cndmask_b32_e64 v82, 0, 32, vcc
	v_ldexp_f32 v59, v59, v82
	v_log_f32_e32 v59, v59
	v_add_f32_e32 v83, 1.0, v83
	v_cndmask_b32_e64 v80, v58, v56, s[50:51]
	v_mul_f32_e32 v82, 0x3f317217, v59
	v_fma_f32 v82, v59, s33, -v82
	v_fmac_f32_e32 v82, 0x3377d1cf, v59
	v_fmac_f32_e32 v82, 0x3f317217, v59
	v_cmp_lt_f32_e64 s[44:45], |v59|, s36
	v_mov_b32_dpp v56, v80 row_shr:1 row_mask:0xf bank_mask:0xf bound_ctrl:1
	s_nop 0
	v_cndmask_b32_e64 v59, v59, v82, s[44:45]
	v_cndmask_b32_e32 v82, 0, v216, vcc
	v_cmp_gt_f32_e32 vcc, s37, v83
	v_sub_f32_e32 v59, v59, v82
	v_max_f32_e32 v82, v52, v52
	v_cndmask_b32_e64 v102, 0, 32, vcc
	v_ldexp_f32 v83, v83, v102
	v_log_f32_e32 v83, v83
	v_mul_f32_e32 v52, 0xbfb8aa3b, v52
	v_exp_f32_e32 v52, v52
	v_min_f32_e32 v82, 0, v82
	v_mul_f32_e32 v102, 0x3f317217, v83
	v_fma_f32 v102, v83, s33, -v102
	v_fmac_f32_e32 v102, 0x3377d1cf, v83
	v_fmac_f32_e32 v102, 0x3f317217, v83
	v_cmp_lt_f32_e64 s[44:45], |v83|, s36
	v_add_f32_e32 v52, 1.0, v52
	v_cndmask_b32_e64 v81, v59, v57, s[54:55]
	v_cndmask_b32_e64 v83, v83, v102, s[44:45]
	v_cndmask_b32_e32 v102, 0, v216, vcc
	v_sub_f32_e32 v102, v83, v102
	v_div_scale_f32 v83, s[2:3], v52, v52, v157
	v_rcp_f32_e32 v103, v83
	v_mov_b32_dpp v57, v81 row_shr:1 row_mask:0xf bank_mask:0xf bound_ctrl:1
	v_pk_add_f32 v[56:57], v[80:81], v[56:57]
	v_fma_f32 v104, -v83, v103, 1.0
	v_fmac_f32_e32 v103, v104, v103
	v_div_scale_f32 v104, vcc, v157, v52, v157
	v_mul_f32_e32 v105, v104, v103
	v_fma_f32 v106, -v83, v105, v104
	v_fmac_f32_e32 v105, v106, v103
	v_fma_f32 v83, -v83, v105, v104
	v_div_fmas_f32 v83, v83, v103, v105
	v_div_fixup_f32 v52, v83, v52, v157
	v_add_f32_e32 v52, v68, v52
	v_cmp_gt_f32_e32 vcc, s37, v52
	v_mov_b32_dpp v58, v56 row_shr:2 row_mask:0xf bank_mask:0xf bound_ctrl:1
	v_mov_b32_dpp v59, v57 row_shr:2 row_mask:0xf bank_mask:0xf bound_ctrl:1
	v_cndmask_b32_e64 v83, 0, 32, vcc
	v_ldexp_f32 v52, v52, v83
	v_log_f32_e32 v52, v52
	v_pk_add_f32 v[56:57], v[56:57], v[58:59]
	v_mul_f32_e32 v83, 0x3f317217, v52
; template <int CTRL> __device__ __forceinline__ float dppx(float v) { return __int_as_float(__builtin_amdgcn_update_dpp(0, __float_as_int(v), CTRL, 0xf, 0xf, true)); }
; __device__ __forceinline__ float log_forget(float z, float lb) {
;   const float r0 = fminf(z, 0.f) - __logf(1.f + __expf(-fabsf(z)));
;   const float r1 = __logf(lb + (1.f - lb) / (1.f + __expf(-z)));
;   return lb <= 0.f ? r0 : r1;
; }
;   __device__ __forceinline__ void operator()(const f32x4 (&acc)[2][2][4][2], const pg8::Unit& u, int wr, int wc, int fr, int fq) const {
;     ...
;                 float sc = gv; sc += dppx<0x111>(sc); sc += dppx<0x112>(sc); sc += dppx<0x114>(sc); sc += dppx<0x118>(sc);
;                 const float tot16 = __int_as_float(__builtin_amdgcn_ds_swizzle(__float_as_int(sc), 0x1F0));
	v_fma_f32 v83, v52, s33, -v83
	v_fmac_f32_e32 v83, 0x3377d1cf, v52
	v_fmac_f32_e32 v83, 0x3f317217, v52
	v_cmp_lt_f32_e64 s[44:45], |v52|, s36
	v_mov_b32_dpp v58, v56 row_shr:4 row_mask:0xf bank_mask:0xf bound_ctrl:1
	v_mov_b32_dpp v59, v57 row_shr:4 row_mask:0xf bank_mask:0xf bound_ctrl:1
	v_cndmask_b32_e64 v52, v52, v83, s[44:45]
	v_cndmask_b32_e32 v83, 0, v216, vcc
	v_sub_f32_e32 v158, v52, v83
	v_max_f32_e32 v52, v53, v53
	v_min_f32_e32 v83, 0, v52
	v_mul_f32_e64 v52, |v53|, s8
	v_exp_f32_e32 v52, v52
	v_pk_add_f32 v[56:57], v[56:57], v[58:59]
	v_add_f32_e32 v52, 1.0, v52
	v_cmp_gt_f32_e32 vcc, s37, v52
	v_mov_b32_dpp v58, v56 row_shr:8 row_mask:0xf bank_mask:0xf bound_ctrl:1
	v_mov_b32_dpp v59, v57 row_shr:8 row_mask:0xf bank_mask:0xf bound_ctrl:1
	v_cndmask_b32_e64 v103, 0, 32, vcc
	v_ldexp_f32 v52, v52, v103
	v_log_f32_e32 v52, v52
	v_pk_add_f32 v[56:57], v[56:57], v[58:59]
	ds_swizzle_b32 v58, v56 offset:swizzle(BROADCAST,16,15)
	ds_swizzle_b32 v59, v57 offset:swizzle(BROADCAST,16,15)
	v_mul_f32_e32 v103, 0x3f317217, v52
	v_fma_f32 v103, v52, s33, -v103
	v_fmac_f32_e32 v103, 0x3377d1cf, v52
	v_fmac_f32_e32 v103, 0x3f317217, v52
	v_cmp_lt_f32_e64 s[44:45], |v52|, s36
	s_nop 1
	v_cndmask_b32_e64 v52, v52, v103, s[44:45]
	v_cndmask_b32_e32 v103, 0, v216, vcc
	v_sub_f32_e32 v103, v52, v103
	v_mul_f32_e32 v52, 0xbfb8aa3b, v53
	v_exp_f32_e32 v52, v52
	v_pk_add_f32 v[82:83], v[82:83], v[102:103] neg_lo:[0,1] neg_hi:[0,1]
	v_add_f32_e32 v52, 1.0, v52
	v_div_scale_f32 v53, s[2:3], v52, v52, v156
	v_rcp_f32_e32 v104, v53
	s_nop 0
	v_fma_f32 v105, -v53, v104, 1.0
	v_fmac_f32_e32 v104, v105, v104
	v_div_scale_f32 v105, vcc, v156, v52, v156
	v_mul_f32_e32 v106, v105, v104
	v_fma_f32 v107, -v53, v106, v105
	v_fmac_f32_e32 v106, v107, v104
	v_fma_f32 v53, -v53, v106, v105
	v_div_fmas_f32 v53, v53, v104, v106
	v_div_fixup_f32 v52, v53, v52, v156
	v_add_f32_e32 v52, v69, v52
	v_cmp_gt_f32_e32 vcc, s37, v52
	s_nop 1
	v_cndmask_b32_e64 v53, 0, 32, vcc
	v_ldexp_f32 v52, v52, v53
	v_log_f32_e32 v52, v52
	s_nop 0
	v_mul_f32_e32 v53, 0x3f317217, v52
	v_fma_f32 v53, v52, s33, -v53
	v_fmac_f32_e32 v53, 0x3377d1cf, v52
	v_fmac_f32_e32 v53, 0x3f317217, v52
	v_cmp_lt_f32_e64 s[44:45], |v52|, s36
	s_nop 1
	v_cndmask_b32_e64 v52, v52, v53, s[44:45]
	v_cndmask_b32_e32 v53, 0, v216, vcc
	v_sub_f32_e32 v159, v52, v53
	v_max_f32_e32 v52, v54, v54
	v_min_f32_e32 v104, 0, v52
	v_mul_f32_e64 v52, |v54|, s8
	v_exp_f32_e32 v52, v52
	v_cndmask_b32_e64 v83, v159, v83, s[46:47]
	v_add_f32_e32 v52, 1.0, v52
	v_cmp_gt_f32_e32 vcc, s37, v52
	v_mov_b32_dpp v103, v83 row_shr:1 row_mask:0xf bank_mask:0xf bound_ctrl:1
	s_nop 0
	v_cndmask_b32_e64 v53, 0, 32, vcc
	v_ldexp_f32 v52, v52, v53
	v_log_f32_e32 v52, v52
	s_nop 0
	v_mul_f32_e32 v53, 0x3f317217, v52
	v_fma_f32 v53, v52, s33, -v53
	v_fmac_f32_e32 v53, 0x3377d1cf, v52
	v_fmac_f32_e32 v53, 0x3f317217, v52
	v_cmp_lt_f32_e64 s[44:45], |v52|, s36
	s_nop 1
	v_cndmask_b32_e64 v52, v52, v53, s[44:45]
	v_cndmask_b32_e32 v53, 0, v216, vcc
	v_sub_f32_e32 v106, v52, v53
	v_mul_f32_e32 v52, 0xbfb8aa3b, v54
	v_exp_f32_e32 v52, v52
	s_nop 0
	v_add_f32_e32 v52, 1.0, v52
	v_div_scale_f32 v53, s[2:3], v52, v52, v155
	v_rcp_f32_e32 v54, v53
	s_nop 0
	v_fma_f32 v105, -v53, v54, 1.0
	v_fmac_f32_e32 v54, v105, v54
	v_div_scale_f32 v105, vcc, v155, v52, v155
	v_mul_f32_e32 v107, v105, v54
	v_fma_f32 v108, -v53, v107, v105
	v_fmac_f32_e32 v107, v108, v54
	v_fma_f32 v53, -v53, v107, v105
	v_div_fmas_f32 v53, v53, v54, v107
	v_div_fixup_f32 v52, v53, v52, v155
	v_add_f32_e32 v52, v70, v52
	v_cmp_gt_f32_e32 vcc, s37, v52
	s_nop 1
	v_cndmask_b32_e64 v53, 0, 32, vcc
	v_ldexp_f32 v52, v52, v53
	v_log_f32_e32 v52, v52
	s_nop 0
	v_mul_f32_e32 v53, 0x3f317217, v52
	v_fma_f32 v53, v52, s33, -v53
	v_fmac_f32_e32 v53, 0x3377d1cf, v52
	v_fmac_f32_e32 v53, 0x3f317217, v52
	v_cmp_lt_f32_e64 s[44:45], |v52|, s36
	s_nop 1
	v_cndmask_b32_e64 v52, v52, v53, s[44:45]
	v_cndmask_b32_e32 v53, 0, v216, vcc
	v_sub_f32_e32 v160, v52, v53
	v_max_f32_e32 v52, v55, v55
	v_min_f32_e32 v105, 0, v52
	v_mul_f32_e64 v52, |v55|, s8
	v_exp_f32_e32 v52, v52
	s_nop 0
	v_add_f32_e32 v52, 1.0, v52
	v_cmp_gt_f32_e32 vcc, s37, v52
	s_nop 1
	v_cndmask_b32_e64 v53, 0, 32, vcc
	v_ldexp_f32 v52, v52, v53
	v_log_f32_e32 v52, v52
	s_nop 0
	v_mul_f32_e32 v53, 0x3f317217, v52
	v_fma_f32 v53, v52, s33, -v53
	v_fmac_f32_e32 v53, 0x3377d1cf, v52
	v_fmac_f32_e32 v53, 0x3f317217, v52
	v_cmp_lt_f32_e64 s[44:45], |v52|, s36
	s_nop 1
	v_cndmask_b32_e64 v52, v52, v53, s[44:45]
	v_cndmask_b32_e32 v53, 0, v216, vcc
	v_sub_f32_e32 v107, v52, v53
	v_mul_f32_e32 v52, 0xbfb8aa3b, v55
	v_exp_f32_e32 v52, v52
	s_nop 0
	v_add_f32_e32 v52, 1.0, v52
	v_div_scale_f32 v53, s[2:3], v52, v52, v154
	v_rcp_f32_e32 v54, v53
	s_nop 0
	v_fma_f32 v55, -v53, v54, 1.0
	v_fmac_f32_e32 v54, v55, v54
	v_div_scale_f32 v55, vcc, v154, v52, v154
	v_mul_f32_e32 v108, v55, v54
	v_fma_f32 v109, -v53, v108, v55
	v_fmac_f32_e32 v108, v109, v54
	v_fma_f32 v53, -v53, v108, v55
	v_div_fmas_f32 v53, v53, v54, v108
	v_div_fixup_f32 v52, v53, v52, v154
	v_add_f32_e32 v52, v71, v52
	v_cmp_gt_f32_e32 vcc, s37, v52
	s_nop 1
	v_cndmask_b32_e64 v53, 0, 32, vcc
	v_ldexp_f32 v52, v52, v53
	v_log_f32_e32 v52, v52
	s_nop 0
	v_mul_f32_e32 v53, 0x3f317217, v52
	v_fma_f32 v53, v52, s33, -v53
	v_fmac_f32_e32 v53, 0x3377d1cf, v52
	v_fmac_f32_e32 v53, 0x3f317217, v52
	v_cmp_lt_f32_e64 s[44:45], |v52|, s36
	s_nop 1
	v_cndmask_b32_e64 v52, v52, v53, s[44:45]
	v_cndmask_b32_e32 v53, 0, v216, vcc
	v_sub_f32_e32 v161, v52, v53
	v_max_f32_e32 v52, v48, v48
	v_min_f32_e32 v108, 0, v52
	v_mul_f32_e64 v52, |v48|, s8
	v_exp_f32_e32 v52, v52
	v_mul_f32_e32 v48, 0xbfb8aa3b, v48
; __device__ __forceinline__ float log_forget(float z, float lb) {
;   const float r0 = fminf(z, 0.f) - __logf(1.f + __expf(-fabsf(z)));
;   const float r1 = __logf(lb + (1.f - lb) / (1.f + __expf(-z)));
;   return lb <= 0.f ? r0 : r1;
; }
	v_exp_f32_e32 v48, v48
	v_add_f32_e32 v52, 1.0, v52
	v_cmp_gt_f32_e32 vcc, s37, v52
	v_add_f32_e32 v48, 1.0, v48
	s_nop 0
	v_cndmask_b32_e64 v53, 0, 32, vcc
	v_ldexp_f32 v52, v52, v53
	v_log_f32_e32 v52, v52
	s_nop 0
	v_mul_f32_e32 v53, 0x3f317217, v52
	v_fma_f32 v53, v52, s33, -v53
	v_fmac_f32_e32 v53, 0x3377d1cf, v52
	v_fmac_f32_e32 v53, 0x3f317217, v52
	v_cmp_lt_f32_e64 s[44:45], |v52|, s36
	s_nop 1
	v_cndmask_b32_e64 v52, v52, v53, s[44:45]
	v_cndmask_b32_e32 v53, 0, v216, vcc
	v_sub_f32_e32 v110, v52, v53
	v_div_scale_f32 v52, s[2:3], v48, v48, v157
	v_rcp_f32_e32 v53, v52
	s_nop 0
	v_fma_f32 v54, -v52, v53, 1.0
	v_fmac_f32_e32 v53, v54, v53
	v_div_scale_f32 v54, vcc, v157, v48, v157
	v_mul_f32_e32 v55, v54, v53
	v_fma_f32 v109, -v52, v55, v54
	v_fmac_f32_e32 v55, v109, v53
	v_fma_f32 v52, -v52, v55, v54
	v_div_fmas_f32 v52, v52, v53, v55
	v_div_fixup_f32 v48, v52, v48, v157
	v_add_f32_e32 v48, v68, v48
	v_cmp_gt_f32_e32 vcc, s37, v48
	s_nop 1
	v_cndmask_b32_e64 v52, 0, 32, vcc
	v_ldexp_f32 v48, v48, v52
	v_log_f32_e32 v48, v48
	s_nop 0
	v_mul_f32_e32 v52, 0x3f317217, v48
	v_fma_f32 v52, v48, s33, -v52
	v_fmac_f32_e32 v52, 0x3377d1cf, v48
	v_fmac_f32_e32 v52, 0x3f317217, v48
	v_cmp_lt_f32_e64 s[44:45], |v48|, s36
	s_nop 1
	v_cndmask_b32_e64 v48, v48, v52, s[44:45]
	v_cndmask_b32_e32 v52, 0, v216, vcc
	v_sub_f32_e32 v162, v48, v52
	v_max_f32_e32 v48, v49, v49
	v_min_f32_e32 v109, 0, v48
	v_mul_f32_e64 v48, |v49|, s8
	v_exp_f32_e32 v48, v48
	s_nop 0
	v_add_f32_e32 v48, 1.0, v48
	v_cmp_gt_f32_e32 vcc, s37, v48
	s_nop 1
	v_cndmask_b32_e64 v52, 0, 32, vcc
	v_ldexp_f32 v48, v48, v52
	v_log_f32_e32 v48, v48
	s_nop 0
	v_mul_f32_e32 v52, 0x3f317217, v48
	v_fma_f32 v52, v48, s33, -v52
	v_fmac_f32_e32 v52, 0x3377d1cf, v48
	v_fmac_f32_e32 v52, 0x3f317217, v48
	v_cmp_lt_f32_e64 s[44:45], |v48|, s36
	s_nop 1
	v_cndmask_b32_e64 v48, v48, v52, s[44:45]
	v_cndmask_b32_e32 v52, 0, v216, vcc
	v_sub_f32_e32 v111, v48, v52
	v_mul_f32_e32 v48, 0xbfb8aa3b, v49
	v_exp_f32_e32 v48, v48
	v_pk_add_f32 v[108:109], v[108:109], v[110:111] neg_lo:[0,1] neg_hi:[0,1]
	v_add_f32_e32 v48, 1.0, v48
	v_div_scale_f32 v49, s[2:3], v48, v48, v156
	v_rcp_f32_e32 v52, v49
	s_nop 0
	v_fma_f32 v53, -v49, v52, 1.0
	v_fmac_f32_e32 v52, v53, v52
	v_div_scale_f32 v53, vcc, v156, v48, v156
	v_mul_f32_e32 v54, v53, v52
	v_fma_f32 v55, -v49, v54, v53
	v_fmac_f32_e32 v54, v55, v52
	v_fma_f32 v49, -v49, v54, v53
	v_div_fmas_f32 v49, v49, v52, v54
	v_div_fixup_f32 v48, v49, v48, v156
	v_add_f32_e32 v48, v69, v48
	v_cmp_gt_f32_e32 vcc, s37, v48
	s_nop 1
	v_cndmask_b32_e64 v49, 0, 32, vcc
	v_ldexp_f32 v48, v48, v49
	v_log_f32_e32 v48, v48
	s_nop 0
	v_mul_f32_e32 v49, 0x3f317217, v48
	v_fma_f32 v49, v48, s33, -v49
	v_fmac_f32_e32 v49, 0x3377d1cf, v48
	v_fmac_f32_e32 v49, 0x3f317217, v48
	v_cmp_lt_f32_e64 s[44:45], |v48|, s36
	s_nop 1
	v_cndmask_b32_e64 v48, v48, v49, s[44:45]
	v_cndmask_b32_e32 v49, 0, v216, vcc
	v_sub_f32_e32 v163, v48, v49
	v_max_f32_e32 v48, v50, v50
	v_min_f32_e32 v112, 0, v48
	v_mul_f32_e64 v48, |v50|, s8
	v_exp_f32_e32 v48, v48
	v_cndmask_b32_e64 v109, v163, v109, s[46:47]
	v_add_f32_e32 v48, 1.0, v48
	v_cmp_gt_f32_e32 vcc, s37, v48
	v_mov_b32_dpp v111, v109 row_shr:1 row_mask:0xf bank_mask:0xf bound_ctrl:1
	s_nop 0
	v_cndmask_b32_e64 v49, 0, 32, vcc
	v_ldexp_f32 v48, v48, v49
	v_log_f32_e32 v48, v48
	s_nop 0
	v_mul_f32_e32 v49, 0x3f317217, v48
	v_fma_f32 v49, v48, s33, -v49
	v_fmac_f32_e32 v49, 0x3377d1cf, v48
	v_fmac_f32_e32 v49, 0x3f317217, v48
	v_cmp_lt_f32_e64 s[44:45], |v48|, s36
	s_nop 1
	v_cndmask_b32_e64 v48, v48, v49, s[44:45]
	v_cndmask_b32_e32 v49, 0, v216, vcc
	v_sub_f32_e32 v114, v48, v49
	v_mul_f32_e32 v48, 0xbfb8aa3b, v50
	v_exp_f32_e32 v48, v48
	s_nop 0
	v_add_f32_e32 v48, 1.0, v48
	v_div_scale_f32 v49, s[2:3], v48, v48, v155
	v_rcp_f32_e32 v50, v49
	s_nop 0
	v_fma_f32 v52, -v49, v50, 1.0
	v_fmac_f32_e32 v50, v52, v50
	v_div_scale_f32 v52, vcc, v155, v48, v155
	v_mul_f32_e32 v53, v52, v50
	v_fma_f32 v54, -v49, v53, v52
	v_fmac_f32_e32 v53, v54, v50
	v_fma_f32 v49, -v49, v53, v52
	v_div_fmas_f32 v49, v49, v50, v53
	v_div_fixup_f32 v48, v49, v48, v155
	v_add_f32_e32 v48, v70, v48
	v_cmp_gt_f32_e32 vcc, s37, v48
	s_nop 1
	v_cndmask_b32_e64 v49, 0, 32, vcc
	v_ldexp_f32 v48, v48, v49
	v_log_f32_e32 v48, v48
	s_nop 0
	v_mul_f32_e32 v49, 0x3f317217, v48
	v_fma_f32 v49, v48, s33, -v49
	v_fmac_f32_e32 v49, 0x3377d1cf, v48
	v_fmac_f32_e32 v49, 0x3f317217, v48
	v_cmp_lt_f32_e64 s[44:45], |v48|, s36
	s_nop 1
	v_cndmask_b32_e64 v48, v48, v49, s[44:45]
	v_cndmask_b32_e32 v49, 0, v216, vcc
	v_sub_f32_e32 v164, v48, v49
	v_max_f32_e32 v48, v51, v51
	v_min_f32_e32 v113, 0, v48
	v_mul_f32_e64 v48, |v51|, s8
	v_exp_f32_e32 v48, v48
	s_nop 0
	v_add_f32_e32 v48, 1.0, v48
	v_cmp_gt_f32_e32 vcc, s37, v48
	s_nop 1
	v_cndmask_b32_e64 v49, 0, 32, vcc
	v_ldexp_f32 v48, v48, v49
	v_log_f32_e32 v48, v48
	s_nop 0
	v_mul_f32_e32 v49, 0x3f317217, v48
	v_fma_f32 v49, v48, s33, -v49
	v_fmac_f32_e32 v49, 0x3377d1cf, v48
	v_fmac_f32_e32 v49, 0x3f317217, v48
	v_cmp_lt_f32_e64 s[44:45], |v48|, s36
	s_nop 1
	v_cndmask_b32_e64 v48, v48, v49, s[44:45]
	v_cndmask_b32_e32 v49, 0, v216, vcc
	v_sub_f32_e32 v115, v48, v49
	v_mul_f32_e32 v48, 0xbfb8aa3b, v51
	v_exp_f32_e32 v48, v48
	v_pk_add_f32 v[112:113], v[112:113], v[114:115] neg_lo:[0,1] neg_hi:[0,1]
	v_add_f32_e32 v48, 1.0, v48
	v_div_scale_f32 v49, s[2:3], v48, v48, v154
	v_rcp_f32_e32 v50, v49
	v_cndmask_b32_e64 v112, v164, v112, s[50:51]
	v_fma_f32 v51, -v49, v50, 1.0
	v_fmac_f32_e32 v50, v51, v50
	v_div_scale_f32 v51, vcc, v154, v48, v154
	v_mul_f32_e32 v52, v51, v50
	v_fma_f32 v53, -v49, v52, v51
	v_fmac_f32_e32 v52, v53, v50
; template <int CTRL> __device__ __forceinline__ float dppx(float v) { return __int_as_float(__builtin_amdgcn_update_dpp(0, __float_as_int(v), CTRL, 0xf, 0xf, true)); }
;   __device__ __forceinline__ void operator()(const f32x4 (&acc)[2][2][4][2], const pg8::Unit& u, int wr, int wc, int fr, int fq) const {
;     ...
;               for (int q = 0; q < 4; ++q) { const float gv = log_forget(acc[ai][bj][m][qh][q], lq[q]); g[m][q] = gv;
;                 float sc = gv; sc += dppx<0x111>(sc); sc += dppx<0x112>(sc); sc += dppx<0x114>(sc); sc += dppx<0x118>(sc);
;                 const float tot16 = __int_as_float(__builtin_amdgcn_ds_swizzle(__float_as_int(sc), 0x1F0));
;                 cs[m][q] = sc + carry[q]; carry[q] += tot16; }
; #pragma unroll
;             for (int m = 0; m < 4; ++m) { const int r = row0 + ai * 128 + m * 16; float bq[4], kq[4];
; #pragma unroll
;               for (int q = 0; q < 4; ++q) { bq[q] = bwd ? (carry[q] - cs[m][q]) + g[m][q] : cs[m][q]; kq[q] = 1.f - __expf(g[m][q]); }
;               *(f32x4*)(logfp + (size_t)r * 1024 + c + 4 * qh) = (f32x4){bq[0], bq[1], bq[2], bq[3]};
	v_fma_f32 v49, -v49, v52, v51
	v_div_fmas_f32 v49, v49, v50, v52
	v_div_fixup_f32 v48, v49, v48, v154
	v_add_f32_e32 v48, v71, v48
	v_cmp_gt_f32_e32 vcc, s37, v48
	v_mov_b32_dpp v114, v112 row_shr:1 row_mask:0xf bank_mask:0xf bound_ctrl:1
	s_nop 0
	v_cndmask_b32_e64 v49, 0, 32, vcc
	v_ldexp_f32 v48, v48, v49
	v_log_f32_e32 v48, v48
	s_nop 0
	v_mul_f32_e32 v49, 0x3f317217, v48
	v_fma_f32 v49, v48, s33, -v49
	v_fmac_f32_e32 v49, 0x3377d1cf, v48
	v_fmac_f32_e32 v49, 0x3f317217, v48
	v_cmp_lt_f32_e64 s[44:45], |v48|, s36
	s_nop 1
	v_cndmask_b32_e64 v48, v48, v49, s[44:45]
	v_cndmask_b32_e32 v49, 0, v216, vcc
	v_sub_f32_e32 v165, v48, v49
	v_pk_add_f32 v[48:49], v[72:73], v[74:75] neg_lo:[0,1] neg_hi:[0,1]
	v_cmp_ge_f32_e64 s[44:45], 0, v68
	v_cndmask_b32_e64 v73, v117, v49, s[46:47]
	v_cndmask_b32_e64 v113, v165, v113, s[54:55]
	v_cndmask_b32_e64 v72, v116, v48, s[44:45]
	v_mov_b32_dpp v49, v73 row_shr:1 row_mask:0xf bank_mask:0xf bound_ctrl:1
	v_cndmask_b32_e64 v78, v120, v62, s[44:45]
	v_mov_b32_dpp v48, v72 row_shr:1 row_mask:0xf bank_mask:0xf bound_ctrl:1
	v_pk_add_f32 v[48:49], v[72:73], v[48:49]
	v_mov_b32_dpp v62, v78 row_shr:1 row_mask:0xf bank_mask:0xf bound_ctrl:1
	v_cndmask_b32_e64 v82, v158, v82, s[44:45]
	v_mov_b32_dpp v50, v48 row_shr:2 row_mask:0xf bank_mask:0xf bound_ctrl:1
	v_mov_b32_dpp v51, v49 row_shr:2 row_mask:0xf bank_mask:0xf bound_ctrl:1
	v_pk_add_f32 v[48:49], v[48:49], v[50:51]
	v_pk_add_f32 v[62:63], v[78:79], v[62:63]
	v_mov_b32_dpp v102, v82 row_shr:1 row_mask:0xf bank_mask:0xf bound_ctrl:1
	v_mov_b32_dpp v50, v48 row_shr:4 row_mask:0xf bank_mask:0xf bound_ctrl:1
	v_mov_b32_dpp v51, v49 row_shr:4 row_mask:0xf bank_mask:0xf bound_ctrl:1
	v_pk_add_f32 v[48:49], v[48:49], v[50:51]
	v_pk_add_f32 v[102:103], v[82:83], v[102:103]
	v_cndmask_b32_e64 v108, v162, v108, s[44:45]
	v_mov_b32_dpp v50, v48 row_shr:8 row_mask:0xf bank_mask:0xf bound_ctrl:1
	v_mov_b32_dpp v51, v49 row_shr:8 row_mask:0xf bank_mask:0xf bound_ctrl:1
	v_pk_add_f32 v[48:49], v[48:49], v[50:51]
	ds_swizzle_b32 v50, v48 offset:swizzle(BROADCAST,16,15)
	v_pk_add_f32 v[74:75], v[48:49], 0 op_sel_hi:[1,0]
	v_mul_f32_e32 v48, 0x3fb8aa3b, v72
	v_exp_f32_e32 v48, v48
	ds_swizzle_b32 v51, v49 offset:swizzle(BROADCAST,16,15)
	v_mov_b32_dpp v110, v108 row_shr:1 row_mask:0xf bank_mask:0xf bound_ctrl:1
	v_pk_add_f32 v[110:111], v[108:109], v[110:111]
	v_sub_f32_e32 v168, 1.0, v48
	v_mul_f32_e32 v48, 0x3fb8aa3b, v73
	v_exp_f32_e32 v48, v48
	s_waitcnt lgkmcnt(0)
	v_pk_add_f32 v[166:167], v[50:51], 0 op_sel_hi:[1,0]
	v_mov_b32_dpp v115, v113 row_shr:1 row_mask:0xf bank_mask:0xf bound_ctrl:1
	v_pk_add_f32 v[114:115], v[112:113], v[114:115]
	v_sub_f32_e32 v169, 1.0, v48
	v_pk_add_f32 v[48:49], v[60:61], v[76:77] neg_lo:[0,1] neg_hi:[0,1]
	s_nop 0
	v_cndmask_b32_e64 v77, v119, v49, s[54:55]
	v_cndmask_b32_e64 v76, v118, v48, s[50:51]
	v_mov_b32_dpp v118, v62 row_shr:2 row_mask:0xf bank_mask:0xf bound_ctrl:1
	v_mov_b32_dpp v49, v77 row_shr:1 row_mask:0xf bank_mask:0xf bound_ctrl:1
	v_mov_b32_dpp v48, v76 row_shr:1 row_mask:0xf bank_mask:0xf bound_ctrl:1
	v_pk_add_f32 v[48:49], v[76:77], v[48:49]
	v_mov_b32_dpp v119, v63 row_shr:2 row_mask:0xf bank_mask:0xf bound_ctrl:1
	v_pk_add_f32 v[62:63], v[62:63], v[118:119]
	v_mov_b32_dpp v50, v48 row_shr:2 row_mask:0xf bank_mask:0xf bound_ctrl:1
	v_mov_b32_dpp v51, v49 row_shr:2 row_mask:0xf bank_mask:0xf bound_ctrl:1
	v_pk_add_f32 v[48:49], v[48:49], v[50:51]
	v_mov_b32_dpp v118, v62 row_shr:4 row_mask:0xf bank_mask:0xf bound_ctrl:1
	v_mov_b32_dpp v119, v63 row_shr:4 row_mask:0xf bank_mask:0xf bound_ctrl:1
	v_mov_b32_dpp v50, v48 row_shr:4 row_mask:0xf bank_mask:0xf bound_ctrl:1
	v_mov_b32_dpp v51, v49 row_shr:4 row_mask:0xf bank_mask:0xf bound_ctrl:1
	v_pk_add_f32 v[48:49], v[48:49], v[50:51]
	v_pk_add_f32 v[62:63], v[62:63], v[118:119]
	s_nop 0
	v_mov_b32_dpp v50, v48 row_shr:8 row_mask:0xf bank_mask:0xf bound_ctrl:1
	v_mov_b32_dpp v51, v49 row_shr:8 row_mask:0xf bank_mask:0xf bound_ctrl:1
	v_pk_add_f32 v[48:49], v[48:49], v[50:51]
	ds_swizzle_b32 v50, v48 offset:swizzle(BROADCAST,16,15)
	ds_swizzle_b32 v51, v49 offset:swizzle(BROADCAST,16,15)
	v_mov_b32_dpp v118, v62 row_shr:8 row_mask:0xf bank_mask:0xf bound_ctrl:1
	v_mov_b32_dpp v119, v63 row_shr:8 row_mask:0xf bank_mask:0xf bound_ctrl:1
	v_pk_add_f32 v[62:63], v[62:63], v[118:119]
	ds_swizzle_b32 v120, v62 offset:swizzle(BROADCAST,16,15)
	s_waitcnt lgkmcnt(1)
	v_pk_add_f32 v[60:61], v[50:51], 0 op_sel_hi:[1,0]
	v_lshlrev_b64 v[50:51], 2, v[96:97]
	v_lshl_add_u64 v[54:55], v[122:123], 0, v[50:51]
	v_mov_b32_dpp v122, v102 row_shr:2 row_mask:0xf bank_mask:0xf bound_ctrl:1
	v_mov_b32_dpp v123, v103 row_shr:2 row_mask:0xf bank_mask:0xf bound_ctrl:1
	v_pk_add_f32 v[102:103], v[102:103], v[122:123]
	ds_swizzle_b32 v121, v63 offset:swizzle(BROADCAST,16,15)
	v_pk_add_f32 v[118:119], v[166:167], v[62:63]
	v_mov_b32_dpp v122, v102 row_shr:4 row_mask:0xf bank_mask:0xf bound_ctrl:1
	v_mov_b32_dpp v123, v103 row_shr:4 row_mask:0xf bank_mask:0xf bound_ctrl:1
	v_pk_add_f32 v[102:103], v[102:103], v[122:123]
	s_waitcnt lgkmcnt(0)
	v_pk_add_f32 v[62:63], v[166:167], v[120:121]
	v_mul_f32_e32 v120, 0x3fb8aa3b, v79
	v_mov_b32_dpp v122, v102 row_shr:8 row_mask:0xf bank_mask:0xf bound_ctrl:1
	v_mov_b32_dpp v123, v103 row_shr:8 row_mask:0xf bank_mask:0xf bound_ctrl:1
	v_pk_add_f32 v[102:103], v[102:103], v[122:123]
	ds_swizzle_b32 v122, v102 offset:swizzle(BROADCAST,16,15)
	ds_swizzle_b32 v123, v103 offset:swizzle(BROADCAST,16,15)
	v_exp_f32_e32 v120, v120
	v_pk_add_f32 v[102:103], v[62:63], v[102:103]
	v_pk_add_f32 v[116:117], v[48:49], 0 op_sel_hi:[1,0]
	v_mul_f32_e32 v48, 0x3fb8aa3b, v76
	s_waitcnt lgkmcnt(0)
; __device__ __forceinline__ unsigned cvt_pk_bf16(float lo, float hi) { unsigned r; asm volatile("v_cvt_pk_bf16_f32 %0, %1, %2" : "=v"(r) : "v"(lo), "v"(hi)); return r; }
;   __device__ __forceinline__ void operator()(const f32x4 (&acc)[2][2][4][2], const pg8::Unit& u, int wr, int wc, int fr, int fq) const {
;     ...
;             for (int m = 0; m < 4; ++m) { const int r = row0 + ai * 128 + m * 16; float bq[4], kq[4];
; #pragma unroll
;               for (int q = 0; q < 4; ++q) { bq[q] = bwd ? (carry[q] - cs[m][q]) + g[m][q] : cs[m][q]; kq[q] = 1.f - __expf(g[m][q]); }
;               *(f32x4*)(logfp + (size_t)r * 1024 + c + 4 * qh) = (f32x4){bq[0], bq[1], bq[2], bq[3]};
;               u32x2 w; w.x = pg8::cvt_pk_bf16(kq[0], kq[1]); w.y = pg8::cvt_pk_bf16(kq[2], kq[3]);
;               *(u32x2*)(km + (size_t)r * 1024 + c + 4 * qh) = w; } } }
	v_pk_add_f32 v[122:123], v[62:63], v[122:123]
	v_mul_f32_e32 v62, 0x3fb8aa3b, v82
	v_exp_f32_e32 v62, v62
	v_sub_f32_e32 v166, 1.0, v120
	v_pk_add_f32 v[120:121], v[60:61], v[56:57]
	v_pk_add_f32 v[60:61], v[60:61], v[58:59]
	v_lshl_add_u64 v[58:59], v[126:127], 0, v[50:51]
	v_mov_b32_dpp v126, v110 row_shr:2 row_mask:0xf bank_mask:0xf bound_ctrl:1
	v_mov_b32_dpp v127, v111 row_shr:2 row_mask:0xf bank_mask:0xf bound_ctrl:1
	v_sub_f32_e32 v158, 1.0, v62
	v_mul_f32_e32 v62, 0x3fb8aa3b, v83
	v_pk_add_f32 v[110:111], v[110:111], v[126:127]
	v_exp_f32_e32 v62, v62
	v_exp_f32_e32 v48, v48
	v_mov_b32_dpp v126, v110 row_shr:4 row_mask:0xf bank_mask:0xf bound_ctrl:1
	v_mov_b32_dpp v127, v111 row_shr:4 row_mask:0xf bank_mask:0xf bound_ctrl:1
	v_pk_add_f32 v[110:111], v[110:111], v[126:127]
	v_sub_f32_e32 v159, 1.0, v62
	v_pk_add_f32 v[62:63], v[104:105], v[106:107] neg_lo:[0,1] neg_hi:[0,1]
	v_mov_b32_dpp v126, v110 row_shr:8 row_mask:0xf bank_mask:0xf bound_ctrl:1
	v_mov_b32_dpp v127, v111 row_shr:8 row_mask:0xf bank_mask:0xf bound_ctrl:1
	v_pk_add_f32 v[110:111], v[110:111], v[126:127]
	ds_swizzle_b32 v126, v110 offset:swizzle(BROADCAST,16,15)
	ds_swizzle_b32 v127, v111 offset:swizzle(BROADCAST,16,15)
	v_cndmask_b32_e64 v105, v161, v63, s[54:55]
	v_cndmask_b32_e64 v104, v160, v62, s[50:51]
	v_sub_f32_e32 v170, 1.0, v48
	v_mov_b32_dpp v63, v105 row_shr:1 row_mask:0xf bank_mask:0xf bound_ctrl:1
	v_mov_b32_dpp v62, v104 row_shr:1 row_mask:0xf bank_mask:0xf bound_ctrl:1
	v_pk_add_f32 v[62:63], v[104:105], v[62:63]
	v_mul_f32_e32 v48, 0x3fb8aa3b, v77
	v_exp_f32_e32 v48, v48
	v_mov_b32_dpp v106, v62 row_shr:2 row_mask:0xf bank_mask:0xf bound_ctrl:1
	v_mov_b32_dpp v107, v63 row_shr:2 row_mask:0xf bank_mask:0xf bound_ctrl:1
	v_pk_add_f32 v[62:63], v[62:63], v[106:107]
	v_pk_add_f32 v[110:111], v[122:123], v[110:111]
	s_waitcnt lgkmcnt(0)
	v_pk_add_f32 v[122:123], v[122:123], v[126:127]
	v_mul_f32_e32 v126, 0x3fb8aa3b, v108
	v_mov_b32_dpp v106, v62 row_shr:4 row_mask:0xf bank_mask:0xf bound_ctrl:1
	v_mov_b32_dpp v107, v63 row_shr:4 row_mask:0xf bank_mask:0xf bound_ctrl:1
	v_exp_f32_e32 v126, v126
	v_pk_add_f32 v[62:63], v[62:63], v[106:107]
	v_sub_f32_e32 v171, 1.0, v48
	v_lshlrev_b64 v[48:49], 1, v[96:97]
	v_mov_b32_dpp v106, v62 row_shr:8 row_mask:0xf bank_mask:0xf bound_ctrl:1
	v_mov_b32_dpp v107, v63 row_shr:8 row_mask:0xf bank_mask:0xf bound_ctrl:1
	v_pk_add_f32 v[62:63], v[62:63], v[106:107]
	v_lshl_add_u64 v[52:53], v[124:125], 0, v[48:49]
	ds_swizzle_b32 v106, v62 offset:swizzle(BROADCAST,16,15)
	ds_swizzle_b32 v107, v63 offset:swizzle(BROADCAST,16,15)
	v_pk_add_f32 v[124:125], v[60:61], v[62:63]
	v_lshl_add_u64 v[62:63], v[130:131], 0, v[50:51]
	v_sub_f32_e32 v130, 1.0, v126
	v_mul_f32_e32 v126, 0x3fb8aa3b, v109
	v_exp_f32_e32 v126, v126
	v_mov_b32_dpp v127, v115 row_shr:2 row_mask:0xf bank_mask:0xf bound_ctrl:1
	v_mul_f32_e32 v56, 0x3fb8aa3b, v80
	v_exp_f32_e32 v56, v56
	v_sub_f32_e32 v131, 1.0, v126
	v_mov_b32_dpp v126, v114 row_shr:2 row_mask:0xf bank_mask:0xf bound_ctrl:1
	v_pk_add_f32 v[114:115], v[114:115], v[126:127]
	v_sub_f32_e32 v167, 1.0, v56
	v_mul_f32_e32 v56, 0x3fb8aa3b, v81
	v_mov_b32_dpp v126, v114 row_shr:4 row_mask:0xf bank_mask:0xf bound_ctrl:1
	v_mov_b32_dpp v127, v115 row_shr:4 row_mask:0xf bank_mask:0xf bound_ctrl:1
	v_pk_add_f32 v[114:115], v[114:115], v[126:127]
	v_exp_f32_e32 v56, v56
	s_waitcnt lgkmcnt(0)
	v_pk_add_f32 v[106:107], v[60:61], v[106:107]
	v_mov_b32_dpp v126, v114 row_shr:8 row_mask:0xf bank_mask:0xf bound_ctrl:1
	v_mov_b32_dpp v127, v115 row_shr:8 row_mask:0xf bank_mask:0xf bound_ctrl:1
	v_pk_add_f32 v[114:115], v[114:115], v[126:127]
	ds_swizzle_b32 v126, v114 offset:swizzle(BROADCAST,16,15)
	ds_swizzle_b32 v127, v115 offset:swizzle(BROADCAST,16,15)
	v_pk_add_f32 v[114:115], v[106:107], v[114:115]
	v_sub_f32_e32 v172, 1.0, v56
	v_lshl_add_u64 v[56:57], v[128:129], 0, v[48:49]
	v_mul_f32_e32 v60, 0x3fb8aa3b, v104
	s_waitcnt lgkmcnt(0)
	v_pk_add_f32 v[106:107], v[106:107], v[126:127]
	v_pk_add_f32 v[126:127], v[122:123], v[74:75] neg_lo:[0,1] neg_hi:[0,1]
	v_pk_add_f32 v[128:129], v[106:107], v[116:117] neg_lo:[0,1] neg_hi:[0,1]
	v_pk_add_f32 v[72:73], v[72:73], v[126:127]
	v_pk_add_f32 v[76:77], v[76:77], v[128:129]
	v_mul_f32_e32 v96, 0x3fb8aa3b, v78
	v_exp_f32_e32 v60, v60
	v_cndmask_b32_e64 v77, v117, v77, s[42:43]
	v_cndmask_b32_e64 v76, v116, v76, s[42:43]
	v_cndmask_b32_e64 v75, v75, v73, s[42:43]
	v_cndmask_b32_e64 v74, v74, v72, s[42:43]
	v_exp_f32_e32 v96, v96
	global_store_dwordx4 v[54:55], v[74:77], off
	v_cvt_pk_bf16_f32 v72, v168, v169
	v_cvt_pk_bf16_f32 v73, v170, v171
	global_store_dwordx2 v[52:53], v[72:73], off
	v_pk_add_f32 v[72:73], v[122:123], v[118:119] neg_lo:[0,1] neg_hi:[0,1]
	v_pk_add_f32 v[74:75], v[106:107], v[120:121] neg_lo:[0,1] neg_hi:[0,1]
	v_pk_add_f32 v[72:73], v[78:79], v[72:73]
	v_pk_add_f32 v[74:75], v[80:81], v[74:75]
	v_sub_f32_e32 v160, 1.0, v60
	v_mul_f32_e32 v60, 0x3fb8aa3b, v105
	v_cndmask_b32_e64 v75, v121, v75, s[42:43]
	v_cndmask_b32_e64 v74, v120, v74, s[42:43]
	v_cndmask_b32_e64 v73, v119, v73, s[42:43]
	v_cndmask_b32_e64 v72, v118, v72, s[42:43]
	v_sub_f32_e32 v96, 1.0, v96
	v_exp_f32_e32 v60, v60
	global_store_dwordx4 v[58:59], v[72:75], off
	v_sub_f32_e32 v161, 1.0, v60
	s_nop 0
	v_cvt_pk_bf16_f32 v72, v96, v166
	v_cvt_pk_bf16_f32 v73, v167, v172
	global_store_dwordx2 v[56:57], v[72:73], off
	v_pk_add_f32 v[72:73], v[122:123], v[102:103] neg_lo:[0,1] neg_hi:[0,1]
	v_pk_add_f32 v[74:75], v[106:107], v[124:125] neg_lo:[0,1] neg_hi:[0,1]
	v_pk_add_f32 v[72:73], v[82:83], v[72:73]
	v_pk_add_f32 v[74:75], v[104:105], v[74:75]
	v_cndmask_b32_e64 v73, v103, v73, s[42:43]
; __device__ __forceinline__ unsigned cvt_pk_bf16(float lo, float hi) { unsigned r; asm volatile("v_cvt_pk_bf16_f32 %0, %1, %2" : "=v"(r) : "v"(lo), "v"(hi)); return r; }
; __device__ __forceinline__ float log_forget(float z, float lb) {
;   const float r0 = fminf(z, 0.f) - __logf(1.f + __expf(-fabsf(z)));
;   const float r1 = __logf(lb + (1.f - lb) / (1.f + __expf(-z)));
;   return lb <= 0.f ? r0 : r1;
; }
;   __device__ __forceinline__ void operator()(const f32x4 (&acc)[2][2][4][2], const pg8::Unit& u, int wr, int wc, int fr, int fq) const {
;     ...
;             for (int m = 0; m < 4; ++m) { const int r = row0 + ai * 128 + m * 16; float bq[4], kq[4];
; #pragma unroll
;               for (int q = 0; q < 4; ++q) { bq[q] = bwd ? (carry[q] - cs[m][q]) + g[m][q] : cs[m][q]; kq[q] = 1.f - __expf(g[m][q]); }
;               *(f32x4*)(logfp + (size_t)r * 1024 + c + 4 * qh) = (f32x4){bq[0], bq[1], bq[2], bq[3]};
;               u32x2 w; w.x = pg8::cvt_pk_bf16(kq[0], kq[1]); w.y = pg8::cvt_pk_bf16(kq[2], kq[3]);
;               *(u32x2*)(km + (size_t)r * 1024 + c + 4 * qh) = w; } } }
	v_cndmask_b32_e64 v75, v125, v75, s[42:43]
	v_cndmask_b32_e64 v74, v124, v74, s[42:43]
	v_cndmask_b32_e64 v72, v102, v72, s[42:43]
	v_lshl_add_u64 v[60:61], v[132:133], 0, v[48:49]
	global_store_dwordx4 v[62:63], v[72:75], off
	s_nop 1
	v_cvt_pk_bf16_f32 v72, v158, v159
	v_cvt_pk_bf16_f32 v73, v160, v161
	global_store_dwordx2 v[60:61], v[72:73], off
	v_mul_f32_e32 v72, 0x3fb8aa3b, v112
	v_exp_f32_e32 v72, v72
	v_pk_add_f32 v[74:75], v[106:107], v[114:115] neg_lo:[0,1] neg_hi:[0,1]
	v_sub_f32_e32 v78, 1.0, v72
	v_pk_add_f32 v[72:73], v[122:123], v[110:111] neg_lo:[0,1] neg_hi:[0,1]
	v_pk_add_f32 v[74:75], v[112:113], v[74:75]
	v_pk_add_f32 v[72:73], v[108:109], v[72:73]
	v_cndmask_b32_e64 v76, v114, v74, s[42:43]
	v_cndmask_b32_e64 v74, v110, v72, s[42:43]
	v_mul_f32_e32 v72, 0x3fb8aa3b, v113
	v_exp_f32_e32 v72, v72
	v_cndmask_b32_e64 v77, v115, v75, s[42:43]
	v_cndmask_b32_e64 v75, v111, v73, s[42:43]
	v_sub_f32_e32 v114, 1.0, v64
	v_sub_f32_e32 v79, 1.0, v72
	v_lshl_add_u64 v[72:73], v[134:135], 0, v[50:51]
	global_store_dwordx4 v[72:73], v[74:77], off
	v_sub_f32_e32 v113, 1.0, v65
	v_sub_f32_e32 v112, 1.0, v66
	v_cvt_pk_bf16_f32 v76, v130, v131
	v_cvt_pk_bf16_f32 v77, v78, v79
	v_lshl_add_u64 v[74:75], v[136:137], 0, v[48:49]
	global_store_dwordx2 v[74:75], v[76:77], off
	v_mul_f32_e64 v77, |v44|, s8
	v_exp_f32_e32 v77, v77
	v_max_f32_e32 v76, v44, v44
	v_mul_f32_e32 v44, 0xbfb8aa3b, v44
	v_exp_f32_e32 v44, v44
	v_add_f32_e32 v77, 1.0, v77
	v_cmp_gt_f32_e32 vcc, s37, v77
	v_min_f32_e32 v76, 0, v76
	v_add_f32_e32 v44, 1.0, v44
	v_cndmask_b32_e64 v78, 0, 32, vcc
	v_ldexp_f32 v77, v77, v78
	v_log_f32_e32 v77, v77
	s_nop 0
	v_mul_f32_e32 v78, 0x3f317217, v77
	v_fma_f32 v78, v77, s33, -v78
	v_fmac_f32_e32 v78, 0x3377d1cf, v77
	v_fmac_f32_e32 v78, 0x3f317217, v77
	v_cmp_lt_f32_e64 s[48:49], |v77|, s36
	s_nop 1
	v_cndmask_b32_e64 v77, v77, v78, s[48:49]
	v_cndmask_b32_e32 v78, 0, v216, vcc
	v_sub_f32_e32 v78, v77, v78
	v_div_scale_f32 v77, s[2:3], v44, v44, v114
	v_rcp_f32_e32 v79, v77
	s_nop 0
	v_fma_f32 v80, -v77, v79, 1.0
	v_fmac_f32_e32 v79, v80, v79
	v_div_scale_f32 v80, vcc, v114, v44, v114
	v_mul_f32_e32 v81, v80, v79
	v_fma_f32 v82, -v77, v81, v80
	v_fmac_f32_e32 v81, v82, v79
	v_fma_f32 v77, -v77, v81, v80
	v_div_fmas_f32 v77, v77, v79, v81
	v_div_fixup_f32 v44, v77, v44, v114
	v_add_f32_e32 v44, v64, v44
	v_cmp_gt_f32_e32 vcc, s37, v44
	s_nop 1
	v_cndmask_b32_e64 v77, 0, 32, vcc
	v_ldexp_f32 v44, v44, v77
	v_log_f32_e32 v44, v44
	s_nop 0
	v_mul_f32_e32 v77, 0x3f317217, v44
	v_fma_f32 v77, v44, s33, -v77
	v_fmac_f32_e32 v77, 0x3377d1cf, v44
	v_fmac_f32_e32 v77, 0x3f317217, v44
	v_cmp_lt_f32_e64 s[48:49], |v44|, s36
	s_nop 1
	v_cndmask_b32_e64 v44, v44, v77, s[48:49]
	v_cndmask_b32_e32 v77, 0, v216, vcc
	v_sub_f32_e32 v115, v44, v77
	v_max_f32_e32 v44, v45, v45
	v_min_f32_e32 v77, 0, v44
	v_mul_f32_e64 v44, |v45|, s8
	v_exp_f32_e32 v44, v44
	s_nop 0
	v_add_f32_e32 v44, 1.0, v44
	v_cmp_gt_f32_e32 vcc, s37, v44
	s_nop 1
	v_cndmask_b32_e64 v79, 0, 32, vcc
	v_ldexp_f32 v44, v44, v79
	v_log_f32_e32 v44, v44
	s_nop 0
	v_mul_f32_e32 v79, 0x3f317217, v44
	v_fma_f32 v79, v44, s33, -v79
	v_fmac_f32_e32 v79, 0x3377d1cf, v44
	v_fmac_f32_e32 v79, 0x3f317217, v44
	v_cmp_lt_f32_e64 s[48:49], |v44|, s36
	s_nop 1
	v_cndmask_b32_e64 v44, v44, v79, s[48:49]
	v_cndmask_b32_e32 v79, 0, v216, vcc
	v_sub_f32_e32 v79, v44, v79
	v_mul_f32_e32 v44, 0xbfb8aa3b, v45
	v_exp_f32_e32 v44, v44
	s_nop 0
	v_add_f32_e32 v44, 1.0, v44
	v_div_scale_f32 v45, s[2:3], v44, v44, v113
	v_rcp_f32_e32 v80, v45
	s_nop 0
	v_fma_f32 v81, -v45, v80, 1.0
	v_fmac_f32_e32 v80, v81, v80
	v_div_scale_f32 v81, vcc, v113, v44, v113
	v_mul_f32_e32 v82, v81, v80
	v_fma_f32 v83, -v45, v82, v81
	v_fmac_f32_e32 v82, v83, v80
	v_fma_f32 v45, -v45, v82, v81
	v_div_fmas_f32 v45, v45, v80, v82
	v_div_fixup_f32 v44, v45, v44, v113
	v_add_f32_e32 v44, v65, v44
	v_cmp_gt_f32_e32 vcc, s37, v44
	s_nop 1
	v_cndmask_b32_e64 v45, 0, 32, vcc
	v_ldexp_f32 v44, v44, v45
	v_log_f32_e32 v44, v44
	s_nop 0
	v_mul_f32_e32 v45, 0x3f317217, v44
	v_fma_f32 v45, v44, s33, -v45
	v_fmac_f32_e32 v45, 0x3377d1cf, v44
	v_fmac_f32_e32 v45, 0x3f317217, v44
	v_cmp_lt_f32_e64 s[48:49], |v44|, s36
	s_nop 1
	v_cndmask_b32_e64 v44, v44, v45, s[48:49]
	v_cndmask_b32_e32 v45, 0, v216, vcc
	v_sub_f32_e32 v116, v44, v45
	v_mul_f32_e64 v45, |v46|, s8
	v_exp_f32_e32 v45, v45
	v_max_f32_e32 v44, v46, v46
	v_min_f32_e32 v44, 0, v44
	v_add_f32_e32 v45, 1.0, v45
	v_cmp_gt_f32_e32 vcc, s37, v45
	s_nop 1
	v_cndmask_b32_e64 v80, 0, 32, vcc
	v_ldexp_f32 v45, v45, v80
	v_log_f32_e32 v45, v45
	s_nop 0
	v_mul_f32_e32 v80, 0x3f317217, v45
	v_fma_f32 v80, v45, s33, -v80
	v_fmac_f32_e32 v80, 0x3377d1cf, v45
	v_fmac_f32_e32 v80, 0x3f317217, v45
	v_cmp_lt_f32_e64 s[48:49], |v45|, s36
	s_nop 1
	v_cndmask_b32_e64 v45, v45, v80, s[48:49]
	v_cndmask_b32_e32 v80, 0, v216, vcc
	v_sub_f32_e32 v80, v45, v80
	v_mul_f32_e32 v45, 0xbfb8aa3b, v46
	v_exp_f32_e32 v45, v45
	s_nop 0
	v_add_f32_e32 v45, 1.0, v45
	v_div_scale_f32 v46, s[2:3], v45, v45, v112
	v_rcp_f32_e32 v81, v46
	s_nop 0
	v_fma_f32 v82, -v46, v81, 1.0
	v_fmac_f32_e32 v81, v82, v81
	v_div_scale_f32 v82, vcc, v112, v45, v112
	v_mul_f32_e32 v83, v82, v81
	v_fma_f32 v96, -v46, v83, v82
	v_fmac_f32_e32 v83, v96, v81
	v_fma_f32 v46, -v46, v83, v82
	v_div_fmas_f32 v46, v46, v81, v83
	v_div_fixup_f32 v45, v46, v45, v112
	v_add_f32_e32 v45, v66, v45
	v_cmp_gt_f32_e32 vcc, s37, v45
	v_sub_f32_e32 v96, 1.0, v67
	s_nop 0
	v_cndmask_b32_e64 v46, 0, 32, vcc
	v_ldexp_f32 v45, v45, v46
	v_log_f32_e32 v45, v45
	s_nop 0
	v_mul_f32_e32 v46, 0x3f317217, v45
	v_fma_f32 v46, v45, s33, -v46
	v_fmac_f32_e32 v46, 0x3377d1cf, v45
; __device__ __forceinline__ float log_forget(float z, float lb) {
;   const float r0 = fminf(z, 0.f) - __logf(1.f + __expf(-fabsf(z)));
;   const float r1 = __logf(lb + (1.f - lb) / (1.f + __expf(-z)));
;   return lb <= 0.f ? r0 : r1;
; }
;   __device__ __forceinline__ void operator()(const f32x4 (&acc)[2][2][4][2], const pg8::Unit& u, int wr, int wc, int fr, int fq) const {
;     ...
;               for (int q = 0; q < 4; ++q) { const float gv = log_forget(acc[ai][bj][m][qh][q], lq[q]); g[m][q] = gv;
	v_fmac_f32_e32 v46, 0x3f317217, v45
	v_cmp_lt_f32_e64 s[48:49], |v45|, s36
	s_nop 1
	v_cndmask_b32_e64 v45, v45, v46, s[48:49]
	v_cndmask_b32_e32 v46, 0, v216, vcc
	v_sub_f32_e32 v117, v45, v46
	v_mul_f32_e64 v46, |v47|, s8
	v_exp_f32_e32 v46, v46
	v_max_f32_e32 v45, v47, v47
	v_min_f32_e32 v45, 0, v45
	v_add_f32_e32 v46, 1.0, v46
	v_cmp_gt_f32_e32 vcc, s37, v46
	s_nop 1
	v_cndmask_b32_e64 v81, 0, 32, vcc
	v_ldexp_f32 v46, v46, v81
	v_log_f32_e32 v46, v46
	s_nop 0
	v_mul_f32_e32 v81, 0x3f317217, v46
	v_fma_f32 v81, v46, s33, -v81
	v_fmac_f32_e32 v81, 0x3377d1cf, v46
	v_fmac_f32_e32 v81, 0x3f317217, v46
	v_cmp_lt_f32_e64 s[48:49], |v46|, s36
	s_nop 1
	v_cndmask_b32_e64 v46, v46, v81, s[48:49]
	v_cndmask_b32_e32 v81, 0, v216, vcc
	v_sub_f32_e32 v81, v46, v81
	v_mul_f32_e32 v46, 0xbfb8aa3b, v47
	v_exp_f32_e32 v46, v46
	v_pk_add_f32 v[44:45], v[44:45], v[80:81] neg_lo:[0,1] neg_hi:[0,1]
	v_add_f32_e32 v46, 1.0, v46
	v_div_scale_f32 v47, s[2:3], v46, v46, v96
	v_rcp_f32_e32 v82, v47
	v_cndmask_b32_e64 v44, v117, v44, s[56:57]
	v_fma_f32 v83, -v47, v82, 1.0
	v_fmac_f32_e32 v82, v83, v82
	v_div_scale_f32 v83, vcc, v96, v46, v96
	v_mul_f32_e32 v102, v83, v82
	v_fma_f32 v103, -v47, v102, v83
	v_fmac_f32_e32 v102, v103, v82
	v_fma_f32 v47, -v47, v102, v83
	v_div_fmas_f32 v47, v47, v82, v102
	v_div_fixup_f32 v46, v47, v46, v96
	v_add_f32_e32 v46, v67, v46
	v_cmp_gt_f32_e32 vcc, s37, v46
	s_nop 1
	v_cndmask_b32_e64 v47, 0, 32, vcc
	v_ldexp_f32 v46, v46, v47
	v_log_f32_e32 v46, v46
	s_nop 0
	v_mul_f32_e32 v47, 0x3f317217, v46
	v_fma_f32 v47, v46, s33, -v47
	v_fmac_f32_e32 v47, 0x3377d1cf, v46
	v_fmac_f32_e32 v47, 0x3f317217, v46
	v_cmp_lt_f32_e64 s[48:49], |v46|, s36
	s_nop 1
	v_cndmask_b32_e64 v46, v46, v47, s[48:49]
	v_cndmask_b32_e32 v47, 0, v216, vcc
	v_sub_f32_e32 v118, v46, v47
	v_mul_f32_e64 v47, |v40|, s8
	v_exp_f32_e32 v47, v47
	v_max_f32_e32 v46, v40, v40
	v_mul_f32_e32 v40, 0xbfb8aa3b, v40
	v_exp_f32_e32 v40, v40
	v_add_f32_e32 v47, 1.0, v47
	v_cmp_gt_f32_e32 vcc, s37, v47
	v_cndmask_b32_e64 v45, v118, v45, s[58:59]
	v_add_f32_e32 v40, 1.0, v40
	v_cndmask_b32_e64 v82, 0, 32, vcc
	v_ldexp_f32 v47, v47, v82
	v_log_f32_e32 v47, v47
	v_min_f32_e32 v46, 0, v46
	v_mul_f32_e32 v82, 0x3f317217, v47
	v_fma_f32 v82, v47, s33, -v82
	v_fmac_f32_e32 v82, 0x3377d1cf, v47
	v_fmac_f32_e32 v82, 0x3f317217, v47
	v_cmp_lt_f32_e64 s[48:49], |v47|, s36
	s_nop 1
	v_cndmask_b32_e64 v47, v47, v82, s[48:49]
	v_cndmask_b32_e32 v82, 0, v216, vcc
	v_sub_f32_e32 v82, v47, v82
	v_div_scale_f32 v47, s[2:3], v40, v40, v114
	v_rcp_f32_e32 v83, v47
	s_nop 0
	v_fma_f32 v102, -v47, v83, 1.0
	v_fmac_f32_e32 v83, v102, v83
	v_div_scale_f32 v102, vcc, v114, v40, v114
	v_mul_f32_e32 v103, v102, v83
	v_fma_f32 v104, -v47, v103, v102
	v_fmac_f32_e32 v103, v104, v83
	v_fma_f32 v47, -v47, v103, v102
	v_div_fmas_f32 v47, v47, v83, v103
	v_div_fixup_f32 v40, v47, v40, v114
	v_add_f32_e32 v40, v64, v40
	v_cmp_gt_f32_e32 vcc, s37, v40
	s_nop 1
	v_cndmask_b32_e64 v47, 0, 32, vcc
	v_ldexp_f32 v40, v40, v47
	v_log_f32_e32 v40, v40
	s_nop 0
	v_mul_f32_e32 v47, 0x3f317217, v40
	v_fma_f32 v47, v40, s33, -v47
	v_fmac_f32_e32 v47, 0x3377d1cf, v40
	v_fmac_f32_e32 v47, 0x3f317217, v40
	v_cmp_lt_f32_e64 s[48:49], |v40|, s36
	s_nop 1
	v_cndmask_b32_e64 v40, v40, v47, s[48:49]
	v_cndmask_b32_e32 v47, 0, v216, vcc
	v_sub_f32_e32 v119, v40, v47
	v_max_f32_e32 v40, v41, v41
	v_min_f32_e32 v47, 0, v40
	v_mul_f32_e64 v40, |v41|, s8
	v_exp_f32_e32 v40, v40
	s_nop 0
	v_add_f32_e32 v40, 1.0, v40
	v_cmp_gt_f32_e32 vcc, s37, v40
	s_nop 1
	v_cndmask_b32_e64 v83, 0, 32, vcc
	v_ldexp_f32 v40, v40, v83
	v_log_f32_e32 v40, v40
	s_nop 0
	v_mul_f32_e32 v83, 0x3f317217, v40
	v_fma_f32 v83, v40, s33, -v83
	v_fmac_f32_e32 v83, 0x3377d1cf, v40
	v_fmac_f32_e32 v83, 0x3f317217, v40
	v_cmp_lt_f32_e64 s[48:49], |v40|, s36
	s_nop 1
	v_cndmask_b32_e64 v40, v40, v83, s[48:49]
	v_cndmask_b32_e32 v83, 0, v216, vcc
	v_sub_f32_e32 v83, v40, v83
	v_mul_f32_e32 v40, 0xbfb8aa3b, v41
	v_exp_f32_e32 v40, v40
	v_pk_add_f32 v[46:47], v[46:47], v[82:83] neg_lo:[0,1] neg_hi:[0,1]
	v_add_f32_e32 v40, 1.0, v40
	v_div_scale_f32 v41, s[2:3], v40, v40, v113
	v_rcp_f32_e32 v102, v41
	s_nop 0
	v_fma_f32 v103, -v41, v102, 1.0
	v_fmac_f32_e32 v102, v103, v102
	v_div_scale_f32 v103, vcc, v113, v40, v113
	v_mul_f32_e32 v104, v103, v102
	v_fma_f32 v105, -v41, v104, v103
	v_fmac_f32_e32 v104, v105, v102
	v_fma_f32 v41, -v41, v104, v103
	v_div_fmas_f32 v41, v41, v102, v104
	v_div_fixup_f32 v40, v41, v40, v113
	v_add_f32_e32 v40, v65, v40
	v_cmp_gt_f32_e32 vcc, s37, v40
	s_nop 1
	v_cndmask_b32_e64 v41, 0, 32, vcc
	v_ldexp_f32 v40, v40, v41
	v_log_f32_e32 v40, v40
	s_nop 0
	v_mul_f32_e32 v41, 0x3f317217, v40
	v_fma_f32 v41, v40, s33, -v41
	v_fmac_f32_e32 v41, 0x3377d1cf, v40
	v_fmac_f32_e32 v41, 0x3f317217, v40
	v_cmp_lt_f32_e64 s[48:49], |v40|, s36
	s_nop 1
	v_cndmask_b32_e64 v40, v40, v41, s[48:49]
	v_cndmask_b32_e32 v41, 0, v216, vcc
	v_sub_f32_e32 v120, v40, v41
	v_mul_f32_e64 v41, |v42|, s8
	v_exp_f32_e32 v41, v41
	v_max_f32_e32 v40, v42, v42
	v_cndmask_b32_e64 v47, v120, v47, s[52:53]
	v_min_f32_e32 v40, 0, v40
	v_add_f32_e32 v41, 1.0, v41
	v_cmp_gt_f32_e32 vcc, s37, v41
	s_nop 1
	v_cndmask_b32_e64 v102, 0, 32, vcc
	v_ldexp_f32 v41, v41, v102
	v_log_f32_e32 v41, v41
	s_nop 0
	v_mul_f32_e32 v102, 0x3f317217, v41
	v_fma_f32 v102, v41, s33, -v102
	v_fmac_f32_e32 v102, 0x3377d1cf, v41
	v_fmac_f32_e32 v102, 0x3f317217, v41
	v_cmp_lt_f32_e64 s[48:49], |v41|, s36
	s_nop 1
	v_cndmask_b32_e64 v41, v41, v102, s[48:49]
	v_cndmask_b32_e32 v102, 0, v216, vcc
	v_sub_f32_e32 v102, v41, v102
	v_mul_f32_e32 v41, 0xbfb8aa3b, v42
	v_exp_f32_e32 v41, v41
	s_nop 0
; __device__ __forceinline__ float log_forget(float z, float lb) {
;   const float r0 = fminf(z, 0.f) - __logf(1.f + __expf(-fabsf(z)));
;   const float r1 = __logf(lb + (1.f - lb) / (1.f + __expf(-z)));
;   return lb <= 0.f ? r0 : r1;
; }
	v_add_f32_e32 v41, 1.0, v41
	v_div_scale_f32 v42, s[2:3], v41, v41, v112
	v_rcp_f32_e32 v103, v42
	s_nop 0
	v_fma_f32 v104, -v42, v103, 1.0
	v_fmac_f32_e32 v103, v104, v103
	v_div_scale_f32 v104, vcc, v112, v41, v112
	v_mul_f32_e32 v105, v104, v103
	v_fma_f32 v106, -v42, v105, v104
	v_fmac_f32_e32 v105, v106, v103
	v_fma_f32 v42, -v42, v105, v104
	v_div_fmas_f32 v42, v42, v103, v105
	v_div_fixup_f32 v41, v42, v41, v112
	v_add_f32_e32 v41, v66, v41
	v_cmp_gt_f32_e32 vcc, s37, v41
	s_nop 1
	v_cndmask_b32_e64 v42, 0, 32, vcc
	v_ldexp_f32 v41, v41, v42
	v_log_f32_e32 v41, v41
	s_nop 0
	v_mul_f32_e32 v42, 0x3f317217, v41
	v_fma_f32 v42, v41, s33, -v42
	v_fmac_f32_e32 v42, 0x3377d1cf, v41
	v_fmac_f32_e32 v42, 0x3f317217, v41
	v_cmp_lt_f32_e64 s[48:49], |v41|, s36
	s_nop 1
	v_cndmask_b32_e64 v41, v41, v42, s[48:49]
	v_cndmask_b32_e32 v42, 0, v216, vcc
	v_sub_f32_e32 v121, v41, v42
	v_mul_f32_e64 v42, |v43|, s8
	v_exp_f32_e32 v42, v42
	v_max_f32_e32 v41, v43, v43
	v_min_f32_e32 v41, 0, v41
	v_add_f32_e32 v42, 1.0, v42
	v_cmp_gt_f32_e32 vcc, s37, v42
	s_nop 1
	v_cndmask_b32_e64 v103, 0, 32, vcc
	v_ldexp_f32 v42, v42, v103
	v_log_f32_e32 v42, v42
	s_nop 0
	v_mul_f32_e32 v103, 0x3f317217, v42
	v_fma_f32 v103, v42, s33, -v103
	v_fmac_f32_e32 v103, 0x3377d1cf, v42
	v_fmac_f32_e32 v103, 0x3f317217, v42
	v_cmp_lt_f32_e64 s[48:49], |v42|, s36
	s_nop 1
	v_cndmask_b32_e64 v42, v42, v103, s[48:49]
	v_cndmask_b32_e32 v103, 0, v216, vcc
	v_sub_f32_e32 v103, v42, v103
	v_mul_f32_e32 v42, 0xbfb8aa3b, v43
	v_exp_f32_e32 v42, v42
	v_pk_add_f32 v[40:41], v[40:41], v[102:103] neg_lo:[0,1] neg_hi:[0,1]
	v_add_f32_e32 v42, 1.0, v42
	v_div_scale_f32 v43, s[2:3], v42, v42, v96
	v_rcp_f32_e32 v104, v43
	v_cndmask_b32_e64 v40, v121, v40, s[56:57]
	v_fma_f32 v105, -v43, v104, 1.0
	v_fmac_f32_e32 v104, v105, v104
	v_div_scale_f32 v105, vcc, v96, v42, v96
	v_mul_f32_e32 v106, v105, v104
	v_fma_f32 v107, -v43, v106, v105
	v_fmac_f32_e32 v106, v107, v104
	v_fma_f32 v43, -v43, v106, v105
	v_div_fmas_f32 v43, v43, v104, v106
	v_div_fixup_f32 v42, v43, v42, v96
	v_add_f32_e32 v42, v67, v42
	v_cmp_gt_f32_e32 vcc, s37, v42
	s_nop 1
	v_cndmask_b32_e64 v43, 0, 32, vcc
	v_ldexp_f32 v42, v42, v43
	v_log_f32_e32 v42, v42
	s_nop 0
	v_mul_f32_e32 v43, 0x3f317217, v42
	v_fma_f32 v43, v42, s33, -v43
	v_fmac_f32_e32 v43, 0x3377d1cf, v42
	v_fmac_f32_e32 v43, 0x3f317217, v42
	v_cmp_lt_f32_e64 s[48:49], |v42|, s36
	s_nop 1
	v_cndmask_b32_e64 v42, v42, v43, s[48:49]
	v_cndmask_b32_e32 v43, 0, v216, vcc
	v_sub_f32_e32 v122, v42, v43
	v_mul_f32_e64 v43, |v36|, s8
	v_exp_f32_e32 v43, v43
	v_max_f32_e32 v42, v36, v36
	v_mul_f32_e32 v36, 0xbfb8aa3b, v36
	v_exp_f32_e32 v36, v36
	v_add_f32_e32 v43, 1.0, v43
	v_cmp_gt_f32_e32 vcc, s37, v43
	v_cndmask_b32_e64 v41, v122, v41, s[58:59]
	v_add_f32_e32 v36, 1.0, v36
	v_cndmask_b32_e64 v104, 0, 32, vcc
	v_ldexp_f32 v43, v43, v104
	v_log_f32_e32 v43, v43
	v_min_f32_e32 v42, 0, v42
	v_mul_f32_e32 v104, 0x3f317217, v43
	v_fma_f32 v104, v43, s33, -v104
	v_fmac_f32_e32 v104, 0x3377d1cf, v43
	v_fmac_f32_e32 v104, 0x3f317217, v43
	v_cmp_lt_f32_e64 s[48:49], |v43|, s36
	s_nop 1
	v_cndmask_b32_e64 v43, v43, v104, s[48:49]
	v_cndmask_b32_e32 v104, 0, v216, vcc
	v_sub_f32_e32 v104, v43, v104
	v_div_scale_f32 v43, s[2:3], v36, v36, v114
	v_rcp_f32_e32 v105, v43
	s_nop 0
	v_fma_f32 v106, -v43, v105, 1.0
	v_fmac_f32_e32 v105, v106, v105
	v_div_scale_f32 v106, vcc, v114, v36, v114
	v_mul_f32_e32 v107, v106, v105
	v_fma_f32 v108, -v43, v107, v106
	v_fmac_f32_e32 v107, v108, v105
	v_fma_f32 v43, -v43, v107, v106
	v_div_fmas_f32 v43, v43, v105, v107
	v_div_fixup_f32 v36, v43, v36, v114
	v_add_f32_e32 v36, v64, v36
	v_cmp_gt_f32_e32 vcc, s37, v36
	s_nop 1
	v_cndmask_b32_e64 v43, 0, 32, vcc
	v_ldexp_f32 v36, v36, v43
	v_log_f32_e32 v36, v36
	s_nop 0
	v_mul_f32_e32 v43, 0x3f317217, v36
	v_fma_f32 v43, v36, s33, -v43
	v_fmac_f32_e32 v43, 0x3377d1cf, v36
	v_fmac_f32_e32 v43, 0x3f317217, v36
	v_cmp_lt_f32_e64 s[48:49], |v36|, s36
	s_nop 1
	v_cndmask_b32_e64 v36, v36, v43, s[48:49]
	v_cndmask_b32_e32 v43, 0, v216, vcc
	v_sub_f32_e32 v123, v36, v43
	v_max_f32_e32 v36, v37, v37
	v_min_f32_e32 v43, 0, v36
	v_mul_f32_e64 v36, |v37|, s8
	v_exp_f32_e32 v36, v36
	s_nop 0
	v_add_f32_e32 v36, 1.0, v36
	v_cmp_gt_f32_e32 vcc, s37, v36
	s_nop 1
	v_cndmask_b32_e64 v105, 0, 32, vcc
	v_ldexp_f32 v36, v36, v105
	v_log_f32_e32 v36, v36
	s_nop 0
	v_mul_f32_e32 v105, 0x3f317217, v36
	v_fma_f32 v105, v36, s33, -v105
	v_fmac_f32_e32 v105, 0x3377d1cf, v36
	v_fmac_f32_e32 v105, 0x3f317217, v36
	v_cmp_lt_f32_e64 s[48:49], |v36|, s36
	s_nop 1
	v_cndmask_b32_e64 v36, v36, v105, s[48:49]
	v_cndmask_b32_e32 v105, 0, v216, vcc
	v_sub_f32_e32 v105, v36, v105
	v_mul_f32_e32 v36, 0xbfb8aa3b, v37
	v_exp_f32_e32 v36, v36
	v_pk_add_f32 v[42:43], v[42:43], v[104:105] neg_lo:[0,1] neg_hi:[0,1]
	v_add_f32_e32 v36, 1.0, v36
	v_div_scale_f32 v37, s[2:3], v36, v36, v113
	v_rcp_f32_e32 v106, v37
	s_nop 0
	v_fma_f32 v107, -v37, v106, 1.0
	v_fmac_f32_e32 v106, v107, v106
	v_div_scale_f32 v107, vcc, v113, v36, v113
	v_mul_f32_e32 v108, v107, v106
	v_fma_f32 v109, -v37, v108, v107
	v_fmac_f32_e32 v108, v109, v106
	v_fma_f32 v37, -v37, v108, v107
	v_div_fmas_f32 v37, v37, v106, v108
	v_div_fixup_f32 v36, v37, v36, v113
	v_add_f32_e32 v36, v65, v36
	v_cmp_gt_f32_e32 vcc, s37, v36
	s_nop 1
	v_cndmask_b32_e64 v37, 0, 32, vcc
	v_ldexp_f32 v36, v36, v37
	v_log_f32_e32 v36, v36
	s_nop 0
	v_mul_f32_e32 v37, 0x3f317217, v36
	v_fma_f32 v37, v36, s33, -v37
	v_fmac_f32_e32 v37, 0x3377d1cf, v36
	v_fmac_f32_e32 v37, 0x3f317217, v36
	v_cmp_lt_f32_e64 s[48:49], |v36|, s36
	s_nop 1
	v_cndmask_b32_e64 v36, v36, v37, s[48:49]
; template <int CTRL> __device__ __forceinline__ float dppx(float v) { return __int_as_float(__builtin_amdgcn_update_dpp(0, __float_as_int(v), CTRL, 0xf, 0xf, true)); }
; __device__ __forceinline__ float log_forget(float z, float lb) {
;   const float r0 = fminf(z, 0.f) - __logf(1.f + __expf(-fabsf(z)));
;   const float r1 = __logf(lb + (1.f - lb) / (1.f + __expf(-z)));
;   return lb <= 0.f ? r0 : r1;
; }
;   __device__ __forceinline__ void operator()(const f32x4 (&acc)[2][2][4][2], const pg8::Unit& u, int wr, int wc, int fr, int fq) const {
;     ...
;                 float sc = gv; sc += dppx<0x111>(sc); sc += dppx<0x112>(sc); sc += dppx<0x114>(sc); sc += dppx<0x118>(sc);
	v_cndmask_b32_e32 v37, 0, v216, vcc
	v_sub_f32_e32 v124, v36, v37
	v_mul_f32_e64 v37, |v38|, s8
	v_exp_f32_e32 v37, v37
	v_max_f32_e32 v36, v38, v38
	v_cndmask_b32_e64 v43, v124, v43, s[52:53]
	v_min_f32_e32 v36, 0, v36
	v_add_f32_e32 v37, 1.0, v37
	v_cmp_gt_f32_e32 vcc, s37, v37
	v_mov_b32_dpp v105, v43 row_shr:1 row_mask:0xf bank_mask:0xf bound_ctrl:1
	s_nop 0
	v_cndmask_b32_e64 v106, 0, 32, vcc
	v_ldexp_f32 v37, v37, v106
	v_log_f32_e32 v37, v37
	s_nop 0
	v_mul_f32_e32 v106, 0x3f317217, v37
	v_fma_f32 v106, v37, s33, -v106
	v_fmac_f32_e32 v106, 0x3377d1cf, v37
	v_fmac_f32_e32 v106, 0x3f317217, v37
	v_cmp_lt_f32_e64 s[48:49], |v37|, s36
	s_nop 1
	v_cndmask_b32_e64 v37, v37, v106, s[48:49]
	v_cndmask_b32_e32 v106, 0, v216, vcc
	v_sub_f32_e32 v106, v37, v106
	v_mul_f32_e32 v37, 0xbfb8aa3b, v38
	v_exp_f32_e32 v37, v37
	s_nop 0
	v_add_f32_e32 v37, 1.0, v37
	v_div_scale_f32 v38, s[2:3], v37, v37, v112
	v_rcp_f32_e32 v107, v38
	s_nop 0
	v_fma_f32 v108, -v38, v107, 1.0
	v_fmac_f32_e32 v107, v108, v107
	v_div_scale_f32 v108, vcc, v112, v37, v112
	v_mul_f32_e32 v109, v108, v107
	v_fma_f32 v110, -v38, v109, v108
	v_fmac_f32_e32 v109, v110, v107
	v_fma_f32 v38, -v38, v109, v108
	v_div_fmas_f32 v38, v38, v107, v109
	v_div_fixup_f32 v37, v38, v37, v112
	v_add_f32_e32 v37, v66, v37
	v_cmp_gt_f32_e32 vcc, s37, v37
	s_nop 1
	v_cndmask_b32_e64 v38, 0, 32, vcc
	v_ldexp_f32 v37, v37, v38
	v_log_f32_e32 v37, v37
	s_nop 0
	v_mul_f32_e32 v38, 0x3f317217, v37
	v_fma_f32 v38, v37, s33, -v38
	v_fmac_f32_e32 v38, 0x3377d1cf, v37
	v_fmac_f32_e32 v38, 0x3f317217, v37
	v_cmp_lt_f32_e64 s[48:49], |v37|, s36
	s_nop 1
	v_cndmask_b32_e64 v37, v37, v38, s[48:49]
	v_cndmask_b32_e32 v38, 0, v216, vcc
	v_sub_f32_e32 v125, v37, v38
	v_mul_f32_e64 v38, |v39|, s8
	v_exp_f32_e32 v38, v38
	v_max_f32_e32 v37, v39, v39
	v_min_f32_e32 v37, 0, v37
	v_add_f32_e32 v38, 1.0, v38
	v_cmp_gt_f32_e32 vcc, s37, v38
	s_nop 1
	v_cndmask_b32_e64 v107, 0, 32, vcc
	v_ldexp_f32 v38, v38, v107
	v_log_f32_e32 v38, v38
	s_nop 0
	v_mul_f32_e32 v107, 0x3f317217, v38
	v_fma_f32 v107, v38, s33, -v107
	v_fmac_f32_e32 v107, 0x3377d1cf, v38
	v_fmac_f32_e32 v107, 0x3f317217, v38
	v_cmp_lt_f32_e64 s[48:49], |v38|, s36
	s_nop 1
	v_cndmask_b32_e64 v38, v38, v107, s[48:49]
	v_cndmask_b32_e32 v107, 0, v216, vcc
	v_sub_f32_e32 v107, v38, v107
	v_mul_f32_e32 v38, 0xbfb8aa3b, v39
	v_exp_f32_e32 v38, v38
	v_pk_add_f32 v[36:37], v[36:37], v[106:107] neg_lo:[0,1] neg_hi:[0,1]
	v_add_f32_e32 v38, 1.0, v38
	v_div_scale_f32 v39, s[2:3], v38, v38, v96
	v_rcp_f32_e32 v108, v39
	v_cndmask_b32_e64 v36, v125, v36, s[56:57]
	v_fma_f32 v109, -v39, v108, 1.0
	v_fmac_f32_e32 v108, v109, v108
	v_div_scale_f32 v109, vcc, v96, v38, v96
	v_mul_f32_e32 v110, v109, v108
	v_fma_f32 v111, -v39, v110, v109
	v_fmac_f32_e32 v110, v111, v108
	v_fma_f32 v39, -v39, v110, v109
	v_div_fmas_f32 v39, v39, v108, v110
	v_div_fixup_f32 v38, v39, v38, v96
	v_add_f32_e32 v38, v67, v38
	v_cmp_gt_f32_e32 vcc, s37, v38
	v_mov_b32_dpp v106, v36 row_shr:1 row_mask:0xf bank_mask:0xf bound_ctrl:1
	s_nop 0
	v_cndmask_b32_e64 v39, 0, 32, vcc
	v_ldexp_f32 v38, v38, v39
	v_log_f32_e32 v38, v38
	s_nop 0
	v_mul_f32_e32 v39, 0x3f317217, v38
	v_fma_f32 v39, v38, s33, -v39
	v_fmac_f32_e32 v39, 0x3377d1cf, v38
	v_fmac_f32_e32 v39, 0x3f317217, v38
	v_cmp_lt_f32_e64 s[48:49], |v38|, s36
	s_nop 1
	v_cndmask_b32_e64 v38, v38, v39, s[48:49]
	v_cndmask_b32_e32 v39, 0, v216, vcc
	v_sub_f32_e32 v126, v38, v39
	v_mul_f32_e64 v39, |v32|, s8
	v_exp_f32_e32 v39, v39
	v_max_f32_e32 v38, v32, v32
	v_mul_f32_e32 v32, 0xbfb8aa3b, v32
	v_exp_f32_e32 v32, v32
	v_add_f32_e32 v39, 1.0, v39
	v_cmp_gt_f32_e32 vcc, s37, v39
	v_cndmask_b32_e64 v37, v126, v37, s[58:59]
	v_add_f32_e32 v32, 1.0, v32
	v_cndmask_b32_e64 v108, 0, 32, vcc
	v_ldexp_f32 v39, v39, v108
	v_log_f32_e32 v39, v39
	v_mov_b32_dpp v107, v37 row_shr:1 row_mask:0xf bank_mask:0xf bound_ctrl:1
	v_pk_add_f32 v[106:107], v[36:37], v[106:107]
	v_min_f32_e32 v38, 0, v38
	v_mul_f32_e32 v108, 0x3f317217, v39
	v_fma_f32 v108, v39, s33, -v108
	v_fmac_f32_e32 v108, 0x3377d1cf, v39
	v_fmac_f32_e32 v108, 0x3f317217, v39
	v_cmp_lt_f32_e64 s[48:49], |v39|, s36
	s_nop 1
	v_cndmask_b32_e64 v39, v39, v108, s[48:49]
	v_cndmask_b32_e32 v108, 0, v216, vcc
	v_sub_f32_e32 v108, v39, v108
	v_div_scale_f32 v39, s[2:3], v32, v32, v114
	v_rcp_f32_e32 v109, v39
	s_nop 0
	v_fma_f32 v110, -v39, v109, 1.0
	v_fmac_f32_e32 v109, v110, v109
	v_div_scale_f32 v110, vcc, v114, v32, v114
	v_mul_f32_e32 v111, v110, v109
	v_fma_f32 v127, -v39, v111, v110
	v_fmac_f32_e32 v111, v127, v109
	v_fma_f32 v39, -v39, v111, v110
	v_div_fmas_f32 v39, v39, v109, v111
	v_div_fixup_f32 v32, v39, v32, v114
	v_add_f32_e32 v32, v64, v32
	v_cmp_gt_f32_e32 vcc, s37, v32
	s_nop 1
	v_cndmask_b32_e64 v39, 0, 32, vcc
	v_ldexp_f32 v32, v32, v39
	v_log_f32_e32 v32, v32
	s_nop 0
	v_mul_f32_e32 v39, 0x3f317217, v32
	v_fma_f32 v39, v32, s33, -v39
	v_fmac_f32_e32 v39, 0x3377d1cf, v32
	v_fmac_f32_e32 v39, 0x3f317217, v32
	v_cmp_lt_f32_e64 s[48:49], |v32|, s36
	s_nop 1
	v_cndmask_b32_e64 v32, v32, v39, s[48:49]
	v_cndmask_b32_e32 v39, 0, v216, vcc
	v_sub_f32_e32 v127, v32, v39
	v_max_f32_e32 v32, v33, v33
	v_min_f32_e32 v39, 0, v32
	v_mul_f32_e64 v32, |v33|, s8
	v_exp_f32_e32 v32, v32
	s_nop 0
	v_add_f32_e32 v32, 1.0, v32
	v_cmp_gt_f32_e32 vcc, s37, v32
	s_nop 1
	v_cndmask_b32_e64 v109, 0, 32, vcc
	v_ldexp_f32 v32, v32, v109
	v_log_f32_e32 v32, v32
	s_nop 0
	v_mul_f32_e32 v109, 0x3f317217, v32
	v_fma_f32 v109, v32, s33, -v109
	v_fmac_f32_e32 v109, 0x3377d1cf, v32
	v_fmac_f32_e32 v109, 0x3f317217, v32
	v_cmp_lt_f32_e64 s[48:49], |v32|, s36
	s_nop 1
	v_cndmask_b32_e64 v32, v32, v109, s[48:49]
; template <int CTRL> __device__ __forceinline__ float dppx(float v) { return __int_as_float(__builtin_amdgcn_update_dpp(0, __float_as_int(v), CTRL, 0xf, 0xf, true)); }
; __device__ __forceinline__ float log_forget(float z, float lb) {
;   const float r0 = fminf(z, 0.f) - __logf(1.f + __expf(-fabsf(z)));
;   const float r1 = __logf(lb + (1.f - lb) / (1.f + __expf(-z)));
;   return lb <= 0.f ? r0 : r1;
; }
;   __device__ __forceinline__ void operator()(const f32x4 (&acc)[2][2][4][2], const pg8::Unit& u, int wr, int wc, int fr, int fq) const {
;     ...
;               for (int q = 0; q < 4; ++q) { const float gv = log_forget(acc[ai][bj][m][qh][q], lq[q]); g[m][q] = gv;
;                 float sc = gv; sc += dppx<0x111>(sc); sc += dppx<0x112>(sc); sc += dppx<0x114>(sc); sc += dppx<0x118>(sc);
;                 const float tot16 = __int_as_float(__builtin_amdgcn_ds_swizzle(__float_as_int(sc), 0x1F0));
	v_cndmask_b32_e32 v109, 0, v216, vcc
	v_sub_f32_e32 v109, v32, v109
	v_mul_f32_e32 v32, 0xbfb8aa3b, v33
	v_exp_f32_e32 v32, v32
	v_pk_add_f32 v[38:39], v[38:39], v[108:109] neg_lo:[0,1] neg_hi:[0,1]
	v_add_f32_e32 v32, 1.0, v32
	v_div_scale_f32 v33, s[2:3], v32, v32, v113
	v_rcp_f32_e32 v110, v33
	s_nop 0
	v_fma_f32 v111, -v33, v110, 1.0
	v_fmac_f32_e32 v110, v111, v110
	v_div_scale_f32 v111, vcc, v113, v32, v113
	v_mul_f32_e32 v128, v111, v110
	v_fma_f32 v129, -v33, v128, v111
	v_fmac_f32_e32 v128, v129, v110
	v_fma_f32 v33, -v33, v128, v111
	v_div_fmas_f32 v33, v33, v110, v128
	v_div_fixup_f32 v32, v33, v32, v113
	v_add_f32_e32 v32, v65, v32
	v_cmp_gt_f32_e32 vcc, s37, v32
	s_nop 1
	v_cndmask_b32_e64 v33, 0, 32, vcc
	v_ldexp_f32 v32, v32, v33
	v_log_f32_e32 v32, v32
	s_nop 0
	v_mul_f32_e32 v33, 0x3f317217, v32
	v_fma_f32 v33, v32, s33, -v33
	v_fmac_f32_e32 v33, 0x3377d1cf, v32
	v_fmac_f32_e32 v33, 0x3f317217, v32
	v_cmp_lt_f32_e64 s[48:49], |v32|, s36
	s_nop 1
	v_cndmask_b32_e64 v32, v32, v33, s[48:49]
	v_cndmask_b32_e32 v33, 0, v216, vcc
	v_sub_f32_e32 v128, v32, v33
	v_mul_f32_e64 v33, |v34|, s8
	v_exp_f32_e32 v33, v33
	v_max_f32_e32 v32, v34, v34
	v_cndmask_b32_e64 v39, v128, v39, s[52:53]
	v_min_f32_e32 v32, 0, v32
	v_add_f32_e32 v33, 1.0, v33
	v_cmp_gt_f32_e32 vcc, s37, v33
	v_mov_b32_dpp v109, v39 row_shr:1 row_mask:0xf bank_mask:0xf bound_ctrl:1
	s_nop 0
	v_cndmask_b32_e64 v110, 0, 32, vcc
	v_ldexp_f32 v33, v33, v110
	v_log_f32_e32 v33, v33
	s_nop 0
	v_mul_f32_e32 v110, 0x3f317217, v33
	v_fma_f32 v110, v33, s33, -v110
	v_fmac_f32_e32 v110, 0x3377d1cf, v33
	v_fmac_f32_e32 v110, 0x3f317217, v33
	v_cmp_lt_f32_e64 s[48:49], |v33|, s36
	s_nop 1
	v_cndmask_b32_e64 v33, v33, v110, s[48:49]
	v_cndmask_b32_e32 v110, 0, v216, vcc
	v_sub_f32_e32 v110, v33, v110
	v_mul_f32_e32 v33, 0xbfb8aa3b, v34
	v_exp_f32_e32 v33, v33
	s_nop 0
	v_add_f32_e32 v33, 1.0, v33
	v_div_scale_f32 v34, s[2:3], v33, v33, v112
	v_rcp_f32_e32 v111, v34
	s_nop 0
	v_fma_f32 v129, -v34, v111, 1.0
	v_fmac_f32_e32 v111, v129, v111
	v_div_scale_f32 v129, vcc, v112, v33, v112
	v_mul_f32_e32 v130, v129, v111
	v_fma_f32 v131, -v34, v130, v129
	v_fmac_f32_e32 v130, v131, v111
	v_fma_f32 v34, -v34, v130, v129
	v_div_fmas_f32 v34, v34, v111, v130
	v_div_fixup_f32 v33, v34, v33, v112
	v_add_f32_e32 v33, v66, v33
	v_cmp_gt_f32_e32 vcc, s37, v33
	s_nop 1
	v_cndmask_b32_e64 v34, 0, 32, vcc
	v_ldexp_f32 v33, v33, v34
	v_log_f32_e32 v33, v33
	s_nop 0
	v_mul_f32_e32 v34, 0x3f317217, v33
	v_fma_f32 v34, v33, s33, -v34
	v_fmac_f32_e32 v34, 0x3377d1cf, v33
	v_fmac_f32_e32 v34, 0x3f317217, v33
	v_cmp_lt_f32_e64 s[48:49], |v33|, s36
	s_nop 1
	v_cndmask_b32_e64 v33, v33, v34, s[48:49]
	v_cndmask_b32_e32 v34, 0, v216, vcc
	v_sub_f32_e32 v129, v33, v34
	v_mul_f32_e64 v34, |v35|, s8
	v_exp_f32_e32 v34, v34
	v_max_f32_e32 v33, v35, v35
	v_min_f32_e32 v33, 0, v33
	v_add_f32_e32 v34, 1.0, v34
	v_cmp_gt_f32_e32 vcc, s37, v34
	s_nop 1
	v_cndmask_b32_e64 v111, 0, 32, vcc
	v_ldexp_f32 v34, v34, v111
	v_log_f32_e32 v34, v34
	s_nop 0
	v_mul_f32_e32 v111, 0x3f317217, v34
	v_fma_f32 v111, v34, s33, -v111
	v_fmac_f32_e32 v111, 0x3377d1cf, v34
	v_fmac_f32_e32 v111, 0x3f317217, v34
	v_cmp_lt_f32_e64 s[48:49], |v34|, s36
	s_nop 1
	v_cndmask_b32_e64 v34, v34, v111, s[48:49]
	v_cndmask_b32_e32 v111, 0, v216, vcc
	v_sub_f32_e32 v111, v34, v111
	v_mul_f32_e32 v34, 0xbfb8aa3b, v35
	v_exp_f32_e32 v34, v34
	v_pk_add_f32 v[32:33], v[32:33], v[110:111] neg_lo:[0,1] neg_hi:[0,1]
	v_add_f32_e32 v34, 1.0, v34
	v_div_scale_f32 v35, s[2:3], v34, v34, v96
	v_rcp_f32_e32 v130, v35
	v_cndmask_b32_e64 v110, v129, v32, s[56:57]
	v_fma_f32 v131, -v35, v130, 1.0
	v_fmac_f32_e32 v130, v131, v130
	v_div_scale_f32 v131, vcc, v96, v34, v96
	v_mul_f32_e32 v132, v131, v130
	v_fma_f32 v133, -v35, v132, v131
	v_fmac_f32_e32 v132, v133, v130
	v_fma_f32 v35, -v35, v132, v131
	v_div_fmas_f32 v35, v35, v130, v132
	v_div_fixup_f32 v34, v35, v34, v96
	v_add_f32_e32 v34, v67, v34
	v_cmp_gt_f32_e32 vcc, s37, v34
	v_mov_b32_dpp v32, v110 row_shr:1 row_mask:0xf bank_mask:0xf bound_ctrl:1
	s_nop 0
	v_cndmask_b32_e64 v35, 0, 32, vcc
	v_ldexp_f32 v34, v34, v35
	v_log_f32_e32 v34, v34
	s_nop 0
	v_mul_f32_e32 v35, 0x3f317217, v34
	v_fma_f32 v35, v34, s33, -v35
	v_fmac_f32_e32 v35, 0x3377d1cf, v34
	v_fmac_f32_e32 v35, 0x3f317217, v34
	v_cmp_lt_f32_e64 s[48:49], |v34|, s36
	s_nop 1
	v_cndmask_b32_e64 v34, v34, v35, s[48:49]
	v_cndmask_b32_e32 v35, 0, v216, vcc
	v_sub_f32_e32 v132, v34, v35
	v_pk_add_f32 v[34:35], v[76:77], v[78:79] neg_lo:[0,1] neg_hi:[0,1]
	v_cmp_ge_f32_e64 s[48:49], 0, v64
	v_cndmask_b32_e64 v35, v116, v35, s[52:53]
	v_cndmask_b32_e64 v111, v132, v33, s[58:59]
	v_cndmask_b32_e64 v34, v115, v34, s[48:49]
	v_mov_b32_dpp v77, v35 row_shr:1 row_mask:0xf bank_mask:0xf bound_ctrl:1
	v_cndmask_b32_e64 v46, v119, v46, s[48:49]
	v_mov_b32_dpp v76, v34 row_shr:1 row_mask:0xf bank_mask:0xf bound_ctrl:1
	v_pk_add_f32 v[76:77], v[34:35], v[76:77]
	v_cndmask_b32_e64 v42, v123, v42, s[48:49]
	v_cndmask_b32_e64 v38, v127, v38, s[48:49]
	v_mov_b32_dpp v78, v76 row_shr:2 row_mask:0xf bank_mask:0xf bound_ctrl:1
	v_mov_b32_dpp v79, v77 row_shr:2 row_mask:0xf bank_mask:0xf bound_ctrl:1
	v_pk_add_f32 v[76:77], v[76:77], v[78:79]
	v_mov_b32_dpp v104, v42 row_shr:1 row_mask:0xf bank_mask:0xf bound_ctrl:1
	v_pk_add_f32 v[104:105], v[42:43], v[104:105]
	v_mov_b32_dpp v78, v76 row_shr:4 row_mask:0xf bank_mask:0xf bound_ctrl:1
	v_mov_b32_dpp v79, v77 row_shr:4 row_mask:0xf bank_mask:0xf bound_ctrl:1
	v_pk_add_f32 v[76:77], v[76:77], v[78:79]
	v_mov_b32_dpp v108, v38 row_shr:1 row_mask:0xf bank_mask:0xf bound_ctrl:1
	v_pk_add_f32 v[108:109], v[38:39], v[108:109]
	v_mov_b32_dpp v78, v76 row_shr:8 row_mask:0xf bank_mask:0xf bound_ctrl:1
	v_mov_b32_dpp v79, v77 row_shr:8 row_mask:0xf bank_mask:0xf bound_ctrl:1
	v_pk_add_f32 v[76:77], v[76:77], v[78:79]
	ds_swizzle_b32 v78, v76 offset:swizzle(BROADCAST,16,15)
	ds_swizzle_b32 v79, v77 offset:swizzle(BROADCAST,16,15)
	v_mov_b32_dpp v33, v111 row_shr:1 row_mask:0xf bank_mask:0xf bound_ctrl:1
	v_pk_add_f32 v[32:33], v[110:111], v[32:33]
	v_pk_add_f32 v[76:77], v[76:77], 0 op_sel_hi:[1,0]
	s_waitcnt lgkmcnt(0)
; template <int CTRL> __device__ __forceinline__ float dppx(float v) { return __int_as_float(__builtin_amdgcn_update_dpp(0, __float_as_int(v), CTRL, 0xf, 0xf, true)); }
;   __device__ __forceinline__ void operator()(const f32x4 (&acc)[2][2][4][2], const pg8::Unit& u, int wr, int wc, int fr, int fq) const {
;     ...
;                 float sc = gv; sc += dppx<0x111>(sc); sc += dppx<0x112>(sc); sc += dppx<0x114>(sc); sc += dppx<0x118>(sc);
;                 const float tot16 = __int_as_float(__builtin_amdgcn_ds_swizzle(__float_as_int(sc), 0x1F0));
;                 cs[m][q] = sc + carry[q]; carry[q] += tot16; }
; #pragma unroll
;             for (int m = 0; m < 4; ++m) { const int r = row0 + ai * 128 + m * 16; float bq[4], kq[4];
; #pragma unroll
;               for (int q = 0; q < 4; ++q) { bq[q] = bwd ? (carry[q] - cs[m][q]) + g[m][q] : cs[m][q]; kq[q] = 1.f - __expf(g[m][q]); }
	v_pk_add_f32 v[130:131], v[78:79], 0 op_sel_hi:[1,0]
	v_mul_f32_e32 v78, 0x3fb8aa3b, v34
	v_exp_f32_e32 v78, v78
	v_mov_b32_dpp v79, v45 row_shr:1 row_mask:0xf bank_mask:0xf bound_ctrl:1
	v_sub_f32_e32 v115, 1.0, v78
	v_mul_f32_e32 v78, 0x3fb8aa3b, v35
	v_exp_f32_e32 v78, v78
	s_nop 0
	v_sub_f32_e32 v133, 1.0, v78
	v_mov_b32_dpp v78, v44 row_shr:1 row_mask:0xf bank_mask:0xf bound_ctrl:1
	v_pk_add_f32 v[78:79], v[44:45], v[78:79]
	s_nop 1
	v_mov_b32_dpp v80, v78 row_shr:2 row_mask:0xf bank_mask:0xf bound_ctrl:1
	v_mov_b32_dpp v81, v79 row_shr:2 row_mask:0xf bank_mask:0xf bound_ctrl:1
	v_pk_add_f32 v[78:79], v[78:79], v[80:81]
	s_nop 1
	v_mov_b32_dpp v80, v78 row_shr:4 row_mask:0xf bank_mask:0xf bound_ctrl:1
	v_mov_b32_dpp v81, v79 row_shr:4 row_mask:0xf bank_mask:0xf bound_ctrl:1
	v_pk_add_f32 v[78:79], v[78:79], v[80:81]
	s_nop 1
	v_mov_b32_dpp v80, v78 row_shr:8 row_mask:0xf bank_mask:0xf bound_ctrl:1
	v_mov_b32_dpp v81, v79 row_shr:8 row_mask:0xf bank_mask:0xf bound_ctrl:1
	v_pk_add_f32 v[78:79], v[78:79], v[80:81]
	ds_swizzle_b32 v80, v78 offset:swizzle(BROADCAST,16,15)
	ds_swizzle_b32 v81, v79 offset:swizzle(BROADCAST,16,15)
	v_pk_add_f32 v[78:79], v[78:79], 0 op_sel_hi:[1,0]
	s_waitcnt lgkmcnt(0)
	v_pk_add_f32 v[116:117], v[80:81], 0 op_sel_hi:[1,0]
	v_mul_f32_e32 v80, 0x3fb8aa3b, v44
	v_exp_f32_e32 v80, v80
	v_mov_b32_dpp v81, v47 row_shr:1 row_mask:0xf bank_mask:0xf bound_ctrl:1
	v_sub_f32_e32 v134, 1.0, v80
	v_mul_f32_e32 v80, 0x3fb8aa3b, v45
	v_exp_f32_e32 v80, v80
	s_nop 0
	v_sub_f32_e32 v135, 1.0, v80
	v_mov_b32_dpp v80, v46 row_shr:1 row_mask:0xf bank_mask:0xf bound_ctrl:1
	v_pk_add_f32 v[80:81], v[46:47], v[80:81]
	s_nop 1
	v_mov_b32_dpp v82, v80 row_shr:2 row_mask:0xf bank_mask:0xf bound_ctrl:1
	v_mov_b32_dpp v83, v81 row_shr:2 row_mask:0xf bank_mask:0xf bound_ctrl:1
	v_pk_add_f32 v[80:81], v[80:81], v[82:83]
	s_nop 1
	v_mov_b32_dpp v82, v80 row_shr:4 row_mask:0xf bank_mask:0xf bound_ctrl:1
	v_mov_b32_dpp v83, v81 row_shr:4 row_mask:0xf bank_mask:0xf bound_ctrl:1
	v_pk_add_f32 v[80:81], v[80:81], v[82:83]
	s_nop 1
	v_mov_b32_dpp v82, v80 row_shr:8 row_mask:0xf bank_mask:0xf bound_ctrl:1
	v_mov_b32_dpp v83, v81 row_shr:8 row_mask:0xf bank_mask:0xf bound_ctrl:1
	v_pk_add_f32 v[80:81], v[80:81], v[82:83]
	ds_swizzle_b32 v82, v80 offset:swizzle(BROADCAST,16,15)
	ds_swizzle_b32 v83, v81 offset:swizzle(BROADCAST,16,15)
	v_pk_add_f32 v[80:81], v[130:131], v[80:81]
	s_waitcnt lgkmcnt(0)
	v_pk_add_f32 v[118:119], v[130:131], v[82:83]
	v_mul_f32_e32 v82, 0x3fb8aa3b, v46
	v_exp_f32_e32 v82, v82
	v_mov_b32_dpp v83, v41 row_shr:1 row_mask:0xf bank_mask:0xf bound_ctrl:1
	v_sub_f32_e32 v130, 1.0, v82
	v_mul_f32_e32 v82, 0x3fb8aa3b, v47
	v_exp_f32_e32 v82, v82
	s_nop 0
	v_sub_f32_e32 v131, 1.0, v82
	v_mov_b32_dpp v82, v40 row_shr:1 row_mask:0xf bank_mask:0xf bound_ctrl:1
	v_pk_add_f32 v[82:83], v[40:41], v[82:83]
	s_nop 1
	v_mov_b32_dpp v102, v82 row_shr:2 row_mask:0xf bank_mask:0xf bound_ctrl:1
	v_mov_b32_dpp v103, v83 row_shr:2 row_mask:0xf bank_mask:0xf bound_ctrl:1
	v_pk_add_f32 v[82:83], v[82:83], v[102:103]
	s_nop 1
	v_mov_b32_dpp v102, v82 row_shr:4 row_mask:0xf bank_mask:0xf bound_ctrl:1
	v_mov_b32_dpp v103, v83 row_shr:4 row_mask:0xf bank_mask:0xf bound_ctrl:1
	v_pk_add_f32 v[82:83], v[82:83], v[102:103]
	s_nop 1
	v_mov_b32_dpp v102, v82 row_shr:8 row_mask:0xf bank_mask:0xf bound_ctrl:1
	v_mov_b32_dpp v103, v83 row_shr:8 row_mask:0xf bank_mask:0xf bound_ctrl:1
	v_pk_add_f32 v[82:83], v[82:83], v[102:103]
	ds_swizzle_b32 v102, v82 offset:swizzle(BROADCAST,16,15)
	ds_swizzle_b32 v103, v83 offset:swizzle(BROADCAST,16,15)
	v_pk_add_f32 v[82:83], v[116:117], v[82:83]
	s_waitcnt lgkmcnt(0)
	v_pk_add_f32 v[102:103], v[116:117], v[102:103]
	v_mul_f32_e32 v116, 0x3fb8aa3b, v40
	v_exp_f32_e32 v116, v116
	v_mov_b32_dpp v117, v105 row_shr:2 row_mask:0xf bank_mask:0xf bound_ctrl:1
	v_sub_f32_e32 v122, 1.0, v116
	v_mul_f32_e32 v116, 0x3fb8aa3b, v41
	v_exp_f32_e32 v116, v116
	s_nop 0
	v_sub_f32_e32 v136, 1.0, v116
	v_mov_b32_dpp v116, v104 row_shr:2 row_mask:0xf bank_mask:0xf bound_ctrl:1
	v_pk_add_f32 v[104:105], v[104:105], v[116:117]
	s_nop 1
	v_mov_b32_dpp v116, v104 row_shr:4 row_mask:0xf bank_mask:0xf bound_ctrl:1
	v_mov_b32_dpp v117, v105 row_shr:4 row_mask:0xf bank_mask:0xf bound_ctrl:1
	v_pk_add_f32 v[104:105], v[104:105], v[116:117]
	s_nop 1
	v_mov_b32_dpp v116, v104 row_shr:8 row_mask:0xf bank_mask:0xf bound_ctrl:1
	v_mov_b32_dpp v117, v105 row_shr:8 row_mask:0xf bank_mask:0xf bound_ctrl:1
	v_pk_add_f32 v[104:105], v[104:105], v[116:117]
	ds_swizzle_b32 v116, v104 offset:swizzle(BROADCAST,16,15)
	ds_swizzle_b32 v117, v105 offset:swizzle(BROADCAST,16,15)
	v_pk_add_f32 v[104:105], v[118:119], v[104:105]
	s_waitcnt lgkmcnt(0)
	v_pk_add_f32 v[116:117], v[118:119], v[116:117]
	v_mul_f32_e32 v118, 0x3fb8aa3b, v42
	v_exp_f32_e32 v118, v118
	v_mov_b32_dpp v119, v107 row_shr:2 row_mask:0xf bank_mask:0xf bound_ctrl:1
	v_sub_f32_e32 v123, 1.0, v118
	v_mul_f32_e32 v118, 0x3fb8aa3b, v43
	v_exp_f32_e32 v118, v118
	s_nop 0
	v_sub_f32_e32 v124, 1.0, v118
	v_mov_b32_dpp v118, v106 row_shr:2 row_mask:0xf bank_mask:0xf bound_ctrl:1
	v_pk_add_f32 v[106:107], v[106:107], v[118:119]
	s_nop 1
	v_mov_b32_dpp v118, v106 row_shr:4 row_mask:0xf bank_mask:0xf bound_ctrl:1
	v_mov_b32_dpp v119, v107 row_shr:4 row_mask:0xf bank_mask:0xf bound_ctrl:1
	v_pk_add_f32 v[106:107], v[106:107], v[118:119]
	s_nop 1
	v_mov_b32_dpp v118, v106 row_shr:8 row_mask:0xf bank_mask:0xf bound_ctrl:1
	v_mov_b32_dpp v119, v107 row_shr:8 row_mask:0xf bank_mask:0xf bound_ctrl:1
	v_pk_add_f32 v[106:107], v[106:107], v[118:119]
	ds_swizzle_b32 v118, v106 offset:swizzle(BROADCAST,16,15)
	ds_swizzle_b32 v119, v107 offset:swizzle(BROADCAST,16,15)
	v_pk_add_f32 v[106:107], v[102:103], v[106:107]
	s_waitcnt lgkmcnt(0)
; __device__ __forceinline__ unsigned cvt_pk_bf16(float lo, float hi) { unsigned r; asm volatile("v_cvt_pk_bf16_f32 %0, %1, %2" : "=v"(r) : "v"(lo), "v"(hi)); return r; }
; __device__ __forceinline__ float log_forget(float z, float lb) {
;   const float r0 = fminf(z, 0.f) - __logf(1.f + __expf(-fabsf(z)));
;   const float r1 = __logf(lb + (1.f - lb) / (1.f + __expf(-z)));
;   return lb <= 0.f ? r0 : r1;
; }
;   __device__ __forceinline__ void operator()(const f32x4 (&acc)[2][2][4][2], const pg8::Unit& u, int wr, int wc, int fr, int fq) const {
;     ...
;             for (int m = 0; m < 4; ++m) { const int r = row0 + ai * 128 + m * 16; float bq[4], kq[4];
; #pragma unroll
;               for (int q = 0; q < 4; ++q) { bq[q] = bwd ? (carry[q] - cs[m][q]) + g[m][q] : cs[m][q]; kq[q] = 1.f - __expf(g[m][q]); }
;               *(f32x4*)(logfp + (size_t)r * 1024 + c + 4 * qh) = (f32x4){bq[0], bq[1], bq[2], bq[3]};
;               u32x2 w; w.x = pg8::cvt_pk_bf16(kq[0], kq[1]); w.y = pg8::cvt_pk_bf16(kq[2], kq[3]);
;               *(u32x2*)(km + (size_t)r * 1024 + c + 4 * qh) = w; } } }
	v_pk_add_f32 v[102:103], v[102:103], v[118:119]
	v_mul_f32_e32 v118, 0x3fb8aa3b, v36
	v_exp_f32_e32 v118, v118
	v_mov_b32_dpp v119, v109 row_shr:2 row_mask:0xf bank_mask:0xf bound_ctrl:1
	v_sub_f32_e32 v125, 1.0, v118
	v_mul_f32_e32 v118, 0x3fb8aa3b, v37
	v_exp_f32_e32 v118, v118
	s_nop 0
	v_sub_f32_e32 v126, 1.0, v118
	v_mov_b32_dpp v118, v108 row_shr:2 row_mask:0xf bank_mask:0xf bound_ctrl:1
	v_pk_add_f32 v[108:109], v[108:109], v[118:119]
	s_nop 1
	v_mov_b32_dpp v118, v108 row_shr:4 row_mask:0xf bank_mask:0xf bound_ctrl:1
	v_mov_b32_dpp v119, v109 row_shr:4 row_mask:0xf bank_mask:0xf bound_ctrl:1
	v_pk_add_f32 v[108:109], v[108:109], v[118:119]
	s_nop 1
	v_mov_b32_dpp v118, v108 row_shr:8 row_mask:0xf bank_mask:0xf bound_ctrl:1
	v_mov_b32_dpp v119, v109 row_shr:8 row_mask:0xf bank_mask:0xf bound_ctrl:1
	v_pk_add_f32 v[108:109], v[108:109], v[118:119]
	ds_swizzle_b32 v118, v108 offset:swizzle(BROADCAST,16,15)
	ds_swizzle_b32 v119, v109 offset:swizzle(BROADCAST,16,15)
	v_pk_add_f32 v[108:109], v[116:117], v[108:109]
	s_waitcnt lgkmcnt(0)
	v_pk_add_f32 v[116:117], v[116:117], v[118:119]
	v_mul_f32_e32 v118, 0x3fb8aa3b, v38
	v_exp_f32_e32 v118, v118
	v_mov_b32_dpp v119, v33 row_shr:2 row_mask:0xf bank_mask:0xf bound_ctrl:1
	v_sub_f32_e32 v127, 1.0, v118
	v_mul_f32_e32 v118, 0x3fb8aa3b, v39
	v_exp_f32_e32 v118, v118
	s_nop 0
	v_sub_f32_e32 v128, 1.0, v118
	v_mov_b32_dpp v118, v32 row_shr:2 row_mask:0xf bank_mask:0xf bound_ctrl:1
	v_pk_add_f32 v[32:33], v[32:33], v[118:119]
	s_nop 1
	v_mov_b32_dpp v118, v32 row_shr:4 row_mask:0xf bank_mask:0xf bound_ctrl:1
	v_mov_b32_dpp v119, v33 row_shr:4 row_mask:0xf bank_mask:0xf bound_ctrl:1
	v_pk_add_f32 v[32:33], v[32:33], v[118:119]
	s_nop 1
	v_mov_b32_dpp v118, v32 row_shr:8 row_mask:0xf bank_mask:0xf bound_ctrl:1
	v_mov_b32_dpp v119, v33 row_shr:8 row_mask:0xf bank_mask:0xf bound_ctrl:1
	v_pk_add_f32 v[32:33], v[32:33], v[118:119]
	ds_swizzle_b32 v118, v32 offset:swizzle(BROADCAST,16,15)
	ds_swizzle_b32 v119, v33 offset:swizzle(BROADCAST,16,15)
	v_pk_add_f32 v[120:121], v[102:103], v[32:33]
	v_pk_add_f32 v[32:33], v[116:117], v[76:77] neg_lo:[0,1] neg_hi:[0,1]
	s_waitcnt lgkmcnt(0)
	v_pk_add_f32 v[102:103], v[102:103], v[118:119]
	s_nop 0
	v_pk_add_f32 v[118:119], v[102:103], v[78:79] neg_lo:[0,1] neg_hi:[0,1]
	v_pk_add_f32 v[32:33], v[34:35], v[32:33]
	v_pk_add_f32 v[34:35], v[44:45], v[118:119]
	v_cndmask_b32_e64 v33, v77, v33, s[42:43]
	v_cndmask_b32_e64 v35, v79, v35, s[42:43]
	v_cndmask_b32_e64 v34, v78, v34, s[42:43]
	v_cndmask_b32_e64 v32, v76, v32, s[42:43]
	global_store_dwordx4 v[54:55], v[32:35], off offset:16
	s_nop 1
	v_cvt_pk_bf16_f32 v32, v115, v133
	v_cvt_pk_bf16_f32 v33, v134, v135
	global_store_dwordx2 v[52:53], v[32:33], off offset:8
	v_pk_add_f32 v[32:33], v[116:117], v[80:81] neg_lo:[0,1] neg_hi:[0,1]
	v_pk_add_f32 v[34:35], v[102:103], v[82:83] neg_lo:[0,1] neg_hi:[0,1]
	v_pk_add_f32 v[32:33], v[46:47], v[32:33]
	v_pk_add_f32 v[34:35], v[40:41], v[34:35]
	v_cndmask_b32_e64 v33, v81, v33, s[42:43]
	v_cndmask_b32_e64 v35, v83, v35, s[42:43]
	v_cndmask_b32_e64 v34, v82, v34, s[42:43]
	v_cndmask_b32_e64 v32, v80, v32, s[42:43]
	global_store_dwordx4 v[58:59], v[32:35], off offset:16
	s_nop 1
	v_cvt_pk_bf16_f32 v32, v130, v131
	v_cvt_pk_bf16_f32 v33, v122, v136
	global_store_dwordx2 v[56:57], v[32:33], off offset:8
	v_pk_add_f32 v[32:33], v[116:117], v[104:105] neg_lo:[0,1] neg_hi:[0,1]
	v_pk_add_f32 v[34:35], v[102:103], v[106:107] neg_lo:[0,1] neg_hi:[0,1]
	v_pk_add_f32 v[32:33], v[42:43], v[32:33]
	v_pk_add_f32 v[34:35], v[36:37], v[34:35]
	v_cndmask_b32_e64 v33, v105, v33, s[42:43]
	v_cndmask_b32_e64 v35, v107, v35, s[42:43]
	v_cndmask_b32_e64 v34, v106, v34, s[42:43]
	v_cndmask_b32_e64 v32, v104, v32, s[42:43]
	global_store_dwordx4 v[62:63], v[32:35], off offset:16
	v_mul_f32_e32 v37, 0x3fb8aa3b, v111
	v_exp_f32_e32 v37, v37
	v_cvt_pk_bf16_f32 v32, v123, v124
	v_cvt_pk_bf16_f32 v33, v125, v126
	global_store_dwordx2 v[60:61], v[32:33], off offset:8
	v_mul_f32_e32 v32, 0x3fb8aa3b, v110
	v_exp_f32_e32 v32, v32
	v_pk_add_f32 v[34:35], v[102:103], v[120:121] neg_lo:[0,1] neg_hi:[0,1]
	v_sub_f32_e32 v37, 1.0, v37
	v_pk_add_f32 v[34:35], v[110:111], v[34:35]
	v_sub_f32_e32 v36, 1.0, v32
	v_pk_add_f32 v[32:33], v[116:117], v[108:109] neg_lo:[0,1] neg_hi:[0,1]
	v_cndmask_b32_e64 v35, v121, v35, s[42:43]
	v_pk_add_f32 v[32:33], v[38:39], v[32:33]
	v_cndmask_b32_e64 v34, v120, v34, s[42:43]
	v_cndmask_b32_e64 v33, v109, v33, s[42:43]
	v_cndmask_b32_e64 v32, v108, v32, s[42:43]
	global_store_dwordx4 v[72:73], v[32:35], off offset:16
	s_nop 1
	v_cvt_pk_bf16_f32 v32, v127, v128
	v_cvt_pk_bf16_f32 v33, v36, v37
	global_store_dwordx2 v[74:75], v[32:33], off offset:8
	v_mul_f32_e64 v33, |v28|, s8
	v_exp_f32_e32 v33, v33
	v_max_f32_e32 v32, v28, v28
	v_mul_f32_e32 v28, 0xbfb8aa3b, v28
	v_exp_f32_e32 v28, v28
	v_add_f32_e32 v33, 1.0, v33
	v_cmp_gt_f32_e32 vcc, s37, v33
	v_min_f32_e32 v32, 0, v32
	v_add_f32_e32 v28, 1.0, v28
	v_cndmask_b32_e64 v34, 0, 32, vcc
	v_ldexp_f32 v33, v33, v34
	v_log_f32_e32 v33, v33
	s_nop 0
	v_mul_f32_e32 v34, 0x3f317217, v33
	v_fma_f32 v34, v33, s33, -v34
	v_fmac_f32_e32 v34, 0x3377d1cf, v33
	v_fmac_f32_e32 v34, 0x3f317217, v33
	v_cmp_lt_f32_e64 s[60:61], |v33|, s36
	s_nop 1
	v_cndmask_b32_e64 v33, v33, v34, s[60:61]
	v_cndmask_b32_e32 v34, 0, v216, vcc
	v_sub_f32_e32 v34, v33, v34
	v_div_scale_f32 v33, s[2:3], v28, v28, v157
	v_rcp_f32_e32 v35, v33
	s_nop 0
	v_fma_f32 v36, -v33, v35, 1.0
	v_fmac_f32_e32 v35, v36, v35
	v_div_scale_f32 v36, vcc, v157, v28, v157
	v_mul_f32_e32 v37, v36, v35
	v_fma_f32 v38, -v33, v37, v36
	v_fmac_f32_e32 v37, v38, v35
	v_fma_f32 v33, -v33, v37, v36
; __device__ __forceinline__ float log_forget(float z, float lb) {
;   const float r0 = fminf(z, 0.f) - __logf(1.f + __expf(-fabsf(z)));
;   const float r1 = __logf(lb + (1.f - lb) / (1.f + __expf(-z)));
;   return lb <= 0.f ? r0 : r1;
; }
	v_div_fmas_f32 v33, v33, v35, v37
	v_div_fixup_f32 v28, v33, v28, v157
	v_add_f32_e32 v28, v68, v28
	v_cmp_gt_f32_e32 vcc, s37, v28
	s_nop 1
	v_cndmask_b32_e64 v33, 0, 32, vcc
	v_ldexp_f32 v28, v28, v33
	v_log_f32_e32 v28, v28
	s_nop 0
	v_mul_f32_e32 v33, 0x3f317217, v28
	v_fma_f32 v33, v28, s33, -v33
	v_fmac_f32_e32 v33, 0x3377d1cf, v28
	v_fmac_f32_e32 v33, 0x3f317217, v28
	v_cmp_lt_f32_e64 s[60:61], |v28|, s36
	s_nop 1
	v_cndmask_b32_e64 v28, v28, v33, s[60:61]
	v_cndmask_b32_e32 v33, 0, v216, vcc
	v_sub_f32_e32 v60, v28, v33
	v_max_f32_e32 v28, v29, v29
	v_min_f32_e32 v33, 0, v28
	v_mul_f32_e64 v28, |v29|, s8
	v_exp_f32_e32 v28, v28
	s_nop 0
	v_add_f32_e32 v28, 1.0, v28
	v_cmp_gt_f32_e32 vcc, s37, v28
	s_nop 1
	v_cndmask_b32_e64 v35, 0, 32, vcc
	v_ldexp_f32 v28, v28, v35
	v_log_f32_e32 v28, v28
	s_nop 0
	v_mul_f32_e32 v35, 0x3f317217, v28
	v_fma_f32 v35, v28, s33, -v35
	v_fmac_f32_e32 v35, 0x3377d1cf, v28
	v_fmac_f32_e32 v35, 0x3f317217, v28
	v_cmp_lt_f32_e64 s[60:61], |v28|, s36
	s_nop 1
	v_cndmask_b32_e64 v28, v28, v35, s[60:61]
	v_cndmask_b32_e32 v35, 0, v216, vcc
	v_sub_f32_e32 v35, v28, v35
	v_mul_f32_e32 v28, 0xbfb8aa3b, v29
	v_exp_f32_e32 v28, v28
	s_nop 0
	v_add_f32_e32 v28, 1.0, v28
	v_div_scale_f32 v29, s[2:3], v28, v28, v156
	v_rcp_f32_e32 v36, v29
	s_nop 0
	v_fma_f32 v37, -v29, v36, 1.0
	v_fmac_f32_e32 v36, v37, v36
	v_div_scale_f32 v37, vcc, v156, v28, v156
	v_mul_f32_e32 v38, v37, v36
	v_fma_f32 v39, -v29, v38, v37
	v_fmac_f32_e32 v38, v39, v36
	v_fma_f32 v29, -v29, v38, v37
	v_div_fmas_f32 v29, v29, v36, v38
	v_div_fixup_f32 v28, v29, v28, v156
	v_add_f32_e32 v28, v69, v28
	v_cmp_gt_f32_e32 vcc, s37, v28
	s_nop 1
	v_cndmask_b32_e64 v29, 0, 32, vcc
	v_ldexp_f32 v28, v28, v29
	v_log_f32_e32 v28, v28
	s_nop 0
	v_mul_f32_e32 v29, 0x3f317217, v28
	v_fma_f32 v29, v28, s33, -v29
	v_fmac_f32_e32 v29, 0x3377d1cf, v28
	v_fmac_f32_e32 v29, 0x3f317217, v28
	v_cmp_lt_f32_e64 s[60:61], |v28|, s36
	s_nop 1
	v_cndmask_b32_e64 v28, v28, v29, s[60:61]
	v_cndmask_b32_e32 v29, 0, v216, vcc
	v_sub_f32_e32 v61, v28, v29
	v_mul_f32_e64 v29, |v30|, s8
	v_exp_f32_e32 v29, v29
	v_max_f32_e32 v28, v30, v30
	v_min_f32_e32 v28, 0, v28
	v_add_f32_e32 v29, 1.0, v29
	v_cmp_gt_f32_e32 vcc, s37, v29
	s_nop 1
	v_cndmask_b32_e64 v36, 0, 32, vcc
	v_ldexp_f32 v29, v29, v36
	v_log_f32_e32 v29, v29
	s_nop 0
	v_mul_f32_e32 v36, 0x3f317217, v29
	v_fma_f32 v36, v29, s33, -v36
	v_fmac_f32_e32 v36, 0x3377d1cf, v29
	v_fmac_f32_e32 v36, 0x3f317217, v29
	v_cmp_lt_f32_e64 s[60:61], |v29|, s36
	s_nop 1
	v_cndmask_b32_e64 v29, v29, v36, s[60:61]
	v_cndmask_b32_e32 v36, 0, v216, vcc
	v_sub_f32_e32 v36, v29, v36
	v_mul_f32_e32 v29, 0xbfb8aa3b, v30
	v_exp_f32_e32 v29, v29
	s_nop 0
	v_add_f32_e32 v29, 1.0, v29
	v_div_scale_f32 v30, s[2:3], v29, v29, v155
	v_rcp_f32_e32 v37, v30
	s_nop 0
	v_fma_f32 v38, -v30, v37, 1.0
	v_fmac_f32_e32 v37, v38, v37
	v_div_scale_f32 v38, vcc, v155, v29, v155
	v_mul_f32_e32 v39, v38, v37
	v_fma_f32 v40, -v30, v39, v38
	v_fmac_f32_e32 v39, v40, v37
	v_fma_f32 v30, -v30, v39, v38
	v_div_fmas_f32 v30, v30, v37, v39
	v_div_fixup_f32 v29, v30, v29, v155
	v_add_f32_e32 v29, v70, v29
	v_cmp_gt_f32_e32 vcc, s37, v29
	s_nop 1
	v_cndmask_b32_e64 v30, 0, 32, vcc
	v_ldexp_f32 v29, v29, v30
	v_log_f32_e32 v29, v29
	s_nop 0
	v_mul_f32_e32 v30, 0x3f317217, v29
	v_fma_f32 v30, v29, s33, -v30
	v_fmac_f32_e32 v30, 0x3377d1cf, v29
	v_fmac_f32_e32 v30, 0x3f317217, v29
	v_cmp_lt_f32_e64 s[60:61], |v29|, s36
	s_nop 1
	v_cndmask_b32_e64 v29, v29, v30, s[60:61]
	v_cndmask_b32_e32 v30, 0, v216, vcc
	v_sub_f32_e32 v62, v29, v30
	v_mul_f32_e64 v30, |v31|, s8
	v_exp_f32_e32 v30, v30
	v_max_f32_e32 v29, v31, v31
	v_min_f32_e32 v29, 0, v29
	v_add_f32_e32 v30, 1.0, v30
	v_cmp_gt_f32_e32 vcc, s37, v30
	s_nop 1
	v_cndmask_b32_e64 v37, 0, 32, vcc
	v_ldexp_f32 v30, v30, v37
	v_log_f32_e32 v30, v30
	s_nop 0
	v_mul_f32_e32 v37, 0x3f317217, v30
	v_fma_f32 v37, v30, s33, -v37
	v_fmac_f32_e32 v37, 0x3377d1cf, v30
	v_fmac_f32_e32 v37, 0x3f317217, v30
	v_cmp_lt_f32_e64 s[60:61], |v30|, s36
	s_nop 1
	v_cndmask_b32_e64 v30, v30, v37, s[60:61]
	v_cndmask_b32_e32 v37, 0, v216, vcc
	v_sub_f32_e32 v37, v30, v37
	v_mul_f32_e32 v30, 0xbfb8aa3b, v31
	v_exp_f32_e32 v30, v30
	s_nop 0
	v_add_f32_e32 v30, 1.0, v30
	v_div_scale_f32 v31, s[2:3], v30, v30, v154
	v_rcp_f32_e32 v38, v31
	s_nop 0
	v_fma_f32 v39, -v31, v38, 1.0
	v_fmac_f32_e32 v38, v39, v38
	v_div_scale_f32 v39, vcc, v154, v30, v154
	v_mul_f32_e32 v40, v39, v38
	v_fma_f32 v41, -v31, v40, v39
	v_fmac_f32_e32 v40, v41, v38
	v_fma_f32 v31, -v31, v40, v39
	v_div_fmas_f32 v31, v31, v38, v40
	v_div_fixup_f32 v30, v31, v30, v154
	v_add_f32_e32 v30, v71, v30
	v_cmp_gt_f32_e32 vcc, s37, v30
	s_nop 1
	v_cndmask_b32_e64 v31, 0, 32, vcc
	v_ldexp_f32 v30, v30, v31
	v_log_f32_e32 v30, v30
	s_nop 0
	v_mul_f32_e32 v31, 0x3f317217, v30
	v_fma_f32 v31, v30, s33, -v31
	v_fmac_f32_e32 v31, 0x3377d1cf, v30
	v_fmac_f32_e32 v31, 0x3f317217, v30
	v_cmp_lt_f32_e64 s[60:61], |v30|, s36
	s_nop 1
	v_cndmask_b32_e64 v30, v30, v31, s[60:61]
	v_cndmask_b32_e32 v31, 0, v216, vcc
	v_sub_f32_e32 v63, v30, v31
	v_mul_f32_e64 v31, |v24|, s8
	v_exp_f32_e32 v31, v31
	v_max_f32_e32 v30, v24, v24
	v_mul_f32_e32 v24, 0xbfb8aa3b, v24
	v_exp_f32_e32 v24, v24
	v_add_f32_e32 v31, 1.0, v31
	v_cmp_gt_f32_e32 vcc, s37, v31
	v_min_f32_e32 v30, 0, v30
	v_add_f32_e32 v24, 1.0, v24
	v_cndmask_b32_e64 v38, 0, 32, vcc
	v_ldexp_f32 v31, v31, v38
	v_log_f32_e32 v31, v31
	s_nop 0
	v_mul_f32_e32 v38, 0x3f317217, v31
	v_fma_f32 v38, v31, s33, -v38
	v_fmac_f32_e32 v38, 0x3377d1cf, v31
	v_fmac_f32_e32 v38, 0x3f317217, v31
	v_cmp_lt_f32_e64 s[60:61], |v31|, s36
	s_nop 1
	v_cndmask_b32_e64 v31, v31, v38, s[60:61]
; template <int CTRL> __device__ __forceinline__ float dppx(float v) { return __int_as_float(__builtin_amdgcn_update_dpp(0, __float_as_int(v), CTRL, 0xf, 0xf, true)); }
; __device__ __forceinline__ float log_forget(float z, float lb) {
;   const float r0 = fminf(z, 0.f) - __logf(1.f + __expf(-fabsf(z)));
;   const float r1 = __logf(lb + (1.f - lb) / (1.f + __expf(-z)));
;   return lb <= 0.f ? r0 : r1;
; }
;   __device__ __forceinline__ void operator()(const f32x4 (&acc)[2][2][4][2], const pg8::Unit& u, int wr, int wc, int fr, int fq) const {
;     ...
;               for (int q = 0; q < 4; ++q) { const float gv = log_forget(acc[ai][bj][m][qh][q], lq[q]); g[m][q] = gv;
;                 float sc = gv; sc += dppx<0x111>(sc); sc += dppx<0x112>(sc); sc += dppx<0x114>(sc); sc += dppx<0x118>(sc);
	v_cndmask_b32_e32 v38, 0, v216, vcc
	v_sub_f32_e32 v38, v31, v38
	v_div_scale_f32 v31, s[2:3], v24, v24, v157
	v_rcp_f32_e32 v39, v31
	s_nop 0
	v_fma_f32 v40, -v31, v39, 1.0
	v_fmac_f32_e32 v39, v40, v39
	v_div_scale_f32 v40, vcc, v157, v24, v157
	v_mul_f32_e32 v41, v40, v39
	v_fma_f32 v42, -v31, v41, v40
	v_fmac_f32_e32 v41, v42, v39
	v_fma_f32 v31, -v31, v41, v40
	v_div_fmas_f32 v31, v31, v39, v41
	v_div_fixup_f32 v24, v31, v24, v157
	v_add_f32_e32 v24, v68, v24
	v_cmp_gt_f32_e32 vcc, s37, v24
	s_nop 1
	v_cndmask_b32_e64 v31, 0, 32, vcc
	v_ldexp_f32 v24, v24, v31
	v_log_f32_e32 v24, v24
	s_nop 0
	v_mul_f32_e32 v31, 0x3f317217, v24
	v_fma_f32 v31, v24, s33, -v31
	v_fmac_f32_e32 v31, 0x3377d1cf, v24
	v_fmac_f32_e32 v31, 0x3f317217, v24
	v_cmp_lt_f32_e64 s[60:61], |v24|, s36
	s_nop 1
	v_cndmask_b32_e64 v24, v24, v31, s[60:61]
	v_cndmask_b32_e32 v31, 0, v216, vcc
	v_sub_f32_e32 v72, v24, v31
	v_max_f32_e32 v24, v25, v25
	v_min_f32_e32 v31, 0, v24
	v_mul_f32_e64 v24, |v25|, s8
	v_exp_f32_e32 v24, v24
	s_nop 0
	v_add_f32_e32 v24, 1.0, v24
	v_cmp_gt_f32_e32 vcc, s37, v24
	s_nop 1
	v_cndmask_b32_e64 v39, 0, 32, vcc
	v_ldexp_f32 v24, v24, v39
	v_log_f32_e32 v24, v24
	s_nop 0
	v_mul_f32_e32 v39, 0x3f317217, v24
	v_fma_f32 v39, v24, s33, -v39
	v_fmac_f32_e32 v39, 0x3377d1cf, v24
	v_fmac_f32_e32 v39, 0x3f317217, v24
	v_cmp_lt_f32_e64 s[60:61], |v24|, s36
	s_nop 1
	v_cndmask_b32_e64 v24, v24, v39, s[60:61]
	v_cndmask_b32_e32 v39, 0, v216, vcc
	v_sub_f32_e32 v39, v24, v39
	v_mul_f32_e32 v24, 0xbfb8aa3b, v25
	v_exp_f32_e32 v24, v24
	v_pk_add_f32 v[30:31], v[30:31], v[38:39] neg_lo:[0,1] neg_hi:[0,1]
	v_add_f32_e32 v24, 1.0, v24
	v_div_scale_f32 v25, s[2:3], v24, v24, v156
	v_rcp_f32_e32 v40, v25
	v_cndmask_b32_e64 v30, v72, v30, s[44:45]
	v_fma_f32 v41, -v25, v40, 1.0
	v_fmac_f32_e32 v40, v41, v40
	v_div_scale_f32 v41, vcc, v156, v24, v156
	v_mul_f32_e32 v42, v41, v40
	v_fma_f32 v43, -v25, v42, v41
	v_fmac_f32_e32 v42, v43, v40
	v_fma_f32 v25, -v25, v42, v41
	v_div_fmas_f32 v25, v25, v40, v42
	v_div_fixup_f32 v24, v25, v24, v156
	v_add_f32_e32 v24, v69, v24
	v_cmp_gt_f32_e32 vcc, s37, v24
	v_mov_b32_dpp v38, v30 row_shr:1 row_mask:0xf bank_mask:0xf bound_ctrl:1
	s_nop 0
	v_cndmask_b32_e64 v25, 0, 32, vcc
	v_ldexp_f32 v24, v24, v25
	v_log_f32_e32 v24, v24
	s_nop 0
	v_mul_f32_e32 v25, 0x3f317217, v24
	v_fma_f32 v25, v24, s33, -v25
	v_fmac_f32_e32 v25, 0x3377d1cf, v24
	v_fmac_f32_e32 v25, 0x3f317217, v24
	v_cmp_lt_f32_e64 s[60:61], |v24|, s36
	s_nop 1
	v_cndmask_b32_e64 v24, v24, v25, s[60:61]
	v_cndmask_b32_e32 v25, 0, v216, vcc
	v_sub_f32_e32 v73, v24, v25
	v_mul_f32_e64 v25, |v26|, s8
	v_exp_f32_e32 v25, v25
	v_max_f32_e32 v24, v26, v26
	v_cndmask_b32_e64 v31, v73, v31, s[46:47]
	v_min_f32_e32 v24, 0, v24
	v_add_f32_e32 v25, 1.0, v25
	v_cmp_gt_f32_e32 vcc, s37, v25
	v_mov_b32_dpp v39, v31 row_shr:1 row_mask:0xf bank_mask:0xf bound_ctrl:1
	v_pk_add_f32 v[38:39], v[30:31], v[38:39]
	v_cndmask_b32_e64 v40, 0, 32, vcc
	v_ldexp_f32 v25, v25, v40
	v_log_f32_e32 v25, v25
	s_nop 0
	v_mul_f32_e32 v40, 0x3f317217, v25
	v_fma_f32 v40, v25, s33, -v40
	v_fmac_f32_e32 v40, 0x3377d1cf, v25
	v_fmac_f32_e32 v40, 0x3f317217, v25
	v_cmp_lt_f32_e64 s[60:61], |v25|, s36
	s_nop 1
	v_cndmask_b32_e64 v25, v25, v40, s[60:61]
	v_cndmask_b32_e32 v40, 0, v216, vcc
	v_sub_f32_e32 v40, v25, v40
	v_mul_f32_e32 v25, 0xbfb8aa3b, v26
	v_exp_f32_e32 v25, v25
	s_nop 0
	v_add_f32_e32 v25, 1.0, v25
	v_div_scale_f32 v26, s[2:3], v25, v25, v155
	v_rcp_f32_e32 v41, v26
	s_nop 0
	v_fma_f32 v42, -v26, v41, 1.0
	v_fmac_f32_e32 v41, v42, v41
	v_div_scale_f32 v42, vcc, v155, v25, v155
	v_mul_f32_e32 v43, v42, v41
	v_fma_f32 v44, -v26, v43, v42
	v_fmac_f32_e32 v43, v44, v41
	v_fma_f32 v26, -v26, v43, v42
	v_div_fmas_f32 v26, v26, v41, v43
	v_div_fixup_f32 v25, v26, v25, v155
	v_add_f32_e32 v25, v70, v25
	v_cmp_gt_f32_e32 vcc, s37, v25
	s_nop 1
	v_cndmask_b32_e64 v26, 0, 32, vcc
	v_ldexp_f32 v25, v25, v26
	v_log_f32_e32 v25, v25
	s_nop 0
	v_mul_f32_e32 v26, 0x3f317217, v25
	v_fma_f32 v26, v25, s33, -v26
	v_fmac_f32_e32 v26, 0x3377d1cf, v25
	v_fmac_f32_e32 v26, 0x3f317217, v25
	v_cmp_lt_f32_e64 s[60:61], |v25|, s36
	s_nop 1
	v_cndmask_b32_e64 v25, v25, v26, s[60:61]
	v_cndmask_b32_e32 v26, 0, v216, vcc
	v_sub_f32_e32 v74, v25, v26
	v_mul_f32_e64 v26, |v27|, s8
	v_exp_f32_e32 v26, v26
	v_max_f32_e32 v25, v27, v27
	v_min_f32_e32 v25, 0, v25
	v_add_f32_e32 v26, 1.0, v26
	v_cmp_gt_f32_e32 vcc, s37, v26
	s_nop 1
	v_cndmask_b32_e64 v41, 0, 32, vcc
	v_ldexp_f32 v26, v26, v41
	v_log_f32_e32 v26, v26
	s_nop 0
	v_mul_f32_e32 v41, 0x3f317217, v26
	v_fma_f32 v41, v26, s33, -v41
	v_fmac_f32_e32 v41, 0x3377d1cf, v26
	v_fmac_f32_e32 v41, 0x3f317217, v26
	v_cmp_lt_f32_e64 s[60:61], |v26|, s36
	s_nop 1
	v_cndmask_b32_e64 v26, v26, v41, s[60:61]
	v_cndmask_b32_e32 v41, 0, v216, vcc
	v_sub_f32_e32 v41, v26, v41
	v_mul_f32_e32 v26, 0xbfb8aa3b, v27
	v_exp_f32_e32 v26, v26
	s_nop 0
	v_add_f32_e32 v26, 1.0, v26
	v_div_scale_f32 v27, s[2:3], v26, v26, v154
	v_rcp_f32_e32 v42, v27
	s_nop 0
	v_fma_f32 v43, -v27, v42, 1.0
	v_fmac_f32_e32 v42, v43, v42
	v_div_scale_f32 v43, vcc, v154, v26, v154
	v_mul_f32_e32 v44, v43, v42
	v_fma_f32 v45, -v27, v44, v43
	v_fmac_f32_e32 v44, v45, v42
	v_fma_f32 v27, -v27, v44, v43
	v_div_fmas_f32 v27, v27, v42, v44
	v_div_fixup_f32 v26, v27, v26, v154
	v_add_f32_e32 v26, v71, v26
	v_cmp_gt_f32_e32 vcc, s37, v26
	s_nop 1
	v_cndmask_b32_e64 v27, 0, 32, vcc
	v_ldexp_f32 v26, v26, v27
	v_log_f32_e32 v26, v26
	s_nop 0
	v_mul_f32_e32 v27, 0x3f317217, v26
	v_fma_f32 v27, v26, s33, -v27
	v_fmac_f32_e32 v27, 0x3377d1cf, v26
	v_fmac_f32_e32 v27, 0x3f317217, v26
	v_cmp_lt_f32_e64 s[60:61], |v26|, s36
; template <int CTRL> __device__ __forceinline__ float dppx(float v) { return __int_as_float(__builtin_amdgcn_update_dpp(0, __float_as_int(v), CTRL, 0xf, 0xf, true)); }
; __device__ __forceinline__ float log_forget(float z, float lb) {
;   const float r0 = fminf(z, 0.f) - __logf(1.f + __expf(-fabsf(z)));
;   const float r1 = __logf(lb + (1.f - lb) / (1.f + __expf(-z)));
;   return lb <= 0.f ? r0 : r1;
; }
;   __device__ __forceinline__ void operator()(const f32x4 (&acc)[2][2][4][2], const pg8::Unit& u, int wr, int wc, int fr, int fq) const {
;     ...
;                 float sc = gv; sc += dppx<0x111>(sc); sc += dppx<0x112>(sc); sc += dppx<0x114>(sc); sc += dppx<0x118>(sc);
;                 const float tot16 = __int_as_float(__builtin_amdgcn_ds_swizzle(__float_as_int(sc), 0x1F0));
	s_nop 1
	v_cndmask_b32_e64 v26, v26, v27, s[60:61]
	v_cndmask_b32_e32 v27, 0, v216, vcc
	v_sub_f32_e32 v75, v26, v27
	v_mul_f32_e64 v27, |v20|, s8
	v_exp_f32_e32 v27, v27
	v_max_f32_e32 v26, v20, v20
	v_mul_f32_e32 v20, 0xbfb8aa3b, v20
	v_exp_f32_e32 v20, v20
	v_add_f32_e32 v27, 1.0, v27
	v_cmp_gt_f32_e32 vcc, s37, v27
	v_min_f32_e32 v26, 0, v26
	v_add_f32_e32 v20, 1.0, v20
	v_cndmask_b32_e64 v42, 0, 32, vcc
	v_ldexp_f32 v27, v27, v42
	v_log_f32_e32 v27, v27
	s_nop 0
	v_mul_f32_e32 v42, 0x3f317217, v27
	v_fma_f32 v42, v27, s33, -v42
	v_fmac_f32_e32 v42, 0x3377d1cf, v27
	v_fmac_f32_e32 v42, 0x3f317217, v27
	v_cmp_lt_f32_e64 s[60:61], |v27|, s36
	s_nop 1
	v_cndmask_b32_e64 v27, v27, v42, s[60:61]
	v_cndmask_b32_e32 v42, 0, v216, vcc
	v_sub_f32_e32 v42, v27, v42
	v_div_scale_f32 v27, s[2:3], v20, v20, v157
	v_rcp_f32_e32 v43, v27
	s_nop 0
	v_fma_f32 v44, -v27, v43, 1.0
	v_fmac_f32_e32 v43, v44, v43
	v_div_scale_f32 v44, vcc, v157, v20, v157
	v_mul_f32_e32 v45, v44, v43
	v_fma_f32 v46, -v27, v45, v44
	v_fmac_f32_e32 v45, v46, v43
	v_fma_f32 v27, -v27, v45, v44
	v_div_fmas_f32 v27, v27, v43, v45
	v_div_fixup_f32 v20, v27, v20, v157
	v_add_f32_e32 v20, v68, v20
	v_cmp_gt_f32_e32 vcc, s37, v20
	s_nop 1
	v_cndmask_b32_e64 v27, 0, 32, vcc
	v_ldexp_f32 v20, v20, v27
	v_log_f32_e32 v20, v20
	s_nop 0
	v_mul_f32_e32 v27, 0x3f317217, v20
	v_fma_f32 v27, v20, s33, -v27
	v_fmac_f32_e32 v27, 0x3377d1cf, v20
	v_fmac_f32_e32 v27, 0x3f317217, v20
	v_cmp_lt_f32_e64 s[60:61], |v20|, s36
	s_nop 1
	v_cndmask_b32_e64 v20, v20, v27, s[60:61]
	v_cndmask_b32_e32 v27, 0, v216, vcc
	v_sub_f32_e32 v76, v20, v27
	v_max_f32_e32 v20, v21, v21
	v_min_f32_e32 v27, 0, v20
	v_mul_f32_e64 v20, |v21|, s8
	v_exp_f32_e32 v20, v20
	s_nop 0
	v_add_f32_e32 v20, 1.0, v20
	v_cmp_gt_f32_e32 vcc, s37, v20
	s_nop 1
	v_cndmask_b32_e64 v43, 0, 32, vcc
	v_ldexp_f32 v20, v20, v43
	v_log_f32_e32 v20, v20
	s_nop 0
	v_mul_f32_e32 v43, 0x3f317217, v20
	v_fma_f32 v43, v20, s33, -v43
	v_fmac_f32_e32 v43, 0x3377d1cf, v20
	v_fmac_f32_e32 v43, 0x3f317217, v20
	v_cmp_lt_f32_e64 s[60:61], |v20|, s36
	s_nop 1
	v_cndmask_b32_e64 v20, v20, v43, s[60:61]
	v_cndmask_b32_e32 v43, 0, v216, vcc
	v_sub_f32_e32 v43, v20, v43
	v_mul_f32_e32 v20, 0xbfb8aa3b, v21
	v_exp_f32_e32 v20, v20
	v_pk_add_f32 v[26:27], v[26:27], v[42:43] neg_lo:[0,1] neg_hi:[0,1]
	v_add_f32_e32 v20, 1.0, v20
	v_div_scale_f32 v21, s[2:3], v20, v20, v156
	v_rcp_f32_e32 v44, v21
	v_cndmask_b32_e64 v42, v76, v26, s[44:45]
	v_fma_f32 v45, -v21, v44, 1.0
	v_fmac_f32_e32 v44, v45, v44
	v_div_scale_f32 v45, vcc, v156, v20, v156
	v_mul_f32_e32 v46, v45, v44
	v_fma_f32 v47, -v21, v46, v45
	v_fmac_f32_e32 v46, v47, v44
	v_fma_f32 v21, -v21, v46, v45
	v_div_fmas_f32 v21, v21, v44, v46
	v_div_fixup_f32 v20, v21, v20, v156
	v_add_f32_e32 v20, v69, v20
	v_cmp_gt_f32_e32 vcc, s37, v20
	v_mov_b32_dpp v26, v42 row_shr:1 row_mask:0xf bank_mask:0xf bound_ctrl:1
	s_nop 0
	v_cndmask_b32_e64 v21, 0, 32, vcc
	v_ldexp_f32 v20, v20, v21
	v_log_f32_e32 v20, v20
	s_nop 0
	v_mul_f32_e32 v21, 0x3f317217, v20
	v_fma_f32 v21, v20, s33, -v21
	v_fmac_f32_e32 v21, 0x3377d1cf, v20
	v_fmac_f32_e32 v21, 0x3f317217, v20
	v_cmp_lt_f32_e64 s[60:61], |v20|, s36
	s_nop 1
	v_cndmask_b32_e64 v20, v20, v21, s[60:61]
	v_cndmask_b32_e32 v21, 0, v216, vcc
	v_sub_f32_e32 v77, v20, v21
	v_max_f32_e32 v20, v22, v22
	v_min_f32_e32 v44, 0, v20
	v_mul_f32_e64 v20, |v22|, s8
	v_exp_f32_e32 v20, v20
	v_cndmask_b32_e64 v43, v77, v27, s[46:47]
	v_add_f32_e32 v20, 1.0, v20
	v_cmp_gt_f32_e32 vcc, s37, v20
	v_mov_b32_dpp v27, v43 row_shr:1 row_mask:0xf bank_mask:0xf bound_ctrl:1
	v_pk_add_f32 v[26:27], v[42:43], v[26:27]
	v_cndmask_b32_e64 v21, 0, 32, vcc
	v_ldexp_f32 v20, v20, v21
	v_log_f32_e32 v20, v20
	v_mov_b32_dpp v72, v26 row_shr:2 row_mask:0xf bank_mask:0xf bound_ctrl:1
	v_mov_b32_dpp v73, v27 row_shr:2 row_mask:0xf bank_mask:0xf bound_ctrl:1
	v_pk_add_f32 v[26:27], v[26:27], v[72:73]
	v_mul_f32_e32 v21, 0x3f317217, v20
	v_fma_f32 v21, v20, s33, -v21
	v_fmac_f32_e32 v21, 0x3377d1cf, v20
	v_fmac_f32_e32 v21, 0x3f317217, v20
	v_cmp_lt_f32_e64 s[60:61], |v20|, s36
	v_mov_b32_dpp v72, v26 row_shr:4 row_mask:0xf bank_mask:0xf bound_ctrl:1
	v_mov_b32_dpp v73, v27 row_shr:4 row_mask:0xf bank_mask:0xf bound_ctrl:1
	v_cndmask_b32_e64 v20, v20, v21, s[60:61]
	v_cndmask_b32_e32 v21, 0, v216, vcc
	v_sub_f32_e32 v46, v20, v21
	v_mul_f32_e32 v20, 0xbfb8aa3b, v22
	v_exp_f32_e32 v20, v20
	v_pk_add_f32 v[26:27], v[26:27], v[72:73]
	v_add_f32_e32 v20, 1.0, v20
	v_div_scale_f32 v21, s[2:3], v20, v20, v155
	v_rcp_f32_e32 v22, v21
	v_mov_b32_dpp v72, v26 row_shr:8 row_mask:0xf bank_mask:0xf bound_ctrl:1
	v_mov_b32_dpp v73, v27 row_shr:8 row_mask:0xf bank_mask:0xf bound_ctrl:1
	v_pk_add_f32 v[26:27], v[26:27], v[72:73]
	v_fma_f32 v45, -v21, v22, 1.0
	v_fmac_f32_e32 v22, v45, v22
	v_div_scale_f32 v45, vcc, v155, v20, v155
	v_mul_f32_e32 v47, v45, v22
	v_fma_f32 v52, -v21, v47, v45
	v_fmac_f32_e32 v47, v52, v22
	v_fma_f32 v21, -v21, v47, v45
	v_div_fmas_f32 v21, v21, v22, v47
	v_div_fixup_f32 v20, v21, v20, v155
	v_add_f32_e32 v20, v70, v20
	v_cmp_gt_f32_e32 vcc, s37, v20
	ds_swizzle_b32 v72, v26 offset:swizzle(BROADCAST,16,15)
	ds_swizzle_b32 v73, v27 offset:swizzle(BROADCAST,16,15)
	v_cndmask_b32_e64 v21, 0, 32, vcc
	v_ldexp_f32 v20, v20, v21
	v_log_f32_e32 v20, v20
	s_nop 0
	v_mul_f32_e32 v21, 0x3f317217, v20
	v_fma_f32 v21, v20, s33, -v21
	v_fmac_f32_e32 v21, 0x3377d1cf, v20
	v_fmac_f32_e32 v21, 0x3f317217, v20
	v_cmp_lt_f32_e64 s[60:61], |v20|, s36
	s_nop 1
	v_cndmask_b32_e64 v20, v20, v21, s[60:61]
	v_cndmask_b32_e32 v21, 0, v216, vcc
	v_sub_f32_e32 v78, v20, v21
	v_max_f32_e32 v20, v23, v23
	v_min_f32_e32 v45, 0, v20
; template <int CTRL> __device__ __forceinline__ float dppx(float v) { return __int_as_float(__builtin_amdgcn_update_dpp(0, __float_as_int(v), CTRL, 0xf, 0xf, true)); }
; __device__ __forceinline__ float log_forget(float z, float lb) {
;   const float r0 = fminf(z, 0.f) - __logf(1.f + __expf(-fabsf(z)));
;   const float r1 = __logf(lb + (1.f - lb) / (1.f + __expf(-z)));
;   return lb <= 0.f ? r0 : r1;
; }
;   __device__ __forceinline__ void operator()(const f32x4 (&acc)[2][2][4][2], const pg8::Unit& u, int wr, int wc, int fr, int fq) const {
;     ...
;               for (int q = 0; q < 4; ++q) { const float gv = log_forget(acc[ai][bj][m][qh][q], lq[q]); g[m][q] = gv;
;                 float sc = gv; sc += dppx<0x111>(sc); sc += dppx<0x112>(sc); sc += dppx<0x114>(sc); sc += dppx<0x118>(sc);
	v_mul_f32_e64 v20, |v23|, s8
	v_exp_f32_e32 v20, v20
	s_nop 0
	v_add_f32_e32 v20, 1.0, v20
	v_cmp_gt_f32_e32 vcc, s37, v20
	s_nop 1
	v_cndmask_b32_e64 v21, 0, 32, vcc
	v_ldexp_f32 v20, v20, v21
	v_log_f32_e32 v20, v20
	s_nop 0
	v_mul_f32_e32 v21, 0x3f317217, v20
	v_fma_f32 v21, v20, s33, -v21
	v_fmac_f32_e32 v21, 0x3377d1cf, v20
	v_fmac_f32_e32 v21, 0x3f317217, v20
	v_cmp_lt_f32_e64 s[60:61], |v20|, s36
	s_nop 1
	v_cndmask_b32_e64 v20, v20, v21, s[60:61]
	v_cndmask_b32_e32 v21, 0, v216, vcc
	v_sub_f32_e32 v47, v20, v21
	v_mul_f32_e32 v20, 0xbfb8aa3b, v23
	v_exp_f32_e32 v20, v20
	s_nop 0
	v_add_f32_e32 v20, 1.0, v20
	v_div_scale_f32 v21, s[2:3], v20, v20, v154
	v_rcp_f32_e32 v22, v21
	s_nop 0
	v_fma_f32 v23, -v21, v22, 1.0
	v_fmac_f32_e32 v22, v23, v22
	v_div_scale_f32 v23, vcc, v154, v20, v154
	v_mul_f32_e32 v52, v23, v22
	v_fma_f32 v53, -v21, v52, v23
	v_fmac_f32_e32 v52, v53, v22
	v_fma_f32 v21, -v21, v52, v23
	v_div_fmas_f32 v21, v21, v22, v52
	v_div_fixup_f32 v20, v21, v20, v154
	v_add_f32_e32 v20, v71, v20
	v_cmp_gt_f32_e32 vcc, s37, v20
	s_nop 1
	v_cndmask_b32_e64 v21, 0, 32, vcc
	v_ldexp_f32 v20, v20, v21
	v_log_f32_e32 v20, v20
	s_nop 0
	v_mul_f32_e32 v21, 0x3f317217, v20
	v_fma_f32 v21, v20, s33, -v21
	v_fmac_f32_e32 v21, 0x3377d1cf, v20
	v_fmac_f32_e32 v21, 0x3f317217, v20
	v_cmp_lt_f32_e64 s[60:61], |v20|, s36
	s_nop 1
	v_cndmask_b32_e64 v20, v20, v21, s[60:61]
	v_cndmask_b32_e32 v21, 0, v216, vcc
	v_sub_f32_e32 v79, v20, v21
	v_max_f32_e32 v20, v16, v16
	v_min_f32_e32 v52, 0, v20
	v_mul_f32_e64 v20, |v16|, s8
	v_exp_f32_e32 v20, v20
	v_mul_f32_e32 v16, 0xbfb8aa3b, v16
	v_exp_f32_e32 v16, v16
	v_add_f32_e32 v20, 1.0, v20
	v_cmp_gt_f32_e32 vcc, s37, v20
	v_add_f32_e32 v16, 1.0, v16
	s_nop 0
	v_cndmask_b32_e64 v21, 0, 32, vcc
	v_ldexp_f32 v20, v20, v21
	v_log_f32_e32 v20, v20
	s_nop 0
	v_mul_f32_e32 v21, 0x3f317217, v20
	v_fma_f32 v21, v20, s33, -v21
	v_fmac_f32_e32 v21, 0x3377d1cf, v20
	v_fmac_f32_e32 v21, 0x3f317217, v20
	v_cmp_lt_f32_e64 s[60:61], |v20|, s36
	s_nop 1
	v_cndmask_b32_e64 v20, v20, v21, s[60:61]
	v_cndmask_b32_e32 v21, 0, v216, vcc
	v_sub_f32_e32 v54, v20, v21
	v_div_scale_f32 v20, s[2:3], v16, v16, v157
	v_rcp_f32_e32 v21, v20
	s_nop 0
	v_fma_f32 v22, -v20, v21, 1.0
	v_fmac_f32_e32 v21, v22, v21
	v_div_scale_f32 v22, vcc, v157, v16, v157
	v_mul_f32_e32 v23, v22, v21
	v_fma_f32 v53, -v20, v23, v22
	v_fmac_f32_e32 v23, v53, v21
	v_fma_f32 v20, -v20, v23, v22
	v_div_fmas_f32 v20, v20, v21, v23
	v_div_fixup_f32 v16, v20, v16, v157
	v_add_f32_e32 v16, v68, v16
	v_cmp_gt_f32_e32 vcc, s37, v16
	s_nop 1
	v_cndmask_b32_e64 v20, 0, 32, vcc
	v_ldexp_f32 v16, v16, v20
	v_log_f32_e32 v16, v16
	s_nop 0
	v_mul_f32_e32 v20, 0x3f317217, v16
	v_fma_f32 v20, v16, s33, -v20
	v_fmac_f32_e32 v20, 0x3377d1cf, v16
	v_fmac_f32_e32 v20, 0x3f317217, v16
	v_cmp_lt_f32_e64 s[60:61], |v16|, s36
	s_nop 1
	v_cndmask_b32_e64 v16, v16, v20, s[60:61]
	v_cndmask_b32_e32 v20, 0, v216, vcc
	v_sub_f32_e32 v68, v16, v20
	v_max_f32_e32 v16, v17, v17
	v_min_f32_e32 v53, 0, v16
	v_mul_f32_e64 v16, |v17|, s8
	v_exp_f32_e32 v16, v16
	s_nop 0
	v_add_f32_e32 v16, 1.0, v16
	v_cmp_gt_f32_e32 vcc, s37, v16
	s_nop 1
	v_cndmask_b32_e64 v20, 0, 32, vcc
	v_ldexp_f32 v16, v16, v20
	v_log_f32_e32 v16, v16
	s_nop 0
	v_mul_f32_e32 v20, 0x3f317217, v16
	v_fma_f32 v20, v16, s33, -v20
	v_fmac_f32_e32 v20, 0x3377d1cf, v16
	v_fmac_f32_e32 v20, 0x3f317217, v16
	v_cmp_lt_f32_e64 s[60:61], |v16|, s36
	s_nop 1
	v_cndmask_b32_e64 v16, v16, v20, s[60:61]
	v_cndmask_b32_e32 v20, 0, v216, vcc
	v_sub_f32_e32 v55, v16, v20
	v_mul_f32_e32 v16, 0xbfb8aa3b, v17
	v_exp_f32_e32 v16, v16
	v_pk_add_f32 v[52:53], v[52:53], v[54:55] neg_lo:[0,1] neg_hi:[0,1]
	v_add_f32_e32 v16, 1.0, v16
	v_div_scale_f32 v17, s[2:3], v16, v16, v156
	v_rcp_f32_e32 v20, v17
	v_cndmask_b32_e64 v52, v68, v52, s[44:45]
	v_fma_f32 v21, -v17, v20, 1.0
	v_fmac_f32_e32 v20, v21, v20
	v_div_scale_f32 v21, vcc, v156, v16, v156
	v_mul_f32_e32 v22, v21, v20
	v_fma_f32 v23, -v17, v22, v21
	v_fmac_f32_e32 v22, v23, v20
	v_fma_f32 v17, -v17, v22, v21
	v_div_fmas_f32 v17, v17, v20, v22
	v_div_fixup_f32 v16, v17, v16, v156
	v_add_f32_e32 v16, v69, v16
	v_cmp_gt_f32_e32 vcc, s37, v16
	v_mov_b32_dpp v54, v52 row_shr:1 row_mask:0xf bank_mask:0xf bound_ctrl:1
	s_nop 0
	v_cndmask_b32_e64 v17, 0, 32, vcc
	v_ldexp_f32 v16, v16, v17
	v_log_f32_e32 v16, v16
	s_nop 0
	v_mul_f32_e32 v17, 0x3f317217, v16
	v_fma_f32 v17, v16, s33, -v17
	v_fmac_f32_e32 v17, 0x3377d1cf, v16
	v_fmac_f32_e32 v17, 0x3f317217, v16
	v_cmp_lt_f32_e64 s[60:61], |v16|, s36
	s_nop 1
	v_cndmask_b32_e64 v16, v16, v17, s[60:61]
	v_cndmask_b32_e32 v17, 0, v216, vcc
	v_sub_f32_e32 v69, v16, v17
	v_max_f32_e32 v16, v18, v18
	v_min_f32_e32 v56, 0, v16
	v_mul_f32_e64 v16, |v18|, s8
	v_exp_f32_e32 v16, v16
	v_cndmask_b32_e64 v53, v69, v53, s[46:47]
	v_add_f32_e32 v16, 1.0, v16
	v_cmp_gt_f32_e32 vcc, s37, v16
	v_mov_b32_dpp v55, v53 row_shr:1 row_mask:0xf bank_mask:0xf bound_ctrl:1
	v_pk_add_f32 v[54:55], v[52:53], v[54:55]
	v_cndmask_b32_e64 v17, 0, 32, vcc
	v_ldexp_f32 v16, v16, v17
	v_log_f32_e32 v16, v16
	v_mov_b32_dpp v68, v54 row_shr:2 row_mask:0xf bank_mask:0xf bound_ctrl:1
	v_mov_b32_dpp v69, v55 row_shr:2 row_mask:0xf bank_mask:0xf bound_ctrl:1
	v_pk_add_f32 v[54:55], v[54:55], v[68:69]
	v_mul_f32_e32 v17, 0x3f317217, v16
	v_fma_f32 v17, v16, s33, -v17
	v_fmac_f32_e32 v17, 0x3377d1cf, v16
	v_fmac_f32_e32 v17, 0x3f317217, v16
	v_cmp_lt_f32_e64 s[60:61], |v16|, s36
	v_mov_b32_dpp v68, v54 row_shr:4 row_mask:0xf bank_mask:0xf bound_ctrl:1
	v_mov_b32_dpp v69, v55 row_shr:4 row_mask:0xf bank_mask:0xf bound_ctrl:1
	v_cndmask_b32_e64 v16, v16, v17, s[60:61]
; template <int CTRL> __device__ __forceinline__ float dppx(float v) { return __int_as_float(__builtin_amdgcn_update_dpp(0, __float_as_int(v), CTRL, 0xf, 0xf, true)); }
; __device__ __forceinline__ float log_forget(float z, float lb) {
;   const float r0 = fminf(z, 0.f) - __logf(1.f + __expf(-fabsf(z)));
;   const float r1 = __logf(lb + (1.f - lb) / (1.f + __expf(-z)));
;   return lb <= 0.f ? r0 : r1;
; }
;   __device__ __forceinline__ void operator()(const f32x4 (&acc)[2][2][4][2], const pg8::Unit& u, int wr, int wc, int fr, int fq) const {
;     ...
;                 float sc = gv; sc += dppx<0x111>(sc); sc += dppx<0x112>(sc); sc += dppx<0x114>(sc); sc += dppx<0x118>(sc);
;                 const float tot16 = __int_as_float(__builtin_amdgcn_ds_swizzle(__float_as_int(sc), 0x1F0));
;                 cs[m][q] = sc + carry[q]; carry[q] += tot16; }
; #pragma unroll
;             for (int m = 0; m < 4; ++m) { const int r = row0 + ai * 128 + m * 16; float bq[4], kq[4];
; #pragma unroll
;               for (int q = 0; q < 4; ++q) { bq[q] = bwd ? (carry[q] - cs[m][q]) + g[m][q] : cs[m][q]; kq[q] = 1.f - __expf(g[m][q]); }
	v_cndmask_b32_e32 v17, 0, v216, vcc
	v_sub_f32_e32 v58, v16, v17
	v_mul_f32_e32 v16, 0xbfb8aa3b, v18
	v_exp_f32_e32 v16, v16
	v_pk_add_f32 v[54:55], v[54:55], v[68:69]
	v_add_f32_e32 v16, 1.0, v16
	v_div_scale_f32 v17, s[2:3], v16, v16, v155
	v_rcp_f32_e32 v18, v17
	v_mov_b32_dpp v68, v54 row_shr:8 row_mask:0xf bank_mask:0xf bound_ctrl:1
	v_mov_b32_dpp v69, v55 row_shr:8 row_mask:0xf bank_mask:0xf bound_ctrl:1
	v_pk_add_f32 v[54:55], v[54:55], v[68:69]
	v_fma_f32 v20, -v17, v18, 1.0
	v_fmac_f32_e32 v18, v20, v18
	v_div_scale_f32 v20, vcc, v155, v16, v155
	v_mul_f32_e32 v21, v20, v18
	v_fma_f32 v22, -v17, v21, v20
	v_fmac_f32_e32 v21, v22, v18
	v_fma_f32 v17, -v17, v21, v20
	v_div_fmas_f32 v17, v17, v18, v21
	v_div_fixup_f32 v16, v17, v16, v155
	v_add_f32_e32 v16, v70, v16
	v_cmp_gt_f32_e32 vcc, s37, v16
	ds_swizzle_b32 v68, v54 offset:swizzle(BROADCAST,16,15)
	ds_swizzle_b32 v69, v55 offset:swizzle(BROADCAST,16,15)
	v_cndmask_b32_e64 v17, 0, 32, vcc
	v_ldexp_f32 v16, v16, v17
	v_log_f32_e32 v16, v16
	s_nop 0
	v_mul_f32_e32 v17, 0x3f317217, v16
	v_fma_f32 v17, v16, s33, -v17
	v_fmac_f32_e32 v17, 0x3377d1cf, v16
	v_fmac_f32_e32 v17, 0x3f317217, v16
	v_cmp_lt_f32_e64 s[60:61], |v16|, s36
	s_nop 1
	v_cndmask_b32_e64 v16, v16, v17, s[60:61]
	v_cndmask_b32_e32 v17, 0, v216, vcc
	v_sub_f32_e32 v70, v16, v17
	v_max_f32_e32 v16, v19, v19
	v_min_f32_e32 v57, 0, v16
	v_mul_f32_e64 v16, |v19|, s8
	v_exp_f32_e32 v16, v16
	s_nop 0
	v_add_f32_e32 v16, 1.0, v16
	v_cmp_gt_f32_e32 vcc, s37, v16
	s_nop 1
	v_cndmask_b32_e64 v17, 0, 32, vcc
	v_ldexp_f32 v16, v16, v17
	v_log_f32_e32 v16, v16
	s_nop 0
	v_mul_f32_e32 v17, 0x3f317217, v16
	v_fma_f32 v17, v16, s33, -v17
	v_fmac_f32_e32 v17, 0x3377d1cf, v16
	v_fmac_f32_e32 v17, 0x3f317217, v16
	v_cmp_lt_f32_e64 s[60:61], |v16|, s36
	s_nop 1
	v_cndmask_b32_e64 v16, v16, v17, s[60:61]
	v_cndmask_b32_e32 v17, 0, v216, vcc
	v_sub_f32_e32 v59, v16, v17
	v_mul_f32_e32 v16, 0xbfb8aa3b, v19
	v_exp_f32_e32 v16, v16
	v_pk_add_f32 v[56:57], v[56:57], v[58:59] neg_lo:[0,1] neg_hi:[0,1]
	v_add_f32_e32 v16, 1.0, v16
	v_div_scale_f32 v17, s[2:3], v16, v16, v154
	v_rcp_f32_e32 v18, v17
	v_cndmask_b32_e64 v56, v70, v56, s[50:51]
	v_fma_f32 v19, -v17, v18, 1.0
	v_fmac_f32_e32 v18, v19, v18
	v_div_scale_f32 v19, vcc, v154, v16, v154
	v_mul_f32_e32 v20, v19, v18
	v_fma_f32 v21, -v17, v20, v19
	v_fmac_f32_e32 v20, v21, v18
	v_fma_f32 v17, -v17, v20, v19
	v_div_fmas_f32 v17, v17, v18, v20
	v_div_fixup_f32 v16, v17, v16, v154
	v_add_f32_e32 v16, v71, v16
	v_cmp_gt_f32_e32 vcc, s37, v16
	v_mov_b32_dpp v58, v56 row_shr:1 row_mask:0xf bank_mask:0xf bound_ctrl:1
	s_nop 0
	v_cndmask_b32_e64 v17, 0, 32, vcc
	v_ldexp_f32 v16, v16, v17
	v_log_f32_e32 v16, v16
	s_nop 0
	v_mul_f32_e32 v17, 0x3f317217, v16
	v_fma_f32 v17, v16, s33, -v17
	v_fmac_f32_e32 v17, 0x3377d1cf, v16
	v_fmac_f32_e32 v17, 0x3f317217, v16
	v_cmp_lt_f32_e64 s[60:61], |v16|, s36
	s_nop 1
	v_cndmask_b32_e64 v16, v16, v17, s[60:61]
	v_cndmask_b32_e32 v17, 0, v216, vcc
	v_sub_f32_e32 v71, v16, v17
	v_pk_add_f32 v[16:17], v[32:33], v[34:35] neg_lo:[0,1] neg_hi:[0,1]
	v_cndmask_b32_e64 v57, v71, v57, s[54:55]
	v_cndmask_b32_e64 v33, v61, v17, s[46:47]
	v_cndmask_b32_e64 v32, v60, v16, s[44:45]
	v_mov_b32_dpp v60, v38 row_shr:2 row_mask:0xf bank_mask:0xf bound_ctrl:1
	v_mov_b32_dpp v17, v33 row_shr:1 row_mask:0xf bank_mask:0xf bound_ctrl:1
	v_mov_b32_dpp v16, v32 row_shr:1 row_mask:0xf bank_mask:0xf bound_ctrl:1
	v_pk_add_f32 v[16:17], v[32:33], v[16:17]
	v_mov_b32_dpp v61, v39 row_shr:2 row_mask:0xf bank_mask:0xf bound_ctrl:1
	v_pk_add_f32 v[38:39], v[38:39], v[60:61]
	v_mov_b32_dpp v18, v16 row_shr:2 row_mask:0xf bank_mask:0xf bound_ctrl:1
	v_mov_b32_dpp v19, v17 row_shr:2 row_mask:0xf bank_mask:0xf bound_ctrl:1
	v_pk_add_f32 v[16:17], v[16:17], v[18:19]
	v_mov_b32_dpp v60, v38 row_shr:4 row_mask:0xf bank_mask:0xf bound_ctrl:1
	v_mov_b32_dpp v61, v39 row_shr:4 row_mask:0xf bank_mask:0xf bound_ctrl:1
	v_mov_b32_dpp v18, v16 row_shr:4 row_mask:0xf bank_mask:0xf bound_ctrl:1
	v_mov_b32_dpp v19, v17 row_shr:4 row_mask:0xf bank_mask:0xf bound_ctrl:1
	v_pk_add_f32 v[16:17], v[16:17], v[18:19]
	v_pk_add_f32 v[38:39], v[38:39], v[60:61]
	v_mov_b32_dpp v59, v57 row_shr:1 row_mask:0xf bank_mask:0xf bound_ctrl:1
	v_mov_b32_dpp v18, v16 row_shr:8 row_mask:0xf bank_mask:0xf bound_ctrl:1
	v_mov_b32_dpp v19, v17 row_shr:8 row_mask:0xf bank_mask:0xf bound_ctrl:1
	v_pk_add_f32 v[16:17], v[16:17], v[18:19]
	ds_swizzle_b32 v18, v16 offset:swizzle(BROADCAST,16,15)
	v_pk_add_f32 v[34:35], v[16:17], 0 op_sel_hi:[1,0]
	v_mul_f32_e32 v16, 0x3fb8aa3b, v32
	v_exp_f32_e32 v16, v16
	ds_swizzle_b32 v19, v17 offset:swizzle(BROADCAST,16,15)
	v_mov_b32_dpp v60, v38 row_shr:8 row_mask:0xf bank_mask:0xf bound_ctrl:1
	v_mov_b32_dpp v61, v39 row_shr:8 row_mask:0xf bank_mask:0xf bound_ctrl:1
	v_sub_f32_e32 v80, 1.0, v16
	v_mul_f32_e32 v16, 0x3fb8aa3b, v33
	v_exp_f32_e32 v16, v16
	s_waitcnt lgkmcnt(0)
	v_pk_add_f32 v[20:21], v[18:19], 0 op_sel_hi:[1,0]
	v_pk_add_f32 v[38:39], v[38:39], v[60:61]
	ds_swizzle_b32 v60, v38 offset:swizzle(BROADCAST,16,15)
	v_sub_f32_e32 v81, 1.0, v16
	v_pk_add_f32 v[16:17], v[28:29], v[36:37] neg_lo:[0,1] neg_hi:[0,1]
	ds_swizzle_b32 v61, v39 offset:swizzle(BROADCAST,16,15)
	v_cndmask_b32_e64 v29, v63, v17, s[54:55]
	v_cndmask_b32_e64 v28, v62, v16, s[50:51]
	v_pk_add_f32 v[38:39], v[20:21], v[38:39]
	v_mov_b32_dpp v17, v29 row_shr:1 row_mask:0xf bank_mask:0xf bound_ctrl:1
	v_mov_b32_dpp v16, v28 row_shr:1 row_mask:0xf bank_mask:0xf bound_ctrl:1
	v_pk_add_f32 v[16:17], v[28:29], v[16:17]
	s_waitcnt lgkmcnt(0)
; template <int CTRL> __device__ __forceinline__ float dppx(float v) { return __int_as_float(__builtin_amdgcn_update_dpp(0, __float_as_int(v), CTRL, 0xf, 0xf, true)); }
;   __device__ __forceinline__ void operator()(const f32x4 (&acc)[2][2][4][2], const pg8::Unit& u, int wr, int wc, int fr, int fq) const {
;     ...
;           for (int qh = 0; qh < 2; ++qh) { float g[4][4], cs[4][4], carry[4];
;             const f32x4 lq = qh == 0 ? l0 : l1;
; #pragma unroll
;             for (int q = 0; q < 4; ++q) carry[q] = 0.f;
; #pragma unroll
;             for (int m = 0; m < 4; ++m)
; #pragma unroll
;               for (int q = 0; q < 4; ++q) { const float gv = log_forget(acc[ai][bj][m][qh][q], lq[q]); g[m][q] = gv;
;                 float sc = gv; sc += dppx<0x111>(sc); sc += dppx<0x112>(sc); sc += dppx<0x114>(sc); sc += dppx<0x118>(sc);
;                 const float tot16 = __int_as_float(__builtin_amdgcn_ds_swizzle(__float_as_int(sc), 0x1F0));
;                 cs[m][q] = sc + carry[q]; carry[q] += tot16; }
; #pragma unroll
;             for (int m = 0; m < 4; ++m) { const int r = row0 + ai * 128 + m * 16; float bq[4], kq[4];
; #pragma unroll
;               for (int q = 0; q < 4; ++q) { bq[q] = bwd ? (carry[q] - cs[m][q]) + g[m][q] : cs[m][q]; kq[q] = 1.f - __expf(g[m][q]); }
	v_pk_add_f32 v[62:63], v[20:21], v[60:61]
	v_mul_f32_e32 v20, 0x3fb8aa3b, v30
	v_mov_b32_dpp v18, v16 row_shr:2 row_mask:0xf bank_mask:0xf bound_ctrl:1
	v_mov_b32_dpp v19, v17 row_shr:2 row_mask:0xf bank_mask:0xf bound_ctrl:1
	v_pk_add_f32 v[16:17], v[16:17], v[18:19]
	v_exp_f32_e32 v20, v20
	v_pk_add_f32 v[58:59], v[56:57], v[58:59]
	v_mov_b32_dpp v18, v16 row_shr:4 row_mask:0xf bank_mask:0xf bound_ctrl:1
	v_mov_b32_dpp v19, v17 row_shr:4 row_mask:0xf bank_mask:0xf bound_ctrl:1
	v_pk_add_f32 v[16:17], v[16:17], v[18:19]
	s_nop 1
	v_mov_b32_dpp v18, v16 row_shr:8 row_mask:0xf bank_mask:0xf bound_ctrl:1
	v_mov_b32_dpp v19, v17 row_shr:8 row_mask:0xf bank_mask:0xf bound_ctrl:1
	v_pk_add_f32 v[16:17], v[16:17], v[18:19]
	ds_swizzle_b32 v18, v16 offset:swizzle(BROADCAST,16,15)
	ds_swizzle_b32 v19, v17 offset:swizzle(BROADCAST,16,15)
	v_pk_add_f32 v[36:37], v[16:17], 0 op_sel_hi:[1,0]
	v_mul_f32_e32 v16, 0x3fb8aa3b, v28
	v_exp_f32_e32 v16, v16
	s_waitcnt lgkmcnt(0)
	v_pk_add_f32 v[22:23], v[18:19], 0 op_sel_hi:[1,0]
	v_lshl_add_u64 v[18:19], v[84:85], 0, v[50:51]
	v_sub_f32_e32 v84, 1.0, v20
	v_mul_f32_e32 v20, 0x3fb8aa3b, v31
	v_exp_f32_e32 v20, v20
	v_sub_f32_e32 v82, 1.0, v16
	v_mul_f32_e32 v16, 0x3fb8aa3b, v29
	v_exp_f32_e32 v16, v16
	v_sub_f32_e32 v85, 1.0, v20
	v_pk_add_f32 v[20:21], v[24:25], v[40:41] neg_lo:[0,1] neg_hi:[0,1]
	v_sub_f32_e32 v83, 1.0, v16
	v_cndmask_b32_e64 v41, v75, v21, s[54:55]
	v_cndmask_b32_e64 v40, v74, v20, s[50:51]
	v_pk_add_f32 v[74:75], v[62:63], v[26:27]
	v_mov_b32_dpp v21, v41 row_shr:1 row_mask:0xf bank_mask:0xf bound_ctrl:1
	v_mov_b32_dpp v20, v40 row_shr:1 row_mask:0xf bank_mask:0xf bound_ctrl:1
	v_pk_add_f32 v[20:21], v[40:41], v[20:21]
	v_mul_f32_e32 v26, 0x3fb8aa3b, v42
	v_exp_f32_e32 v26, v26
	v_mov_b32_dpp v24, v20 row_shr:2 row_mask:0xf bank_mask:0xf bound_ctrl:1
	v_mov_b32_dpp v25, v21 row_shr:2 row_mask:0xf bank_mask:0xf bound_ctrl:1
	v_pk_add_f32 v[20:21], v[20:21], v[24:25]
	v_pk_add_f32 v[62:63], v[62:63], v[72:73]
	v_sub_f32_e32 v76, 1.0, v26
	v_mov_b32_dpp v24, v20 row_shr:4 row_mask:0xf bank_mask:0xf bound_ctrl:1
	v_mov_b32_dpp v25, v21 row_shr:4 row_mask:0xf bank_mask:0xf bound_ctrl:1
	v_pk_add_f32 v[20:21], v[20:21], v[24:25]
	v_mul_f32_e32 v26, 0x3fb8aa3b, v43
	v_pk_add_f32 v[54:55], v[62:63], v[54:55]
	v_mov_b32_dpp v24, v20 row_shr:8 row_mask:0xf bank_mask:0xf bound_ctrl:1
	v_mov_b32_dpp v25, v21 row_shr:8 row_mask:0xf bank_mask:0xf bound_ctrl:1
	v_pk_add_f32 v[20:21], v[20:21], v[24:25]
	ds_swizzle_b32 v24, v20 offset:swizzle(BROADCAST,16,15)
	ds_swizzle_b32 v25, v21 offset:swizzle(BROADCAST,16,15)
	v_pk_add_f32 v[62:63], v[62:63], v[68:69]
	v_mul_f32_e32 v68, 0x3fb8aa3b, v52
	v_exp_f32_e32 v26, v26
	v_exp_f32_e32 v68, v68
	v_pk_add_f32 v[60:61], v[22:23], v[20:21]
	s_waitcnt lgkmcnt(0)
	v_pk_add_f32 v[24:25], v[22:23], v[24:25]
	v_lshl_add_u64 v[22:23], v[88:89], 0, v[50:51]
	v_sub_f32_e32 v77, 1.0, v26
	v_pk_add_f32 v[26:27], v[44:45], v[46:47] neg_lo:[0,1] neg_hi:[0,1]
	v_sub_f32_e32 v88, 1.0, v68
	v_mul_f32_e32 v68, 0x3fb8aa3b, v53
	v_cndmask_b32_e64 v45, v79, v27, s[54:55]
	v_cndmask_b32_e64 v44, v78, v26, s[50:51]
	v_exp_f32_e32 v68, v68
	v_mov_b32_dpp v27, v45 row_shr:1 row_mask:0xf bank_mask:0xf bound_ctrl:1
	v_mov_b32_dpp v26, v44 row_shr:1 row_mask:0xf bank_mask:0xf bound_ctrl:1
	v_pk_add_f32 v[26:27], v[44:45], v[26:27]
	v_sub_f32_e32 v89, 1.0, v68
	v_mov_b32_dpp v68, v58 row_shr:2 row_mask:0xf bank_mask:0xf bound_ctrl:1
	v_mov_b32_dpp v46, v26 row_shr:2 row_mask:0xf bank_mask:0xf bound_ctrl:1
	v_mov_b32_dpp v47, v27 row_shr:2 row_mask:0xf bank_mask:0xf bound_ctrl:1
	v_pk_add_f32 v[26:27], v[26:27], v[46:47]
	v_mov_b32_dpp v69, v59 row_shr:2 row_mask:0xf bank_mask:0xf bound_ctrl:1
	v_pk_add_f32 v[58:59], v[58:59], v[68:69]
	v_mov_b32_dpp v46, v26 row_shr:4 row_mask:0xf bank_mask:0xf bound_ctrl:1
	v_mov_b32_dpp v47, v27 row_shr:4 row_mask:0xf bank_mask:0xf bound_ctrl:1
	v_pk_add_f32 v[26:27], v[26:27], v[46:47]
	v_mov_b32_dpp v68, v58 row_shr:4 row_mask:0xf bank_mask:0xf bound_ctrl:1
	v_mov_b32_dpp v69, v59 row_shr:4 row_mask:0xf bank_mask:0xf bound_ctrl:1
	v_mov_b32_dpp v46, v26 row_shr:8 row_mask:0xf bank_mask:0xf bound_ctrl:1
	v_mov_b32_dpp v47, v27 row_shr:8 row_mask:0xf bank_mask:0xf bound_ctrl:1
	v_pk_add_f32 v[58:59], v[58:59], v[68:69]
	v_pk_add_f32 v[26:27], v[26:27], v[46:47]
	ds_swizzle_b32 v46, v26 offset:swizzle(BROADCAST,16,15)
	v_mov_b32_dpp v68, v58 row_shr:8 row_mask:0xf bank_mask:0xf bound_ctrl:1
	v_mov_b32_dpp v69, v59 row_shr:8 row_mask:0xf bank_mask:0xf bound_ctrl:1
	ds_swizzle_b32 v47, v27 offset:swizzle(BROADCAST,16,15)
	v_pk_add_f32 v[58:59], v[58:59], v[68:69]
	ds_swizzle_b32 v68, v58 offset:swizzle(BROADCAST,16,15)
	ds_swizzle_b32 v69, v59 offset:swizzle(BROADCAST,16,15)
	v_mul_f32_e32 v20, 0x3fb8aa3b, v40
	v_exp_f32_e32 v20, v20
	s_waitcnt lgkmcnt(2)
	v_pk_add_f32 v[46:47], v[24:25], v[46:47]
	v_pk_add_f32 v[72:73], v[24:25], v[26:27]
	v_pk_add_f32 v[58:59], v[46:47], v[58:59]
	s_waitcnt lgkmcnt(0)
; template <int CTRL> __device__ __forceinline__ float dppx(float v) { return __int_as_float(__builtin_amdgcn_update_dpp(0, __float_as_int(v), CTRL, 0xf, 0xf, true)); }
; __device__ __forceinline__ unsigned cvt_pk_bf16(float lo, float hi) { unsigned r; asm volatile("v_cvt_pk_bf16_f32 %0, %1, %2" : "=v"(r) : "v"(lo), "v"(hi)); return r; }
; __device__ __forceinline__ float log_forget(float z, float lb) {
;   const float r0 = fminf(z, 0.f) - __logf(1.f + __expf(-fabsf(z)));
;   const float r1 = __logf(lb + (1.f - lb) / (1.f + __expf(-z)));
;   return lb <= 0.f ? r0 : r1;
; }
;   __device__ __forceinline__ void operator()(const f32x4 (&acc)[2][2][4][2], const pg8::Unit& u, int wr, int wc, int fr, int fq) const {
;     ...
;               for (int q = 0; q < 4; ++q) { const float gv = log_forget(acc[ai][bj][m][qh][q], lq[q]); g[m][q] = gv;
;                 float sc = gv; sc += dppx<0x111>(sc); sc += dppx<0x112>(sc); sc += dppx<0x114>(sc); sc += dppx<0x118>(sc);
;                 const float tot16 = __int_as_float(__builtin_amdgcn_ds_swizzle(__float_as_int(sc), 0x1F0));
;                 cs[m][q] = sc + carry[q]; carry[q] += tot16; }
; #pragma unroll
;             for (int m = 0; m < 4; ++m) { const int r = row0 + ai * 128 + m * 16; float bq[4], kq[4];
; #pragma unroll
;               for (int q = 0; q < 4; ++q) { bq[q] = bwd ? (carry[q] - cs[m][q]) + g[m][q] : cs[m][q]; kq[q] = 1.f - __expf(g[m][q]); }
;               *(f32x4*)(logfp + (size_t)r * 1024 + c + 4 * qh) = (f32x4){bq[0], bq[1], bq[2], bq[3]};
;               u32x2 w; w.x = pg8::cvt_pk_bf16(kq[0], kq[1]); w.y = pg8::cvt_pk_bf16(kq[2], kq[3]);
;               *(u32x2*)(km + (size_t)r * 1024 + c + 4 * qh) = w; } } }
	v_pk_add_f32 v[46:47], v[46:47], v[68:69]
	v_pk_add_f32 v[68:69], v[62:63], v[34:35] neg_lo:[0,1] neg_hi:[0,1]
	v_pk_add_f32 v[70:71], v[46:47], v[36:37] neg_lo:[0,1] neg_hi:[0,1]
	v_mul_f32_e32 v24, 0x3fb8aa3b, v44
	v_pk_add_f32 v[32:33], v[32:33], v[68:69]
	v_pk_add_f32 v[28:29], v[28:29], v[70:71]
	v_lshl_add_u64 v[16:17], v[86:87], 0, v[48:49]
	v_sub_f32_e32 v86, 1.0, v20
	v_mul_f32_e32 v20, 0x3fb8aa3b, v41
	v_exp_f32_e32 v24, v24
	v_cndmask_b32_e64 v37, v37, v29, s[42:43]
	v_cndmask_b32_e64 v36, v36, v28, s[42:43]
	v_cndmask_b32_e64 v35, v35, v33, s[42:43]
	v_cndmask_b32_e64 v34, v34, v32, s[42:43]
	v_exp_f32_e32 v20, v20
	global_store_dwordx4 v[18:19], v[34:37], off
	v_cvt_pk_bf16_f32 v28, v80, v81
	v_cvt_pk_bf16_f32 v29, v82, v83
	global_store_dwordx2 v[16:17], v[28:29], off
	v_pk_add_f32 v[28:29], v[62:63], v[38:39] neg_lo:[0,1] neg_hi:[0,1]
	v_pk_add_f32 v[32:33], v[46:47], v[60:61] neg_lo:[0,1] neg_hi:[0,1]
	v_pk_add_f32 v[28:29], v[30:31], v[28:29]
	v_pk_add_f32 v[30:31], v[40:41], v[32:33]
	v_sub_f32_e32 v78, 1.0, v24
	v_mul_f32_e32 v24, 0x3fb8aa3b, v45
	v_cndmask_b32_e64 v31, v61, v31, s[42:43]
	v_cndmask_b32_e64 v30, v60, v30, s[42:43]
	v_cndmask_b32_e64 v29, v39, v29, s[42:43]
	v_cndmask_b32_e64 v28, v38, v28, s[42:43]
	v_sub_f32_e32 v87, 1.0, v20
	v_lshl_add_u64 v[20:21], v[90:91], 0, v[48:49]
	v_exp_f32_e32 v24, v24
	global_store_dwordx4 v[22:23], v[28:31], off
	v_lshl_add_u64 v[26:27], v[92:93], 0, v[50:51]
	v_sub_f32_e32 v79, 1.0, v24
	v_cvt_pk_bf16_f32 v28, v84, v85
	v_cvt_pk_bf16_f32 v29, v86, v87
	global_store_dwordx2 v[20:21], v[28:29], off
	v_pk_add_f32 v[28:29], v[62:63], v[74:75] neg_lo:[0,1] neg_hi:[0,1]
	v_pk_add_f32 v[30:31], v[46:47], v[72:73] neg_lo:[0,1] neg_hi:[0,1]
	v_pk_add_f32 v[28:29], v[42:43], v[28:29]
	v_pk_add_f32 v[30:31], v[44:45], v[30:31]
	v_cndmask_b32_e64 v29, v75, v29, s[42:43]
	v_cndmask_b32_e64 v31, v73, v31, s[42:43]
	v_cndmask_b32_e64 v30, v72, v30, s[42:43]
	v_cndmask_b32_e64 v28, v74, v28, s[42:43]
	v_lshl_add_u64 v[24:25], v[94:95], 0, v[48:49]
	global_store_dwordx4 v[26:27], v[28:31], off
	s_nop 1
	v_cvt_pk_bf16_f32 v28, v76, v77
	v_cvt_pk_bf16_f32 v29, v78, v79
	global_store_dwordx2 v[24:25], v[28:29], off
	v_mul_f32_e32 v28, 0x3fb8aa3b, v56
	v_exp_f32_e32 v28, v28
	v_pk_add_f32 v[30:31], v[46:47], v[58:59] neg_lo:[0,1] neg_hi:[0,1]
	v_sub_f32_e32 v34, 1.0, v28
	v_pk_add_f32 v[28:29], v[62:63], v[54:55] neg_lo:[0,1] neg_hi:[0,1]
	v_pk_add_f32 v[30:31], v[56:57], v[30:31]
	v_pk_add_f32 v[28:29], v[52:53], v[28:29]
	v_cndmask_b32_e64 v32, v58, v30, s[42:43]
	v_cndmask_b32_e64 v30, v54, v28, s[42:43]
	v_mul_f32_e32 v28, 0x3fb8aa3b, v57
	v_exp_f32_e32 v28, v28
	v_cndmask_b32_e64 v33, v59, v31, s[42:43]
	v_cndmask_b32_e64 v31, v55, v29, s[42:43]
	v_sub_f32_e32 v35, 1.0, v28
	v_lshl_add_u64 v[28:29], v[98:99], 0, v[50:51]
	global_store_dwordx4 v[28:29], v[30:33], off
	s_nop 1
	v_cvt_pk_bf16_f32 v32, v88, v89
	v_cvt_pk_bf16_f32 v33, v34, v35
	v_lshl_add_u64 v[30:31], v[100:101], 0, v[48:49]
	global_store_dwordx2 v[30:31], v[32:33], off
	v_mul_f32_e64 v33, |v12|, s8
	v_exp_f32_e32 v33, v33
	v_max_f32_e32 v32, v12, v12
	v_mul_f32_e32 v12, 0xbfb8aa3b, v12
	v_exp_f32_e32 v12, v12
	v_add_f32_e32 v33, 1.0, v33
	v_cmp_gt_f32_e32 vcc, s37, v33
	v_min_f32_e32 v32, 0, v32
	v_add_f32_e32 v12, 1.0, v12
	v_cndmask_b32_e64 v34, 0, 32, vcc
	v_ldexp_f32 v33, v33, v34
	v_log_f32_e32 v33, v33
	s_nop 0
	v_mul_f32_e32 v34, 0x3f317217, v33
	v_fma_f32 v34, v33, s33, -v34
	v_fmac_f32_e32 v34, 0x3377d1cf, v33
	v_fmac_f32_e32 v34, 0x3f317217, v33
	v_cmp_lt_f32_e64 s[44:45], |v33|, s36
	s_nop 1
	v_cndmask_b32_e64 v33, v33, v34, s[44:45]
	v_cndmask_b32_e32 v34, 0, v216, vcc
	v_sub_f32_e32 v34, v33, v34
	v_div_scale_f32 v33, s[2:3], v12, v12, v114
	v_rcp_f32_e32 v35, v33
	s_nop 0
	v_fma_f32 v36, -v33, v35, 1.0
	v_fmac_f32_e32 v35, v36, v35
	v_div_scale_f32 v36, vcc, v114, v12, v114
	v_mul_f32_e32 v37, v36, v35
	v_fma_f32 v38, -v33, v37, v36
	v_fmac_f32_e32 v37, v38, v35
	v_fma_f32 v33, -v33, v37, v36
	v_div_fmas_f32 v33, v33, v35, v37
	v_div_fixup_f32 v12, v33, v12, v114
	v_add_f32_e32 v12, v64, v12
	v_cmp_gt_f32_e32 vcc, s37, v12
	s_nop 1
	v_cndmask_b32_e64 v33, 0, 32, vcc
	v_ldexp_f32 v12, v12, v33
	v_log_f32_e32 v12, v12
	s_nop 0
	v_mul_f32_e32 v33, 0x3f317217, v12
	v_fma_f32 v33, v12, s33, -v33
	v_fmac_f32_e32 v33, 0x3377d1cf, v12
	v_fmac_f32_e32 v33, 0x3f317217, v12
	v_cmp_lt_f32_e64 s[44:45], |v12|, s36
	s_nop 1
	v_cndmask_b32_e64 v12, v12, v33, s[44:45]
	v_cndmask_b32_e32 v33, 0, v216, vcc
	v_sub_f32_e32 v50, v12, v33
	v_max_f32_e32 v12, v13, v13
	v_min_f32_e32 v33, 0, v12
	v_mul_f32_e64 v12, |v13|, s8
	v_exp_f32_e32 v12, v12
	s_nop 0
	v_add_f32_e32 v12, 1.0, v12
	v_cmp_gt_f32_e32 vcc, s37, v12
	s_nop 1
	v_cndmask_b32_e64 v35, 0, 32, vcc
	v_ldexp_f32 v12, v12, v35
	v_log_f32_e32 v12, v12
	s_nop 0
	v_mul_f32_e32 v35, 0x3f317217, v12
	v_fma_f32 v35, v12, s33, -v35
	v_fmac_f32_e32 v35, 0x3377d1cf, v12
	v_fmac_f32_e32 v35, 0x3f317217, v12
	v_cmp_lt_f32_e64 s[44:45], |v12|, s36
	s_nop 1
	v_cndmask_b32_e64 v12, v12, v35, s[44:45]
	v_cndmask_b32_e32 v35, 0, v216, vcc
	v_sub_f32_e32 v35, v12, v35
	v_mul_f32_e32 v12, 0xbfb8aa3b, v13
	v_exp_f32_e32 v12, v12
	s_nop 0
	v_add_f32_e32 v12, 1.0, v12
	v_div_scale_f32 v13, s[2:3], v12, v12, v113
	v_rcp_f32_e32 v36, v13
	s_nop 0
	v_fma_f32 v37, -v13, v36, 1.0
	v_fmac_f32_e32 v36, v37, v36
	v_div_scale_f32 v37, vcc, v113, v12, v113
	v_mul_f32_e32 v38, v37, v36
	v_fma_f32 v39, -v13, v38, v37
	v_fmac_f32_e32 v38, v39, v36
	v_fma_f32 v13, -v13, v38, v37
	v_div_fmas_f32 v13, v13, v36, v38
	v_div_fixup_f32 v12, v13, v12, v113
	v_add_f32_e32 v12, v65, v12
	v_cmp_gt_f32_e32 vcc, s37, v12
; __device__ __forceinline__ float log_forget(float z, float lb) {
;   const float r0 = fminf(z, 0.f) - __logf(1.f + __expf(-fabsf(z)));
;   const float r1 = __logf(lb + (1.f - lb) / (1.f + __expf(-z)));
;   return lb <= 0.f ? r0 : r1;
; }
	s_nop 1
	v_cndmask_b32_e64 v13, 0, 32, vcc
	v_ldexp_f32 v12, v12, v13
	v_log_f32_e32 v12, v12
	s_nop 0
	v_mul_f32_e32 v13, 0x3f317217, v12
	v_fma_f32 v13, v12, s33, -v13
	v_fmac_f32_e32 v13, 0x3377d1cf, v12
	v_fmac_f32_e32 v13, 0x3f317217, v12
	v_cmp_lt_f32_e64 s[44:45], |v12|, s36
	s_nop 1
	v_cndmask_b32_e64 v12, v12, v13, s[44:45]
	v_cndmask_b32_e32 v13, 0, v216, vcc
	v_sub_f32_e32 v51, v12, v13
	v_mul_f32_e64 v13, |v14|, s8
	v_exp_f32_e32 v13, v13
	v_max_f32_e32 v12, v14, v14
	v_min_f32_e32 v12, 0, v12
	v_add_f32_e32 v13, 1.0, v13
	v_cmp_gt_f32_e32 vcc, s37, v13
	s_nop 1
	v_cndmask_b32_e64 v36, 0, 32, vcc
	v_ldexp_f32 v13, v13, v36
	v_log_f32_e32 v13, v13
	s_nop 0
	v_mul_f32_e32 v36, 0x3f317217, v13
	v_fma_f32 v36, v13, s33, -v36
	v_fmac_f32_e32 v36, 0x3377d1cf, v13
	v_fmac_f32_e32 v36, 0x3f317217, v13
	v_cmp_lt_f32_e64 s[44:45], |v13|, s36
	s_nop 1
	v_cndmask_b32_e64 v13, v13, v36, s[44:45]
	v_cndmask_b32_e32 v36, 0, v216, vcc
	v_sub_f32_e32 v36, v13, v36
	v_mul_f32_e32 v13, 0xbfb8aa3b, v14
	v_exp_f32_e32 v13, v13
	s_nop 0
	v_add_f32_e32 v13, 1.0, v13
	v_div_scale_f32 v14, s[2:3], v13, v13, v112
	v_rcp_f32_e32 v37, v14
	s_nop 0
	v_fma_f32 v38, -v14, v37, 1.0
	v_fmac_f32_e32 v37, v38, v37
	v_div_scale_f32 v38, vcc, v112, v13, v112
	v_mul_f32_e32 v39, v38, v37
	v_fma_f32 v40, -v14, v39, v38
	v_fmac_f32_e32 v39, v40, v37
	v_fma_f32 v14, -v14, v39, v38
	v_div_fmas_f32 v14, v14, v37, v39
	v_div_fixup_f32 v13, v14, v13, v112
	v_add_f32_e32 v13, v66, v13
	v_cmp_gt_f32_e32 vcc, s37, v13
	s_nop 1
	v_cndmask_b32_e64 v14, 0, 32, vcc
	v_ldexp_f32 v13, v13, v14
	v_log_f32_e32 v13, v13
	s_nop 0
	v_mul_f32_e32 v14, 0x3f317217, v13
	v_fma_f32 v14, v13, s33, -v14
	v_fmac_f32_e32 v14, 0x3377d1cf, v13
	v_fmac_f32_e32 v14, 0x3f317217, v13
	v_cmp_lt_f32_e64 s[44:45], |v13|, s36
	s_nop 1
	v_cndmask_b32_e64 v13, v13, v14, s[44:45]
	v_cndmask_b32_e32 v14, 0, v216, vcc
	v_sub_f32_e32 v52, v13, v14
	v_mul_f32_e64 v14, |v15|, s8
	v_exp_f32_e32 v14, v14
	v_max_f32_e32 v13, v15, v15
	v_min_f32_e32 v13, 0, v13
	v_add_f32_e32 v14, 1.0, v14
	v_cmp_gt_f32_e32 vcc, s37, v14
	s_nop 1
	v_cndmask_b32_e64 v37, 0, 32, vcc
	v_ldexp_f32 v14, v14, v37
	v_log_f32_e32 v14, v14
	s_nop 0
	v_mul_f32_e32 v37, 0x3f317217, v14
	v_fma_f32 v37, v14, s33, -v37
	v_fmac_f32_e32 v37, 0x3377d1cf, v14
	v_fmac_f32_e32 v37, 0x3f317217, v14
	v_cmp_lt_f32_e64 s[44:45], |v14|, s36
	s_nop 1
	v_cndmask_b32_e64 v14, v14, v37, s[44:45]
	v_cndmask_b32_e32 v37, 0, v216, vcc
	v_sub_f32_e32 v37, v14, v37
	v_mul_f32_e32 v14, 0xbfb8aa3b, v15
	v_exp_f32_e32 v14, v14
	v_pk_add_f32 v[12:13], v[12:13], v[36:37] neg_lo:[0,1] neg_hi:[0,1]
	v_add_f32_e32 v14, 1.0, v14
	v_div_scale_f32 v15, s[2:3], v14, v14, v96
	v_rcp_f32_e32 v38, v15
	v_cndmask_b32_e64 v12, v52, v12, s[56:57]
	v_fma_f32 v39, -v15, v38, 1.0
	v_fmac_f32_e32 v38, v39, v38
	v_div_scale_f32 v39, vcc, v96, v14, v96
	v_mul_f32_e32 v40, v39, v38
	v_fma_f32 v41, -v15, v40, v39
	v_fmac_f32_e32 v40, v41, v38
	v_fma_f32 v15, -v15, v40, v39
	v_div_fmas_f32 v15, v15, v38, v40
	v_div_fixup_f32 v14, v15, v14, v96
	v_add_f32_e32 v14, v67, v14
	v_cmp_gt_f32_e32 vcc, s37, v14
	s_nop 1
	v_cndmask_b32_e64 v15, 0, 32, vcc
	v_ldexp_f32 v14, v14, v15
	v_log_f32_e32 v14, v14
	s_nop 0
	v_mul_f32_e32 v15, 0x3f317217, v14
	v_fma_f32 v15, v14, s33, -v15
	v_fmac_f32_e32 v15, 0x3377d1cf, v14
	v_fmac_f32_e32 v15, 0x3f317217, v14
	v_cmp_lt_f32_e64 s[44:45], |v14|, s36
	s_nop 1
	v_cndmask_b32_e64 v14, v14, v15, s[44:45]
	v_cndmask_b32_e32 v15, 0, v216, vcc
	v_sub_f32_e32 v53, v14, v15
	v_mul_f32_e64 v15, |v8|, s8
	v_exp_f32_e32 v15, v15
	v_max_f32_e32 v14, v8, v8
	v_mul_f32_e32 v8, 0xbfb8aa3b, v8
	v_exp_f32_e32 v8, v8
	v_add_f32_e32 v15, 1.0, v15
	v_cmp_gt_f32_e32 vcc, s37, v15
	v_cndmask_b32_e64 v13, v53, v13, s[58:59]
	v_add_f32_e32 v8, 1.0, v8
	v_cndmask_b32_e64 v38, 0, 32, vcc
	v_ldexp_f32 v15, v15, v38
	v_log_f32_e32 v15, v15
	v_min_f32_e32 v14, 0, v14
	v_mul_f32_e32 v38, 0x3f317217, v15
	v_fma_f32 v38, v15, s33, -v38
	v_fmac_f32_e32 v38, 0x3377d1cf, v15
	v_fmac_f32_e32 v38, 0x3f317217, v15
	v_cmp_lt_f32_e64 s[44:45], |v15|, s36
	s_nop 1
	v_cndmask_b32_e64 v15, v15, v38, s[44:45]
	v_cndmask_b32_e32 v38, 0, v216, vcc
	v_sub_f32_e32 v38, v15, v38
	v_div_scale_f32 v15, s[2:3], v8, v8, v114
	v_rcp_f32_e32 v39, v15
	s_nop 0
	v_fma_f32 v40, -v15, v39, 1.0
	v_fmac_f32_e32 v39, v40, v39
	v_div_scale_f32 v40, vcc, v114, v8, v114
	v_mul_f32_e32 v41, v40, v39
	v_fma_f32 v42, -v15, v41, v40
	v_fmac_f32_e32 v41, v42, v39
	v_fma_f32 v15, -v15, v41, v40
	v_div_fmas_f32 v15, v15, v39, v41
	v_div_fixup_f32 v8, v15, v8, v114
	v_add_f32_e32 v8, v64, v8
	v_cmp_gt_f32_e32 vcc, s37, v8
	s_nop 1
	v_cndmask_b32_e64 v15, 0, 32, vcc
	v_ldexp_f32 v8, v8, v15
	v_log_f32_e32 v8, v8
	s_nop 0
	v_mul_f32_e32 v15, 0x3f317217, v8
	v_fma_f32 v15, v8, s33, -v15
	v_fmac_f32_e32 v15, 0x3377d1cf, v8
	v_fmac_f32_e32 v15, 0x3f317217, v8
	v_cmp_lt_f32_e64 s[44:45], |v8|, s36
	s_nop 1
	v_cndmask_b32_e64 v8, v8, v15, s[44:45]
	v_cndmask_b32_e32 v15, 0, v216, vcc
	v_sub_f32_e32 v54, v8, v15
	v_max_f32_e32 v8, v9, v9
	v_min_f32_e32 v15, 0, v8
	v_mul_f32_e64 v8, |v9|, s8
	v_exp_f32_e32 v8, v8
	s_nop 0
	v_add_f32_e32 v8, 1.0, v8
	v_cmp_gt_f32_e32 vcc, s37, v8
	s_nop 1
	v_cndmask_b32_e64 v39, 0, 32, vcc
	v_ldexp_f32 v8, v8, v39
	v_log_f32_e32 v8, v8
	s_nop 0
	v_mul_f32_e32 v39, 0x3f317217, v8
	v_fma_f32 v39, v8, s33, -v39
	v_fmac_f32_e32 v39, 0x3377d1cf, v8
	v_fmac_f32_e32 v39, 0x3f317217, v8
	v_cmp_lt_f32_e64 s[44:45], |v8|, s36
	s_nop 1
	v_cndmask_b32_e64 v8, v8, v39, s[44:45]
	v_cndmask_b32_e32 v39, 0, v216, vcc
	v_sub_f32_e32 v39, v8, v39
	v_mul_f32_e32 v8, 0xbfb8aa3b, v9
	v_exp_f32_e32 v8, v8
; __device__ __forceinline__ float log_forget(float z, float lb) {
;   const float r0 = fminf(z, 0.f) - __logf(1.f + __expf(-fabsf(z)));
;   const float r1 = __logf(lb + (1.f - lb) / (1.f + __expf(-z)));
;   return lb <= 0.f ? r0 : r1;
; }
	v_pk_add_f32 v[14:15], v[14:15], v[38:39] neg_lo:[0,1] neg_hi:[0,1]
	v_add_f32_e32 v8, 1.0, v8
	v_div_scale_f32 v9, s[2:3], v8, v8, v113
	v_rcp_f32_e32 v40, v9
	v_cndmask_b32_e64 v14, v54, v14, s[48:49]
	v_fma_f32 v41, -v9, v40, 1.0
	v_fmac_f32_e32 v40, v41, v40
	v_div_scale_f32 v41, vcc, v113, v8, v113
	v_mul_f32_e32 v42, v41, v40
	v_fma_f32 v43, -v9, v42, v41
	v_fmac_f32_e32 v42, v43, v40
	v_fma_f32 v9, -v9, v42, v41
	v_div_fmas_f32 v9, v9, v40, v42
	v_div_fixup_f32 v8, v9, v8, v113
	v_add_f32_e32 v8, v65, v8
	v_cmp_gt_f32_e32 vcc, s37, v8
	s_nop 1
	v_cndmask_b32_e64 v9, 0, 32, vcc
	v_ldexp_f32 v8, v8, v9
	v_log_f32_e32 v8, v8
	s_nop 0
	v_mul_f32_e32 v9, 0x3f317217, v8
	v_fma_f32 v9, v8, s33, -v9
	v_fmac_f32_e32 v9, 0x3377d1cf, v8
	v_fmac_f32_e32 v9, 0x3f317217, v8
	v_cmp_lt_f32_e64 s[44:45], |v8|, s36
	s_nop 1
	v_cndmask_b32_e64 v8, v8, v9, s[44:45]
	v_cndmask_b32_e32 v9, 0, v216, vcc
	v_sub_f32_e32 v55, v8, v9
	v_mul_f32_e64 v9, |v10|, s8
	v_exp_f32_e32 v9, v9
	v_max_f32_e32 v8, v10, v10
	v_cndmask_b32_e64 v15, v55, v15, s[52:53]
	v_min_f32_e32 v8, 0, v8
	v_add_f32_e32 v9, 1.0, v9
	v_cmp_gt_f32_e32 vcc, s37, v9
	s_nop 1
	v_cndmask_b32_e64 v40, 0, 32, vcc
	v_ldexp_f32 v9, v9, v40
	v_log_f32_e32 v9, v9
	s_nop 0
	v_mul_f32_e32 v40, 0x3f317217, v9
	v_fma_f32 v40, v9, s33, -v40
	v_fmac_f32_e32 v40, 0x3377d1cf, v9
	v_fmac_f32_e32 v40, 0x3f317217, v9
	v_cmp_lt_f32_e64 s[44:45], |v9|, s36
	s_nop 1
	v_cndmask_b32_e64 v9, v9, v40, s[44:45]
	v_cndmask_b32_e32 v40, 0, v216, vcc
	v_sub_f32_e32 v40, v9, v40
	v_mul_f32_e32 v9, 0xbfb8aa3b, v10
	v_exp_f32_e32 v9, v9
	s_nop 0
	v_add_f32_e32 v9, 1.0, v9
	v_div_scale_f32 v10, s[2:3], v9, v9, v112
	v_rcp_f32_e32 v41, v10
	s_nop 0
	v_fma_f32 v42, -v10, v41, 1.0
	v_fmac_f32_e32 v41, v42, v41
	v_div_scale_f32 v42, vcc, v112, v9, v112
	v_mul_f32_e32 v43, v42, v41
	v_fma_f32 v44, -v10, v43, v42
	v_fmac_f32_e32 v43, v44, v41
	v_fma_f32 v10, -v10, v43, v42
	v_div_fmas_f32 v10, v10, v41, v43
	v_div_fixup_f32 v9, v10, v9, v112
	v_add_f32_e32 v9, v66, v9
	v_cmp_gt_f32_e32 vcc, s37, v9
	s_nop 1
	v_cndmask_b32_e64 v10, 0, 32, vcc
	v_ldexp_f32 v9, v9, v10
	v_log_f32_e32 v9, v9
	s_nop 0
	v_mul_f32_e32 v10, 0x3f317217, v9
	v_fma_f32 v10, v9, s33, -v10
	v_fmac_f32_e32 v10, 0x3377d1cf, v9
	v_fmac_f32_e32 v10, 0x3f317217, v9
	v_cmp_lt_f32_e64 s[44:45], |v9|, s36
	s_nop 1
	v_cndmask_b32_e64 v9, v9, v10, s[44:45]
	v_cndmask_b32_e32 v10, 0, v216, vcc
	v_sub_f32_e32 v56, v9, v10
	v_mul_f32_e64 v10, |v11|, s8
	v_exp_f32_e32 v10, v10
	v_max_f32_e32 v9, v11, v11
	v_min_f32_e32 v9, 0, v9
	v_add_f32_e32 v10, 1.0, v10
	v_cmp_gt_f32_e32 vcc, s37, v10
	s_nop 1
	v_cndmask_b32_e64 v41, 0, 32, vcc
	v_ldexp_f32 v10, v10, v41
	v_log_f32_e32 v10, v10
	s_nop 0
	v_mul_f32_e32 v41, 0x3f317217, v10
	v_fma_f32 v41, v10, s33, -v41
	v_fmac_f32_e32 v41, 0x3377d1cf, v10
	v_fmac_f32_e32 v41, 0x3f317217, v10
	v_cmp_lt_f32_e64 s[44:45], |v10|, s36
	s_nop 1
	v_cndmask_b32_e64 v10, v10, v41, s[44:45]
	v_cndmask_b32_e32 v41, 0, v216, vcc
	v_sub_f32_e32 v41, v10, v41
	v_mul_f32_e32 v10, 0xbfb8aa3b, v11
	v_exp_f32_e32 v10, v10
	v_pk_add_f32 v[8:9], v[8:9], v[40:41] neg_lo:[0,1] neg_hi:[0,1]
	v_add_f32_e32 v10, 1.0, v10
	v_div_scale_f32 v11, s[2:3], v10, v10, v96
	v_rcp_f32_e32 v42, v11
	v_cndmask_b32_e64 v8, v56, v8, s[56:57]
	v_fma_f32 v43, -v11, v42, 1.0
	v_fmac_f32_e32 v42, v43, v42
	v_div_scale_f32 v43, vcc, v96, v10, v96
	v_mul_f32_e32 v44, v43, v42
	v_fma_f32 v45, -v11, v44, v43
	v_fmac_f32_e32 v44, v45, v42
	v_fma_f32 v11, -v11, v44, v43
	v_div_fmas_f32 v11, v11, v42, v44
	v_div_fixup_f32 v10, v11, v10, v96
	v_add_f32_e32 v10, v67, v10
	v_cmp_gt_f32_e32 vcc, s37, v10
	s_nop 1
	v_cndmask_b32_e64 v11, 0, 32, vcc
	v_ldexp_f32 v10, v10, v11
	v_log_f32_e32 v10, v10
	s_nop 0
	v_mul_f32_e32 v11, 0x3f317217, v10
	v_fma_f32 v11, v10, s33, -v11
	v_fmac_f32_e32 v11, 0x3377d1cf, v10
	v_fmac_f32_e32 v11, 0x3f317217, v10
	v_cmp_lt_f32_e64 s[44:45], |v10|, s36
	s_nop 1
	v_cndmask_b32_e64 v10, v10, v11, s[44:45]
	v_cndmask_b32_e32 v11, 0, v216, vcc
	v_sub_f32_e32 v57, v10, v11
	v_mul_f32_e64 v11, |v4|, s8
	v_exp_f32_e32 v11, v11
	v_max_f32_e32 v10, v4, v4
	v_mul_f32_e32 v4, 0xbfb8aa3b, v4
	v_exp_f32_e32 v4, v4
	v_add_f32_e32 v11, 1.0, v11
	v_cmp_gt_f32_e32 vcc, s37, v11
	v_cndmask_b32_e64 v9, v57, v9, s[58:59]
	v_add_f32_e32 v4, 1.0, v4
	v_cndmask_b32_e64 v42, 0, 32, vcc
	v_ldexp_f32 v11, v11, v42
	v_log_f32_e32 v11, v11
	v_min_f32_e32 v10, 0, v10
	v_mul_f32_e32 v42, 0x3f317217, v11
	v_fma_f32 v42, v11, s33, -v42
	v_fmac_f32_e32 v42, 0x3377d1cf, v11
	v_fmac_f32_e32 v42, 0x3f317217, v11
	v_cmp_lt_f32_e64 s[44:45], |v11|, s36
	s_nop 1
	v_cndmask_b32_e64 v11, v11, v42, s[44:45]
	v_cndmask_b32_e32 v42, 0, v216, vcc
	v_sub_f32_e32 v42, v11, v42
	v_div_scale_f32 v11, s[2:3], v4, v4, v114
	v_rcp_f32_e32 v43, v11
	s_nop 0
	v_fma_f32 v44, -v11, v43, 1.0
	v_fmac_f32_e32 v43, v44, v43
	v_div_scale_f32 v44, vcc, v114, v4, v114
	v_mul_f32_e32 v45, v44, v43
	v_fma_f32 v46, -v11, v45, v44
	v_fmac_f32_e32 v45, v46, v43
	v_fma_f32 v11, -v11, v45, v44
	v_div_fmas_f32 v11, v11, v43, v45
	v_div_fixup_f32 v4, v11, v4, v114
	v_add_f32_e32 v4, v64, v4
	v_cmp_gt_f32_e32 vcc, s37, v4
	s_nop 1
	v_cndmask_b32_e64 v11, 0, 32, vcc
	v_ldexp_f32 v4, v4, v11
	v_log_f32_e32 v4, v4
	s_nop 0
	v_mul_f32_e32 v11, 0x3f317217, v4
	v_fma_f32 v11, v4, s33, -v11
	v_fmac_f32_e32 v11, 0x3377d1cf, v4
	v_fmac_f32_e32 v11, 0x3f317217, v4
	v_cmp_lt_f32_e64 s[44:45], |v4|, s36
	s_nop 1
	v_cndmask_b32_e64 v4, v4, v11, s[44:45]
	v_cndmask_b32_e32 v11, 0, v216, vcc
	v_sub_f32_e32 v58, v4, v11
	v_max_f32_e32 v4, v5, v5
	v_min_f32_e32 v11, 0, v4
	v_mul_f32_e64 v4, |v5|, s8
	v_exp_f32_e32 v4, v4
	s_nop 0
; template <int CTRL> __device__ __forceinline__ float dppx(float v) { return __int_as_float(__builtin_amdgcn_update_dpp(0, __float_as_int(v), CTRL, 0xf, 0xf, true)); }
; __device__ __forceinline__ float log_forget(float z, float lb) {
;   const float r0 = fminf(z, 0.f) - __logf(1.f + __expf(-fabsf(z)));
;   const float r1 = __logf(lb + (1.f - lb) / (1.f + __expf(-z)));
;   return lb <= 0.f ? r0 : r1;
; }
;   __device__ __forceinline__ void operator()(const f32x4 (&acc)[2][2][4][2], const pg8::Unit& u, int wr, int wc, int fr, int fq) const {
;     ...
;               for (int q = 0; q < 4; ++q) { const float gv = log_forget(acc[ai][bj][m][qh][q], lq[q]); g[m][q] = gv;
;                 float sc = gv; sc += dppx<0x111>(sc); sc += dppx<0x112>(sc); sc += dppx<0x114>(sc); sc += dppx<0x118>(sc);
	v_add_f32_e32 v4, 1.0, v4
	v_cmp_gt_f32_e32 vcc, s37, v4
	s_nop 1
	v_cndmask_b32_e64 v43, 0, 32, vcc
	v_ldexp_f32 v4, v4, v43
	v_log_f32_e32 v4, v4
	s_nop 0
	v_mul_f32_e32 v43, 0x3f317217, v4
	v_fma_f32 v43, v4, s33, -v43
	v_fmac_f32_e32 v43, 0x3377d1cf, v4
	v_fmac_f32_e32 v43, 0x3f317217, v4
	v_cmp_lt_f32_e64 s[44:45], |v4|, s36
	s_nop 1
	v_cndmask_b32_e64 v4, v4, v43, s[44:45]
	v_cndmask_b32_e32 v43, 0, v216, vcc
	v_sub_f32_e32 v43, v4, v43
	v_mul_f32_e32 v4, 0xbfb8aa3b, v5
	v_exp_f32_e32 v4, v4
	v_pk_add_f32 v[10:11], v[10:11], v[42:43] neg_lo:[0,1] neg_hi:[0,1]
	v_add_f32_e32 v4, 1.0, v4
	v_div_scale_f32 v5, s[2:3], v4, v4, v113
	v_rcp_f32_e32 v44, v5
	v_cndmask_b32_e64 v10, v58, v10, s[48:49]
	v_fma_f32 v45, -v5, v44, 1.0
	v_fmac_f32_e32 v44, v45, v44
	v_div_scale_f32 v45, vcc, v113, v4, v113
	v_mul_f32_e32 v46, v45, v44
	v_fma_f32 v47, -v5, v46, v45
	v_fmac_f32_e32 v46, v47, v44
	v_fma_f32 v5, -v5, v46, v45
	v_div_fmas_f32 v5, v5, v44, v46
	v_div_fixup_f32 v4, v5, v4, v113
	v_add_f32_e32 v4, v65, v4
	v_cmp_gt_f32_e32 vcc, s37, v4
	v_mov_b32_dpp v42, v10 row_shr:1 row_mask:0xf bank_mask:0xf bound_ctrl:1
	s_nop 0
	v_cndmask_b32_e64 v5, 0, 32, vcc
	v_ldexp_f32 v4, v4, v5
	v_log_f32_e32 v4, v4
	s_nop 0
	v_mul_f32_e32 v5, 0x3f317217, v4
	v_fma_f32 v5, v4, s33, -v5
	v_fmac_f32_e32 v5, 0x3377d1cf, v4
	v_fmac_f32_e32 v5, 0x3f317217, v4
	v_cmp_lt_f32_e64 s[44:45], |v4|, s36
	s_nop 1
	v_cndmask_b32_e64 v4, v4, v5, s[44:45]
	v_cndmask_b32_e32 v5, 0, v216, vcc
	v_sub_f32_e32 v59, v4, v5
	v_mul_f32_e64 v5, |v6|, s8
	v_exp_f32_e32 v5, v5
	v_max_f32_e32 v4, v6, v6
	v_cndmask_b32_e64 v11, v59, v11, s[52:53]
	v_min_f32_e32 v4, 0, v4
	v_add_f32_e32 v5, 1.0, v5
	v_cmp_gt_f32_e32 vcc, s37, v5
	v_mov_b32_dpp v43, v11 row_shr:1 row_mask:0xf bank_mask:0xf bound_ctrl:1
	v_pk_add_f32 v[42:43], v[10:11], v[42:43]
	v_cndmask_b32_e64 v44, 0, 32, vcc
	v_ldexp_f32 v5, v5, v44
	v_log_f32_e32 v5, v5
	s_nop 0
	v_mul_f32_e32 v44, 0x3f317217, v5
	v_fma_f32 v44, v5, s33, -v44
	v_fmac_f32_e32 v44, 0x3377d1cf, v5
	v_fmac_f32_e32 v44, 0x3f317217, v5
	v_cmp_lt_f32_e64 s[44:45], |v5|, s36
	s_nop 1
	v_cndmask_b32_e64 v5, v5, v44, s[44:45]
	v_cndmask_b32_e32 v44, 0, v216, vcc
	v_sub_f32_e32 v44, v5, v44
	v_mul_f32_e32 v5, 0xbfb8aa3b, v6
	v_exp_f32_e32 v5, v5
	s_nop 0
	v_add_f32_e32 v5, 1.0, v5
	v_div_scale_f32 v6, s[2:3], v5, v5, v112
	v_rcp_f32_e32 v45, v6
	s_nop 0
	v_fma_f32 v46, -v6, v45, 1.0
	v_fmac_f32_e32 v45, v46, v45
	v_div_scale_f32 v46, vcc, v112, v5, v112
	v_mul_f32_e32 v47, v46, v45
	v_fma_f32 v48, -v6, v47, v46
	v_fmac_f32_e32 v47, v48, v45
	v_fma_f32 v6, -v6, v47, v46
	v_div_fmas_f32 v6, v6, v45, v47
	v_div_fixup_f32 v5, v6, v5, v112
	v_add_f32_e32 v5, v66, v5
	v_cmp_gt_f32_e32 vcc, s37, v5
	s_nop 1
	v_cndmask_b32_e64 v6, 0, 32, vcc
	v_ldexp_f32 v5, v5, v6
	v_log_f32_e32 v5, v5
	s_nop 0
	v_mul_f32_e32 v6, 0x3f317217, v5
	v_fma_f32 v6, v5, s33, -v6
	v_fmac_f32_e32 v6, 0x3377d1cf, v5
	v_fmac_f32_e32 v6, 0x3f317217, v5
	v_cmp_lt_f32_e64 s[44:45], |v5|, s36
	s_nop 1
	v_cndmask_b32_e64 v5, v5, v6, s[44:45]
	v_cndmask_b32_e32 v6, 0, v216, vcc
	v_sub_f32_e32 v60, v5, v6
	v_mul_f32_e64 v6, |v7|, s8
	v_exp_f32_e32 v6, v6
	v_max_f32_e32 v5, v7, v7
	v_min_f32_e32 v5, 0, v5
	v_add_f32_e32 v6, 1.0, v6
	v_cmp_gt_f32_e32 vcc, s37, v6
	s_nop 1
	v_cndmask_b32_e64 v45, 0, 32, vcc
	v_ldexp_f32 v6, v6, v45
	v_log_f32_e32 v6, v6
	s_nop 0
	v_mul_f32_e32 v45, 0x3f317217, v6
	v_fma_f32 v45, v6, s33, -v45
	v_fmac_f32_e32 v45, 0x3377d1cf, v6
	v_fmac_f32_e32 v45, 0x3f317217, v6
	v_cmp_lt_f32_e64 s[44:45], |v6|, s36
	s_nop 1
	v_cndmask_b32_e64 v6, v6, v45, s[44:45]
	v_cndmask_b32_e32 v45, 0, v216, vcc
	v_sub_f32_e32 v45, v6, v45
	v_mul_f32_e32 v6, 0xbfb8aa3b, v7
	v_exp_f32_e32 v6, v6
	v_pk_add_f32 v[4:5], v[4:5], v[44:45] neg_lo:[0,1] neg_hi:[0,1]
	v_add_f32_e32 v6, 1.0, v6
	v_div_scale_f32 v7, s[2:3], v6, v6, v96
	v_rcp_f32_e32 v46, v7
	v_cndmask_b32_e64 v4, v60, v4, s[56:57]
	v_fma_f32 v47, -v7, v46, 1.0
	v_fmac_f32_e32 v46, v47, v46
	v_div_scale_f32 v47, vcc, v96, v6, v96
	v_mul_f32_e32 v48, v47, v46
	v_fma_f32 v49, -v7, v48, v47
	v_fmac_f32_e32 v48, v49, v46
	v_fma_f32 v7, -v7, v48, v47
	v_div_fmas_f32 v7, v7, v46, v48
	v_div_fixup_f32 v6, v7, v6, v96
	v_add_f32_e32 v6, v67, v6
	v_cmp_gt_f32_e32 vcc, s37, v6
	v_mov_b32_dpp v44, v4 row_shr:1 row_mask:0xf bank_mask:0xf bound_ctrl:1
	s_nop 0
	v_cndmask_b32_e64 v7, 0, 32, vcc
	v_ldexp_f32 v6, v6, v7
	v_log_f32_e32 v6, v6
	s_nop 0
	v_mul_f32_e32 v7, 0x3f317217, v6
	v_fma_f32 v7, v6, s33, -v7
	v_fmac_f32_e32 v7, 0x3377d1cf, v6
	v_fmac_f32_e32 v7, 0x3f317217, v6
	v_cmp_lt_f32_e64 s[44:45], |v6|, s36
	s_nop 1
	v_cndmask_b32_e64 v6, v6, v7, s[44:45]
	v_cndmask_b32_e32 v7, 0, v216, vcc
	v_sub_f32_e32 v61, v6, v7
	v_mul_f32_e64 v7, |v0|, s8
	v_exp_f32_e32 v7, v7
	v_max_f32_e32 v6, v0, v0
	v_mul_f32_e32 v0, 0xbfb8aa3b, v0
	v_exp_f32_e32 v0, v0
	v_add_f32_e32 v7, 1.0, v7
	v_cmp_gt_f32_e32 vcc, s37, v7
	v_cndmask_b32_e64 v5, v61, v5, s[58:59]
	v_add_f32_e32 v0, 1.0, v0
	v_cndmask_b32_e64 v46, 0, 32, vcc
	v_ldexp_f32 v7, v7, v46
	v_log_f32_e32 v7, v7
	v_mov_b32_dpp v45, v5 row_shr:1 row_mask:0xf bank_mask:0xf bound_ctrl:1
	v_pk_add_f32 v[44:45], v[4:5], v[44:45]
	v_min_f32_e32 v6, 0, v6
	v_mul_f32_e32 v46, 0x3f317217, v7
	v_fma_f32 v46, v7, s33, -v46
	v_fmac_f32_e32 v46, 0x3377d1cf, v7
	v_fmac_f32_e32 v46, 0x3f317217, v7
	v_cmp_lt_f32_e64 s[44:45], |v7|, s36
	s_nop 1
	v_cndmask_b32_e64 v7, v7, v46, s[44:45]
	v_cndmask_b32_e32 v46, 0, v216, vcc
	v_sub_f32_e32 v46, v7, v46
	v_div_scale_f32 v7, s[2:3], v0, v0, v114
	v_rcp_f32_e32 v47, v7
	s_nop 0
	v_fma_f32 v48, -v7, v47, 1.0
	v_fmac_f32_e32 v47, v48, v47
	v_div_scale_f32 v48, vcc, v114, v0, v114
; template <int CTRL> __device__ __forceinline__ float dppx(float v) { return __int_as_float(__builtin_amdgcn_update_dpp(0, __float_as_int(v), CTRL, 0xf, 0xf, true)); }
; __device__ __forceinline__ float log_forget(float z, float lb) {
;   const float r0 = fminf(z, 0.f) - __logf(1.f + __expf(-fabsf(z)));
;   const float r1 = __logf(lb + (1.f - lb) / (1.f + __expf(-z)));
;   return lb <= 0.f ? r0 : r1;
; }
;   __device__ __forceinline__ void operator()(const f32x4 (&acc)[2][2][4][2], const pg8::Unit& u, int wr, int wc, int fr, int fq) const {
;     ...
;               for (int q = 0; q < 4; ++q) { const float gv = log_forget(acc[ai][bj][m][qh][q], lq[q]); g[m][q] = gv;
;                 float sc = gv; sc += dppx<0x111>(sc); sc += dppx<0x112>(sc); sc += dppx<0x114>(sc); sc += dppx<0x118>(sc);
;                 const float tot16 = __int_as_float(__builtin_amdgcn_ds_swizzle(__float_as_int(sc), 0x1F0));
;                 cs[m][q] = sc + carry[q]; carry[q] += tot16; }
	v_mul_f32_e32 v49, v48, v47
	v_fma_f32 v62, -v7, v49, v48
	v_fmac_f32_e32 v49, v62, v47
	v_fma_f32 v7, -v7, v49, v48
	v_div_fmas_f32 v7, v7, v47, v49
	v_div_fixup_f32 v0, v7, v0, v114
	v_add_f32_e32 v0, v64, v0
	v_cmp_gt_f32_e32 vcc, s37, v0
	s_nop 1
	v_cndmask_b32_e64 v7, 0, 32, vcc
	v_ldexp_f32 v0, v0, v7
	v_log_f32_e32 v0, v0
	s_nop 0
	v_mul_f32_e32 v7, 0x3f317217, v0
	v_fma_f32 v7, v0, s33, -v7
	v_fmac_f32_e32 v7, 0x3377d1cf, v0
	v_fmac_f32_e32 v7, 0x3f317217, v0
	v_cmp_lt_f32_e64 s[44:45], |v0|, s36
	s_nop 1
	v_cndmask_b32_e64 v0, v0, v7, s[44:45]
	v_cndmask_b32_e32 v7, 0, v216, vcc
	v_sub_f32_e32 v62, v0, v7
	v_max_f32_e32 v0, v1, v1
	v_min_f32_e32 v7, 0, v0
	v_mul_f32_e64 v0, |v1|, s8
	v_exp_f32_e32 v0, v0
	s_nop 0
	v_add_f32_e32 v0, 1.0, v0
	v_cmp_gt_f32_e32 vcc, s37, v0
	s_nop 1
	v_cndmask_b32_e64 v47, 0, 32, vcc
	v_ldexp_f32 v0, v0, v47
	v_log_f32_e32 v0, v0
	s_nop 0
	v_mul_f32_e32 v47, 0x3f317217, v0
	v_fma_f32 v47, v0, s33, -v47
	v_fmac_f32_e32 v47, 0x3377d1cf, v0
	v_fmac_f32_e32 v47, 0x3f317217, v0
	v_cmp_lt_f32_e64 s[44:45], |v0|, s36
	s_nop 1
	v_cndmask_b32_e64 v0, v0, v47, s[44:45]
	v_cndmask_b32_e32 v47, 0, v216, vcc
	v_sub_f32_e32 v47, v0, v47
	v_mul_f32_e32 v0, 0xbfb8aa3b, v1
	v_exp_f32_e32 v0, v0
	v_pk_add_f32 v[6:7], v[6:7], v[46:47] neg_lo:[0,1] neg_hi:[0,1]
	v_add_f32_e32 v0, 1.0, v0
	v_div_scale_f32 v1, s[2:3], v0, v0, v113
	v_rcp_f32_e32 v48, v1
	v_cndmask_b32_e64 v6, v62, v6, s[48:49]
	v_fma_f32 v49, -v1, v48, 1.0
	v_fmac_f32_e32 v48, v49, v48
	v_div_scale_f32 v49, vcc, v113, v0, v113
	v_mul_f32_e32 v63, v49, v48
	v_fma_f32 v64, -v1, v63, v49
	v_fmac_f32_e32 v63, v64, v48
	v_fma_f32 v1, -v1, v63, v49
	v_div_fmas_f32 v1, v1, v48, v63
	v_div_fixup_f32 v0, v1, v0, v113
	v_add_f32_e32 v0, v65, v0
	v_cmp_gt_f32_e32 vcc, s37, v0
	v_mov_b32_dpp v46, v6 row_shr:1 row_mask:0xf bank_mask:0xf bound_ctrl:1
	s_nop 0
	v_cndmask_b32_e64 v1, 0, 32, vcc
	v_ldexp_f32 v0, v0, v1
	v_log_f32_e32 v0, v0
	s_nop 0
	v_mul_f32_e32 v1, 0x3f317217, v0
	v_fma_f32 v1, v0, s33, -v1
	v_fmac_f32_e32 v1, 0x3377d1cf, v0
	v_fmac_f32_e32 v1, 0x3f317217, v0
	v_cmp_lt_f32_e64 s[44:45], |v0|, s36
	s_nop 1
	v_cndmask_b32_e64 v0, v0, v1, s[44:45]
	v_cndmask_b32_e32 v1, 0, v216, vcc
	v_sub_f32_e32 v63, v0, v1
	v_mul_f32_e64 v1, |v2|, s8
	v_exp_f32_e32 v1, v1
	v_max_f32_e32 v0, v2, v2
	v_cndmask_b32_e64 v7, v63, v7, s[52:53]
	v_min_f32_e32 v0, 0, v0
	v_add_f32_e32 v1, 1.0, v1
	v_cmp_gt_f32_e32 vcc, s37, v1
	v_mov_b32_dpp v47, v7 row_shr:1 row_mask:0xf bank_mask:0xf bound_ctrl:1
	v_pk_add_f32 v[46:47], v[6:7], v[46:47]
	v_cndmask_b32_e64 v48, 0, 32, vcc
	v_ldexp_f32 v1, v1, v48
	v_log_f32_e32 v1, v1
	s_nop 0
	v_mul_f32_e32 v48, 0x3f317217, v1
	v_fma_f32 v48, v1, s33, -v48
	v_fmac_f32_e32 v48, 0x3377d1cf, v1
	v_fmac_f32_e32 v48, 0x3f317217, v1
	v_cmp_lt_f32_e64 s[44:45], |v1|, s36
	s_nop 1
	v_cndmask_b32_e64 v1, v1, v48, s[44:45]
	v_cndmask_b32_e32 v48, 0, v216, vcc
	v_sub_f32_e32 v48, v1, v48
	v_mul_f32_e32 v1, 0xbfb8aa3b, v2
	v_exp_f32_e32 v1, v1
	s_nop 0
	v_add_f32_e32 v1, 1.0, v1
	v_div_scale_f32 v2, s[2:3], v1, v1, v112
	v_rcp_f32_e32 v49, v2
	s_nop 0
	v_fma_f32 v64, -v2, v49, 1.0
	v_fmac_f32_e32 v49, v64, v49
	v_div_scale_f32 v64, vcc, v112, v1, v112
	v_mul_f32_e32 v65, v64, v49
	v_fma_f32 v68, -v2, v65, v64
	v_fmac_f32_e32 v65, v68, v49
	v_fma_f32 v2, -v2, v65, v64
	v_div_fmas_f32 v2, v2, v49, v65
	v_div_fixup_f32 v1, v2, v1, v112
	v_add_f32_e32 v1, v66, v1
	v_cmp_gt_f32_e32 vcc, s37, v1
	s_nop 1
	v_cndmask_b32_e64 v2, 0, 32, vcc
	v_ldexp_f32 v1, v1, v2
	v_log_f32_e32 v1, v1
	s_nop 0
	v_mul_f32_e32 v2, 0x3f317217, v1
	v_fma_f32 v2, v1, s33, -v2
	v_fmac_f32_e32 v2, 0x3377d1cf, v1
	v_fmac_f32_e32 v2, 0x3f317217, v1
	v_cmp_lt_f32_e64 s[44:45], |v1|, s36
	s_nop 1
	v_cndmask_b32_e64 v1, v1, v2, s[44:45]
	v_cndmask_b32_e32 v2, 0, v216, vcc
	v_sub_f32_e32 v64, v1, v2
	v_mul_f32_e64 v2, |v3|, s8
	v_exp_f32_e32 v2, v2
	v_max_f32_e32 v1, v3, v3
	v_min_f32_e32 v1, 0, v1
	v_add_f32_e32 v2, 1.0, v2
	v_cmp_gt_f32_e32 vcc, s37, v2
	s_nop 1
	v_cndmask_b32_e64 v49, 0, 32, vcc
	v_ldexp_f32 v2, v2, v49
	v_log_f32_e32 v2, v2
	s_nop 0
	v_mul_f32_e32 v49, 0x3f317217, v2
	v_fma_f32 v49, v2, s33, -v49
	v_fmac_f32_e32 v49, 0x3377d1cf, v2
	v_fmac_f32_e32 v49, 0x3f317217, v2
	v_cmp_lt_f32_e64 s[44:45], |v2|, s36
	s_nop 1
	v_cndmask_b32_e64 v2, v2, v49, s[44:45]
	v_cndmask_b32_e32 v49, 0, v216, vcc
	v_sub_f32_e32 v49, v2, v49
	v_mul_f32_e32 v2, 0xbfb8aa3b, v3
	v_exp_f32_e32 v2, v2
	v_pk_add_f32 v[0:1], v[0:1], v[48:49] neg_lo:[0,1] neg_hi:[0,1]
	v_add_f32_e32 v2, 1.0, v2
	v_div_scale_f32 v3, s[2:3], v2, v2, v96
	v_rcp_f32_e32 v65, v3
	v_cndmask_b32_e64 v48, v64, v0, s[56:57]
	v_fma_f32 v66, -v3, v65, 1.0
	v_fmac_f32_e32 v65, v66, v65
	v_div_scale_f32 v66, vcc, v96, v2, v96
	v_mul_f32_e32 v68, v66, v65
	v_fma_f32 v69, -v3, v68, v66
	v_fmac_f32_e32 v68, v69, v65
	v_fma_f32 v3, -v3, v68, v66
	v_div_fmas_f32 v3, v3, v65, v68
	v_div_fixup_f32 v2, v3, v2, v96
	v_add_f32_e32 v2, v67, v2
	v_cmp_gt_f32_e32 vcc, s37, v2
	v_mov_b32_dpp v0, v48 row_shr:1 row_mask:0xf bank_mask:0xf bound_ctrl:1
	s_nop 0
	v_cndmask_b32_e64 v3, 0, 32, vcc
	v_ldexp_f32 v2, v2, v3
	v_log_f32_e32 v2, v2
	s_nop 0
	v_mul_f32_e32 v3, 0x3f317217, v2
	v_fma_f32 v3, v2, s33, -v3
	v_fmac_f32_e32 v3, 0x3377d1cf, v2
	v_fmac_f32_e32 v3, 0x3f317217, v2
	v_cmp_lt_f32_e64 s[44:45], |v2|, s36
	s_nop 1
	v_cndmask_b32_e64 v2, v2, v3, s[44:45]
	v_cndmask_b32_e32 v3, 0, v216, vcc
	v_sub_f32_e32 v65, v2, v3
	v_pk_add_f32 v[2:3], v[32:33], v[34:35] neg_lo:[0,1] neg_hi:[0,1]
	v_cndmask_b32_e64 v49, v65, v1, s[58:59]
	v_cndmask_b32_e64 v3, v51, v3, s[52:53]
	v_cndmask_b32_e64 v2, v50, v2, s[48:49]
	v_mov_b32_dpp v1, v49 row_shr:1 row_mask:0xf bank_mask:0xf bound_ctrl:1
	v_mov_b32_dpp v33, v3 row_shr:1 row_mask:0xf bank_mask:0xf bound_ctrl:1
	v_mov_b32_dpp v32, v2 row_shr:1 row_mask:0xf bank_mask:0xf bound_ctrl:1
	v_pk_add_f32 v[32:33], v[2:3], v[32:33]
	v_pk_add_f32 v[0:1], v[48:49], v[0:1]
	s_nop 0
	v_mov_b32_dpp v34, v32 row_shr:2 row_mask:0xf bank_mask:0xf bound_ctrl:1
	v_mov_b32_dpp v35, v33 row_shr:2 row_mask:0xf bank_mask:0xf bound_ctrl:1
	v_pk_add_f32 v[32:33], v[32:33], v[34:35]
	s_nop 1
	v_mov_b32_dpp v34, v32 row_shr:4 row_mask:0xf bank_mask:0xf bound_ctrl:1
	v_mov_b32_dpp v35, v33 row_shr:4 row_mask:0xf bank_mask:0xf bound_ctrl:1
	v_pk_add_f32 v[32:33], v[32:33], v[34:35]
	s_nop 1
	v_mov_b32_dpp v34, v32 row_shr:8 row_mask:0xf bank_mask:0xf bound_ctrl:1
	v_mov_b32_dpp v35, v33 row_shr:8 row_mask:0xf bank_mask:0xf bound_ctrl:1
	v_pk_add_f32 v[32:33], v[32:33], v[34:35]
	ds_swizzle_b32 v34, v32 offset:swizzle(BROADCAST,16,15)
	ds_swizzle_b32 v35, v33 offset:swizzle(BROADCAST,16,15)
	v_pk_add_f32 v[32:33], v[32:33], 0 op_sel_hi:[1,0]
	s_waitcnt lgkmcnt(0)
; template <int CTRL> __device__ __forceinline__ float dppx(float v) { return __int_as_float(__builtin_amdgcn_update_dpp(0, __float_as_int(v), CTRL, 0xf, 0xf, true)); }
;   __device__ __forceinline__ void operator()(const f32x4 (&acc)[2][2][4][2], const pg8::Unit& u, int wr, int wc, int fr, int fq) const {
;     ...
;                 float sc = gv; sc += dppx<0x111>(sc); sc += dppx<0x112>(sc); sc += dppx<0x114>(sc); sc += dppx<0x118>(sc);
;                 const float tot16 = __int_as_float(__builtin_amdgcn_ds_swizzle(__float_as_int(sc), 0x1F0));
;                 cs[m][q] = sc + carry[q]; carry[q] += tot16; }
; #pragma unroll
;             for (int m = 0; m < 4; ++m) { const int r = row0 + ai * 128 + m * 16; float bq[4], kq[4];
; #pragma unroll
;               for (int q = 0; q < 4; ++q) { bq[q] = bwd ? (carry[q] - cs[m][q]) + g[m][q] : cs[m][q]; kq[q] = 1.f - __expf(g[m][q]); }
	v_pk_add_f32 v[50:51], v[34:35], 0 op_sel_hi:[1,0]
	v_mul_f32_e32 v34, 0x3fb8aa3b, v2
	v_exp_f32_e32 v34, v34
	v_mov_b32_dpp v35, v13 row_shr:1 row_mask:0xf bank_mask:0xf bound_ctrl:1
	v_sub_f32_e32 v66, 1.0, v34
	v_mul_f32_e32 v34, 0x3fb8aa3b, v3
	v_exp_f32_e32 v34, v34
	s_nop 0
	v_sub_f32_e32 v67, 1.0, v34
	v_mov_b32_dpp v34, v12 row_shr:1 row_mask:0xf bank_mask:0xf bound_ctrl:1
	v_pk_add_f32 v[34:35], v[12:13], v[34:35]
	s_nop 1
	v_mov_b32_dpp v36, v34 row_shr:2 row_mask:0xf bank_mask:0xf bound_ctrl:1
	v_mov_b32_dpp v37, v35 row_shr:2 row_mask:0xf bank_mask:0xf bound_ctrl:1
	v_pk_add_f32 v[34:35], v[34:35], v[36:37]
	s_nop 1
	v_mov_b32_dpp v36, v34 row_shr:4 row_mask:0xf bank_mask:0xf bound_ctrl:1
	v_mov_b32_dpp v37, v35 row_shr:4 row_mask:0xf bank_mask:0xf bound_ctrl:1
	v_pk_add_f32 v[34:35], v[34:35], v[36:37]
	s_nop 1
	v_mov_b32_dpp v36, v34 row_shr:8 row_mask:0xf bank_mask:0xf bound_ctrl:1
	v_mov_b32_dpp v37, v35 row_shr:8 row_mask:0xf bank_mask:0xf bound_ctrl:1
	v_pk_add_f32 v[34:35], v[34:35], v[36:37]
	ds_swizzle_b32 v36, v34 offset:swizzle(BROADCAST,16,15)
	ds_swizzle_b32 v37, v35 offset:swizzle(BROADCAST,16,15)
	v_pk_add_f32 v[34:35], v[34:35], 0 op_sel_hi:[1,0]
	s_waitcnt lgkmcnt(0)
	v_pk_add_f32 v[52:53], v[36:37], 0 op_sel_hi:[1,0]
	v_mul_f32_e32 v36, 0x3fb8aa3b, v12
	v_exp_f32_e32 v36, v36
	v_mov_b32_dpp v37, v15 row_shr:1 row_mask:0xf bank_mask:0xf bound_ctrl:1
	v_sub_f32_e32 v68, 1.0, v36
	v_mul_f32_e32 v36, 0x3fb8aa3b, v13
	v_exp_f32_e32 v36, v36
	s_nop 0
	v_sub_f32_e32 v69, 1.0, v36
	v_mov_b32_dpp v36, v14 row_shr:1 row_mask:0xf bank_mask:0xf bound_ctrl:1
	v_pk_add_f32 v[36:37], v[14:15], v[36:37]
	s_nop 1
	v_mov_b32_dpp v38, v36 row_shr:2 row_mask:0xf bank_mask:0xf bound_ctrl:1
	v_mov_b32_dpp v39, v37 row_shr:2 row_mask:0xf bank_mask:0xf bound_ctrl:1
	v_pk_add_f32 v[36:37], v[36:37], v[38:39]
	s_nop 1
	v_mov_b32_dpp v38, v36 row_shr:4 row_mask:0xf bank_mask:0xf bound_ctrl:1
	v_mov_b32_dpp v39, v37 row_shr:4 row_mask:0xf bank_mask:0xf bound_ctrl:1
	v_pk_add_f32 v[36:37], v[36:37], v[38:39]
	s_nop 1
	v_mov_b32_dpp v38, v36 row_shr:8 row_mask:0xf bank_mask:0xf bound_ctrl:1
	v_mov_b32_dpp v39, v37 row_shr:8 row_mask:0xf bank_mask:0xf bound_ctrl:1
	v_pk_add_f32 v[36:37], v[36:37], v[38:39]
	ds_swizzle_b32 v38, v36 offset:swizzle(BROADCAST,16,15)
	ds_swizzle_b32 v39, v37 offset:swizzle(BROADCAST,16,15)
	v_pk_add_f32 v[36:37], v[50:51], v[36:37]
	s_waitcnt lgkmcnt(0)
	v_pk_add_f32 v[50:51], v[50:51], v[38:39]
	v_mul_f32_e32 v38, 0x3fb8aa3b, v14
	v_exp_f32_e32 v38, v38
	v_mov_b32_dpp v39, v9 row_shr:1 row_mask:0xf bank_mask:0xf bound_ctrl:1
	v_sub_f32_e32 v70, 1.0, v38
	v_mul_f32_e32 v38, 0x3fb8aa3b, v15
	v_exp_f32_e32 v38, v38
	s_nop 0
	v_sub_f32_e32 v71, 1.0, v38
	v_mov_b32_dpp v38, v8 row_shr:1 row_mask:0xf bank_mask:0xf bound_ctrl:1
	v_pk_add_f32 v[38:39], v[8:9], v[38:39]
	s_nop 1
	v_mov_b32_dpp v40, v38 row_shr:2 row_mask:0xf bank_mask:0xf bound_ctrl:1
	v_mov_b32_dpp v41, v39 row_shr:2 row_mask:0xf bank_mask:0xf bound_ctrl:1
	v_pk_add_f32 v[38:39], v[38:39], v[40:41]
	s_nop 1
	v_mov_b32_dpp v40, v38 row_shr:4 row_mask:0xf bank_mask:0xf bound_ctrl:1
	v_mov_b32_dpp v41, v39 row_shr:4 row_mask:0xf bank_mask:0xf bound_ctrl:1
	v_pk_add_f32 v[38:39], v[38:39], v[40:41]
	s_nop 1
	v_mov_b32_dpp v40, v38 row_shr:8 row_mask:0xf bank_mask:0xf bound_ctrl:1
	v_mov_b32_dpp v41, v39 row_shr:8 row_mask:0xf bank_mask:0xf bound_ctrl:1
	v_pk_add_f32 v[38:39], v[38:39], v[40:41]
	ds_swizzle_b32 v40, v38 offset:swizzle(BROADCAST,16,15)
	ds_swizzle_b32 v41, v39 offset:swizzle(BROADCAST,16,15)
	v_pk_add_f32 v[38:39], v[52:53], v[38:39]
	s_waitcnt lgkmcnt(0)
	v_pk_add_f32 v[40:41], v[52:53], v[40:41]
	v_mul_f32_e32 v52, 0x3fb8aa3b, v8
	v_exp_f32_e32 v52, v52
	v_mov_b32_dpp v53, v43 row_shr:2 row_mask:0xf bank_mask:0xf bound_ctrl:1
	v_sub_f32_e32 v56, 1.0, v52
	v_mul_f32_e32 v52, 0x3fb8aa3b, v9
	v_exp_f32_e32 v52, v52
	s_nop 0
	v_sub_f32_e32 v57, 1.0, v52
	v_mov_b32_dpp v52, v42 row_shr:2 row_mask:0xf bank_mask:0xf bound_ctrl:1
	v_pk_add_f32 v[42:43], v[42:43], v[52:53]
	s_nop 1
	v_mov_b32_dpp v52, v42 row_shr:4 row_mask:0xf bank_mask:0xf bound_ctrl:1
	v_mov_b32_dpp v53, v43 row_shr:4 row_mask:0xf bank_mask:0xf bound_ctrl:1
	v_pk_add_f32 v[42:43], v[42:43], v[52:53]
	s_nop 1
	v_mov_b32_dpp v52, v42 row_shr:8 row_mask:0xf bank_mask:0xf bound_ctrl:1
	v_mov_b32_dpp v53, v43 row_shr:8 row_mask:0xf bank_mask:0xf bound_ctrl:1
	v_pk_add_f32 v[42:43], v[42:43], v[52:53]
	ds_swizzle_b32 v52, v42 offset:swizzle(BROADCAST,16,15)
	ds_swizzle_b32 v53, v43 offset:swizzle(BROADCAST,16,15)
	v_pk_add_f32 v[42:43], v[50:51], v[42:43]
	s_waitcnt lgkmcnt(0)
; template <int CTRL> __device__ __forceinline__ float dppx(float v) { return __int_as_float(__builtin_amdgcn_update_dpp(0, __float_as_int(v), CTRL, 0xf, 0xf, true)); }
; __device__ __forceinline__ unsigned cvt_pk_bf16(float lo, float hi) { unsigned r; asm volatile("v_cvt_pk_bf16_f32 %0, %1, %2" : "=v"(r) : "v"(lo), "v"(hi)); return r; }
;   __device__ __forceinline__ void operator()(const f32x4 (&acc)[2][2][4][2], const pg8::Unit& u, int wr, int wc, int fr, int fq) const {
;     ...
;                 float sc = gv; sc += dppx<0x111>(sc); sc += dppx<0x112>(sc); sc += dppx<0x114>(sc); sc += dppx<0x118>(sc);
;                 const float tot16 = __int_as_float(__builtin_amdgcn_ds_swizzle(__float_as_int(sc), 0x1F0));
;                 cs[m][q] = sc + carry[q]; carry[q] += tot16; }
; #pragma unroll
;             for (int m = 0; m < 4; ++m) { const int r = row0 + ai * 128 + m * 16; float bq[4], kq[4];
; #pragma unroll
;               for (int q = 0; q < 4; ++q) { bq[q] = bwd ? (carry[q] - cs[m][q]) + g[m][q] : cs[m][q]; kq[q] = 1.f - __expf(g[m][q]); }
;               *(f32x4*)(logfp + (size_t)r * 1024 + c + 4 * qh) = (f32x4){bq[0], bq[1], bq[2], bq[3]};
;               u32x2 w; w.x = pg8::cvt_pk_bf16(kq[0], kq[1]); w.y = pg8::cvt_pk_bf16(kq[2], kq[3]);
;               *(u32x2*)(km + (size_t)r * 1024 + c + 4 * qh) = w; } } }
	v_pk_add_f32 v[50:51], v[50:51], v[52:53]
	v_mul_f32_e32 v52, 0x3fb8aa3b, v10
	v_exp_f32_e32 v52, v52
	v_mov_b32_dpp v53, v45 row_shr:2 row_mask:0xf bank_mask:0xf bound_ctrl:1
	v_sub_f32_e32 v58, 1.0, v52
	v_mul_f32_e32 v52, 0x3fb8aa3b, v11
	v_exp_f32_e32 v52, v52
	s_nop 0
	v_sub_f32_e32 v59, 1.0, v52
	v_mov_b32_dpp v52, v44 row_shr:2 row_mask:0xf bank_mask:0xf bound_ctrl:1
	v_pk_add_f32 v[44:45], v[44:45], v[52:53]
	s_nop 1
	v_mov_b32_dpp v52, v44 row_shr:4 row_mask:0xf bank_mask:0xf bound_ctrl:1
	v_mov_b32_dpp v53, v45 row_shr:4 row_mask:0xf bank_mask:0xf bound_ctrl:1
	v_pk_add_f32 v[44:45], v[44:45], v[52:53]
	s_nop 1
	v_mov_b32_dpp v52, v44 row_shr:8 row_mask:0xf bank_mask:0xf bound_ctrl:1
	v_mov_b32_dpp v53, v45 row_shr:8 row_mask:0xf bank_mask:0xf bound_ctrl:1
	v_pk_add_f32 v[44:45], v[44:45], v[52:53]
	ds_swizzle_b32 v52, v44 offset:swizzle(BROADCAST,16,15)
	ds_swizzle_b32 v53, v45 offset:swizzle(BROADCAST,16,15)
	v_pk_add_f32 v[44:45], v[40:41], v[44:45]
	s_waitcnt lgkmcnt(0)
	v_pk_add_f32 v[40:41], v[40:41], v[52:53]
	v_mul_f32_e32 v52, 0x3fb8aa3b, v4
	v_exp_f32_e32 v52, v52
	v_mov_b32_dpp v53, v47 row_shr:2 row_mask:0xf bank_mask:0xf bound_ctrl:1
	v_sub_f32_e32 v60, 1.0, v52
	v_mul_f32_e32 v52, 0x3fb8aa3b, v5
	v_exp_f32_e32 v52, v52
	s_nop 0
	v_sub_f32_e32 v61, 1.0, v52
	v_mov_b32_dpp v52, v46 row_shr:2 row_mask:0xf bank_mask:0xf bound_ctrl:1
	v_pk_add_f32 v[46:47], v[46:47], v[52:53]
	s_nop 1
	v_mov_b32_dpp v52, v46 row_shr:4 row_mask:0xf bank_mask:0xf bound_ctrl:1
	v_mov_b32_dpp v53, v47 row_shr:4 row_mask:0xf bank_mask:0xf bound_ctrl:1
	v_pk_add_f32 v[46:47], v[46:47], v[52:53]
	s_nop 1
	v_mov_b32_dpp v52, v46 row_shr:8 row_mask:0xf bank_mask:0xf bound_ctrl:1
	v_mov_b32_dpp v53, v47 row_shr:8 row_mask:0xf bank_mask:0xf bound_ctrl:1
	v_pk_add_f32 v[46:47], v[46:47], v[52:53]
	ds_swizzle_b32 v52, v46 offset:swizzle(BROADCAST,16,15)
	ds_swizzle_b32 v53, v47 offset:swizzle(BROADCAST,16,15)
	v_pk_add_f32 v[46:47], v[50:51], v[46:47]
	s_waitcnt lgkmcnt(0)
	v_pk_add_f32 v[50:51], v[50:51], v[52:53]
	v_mul_f32_e32 v52, 0x3fb8aa3b, v6
	v_exp_f32_e32 v52, v52
	v_mov_b32_dpp v53, v1 row_shr:2 row_mask:0xf bank_mask:0xf bound_ctrl:1
	v_sub_f32_e32 v62, 1.0, v52
	v_mul_f32_e32 v52, 0x3fb8aa3b, v7
	v_exp_f32_e32 v52, v52
	s_nop 0
	v_sub_f32_e32 v63, 1.0, v52
	v_mov_b32_dpp v52, v0 row_shr:2 row_mask:0xf bank_mask:0xf bound_ctrl:1
	v_pk_add_f32 v[0:1], v[0:1], v[52:53]
	s_nop 1
	v_mov_b32_dpp v52, v0 row_shr:4 row_mask:0xf bank_mask:0xf bound_ctrl:1
	v_mov_b32_dpp v53, v1 row_shr:4 row_mask:0xf bank_mask:0xf bound_ctrl:1
	v_pk_add_f32 v[0:1], v[0:1], v[52:53]
	s_nop 1
	v_mov_b32_dpp v52, v0 row_shr:8 row_mask:0xf bank_mask:0xf bound_ctrl:1
	v_mov_b32_dpp v53, v1 row_shr:8 row_mask:0xf bank_mask:0xf bound_ctrl:1
	v_pk_add_f32 v[0:1], v[0:1], v[52:53]
	ds_swizzle_b32 v52, v0 offset:swizzle(BROADCAST,16,15)
	ds_swizzle_b32 v53, v1 offset:swizzle(BROADCAST,16,15)
	v_pk_add_f32 v[54:55], v[40:41], v[0:1]
	v_pk_add_f32 v[0:1], v[50:51], v[32:33] neg_lo:[0,1] neg_hi:[0,1]
	s_waitcnt lgkmcnt(0)
	v_pk_add_f32 v[40:41], v[40:41], v[52:53]
	s_nop 0
	v_pk_add_f32 v[52:53], v[40:41], v[34:35] neg_lo:[0,1] neg_hi:[0,1]
	v_pk_add_f32 v[0:1], v[2:3], v[0:1]
	v_pk_add_f32 v[2:3], v[12:13], v[52:53]
	v_cndmask_b32_e64 v1, v33, v1, s[42:43]
	v_cndmask_b32_e64 v3, v35, v3, s[42:43]
	v_cndmask_b32_e64 v2, v34, v2, s[42:43]
	v_cndmask_b32_e64 v0, v32, v0, s[42:43]
	global_store_dwordx4 v[18:19], v[0:3], off offset:16
	s_nop 1
	v_cvt_pk_bf16_f32 v0, v66, v67
	v_cvt_pk_bf16_f32 v1, v68, v69
	global_store_dwordx2 v[16:17], v[0:1], off offset:8
	v_pk_add_f32 v[0:1], v[50:51], v[36:37] neg_lo:[0,1] neg_hi:[0,1]
	v_pk_add_f32 v[2:3], v[40:41], v[38:39] neg_lo:[0,1] neg_hi:[0,1]
	v_pk_add_f32 v[0:1], v[14:15], v[0:1]
	v_pk_add_f32 v[2:3], v[8:9], v[2:3]
	v_cndmask_b32_e64 v1, v37, v1, s[42:43]
	v_cndmask_b32_e64 v3, v39, v3, s[42:43]
	v_cndmask_b32_e64 v2, v38, v2, s[42:43]
	v_cndmask_b32_e64 v0, v36, v0, s[42:43]
	global_store_dwordx4 v[22:23], v[0:3], off offset:16
	s_nop 1
	v_cvt_pk_bf16_f32 v0, v70, v71
	v_cvt_pk_bf16_f32 v1, v56, v57
	global_store_dwordx2 v[20:21], v[0:1], off offset:8
	v_pk_add_f32 v[0:1], v[50:51], v[42:43] neg_lo:[0,1] neg_hi:[0,1]
	v_pk_add_f32 v[2:3], v[40:41], v[44:45] neg_lo:[0,1] neg_hi:[0,1]
	v_pk_add_f32 v[0:1], v[10:11], v[0:1]
	v_pk_add_f32 v[2:3], v[4:5], v[2:3]
	v_cndmask_b32_e64 v1, v43, v1, s[42:43]
	v_cndmask_b32_e64 v3, v45, v3, s[42:43]
	v_cndmask_b32_e64 v2, v44, v2, s[42:43]
	v_cndmask_b32_e64 v0, v42, v0, s[42:43]
	global_store_dwordx4 v[26:27], v[0:3], off offset:16
	v_mul_f32_e32 v5, 0x3fb8aa3b, v49
	v_exp_f32_e32 v5, v5
	v_cvt_pk_bf16_f32 v0, v58, v59
	v_cvt_pk_bf16_f32 v1, v60, v61
	global_store_dwordx2 v[24:25], v[0:1], off offset:8
	v_mul_f32_e32 v0, 0x3fb8aa3b, v48
	v_exp_f32_e32 v0, v0
	v_pk_add_f32 v[2:3], v[40:41], v[54:55] neg_lo:[0,1] neg_hi:[0,1]
	v_sub_f32_e32 v5, 1.0, v5
	v_pk_add_f32 v[2:3], v[48:49], v[2:3]
	v_sub_f32_e32 v4, 1.0, v0
	v_pk_add_f32 v[0:1], v[50:51], v[46:47] neg_lo:[0,1] neg_hi:[0,1]
	v_cndmask_b32_e64 v3, v55, v3, s[42:43]
	v_pk_add_f32 v[0:1], v[6:7], v[0:1]
	v_cndmask_b32_e64 v2, v54, v2, s[42:43]
	v_cndmask_b32_e64 v1, v47, v1, s[42:43]
	v_cndmask_b32_e64 v0, v46, v0, s[42:43]
	global_store_dwordx4 v[28:29], v[0:3], off offset:16
	s_nop 1
	v_cvt_pk_bf16_f32 v0, v62, v63
	v_cvt_pk_bf16_f32 v1, v4, v5
	global_store_dwordx2 v[30:31], v[0:1], off offset:8
	s_and_b64 vcc, exec, s[40:41]
	s_mov_b64 s[6:7], -1
	s_cbranch_vccnz .LBB0_189
